# fp8 MFMAs: unit-scale MX form (v_mfma_scale..., scales 2^0) replaced by the plain f8f6f4 form of the same instruction (identical arithmetic, half the encoding, no scale operands)
# baseline (speedup 1.0000x reference)
.LBB0_243:
	ds_read_b128 v[8:11], v180
	ds_read_b128 v[12:15], v180 offset:1024
	s_waitcnt lgkmcnt(0)
	ds_read_b128 v[0:3], v180 offset:2048
	ds_read_b128 v[4:7], v180 offset:3072
	s_add_u32 s22, s4, 0xfffc0080
	s_addc_u32 s23, s5, -1
	s_cmp_eq_u32 s75, 12
	s_cselect_b32 s25, s69, s23
	s_cselect_b32 s24, s70, s22
	s_cselect_b32 s23, s71, s74
	s_cselect_b32 s22, s72, s73
	v_lshl_add_u64 v[166:167], s[4:5], 0, v[160:161]
	s_add_i32 m0, s39, 0xc000
	ds_read_b128 v[186:189], v181
	ds_read_b128 v[190:193], v181 offset:1024
	ds_read_b128 v[194:197], v181 offset:2048
	ds_read_b128 v[198:201], v181 offset:3072
	ds_read_b128 v[202:205], v181 offset:4096
	ds_read_b128 v[206:209], v181 offset:5120
	ds_read_b128 v[210:213], v181 offset:6144
	ds_read_b128 v[214:217], v181 offset:7168
	global_load_lds_dwordx4 v[166:167], off
	v_lshl_add_u64 v[166:167], s[4:5], 0, v[158:159]
	s_add_i32 m0, s39, 0xe000
	s_nop 0
	global_load_lds_dwordx4 v[166:167], off
	s_waitcnt lgkmcnt(8)
	s_barrier
	s_waitcnt lgkmcnt(0)
	s_setprio 1
	s_waitcnt lgkmcnt(0)
	v_mfma_f32_16x16x128_f8f6f4 v[140:143], v[8:15], v[186:193], v[140:143]
	v_mfma_f32_16x16x128_f8f6f4 v[136:139], v[0:7], v[186:193], v[136:139]
	v_mfma_f32_16x16x128_f8f6f4 v[124:127], v[8:15], v[194:201], v[124:127]
	v_mfma_f32_16x16x128_f8f6f4 v[120:123], v[0:7], v[194:201], v[120:123]
	v_mfma_f32_16x16x128_f8f6f4 v[108:111], v[8:15], v[202:209], v[108:111]
	v_mfma_f32_16x16x128_f8f6f4 v[104:107], v[0:7], v[202:209], v[104:107]
	v_mfma_f32_16x16x128_f8f6f4 v[92:95], v[8:15], v[210:217], v[92:95]
	v_mfma_f32_16x16x128_f8f6f4 v[88:91], v[0:7], v[210:217], v[88:91]
	s_setprio 0
	s_barrier
	s_add_i32 s76, s51, s38
	v_lshl_add_u64 v[166:167], s[22:23], 0, v[146:147]
	s_mov_b32 m0, s76
	ds_read_b128 v[224:227], v182
	ds_read_b128 v[228:231], v182 offset:1024
	ds_read_b128 v[232:235], v182 offset:2048
	ds_read_b128 v[236:239], v182 offset:3072
	global_load_lds_dwordx4 v[166:167], off
	v_lshl_add_u64 v[168:169], s[22:23], 0, v[150:151]
	s_add_i32 m0, s76, 0x2000
	s_nop 0
	global_load_lds_dwordx4 v[168:169], off
	s_barrier
	s_waitcnt lgkmcnt(0)
	s_setprio 1
	s_waitcnt lgkmcnt(0)
	v_mfma_f32_16x16x128_f8f6f4 v[132:135], v[224:231], v[186:193], v[132:135]
	v_mfma_f32_16x16x128_f8f6f4 v[128:131], v[232:239], v[186:193], v[128:131]
	v_mfma_f32_16x16x128_f8f6f4 v[116:119], v[224:231], v[194:201], v[116:119]
	v_mfma_f32_16x16x128_f8f6f4 v[112:115], v[232:239], v[194:201], v[112:115]
	v_mfma_f32_16x16x128_f8f6f4 v[100:103], v[224:231], v[202:209], v[100:103]
	v_mfma_f32_16x16x128_f8f6f4 v[96:99], v[232:239], v[202:209], v[96:99]
	v_mfma_f32_16x16x128_f8f6f4 v[84:87], v[224:231], v[210:217], v[84:87]
	v_mfma_f32_16x16x128_f8f6f4 v[80:83], v[232:239], v[210:217], v[80:83]
	s_setprio 0
	s_mov_b32 m0, s39
	v_lshl_add_u64 v[170:171], s[24:25], 0, v[144:145]
	s_barrier
	ds_read_b128 v[186:189], v181 offset:16384
	ds_read_b128 v[190:193], v181 offset:17408
	ds_read_b128 v[194:197], v181 offset:18432
	ds_read_b128 v[198:201], v181 offset:19456
	ds_read_b128 v[202:205], v181 offset:20480
	ds_read_b128 v[206:209], v181 offset:21504
	ds_read_b128 v[210:213], v181 offset:22528
	ds_read_b128 v[214:217], v181 offset:23552
	global_load_lds_dwordx4 v[170:171], off
	v_lshl_add_u64 v[172:173], s[24:25], 0, v[148:149]
	s_mov_b32 m0, s40
	s_nop 0
	global_load_lds_dwordx4 v[172:173], off
	s_barrier
	s_waitcnt lgkmcnt(0)
	s_setprio 1
	s_waitcnt lgkmcnt(0)
	v_mfma_f32_16x16x128_f8f6f4 v[76:79], v[8:15], v[186:193], v[76:79]
	v_mfma_f32_16x16x128_f8f6f4 v[72:75], v[0:7], v[186:193], v[72:75]
	v_mfma_f32_16x16x128_f8f6f4 v[60:63], v[8:15], v[194:201], v[60:63]
	v_mfma_f32_16x16x128_f8f6f4 v[56:59], v[0:7], v[194:201], v[56:59]
	v_mfma_f32_16x16x128_f8f6f4 v[44:47], v[8:15], v[202:209], v[44:47]
	v_mfma_f32_16x16x128_f8f6f4 v[40:43], v[0:7], v[202:209], v[40:43]
	v_mfma_f32_16x16x128_f8f6f4 v[28:31], v[8:15], v[210:217], v[28:31]
	v_mfma_f32_16x16x128_f8f6f4 v[24:27], v[0:7], v[210:217], v[24:27]
	s_setprio 0
	s_barrier
	s_add_u32 s76, s22, 0x40000
	s_addc_u32 s77, s23, 0
	s_add_i32 s78, s53, s38
	v_lshl_add_u64 v[0:1], s[76:77], 0, v[146:147]
	s_mov_b32 m0, s78
	s_nop 0
	global_load_lds_dwordx4 v[0:1], off
	v_lshl_add_u64 v[0:1], s[76:77], 0, v[150:151]
	s_add_i32 m0, s78, 0x2000
	s_nop 0
	global_load_lds_dwordx4 v[0:1], off
	s_waitcnt vmcnt(6)
	s_barrier
	s_setprio 1
	v_mfma_f32_16x16x128_f8f6f4 v[68:71], v[224:231], v[186:193], v[68:71]
	v_mfma_f32_16x16x128_f8f6f4 v[64:67], v[232:239], v[186:193], v[64:67]
	v_mfma_f32_16x16x128_f8f6f4 v[52:55], v[224:231], v[194:201], v[52:55]
	v_mfma_f32_16x16x128_f8f6f4 v[48:51], v[232:239], v[194:201], v[48:51]
	v_mfma_f32_16x16x128_f8f6f4 v[36:39], v[224:231], v[202:209], v[36:39]
	v_mfma_f32_16x16x128_f8f6f4 v[32:35], v[232:239], v[202:209], v[32:35]
	v_mfma_f32_16x16x128_f8f6f4 v[20:23], v[224:231], v[210:217], v[20:23]
	v_mfma_f32_16x16x128_f8f6f4 v[16:19], v[232:239], v[210:217], v[16:19]
	s_setprio 0
	s_add_i32 s76, 0, 0x18000
	v_add_u32_e32 v12, s76, v179
	s_barrier
	ds_read_b128 v[0:3], v12
	ds_read_b128 v[4:7], v12 offset:1024
	ds_read_b128 v[8:11], v12 offset:2048
	ds_read_b128 v[12:15], v12 offset:3072
	s_add_u32 s24, s24, 0x40000
	s_addc_u32 s25, s25, 0
	s_mov_b32 m0, s41
	v_lshl_add_u64 v[218:219], s[24:25], 0, v[144:145]
	ds_read_b128 v[186:189], v181 offset:32768
	ds_read_b128 v[190:193], v181 offset:33792
	ds_read_b128 v[194:197], v181 offset:34816
	ds_read_b128 v[198:201], v181 offset:35840
	ds_read_b128 v[202:205], v181 offset:36864
	ds_read_b128 v[206:209], v181 offset:37888
	ds_read_b128 v[210:213], v181 offset:38912
	ds_read_b128 v[214:217], v181 offset:39936
	global_load_lds_dwordx4 v[218:219], off
	v_lshl_add_u64 v[218:219], s[24:25], 0, v[148:149]
	s_mov_b32 m0, s42
	s_nop 0
	global_load_lds_dwordx4 v[218:219], off
	s_waitcnt lgkmcnt(8)
	s_barrier
	s_waitcnt lgkmcnt(0)
	s_setprio 1
	s_waitcnt lgkmcnt(0)
	v_mfma_f32_16x16x128_f8f6f4 v[140:143], v[0:7], v[186:193], v[140:143]
	v_mfma_f32_16x16x128_f8f6f4 v[136:139], v[8:15], v[186:193], v[136:139]
	v_mfma_f32_16x16x128_f8f6f4 v[124:127], v[0:7], v[194:201], v[124:127]
	v_mfma_f32_16x16x128_f8f6f4 v[120:123], v[8:15], v[194:201], v[120:123]
	v_mfma_f32_16x16x128_f8f6f4 v[108:111], v[0:7], v[202:209], v[108:111]
	v_mfma_f32_16x16x128_f8f6f4 v[104:107], v[8:15], v[202:209], v[104:107]
	v_mfma_f32_16x16x128_f8f6f4 v[92:95], v[0:7], v[210:217], v[92:95]
	v_mfma_f32_16x16x128_f8f6f4 v[88:91], v[8:15], v[210:217], v[88:91]
	s_setprio 0
	s_barrier
	s_add_i32 s24, 0, 0x1c000
	s_add_i32 s25, s76, s38
	v_add_u32_e32 v152, s24, v179
	v_lshl_add_u64 v[166:167], v[166:167], 0, s[12:13]
	s_mov_b32 m0, s25
	ds_read_b128 v[224:227], v152
	ds_read_b128 v[228:231], v152 offset:1024
	ds_read_b128 v[232:235], v152 offset:2048
	ds_read_b128 v[236:239], v152 offset:3072
	global_load_lds_dwordx4 v[166:167], off
	v_lshl_add_u64 v[166:167], v[168:169], 0, s[12:13]
	s_add_i32 m0, s25, 0x2000
	s_nop 0
	global_load_lds_dwordx4 v[166:167], off
	s_barrier
	s_waitcnt lgkmcnt(0)
	s_setprio 1
	s_waitcnt lgkmcnt(0)
	v_mfma_f32_16x16x128_f8f6f4 v[132:135], v[224:231], v[186:193], v[132:135]
	v_mfma_f32_16x16x128_f8f6f4 v[128:131], v[232:239], v[186:193], v[128:131]
	v_mfma_f32_16x16x128_f8f6f4 v[116:119], v[224:231], v[194:201], v[116:119]
	v_mfma_f32_16x16x128_f8f6f4 v[112:115], v[232:239], v[194:201], v[112:115]
	v_mfma_f32_16x16x128_f8f6f4 v[100:103], v[224:231], v[202:209], v[100:103]
	v_mfma_f32_16x16x128_f8f6f4 v[96:99], v[232:239], v[202:209], v[96:99]
	v_mfma_f32_16x16x128_f8f6f4 v[84:87], v[224:231], v[210:217], v[84:87]
	v_mfma_f32_16x16x128_f8f6f4 v[80:83], v[232:239], v[210:217], v[80:83]
	s_setprio 0
	s_mov_b32 m0, s46
	v_lshl_add_u64 v[166:167], v[170:171], 0, s[12:13]
	s_barrier
	ds_read_b128 v[186:189], v181 offset:49152
	ds_read_b128 v[190:193], v181 offset:50176
	ds_read_b128 v[194:197], v181 offset:51200
	ds_read_b128 v[198:201], v181 offset:52224
	ds_read_b128 v[202:205], v181 offset:53248
	ds_read_b128 v[206:209], v181 offset:54272
	ds_read_b128 v[210:213], v181 offset:55296
	ds_read_b128 v[214:217], v181 offset:56320
	global_load_lds_dwordx4 v[166:167], off
	v_lshl_add_u64 v[166:167], v[172:173], 0, s[12:13]
	s_mov_b32 m0, s47
	s_nop 0
	global_load_lds_dwordx4 v[166:167], off
	s_barrier
	s_waitcnt lgkmcnt(0)
	s_setprio 1
	s_waitcnt lgkmcnt(0)
	v_mfma_f32_16x16x128_f8f6f4 v[76:79], v[0:7], v[186:193], v[76:79]
	v_mfma_f32_16x16x128_f8f6f4 v[72:75], v[8:15], v[186:193], v[72:75]
	v_mfma_f32_16x16x128_f8f6f4 v[60:63], v[0:7], v[194:201], v[60:63]
	v_mfma_f32_16x16x128_f8f6f4 v[56:59], v[8:15], v[194:201], v[56:59]
	v_mfma_f32_16x16x128_f8f6f4 v[44:47], v[0:7], v[202:209], v[44:47]
	v_mfma_f32_16x16x128_f8f6f4 v[40:43], v[8:15], v[202:209], v[40:43]
	v_mfma_f32_16x16x128_f8f6f4 v[28:31], v[0:7], v[210:217], v[28:31]
	v_mfma_f32_16x16x128_f8f6f4 v[24:27], v[8:15], v[210:217], v[24:27]
	s_setprio 0
	s_barrier
	s_add_u32 s22, s22, 0x40080
	s_addc_u32 s23, s23, 0
	s_add_i32 s24, s24, s38
	v_lshl_add_u64 v[0:1], s[22:23], 0, v[146:147]
	s_mov_b32 m0, s24
	s_nop 0
	global_load_lds_dwordx4 v[0:1], off
	v_lshl_add_u64 v[0:1], s[22:23], 0, v[150:151]
	s_add_i32 m0, s24, 0x2000
	s_nop 0
	global_load_lds_dwordx4 v[0:1], off
	s_waitcnt vmcnt(6)
	s_barrier
	s_setprio 1
	v_mfma_f32_16x16x128_f8f6f4 v[68:71], v[224:231], v[186:193], v[68:71]
	v_mfma_f32_16x16x128_f8f6f4 v[64:67], v[232:239], v[186:193], v[64:67]
	v_mfma_f32_16x16x128_f8f6f4 v[52:55], v[224:231], v[194:201], v[52:55]
	v_mfma_f32_16x16x128_f8f6f4 v[48:51], v[232:239], v[194:201], v[48:51]
	v_mfma_f32_16x16x128_f8f6f4 v[36:39], v[224:231], v[202:209], v[36:39]
	v_mfma_f32_16x16x128_f8f6f4 v[32:35], v[232:239], v[202:209], v[32:35]
	v_mfma_f32_16x16x128_f8f6f4 v[20:23], v[224:231], v[210:217], v[20:23]
	v_mfma_f32_16x16x128_f8f6f4 v[16:19], v[232:239], v[210:217], v[16:19]
	s_setprio 0
	s_add_i32 s75, s75, 2
	s_add_u32 s73, s73, 0x100
	s_addc_u32 s74, s74, 0
	s_add_u32 s4, s4, 0x100
	s_addc_u32 s5, s5, 0
	s_cmp_gt_u32 s75, 13
	s_barrier
	s_cbranch_scc0 .LBB0_243
	s_nop 7
	s_nop 7
	s_nop 7
	s_cmp_gt_i32 s67, 3
	s_cselect_b64 s[4:5], -1, 0
	v_lshl_add_u32 v0, s68, 8, v178
	s_and_b64 vcc, exec, s[4:5]
	s_cbranch_vccz .LBB0_247
	s_mov_b64 s[22:23], -1
	s_and_b64 vcc, exec, s[4:5]
	s_cbranch_vccnz .LBB0_264

.LBB0_365:
	ds_read_b128 v[12:15], v176
	ds_read_b128 v[16:19], v176 offset:1024
	ds_read_b128 v[28:31], v176 offset:2048
	ds_read_b128 v[32:35], v176 offset:3072
	s_add_u32 s18, s29, s57
	v_cmp_lt_i64_e32 vcc, s[6:7], v[144:145]
	s_addc_u32 s19, s30, 0
	s_and_b64 s[2:3], vcc, exec
	s_cselect_b32 s25, s19, s23
	s_cselect_b32 s24, s18, s22
	s_add_u32 s20, s31, s58
	s_addc_u32 s21, s38, 0
	s_and_b64 s[2:3], vcc, exec
	s_cselect_b32 s3, s21, s27
	s_cselect_b32 s2, s20, s26
	s_add_u32 s62, s22, 0x20080
	s_addc_u32 s63, s23, 0
	s_add_i32 s67, s40, 0xc000
	v_lshl_add_u64 v[44:45], s[62:63], 0, v[136:137]
	s_mov_b32 m0, s67
	s_add_i32 s61, s40, 0xe000
	ds_read_b128 v[4:7], v177
	ds_read_b128 v[8:11], v177 offset:1024
	ds_read_b128 v[20:23], v177 offset:2048
	ds_read_b128 v[24:27], v177 offset:3072
	ds_read_b128 v[36:39], v177 offset:4096
	ds_read_b128 v[40:43], v177 offset:5120
	ds_read_b128 v[52:55], v177 offset:6144
	ds_read_b128 v[56:59], v177 offset:7168
	global_load_lds_dwordx4 v[44:45], off
	v_lshl_add_u64 v[44:45], s[62:63], 0, v[140:141]
	s_mov_b32 m0, s61
	s_nop 0
	global_load_lds_dwordx4 v[44:45], off
	s_waitcnt lgkmcnt(8)
	s_barrier
	s_waitcnt lgkmcnt(0)
	s_setprio 1
	v_mov_b64_e32 v[110:111], v[2:3]
	v_mov_b64_e32 v[114:115], v[2:3]
	v_mov_b64_e32 v[106:107], v[2:3]
	v_mov_b64_e32 v[102:103], v[2:3]
	v_mov_b64_e32 v[82:83], v[2:3]
	v_mov_b64_e32 v[78:79], v[2:3]
	v_mov_b64_e32 v[50:51], v[2:3]
	v_mov_b64_e32 v[46:47], v[2:3]
	v_mov_b64_e32 v[108:109], v[0:1]
	v_mov_b64_e32 v[112:113], v[0:1]
	v_mov_b64_e32 v[104:105], v[0:1]
	v_mov_b64_e32 v[100:101], v[0:1]
	v_mov_b64_e32 v[80:81], v[0:1]
	v_mov_b64_e32 v[76:77], v[0:1]
	v_mov_b64_e32 v[48:49], v[0:1]
	v_mov_b64_e32 v[44:45], v[0:1]
	s_waitcnt lgkmcnt(0)
	v_mfma_f32_16x16x128_f8f6f4 v[108:111], v[12:19], v[4:11], v[108:111]
	v_mfma_f32_16x16x128_f8f6f4 v[112:115], v[28:35], v[4:11], v[112:115]
	v_mfma_f32_16x16x128_f8f6f4 v[104:107], v[12:19], v[20:27], v[104:107]
	v_mfma_f32_16x16x128_f8f6f4 v[100:103], v[28:35], v[20:27], v[100:103]
	v_mfma_f32_16x16x128_f8f6f4 v[80:83], v[12:19], v[36:43], v[80:83]
	v_mfma_f32_16x16x128_f8f6f4 v[76:79], v[28:35], v[36:43], v[76:79]
	v_mfma_f32_16x16x128_f8f6f4 v[48:51], v[12:19], v[52:59], v[48:51]
	v_mfma_f32_16x16x128_f8f6f4 v[44:47], v[28:35], v[52:59], v[44:47]
	s_setprio 0
	s_barrier
	v_lshl_add_u64 v[132:133], s[26:27], 0, v[138:139]
	s_add_i32 s64, s50, s39
	v_lshl_add_u64 v[60:61], v[132:133], 0, s[10:11]
	s_mov_b32 m0, s64
	v_lshl_add_u64 v[134:135], s[26:27], 0, v[142:143]
	s_add_i32 s62, s64, 0x2000
	ds_read_b128 v[154:157], v178
	ds_read_b128 v[158:161], v178 offset:1024
	ds_read_b128 v[180:183], v178 offset:2048
	ds_read_b128 v[184:187], v178 offset:3072
	global_load_lds_dwordx4 v[60:61], off
	v_lshl_add_u64 v[60:61], v[134:135], 0, s[10:11]
	s_mov_b32 m0, s62
	s_nop 0
	global_load_lds_dwordx4 v[60:61], off
	s_barrier
	s_waitcnt lgkmcnt(0)
	s_setprio 1
	v_mov_b64_e32 v[126:127], v[2:3]
	v_mov_b64_e32 v[130:131], v[2:3]
	v_mov_b64_e32 v[122:123], v[2:3]
	v_mov_b64_e32 v[118:119], v[2:3]
	v_mov_b64_e32 v[98:99], v[2:3]
	v_mov_b64_e32 v[94:95], v[2:3]
	v_mov_b64_e32 v[66:67], v[2:3]
	v_mov_b64_e32 v[62:63], v[2:3]
	v_mov_b64_e32 v[124:125], v[0:1]
	v_mov_b64_e32 v[128:129], v[0:1]
	v_mov_b64_e32 v[120:121], v[0:1]
	v_mov_b64_e32 v[116:117], v[0:1]
	v_mov_b64_e32 v[96:97], v[0:1]
	v_mov_b64_e32 v[92:93], v[0:1]
	v_mov_b64_e32 v[64:65], v[0:1]
	v_mov_b64_e32 v[60:61], v[0:1]
	s_waitcnt lgkmcnt(0)
	v_mfma_f32_16x16x128_f8f6f4 v[124:127], v[154:161], v[4:11], v[124:127]
	v_mfma_f32_16x16x128_f8f6f4 v[128:131], v[180:187], v[4:11], v[128:131]
	v_mfma_f32_16x16x128_f8f6f4 v[120:123], v[154:161], v[20:27], v[120:123]
	v_mfma_f32_16x16x128_f8f6f4 v[116:119], v[180:187], v[20:27], v[116:119]
	v_mfma_f32_16x16x128_f8f6f4 v[96:99], v[154:161], v[36:43], v[96:99]
	v_mfma_f32_16x16x128_f8f6f4 v[92:95], v[180:187], v[36:43], v[92:95]
	v_mfma_f32_16x16x128_f8f6f4 v[64:67], v[154:161], v[52:59], v[64:67]
	v_mfma_f32_16x16x128_f8f6f4 v[60:63], v[180:187], v[52:59], v[60:63]
	s_setprio 0
	v_lshl_add_u64 v[150:151], s[22:23], 0, v[136:137]
	s_mov_b32 m0, s40
	v_lshl_add_u64 v[4:5], v[150:151], 0, s[10:11]
	v_lshl_add_u64 v[152:153], s[22:23], 0, v[140:141]
	s_barrier
	ds_read_b128 v[52:55], v177 offset:16384
	ds_read_b128 v[56:59], v177 offset:17408
	ds_read_b128 v[188:191], v177 offset:18432
	ds_read_b128 v[192:195], v177 offset:19456
	ds_read_b128 v[196:199], v177 offset:20480
	ds_read_b128 v[200:203], v177 offset:21504
	ds_read_b128 v[204:207], v177 offset:22528
	ds_read_b128 v[208:211], v177 offset:23552
	global_load_lds_dwordx4 v[4:5], off
	v_lshl_add_u64 v[4:5], v[152:153], 0, s[10:11]
	s_mov_b32 m0, s41
	s_nop 0
	global_load_lds_dwordx4 v[4:5], off
	s_barrier
	s_waitcnt lgkmcnt(0)
	s_setprio 1
	v_mov_b64_e32 v[74:75], v[2:3]
	v_mov_b64_e32 v[70:71], v[2:3]
	v_mov_b64_e32 v[42:43], v[2:3]
	v_mov_b64_e32 v[38:39], v[2:3]
	v_mov_b64_e32 v[26:27], v[2:3]
	v_mov_b64_e32 v[22:23], v[2:3]
	v_mov_b64_e32 v[10:11], v[2:3]
	v_mov_b64_e32 v[6:7], v[2:3]
	v_mov_b64_e32 v[72:73], v[0:1]
	v_mov_b64_e32 v[68:69], v[0:1]
	v_mov_b64_e32 v[40:41], v[0:1]
	v_mov_b64_e32 v[36:37], v[0:1]
	v_mov_b64_e32 v[24:25], v[0:1]
	v_mov_b64_e32 v[20:21], v[0:1]
	v_mov_b64_e32 v[8:9], v[0:1]
	v_mov_b64_e32 v[4:5], v[0:1]
	s_waitcnt lgkmcnt(0)
	v_mfma_f32_16x16x128_f8f6f4 v[72:75], v[12:19], v[52:59], v[72:75]
	v_mfma_f32_16x16x128_f8f6f4 v[68:71], v[28:35], v[52:59], v[68:71]
	v_mfma_f32_16x16x128_f8f6f4 v[40:43], v[12:19], v[188:195], v[40:43]
	v_mfma_f32_16x16x128_f8f6f4 v[36:39], v[28:35], v[188:195], v[36:39]
	v_mfma_f32_16x16x128_f8f6f4 v[24:27], v[12:19], v[196:203], v[24:27]
	v_mfma_f32_16x16x128_f8f6f4 v[20:23], v[28:35], v[196:203], v[20:23]
	v_mfma_f32_16x16x128_f8f6f4 v[8:11], v[12:19], v[204:211], v[8:11]
	v_mfma_f32_16x16x128_f8f6f4 v[4:7], v[28:35], v[204:211], v[4:7]
	s_setprio 0
	s_barrier
	s_add_u32 s68, s26, 0x10100
	s_addc_u32 s69, s27, 0
	s_add_i32 s65, s51, s39
	v_lshl_add_u64 v[12:13], s[68:69], 0, v[138:139]
	s_mov_b32 m0, s65
	s_add_i32 s63, s65, 0x2000
	global_load_lds_dwordx4 v[12:13], off
	v_lshl_add_u64 v[12:13], s[68:69], 0, v[142:143]
	s_mov_b32 m0, s63
	s_nop 0
	global_load_lds_dwordx4 v[12:13], off
	s_waitcnt vmcnt(6)
	s_barrier
	s_setprio 1
	v_mov_b64_e32 v[90:91], v[2:3]
	v_mov_b64_e32 v[86:87], v[2:3]
	v_mov_b64_e32 v[88:89], v[0:1]
	v_mov_b64_e32 v[84:85], v[0:1]
	v_mfma_f32_16x16x128_f8f6f4 v[88:91], v[154:161], v[52:59], v[88:91]
	v_mfma_f32_16x16x128_f8f6f4 v[84:87], v[180:187], v[52:59], v[84:87]
	v_mov_b64_e32 v[58:59], v[2:3]
	v_mov_b64_e32 v[54:55], v[2:3]
	v_mov_b64_e32 v[34:35], v[2:3]
	v_mov_b64_e32 v[30:31], v[2:3]
	v_mov_b64_e32 v[18:19], v[2:3]
	v_mov_b64_e32 v[14:15], v[2:3]
	v_mov_b64_e32 v[56:57], v[0:1]
	v_mov_b64_e32 v[52:53], v[0:1]
	v_mov_b64_e32 v[32:33], v[0:1]
	v_mov_b64_e32 v[28:29], v[0:1]
	v_mov_b64_e32 v[16:17], v[0:1]
	v_mov_b64_e32 v[12:13], v[0:1]
	v_mfma_f32_16x16x128_f8f6f4 v[56:59], v[154:161], v[188:195], v[56:59]
	v_mfma_f32_16x16x128_f8f6f4 v[52:55], v[180:187], v[188:195], v[52:55]
	v_mfma_f32_16x16x128_f8f6f4 v[32:35], v[154:161], v[196:203], v[32:35]
	v_mfma_f32_16x16x128_f8f6f4 v[28:31], v[180:187], v[196:203], v[28:31]
	v_mfma_f32_16x16x128_f8f6f4 v[16:19], v[154:161], v[204:211], v[16:19]
	v_mfma_f32_16x16x128_f8f6f4 v[12:15], v[180:187], v[204:211], v[12:15]
	s_setprio 0
	s_add_i32 s66, 0, 0x18000
	v_add_u32_e32 v154, s66, v174
	s_barrier
	ds_read_b128 v[156:159], v154
	ds_read_b128 v[160:163], v154 offset:1024
	ds_read_b128 v[180:183], v154 offset:2048
	ds_read_b128 v[184:187], v154 offset:3072
	s_add_u32 s68, s22, 0x20100
	s_addc_u32 s69, s23, 0
	s_mov_b32 m0, s42
	v_lshl_add_u64 v[164:165], s[68:69], 0, v[136:137]
	ds_read_b128 v[188:191], v177 offset:32768
	ds_read_b128 v[192:195], v177 offset:33792
	ds_read_b128 v[196:199], v177 offset:34816
	ds_read_b128 v[200:203], v177 offset:35840
	ds_read_b128 v[204:207], v177 offset:36864
	ds_read_b128 v[208:211], v177 offset:37888
	ds_read_b128 v[212:215], v177 offset:38912
	ds_read_b128 v[216:219], v177 offset:39936
	global_load_lds_dwordx4 v[164:165], off
	v_lshl_add_u64 v[164:165], s[68:69], 0, v[140:141]
	s_mov_b32 m0, s43
	s_nop 0
	global_load_lds_dwordx4 v[164:165], off
	s_waitcnt lgkmcnt(8)
	s_barrier
	s_waitcnt lgkmcnt(0)
	s_setprio 1
	s_waitcnt lgkmcnt(0)
	v_mfma_f32_16x16x128_f8f6f4 v[108:111], v[156:163], v[188:195], v[108:111]
	v_mfma_f32_16x16x128_f8f6f4 v[112:115], v[180:187], v[188:195], v[112:115]
	v_mfma_f32_16x16x128_f8f6f4 v[104:107], v[156:163], v[196:203], v[104:107]
	v_mfma_f32_16x16x128_f8f6f4 v[100:103], v[180:187], v[196:203], v[100:103]
	v_mfma_f32_16x16x128_f8f6f4 v[80:83], v[156:163], v[204:211], v[80:83]
	v_mfma_f32_16x16x128_f8f6f4 v[76:79], v[180:187], v[204:211], v[76:79]
	v_mfma_f32_16x16x128_f8f6f4 v[48:51], v[156:163], v[212:219], v[48:51]
	v_mfma_f32_16x16x128_f8f6f4 v[44:47], v[180:187], v[212:219], v[44:47]
	s_setprio 0
	s_barrier
	s_add_i32 s69, 0, 0x1c000
	s_add_i32 s68, s66, s39
	v_add_u32_e32 v155, s69, v174
	v_lshl_add_u64 v[132:133], v[132:133], 0, s[12:13]
	s_mov_b32 m0, s68
	s_add_i32 s66, s68, 0x2000
	ds_read_b128 v[224:227], v155
	ds_read_b128 v[228:231], v155 offset:1024
	ds_read_b128 v[232:235], v155 offset:2048
	ds_read_b128 v[236:239], v155 offset:3072
	global_load_lds_dwordx4 v[132:133], off
	v_lshl_add_u64 v[132:133], v[134:135], 0, s[12:13]
	s_mov_b32 m0, s66
	s_nop 0
	global_load_lds_dwordx4 v[132:133], off
	s_barrier
	s_waitcnt lgkmcnt(0)
	s_setprio 1
	s_waitcnt lgkmcnt(0)
	v_mfma_f32_16x16x128_f8f6f4 v[124:127], v[224:231], v[188:195], v[124:127]
	v_mfma_f32_16x16x128_f8f6f4 v[128:131], v[232:239], v[188:195], v[128:131]
	v_mfma_f32_16x16x128_f8f6f4 v[120:123], v[224:231], v[196:203], v[120:123]
	v_mfma_f32_16x16x128_f8f6f4 v[116:119], v[232:239], v[196:203], v[116:119]
	v_mfma_f32_16x16x128_f8f6f4 v[96:99], v[224:231], v[204:211], v[96:99]
	v_mfma_f32_16x16x128_f8f6f4 v[92:95], v[232:239], v[204:211], v[92:95]
	v_mfma_f32_16x16x128_f8f6f4 v[64:67], v[224:231], v[212:219], v[64:67]
	v_mfma_f32_16x16x128_f8f6f4 v[60:63], v[232:239], v[212:219], v[60:63]
	s_setprio 0
	s_mov_b32 m0, s46
	v_lshl_add_u64 v[132:133], v[150:151], 0, s[12:13]
	s_barrier
	ds_read_b128 v[188:191], v177 offset:49152
	ds_read_b128 v[192:195], v177 offset:50176
	ds_read_b128 v[196:199], v177 offset:51200
	ds_read_b128 v[200:203], v177 offset:52224
	ds_read_b128 v[204:207], v177 offset:53248
	ds_read_b128 v[208:211], v177 offset:54272
	ds_read_b128 v[212:215], v177 offset:55296
	ds_read_b128 v[216:219], v177 offset:56320
	global_load_lds_dwordx4 v[132:133], off
	v_lshl_add_u64 v[132:133], v[152:153], 0, s[12:13]
	s_mov_b32 m0, s47
	s_nop 0
	global_load_lds_dwordx4 v[132:133], off
	s_barrier
	s_waitcnt lgkmcnt(0)
	s_setprio 1
	s_waitcnt lgkmcnt(0)
	v_mfma_f32_16x16x128_f8f6f4 v[72:75], v[156:163], v[188:195], v[72:75]
	v_mfma_f32_16x16x128_f8f6f4 v[68:71], v[180:187], v[188:195], v[68:71]
	v_mfma_f32_16x16x128_f8f6f4 v[40:43], v[156:163], v[196:203], v[40:43]
	v_mfma_f32_16x16x128_f8f6f4 v[36:39], v[180:187], v[196:203], v[36:39]
	v_mfma_f32_16x16x128_f8f6f4 v[24:27], v[156:163], v[204:211], v[24:27]
	v_mfma_f32_16x16x128_f8f6f4 v[20:23], v[180:187], v[204:211], v[20:23]
	v_mfma_f32_16x16x128_f8f6f4 v[8:11], v[156:163], v[212:219], v[8:11]
	v_mfma_f32_16x16x128_f8f6f4 v[4:7], v[180:187], v[212:219], v[4:7]
	s_setprio 0
	s_barrier
	s_add_u32 s70, s26, 0x10180
	s_addc_u32 s71, s27, 0
	s_add_i32 s27, s69, s39
	v_lshl_add_u64 v[132:133], s[70:71], 0, v[138:139]
	s_mov_b32 m0, s27
	s_add_i32 s26, s27, 0x2000
	global_load_lds_dwordx4 v[132:133], off
	v_lshl_add_u64 v[132:133], s[70:71], 0, v[142:143]
	s_mov_b32 m0, s26
	s_nop 0
	global_load_lds_dwordx4 v[132:133], off
	s_waitcnt vmcnt(6)
	s_barrier
	s_setprio 1
	v_mfma_f32_16x16x128_f8f6f4 v[88:91], v[224:231], v[188:195], v[88:91]
	v_mfma_f32_16x16x128_f8f6f4 v[84:87], v[232:239], v[188:195], v[84:87]
	v_mfma_f32_16x16x128_f8f6f4 v[56:59], v[224:231], v[196:203], v[56:59]
	v_mfma_f32_16x16x128_f8f6f4 v[52:55], v[232:239], v[196:203], v[52:55]
	v_mfma_f32_16x16x128_f8f6f4 v[32:35], v[224:231], v[204:211], v[32:35]
	v_mfma_f32_16x16x128_f8f6f4 v[28:31], v[232:239], v[204:211], v[28:31]
	v_mfma_f32_16x16x128_f8f6f4 v[16:19], v[224:231], v[212:219], v[16:19]
	v_mfma_f32_16x16x128_f8f6f4 v[12:15], v[232:239], v[212:219], v[12:15]
	s_setprio 0
	s_barrier
	ds_read_b128 v[156:159], v176
	ds_read_b128 v[160:163], v176 offset:1024
	ds_read_b128 v[180:183], v176 offset:2048
	ds_read_b128 v[184:187], v176 offset:3072
	s_add_u32 s22, s22, 0x20180
	s_addc_u32 s23, s23, 0
	s_mov_b32 m0, s67
	v_lshl_add_u64 v[132:133], s[22:23], 0, v[136:137]
	ds_read_b128 v[188:191], v177
	ds_read_b128 v[192:195], v177 offset:1024
	ds_read_b128 v[196:199], v177 offset:2048
	ds_read_b128 v[200:203], v177 offset:3072
	ds_read_b128 v[204:207], v177 offset:4096
	ds_read_b128 v[208:211], v177 offset:5120
	ds_read_b128 v[212:215], v177 offset:6144
	ds_read_b128 v[216:219], v177 offset:7168
	global_load_lds_dwordx4 v[132:133], off
	v_lshl_add_u64 v[132:133], s[22:23], 0, v[140:141]
	s_mov_b32 m0, s61
	s_nop 0
	global_load_lds_dwordx4 v[132:133], off
	s_waitcnt lgkmcnt(8)
	s_barrier
	s_waitcnt lgkmcnt(0)
	s_setprio 1
	s_waitcnt lgkmcnt(0)
	v_mfma_f32_16x16x128_f8f6f4 v[108:111], v[156:163], v[188:195], v[108:111]
	v_mfma_f32_16x16x128_f8f6f4 v[112:115], v[180:187], v[188:195], v[112:115]
	v_mfma_f32_16x16x128_f8f6f4 v[104:107], v[156:163], v[196:203], v[104:107]
	v_mfma_f32_16x16x128_f8f6f4 v[100:103], v[180:187], v[196:203], v[100:103]
	v_mfma_f32_16x16x128_f8f6f4 v[80:83], v[156:163], v[204:211], v[80:83]
	v_mfma_f32_16x16x128_f8f6f4 v[76:79], v[180:187], v[204:211], v[76:79]
	v_mfma_f32_16x16x128_f8f6f4 v[48:51], v[156:163], v[212:219], v[48:51]
	v_mfma_f32_16x16x128_f8f6f4 v[44:47], v[180:187], v[212:219], v[44:47]
	s_setprio 0
	s_barrier
	s_mov_b32 m0, s64
	v_lshl_add_u64 v[132:133], s[2:3], 0, v[138:139]
	ds_read_b128 v[224:227], v178
	ds_read_b128 v[228:231], v178 offset:1024
	ds_read_b128 v[232:235], v178 offset:2048
	ds_read_b128 v[236:239], v178 offset:3072
	global_load_lds_dwordx4 v[132:133], off
	v_lshl_add_u64 v[134:135], s[2:3], 0, v[142:143]
	s_mov_b32 m0, s62
	s_nop 0
	global_load_lds_dwordx4 v[134:135], off
	s_barrier
	s_waitcnt lgkmcnt(0)
	s_setprio 1
	s_waitcnt lgkmcnt(0)
	v_mfma_f32_16x16x128_f8f6f4 v[124:127], v[224:231], v[188:195], v[124:127]
	v_mfma_f32_16x16x128_f8f6f4 v[128:131], v[232:239], v[188:195], v[128:131]
	v_mfma_f32_16x16x128_f8f6f4 v[120:123], v[224:231], v[196:203], v[120:123]
	v_mfma_f32_16x16x128_f8f6f4 v[116:119], v[232:239], v[196:203], v[116:119]
	v_mfma_f32_16x16x128_f8f6f4 v[96:99], v[224:231], v[204:211], v[96:99]
	v_mfma_f32_16x16x128_f8f6f4 v[92:95], v[232:239], v[204:211], v[92:95]
	v_mfma_f32_16x16x128_f8f6f4 v[64:67], v[224:231], v[212:219], v[64:67]
	v_mfma_f32_16x16x128_f8f6f4 v[60:63], v[232:239], v[212:219], v[60:63]
	s_setprio 0
	s_mov_b32 m0, s40
	v_lshl_add_u64 v[150:151], s[24:25], 0, v[136:137]
	s_barrier
	ds_read_b128 v[188:191], v177 offset:16384
	ds_read_b128 v[192:195], v177 offset:17408
	ds_read_b128 v[196:199], v177 offset:18432
	ds_read_b128 v[200:203], v177 offset:19456
	ds_read_b128 v[204:207], v177 offset:20480
	ds_read_b128 v[208:211], v177 offset:21504
	ds_read_b128 v[212:215], v177 offset:22528
	ds_read_b128 v[216:219], v177 offset:23552
	global_load_lds_dwordx4 v[150:151], off
	v_lshl_add_u64 v[152:153], s[24:25], 0, v[140:141]
	s_mov_b32 m0, s41
	s_nop 0
	global_load_lds_dwordx4 v[152:153], off
	s_barrier
	s_waitcnt lgkmcnt(0)
	s_setprio 1
	s_waitcnt lgkmcnt(0)
	v_mfma_f32_16x16x128_f8f6f4 v[72:75], v[156:163], v[188:195], v[72:75]
	v_mfma_f32_16x16x128_f8f6f4 v[68:71], v[180:187], v[188:195], v[68:71]
	v_mfma_f32_16x16x128_f8f6f4 v[40:43], v[156:163], v[196:203], v[40:43]
	v_mfma_f32_16x16x128_f8f6f4 v[36:39], v[180:187], v[196:203], v[36:39]
	v_mfma_f32_16x16x128_f8f6f4 v[24:27], v[156:163], v[204:211], v[24:27]
	v_mfma_f32_16x16x128_f8f6f4 v[20:23], v[180:187], v[204:211], v[20:23]
	v_mfma_f32_16x16x128_f8f6f4 v[8:11], v[156:163], v[212:219], v[8:11]
	v_mfma_f32_16x16x128_f8f6f4 v[4:7], v[180:187], v[212:219], v[4:7]
	s_setprio 0
	s_barrier
	s_add_u32 s22, s2, 0x10000
	s_addc_u32 s23, s3, 0
	s_mov_b32 m0, s65
	v_lshl_add_u64 v[156:157], s[22:23], 0, v[138:139]
	global_load_lds_dwordx4 v[156:157], off
	v_lshl_add_u64 v[156:157], s[22:23], 0, v[142:143]
	s_mov_b32 m0, s63
	s_nop 0
	global_load_lds_dwordx4 v[156:157], off
	s_waitcnt vmcnt(6)
	s_barrier
	s_setprio 1
	v_mfma_f32_16x16x128_f8f6f4 v[88:91], v[224:231], v[188:195], v[88:91]
	v_mfma_f32_16x16x128_f8f6f4 v[84:87], v[232:239], v[188:195], v[84:87]
	v_mfma_f32_16x16x128_f8f6f4 v[56:59], v[224:231], v[196:203], v[56:59]
	v_mfma_f32_16x16x128_f8f6f4 v[52:55], v[232:239], v[196:203], v[52:55]
	v_mfma_f32_16x16x128_f8f6f4 v[32:35], v[224:231], v[204:211], v[32:35]
	v_mfma_f32_16x16x128_f8f6f4 v[28:31], v[232:239], v[204:211], v[28:31]
	v_mfma_f32_16x16x128_f8f6f4 v[16:19], v[224:231], v[212:219], v[16:19]
	v_mfma_f32_16x16x128_f8f6f4 v[12:15], v[232:239], v[212:219], v[12:15]
	s_setprio 0
	s_barrier
	ds_read_b128 v[156:159], v154
	ds_read_b128 v[160:163], v154 offset:1024
	ds_read_b128 v[180:183], v154 offset:2048
	ds_read_b128 v[184:187], v154 offset:3072
	s_add_u32 s22, s24, 0x20000
	s_addc_u32 s23, s25, 0
	s_mov_b32 m0, s42
	v_lshl_add_u64 v[164:165], s[22:23], 0, v[136:137]
	ds_read_b128 v[188:191], v177 offset:32768
	ds_read_b128 v[192:195], v177 offset:33792
	ds_read_b128 v[196:199], v177 offset:34816
	ds_read_b128 v[200:203], v177 offset:35840
	ds_read_b128 v[204:207], v177 offset:36864
	ds_read_b128 v[208:211], v177 offset:37888
	ds_read_b128 v[212:215], v177 offset:38912
	ds_read_b128 v[216:219], v177 offset:39936
	global_load_lds_dwordx4 v[164:165], off
	v_lshl_add_u64 v[164:165], s[22:23], 0, v[140:141]
	s_mov_b32 m0, s43
	s_nop 0
	global_load_lds_dwordx4 v[164:165], off
	s_waitcnt lgkmcnt(8)
	s_barrier
	s_waitcnt lgkmcnt(0)
	s_setprio 1
	s_waitcnt lgkmcnt(0)
	v_mfma_f32_16x16x128_f8f6f4 v[108:111], v[156:163], v[188:195], v[108:111]
	v_mfma_f32_16x16x128_f8f6f4 v[112:115], v[180:187], v[188:195], v[112:115]
	v_mfma_f32_16x16x128_f8f6f4 v[104:107], v[156:163], v[196:203], v[104:107]
	v_mfma_f32_16x16x128_f8f6f4 v[100:103], v[180:187], v[196:203], v[100:103]
	v_mfma_f32_16x16x128_f8f6f4 v[80:83], v[156:163], v[204:211], v[80:83]
	v_mfma_f32_16x16x128_f8f6f4 v[76:79], v[180:187], v[204:211], v[76:79]
	v_mfma_f32_16x16x128_f8f6f4 v[48:51], v[156:163], v[212:219], v[48:51]
	v_mfma_f32_16x16x128_f8f6f4 v[44:47], v[180:187], v[212:219], v[44:47]
	s_setprio 0
	s_barrier
	s_mov_b32 m0, s68
	v_lshl_add_u64 v[132:133], v[132:133], 0, s[8:9]
	ds_read_b128 v[224:227], v155
	ds_read_b128 v[228:231], v155 offset:1024
	ds_read_b128 v[232:235], v155 offset:2048
	ds_read_b128 v[236:239], v155 offset:3072
	global_load_lds_dwordx4 v[132:133], off
	v_lshl_add_u64 v[132:133], v[134:135], 0, s[8:9]
	s_mov_b32 m0, s66
	s_nop 0
	global_load_lds_dwordx4 v[132:133], off
	s_barrier
	s_waitcnt lgkmcnt(0)
	s_setprio 1
	s_waitcnt lgkmcnt(0)
	v_mfma_f32_16x16x128_f8f6f4 v[124:127], v[224:231], v[188:195], v[124:127]
	v_mfma_f32_16x16x128_f8f6f4 v[128:131], v[232:239], v[188:195], v[128:131]
	v_mfma_f32_16x16x128_f8f6f4 v[120:123], v[224:231], v[196:203], v[120:123]
	v_mfma_f32_16x16x128_f8f6f4 v[116:119], v[232:239], v[196:203], v[116:119]
	v_mfma_f32_16x16x128_f8f6f4 v[96:99], v[224:231], v[204:211], v[96:99]
	v_mfma_f32_16x16x128_f8f6f4 v[92:95], v[232:239], v[204:211], v[92:95]
	v_mfma_f32_16x16x128_f8f6f4 v[64:67], v[224:231], v[212:219], v[64:67]
	v_mfma_f32_16x16x128_f8f6f4 v[60:63], v[232:239], v[212:219], v[60:63]
	s_setprio 0
	s_mov_b32 m0, s46
	v_lshl_add_u64 v[132:133], v[150:151], 0, s[8:9]
	s_barrier
	ds_read_b128 v[188:191], v177 offset:49152
	ds_read_b128 v[192:195], v177 offset:50176
	ds_read_b128 v[196:199], v177 offset:51200
	ds_read_b128 v[200:203], v177 offset:52224
	ds_read_b128 v[204:207], v177 offset:53248
	ds_read_b128 v[208:211], v177 offset:54272
	ds_read_b128 v[212:215], v177 offset:55296
	ds_read_b128 v[216:219], v177 offset:56320
	global_load_lds_dwordx4 v[132:133], off
	v_lshl_add_u64 v[132:133], v[152:153], 0, s[8:9]
	s_mov_b32 m0, s47
	s_nop 0
	global_load_lds_dwordx4 v[132:133], off
	s_barrier
	s_waitcnt lgkmcnt(0)
	s_setprio 1
	s_waitcnt lgkmcnt(0)
	v_mfma_f32_16x16x128_f8f6f4 v[72:75], v[156:163], v[188:195], v[72:75]
	v_mfma_f32_16x16x128_f8f6f4 v[68:71], v[180:187], v[188:195], v[68:71]
	v_mfma_f32_16x16x128_f8f6f4 v[40:43], v[156:163], v[196:203], v[40:43]
	v_mfma_f32_16x16x128_f8f6f4 v[36:39], v[180:187], v[196:203], v[36:39]
	v_mfma_f32_16x16x128_f8f6f4 v[24:27], v[156:163], v[204:211], v[24:27]
	v_mfma_f32_16x16x128_f8f6f4 v[20:23], v[180:187], v[204:211], v[20:23]
	v_mfma_f32_16x16x128_f8f6f4 v[8:11], v[156:163], v[212:219], v[8:11]
	v_mfma_f32_16x16x128_f8f6f4 v[4:7], v[180:187], v[212:219], v[4:7]
	s_setprio 0
	s_barrier
	s_add_u32 s2, s2, 0x10080
	s_addc_u32 s3, s3, 0
	s_mov_b32 m0, s27
	v_lshl_add_u64 v[132:133], s[2:3], 0, v[138:139]
	global_load_lds_dwordx4 v[132:133], off
	v_lshl_add_u64 v[132:133], s[2:3], 0, v[142:143]
	s_mov_b32 m0, s26
	s_nop 0
	global_load_lds_dwordx4 v[132:133], off
	s_waitcnt vmcnt(6)
	s_barrier
	s_setprio 1
	v_mfma_f32_16x16x128_f8f6f4 v[88:91], v[224:231], v[188:195], v[88:91]
	v_mfma_f32_16x16x128_f8f6f4 v[84:87], v[232:239], v[188:195], v[84:87]
	v_mfma_f32_16x16x128_f8f6f4 v[56:59], v[224:231], v[196:203], v[56:59]
	v_mfma_f32_16x16x128_f8f6f4 v[52:55], v[232:239], v[196:203], v[52:55]
	v_mfma_f32_16x16x128_f8f6f4 v[32:35], v[224:231], v[204:211], v[32:35]
	v_mfma_f32_16x16x128_f8f6f4 v[28:31], v[232:239], v[204:211], v[28:31]
	v_mfma_f32_16x16x128_f8f6f4 v[16:19], v[224:231], v[212:219], v[16:19]
	v_mfma_f32_16x16x128_f8f6f4 v[12:15], v[232:239], v[212:219], v[12:15]
	s_setprio 0
	v_lshl_add_u32 v164, s60, 8, v173
	s_cmp_lt_i32 s59, 6
	s_cselect_b32 s2, 0, 32
	v_or_b32_e32 v162, 16, v164
	s_cselect_b32 s24, s52, 0x47b1c000
	s_cselect_b32 s22, s53, 0x800
	s_cselect_b32 s23, 0, -6
	s_add_u32 s2, s44, s2
	v_ashrrev_i32_e32 v165, 31, v164
	v_ashrrev_i32_e32 v163, 31, v162
	s_addc_u32 s3, s45, 0
	v_lshlrev_b64 v[132:133], 6, v[164:165]
	v_lshlrev_b64 v[150:151], 6, v[162:163]
	s_barrier
	s_nop 7
	s_nop 7
	s_nop 7
	v_lshl_add_u64 v[132:133], s[2:3], 0, v[132:133]
	v_lshl_add_u64 v[150:151], s[2:3], 0, v[150:151]
	global_load_dwordx4 v[180:183], v[132:133], off
	s_nop 0
	global_load_dwordx4 v[132:135], v[132:133], off offset:16
	s_nop 0
	global_load_dwordx4 v[184:187], v[150:151], off
	global_load_dwordx4 v[188:191], v[150:151], off offset:16
	v_or_b32_e32 v160, 32, v164
	v_ashrrev_i32_e32 v161, 31, v160
	v_lshlrev_b64 v[150:151], 6, v[160:161]
	v_or_b32_e32 v158, 48, v164
	v_lshl_add_u64 v[150:151], s[2:3], 0, v[150:151]
	v_ashrrev_i32_e32 v159, 31, v158
	global_load_dwordx4 v[192:195], v[150:151], off
	global_load_dwordx4 v[196:199], v[150:151], off offset:16
	v_lshlrev_b64 v[150:151], 6, v[158:159]
	v_lshl_add_u64 v[150:151], s[2:3], 0, v[150:151]
	global_load_dwordx4 v[200:203], v[150:151], off
	global_load_dwordx4 v[204:207], v[150:151], off offset:16
	v_add_u32_e32 v156, 0x80, v164
	v_add_u32_e32 v152, 0xa0, v164
	v_add_u32_e32 v150, 0xb0, v164
	v_add_u32_e32 v154, 0x90, v164
	v_ashrrev_i32_e32 v157, 31, v156
	v_ashrrev_i32_e32 v153, 31, v152
	v_ashrrev_i32_e32 v151, 31, v150
	v_ashrrev_i32_e32 v155, 31, v154
	v_lshlrev_b64 v[208:209], 6, v[156:157]
	v_lshlrev_b64 v[212:213], 6, v[152:153]
	v_lshlrev_b64 v[214:215], 6, v[150:151]
	v_lshlrev_b64 v[210:211], 6, v[154:155]
	v_lshl_add_u64 v[216:217], s[2:3], 0, v[208:209]
	v_lshl_add_u64 v[232:233], s[2:3], 0, v[212:213]
	v_lshl_add_u64 v[240:241], s[2:3], 0, v[214:215]
	v_lshl_add_u64 v[220:221], s[2:3], 0, v[210:211]
	global_load_dwordx4 v[208:211], v[216:217], off
	global_load_dwordx4 v[212:215], v[216:217], off offset:16
	s_nop 0
	global_load_dwordx4 v[216:219], v[220:221], off
	global_load_dwordx4 v[224:227], v[220:221], off offset:16
	global_load_dwordx4 v[228:231], v[232:233], off
	s_nop 0
	global_load_dwordx4 v[232:235], v[232:233], off offset:16
	s_nop 0
	global_load_dwordx4 v[236:239], v[240:241], off
	s_nop 0
	global_load_dwordx4 v[240:243], v[240:241], off offset:16
	s_mov_b32 s60, s56
	s_mov_b64 s[26:27], s[20:21]
	s_waitcnt vmcnt(0)
	v_mov_b32_e32 v220, v180
	v_mov_b32_e32 v221, v132
	v_mov_b32_e32 v132, v181
	v_mov_b32_e32 v180, v182
	v_mov_b32_e32 v181, v134
	v_mov_b32_e32 v134, v183
	v_mov_b32_e32 v182, v184
	v_mov_b32_e32 v183, v188
	v_mov_b32_e32 v188, v185
	v_mov_b32_e32 v184, v186
	v_mov_b32_e32 v185, v190
	v_mov_b32_e32 v190, v187
	v_pk_add_f32 v[132:133], v[220:221], v[132:133]
	v_pk_add_f32 v[134:135], v[180:181], v[134:135]
	v_pk_add_f32 v[180:181], v[182:183], v[188:189]
	v_pk_add_f32 v[182:183], v[184:185], v[190:191]
	v_pk_add_f32 v[132:133], v[132:133], v[134:135]
	v_pk_add_f32 v[134:135], v[180:181], v[182:183]
	v_mov_b32_e32 v181, v132
	v_mov_b32_e32 v180, v134
	v_mov_b32_e32 v132, v135
	v_pk_add_f32 v[132:133], v[180:181], v[132:133]
	v_mov_b32_e32 v186, v192
	v_pk_fma_f32 v[132:133], v[132:133], s[16:17], v[148:149] op_sel_hi:[1,0,0]
	v_mov_b32_e32 v187, v196
	v_mul_f32_e32 v134, 0x4b800000, v133
	v_mul_f32_e32 v135, 0x4b800000, v132
	v_cmp_gt_f32_e32 vcc, s54, v133
	v_cmp_gt_f32_e64 s[2:3], s54, v132
	v_mov_b32_e32 v196, v193
	v_cndmask_b32_e32 v133, v133, v134, vcc
	v_cndmask_b32_e64 v132, v132, v135, s[2:3]
	v_rsq_f32_e32 v134, v133
	v_rsq_f32_e32 v135, v132
	v_mov_b32_e32 v192, v194
	v_mov_b32_e32 v193, v198
	v_mul_f32_e32 v151, 0x45800000, v134
	v_mul_f32_e32 v153, 0x45800000, v135
	v_cndmask_b32_e32 v134, v134, v151, vcc
	v_cndmask_b32_e64 v135, v135, v153, s[2:3]
	v_mov_b32_e32 v198, v195
	v_pk_add_f32 v[132:133], v[186:187], v[196:197]
	v_mul_f32_e32 v180, 0x3c800000, v134
	v_mul_f32_e32 v182, 0x3c800000, v135
	v_pk_add_f32 v[134:135], v[192:193], v[198:199]
	v_mov_b32_e32 v184, v202
	v_pk_add_f32 v[132:133], v[132:133], v[134:135]
	v_mov_b32_e32 v134, v200
	v_mov_b32_e32 v135, v204
	v_mov_b32_e32 v204, v201
	v_mov_b32_e32 v185, v206
	v_mov_b32_e32 v206, v203
	v_pk_add_f32 v[134:135], v[134:135], v[204:205]
	v_pk_add_f32 v[184:185], v[184:185], v[206:207]
	v_mov_b32_e32 v186, v218
	v_pk_add_f32 v[134:135], v[134:135], v[184:185]
	v_mov_b32_e32 v185, v132
	v_mov_b32_e32 v184, v134
	v_mov_b32_e32 v132, v135
	v_pk_add_f32 v[132:133], v[184:185], v[132:133]
	v_mov_b32_e32 v135, v214
	v_pk_fma_f32 v[132:133], v[132:133], s[16:17], v[148:149] op_sel_hi:[1,0,0]
	v_mov_b32_e32 v214, v211
	v_mul_f32_e32 v134, 0x4b800000, v133
	v_cmp_gt_f32_e32 vcc, s54, v133
	v_cmp_gt_f32_e64 s[2:3], s54, v132
	v_mov_b32_e32 v187, v226
	v_cndmask_b32_e32 v133, v133, v134, vcc
	v_rsq_f32_e32 v133, v133
	v_mul_f32_e32 v134, 0x4b800000, v132
	v_cndmask_b32_e64 v132, v132, v134, s[2:3]
	v_rsq_f32_e32 v132, v132
	v_mul_f32_e32 v134, 0x45800000, v133
	v_cndmask_b32_e32 v133, v133, v134, vcc
	v_mul_f32_e32 v184, 0x3c800000, v133
	v_mul_f32_e32 v133, 0x45800000, v132
	v_cndmask_b32_e64 v132, v132, v133, s[2:3]
	v_mul_f32_e32 v172, 0x3c800000, v132
	v_mov_b32_e32 v132, v208
	v_mov_b32_e32 v133, v212
	v_mov_b32_e32 v212, v209
	v_mov_b32_e32 v134, v210
	v_pk_add_f32 v[132:133], v[132:133], v[212:213]
	v_pk_add_f32 v[134:135], v[134:135], v[214:215]
	v_mov_b32_e32 v226, v219
	v_pk_add_f32 v[132:133], v[132:133], v[134:135]
	v_mov_b32_e32 v134, v216
	v_mov_b32_e32 v135, v224
	v_mov_b32_e32 v224, v217
	v_pk_add_f32 v[134:135], v[134:135], v[224:225]
	v_pk_add_f32 v[186:187], v[186:187], v[226:227]
	v_pk_mul_f32 v[108:109], v[108:109], v[180:181] op_sel_hi:[1,0]
	v_pk_add_f32 v[134:135], v[134:135], v[186:187]
	v_mov_b32_e32 v187, v132
	v_mov_b32_e32 v186, v134
	v_mov_b32_e32 v132, v135
	v_pk_add_f32 v[132:133], v[186:187], v[132:133]
	v_mov_b32_e32 v135, v234
	v_pk_fma_f32 v[132:133], v[132:133], s[16:17], v[148:149] op_sel_hi:[1,0,0]
	v_mov_b32_e32 v234, v231
	v_mul_f32_e32 v134, 0x4b800000, v133
	v_cmp_gt_f32_e32 vcc, s54, v133
	v_cmp_gt_f32_e64 s[2:3], s54, v132
	v_mov_b32_e32 v186, v238
	v_cndmask_b32_e32 v133, v133, v134, vcc
	v_rsq_f32_e32 v133, v133
	v_mul_f32_e32 v134, 0x4b800000, v132
	v_cndmask_b32_e64 v132, v132, v134, s[2:3]
	v_rsq_f32_e32 v132, v132
	v_mul_f32_e32 v134, 0x45800000, v133
	v_cndmask_b32_e32 v133, v133, v134, vcc
	v_mul_f32_e32 v170, 0x3c800000, v133
	v_mul_f32_e32 v133, 0x45800000, v132
	v_cndmask_b32_e64 v132, v132, v133, s[2:3]
	v_mul_f32_e32 v168, 0x3c800000, v132
	v_mov_b32_e32 v132, v228
	v_mov_b32_e32 v133, v232
	v_mov_b32_e32 v232, v229
	v_mov_b32_e32 v134, v230
	v_pk_add_f32 v[132:133], v[132:133], v[232:233]
	v_pk_add_f32 v[134:135], v[134:135], v[234:235]
	v_mov_b32_e32 v187, v242
	v_pk_add_f32 v[132:133], v[132:133], v[134:135]
	v_mov_b32_e32 v134, v236
	v_mov_b32_e32 v135, v240
	v_mov_b32_e32 v240, v237
	v_mov_b32_e32 v242, v239
	v_pk_add_f32 v[134:135], v[134:135], v[240:241]
	v_pk_add_f32 v[186:187], v[186:187], v[242:243]
	v_pk_mul_f32 v[110:111], v[110:111], v[180:181] op_sel_hi:[1,0]
	v_pk_add_f32 v[134:135], v[134:135], v[186:187]
	v_mov_b32_e32 v187, v132
	v_mov_b32_e32 v186, v134
	v_mov_b32_e32 v132, v135
	v_pk_add_f32 v[132:133], v[186:187], v[132:133]
	v_cvt_pk_bf16_f32 v108, v108, v109
	v_cvt_pk_bf16_f32 v109, v110, v111
	v_pk_mul_f32 v[114:115], v[114:115], v[180:181] op_sel_hi:[1,0]
	v_pk_fma_f32 v[132:133], v[132:133], s[16:17], v[148:149] op_sel_hi:[1,0,0]
	v_pk_mul_f32 v[112:113], v[112:113], v[180:181] op_sel_hi:[1,0]
	v_mul_f32_e32 v134, 0x4b800000, v133
	v_cmp_gt_f32_e32 vcc, s54, v133
	v_cmp_gt_f32_e64 s[2:3], s54, v132
	v_cvt_pk_bf16_f32 v110, v112, v113
	v_cvt_pk_bf16_f32 v111, v114, v115
	v_pk_mul_f32 v[112:113], v[130:131], v[180:181] op_sel_hi:[1,0]
	v_cndmask_b32_e32 v133, v133, v134, vcc
	v_rsq_f32_e32 v133, v133
	v_mul_f32_e32 v134, 0x4b800000, v132
	v_cndmask_b32_e64 v132, v132, v134, s[2:3]
	v_rsq_f32_e32 v132, v132
	v_mul_f32_e32 v134, 0x45800000, v133
	v_cndmask_b32_e32 v133, v133, v134, vcc
	v_mul_f32_e32 v166, 0x3c800000, v133
	v_mul_f32_e32 v133, 0x45800000, v132
	v_cndmask_b32_e64 v132, v132, v133, s[2:3]
	s_add_u32 s2, s4, s24
	s_addc_u32 s3, s5, 0
	s_add_i32 s23, s23, s59
	v_lshl_or_b32 v134, s23, 8, v175
	v_ashrrev_i32_e32 v135, 31, v134
	v_lshl_add_u64 v[134:135], v[134:135], 1, s[2:3]
	v_mad_i64_i32 v[164:165], s[2:3], s22, v164, 0
	v_lshl_add_u64 v[164:165], v[164:165], 1, v[134:135]
	global_store_dwordx4 v[164:165], v[108:111], off
	v_pk_mul_f32 v[114:115], v[128:129], v[180:181] op_sel_hi:[1,0]
	v_pk_mul_f32 v[106:107], v[106:107], v[182:183] op_sel_hi:[1,0]
	v_pk_mul_f32 v[108:109], v[124:125], v[180:181] op_sel_hi:[1,0]
	v_pk_mul_f32 v[110:111], v[126:127], v[180:181] op_sel_hi:[1,0]
	v_cvt_pk_bf16_f32 v108, v108, v109
	v_pk_mul_f32 v[104:105], v[104:105], v[182:183] op_sel_hi:[1,0]
	v_cvt_pk_bf16_f32 v109, v110, v111
	v_cvt_pk_bf16_f32 v110, v114, v115
	v_cvt_pk_bf16_f32 v111, v112, v113
	global_store_dwordx4 v[164:165], v[108:111], off offset:256
	v_pk_mul_f32 v[82:83], v[82:83], v[184:185] op_sel_hi:[1,0]
	v_pk_mul_f32 v[80:81], v[80:81], v[184:185] op_sel_hi:[1,0]
	v_mad_i64_i32 v[108:109], s[2:3], s22, v162, 0
	v_lshl_add_u64 v[108:109], v[108:109], 1, v[134:135]
	v_pk_mul_f32 v[110:111], v[102:103], v[182:183] op_sel_hi:[1,0]
	v_pk_mul_f32 v[102:103], v[100:101], v[182:183] op_sel_hi:[1,0]
	v_cvt_pk_bf16_f32 v100, v104, v105
	v_cvt_pk_bf16_f32 v101, v106, v107
	v_pk_mul_f32 v[104:105], v[118:119], v[182:183] op_sel_hi:[1,0]
	v_cvt_pk_bf16_f32 v102, v102, v103
	v_cvt_pk_bf16_f32 v103, v110, v111
	global_store_dwordx4 v[108:109], v[100:103], off
	v_pk_mul_f32 v[106:107], v[116:117], v[182:183] op_sel_hi:[1,0]
	v_pk_mul_f32 v[50:51], v[50:51], v[172:173] op_sel_hi:[1,0]
	v_pk_mul_f32 v[100:101], v[120:121], v[182:183] op_sel_hi:[1,0]
	v_pk_mul_f32 v[102:103], v[122:123], v[182:183] op_sel_hi:[1,0]
	v_cvt_pk_bf16_f32 v100, v100, v101
	v_pk_mul_f32 v[48:49], v[48:49], v[172:173] op_sel_hi:[1,0]
	v_cvt_pk_bf16_f32 v101, v102, v103
	v_cvt_pk_bf16_f32 v102, v106, v107
	v_cvt_pk_bf16_f32 v103, v104, v105
	global_store_dwordx4 v[108:109], v[100:103], off offset:256
	v_pk_mul_f32 v[42:43], v[42:43], v[168:169] op_sel_hi:[1,0]
	v_pk_mul_f32 v[40:41], v[40:41], v[168:169] op_sel_hi:[1,0]
	v_mad_i64_i32 v[100:101], s[2:3], s22, v160, 0
	v_lshl_add_u64 v[100:101], v[100:101], 1, v[134:135]
	v_pk_mul_f32 v[102:103], v[78:79], v[184:185] op_sel_hi:[1,0]
	v_pk_mul_f32 v[78:79], v[76:77], v[184:185] op_sel_hi:[1,0]
	v_cvt_pk_bf16_f32 v76, v80, v81
	v_cvt_pk_bf16_f32 v77, v82, v83
	v_pk_mul_f32 v[80:81], v[94:95], v[184:185] op_sel_hi:[1,0]
	v_cvt_pk_bf16_f32 v78, v78, v79
	v_cvt_pk_bf16_f32 v79, v102, v103
	global_store_dwordx4 v[100:101], v[76:79], off
	v_pk_mul_f32 v[82:83], v[92:93], v[184:185] op_sel_hi:[1,0]
	v_pk_mul_f32 v[26:27], v[26:27], v[166:167] op_sel_hi:[1,0]
	v_pk_mul_f32 v[76:77], v[96:97], v[184:185] op_sel_hi:[1,0]
	v_pk_mul_f32 v[78:79], v[98:99], v[184:185] op_sel_hi:[1,0]
	v_cvt_pk_bf16_f32 v76, v76, v77
	v_pk_mul_f32 v[24:25], v[24:25], v[166:167] op_sel_hi:[1,0]
	v_cvt_pk_bf16_f32 v77, v78, v79
	v_cvt_pk_bf16_f32 v78, v82, v83
	v_cvt_pk_bf16_f32 v79, v80, v81
	global_store_dwordx4 v[100:101], v[76:79], off offset:256
	v_mul_f32_e32 v132, 0x3c800000, v132
	v_pk_mul_f32 v[10:11], v[10:11], v[132:133] op_sel_hi:[1,0]
	v_mad_i64_i32 v[76:77], s[2:3], s22, v158, 0
	v_lshl_add_u64 v[76:77], v[76:77], 1, v[134:135]
	v_pk_mul_f32 v[78:79], v[46:47], v[172:173] op_sel_hi:[1,0]
	v_pk_mul_f32 v[46:47], v[44:45], v[172:173] op_sel_hi:[1,0]
	v_cvt_pk_bf16_f32 v44, v48, v49
	v_cvt_pk_bf16_f32 v45, v50, v51
	v_pk_mul_f32 v[48:49], v[62:63], v[172:173] op_sel_hi:[1,0]
	v_cvt_pk_bf16_f32 v46, v46, v47
	v_cvt_pk_bf16_f32 v47, v78, v79
	global_store_dwordx4 v[76:77], v[44:47], off
	v_pk_mul_f32 v[50:51], v[60:61], v[172:173] op_sel_hi:[1,0]
	v_pk_mul_f32 v[60:61], v[68:69], v[170:171] op_sel_hi:[1,0]
	v_pk_mul_f32 v[44:45], v[64:65], v[172:173] op_sel_hi:[1,0]
	v_pk_mul_f32 v[46:47], v[66:67], v[172:173] op_sel_hi:[1,0]
	v_cvt_pk_bf16_f32 v44, v44, v45
	v_pk_mul_f32 v[8:9], v[8:9], v[132:133] op_sel_hi:[1,0]
	v_cvt_pk_bf16_f32 v45, v46, v47
	v_cvt_pk_bf16_f32 v46, v50, v51
	v_cvt_pk_bf16_f32 v47, v48, v49
	global_store_dwordx4 v[76:77], v[44:47], off offset:256
	v_pk_mul_f32 v[50:51], v[70:71], v[170:171] op_sel_hi:[1,0]
	s_add_i32 s49, s49, s17
	v_mad_i64_i32 v[44:45], s[2:3], s22, v156, 0
	v_lshl_add_u64 v[48:49], v[44:45], 1, v[134:135]
	v_pk_mul_f32 v[46:47], v[74:75], v[170:171] op_sel_hi:[1,0]
	v_pk_mul_f32 v[44:45], v[72:73], v[170:171] op_sel_hi:[1,0]
	s_andn2_b64 vcc, exec, s[0:1]
	v_cvt_pk_bf16_f32 v44, v44, v45
	v_cvt_pk_bf16_f32 v45, v46, v47
	v_cvt_pk_bf16_f32 v46, v60, v61
	v_cvt_pk_bf16_f32 v47, v50, v51
	global_store_dwordx4 v[48:49], v[44:47], off
	v_pk_mul_f32 v[50:51], v[86:87], v[170:171] op_sel_hi:[1,0]
	v_pk_mul_f32 v[60:61], v[84:85], v[170:171] op_sel_hi:[1,0]
	v_pk_mul_f32 v[46:47], v[90:91], v[170:171] op_sel_hi:[1,0]
	v_pk_mul_f32 v[44:45], v[88:89], v[170:171] op_sel_hi:[1,0]
	s_mov_b32 s59, s55
	v_cvt_pk_bf16_f32 v44, v44, v45
	v_cvt_pk_bf16_f32 v45, v46, v47
	v_cvt_pk_bf16_f32 v46, v60, v61
	v_cvt_pk_bf16_f32 v47, v50, v51
	global_store_dwordx4 v[48:49], v[44:47], off offset:256
	s_nop 1
	v_mad_i64_i32 v[44:45], s[2:3], s22, v154, 0
	v_pk_mul_f32 v[46:47], v[38:39], v[168:169] op_sel_hi:[1,0]
	v_pk_mul_f32 v[38:39], v[36:37], v[168:169] op_sel_hi:[1,0]
	v_lshl_add_u64 v[44:45], v[44:45], 1, v[134:135]
	v_cvt_pk_bf16_f32 v36, v40, v41
	v_cvt_pk_bf16_f32 v37, v42, v43
	v_cvt_pk_bf16_f32 v38, v38, v39
	v_cvt_pk_bf16_f32 v39, v46, v47
	global_store_dwordx4 v[44:45], v[36:39], off
	v_pk_mul_f32 v[40:41], v[54:55], v[168:169] op_sel_hi:[1,0]
	v_pk_mul_f32 v[42:43], v[52:53], v[168:169] op_sel_hi:[1,0]
	v_pk_mul_f32 v[38:39], v[58:59], v[168:169] op_sel_hi:[1,0]
	v_pk_mul_f32 v[36:37], v[56:57], v[168:169] op_sel_hi:[1,0]
	s_nop 0
	v_cvt_pk_bf16_f32 v36, v36, v37
	v_cvt_pk_bf16_f32 v37, v38, v39
	v_cvt_pk_bf16_f32 v38, v42, v43
	v_cvt_pk_bf16_f32 v39, v40, v41
	global_store_dwordx4 v[44:45], v[36:39], off offset:256
	s_nop 1
	v_mad_i64_i32 v[36:37], s[2:3], s22, v152, 0
	v_pk_mul_f32 v[38:39], v[22:23], v[166:167] op_sel_hi:[1,0]
	v_pk_mul_f32 v[22:23], v[20:21], v[166:167] op_sel_hi:[1,0]
	v_lshl_add_u64 v[36:37], v[36:37], 1, v[134:135]
	v_cvt_pk_bf16_f32 v20, v24, v25
	v_cvt_pk_bf16_f32 v21, v26, v27
	v_cvt_pk_bf16_f32 v22, v22, v23
	v_cvt_pk_bf16_f32 v23, v38, v39
	global_store_dwordx4 v[36:37], v[20:23], off
	v_pk_mul_f32 v[24:25], v[30:31], v[166:167] op_sel_hi:[1,0]
	v_pk_mul_f32 v[26:27], v[28:29], v[166:167] op_sel_hi:[1,0]
	v_pk_mul_f32 v[22:23], v[34:35], v[166:167] op_sel_hi:[1,0]
	v_pk_mul_f32 v[20:21], v[32:33], v[166:167] op_sel_hi:[1,0]
	s_nop 0
	v_cvt_pk_bf16_f32 v20, v20, v21
	v_cvt_pk_bf16_f32 v21, v22, v23
	v_cvt_pk_bf16_f32 v22, v26, v27
	v_cvt_pk_bf16_f32 v23, v24, v25
	global_store_dwordx4 v[36:37], v[20:23], off offset:256
	s_nop 1
	v_mad_i64_i32 v[20:21], s[2:3], s22, v150, 0
	v_pk_mul_f32 v[22:23], v[6:7], v[132:133] op_sel_hi:[1,0]
	v_pk_mul_f32 v[6:7], v[4:5], v[132:133] op_sel_hi:[1,0]
	v_lshl_add_u64 v[20:21], v[20:21], 1, v[134:135]
	v_cvt_pk_bf16_f32 v4, v8, v9
	v_cvt_pk_bf16_f32 v5, v10, v11
	v_cvt_pk_bf16_f32 v6, v6, v7
	v_cvt_pk_bf16_f32 v7, v22, v23
	global_store_dwordx4 v[20:21], v[4:7], off
	s_mov_b64 s[22:23], s[18:19]
	v_pk_mul_f32 v[8:9], v[14:15], v[132:133] op_sel_hi:[1,0]
	v_pk_mul_f32 v[6:7], v[18:19], v[132:133] op_sel_hi:[1,0]
	v_pk_mul_f32 v[4:5], v[16:17], v[132:133] op_sel_hi:[1,0]
	v_pk_mul_f32 v[10:11], v[12:13], v[132:133] op_sel_hi:[1,0]
	v_cvt_pk_bf16_f32 v4, v4, v5
	v_cvt_pk_bf16_f32 v5, v6, v7
	s_nop 0
	v_cvt_pk_bf16_f32 v6, v10, v11
	v_cvt_pk_bf16_f32 v7, v8, v9
	global_store_dwordx4 v[20:21], v[4:7], off offset:256
	s_cbranch_vccz .LBB0_371

.LBB0_563:
	s_or_b64 exec, exec, s[2:3]
	v_mul_f32_e32 v0, v108, v0
	v_mul_f32_e32 v1, v108, v1
	v_mul_f32_e32 v27, v108, v27
	v_mul_f32_e32 v0, v0, v114
	v_mul_f32_e32 v1, v1, v113
	v_mul_f32_e32 v27, v27, v135
	v_med3_f32 v0, v0, s69, v203
	v_med3_f32 v1, v1, s69, v203
	v_mov_b32_e32 v135, v187
	v_cvt_pk_fp8_f32 v135, v0, v1
	v_mul_f32_e32 v2, v108, v2
	v_mul_f32_e32 v3, v108, v3
	v_mul_f32_e32 v2, v2, v112
	v_mul_f32_e32 v3, v3, v111
	v_med3_f32 v0, v2, s69, v203
	v_med3_f32 v1, v3, s69, v203
	v_mul_f32_e32 v26, v108, v26
	v_cvt_pk_fp8_f32 v135, v0, v1 op_sel:[0,0,1]
	v_max_f32_e32 v0, v106, v106
	v_max_f32_e32 v1, v107, v107
	v_mul_f32_e32 v26, v26, v136
	v_med3_f32 v0, v0, s69, v203
	v_med3_f32 v1, v1, s69, v203
	v_mov_b32_e32 v136, v187
	v_cvt_pk_fp8_f32 v136, v0, v1
	v_max_f32_e32 v2, v102, v102
	v_max_f32_e32 v1, v103, v103
	v_med3_f32 v0, v2, s69, v203
	v_med3_f32 v1, v1, s69, v203
	v_mul_f32_e32 v25, v108, v25
	v_cvt_pk_fp8_f32 v136, v0, v1 op_sel:[0,0,1]
	v_max_f32_e32 v0, v100, v100
	v_max_f32_e32 v1, v101, v101
	v_mul_f32_e32 v25, v25, v137
	v_med3_f32 v0, v0, s69, v203
	v_med3_f32 v1, v1, s69, v203
	v_mov_b32_e32 v137, v187
	v_cvt_pk_fp8_f32 v137, v0, v1
	v_max_f32_e32 v2, v98, v98
	v_max_f32_e32 v1, v99, v99
	v_med3_f32 v0, v2, s69, v203
	v_med3_f32 v1, v1, s69, v203
	v_mul_f32_e32 v24, v108, v24
	v_cvt_pk_fp8_f32 v137, v0, v1 op_sel:[0,0,1]
	v_max_f32_e32 v0, v96, v96
	v_max_f32_e32 v1, v97, v97
	v_mul_f32_e32 v24, v24, v138
	v_med3_f32 v0, v0, s69, v203
	v_med3_f32 v1, v1, s69, v203
	v_mov_b32_e32 v138, v187
	v_cvt_pk_fp8_f32 v138, v0, v1
	v_max_f32_e32 v2, v94, v94
	v_max_f32_e32 v1, v95, v95
	v_med3_f32 v0, v2, s69, v203
	v_med3_f32 v1, v1, s69, v203
	v_mul_f32_e32 v31, v108, v31
	v_cvt_pk_fp8_f32 v138, v0, v1 op_sel:[0,0,1]
	v_max_f32_e32 v0, v92, v92
	v_max_f32_e32 v1, v93, v93
	v_mul_f32_e32 v31, v31, v139
	v_med3_f32 v0, v0, s69, v203
	v_med3_f32 v1, v1, s69, v203
	v_mov_b32_e32 v139, v187
	v_cvt_pk_fp8_f32 v139, v0, v1
	v_max_f32_e32 v2, v90, v90
	v_max_f32_e32 v1, v91, v91
	v_med3_f32 v0, v2, s69, v203
	v_med3_f32 v1, v1, s69, v203
	v_mul_f32_e32 v30, v108, v30
	v_cvt_pk_fp8_f32 v139, v0, v1 op_sel:[0,0,1]
	v_max_f32_e32 v0, v88, v88
	v_max_f32_e32 v1, v89, v89
	v_mul_f32_e32 v30, v30, v140
	v_med3_f32 v0, v0, s69, v203
	v_med3_f32 v1, v1, s69, v203
	v_mov_b32_e32 v140, v187
	v_cvt_pk_fp8_f32 v140, v0, v1
	v_max_f32_e32 v2, v86, v86
	v_max_f32_e32 v1, v87, v87
	v_med3_f32 v0, v2, s69, v203
	v_med3_f32 v1, v1, s69, v203
	v_mul_f32_e32 v29, v108, v29
	v_cvt_pk_fp8_f32 v140, v0, v1 op_sel:[0,0,1]
	v_max_f32_e32 v0, v84, v84
	v_max_f32_e32 v1, v85, v85
	v_mul_f32_e32 v29, v29, v141
	v_med3_f32 v0, v0, s69, v203
	v_med3_f32 v1, v1, s69, v203
	v_mov_b32_e32 v141, v187
	v_cvt_pk_fp8_f32 v141, v0, v1
	v_max_f32_e32 v2, v82, v82
	v_max_f32_e32 v1, v83, v83
	v_med3_f32 v0, v2, s69, v203
	v_med3_f32 v1, v1, s69, v203
	v_mul_f32_e32 v28, v108, v28
	v_cvt_pk_fp8_f32 v141, v0, v1 op_sel:[0,0,1]
	v_max_f32_e32 v0, v80, v80
	v_max_f32_e32 v1, v81, v81
	v_mul_f32_e32 v28, v28, v142
	v_med3_f32 v0, v0, s69, v203
	v_med3_f32 v1, v1, s69, v203
	v_mov_b32_e32 v142, v187
	v_cvt_pk_fp8_f32 v142, v0, v1
	v_mul_f32_e32 v4, v108, v4
	v_mul_f32_e32 v5, v108, v5
	v_mul_f32_e32 v60, v60, v108
	v_mul_f32_e32 v61, v61, v108
	v_mul_f32_e32 v56, v56, v108
	v_mul_f32_e32 v57, v57, v108
	v_mul_f32_e32 v52, v52, v108
	v_mul_f32_e32 v53, v108, v53
	v_mul_f32_e32 v48, v108, v48
	v_mul_f32_e32 v49, v108, v49
	v_mul_f32_e32 v44, v108, v44
	v_mul_f32_e32 v45, v108, v45
	v_mul_f32_e32 v40, v108, v40
	v_mul_f32_e32 v41, v108, v41
	v_mul_f32_e32 v36, v108, v36
	v_mul_f32_e32 v37, v108, v37
	v_mul_f32_e32 v32, v108, v32
	v_mul_f32_e32 v33, v108, v33
	v_mul_f32_e32 v20, v108, v20
	v_mul_f32_e32 v4, v4, v118
	v_mul_f32_e32 v5, v5, v117
	v_max_f32_e32 v2, v78, v78
	v_max_f32_e32 v1, v79, v79
	v_mul_f32_e32 v60, v60, v182
	v_mul_f32_e32 v61, v61, v181
	v_mul_f32_e32 v56, v56, v178
	v_mul_f32_e32 v57, v57, v177
	v_mul_f32_e32 v52, v52, v174
	v_mul_f32_e32 v53, v53, v173
	v_mul_f32_e32 v48, v48, v162
	v_mul_f32_e32 v49, v49, v161
	v_mul_f32_e32 v44, v44, v158
	v_mul_f32_e32 v45, v45, v157
	v_mul_f32_e32 v40, v40, v154
	v_mul_f32_e32 v41, v41, v153
	v_mul_f32_e32 v36, v36, v150
	v_mul_f32_e32 v37, v37, v149
	v_mul_f32_e32 v32, v32, v146
	v_mul_f32_e32 v33, v33, v145
	v_mul_f32_e32 v20, v20, v134
	v_mul_f32_e32 v19, v108, v19
	v_mul_f32_e32 v12, v108, v12
	v_mul_f32_e32 v13, v108, v13
	v_mul_f32_e32 v14, v108, v14
	v_mul_f32_e32 v15, v108, v15
	v_mul_f32_e32 v8, v108, v8
	v_mul_f32_e32 v9, v108, v9
	v_mul_f32_e32 v10, v108, v10
	v_med3_f32 v4, v4, s69, v203
	v_med3_f32 v5, v5, s69, v203
	v_mov_b32_e32 v134, v187
	v_med3_f32 v0, v2, s69, v203
	v_med3_f32 v1, v1, s69, v203
	v_mul_f32_e32 v35, v108, v35
	v_mul_f32_e32 v21, v108, v21
	v_mul_f32_e32 v19, v19, v127
	v_mul_f32_e32 v12, v12, v126
	v_mul_f32_e32 v13, v13, v125
	v_mul_f32_e32 v14, v14, v124
	v_mul_f32_e32 v15, v15, v123
	v_mul_f32_e32 v8, v8, v122
	v_mul_f32_e32 v9, v9, v121
	v_mul_f32_e32 v10, v10, v120
	v_med3_f32 v60, v60, s69, v203
	v_med3_f32 v61, v61, s69, v203
	v_mov_b32_e32 v120, v187
	v_med3_f32 v56, v56, s69, v203
	v_med3_f32 v57, v57, s69, v203
	v_mov_b32_e32 v121, v187
	v_med3_f32 v52, v52, s69, v203
	v_med3_f32 v53, v53, s69, v203
	v_mov_b32_e32 v122, v187
	v_med3_f32 v48, v48, s69, v203
	v_med3_f32 v49, v49, s69, v203
	v_mov_b32_e32 v123, v187
	v_med3_f32 v44, v44, s69, v203
	v_med3_f32 v45, v45, s69, v203
	v_mov_b32_e32 v124, v187
	v_med3_f32 v40, v40, s69, v203
	v_med3_f32 v41, v41, s69, v203
	v_mov_b32_e32 v125, v187
	v_med3_f32 v36, v36, s69, v203
	v_med3_f32 v37, v37, s69, v203
	v_mov_b32_e32 v126, v187
	v_med3_f32 v32, v32, s69, v203
	v_med3_f32 v33, v33, s69, v203
	v_mov_b32_e32 v127, v187
	v_cvt_pk_fp8_f32 v134, v4, v5
	v_cvt_pk_fp8_f32 v142, v0, v1 op_sel:[0,0,1]
	v_max_f32_e32 v0, v76, v76
	v_max_f32_e32 v1, v77, v77
	v_mul_f32_e32 v35, v35, v143
	v_mul_f32_e32 v21, v21, v133
	v_mul_f32_e32 v6, v108, v6
	v_mul_f32_e32 v7, v108, v7
	v_cvt_pk_fp8_f32 v120, v60, v61
	v_cvt_pk_fp8_f32 v121, v56, v57
	v_cvt_pk_fp8_f32 v122, v52, v53
	v_cvt_pk_fp8_f32 v123, v48, v49
	v_cvt_pk_fp8_f32 v124, v44, v45
	v_cvt_pk_fp8_f32 v125, v40, v41
	v_cvt_pk_fp8_f32 v126, v36, v37
	v_cvt_pk_fp8_f32 v127, v32, v33
	v_med3_f32 v8, v8, s69, v203
	v_med3_f32 v9, v9, s69, v203
	v_mov_b32_e32 v133, v187
	v_med3_f32 v0, v0, s69, v203
	v_med3_f32 v1, v1, s69, v203
	v_mov_b32_e32 v143, v187
	v_mul_f32_e32 v62, v62, v108
	v_mul_f32_e32 v63, v63, v108
	v_mul_f32_e32 v58, v58, v108
	v_mul_f32_e32 v59, v59, v108
	v_mul_f32_e32 v54, v108, v54
	v_mul_f32_e32 v55, v108, v55
	v_mul_f32_e32 v50, v108, v50
	v_mul_f32_e32 v51, v108, v51
	v_mul_f32_e32 v46, v108, v46
	v_mul_f32_e32 v47, v108, v47
	v_mul_f32_e32 v42, v108, v42
	v_mul_f32_e32 v43, v108, v43
	v_mul_f32_e32 v38, v108, v38
	v_mul_f32_e32 v39, v108, v39
	v_mul_f32_e32 v34, v108, v34
	v_mul_f32_e32 v16, v108, v16
	v_mul_f32_e32 v17, v108, v17
	v_mul_f32_e32 v6, v6, v116
	v_mul_f32_e32 v7, v7, v115
	v_cvt_pk_fp8_f32 v133, v8, v9
	v_cvt_pk_fp8_f32 v143, v0, v1
	v_mul_u32_u24_e32 v0, 0xd0, v186
	s_and_b32 s3, s17, 0x3fffffc0
	v_mul_f32_e32 v62, v62, v180
	v_mul_f32_e32 v63, v63, v179
	v_mul_f32_e32 v58, v58, v176
	v_mul_f32_e32 v59, v59, v175
	v_mul_f32_e32 v54, v54, v172
	v_mul_f32_e32 v55, v55, v163
	v_mul_f32_e32 v50, v50, v160
	v_mul_f32_e32 v51, v51, v159
	v_mul_f32_e32 v46, v46, v156
	v_mul_f32_e32 v47, v47, v155
	v_mul_f32_e32 v42, v42, v152
	v_mul_f32_e32 v43, v43, v151
	v_mul_f32_e32 v38, v38, v148
	v_mul_f32_e32 v39, v39, v147
	v_mul_f32_e32 v34, v34, v144
	v_mul_f32_e32 v23, v108, v23
	v_mul_f32_e32 v16, v16, v130
	v_mul_f32_e32 v17, v17, v129
	v_mul_f32_e32 v18, v108, v18
	v_mul_f32_e32 v11, v108, v11
	v_med3_f32 v6, v6, s69, v203
	v_med3_f32 v7, v7, s69, v203
	v_add3_u32 v216, 0, v0, v72
	s_lshl_b32 s3, s3, 2
	s_ashr_i32 s18, s18, 6
	v_mul_f32_e32 v23, v23, v131
	v_mul_f32_e32 v18, v18, v128
	v_mul_f32_e32 v11, v11, v119
	v_med3_f32 v62, v62, s69, v203
	v_med3_f32 v63, v63, s69, v203
	v_med3_f32 v56, v58, s69, v203
	v_med3_f32 v57, v59, s69, v203
	v_med3_f32 v54, v54, s69, v203
	v_med3_f32 v55, v55, s69, v203
	v_med3_f32 v48, v50, s69, v203
	v_med3_f32 v49, v51, s69, v203
	v_med3_f32 v46, v46, s69, v203
	v_med3_f32 v47, v47, s69, v203
	v_med3_f32 v40, v42, s69, v203
	v_med3_f32 v41, v43, s69, v203
	v_med3_f32 v38, v38, s69, v203
	v_med3_f32 v39, v39, s69, v203
	v_med3_f32 v32, v34, s69, v203
	v_med3_f32 v33, v35, s69, v203
	v_med3_f32 v28, v28, s69, v203
	v_med3_f32 v29, v29, s69, v203
	v_mov_b32_e32 v128, v187
	v_med3_f32 v24, v24, s69, v203
	v_med3_f32 v25, v25, s69, v203
	v_mov_b32_e32 v129, v187
	v_med3_f32 v20, v20, s69, v203
	v_med3_f32 v21, v21, s69, v203
	v_mov_b32_e32 v130, v187
	v_med3_f32 v16, v16, s69, v203
	v_med3_f32 v17, v17, s69, v203
	v_mov_b32_e32 v131, v187
	v_cvt_pk_fp8_f32 v134, v6, v7 op_sel:[0,0,1]
	ds_read_b128 v[0:3], v216
	ds_read_b128 v[4:7], v216 offset:16
	s_add_i32 s3, s3, 0
	s_ashr_i32 s19, s18, 31
	s_lshl_b32 s2, s74, 1
	v_cvt_pk_fp8_f32 v120, v62, v63 op_sel:[0,0,1]
	v_cvt_pk_fp8_f32 v121, v56, v57 op_sel:[0,0,1]
	v_cvt_pk_fp8_f32 v122, v54, v55 op_sel:[0,0,1]
	v_cvt_pk_fp8_f32 v123, v48, v49 op_sel:[0,0,1]
	v_cvt_pk_fp8_f32 v124, v46, v47 op_sel:[0,0,1]
	v_cvt_pk_fp8_f32 v125, v40, v41 op_sel:[0,0,1]
	v_cvt_pk_fp8_f32 v126, v38, v39 op_sel:[0,0,1]
	v_cvt_pk_fp8_f32 v127, v32, v33 op_sel:[0,0,1]
	v_cvt_pk_fp8_f32 v128, v28, v29
	v_cvt_pk_fp8_f32 v129, v24, v25
	v_cvt_pk_fp8_f32 v130, v20, v21
	v_cvt_pk_fp8_f32 v131, v16, v17
	v_med3_f32 v8, v10, s69, v203
	v_med3_f32 v9, v11, s69, v203
	s_add_i32 s79, s3, 0x18000
	s_lshl_b64 s[18:19], s[18:19], 16
	v_mul_f32_e32 v22, v108, v22
	v_cvt_pk_fp8_f32 v133, v8, v9 op_sel:[0,0,1]
	v_max_f32_e32 v8, v74, v74
	v_max_f32_e32 v9, v75, v75
	s_add_u32 s18, s44, s18
	v_mul_f32_e32 v22, v22, v132
	v_med3_f32 v8, v8, s69, v203
	v_med3_f32 v9, v9, s69, v203
	s_addc_u32 s19, s45, s19
	v_med3_f32 v30, v30, s69, v203
	v_med3_f32 v31, v31, s69, v203
	v_med3_f32 v24, v26, s69, v203
	v_med3_f32 v25, v27, s69, v203
	v_med3_f32 v22, v22, s69, v203
	v_med3_f32 v23, v23, s69, v203
	v_med3_f32 v16, v18, s69, v203
	v_med3_f32 v17, v19, s69, v203
	v_cvt_pk_fp8_f32 v143, v8, v9 op_sel:[0,0,1]
	v_lshl_add_u64 v[8:9], s[18:19], 0, v[104:105]
	v_cvt_pk_fp8_f32 v128, v30, v31 op_sel:[0,0,1]
	v_cvt_pk_fp8_f32 v129, v24, v25 op_sel:[0,0,1]
	v_cvt_pk_fp8_f32 v130, v22, v23 op_sel:[0,0,1]
	v_cvt_pk_fp8_f32 v131, v16, v17 op_sel:[0,0,1]
	s_waitcnt lgkmcnt(0)
	v_mfma_f32_32x32x64_f8f6f4 v[16:31], v[0:7], v[120:127], 0
	ds_read_b128 v[0:3], v216 offset:64
	ds_read_b128 v[4:7], v216 offset:80
	global_load_dwordx4 v[172:175], v[8:9], off
	v_med3_f32 v12, v12, s69, v203
	v_med3_f32 v13, v13, s69, v203
	v_mov_b32_e32 v132, v187
	v_cvt_pk_fp8_f32 v132, v12, v13
	v_med3_f32 v14, v14, s69, v203
	v_med3_f32 v15, v15, s69, v203
	s_mov_b32 s17, s16
	v_cvt_pk_fp8_f32 v132, v14, v15 op_sel:[0,0,1]
	s_mov_b32 s18, s16
	s_mov_b32 s19, s16
	s_mov_b32 s20, s16
	s_mov_b32 s21, s16
	s_mov_b32 s22, s16
	s_waitcnt lgkmcnt(0)
	v_mfma_f32_32x32x64_f8f6f4 v[16:31], v[0:7], v[128:135], v[16:31]
	v_sub_u32_e32 v0, v216, v73
	ds_read_b128 v[32:35], v0 offset:128
	ds_read_b128 v[36:39], v0 offset:160
	s_mov_b32 s23, s16
	s_mov_b32 s24, s16
	s_mov_b32 s25, s16
	s_mov_b32 s26, s16
	s_mov_b32 s27, s16
	s_mov_b32 s28, s16
	s_mov_b32 s29, s16
	s_mov_b32 s30, s16
	s_mov_b32 s31, s16
	v_mov_b64_e32 v[0:1], s[16:17]
	v_and_b32_e32 v64, 63, v110
	v_mov_b64_e32 v[14:15], s[30:31]
	v_mov_b64_e32 v[2:3], s[18:19]
	s_waitcnt lgkmcnt(0)
	v_mfma_f32_32x32x64_f8f6f4 v[16:31], v[32:39], v[136:143], v[16:31]
	v_mov_b64_e32 v[4:5], s[20:21]
	v_mov_b64_e32 v[6:7], s[22:23]
	v_mov_b64_e32 v[8:9], s[24:25]
	v_mov_b64_e32 v[10:11], s[26:27]
	v_mov_b64_e32 v[12:13], s[28:29]
	v_sub_u32_e32 v217, 0, v73
	v_mov_b32_e32 v112, 0x38383838
	v_mov_b64_e32 v[62:63], v[14:15]
	s_mov_b32 s78, 2
	v_lshl_add_u32 v209, v186, 2, s79
	v_mov_b32_e32 v113, v112
	v_mov_b32_e32 v114, v112
	v_mov_b32_e32 v115, v112
	v_mov_b32_e32 v116, v112
	s_nop 5
	v_max_f32_e32 v32, v16, v17
	v_max3_f32 v32, v32, v18, v19
	v_max3_f32 v32, v32, v20, v21
	v_max3_f32 v32, v32, v22, v23
	v_max3_f32 v32, v32, v24, v25
	v_max3_f32 v32, v32, v26, v27
	v_max3_f32 v32, v32, v28, v29
	v_max3_f32 v32, v32, v30, v31
	v_mov_b32_e32 v33, v32
	s_nop 1
	v_permlane32_swap_b32_e32 v32, v33
	v_max_f32_e32 v32, v32, v33
	v_fmamk_f32 v33, v32, 0x3dd53b94, v201
	v_fmamk_f32 v32, v32, 0x3dd53b94, v202
	v_max_f32_e32 v32, 0xf149f2ca, v32
	v_cmp_ge_f32_e32 vcc, s70, v33
	v_sub_f32_e32 v33, 0xf149f2ca, v32
	s_cmp_eq_u64 vcc, exec
	v_exp_f32_e32 v33, v33
	s_cselect_b64 vcc, -1, 0
	v_cndmask_b32_e32 v192, v32, v204, vcc
	v_pk_fma_f32 v[178:179], v[16:17], s[40:41], v[192:193] op_sel_hi:[1,0,0] neg_lo:[0,0,1] neg_hi:[0,0,1]
	v_mul_u32_u24_e32 v16, 0x50, v186
	v_pk_fma_f32 v[152:153], v[30:31], s[40:41], v[192:193] op_sel_hi:[1,0,0] neg_lo:[0,0,1] neg_hi:[0,0,1]
	v_pk_fma_f32 v[154:155], v[28:29], s[40:41], v[192:193] op_sel_hi:[1,0,0] neg_lo:[0,0,1] neg_hi:[0,0,1]
	v_pk_fma_f32 v[156:157], v[26:27], s[40:41], v[192:193] op_sel_hi:[1,0,0] neg_lo:[0,0,1] neg_hi:[0,0,1]
	v_pk_fma_f32 v[158:159], v[24:25], s[40:41], v[192:193] op_sel_hi:[1,0,0] neg_lo:[0,0,1] neg_hi:[0,0,1]
	v_pk_fma_f32 v[160:161], v[22:23], s[40:41], v[192:193] op_sel_hi:[1,0,0] neg_lo:[0,0,1] neg_hi:[0,0,1]
	v_pk_fma_f32 v[162:163], v[20:21], s[40:41], v[192:193] op_sel_hi:[1,0,0] neg_lo:[0,0,1] neg_hi:[0,0,1]
	v_pk_fma_f32 v[176:177], v[18:19], s[40:41], v[192:193] op_sel_hi:[1,0,0] neg_lo:[0,0,1] neg_hi:[0,0,1]
	v_cndmask_b32_e64 v88, v33, 1.0, vcc
	v_add3_u32 v211, s67, v16, v72
	s_add_i32 s17, s2, -2
	v_cmp_gt_u32_e64 s[2:3], 32, v64
	v_mov_b64_e32 v[30:31], v[14:15]
	v_mov_b64_e32 v[46:47], v[14:15]
	v_mov_b64_e32 v[78:79], v[14:15]
	v_mov_b32_e32 v117, v112
	v_mov_b32_e32 v118, v112
	v_mov_b32_e32 v119, v112
	v_lshlrev_b32_e32 v208, 2, v109
	v_mul_lo_u32 v215, v213, s65
	v_lshl_add_u32 v214, v109, 4, s79
	s_add_i32 s20, s74, -1
	v_lshl_add_u64 v[194:195], s[4:5], 0, v[190:191]
	v_lshl_add_u64 v[196:197], s[4:5], 0, v[188:189]
	v_lshl_add_u64 v[198:199], s[44:45], 0, v[104:105]
	s_mov_b32 s21, 0
	s_movk_i32 s22, 0x80
	v_mov_b64_e32 v[28:29], v[12:13]
	v_mov_b64_e32 v[26:27], v[10:11]
	v_mov_b64_e32 v[24:25], v[8:9]
	v_mov_b64_e32 v[22:23], v[6:7]
	v_mov_b64_e32 v[20:21], v[4:5]
	v_mov_b64_e32 v[18:19], v[2:3]
	v_mov_b64_e32 v[16:17], v[0:1]
	v_mov_b64_e32 v[44:45], v[12:13]
	v_mov_b64_e32 v[42:43], v[10:11]
	v_mov_b64_e32 v[40:41], v[8:9]
	v_mov_b64_e32 v[38:39], v[6:7]
	v_mov_b64_e32 v[36:37], v[4:5]
	v_mov_b64_e32 v[34:35], v[2:3]
	v_mov_b64_e32 v[32:33], v[0:1]
	v_mov_b64_e32 v[60:61], v[12:13]
	v_mov_b64_e32 v[58:59], v[10:11]
	v_mov_b64_e32 v[56:57], v[8:9]
	v_mov_b64_e32 v[54:55], v[6:7]
	v_mov_b64_e32 v[52:53], v[4:5]
	v_mov_b64_e32 v[50:51], v[2:3]
	v_mov_b64_e32 v[48:49], v[0:1]
	v_mov_b64_e32 v[76:77], v[12:13]
	v_mov_b64_e32 v[74:75], v[10:11]
	v_mov_b64_e32 v[72:73], v[8:9]
	v_mov_b64_e32 v[70:71], v[6:7]
	v_mov_b64_e32 v[68:69], v[4:5]
	v_mov_b64_e32 v[66:67], v[2:3]
	v_mov_b64_e32 v[64:65], v[0:1]
	s_branch .LBB0_566

.LBB0_565:
	s_waitcnt lgkmcnt(4)
	v_mfma_f32_32x32x64_f8f6f4 v[96:111], v[96:103], v[120:127], 0
	v_cndmask_b32_e64 v176, v189, v192, s[4:5]
	v_fma_f32 v80, v80, s40, -v176
	v_fma_f32 v81, v81, s40, -v176
	v_fma_f32 v84, v84, s40, -v176
	v_fma_f32 v85, v85, s40, -v176
	v_fma_f32 v88, v88, s40, -v176
	v_fma_f32 v89, v89, s40, -v176
	v_fma_f32 v92, v92, s40, -v176
	v_fma_f32 v93, v93, s40, -v176
	v_exp_f32_e32 v80, v80
	v_exp_f32_e32 v81, v81
	v_exp_f32_e32 v84, v84
	v_exp_f32_e32 v85, v85
	v_exp_f32_e32 v88, v88
	v_exp_f32_e32 v89, v89
	s_waitcnt lgkmcnt(2)
	v_mfma_f32_32x32x64_f8f6f4 v[96:111], v[156:163], v[128:135], v[96:111]
	v_exp_f32_e32 v92, v92
	v_exp_f32_e32 v93, v93
	v_fma_f32 v82, v82, s40, -v176
	v_fma_f32 v83, v83, s40, -v176
	v_fma_f32 v86, v86, s40, -v176
	v_fma_f32 v87, v87, s40, -v176
	v_fma_f32 v90, v90, s40, -v176
	v_fma_f32 v91, v91, s40, -v176
	v_fma_f32 v94, v94, s40, -v176
	v_fma_f32 v95, v95, s40, -v176
	v_exp_f32_e32 v82, v82
	v_exp_f32_e32 v83, v83
	v_exp_f32_e32 v86, v86
	v_exp_f32_e32 v87, v87
	v_exp_f32_e32 v90, v90
	s_waitcnt lgkmcnt(0)
	v_mfma_f32_32x32x64_f8f6f4 v[96:111], v[148:155], v[136:143], v[96:111]
	v_lshl_add_u32 v240, s23, 14, v211
	ds_read_b128 v[224:227], v240
	ds_read_b128 v[228:231], v240 offset:16
	ds_read_b128 v[232:235], v240 offset:2560
	ds_read_b128 v[236:239], v240 offset:2576
	v_exp_f32_e32 v91, v91
	v_exp_f32_e32 v94, v94
	v_exp_f32_e32 v95, v95
	v_cvt_pk_fp8_f32 v148, v80, v81
	v_cvt_pk_fp8_f32 v149, v84, v85
	v_cvt_pk_fp8_f32 v150, v88, v89
	v_cvt_pk_fp8_f32 v151, v92, v93
	v_cvt_pk_fp8_f32 v148, v82, v83 op_sel:[0,0,1]
	v_cvt_pk_fp8_f32 v149, v86, v87 op_sel:[0,0,1]
	v_cvt_pk_fp8_f32 v150, v90, v91 op_sel:[0,0,1]
	v_cvt_pk_fp8_f32 v151, v94, v95 op_sel:[0,0,1]
	s_nop 0
	s_waitcnt lgkmcnt(2)
	v_mfma_f32_32x32x64_f8f6f4 v[48:63], v[144:151], v[224:231], v[48:63]
	ds_read_b128 v[80:83], v240 offset:5120
	ds_read_b128 v[84:87], v240 offset:5136
	ds_read_b128 v[152:155], v240 offset:7680
	ds_read_b128 v[156:159], v240 offset:7696
	s_waitcnt lgkmcnt(4)
	v_mfma_f32_32x32x64_f8f6f4 v[32:47], v[144:151], v[232:239], v[32:47]
	v_max_f32_e32 v88, v96, v97
	v_max3_f32 v88, v88, v98, v99
	v_max3_f32 v88, v88, v100, v101
	v_max3_f32 v88, v88, v102, v103
	v_max3_f32 v88, v88, v104, v105
	v_max3_f32 v88, v88, v106, v107
	s_waitcnt lgkmcnt(2)
	v_mfma_f32_32x32x64_f8f6f4 v[16:31], v[144:151], v[80:87], v[16:31]
	v_max3_f32 v88, v88, v108, v109
	v_max3_f32 v88, v88, v110, v111
	v_mov_b32_e32 v89, v88
	s_nop 1
	v_permlane32_swap_b32_e32 v88, v89
	v_max_f32_e32 v80, v88, v89
	v_fma_f32 v81, v80, s40, -v176
	v_cmp_ge_f32_e32 vcc, s70, v81
	s_waitcnt lgkmcnt(0)
	v_mfma_f32_32x32x64_f8f6f4 v[0:15], v[144:151], v[152:159], v[0:15]
	s_cmp_eq_u64 vcc, exec
	s_cbranch_scc0 .Lmla_rare_a0
	v_mov_b32_e32 v192, v176
	v_mov_b32_e32 v88, 1.0
.Lmla_back_a0:
	s_add_i32 s21, s21, 2
	s_add_i32 s78, s78, 1
	s_add_i32 s22, s22, 64
	v_fma_f32 v178, v96, s40, -v192
	v_fma_f32 v179, v97, s40, -v192
	v_fma_f32 v176, v98, s40, -v192
	v_fma_f32 v177, v99, s40, -v192
	v_fma_f32 v162, v100, s40, -v192
	v_fma_f32 v163, v101, s40, -v192
	v_fma_f32 v160, v102, s40, -v192
	v_fma_f32 v161, v103, s40, -v192
	v_fma_f32 v158, v104, s40, -v192
	v_fma_f32 v159, v105, s40, -v192
	v_fma_f32 v156, v106, s40, -v192
	v_fma_f32 v157, v107, s40, -v192
	v_fma_f32 v154, v108, s40, -v192
	v_fma_f32 v155, v109, s40, -v192
	v_fma_f32 v152, v110, s40, -v192
	v_fma_f32 v153, v111, s40, -v192
	v_mfma_f32_32x32x64_f8f6f4 v[64:79], v[144:151], v[112:119], v[64:79]
	s_cmp_ge_u32 s21, s17
	s_barrier
	s_cbranch_scc1 .LBB0_580

.LBB0_570:
	s_waitcnt lgkmcnt(4)
	v_mfma_f32_32x32x64_f8f6f4 v[80:95], v[80:87], v[120:127], 0
	s_mov_b64 s[4:5], exec
	s_cmp_ge_u32 s18, s20
	s_waitcnt lgkmcnt(2)
	v_mfma_f32_32x32x64_f8f6f4 v[80:95], v[104:111], v[128:135], v[80:95]
	s_waitcnt lgkmcnt(0)
	v_mfma_f32_32x32x64_f8f6f4 v[80:95], v[96:103], v[136:143], v[80:95]
	s_nop 15
	s_nop 3
	v_max_f32_e32 v96, v80, v81
	v_max3_f32 v96, v96, v82, v83
	v_max3_f32 v96, v96, v84, v85
	v_max3_f32 v96, v96, v86, v87
	v_max3_f32 v96, v96, v88, v89
	v_max3_f32 v96, v96, v90, v91
	v_max3_f32 v96, v96, v92, v93
	v_max3_f32 v96, v96, v94, v95
	v_mov_b32_e32 v97, v96
	s_nop 1
	v_permlane32_swap_b32_e32 v96, v97
	v_max_f32_e32 v96, v96, v97
	v_fma_f32 v97, v96, s40, -v192
	v_cmp_ge_f32_e32 vcc, s70, v97
	s_cbranch_scc1 .LBB0_577
	s_xor_b32 s25, s23, 1
	s_lshl_b32 s18, s25, 15
	s_add_i32 s26, s18, 0
	v_add3_u32 v97, s26, v212, v190
	s_waitcnt vmcnt(1)
	ds_write_b128 v97, v[168:171]
	s_and_saveexec_b64 s[18:19], s[0:1]
	v_add3_u32 v97, s26, v215, v188
	ds_write_b128 v97, v[164:167]
	s_or_b64 exec, exec, s[18:19]
	v_lshl_add_u32 v97, s25, 14, v207
	s_cmp_ge_u32 s78, s74
	s_waitcnt vmcnt(0)
	ds_write_b128 v97, v[172:175]
	s_cbranch_scc1 .LBB0_577
	s_cmp_lt_u32 s78, s77
	s_cselect_b32 s18, 0, s77
	s_cselect_b32 s19, s76, s75
	s_lshl_b32 s18, s18, 6
	s_sub_i32 s25, s19, s18
	s_add_i32 s25, s25, s22
	v_add_u32_e32 v97, s25, v210
	v_mad_i64_i32 v[98:99], s[18:19], v97, s64, v[194:195]
	global_load_dwordx4 v[168:171], v[98:99], off
	s_and_saveexec_b64 s[18:19], s[0:1]
	s_cbranch_execz .LBB0_576
	v_add_u32_e32 v97, s25, v213
	v_mad_i64_i32 v[98:99], s[26:27], v97, s64, v[196:197]
	global_load_dwordx4 v[164:167], v[98:99], off

.LBB0_584:
	s_waitcnt lgkmcnt(4)
	v_mfma_f32_32x32x64_f8f6f4 v[80:95], v[80:87], v[120:127], 0
	s_lshr_b32 s17, s17, 1
	s_add_i32 s17, s17, 1
	s_mov_b64 s[4:5], exec
	s_cmp_ge_u32 s17, s74
	s_waitcnt lgkmcnt(2)
	v_mfma_f32_32x32x64_f8f6f4 v[80:95], v[104:111], v[128:135], v[80:95]
	s_waitcnt lgkmcnt(0)
	v_mfma_f32_32x32x64_f8f6f4 v[80:95], v[96:103], v[136:143], v[80:95]
	s_nop 15
	s_nop 3
	v_max_f32_e32 v96, v80, v81
	v_max3_f32 v96, v96, v82, v83
	v_max3_f32 v96, v96, v84, v85
	v_max3_f32 v96, v96, v86, v87
	v_max3_f32 v96, v96, v88, v89
	v_max3_f32 v96, v96, v90, v91
	v_max3_f32 v96, v96, v92, v93
	v_max3_f32 v96, v96, v94, v95
	v_mov_b32_e32 v97, v96
	s_nop 1
	v_permlane32_swap_b32_e32 v96, v97
	v_max_f32_e32 v96, v96, v97
	v_fma_f32 v97, v96, s40, -v192
	v_cmp_ge_f32_e32 vcc, s70, v97
	s_cbranch_scc1 .LBB0_588
	s_waitcnt vmcnt(1)
	ds_write_b128 v206, v[168:171]
	s_and_saveexec_b64 s[18:19], s[0:1]
	v_add3_u32 v97, 0, v215, v188
	ds_write_b128 v97, v[164:167]
	s_or_b64 exec, exec, s[18:19]
	s_waitcnt vmcnt(0)
	ds_write_b128 v207, v[172:175]

.LBB0_592:
	v_cndmask_b32_e64 v104, v124, v192, s[0:1]
	v_fma_f32 v100, v80, s40, -v104
	v_fma_f32 v101, v81, s40, -v104
	v_fma_f32 v102, v82, s40, -v104
	v_fma_f32 v103, v83, s40, -v104
	v_fma_f32 v128, v84, s40, -v104
	v_fma_f32 v129, v85, s40, -v104
	v_fma_f32 v130, v86, s40, -v104
	v_fma_f32 v131, v87, s40, -v104
	v_fma_f32 v132, v88, s40, -v104
	v_fma_f32 v133, v89, s40, -v104
	v_fma_f32 v134, v90, s40, -v104
	v_fma_f32 v135, v91, s40, -v104
	v_fma_f32 v136, v92, s40, -v104
	v_fma_f32 v137, v93, s40, -v104
	v_fma_f32 v138, v94, s40, -v104
	v_fma_f32 v139, v95, s40, -v104
	ds_read_b128 v[120:123], v211 offset:16384
	ds_read_b128 v[124:127], v211 offset:16400
	ds_read_b128 v[104:107], v211 offset:18944
	ds_read_b128 v[108:111], v211 offset:18960
	s_waitcnt lgkmcnt(0)
	ds_read_b128 v[88:91], v211 offset:21504
	ds_read_b128 v[92:95], v211 offset:21520
	ds_read_b128 v[80:83], v211 offset:24064
	ds_read_b128 v[84:87], v211 offset:24080
	s_waitcnt lgkmcnt(0)
	s_waitcnt lgkmcnt(0)
	s_barrier
	s_and_saveexec_b64 s[0:1], s[2:3]
	ds_write_b32 v209, v187
	s_or_b64 exec, exec, s[0:1]
	v_exp_f32_e32 v140, v100
	v_exp_f32_e32 v101, v101
	v_exp_f32_e32 v141, v102
	v_exp_f32_e32 v142, v103
	v_exp_f32_e32 v102, v128
	v_exp_f32_e32 v103, v129
	v_exp_f32_e32 v128, v130
	v_exp_f32_e32 v129, v131
	v_exp_f32_e32 v130, v132
	v_exp_f32_e32 v131, v133
	v_exp_f32_e32 v132, v134
	v_exp_f32_e32 v133, v135
	v_exp_f32_e32 v134, v136
	v_exp_f32_e32 v135, v137
	v_mov_b32_e32 v100, v187
	v_cvt_pk_fp8_f32 v100, v140, v101
	v_mov_b32_e32 v101, v187
	v_cvt_pk_fp8_f32 v101, v102, v103
	v_mov_b32_e32 v102, v187
	v_mov_b32_e32 v103, v187
	v_exp_f32_e32 v136, v138
	v_exp_f32_e32 v137, v139
	v_cvt_pk_fp8_f32 v102, v130, v131
	v_cvt_pk_fp8_f32 v103, v134, v135
	v_cvt_pk_fp8_f32 v100, v141, v142 op_sel:[0,0,1]
	v_cvt_pk_fp8_f32 v101, v128, v129 op_sel:[0,0,1]
	v_cvt_pk_fp8_f32 v102, v132, v133 op_sel:[0,0,1]
	v_cvt_pk_fp8_f32 v103, v136, v137 op_sel:[0,0,1]
	s_waitcnt lgkmcnt(0)
	s_lshl_b32 s2, s73, 7
	s_mov_b64 s[0:1], -1
	v_mfma_f32_32x32x64_f8f6f4 v[64:79], v[96:103], v[112:119], v[64:79]
	v_add_u32_e32 v118, s72, v208
	s_andn2_b64 vcc, exec, s[42:43]
	v_ashrrev_i32_e32 v119, 31, v118
	v_add3_u32 v116, s72, 1, v208
	v_add3_u32 v114, s72, 2, v208
	v_add3_u32 v112, s72, 3, v208
	s_nop 13
	v_rcp_f32_e32 v130, v64
	v_mfma_f32_32x32x64_f8f6f4 v[48:63], v[96:103], v[120:127], v[48:63]
	v_rcp_f32_e32 v129, v65
	v_rcp_f32_e32 v128, v66
	v_rcp_f32_e32 v127, v67
	v_rcp_f32_e32 v126, v68
	v_rcp_f32_e32 v125, v69
	v_rcp_f32_e32 v124, v70
	v_rcp_f32_e32 v123, v71
	v_rcp_f32_e32 v122, v72
	v_rcp_f32_e32 v121, v73
	v_rcp_f32_e32 v120, v74
	v_add3_u32 v74, s72, 18, v208
	v_add3_u32 v72, s72, 19, v208
	v_add3_u32 v70, s72, 24, v208
	v_add3_u32 v68, s72, 25, v208
	v_add3_u32 v66, s72, 26, v208
	v_mfma_f32_32x32x64_f8f6f4 v[32:47], v[96:103], v[104:111], v[32:47]
	v_add3_u32 v110, s72, 8, v208
	v_add3_u32 v108, s72, 9, v208
	v_add3_u32 v106, s72, 10, v208
	v_add3_u32 v104, s72, 11, v208
	v_add3_u32 v64, s72, 27, v208
	v_mfma_f32_32x32x64_f8f6f4 v[16:31], v[96:103], v[88:95], v[16:31]
	v_rcp_f32_e32 v95, v75
	v_rcp_f32_e32 v94, v76
	v_rcp_f32_e32 v93, v77
	v_rcp_f32_e32 v92, v78
	v_rcp_f32_e32 v78, v79
	v_add3_u32 v90, s72, 16, v208
	v_add3_u32 v88, s72, 17, v208
	v_mfma_f32_32x32x64_f8f6f4 v[0:15], v[96:103], v[80:87], v[0:15]
	s_cbranch_vccnz .LBB0_596
	v_mul_f32_e32 v65, 0x41800000, v130
	v_mul_f32_e32 v67, v48, v65
	s_nop 2
	v_mul_f32_e32 v69, v32, v65
	v_med3_f32 v67, v67, s69, v203
	v_med3_f32 v69, v69, s69, v203
	v_mov_b32_e32 v73, v187
	v_cvt_pk_fp8_f32 v73, v67, v69
	v_mul_f32_e32 v71, v16, v65
	s_nop 7
	v_mul_f32_e32 v65, v0, v65
	v_med3_f32 v67, v71, s69, v203
	v_med3_f32 v65, v65, s69, v203
	v_cvt_pk_fp8_f32 v73, v67, v65 op_sel:[0,0,1]
	s_add_u32 s0, s54, s2
	s_addc_u32 s1, s55, 0
	v_lshl_add_u64 v[76:77], s[0:1], 0, v[186:187]
	v_lshlrev_b64 v[80:81], 11, v[118:119]
	v_lshl_add_u64 v[80:81], v[76:77], 0, v[80:81]
	v_lshrrev_b32_e32 v65, 8, v73
	global_store_byte v[80:81], v73, off
	global_store_byte v[80:81], v65, off offset:32
	global_store_byte_d16_hi v[80:81], v73, off offset:64
	v_lshrrev_b32_e32 v65, 24, v73
	global_store_byte v[80:81], v65, off offset:96
	v_mul_f32_e32 v65, 0x41800000, v129
	v_mul_f32_e32 v67, v49, v65
	v_mul_f32_e32 v69, v33, v65
	v_med3_f32 v67, v67, s69, v203
	v_med3_f32 v69, v69, s69, v203
	v_mov_b32_e32 v73, v187
	v_cvt_pk_fp8_f32 v73, v67, v69
	v_mul_f32_e32 v71, v17, v65
	v_mul_f32_e32 v65, v1, v65
	v_med3_f32 v67, v71, s69, v203
	v_med3_f32 v65, v65, s69, v203
	v_cvt_pk_fp8_f32 v73, v67, v65 op_sel:[0,0,1]
	v_ashrrev_i32_e32 v117, 31, v116
	v_lshlrev_b64 v[80:81], 11, v[116:117]
	v_lshl_add_u64 v[80:81], v[76:77], 0, v[80:81]
	v_lshrrev_b32_e32 v65, 8, v73
	global_store_byte v[80:81], v73, off
	global_store_byte v[80:81], v65, off offset:32
	global_store_byte_d16_hi v[80:81], v73, off offset:64
	v_lshrrev_b32_e32 v65, 24, v73
	global_store_byte v[80:81], v65, off offset:96
	v_mul_f32_e32 v65, 0x41800000, v128
	v_mul_f32_e32 v67, v50, v65
	v_mul_f32_e32 v69, v34, v65
	v_med3_f32 v67, v67, s69, v203
	v_med3_f32 v69, v69, s69, v203
	v_mov_b32_e32 v73, v187
	v_cvt_pk_fp8_f32 v73, v67, v69
	v_mul_f32_e32 v71, v18, v65
	v_mul_f32_e32 v65, v2, v65
	v_med3_f32 v67, v71, s69, v203
	v_med3_f32 v65, v65, s69, v203
	v_cvt_pk_fp8_f32 v73, v67, v65 op_sel:[0,0,1]
	v_ashrrev_i32_e32 v115, 31, v114
	v_lshlrev_b64 v[80:81], 11, v[114:115]
	v_lshl_add_u64 v[80:81], v[76:77], 0, v[80:81]
	v_lshrrev_b32_e32 v65, 8, v73
	global_store_byte v[80:81], v73, off
	global_store_byte v[80:81], v65, off offset:32
	global_store_byte_d16_hi v[80:81], v73, off offset:64
	v_lshrrev_b32_e32 v65, 24, v73
	global_store_byte v[80:81], v65, off offset:96
	v_mul_f32_e32 v65, 0x41800000, v127
	v_mul_f32_e32 v67, v51, v65
	v_mul_f32_e32 v69, v35, v65
	v_med3_f32 v67, v67, s69, v203
	v_med3_f32 v69, v69, s69, v203
	v_mov_b32_e32 v73, v187
	v_cvt_pk_fp8_f32 v73, v67, v69
	v_mul_f32_e32 v71, v19, v65
	v_mul_f32_e32 v65, v3, v65
	v_med3_f32 v67, v71, s69, v203
	v_med3_f32 v65, v65, s69, v203
	v_cvt_pk_fp8_f32 v73, v67, v65 op_sel:[0,0,1]
	v_ashrrev_i32_e32 v113, 31, v112
	v_lshlrev_b64 v[80:81], 11, v[112:113]
	v_lshl_add_u64 v[80:81], v[76:77], 0, v[80:81]
	v_lshrrev_b32_e32 v65, 8, v73
	global_store_byte v[80:81], v73, off
	global_store_byte v[80:81], v65, off offset:32
	global_store_byte_d16_hi v[80:81], v73, off offset:64
	v_lshrrev_b32_e32 v65, 24, v73
	global_store_byte v[80:81], v65, off offset:96
	v_mul_f32_e32 v65, 0x41800000, v126
	v_mul_f32_e32 v67, v52, v65
	v_mul_f32_e32 v69, v36, v65
	v_med3_f32 v67, v67, s69, v203
	v_med3_f32 v69, v69, s69, v203
	v_mov_b32_e32 v73, v187
	v_cvt_pk_fp8_f32 v73, v67, v69
	v_mul_f32_e32 v71, v20, v65
	v_mul_f32_e32 v65, v4, v65
	v_med3_f32 v67, v71, s69, v203
	v_med3_f32 v65, v65, s69, v203
	v_cvt_pk_fp8_f32 v73, v67, v65 op_sel:[0,0,1]
	v_ashrrev_i32_e32 v111, 31, v110
	v_lshlrev_b64 v[80:81], 11, v[110:111]
	v_lshl_add_u64 v[80:81], v[76:77], 0, v[80:81]
	v_lshrrev_b32_e32 v65, 8, v73
	global_store_byte v[80:81], v73, off
	global_store_byte v[80:81], v65, off offset:32
	global_store_byte_d16_hi v[80:81], v73, off offset:64
	v_lshrrev_b32_e32 v65, 24, v73
	global_store_byte v[80:81], v65, off offset:96
	v_mul_f32_e32 v65, 0x41800000, v125
	v_mul_f32_e32 v67, v53, v65
	v_mul_f32_e32 v69, v37, v65
	v_med3_f32 v67, v67, s69, v203
	v_med3_f32 v69, v69, s69, v203
	v_mov_b32_e32 v73, v187
	v_cvt_pk_fp8_f32 v73, v67, v69
	v_mul_f32_e32 v71, v21, v65
	v_mul_f32_e32 v65, v5, v65
	v_med3_f32 v67, v71, s69, v203
	v_med3_f32 v65, v65, s69, v203
	v_cvt_pk_fp8_f32 v73, v67, v65 op_sel:[0,0,1]
	v_ashrrev_i32_e32 v109, 31, v108
	v_lshlrev_b64 v[80:81], 11, v[108:109]
	v_lshl_add_u64 v[80:81], v[76:77], 0, v[80:81]
	v_lshrrev_b32_e32 v65, 8, v73
	global_store_byte v[80:81], v73, off
	global_store_byte v[80:81], v65, off offset:32
	global_store_byte_d16_hi v[80:81], v73, off offset:64
	v_lshrrev_b32_e32 v65, 24, v73
	global_store_byte v[80:81], v65, off offset:96
	v_mul_f32_e32 v65, 0x41800000, v124
	v_mul_f32_e32 v67, v54, v65
	v_mul_f32_e32 v69, v38, v65
	v_med3_f32 v67, v67, s69, v203
	v_med3_f32 v69, v69, s69, v203
	v_mov_b32_e32 v73, v187
	v_cvt_pk_fp8_f32 v73, v67, v69
	v_mul_f32_e32 v71, v22, v65
	v_mul_f32_e32 v65, v6, v65
	v_med3_f32 v67, v71, s69, v203
	v_med3_f32 v65, v65, s69, v203
	v_cvt_pk_fp8_f32 v73, v67, v65 op_sel:[0,0,1]
	v_ashrrev_i32_e32 v107, 31, v106
	v_lshlrev_b64 v[80:81], 11, v[106:107]
	v_lshl_add_u64 v[80:81], v[76:77], 0, v[80:81]
	v_lshrrev_b32_e32 v65, 8, v73
	global_store_byte v[80:81], v73, off
	global_store_byte v[80:81], v65, off offset:32
	global_store_byte_d16_hi v[80:81], v73, off offset:64
	v_lshrrev_b32_e32 v65, 24, v73
	global_store_byte v[80:81], v65, off offset:96
	v_mul_f32_e32 v65, 0x41800000, v123
	v_mul_f32_e32 v67, v55, v65
	v_mul_f32_e32 v69, v39, v65
	v_med3_f32 v67, v67, s69, v203
	v_med3_f32 v69, v69, s69, v203
	v_mov_b32_e32 v73, v187
	v_cvt_pk_fp8_f32 v73, v67, v69
	v_mul_f32_e32 v71, v23, v65
	v_mul_f32_e32 v65, v7, v65
	v_med3_f32 v67, v71, s69, v203
	v_med3_f32 v65, v65, s69, v203
	v_cvt_pk_fp8_f32 v73, v67, v65 op_sel:[0,0,1]
	v_ashrrev_i32_e32 v105, 31, v104
	v_lshlrev_b64 v[80:81], 11, v[104:105]
	v_lshl_add_u64 v[80:81], v[76:77], 0, v[80:81]
	v_lshrrev_b32_e32 v65, 8, v73
	global_store_byte v[80:81], v73, off
	global_store_byte v[80:81], v65, off offset:32
	global_store_byte_d16_hi v[80:81], v73, off offset:64
	v_lshrrev_b32_e32 v65, 24, v73
	global_store_byte v[80:81], v65, off offset:96
	v_mul_f32_e32 v65, 0x41800000, v122
	v_mul_f32_e32 v67, v56, v65
	v_mul_f32_e32 v69, v40, v65
	v_med3_f32 v67, v67, s69, v203
	v_med3_f32 v69, v69, s69, v203
	v_mov_b32_e32 v73, v187
	v_cvt_pk_fp8_f32 v73, v67, v69
	v_mul_f32_e32 v71, v24, v65
	v_mul_f32_e32 v65, v8, v65
	v_med3_f32 v67, v71, s69, v203
	v_med3_f32 v65, v65, s69, v203
	v_cvt_pk_fp8_f32 v73, v67, v65 op_sel:[0,0,1]
	v_ashrrev_i32_e32 v91, 31, v90
	v_lshlrev_b64 v[80:81], 11, v[90:91]
	v_lshl_add_u64 v[80:81], v[76:77], 0, v[80:81]
	v_lshrrev_b32_e32 v65, 8, v73
	global_store_byte v[80:81], v73, off
	global_store_byte v[80:81], v65, off offset:32
	global_store_byte_d16_hi v[80:81], v73, off offset:64
	v_lshrrev_b32_e32 v65, 24, v73
	global_store_byte v[80:81], v65, off offset:96
	v_mul_f32_e32 v65, 0x41800000, v121
	v_mul_f32_e32 v67, v57, v65
	v_mul_f32_e32 v69, v41, v65
	v_med3_f32 v67, v67, s69, v203
	v_med3_f32 v69, v69, s69, v203
	v_mov_b32_e32 v73, v187
	v_cvt_pk_fp8_f32 v73, v67, v69
	v_mul_f32_e32 v71, v25, v65
	v_mul_f32_e32 v65, v9, v65
	v_med3_f32 v67, v71, s69, v203
	v_med3_f32 v65, v65, s69, v203
	v_cvt_pk_fp8_f32 v73, v67, v65 op_sel:[0,0,1]
	v_ashrrev_i32_e32 v89, 31, v88
	v_lshlrev_b64 v[80:81], 11, v[88:89]
	v_lshl_add_u64 v[80:81], v[76:77], 0, v[80:81]
	v_lshrrev_b32_e32 v65, 8, v73
	global_store_byte v[80:81], v73, off
	global_store_byte v[80:81], v65, off offset:32
	global_store_byte_d16_hi v[80:81], v73, off offset:64
	v_lshrrev_b32_e32 v65, 24, v73
	global_store_byte v[80:81], v65, off offset:96
	v_mul_f32_e32 v65, 0x41800000, v120
	v_mul_f32_e32 v67, v58, v65
	v_mul_f32_e32 v69, v42, v65
	v_med3_f32 v67, v67, s69, v203
	v_med3_f32 v69, v69, s69, v203
	v_mov_b32_e32 v73, v187
	v_cvt_pk_fp8_f32 v73, v67, v69
	v_mul_f32_e32 v71, v26, v65
	v_mul_f32_e32 v65, v10, v65
	v_med3_f32 v67, v71, s69, v203
	v_med3_f32 v65, v65, s69, v203
	v_cvt_pk_fp8_f32 v73, v67, v65 op_sel:[0,0,1]
	v_ashrrev_i32_e32 v75, 31, v74
	v_lshlrev_b64 v[80:81], 11, v[74:75]
	v_lshl_add_u64 v[80:81], v[76:77], 0, v[80:81]
	v_lshrrev_b32_e32 v65, 8, v73
	global_store_byte v[80:81], v73, off
	global_store_byte v[80:81], v65, off offset:32
	global_store_byte_d16_hi v[80:81], v73, off offset:64
	v_lshrrev_b32_e32 v65, 24, v73
	global_store_byte v[80:81], v65, off offset:96
	v_mul_f32_e32 v65, 0x41800000, v95
	v_mul_f32_e32 v67, v59, v65
	v_mul_f32_e32 v69, v43, v65
	v_med3_f32 v67, v67, s69, v203
	v_med3_f32 v69, v69, s69, v203
	v_mov_b32_e32 v75, v187
	v_cvt_pk_fp8_f32 v75, v67, v69
	v_mul_f32_e32 v71, v27, v65
	v_mul_f32_e32 v65, v11, v65
	v_med3_f32 v67, v71, s69, v203
	v_med3_f32 v65, v65, s69, v203
	v_cvt_pk_fp8_f32 v75, v67, v65 op_sel:[0,0,1]
	v_ashrrev_i32_e32 v73, 31, v72
	v_lshlrev_b64 v[80:81], 11, v[72:73]
	v_lshl_add_u64 v[80:81], v[76:77], 0, v[80:81]
	v_lshrrev_b32_e32 v65, 8, v75
	global_store_byte v[80:81], v75, off
	global_store_byte v[80:81], v65, off offset:32
	global_store_byte_d16_hi v[80:81], v75, off offset:64
	v_lshrrev_b32_e32 v65, 24, v75
	global_store_byte v[80:81], v65, off offset:96
	v_mul_f32_e32 v65, 0x41800000, v94
	v_mul_f32_e32 v67, v60, v65
	v_mul_f32_e32 v69, v44, v65
	v_med3_f32 v67, v67, s69, v203
	v_med3_f32 v69, v69, s69, v203
	v_mov_b32_e32 v73, v187
	v_cvt_pk_fp8_f32 v73, v67, v69
	v_mul_f32_e32 v71, v28, v65
	v_mul_f32_e32 v65, v12, v65
	v_med3_f32 v67, v71, s69, v203
	v_med3_f32 v65, v65, s69, v203
	v_cvt_pk_fp8_f32 v73, v67, v65 op_sel:[0,0,1]
	v_ashrrev_i32_e32 v71, 31, v70
	v_lshlrev_b64 v[80:81], 11, v[70:71]
	v_lshl_add_u64 v[80:81], v[76:77], 0, v[80:81]
	v_lshrrev_b32_e32 v65, 8, v73
	global_store_byte v[80:81], v73, off
	global_store_byte v[80:81], v65, off offset:32
	global_store_byte_d16_hi v[80:81], v73, off offset:64
	v_lshrrev_b32_e32 v65, 24, v73
	global_store_byte v[80:81], v65, off offset:96
	v_mul_f32_e32 v65, 0x41800000, v93
	v_mul_f32_e32 v67, v61, v65
	v_mul_f32_e32 v69, v45, v65
	v_med3_f32 v67, v67, s69, v203
	v_med3_f32 v69, v69, s69, v203
	v_mov_b32_e32 v73, v187
	v_cvt_pk_fp8_f32 v73, v67, v69
	v_mul_f32_e32 v71, v29, v65
	v_mul_f32_e32 v65, v13, v65
	v_med3_f32 v67, v71, s69, v203
	v_med3_f32 v65, v65, s69, v203
	v_cvt_pk_fp8_f32 v73, v67, v65 op_sel:[0,0,1]
	v_ashrrev_i32_e32 v69, 31, v68
	v_lshlrev_b64 v[80:81], 11, v[68:69]
	v_lshl_add_u64 v[80:81], v[76:77], 0, v[80:81]
	v_lshrrev_b32_e32 v65, 8, v73
	global_store_byte v[80:81], v73, off
	global_store_byte v[80:81], v65, off offset:32
	global_store_byte_d16_hi v[80:81], v73, off offset:64
	v_lshrrev_b32_e32 v65, 24, v73
	global_store_byte v[80:81], v65, off offset:96
	v_mul_f32_e32 v65, 0x41800000, v92
	v_mul_f32_e32 v67, v62, v65
	v_mul_f32_e32 v69, v46, v65
	v_med3_f32 v67, v67, s69, v203
	v_med3_f32 v69, v69, s69, v203
	v_mov_b32_e32 v73, v187
	v_cvt_pk_fp8_f32 v73, v67, v69
	v_mul_f32_e32 v71, v30, v65
	v_mul_f32_e32 v65, v14, v65
	v_med3_f32 v67, v71, s69, v203
	v_med3_f32 v65, v65, s69, v203
	v_cvt_pk_fp8_f32 v73, v67, v65 op_sel:[0,0,1]
	v_ashrrev_i32_e32 v67, 31, v66
	v_lshlrev_b64 v[80:81], 11, v[66:67]
	v_lshl_add_u64 v[80:81], v[76:77], 0, v[80:81]
	v_lshrrev_b32_e32 v65, 8, v73
	global_store_byte v[80:81], v73, off
	global_store_byte v[80:81], v65, off offset:32
	global_store_byte_d16_hi v[80:81], v73, off offset:64
	v_lshrrev_b32_e32 v65, 24, v73
	global_store_byte v[80:81], v65, off offset:96
	v_mul_f32_e32 v65, 0x41800000, v78
	v_mul_f32_e32 v67, v63, v65
	v_mul_f32_e32 v69, v47, v65
	v_med3_f32 v67, v67, s69, v203
	v_med3_f32 v69, v69, s69, v203
	v_mov_b32_e32 v73, v187
	v_cvt_pk_fp8_f32 v73, v67, v69
	v_mul_f32_e32 v71, v31, v65
	v_mul_f32_e32 v65, v15, v65
	v_med3_f32 v67, v71, s69, v203
	v_med3_f32 v65, v65, s69, v203
	v_cvt_pk_fp8_f32 v73, v67, v65 op_sel:[0,0,1]
	v_ashrrev_i32_e32 v65, 31, v64
	v_lshlrev_b64 v[80:81], 11, v[64:65]
	v_lshl_add_u64 v[76:77], v[76:77], 0, v[80:81]
	v_lshrrev_b32_e32 v65, 8, v73
	global_store_byte v[76:77], v73, off
	global_store_byte v[76:77], v65, off offset:32
	global_store_byte_d16_hi v[76:77], v73, off offset:64
	v_lshrrev_b32_e32 v65, 24, v73
	s_mov_b64 s[0:1], 0
	global_store_byte v[76:77], v65, off offset:96

.LBB0_911:
	ds_read_b128 v[8:11], v231
	ds_read_b128 v[12:15], v231 offset:1024
	ds_read_b128 v[0:3], v231 offset:2048
	ds_read_b128 v[4:7], v231 offset:3072
	v_lshl_add_u64 v[172:173], v[170:171], 0, s[2:3]
	s_add_i32 s94, s73, 0xc000
	v_lshl_add_u64 v[174:175], v[172:173], 0, s[10:11]
	s_mov_b32 m0, s94
	ds_read_b128 v[180:183], v228
	ds_read_b128 v[184:187], v228 offset:1024
	ds_read_b128 v[188:191], v228 offset:2048
	ds_read_b128 v[192:195], v228 offset:3072
	ds_read_b128 v[196:199], v228 offset:4096
	ds_read_b128 v[200:203], v228 offset:5120
	ds_read_b128 v[204:207], v228 offset:6144
	ds_read_b128 v[208:211], v228 offset:7168
	global_load_lds_dwordx4 v[174:175], off
	v_lshl_add_u64 v[174:175], v[168:169], 0, s[2:3]
	s_add_i32 s93, s73, 0xe000
	v_lshl_add_u64 v[176:177], v[174:175], 0, s[10:11]
	s_mov_b32 m0, s93
	s_nop 0
	global_load_lds_dwordx4 v[176:177], off
	s_waitcnt lgkmcnt(8)
	s_barrier
	s_waitcnt lgkmcnt(0)
	s_setprio 1
	s_waitcnt lgkmcnt(0)
	v_mfma_f32_16x16x128_f8f6f4 v[16:19], v[8:15], v[180:187], v[16:19]
	v_mfma_f32_16x16x128_f8f6f4 v[20:23], v[0:7], v[180:187], v[20:23]
	v_mfma_f32_16x16x128_f8f6f4 v[24:27], v[8:15], v[188:195], v[24:27]
	v_mfma_f32_16x16x128_f8f6f4 v[28:31], v[0:7], v[188:195], v[28:31]
	v_mfma_f32_16x16x128_f8f6f4 v[32:35], v[8:15], v[196:203], v[32:35]
	v_mfma_f32_16x16x128_f8f6f4 v[36:39], v[0:7], v[196:203], v[36:39]
	v_mfma_f32_16x16x128_f8f6f4 v[40:43], v[8:15], v[204:211], v[40:43]
	v_mfma_f32_16x16x128_f8f6f4 v[44:47], v[0:7], v[204:211], v[44:47]
	s_setprio 0
	s_barrier
	v_lshl_add_u64 v[176:177], v[146:147], 0, s[2:3]
	s_add_i32 s96, s83, s72
	v_lshl_add_u64 v[178:179], v[176:177], 0, s[12:13]
	s_mov_b32 m0, s96
	ds_read_b128 v[212:215], v232
	ds_read_b128 v[216:219], v232 offset:1024
	ds_read_b128 v[234:237], v232 offset:2048
	ds_read_b128 v[238:241], v232 offset:3072
	global_load_lds_dwordx4 v[178:179], off
	v_lshl_add_u64 v[178:179], v[144:145], 0, s[2:3]
	s_add_i32 s95, s96, 0x2000
	v_lshl_add_u64 v[220:221], v[178:179], 0, s[12:13]
	s_mov_b32 m0, s95
	s_nop 0
	global_load_lds_dwordx4 v[220:221], off
	s_barrier
	s_waitcnt lgkmcnt(0)
	s_setprio 1
	s_waitcnt lgkmcnt(0)
	v_mfma_f32_16x16x128_f8f6f4 v[48:51], v[212:219], v[180:187], v[48:51]
	v_mfma_f32_16x16x128_f8f6f4 v[52:55], v[234:241], v[180:187], v[52:55]
	v_mfma_f32_16x16x128_f8f6f4 v[56:59], v[212:219], v[188:195], v[56:59]
	v_mfma_f32_16x16x128_f8f6f4 v[60:63], v[234:241], v[188:195], v[60:63]
	v_mfma_f32_16x16x128_f8f6f4 v[64:67], v[212:219], v[196:203], v[64:67]
	v_mfma_f32_16x16x128_f8f6f4 v[68:71], v[234:241], v[196:203], v[68:71]
	v_mfma_f32_16x16x128_f8f6f4 v[72:75], v[212:219], v[204:211], v[72:75]
	v_mfma_f32_16x16x128_f8f6f4 v[76:79], v[234:241], v[204:211], v[76:79]
	s_setprio 0
	s_mov_b32 m0, s73
	v_lshl_add_u64 v[220:221], v[172:173], 0, s[12:13]
	s_barrier
	ds_read_b128 v[180:183], v228 offset:16384
	ds_read_b128 v[184:187], v228 offset:17408
	ds_read_b128 v[188:191], v228 offset:18432
	ds_read_b128 v[192:195], v228 offset:19456
	ds_read_b128 v[196:199], v228 offset:20480
	ds_read_b128 v[200:203], v228 offset:21504
	ds_read_b128 v[204:207], v228 offset:22528
	ds_read_b128 v[208:211], v228 offset:23552
	global_load_lds_dwordx4 v[220:221], off
	v_lshl_add_u64 v[220:221], v[174:175], 0, s[12:13]
	s_mov_b32 m0, s74
	s_nop 0
	global_load_lds_dwordx4 v[220:221], off
	s_barrier
	s_waitcnt lgkmcnt(0)
	s_setprio 1
	s_waitcnt lgkmcnt(0)
	v_mfma_f32_16x16x128_f8f6f4 v[80:83], v[8:15], v[180:187], v[80:83]
	v_mfma_f32_16x16x128_f8f6f4 v[84:87], v[0:7], v[180:187], v[84:87]
	v_mfma_f32_16x16x128_f8f6f4 v[88:91], v[8:15], v[188:195], v[88:91]
	v_mfma_f32_16x16x128_f8f6f4 v[92:95], v[0:7], v[188:195], v[92:95]
	v_mfma_f32_16x16x128_f8f6f4 v[96:99], v[8:15], v[196:203], v[96:99]
	v_mfma_f32_16x16x128_f8f6f4 v[100:103], v[0:7], v[196:203], v[100:103]
	v_mfma_f32_16x16x128_f8f6f4 v[104:107], v[8:15], v[204:211], v[104:107]
	v_mfma_f32_16x16x128_f8f6f4 v[108:111], v[0:7], v[204:211], v[108:111]
	s_setprio 0
	s_barrier
	s_add_i32 s97, s84, s72
	v_lshl_add_u64 v[0:1], v[176:177], 0, s[16:17]
	s_mov_b32 m0, s97
	s_add_i32 s52, s97, 0x2000
	global_load_lds_dwordx4 v[0:1], off
	v_lshl_add_u64 v[0:1], v[178:179], 0, s[16:17]
	s_mov_b32 m0, s52
	s_nop 0
	global_load_lds_dwordx4 v[0:1], off
	s_waitcnt vmcnt(6)
	s_barrier
	s_setprio 1
	v_mfma_f32_16x16x128_f8f6f4 v[112:115], v[212:219], v[180:187], v[112:115]
	v_mfma_f32_16x16x128_f8f6f4 v[116:119], v[234:241], v[180:187], v[116:119]
	v_mfma_f32_16x16x128_f8f6f4 v[120:123], v[212:219], v[188:195], v[120:123]
	v_mfma_f32_16x16x128_f8f6f4 v[124:127], v[234:241], v[188:195], v[124:127]
	v_mfma_f32_16x16x128_f8f6f4 v[128:131], v[212:219], v[196:203], v[128:131]
	v_mfma_f32_16x16x128_f8f6f4 v[132:135], v[234:241], v[196:203], v[132:135]
	v_mfma_f32_16x16x128_f8f6f4 v[136:139], v[212:219], v[204:211], v[136:139]
	v_mfma_f32_16x16x128_f8f6f4 v[140:143], v[234:241], v[204:211], v[140:143]
	s_setprio 0
	s_add_i32 s62, 0, 0x18000
	v_add_u32_e32 v235, s62, v227
	s_barrier
	ds_read_b128 v[0:3], v235
	ds_read_b128 v[4:7], v235 offset:1024
	ds_read_b128 v[8:11], v235 offset:2048
	ds_read_b128 v[12:15], v235 offset:3072
	s_mov_b32 m0, s75
	v_lshl_add_u64 v[212:213], v[172:173], 0, s[16:17]
	ds_read_b128 v[180:183], v228 offset:32768
	ds_read_b128 v[184:187], v228 offset:33792
	ds_read_b128 v[188:191], v228 offset:34816
	ds_read_b128 v[192:195], v228 offset:35840
	ds_read_b128 v[196:199], v228 offset:36864
	ds_read_b128 v[200:203], v228 offset:37888
	ds_read_b128 v[204:207], v228 offset:38912
	ds_read_b128 v[208:211], v228 offset:39936
	global_load_lds_dwordx4 v[212:213], off
	v_lshl_add_u64 v[212:213], v[174:175], 0, s[16:17]
	s_mov_b32 m0, s76
	s_nop 0
	global_load_lds_dwordx4 v[212:213], off
	s_waitcnt lgkmcnt(8)
	s_barrier
	s_waitcnt lgkmcnt(0)
	s_setprio 1
	s_waitcnt lgkmcnt(0)
	v_mfma_f32_16x16x128_f8f6f4 v[16:19], v[0:7], v[180:187], v[16:19]
	v_mfma_f32_16x16x128_f8f6f4 v[20:23], v[8:15], v[180:187], v[20:23]
	v_mfma_f32_16x16x128_f8f6f4 v[24:27], v[0:7], v[188:195], v[24:27]
	v_mfma_f32_16x16x128_f8f6f4 v[28:31], v[8:15], v[188:195], v[28:31]
	v_mfma_f32_16x16x128_f8f6f4 v[32:35], v[0:7], v[196:203], v[32:35]
	v_mfma_f32_16x16x128_f8f6f4 v[36:39], v[8:15], v[196:203], v[36:39]
	v_mfma_f32_16x16x128_f8f6f4 v[40:43], v[0:7], v[204:211], v[40:43]
	v_mfma_f32_16x16x128_f8f6f4 v[44:47], v[8:15], v[204:211], v[44:47]
	s_setprio 0
	s_barrier
	s_add_i32 s53, 0, 0x1c000
	s_add_i32 s62, s62, s72
	v_add_u32_e32 v234, s53, v227
	v_lshl_add_u64 v[220:221], v[176:177], 0, s[18:19]
	s_mov_b32 m0, s62
	s_add_i32 s63, s62, 0x2000
	ds_read_b128 v[212:215], v234
	ds_read_b128 v[216:219], v234 offset:1024
	ds_read_b128 v[236:239], v234 offset:2048
	ds_read_b128 v[240:243], v234 offset:3072
	global_load_lds_dwordx4 v[220:221], off
	v_lshl_add_u64 v[220:221], v[178:179], 0, s[18:19]
	s_mov_b32 m0, s63
	s_nop 0
	global_load_lds_dwordx4 v[220:221], off
	s_barrier
	s_waitcnt lgkmcnt(0)
	s_setprio 1
	s_waitcnt lgkmcnt(0)
	v_mfma_f32_16x16x128_f8f6f4 v[48:51], v[212:219], v[180:187], v[48:51]
	v_mfma_f32_16x16x128_f8f6f4 v[52:55], v[236:243], v[180:187], v[52:55]
	v_mfma_f32_16x16x128_f8f6f4 v[56:59], v[212:219], v[188:195], v[56:59]
	v_mfma_f32_16x16x128_f8f6f4 v[60:63], v[236:243], v[188:195], v[60:63]
	v_mfma_f32_16x16x128_f8f6f4 v[64:67], v[212:219], v[196:203], v[64:67]
	v_mfma_f32_16x16x128_f8f6f4 v[68:71], v[236:243], v[196:203], v[68:71]
	v_mfma_f32_16x16x128_f8f6f4 v[72:75], v[212:219], v[204:211], v[72:75]
	v_mfma_f32_16x16x128_f8f6f4 v[76:79], v[236:243], v[204:211], v[76:79]
	s_setprio 0
	s_mov_b32 m0, s80
	v_lshl_add_u64 v[172:173], v[172:173], 0, s[18:19]
	s_barrier
	ds_read_b128 v[180:183], v228 offset:49152
	ds_read_b128 v[184:187], v228 offset:50176
	ds_read_b128 v[188:191], v228 offset:51200
	ds_read_b128 v[192:195], v228 offset:52224
	ds_read_b128 v[196:199], v228 offset:53248
	ds_read_b128 v[200:203], v228 offset:54272
	ds_read_b128 v[204:207], v228 offset:55296
	ds_read_b128 v[208:211], v228 offset:56320
	global_load_lds_dwordx4 v[172:173], off
	v_lshl_add_u64 v[172:173], v[174:175], 0, s[18:19]
	s_mov_b32 m0, s81
	s_nop 0
	global_load_lds_dwordx4 v[172:173], off
	s_barrier
	s_waitcnt lgkmcnt(0)
	s_setprio 1
	s_waitcnt lgkmcnt(0)
	v_mfma_f32_16x16x128_f8f6f4 v[80:83], v[0:7], v[180:187], v[80:83]
	v_mfma_f32_16x16x128_f8f6f4 v[84:87], v[8:15], v[180:187], v[84:87]
	v_mfma_f32_16x16x128_f8f6f4 v[88:91], v[0:7], v[188:195], v[88:91]
	v_mfma_f32_16x16x128_f8f6f4 v[92:95], v[8:15], v[188:195], v[92:95]
	v_mfma_f32_16x16x128_f8f6f4 v[96:99], v[0:7], v[196:203], v[96:99]
	v_mfma_f32_16x16x128_f8f6f4 v[100:103], v[8:15], v[196:203], v[100:103]
	v_mfma_f32_16x16x128_f8f6f4 v[104:107], v[0:7], v[204:211], v[104:107]
	v_mfma_f32_16x16x128_f8f6f4 v[108:111], v[8:15], v[204:211], v[108:111]
	s_setprio 0
	s_barrier
	s_add_i32 s53, s53, s72
	v_lshl_add_u64 v[0:1], v[176:177], 0, s[20:21]
	s_mov_b32 m0, s53
	s_add_i32 s64, s53, 0x2000
	global_load_lds_dwordx4 v[0:1], off
	v_lshl_add_u64 v[0:1], v[178:179], 0, s[20:21]
	s_mov_b32 m0, s64
	s_nop 0
	global_load_lds_dwordx4 v[0:1], off
	s_waitcnt vmcnt(6)
	s_barrier
	s_setprio 1
	v_mfma_f32_16x16x128_f8f6f4 v[112:115], v[212:219], v[180:187], v[112:115]
	v_mfma_f32_16x16x128_f8f6f4 v[116:119], v[236:243], v[180:187], v[116:119]
	v_mfma_f32_16x16x128_f8f6f4 v[120:123], v[212:219], v[188:195], v[120:123]
	v_mfma_f32_16x16x128_f8f6f4 v[124:127], v[236:243], v[188:195], v[124:127]
	v_mfma_f32_16x16x128_f8f6f4 v[128:131], v[212:219], v[196:203], v[128:131]
	v_mfma_f32_16x16x128_f8f6f4 v[132:135], v[236:243], v[196:203], v[132:135]
	v_mfma_f32_16x16x128_f8f6f4 v[136:139], v[212:219], v[204:211], v[136:139]
	v_mfma_f32_16x16x128_f8f6f4 v[140:143], v[236:243], v[204:211], v[140:143]
	s_setprio 0
	s_add_i32 s44, s44, 2
	s_add_u32 s2, s2, 0x100
	s_addc_u32 s3, s3, 0
	s_cmp_gt_u32 s44, 5
	s_barrier
	s_cbranch_scc0 .LBB0_911
	s_add_u32 s44, s65, s89
	s_addc_u32 s45, s66, 0
	s_add_u32 s46, s70, s90
	s_addc_u32 s47, s71, 0
	s_and_b64 s[2:3], vcc, exec
	s_mul_i32 s2, s92, 24
	s_cselect_b32 s55, s45, s49
	s_cselect_b32 s54, s44, s48
	s_add_i32 s58, s2, s91
	s_ashr_i32 s59, s58, 31
	s_lshl_b64 s[2:3], s[58:59], 16
	s_add_u32 s2, s78, s2
	s_addc_u32 s3, s79, s3
	s_add_i32 s56, s58, 8
	s_ashr_i32 s57, s56, 31
	v_mov_b32_e32 v156, v230
	s_lshl_b64 s[56:57], s[56:57], 16
	s_nop 7
	s_nop 7
	s_nop 7
	s_add_u32 s56, s78, s56
	s_addc_u32 s57, s79, s57
	global_load_dwordx2 v[210:211], v156, s[2:3]
	global_load_dwordx2 v[216:217], v156, s[56:57]
	global_load_dwordx2 v[206:207], v156, s[2:3] offset:512
	global_load_dwordx2 v[208:209], v156, s[56:57] offset:512
	global_load_dwordx2 v[202:203], v156, s[2:3] offset:1024
	global_load_dwordx2 v[204:205], v156, s[56:57] offset:1024
	global_load_dwordx2 v[198:199], v156, s[2:3] offset:1536
	global_load_dwordx2 v[200:201], v156, s[56:57] offset:1536
	global_load_dwordx2 v[194:195], v156, s[2:3] offset:2048
	global_load_dwordx2 v[196:197], v156, s[56:57] offset:2048
	global_load_dwordx2 v[190:191], v156, s[2:3] offset:2560
	global_load_dwordx2 v[192:193], v156, s[56:57] offset:2560
	global_load_dwordx2 v[186:187], v156, s[2:3] offset:3072
	global_load_dwordx2 v[188:189], v156, s[56:57] offset:3072
	global_load_dwordx2 v[182:183], v156, s[2:3] offset:3584
	global_load_dwordx2 v[184:185], v156, s[56:57] offset:3584
	v_lshl_add_u64 v[0:1], s[2:3], 0, v[156:157]
	v_lshl_add_u64 v[2:3], s[56:57], 0, v[156:157]
	v_add_co_u32_e64 v0, s[2:3], s85, v0
	s_waitcnt vmcnt(0)
	v_cvt_f32_ubyte3_e32 v237, v210
	v_cvt_f32_ubyte0_e32 v156, v216
	v_add_f32_e32 v156, 0.5, v156
	v_rcp_f32_e32 v218, v156
	v_cvt_f32_ubyte0_e32 v156, v217
	v_add_f32_e32 v156, 0.5, v156
	v_rcp_f32_e32 v212, v156
	v_cvt_f32_ubyte1_e32 v156, v216
	v_add_f32_e32 v156, 0.5, v156
	v_rcp_f32_e32 v219, v156
	v_cvt_f32_ubyte1_e32 v156, v217
	v_add_f32_e32 v156, 0.5, v156
	v_rcp_f32_e32 v213, v156
	v_cvt_f32_ubyte2_e32 v156, v216
	v_add_f32_e32 v156, 0.5, v156
	v_rcp_f32_e32 v220, v156
	v_cvt_f32_ubyte2_e32 v156, v217
	v_add_f32_e32 v156, 0.5, v156
	v_rcp_f32_e32 v214, v156
	v_cvt_f32_ubyte3_e32 v156, v216
	v_add_f32_e32 v156, 0.5, v156
	v_rcp_f32_e32 v221, v156
	v_cvt_f32_ubyte3_e32 v156, v217
	v_add_f32_e32 v156, 0.5, v156
	v_cvt_f32_ubyte1_e32 v217, v210
	v_cvt_f32_ubyte0_e32 v216, v210
	v_cvt_f32_ubyte2_e32 v236, v210
	v_rcp_f32_e32 v215, v156
	v_pk_add_f32 v[236:237], v[236:237], 0.5 op_sel_hi:[1,0]
	v_pk_add_f32 v[216:217], v[216:217], 0.5 op_sel_hi:[1,0]
	v_cvt_f32_ubyte0_e32 v156, v208
	v_pk_mul_f32 v[216:217], v[216:217], v[218:219]
	v_pk_mul_f32 v[218:219], v[236:237], v[220:221]
	v_pk_mul_f32 v[16:17], v[16:17], v[216:217]
	v_pk_mul_f32 v[18:19], v[18:19], v[218:219]
	v_cvt_f32_ubyte3_e32 v219, v211
	v_cvt_f32_ubyte2_e32 v218, v211
	v_cvt_f32_ubyte1_e32 v217, v211
	v_cvt_f32_ubyte0_e32 v216, v211
	v_pk_add_f32 v[210:211], v[218:219], 0.5 op_sel_hi:[1,0]
	v_add_f32_e32 v156, 0.5, v156
	v_pk_mul_f32 v[210:211], v[210:211], v[214:215]
	v_pk_add_f32 v[216:217], v[216:217], 0.5 op_sel_hi:[1,0]
	v_pk_mul_f32 v[22:23], v[22:23], v[210:211]
	v_rcp_f32_e32 v210, v156
	v_cvt_f32_ubyte0_e32 v156, v209
	v_pk_mul_f32 v[212:213], v[216:217], v[212:213]
	v_add_f32_e32 v156, 0.5, v156
	v_pk_mul_f32 v[20:21], v[20:21], v[212:213]
	v_rcp_f32_e32 v212, v156
	v_cvt_f32_ubyte1_e32 v156, v208
	v_add_f32_e32 v156, 0.5, v156
	v_rcp_f32_e32 v211, v156
	v_cvt_f32_ubyte1_e32 v156, v209
	v_add_f32_e32 v156, 0.5, v156
	v_rcp_f32_e32 v213, v156
	v_cvt_f32_ubyte2_e32 v156, v208
	v_add_f32_e32 v156, 0.5, v156
	v_rcp_f32_e32 v214, v156
	v_cvt_f32_ubyte2_e32 v156, v209
	v_add_f32_e32 v156, 0.5, v156
	v_rcp_f32_e32 v216, v156
	v_cvt_f32_ubyte3_e32 v156, v208
	v_add_f32_e32 v156, 0.5, v156
	v_rcp_f32_e32 v215, v156
	v_cvt_f32_ubyte3_e32 v156, v209
	v_add_f32_e32 v156, 0.5, v156
	v_cvt_f32_ubyte1_e32 v209, v206
	v_cvt_f32_ubyte0_e32 v208, v206
	v_cvt_f32_ubyte3_e32 v219, v206
	v_cvt_f32_ubyte2_e32 v218, v206
	v_rcp_f32_e32 v217, v156
	v_pk_add_f32 v[218:219], v[218:219], 0.5 op_sel_hi:[1,0]
	v_pk_add_f32 v[208:209], v[208:209], 0.5 op_sel_hi:[1,0]
	v_cvt_f32_ubyte0_e32 v156, v204
	v_pk_mul_f32 v[208:209], v[208:209], v[210:211]
	v_pk_mul_f32 v[210:211], v[218:219], v[214:215]
	v_pk_mul_f32 v[48:49], v[48:49], v[208:209]
	v_pk_mul_f32 v[50:51], v[50:51], v[210:211]
	v_cvt_f32_ubyte3_e32 v211, v207
	v_cvt_f32_ubyte2_e32 v210, v207
	v_cvt_f32_ubyte1_e32 v209, v207
	v_cvt_f32_ubyte0_e32 v208, v207
	v_pk_add_f32 v[206:207], v[210:211], 0.5 op_sel_hi:[1,0]
	v_add_f32_e32 v156, 0.5, v156
	v_pk_mul_f32 v[206:207], v[206:207], v[216:217]
	v_pk_add_f32 v[208:209], v[208:209], 0.5 op_sel_hi:[1,0]
	v_pk_mul_f32 v[54:55], v[54:55], v[206:207]
	v_rcp_f32_e32 v206, v156
	v_cvt_f32_ubyte0_e32 v156, v205
	v_pk_mul_f32 v[208:209], v[208:209], v[212:213]
	v_add_f32_e32 v156, 0.5, v156
	v_pk_mul_f32 v[52:53], v[52:53], v[208:209]
	v_rcp_f32_e32 v208, v156
	v_cvt_f32_ubyte1_e32 v156, v204
	v_add_f32_e32 v156, 0.5, v156
	v_rcp_f32_e32 v207, v156
	v_cvt_f32_ubyte1_e32 v156, v205
	v_add_f32_e32 v156, 0.5, v156
	v_rcp_f32_e32 v209, v156
	v_cvt_f32_ubyte2_e32 v156, v204
	v_add_f32_e32 v156, 0.5, v156
	v_rcp_f32_e32 v210, v156
	v_cvt_f32_ubyte2_e32 v156, v205
	v_add_f32_e32 v156, 0.5, v156
	v_rcp_f32_e32 v212, v156
	v_cvt_f32_ubyte3_e32 v156, v204
	v_add_f32_e32 v156, 0.5, v156
	v_rcp_f32_e32 v211, v156
	v_cvt_f32_ubyte3_e32 v156, v205
	v_add_f32_e32 v156, 0.5, v156
	v_cvt_f32_ubyte1_e32 v205, v202
	v_cvt_f32_ubyte0_e32 v204, v202
	v_cvt_f32_ubyte3_e32 v215, v202
	v_cvt_f32_ubyte2_e32 v214, v202
	v_rcp_f32_e32 v213, v156
	v_pk_add_f32 v[214:215], v[214:215], 0.5 op_sel_hi:[1,0]
	v_pk_add_f32 v[204:205], v[204:205], 0.5 op_sel_hi:[1,0]
	v_cvt_f32_ubyte0_e32 v156, v200
	v_pk_mul_f32 v[204:205], v[204:205], v[206:207]
	v_pk_mul_f32 v[206:207], v[214:215], v[210:211]
	v_pk_mul_f32 v[24:25], v[24:25], v[204:205]
	v_pk_mul_f32 v[26:27], v[26:27], v[206:207]
	v_cvt_f32_ubyte3_e32 v207, v203
	v_cvt_f32_ubyte2_e32 v206, v203
	v_cvt_f32_ubyte1_e32 v205, v203
	v_cvt_f32_ubyte0_e32 v204, v203
	v_pk_add_f32 v[202:203], v[206:207], 0.5 op_sel_hi:[1,0]
	v_add_f32_e32 v156, 0.5, v156
	v_pk_mul_f32 v[202:203], v[202:203], v[212:213]
	v_pk_add_f32 v[204:205], v[204:205], 0.5 op_sel_hi:[1,0]
	v_pk_mul_f32 v[30:31], v[30:31], v[202:203]
	v_rcp_f32_e32 v202, v156
	v_cvt_f32_ubyte0_e32 v156, v201
	v_pk_mul_f32 v[204:205], v[204:205], v[208:209]
	v_add_f32_e32 v156, 0.5, v156
	v_pk_mul_f32 v[28:29], v[28:29], v[204:205]
	v_rcp_f32_e32 v204, v156
	v_cvt_f32_ubyte1_e32 v156, v200
	v_add_f32_e32 v156, 0.5, v156
	v_rcp_f32_e32 v203, v156
	v_cvt_f32_ubyte1_e32 v156, v201
	v_add_f32_e32 v156, 0.5, v156
	v_rcp_f32_e32 v205, v156
	v_cvt_f32_ubyte2_e32 v156, v200
	v_add_f32_e32 v156, 0.5, v156
	v_rcp_f32_e32 v206, v156
	v_cvt_f32_ubyte2_e32 v156, v201
	v_add_f32_e32 v156, 0.5, v156
	v_rcp_f32_e32 v208, v156
	v_cvt_f32_ubyte3_e32 v156, v200
	v_add_f32_e32 v156, 0.5, v156
	v_rcp_f32_e32 v207, v156
	v_cvt_f32_ubyte3_e32 v156, v201
	v_add_f32_e32 v156, 0.5, v156
	v_cvt_f32_ubyte1_e32 v201, v198
	v_cvt_f32_ubyte0_e32 v200, v198
	v_cvt_f32_ubyte3_e32 v211, v198
	v_cvt_f32_ubyte2_e32 v210, v198
	v_rcp_f32_e32 v209, v156
	v_pk_add_f32 v[210:211], v[210:211], 0.5 op_sel_hi:[1,0]
	v_pk_add_f32 v[200:201], v[200:201], 0.5 op_sel_hi:[1,0]
	v_cvt_f32_ubyte0_e32 v156, v196
	v_pk_mul_f32 v[200:201], v[200:201], v[202:203]
	v_pk_mul_f32 v[202:203], v[210:211], v[206:207]
	v_pk_mul_f32 v[56:57], v[56:57], v[200:201]
	v_pk_mul_f32 v[58:59], v[58:59], v[202:203]
	v_cvt_f32_ubyte3_e32 v203, v199
	v_cvt_f32_ubyte2_e32 v202, v199
	v_cvt_f32_ubyte1_e32 v201, v199
	v_cvt_f32_ubyte0_e32 v200, v199
	v_pk_add_f32 v[198:199], v[202:203], 0.5 op_sel_hi:[1,0]
	v_add_f32_e32 v156, 0.5, v156
	v_pk_mul_f32 v[198:199], v[198:199], v[208:209]
	v_pk_add_f32 v[200:201], v[200:201], 0.5 op_sel_hi:[1,0]
	v_pk_mul_f32 v[62:63], v[62:63], v[198:199]
	v_rcp_f32_e32 v198, v156
	v_cvt_f32_ubyte0_e32 v156, v197
	v_pk_mul_f32 v[200:201], v[200:201], v[204:205]
	v_add_f32_e32 v156, 0.5, v156
	v_pk_mul_f32 v[60:61], v[60:61], v[200:201]
	v_rcp_f32_e32 v200, v156
	v_cvt_f32_ubyte1_e32 v156, v196
	v_add_f32_e32 v156, 0.5, v156
	v_rcp_f32_e32 v199, v156
	v_cvt_f32_ubyte1_e32 v156, v197
	v_add_f32_e32 v156, 0.5, v156
	v_rcp_f32_e32 v201, v156
	v_cvt_f32_ubyte2_e32 v156, v196
	v_add_f32_e32 v156, 0.5, v156
	v_rcp_f32_e32 v202, v156
	v_cvt_f32_ubyte2_e32 v156, v197
	v_addc_co_u32_e64 v1, s[2:3], 0, v1, s[2:3]
	v_add_f32_e32 v156, 0.5, v156
	v_add_co_u32_e64 v6, s[2:3], s85, v2
	v_rcp_f32_e32 v204, v156
	v_cvt_f32_ubyte3_e32 v156, v196
	v_addc_co_u32_e64 v7, s[2:3], 0, v3, s[2:3]
	v_add_f32_e32 v156, 0.5, v156
	global_load_dwordx2 v[178:179], v[0:1], off
	global_load_dwordx2 v[180:181], v[6:7], off
	global_load_dwordx2 v[174:175], v[0:1], off offset:512
	global_load_dwordx2 v[176:177], v[6:7], off offset:512
	global_load_dwordx2 v[170:171], v[0:1], off offset:1024
	global_load_dwordx2 v[172:173], v[6:7], off offset:1024
	global_load_dwordx2 v[144:145], v[0:1], off offset:1536
	global_load_dwordx2 v[146:147], v[6:7], off offset:1536
	global_load_dwordx2 v[12:13], v[0:1], off offset:2048
	global_load_dwordx2 v[14:15], v[6:7], off offset:2048
	global_load_dwordx2 v[8:9], v[0:1], off offset:2560
	global_load_dwordx2 v[10:11], v[6:7], off offset:2560
	global_load_dwordx2 v[2:3], v[0:1], off offset:3072
	global_load_dwordx2 v[4:5], v[6:7], off offset:3072
	s_nop 0
	global_load_dwordx2 v[0:1], v[0:1], off offset:3584
	s_nop 0
	global_load_dwordx2 v[6:7], v[6:7], off offset:3584
	v_rcp_f32_e32 v203, v156
	v_cvt_f32_ubyte3_e32 v156, v197
	v_add_f32_e32 v156, 0.5, v156
	v_cvt_f32_ubyte1_e32 v197, v194
	v_cvt_f32_ubyte0_e32 v196, v194
	v_cvt_f32_ubyte3_e32 v207, v194
	v_cvt_f32_ubyte2_e32 v206, v194
	v_rcp_f32_e32 v205, v156
	v_pk_add_f32 v[206:207], v[206:207], 0.5 op_sel_hi:[1,0]
	v_pk_add_f32 v[196:197], v[196:197], 0.5 op_sel_hi:[1,0]
	v_cvt_f32_ubyte0_e32 v156, v192
	v_pk_mul_f32 v[196:197], v[196:197], v[198:199]
	v_pk_mul_f32 v[198:199], v[206:207], v[202:203]
	v_pk_mul_f32 v[32:33], v[32:33], v[196:197]
	v_pk_mul_f32 v[34:35], v[34:35], v[198:199]
	v_cvt_f32_ubyte3_e32 v199, v195
	v_cvt_f32_ubyte2_e32 v198, v195
	v_cvt_f32_ubyte1_e32 v197, v195
	v_cvt_f32_ubyte0_e32 v196, v195
	v_pk_add_f32 v[194:195], v[198:199], 0.5 op_sel_hi:[1,0]
	v_add_f32_e32 v156, 0.5, v156
	v_pk_mul_f32 v[194:195], v[194:195], v[204:205]
	v_pk_add_f32 v[196:197], v[196:197], 0.5 op_sel_hi:[1,0]
	v_pk_mul_f32 v[38:39], v[38:39], v[194:195]
	v_rcp_f32_e32 v194, v156
	v_cvt_f32_ubyte0_e32 v156, v193
	v_pk_mul_f32 v[196:197], v[196:197], v[200:201]
	v_add_f32_e32 v156, 0.5, v156
	v_pk_mul_f32 v[36:37], v[36:37], v[196:197]
	v_rcp_f32_e32 v196, v156
	v_cvt_f32_ubyte1_e32 v156, v192
	v_add_f32_e32 v156, 0.5, v156
	v_rcp_f32_e32 v195, v156
	v_cvt_f32_ubyte1_e32 v156, v193
	v_add_f32_e32 v156, 0.5, v156
	v_rcp_f32_e32 v197, v156
	v_cvt_f32_ubyte2_e32 v156, v192
	v_add_f32_e32 v156, 0.5, v156
	v_rcp_f32_e32 v198, v156
	v_cvt_f32_ubyte2_e32 v156, v193
	v_add_f32_e32 v156, 0.5, v156
	v_rcp_f32_e32 v200, v156
	v_cvt_f32_ubyte3_e32 v156, v192
	v_add_f32_e32 v156, 0.5, v156
	v_rcp_f32_e32 v199, v156
	v_cvt_f32_ubyte3_e32 v156, v193
	v_add_f32_e32 v156, 0.5, v156
	v_cvt_f32_ubyte1_e32 v193, v190
	v_cvt_f32_ubyte0_e32 v192, v190
	v_cvt_f32_ubyte3_e32 v203, v190
	v_cvt_f32_ubyte2_e32 v202, v190
	v_rcp_f32_e32 v201, v156
	v_pk_add_f32 v[202:203], v[202:203], 0.5 op_sel_hi:[1,0]
	v_pk_add_f32 v[192:193], v[192:193], 0.5 op_sel_hi:[1,0]
	v_cvt_f32_ubyte0_e32 v156, v188
	v_pk_mul_f32 v[192:193], v[192:193], v[194:195]
	v_pk_mul_f32 v[194:195], v[202:203], v[198:199]
	v_pk_mul_f32 v[64:65], v[64:65], v[192:193]
	v_pk_mul_f32 v[66:67], v[66:67], v[194:195]
	v_cvt_f32_ubyte3_e32 v195, v191
	v_cvt_f32_ubyte2_e32 v194, v191
	v_cvt_f32_ubyte1_e32 v193, v191
	v_cvt_f32_ubyte0_e32 v192, v191
	v_pk_add_f32 v[190:191], v[194:195], 0.5 op_sel_hi:[1,0]
	v_add_f32_e32 v156, 0.5, v156
	v_pk_mul_f32 v[190:191], v[190:191], v[200:201]
	v_pk_add_f32 v[192:193], v[192:193], 0.5 op_sel_hi:[1,0]
	v_pk_mul_f32 v[70:71], v[70:71], v[190:191]
	v_rcp_f32_e32 v190, v156
	v_cvt_f32_ubyte0_e32 v156, v189
	v_pk_mul_f32 v[192:193], v[192:193], v[196:197]
	v_add_f32_e32 v156, 0.5, v156
	v_pk_mul_f32 v[68:69], v[68:69], v[192:193]
	v_rcp_f32_e32 v192, v156
	v_cvt_f32_ubyte1_e32 v156, v188
	v_add_f32_e32 v156, 0.5, v156
	v_rcp_f32_e32 v191, v156
	v_cvt_f32_ubyte1_e32 v156, v189
	v_add_f32_e32 v156, 0.5, v156
	v_rcp_f32_e32 v193, v156
	v_cvt_f32_ubyte2_e32 v156, v188
	v_add_f32_e32 v156, 0.5, v156
	v_rcp_f32_e32 v194, v156
	v_cvt_f32_ubyte2_e32 v156, v189
	v_add_f32_e32 v156, 0.5, v156
	v_rcp_f32_e32 v196, v156
	v_cvt_f32_ubyte3_e32 v156, v188
	v_add_f32_e32 v156, 0.5, v156
	v_rcp_f32_e32 v195, v156
	v_cvt_f32_ubyte3_e32 v156, v189
	v_add_f32_e32 v156, 0.5, v156
	v_cvt_f32_ubyte1_e32 v189, v186
	v_cvt_f32_ubyte0_e32 v188, v186
	v_cvt_f32_ubyte3_e32 v199, v186
	v_cvt_f32_ubyte2_e32 v198, v186
	v_rcp_f32_e32 v197, v156
	v_pk_add_f32 v[198:199], v[198:199], 0.5 op_sel_hi:[1,0]
	v_pk_add_f32 v[188:189], v[188:189], 0.5 op_sel_hi:[1,0]
	v_cvt_f32_ubyte0_e32 v156, v184
	v_pk_mul_f32 v[188:189], v[188:189], v[190:191]
	v_pk_mul_f32 v[190:191], v[198:199], v[194:195]
	v_pk_mul_f32 v[40:41], v[40:41], v[188:189]
	v_pk_mul_f32 v[42:43], v[42:43], v[190:191]
	v_cvt_f32_ubyte3_e32 v191, v187
	v_cvt_f32_ubyte2_e32 v190, v187
	v_cvt_f32_ubyte1_e32 v189, v187
	v_cvt_f32_ubyte0_e32 v188, v187
	v_pk_add_f32 v[186:187], v[190:191], 0.5 op_sel_hi:[1,0]
	v_add_f32_e32 v156, 0.5, v156
	v_pk_mul_f32 v[186:187], v[186:187], v[196:197]
	v_pk_add_f32 v[188:189], v[188:189], 0.5 op_sel_hi:[1,0]
	v_pk_mul_f32 v[46:47], v[46:47], v[186:187]
	v_rcp_f32_e32 v186, v156
	v_cvt_f32_ubyte0_e32 v156, v185
	v_pk_mul_f32 v[188:189], v[188:189], v[192:193]
	v_add_f32_e32 v156, 0.5, v156
	v_pk_mul_f32 v[44:45], v[44:45], v[188:189]
	v_rcp_f32_e32 v188, v156
	v_cvt_f32_ubyte1_e32 v156, v184
	v_add_f32_e32 v156, 0.5, v156
	v_rcp_f32_e32 v187, v156
	v_cvt_f32_ubyte1_e32 v156, v185
	v_add_f32_e32 v156, 0.5, v156
	v_rcp_f32_e32 v189, v156
	v_cvt_f32_ubyte2_e32 v156, v184
	v_add_f32_e32 v156, 0.5, v156
	v_rcp_f32_e32 v190, v156
	v_cvt_f32_ubyte2_e32 v156, v185
	v_add_f32_e32 v156, 0.5, v156
	v_rcp_f32_e32 v192, v156
	v_cvt_f32_ubyte3_e32 v156, v184
	v_add_f32_e32 v156, 0.5, v156
	v_rcp_f32_e32 v191, v156
	v_cvt_f32_ubyte3_e32 v156, v185
	v_add_f32_e32 v156, 0.5, v156
	v_cvt_f32_ubyte1_e32 v185, v182
	v_cvt_f32_ubyte0_e32 v184, v182
	v_cvt_f32_ubyte3_e32 v195, v182
	v_cvt_f32_ubyte2_e32 v194, v182
	v_rcp_f32_e32 v193, v156
	v_pk_add_f32 v[194:195], v[194:195], 0.5 op_sel_hi:[1,0]
	v_pk_add_f32 v[184:185], v[184:185], 0.5 op_sel_hi:[1,0]
	s_waitcnt vmcnt(0)
	v_cvt_f32_ubyte0_e32 v156, v180
	v_pk_mul_f32 v[184:185], v[184:185], v[186:187]
	v_pk_mul_f32 v[186:187], v[194:195], v[190:191]
	v_pk_mul_f32 v[72:73], v[72:73], v[184:185]
	v_pk_mul_f32 v[74:75], v[74:75], v[186:187]
	v_cvt_f32_ubyte3_e32 v187, v183
	v_cvt_f32_ubyte2_e32 v186, v183
	v_cvt_f32_ubyte1_e32 v185, v183
	v_cvt_f32_ubyte0_e32 v184, v183
	v_pk_add_f32 v[182:183], v[186:187], 0.5 op_sel_hi:[1,0]
	v_add_f32_e32 v156, 0.5, v156
	v_pk_mul_f32 v[182:183], v[182:183], v[192:193]
	v_pk_add_f32 v[184:185], v[184:185], 0.5 op_sel_hi:[1,0]
	v_pk_mul_f32 v[78:79], v[78:79], v[182:183]
	v_rcp_f32_e32 v182, v156
	v_cvt_f32_ubyte0_e32 v156, v181
	v_pk_mul_f32 v[184:185], v[184:185], v[188:189]
	v_add_f32_e32 v156, 0.5, v156
	v_pk_mul_f32 v[76:77], v[76:77], v[184:185]
	v_rcp_f32_e32 v184, v156
	v_cvt_f32_ubyte1_e32 v156, v180
	v_add_f32_e32 v156, 0.5, v156
	v_rcp_f32_e32 v183, v156
	v_cvt_f32_ubyte1_e32 v156, v181
	v_add_f32_e32 v156, 0.5, v156
	v_rcp_f32_e32 v185, v156
	v_cvt_f32_ubyte2_e32 v156, v180
	v_add_f32_e32 v156, 0.5, v156
	v_rcp_f32_e32 v186, v156
	v_cvt_f32_ubyte2_e32 v156, v181
	v_add_f32_e32 v156, 0.5, v156
	v_rcp_f32_e32 v188, v156
	v_cvt_f32_ubyte3_e32 v156, v180
	v_add_f32_e32 v156, 0.5, v156
	v_rcp_f32_e32 v187, v156
	v_cvt_f32_ubyte3_e32 v156, v181
	v_add_f32_e32 v156, 0.5, v156
	v_cvt_f32_ubyte1_e32 v181, v178
	v_cvt_f32_ubyte0_e32 v180, v178
	v_cvt_f32_ubyte3_e32 v191, v178
	v_cvt_f32_ubyte2_e32 v190, v178
	v_rcp_f32_e32 v189, v156
	v_pk_add_f32 v[190:191], v[190:191], 0.5 op_sel_hi:[1,0]
	v_pk_add_f32 v[180:181], v[180:181], 0.5 op_sel_hi:[1,0]
	v_cvt_f32_ubyte0_e32 v156, v176
	v_pk_mul_f32 v[180:181], v[180:181], v[182:183]
	v_pk_mul_f32 v[182:183], v[190:191], v[186:187]
	v_pk_mul_f32 v[80:81], v[80:81], v[180:181]
	v_pk_mul_f32 v[82:83], v[82:83], v[182:183]
	v_cvt_f32_ubyte3_e32 v183, v179
	v_cvt_f32_ubyte2_e32 v182, v179
	v_cvt_f32_ubyte1_e32 v181, v179
	v_cvt_f32_ubyte0_e32 v180, v179
	v_pk_add_f32 v[178:179], v[182:183], 0.5 op_sel_hi:[1,0]
	v_add_f32_e32 v156, 0.5, v156
	v_pk_mul_f32 v[178:179], v[178:179], v[188:189]
	v_pk_add_f32 v[180:181], v[180:181], 0.5 op_sel_hi:[1,0]
	v_pk_mul_f32 v[86:87], v[86:87], v[178:179]
	v_rcp_f32_e32 v178, v156
	v_cvt_f32_ubyte0_e32 v156, v177
	v_pk_mul_f32 v[180:181], v[180:181], v[184:185]
	v_add_f32_e32 v156, 0.5, v156
	v_pk_mul_f32 v[84:85], v[84:85], v[180:181]
	v_rcp_f32_e32 v180, v156
	v_cvt_f32_ubyte1_e32 v156, v176
	v_add_f32_e32 v156, 0.5, v156
	v_rcp_f32_e32 v179, v156
	v_cvt_f32_ubyte1_e32 v156, v177
	v_add_f32_e32 v156, 0.5, v156
	v_rcp_f32_e32 v181, v156
	v_cvt_f32_ubyte2_e32 v156, v176
	v_add_f32_e32 v156, 0.5, v156
	v_rcp_f32_e32 v182, v156
	v_cvt_f32_ubyte2_e32 v156, v177
	v_add_f32_e32 v156, 0.5, v156
	v_rcp_f32_e32 v184, v156
	v_cvt_f32_ubyte3_e32 v156, v176
	v_add_f32_e32 v156, 0.5, v156
	v_rcp_f32_e32 v183, v156
	v_cvt_f32_ubyte3_e32 v156, v177
	v_add_f32_e32 v156, 0.5, v156
	v_cvt_f32_ubyte1_e32 v177, v174
	v_cvt_f32_ubyte0_e32 v176, v174
	v_cvt_f32_ubyte3_e32 v187, v174
	v_cvt_f32_ubyte2_e32 v186, v174
	v_rcp_f32_e32 v185, v156
	v_pk_add_f32 v[186:187], v[186:187], 0.5 op_sel_hi:[1,0]
	v_pk_add_f32 v[176:177], v[176:177], 0.5 op_sel_hi:[1,0]
	v_cvt_f32_ubyte0_e32 v156, v172
	v_pk_mul_f32 v[176:177], v[176:177], v[178:179]
	v_pk_mul_f32 v[178:179], v[186:187], v[182:183]
	v_pk_mul_f32 v[112:113], v[112:113], v[176:177]
	v_pk_mul_f32 v[114:115], v[114:115], v[178:179]
	v_cvt_f32_ubyte3_e32 v179, v175
	v_cvt_f32_ubyte2_e32 v178, v175
	v_cvt_f32_ubyte1_e32 v177, v175
	v_cvt_f32_ubyte0_e32 v176, v175
	v_pk_add_f32 v[174:175], v[178:179], 0.5 op_sel_hi:[1,0]
	v_add_f32_e32 v156, 0.5, v156
	v_pk_mul_f32 v[174:175], v[174:175], v[184:185]
	v_pk_add_f32 v[176:177], v[176:177], 0.5 op_sel_hi:[1,0]
	v_pk_mul_f32 v[118:119], v[118:119], v[174:175]
	v_rcp_f32_e32 v174, v156
	v_cvt_f32_ubyte0_e32 v156, v173
	v_pk_mul_f32 v[176:177], v[176:177], v[180:181]
	v_add_f32_e32 v156, 0.5, v156
	v_pk_mul_f32 v[116:117], v[116:117], v[176:177]
	v_rcp_f32_e32 v176, v156
	v_cvt_f32_ubyte1_e32 v156, v172
	v_add_f32_e32 v156, 0.5, v156
	v_rcp_f32_e32 v175, v156
	v_cvt_f32_ubyte1_e32 v156, v173
	v_add_f32_e32 v156, 0.5, v156
	v_rcp_f32_e32 v177, v156
	v_cvt_f32_ubyte2_e32 v156, v172
	v_add_f32_e32 v156, 0.5, v156
	v_rcp_f32_e32 v178, v156
	v_cvt_f32_ubyte2_e32 v156, v173
	v_add_f32_e32 v156, 0.5, v156
	v_rcp_f32_e32 v180, v156
	v_cvt_f32_ubyte3_e32 v156, v172
	v_add_f32_e32 v156, 0.5, v156
	v_rcp_f32_e32 v179, v156
	v_cvt_f32_ubyte3_e32 v156, v173
	v_add_f32_e32 v156, 0.5, v156
	v_cvt_f32_ubyte1_e32 v173, v170
	v_cvt_f32_ubyte0_e32 v172, v170
	v_cvt_f32_ubyte3_e32 v183, v170
	v_cvt_f32_ubyte2_e32 v182, v170
	v_rcp_f32_e32 v181, v156
	v_pk_add_f32 v[182:183], v[182:183], 0.5 op_sel_hi:[1,0]
	v_pk_add_f32 v[172:173], v[172:173], 0.5 op_sel_hi:[1,0]
	v_cvt_f32_ubyte0_e32 v156, v146
	v_pk_mul_f32 v[172:173], v[172:173], v[174:175]
	v_pk_mul_f32 v[174:175], v[182:183], v[178:179]
	v_pk_mul_f32 v[88:89], v[88:89], v[172:173]
	v_pk_mul_f32 v[90:91], v[90:91], v[174:175]
	v_cvt_f32_ubyte3_e32 v175, v171
	v_cvt_f32_ubyte2_e32 v174, v171
	v_cvt_f32_ubyte1_e32 v173, v171
	v_cvt_f32_ubyte0_e32 v172, v171
	v_pk_add_f32 v[170:171], v[174:175], 0.5 op_sel_hi:[1,0]
	v_add_f32_e32 v156, 0.5, v156
	v_pk_mul_f32 v[170:171], v[170:171], v[180:181]
	v_pk_add_f32 v[172:173], v[172:173], 0.5 op_sel_hi:[1,0]
	v_pk_mul_f32 v[94:95], v[94:95], v[170:171]
	v_rcp_f32_e32 v170, v156
	v_cvt_f32_ubyte0_e32 v156, v147
	v_pk_mul_f32 v[172:173], v[172:173], v[176:177]
	v_add_f32_e32 v156, 0.5, v156
	v_pk_mul_f32 v[92:93], v[92:93], v[172:173]
	v_rcp_f32_e32 v172, v156
	v_cvt_f32_ubyte1_e32 v156, v146
	v_add_f32_e32 v156, 0.5, v156
	v_rcp_f32_e32 v171, v156
	v_cvt_f32_ubyte1_e32 v156, v147
	v_add_f32_e32 v156, 0.5, v156
	v_rcp_f32_e32 v173, v156
	v_cvt_f32_ubyte2_e32 v156, v146
	v_cvt_f32_ubyte3_e32 v146, v146
	v_add_f32_e32 v156, 0.5, v156
	v_add_f32_e32 v146, 0.5, v146
	v_rcp_f32_e32 v174, v156
	v_rcp_f32_e32 v175, v146
	v_cvt_f32_ubyte3_e32 v146, v147
	v_cvt_f32_ubyte2_e32 v156, v147
	v_add_f32_e32 v146, 0.5, v146
	v_add_f32_e32 v156, 0.5, v156
	v_rcp_f32_e32 v177, v146
	v_cvt_f32_ubyte1_e32 v147, v144
	v_cvt_f32_ubyte0_e32 v146, v144
	v_cvt_f32_ubyte3_e32 v179, v144
	v_cvt_f32_ubyte2_e32 v178, v144
	v_rcp_f32_e32 v176, v156
	v_pk_add_f32 v[178:179], v[178:179], 0.5 op_sel_hi:[1,0]
	v_pk_add_f32 v[146:147], v[146:147], 0.5 op_sel_hi:[1,0]
	v_cvt_f32_ubyte2_e32 v156, v14
	v_pk_mul_f32 v[146:147], v[146:147], v[170:171]
	v_pk_mul_f32 v[170:171], v[178:179], v[174:175]
	v_pk_mul_f32 v[120:121], v[120:121], v[146:147]
	v_pk_mul_f32 v[122:123], v[122:123], v[170:171]
	v_cvt_f32_ubyte3_e32 v171, v145
	v_cvt_f32_ubyte2_e32 v170, v145
	v_cvt_f32_ubyte1_e32 v147, v145
	v_cvt_f32_ubyte0_e32 v146, v145
	v_pk_add_f32 v[144:145], v[170:171], 0.5 op_sel_hi:[1,0]
	v_pk_add_f32 v[146:147], v[146:147], 0.5 op_sel_hi:[1,0]
	v_pk_mul_f32 v[144:145], v[144:145], v[176:177]
	v_pk_mul_f32 v[146:147], v[146:147], v[172:173]
	v_pk_mul_f32 v[126:127], v[126:127], v[144:145]
	v_cvt_f32_ubyte0_e32 v145, v15
	v_add_f32_e32 v145, 0.5, v145
	v_pk_mul_f32 v[124:125], v[124:125], v[146:147]
	v_cvt_f32_ubyte0_e32 v144, v14
	v_rcp_f32_e32 v146, v145
	v_cvt_f32_ubyte1_e32 v145, v14
	v_cvt_f32_ubyte3_e32 v14, v14
	v_add_f32_e32 v144, 0.5, v144
	v_add_f32_e32 v145, 0.5, v145
	v_add_f32_e32 v156, 0.5, v156
	v_add_f32_e32 v14, 0.5, v14
	v_rcp_f32_e32 v144, v144
	v_rcp_f32_e32 v145, v145
	v_rcp_f32_e32 v170, v156
	v_rcp_f32_e32 v171, v14
	v_cvt_f32_ubyte3_e32 v14, v15
	v_cvt_f32_ubyte2_e32 v156, v15
	v_add_f32_e32 v14, 0.5, v14
	v_cvt_f32_ubyte1_e32 v147, v15
	v_add_f32_e32 v156, 0.5, v156
	v_rcp_f32_e32 v173, v14
	v_cvt_f32_ubyte1_e32 v15, v12
	v_cvt_f32_ubyte0_e32 v14, v12
	v_cvt_f32_ubyte3_e32 v175, v12
	v_cvt_f32_ubyte2_e32 v174, v12
	v_rcp_f32_e32 v172, v156
	v_pk_add_f32 v[174:175], v[174:175], 0.5 op_sel_hi:[1,0]
	v_pk_add_f32 v[14:15], v[14:15], 0.5 op_sel_hi:[1,0]
	v_add_f32_e32 v147, 0.5, v147
	v_pk_mul_f32 v[14:15], v[14:15], v[144:145]
	v_pk_mul_f32 v[144:145], v[174:175], v[170:171]
	v_rcp_f32_e32 v147, v147
	v_pk_mul_f32 v[98:99], v[98:99], v[144:145]
	v_cvt_f32_ubyte3_e32 v145, v13
	v_cvt_f32_ubyte2_e32 v144, v13
	v_pk_mul_f32 v[96:97], v[96:97], v[14:15]
	v_cvt_f32_ubyte1_e32 v15, v13
	v_cvt_f32_ubyte0_e32 v14, v13
	v_pk_add_f32 v[12:13], v[144:145], 0.5 op_sel_hi:[1,0]
	v_pk_add_f32 v[14:15], v[14:15], 0.5 op_sel_hi:[1,0]
	v_pk_mul_f32 v[12:13], v[12:13], v[172:173]
	v_pk_mul_f32 v[14:15], v[14:15], v[146:147]
	v_pk_mul_f32 v[102:103], v[102:103], v[12:13]
	v_cvt_f32_ubyte0_e32 v13, v11
	v_add_f32_e32 v13, 0.5, v13
	v_pk_mul_f32 v[100:101], v[100:101], v[14:15]
	v_cvt_f32_ubyte0_e32 v12, v10
	v_rcp_f32_e32 v14, v13
	v_cvt_f32_ubyte1_e32 v13, v10
	v_cvt_f32_ubyte2_e32 v144, v10
	v_cvt_f32_ubyte2_e32 v145, v11
	v_cvt_f32_ubyte3_e32 v10, v10
	v_add_f32_e32 v12, 0.5, v12
	v_add_f32_e32 v13, 0.5, v13
	v_add_f32_e32 v144, 0.5, v144
	v_add_f32_e32 v145, 0.5, v145
	v_add_f32_e32 v10, 0.5, v10
	v_rcp_f32_e32 v12, v12
	v_rcp_f32_e32 v13, v13
	v_rcp_f32_e32 v144, v144
	v_rcp_f32_e32 v146, v145
	v_rcp_f32_e32 v145, v10
	v_cvt_f32_ubyte3_e32 v10, v11
	v_add_f32_e32 v10, 0.5, v10
	v_cvt_f32_ubyte1_e32 v15, v11
	v_rcp_f32_e32 v147, v10
	v_cvt_f32_ubyte1_e32 v11, v8
	v_cvt_f32_ubyte0_e32 v10, v8
	v_cvt_f32_ubyte3_e32 v171, v8
	v_cvt_f32_ubyte2_e32 v170, v8
	v_pk_add_f32 v[170:171], v[170:171], 0.5 op_sel_hi:[1,0]
	v_pk_add_f32 v[10:11], v[10:11], 0.5 op_sel_hi:[1,0]
	v_add_f32_e32 v15, 0.5, v15
	v_pk_mul_f32 v[10:11], v[10:11], v[12:13]
	v_pk_mul_f32 v[12:13], v[170:171], v[144:145]
	v_rcp_f32_e32 v15, v15
	v_pk_mul_f32 v[130:131], v[130:131], v[12:13]
	v_cvt_f32_ubyte3_e32 v13, v9
	v_cvt_f32_ubyte2_e32 v12, v9
	v_pk_mul_f32 v[128:129], v[128:129], v[10:11]
	v_cvt_f32_ubyte1_e32 v11, v9
	v_cvt_f32_ubyte0_e32 v10, v9
	v_pk_add_f32 v[8:9], v[12:13], 0.5 op_sel_hi:[1,0]
	v_pk_add_f32 v[10:11], v[10:11], 0.5 op_sel_hi:[1,0]
	v_pk_mul_f32 v[8:9], v[8:9], v[146:147]
	v_pk_mul_f32 v[10:11], v[10:11], v[14:15]
	v_pk_mul_f32 v[134:135], v[134:135], v[8:9]
	v_cvt_f32_ubyte0_e32 v9, v5
	v_add_f32_e32 v9, 0.5, v9
	v_pk_mul_f32 v[132:133], v[132:133], v[10:11]
	v_cvt_f32_ubyte0_e32 v8, v4
	v_rcp_f32_e32 v10, v9
	v_cvt_f32_ubyte1_e32 v9, v4
	v_cvt_f32_ubyte2_e32 v12, v4
	v_cvt_f32_ubyte2_e32 v13, v5
	v_cvt_f32_ubyte3_e32 v4, v4
	v_add_f32_e32 v8, 0.5, v8
	v_add_f32_e32 v9, 0.5, v9
	v_add_f32_e32 v12, 0.5, v12
	v_add_f32_e32 v13, 0.5, v13
	v_add_f32_e32 v4, 0.5, v4
	v_rcp_f32_e32 v8, v8
	v_rcp_f32_e32 v9, v9
	v_rcp_f32_e32 v12, v12
	v_rcp_f32_e32 v14, v13
	v_rcp_f32_e32 v13, v4
	v_cvt_f32_ubyte3_e32 v4, v5
	v_add_f32_e32 v4, 0.5, v4
	v_cvt_f32_ubyte1_e32 v11, v5
	v_rcp_f32_e32 v15, v4
	v_cvt_f32_ubyte1_e32 v5, v2
	v_cvt_f32_ubyte0_e32 v4, v2
	v_cvt_f32_ubyte3_e32 v145, v2
	v_cvt_f32_ubyte2_e32 v144, v2
	v_pk_add_f32 v[144:145], v[144:145], 0.5 op_sel_hi:[1,0]
	v_pk_add_f32 v[4:5], v[4:5], 0.5 op_sel_hi:[1,0]
	v_add_f32_e32 v11, 0.5, v11
	v_pk_mul_f32 v[4:5], v[4:5], v[8:9]
	v_pk_mul_f32 v[8:9], v[144:145], v[12:13]
	v_rcp_f32_e32 v11, v11
	v_pk_mul_f32 v[106:107], v[106:107], v[8:9]
	v_cvt_f32_ubyte3_e32 v9, v3
	v_cvt_f32_ubyte2_e32 v8, v3
	v_pk_mul_f32 v[104:105], v[104:105], v[4:5]
	v_cvt_f32_ubyte1_e32 v5, v3
	v_cvt_f32_ubyte0_e32 v4, v3
	v_pk_add_f32 v[2:3], v[8:9], 0.5 op_sel_hi:[1,0]
	v_pk_add_f32 v[4:5], v[4:5], 0.5 op_sel_hi:[1,0]
	v_pk_mul_f32 v[2:3], v[2:3], v[14:15]
	v_pk_mul_f32 v[4:5], v[4:5], v[10:11]
	v_pk_mul_f32 v[110:111], v[110:111], v[2:3]
	v_cvt_f32_ubyte0_e32 v3, v7
	v_add_f32_e32 v3, 0.5, v3
	v_pk_mul_f32 v[108:109], v[108:109], v[4:5]
	v_cvt_f32_ubyte0_e32 v2, v6
	v_rcp_f32_e32 v4, v3
	v_cvt_f32_ubyte1_e32 v3, v6
	v_cvt_f32_ubyte2_e32 v8, v6
	v_cvt_f32_ubyte2_e32 v9, v7
	v_cvt_f32_ubyte3_e32 v6, v6
	v_add_f32_e32 v2, 0.5, v2
	v_add_f32_e32 v3, 0.5, v3
	v_add_f32_e32 v8, 0.5, v8
	v_add_f32_e32 v9, 0.5, v9
	v_add_f32_e32 v6, 0.5, v6
	v_rcp_f32_e32 v2, v2
	v_rcp_f32_e32 v3, v3
	v_rcp_f32_e32 v8, v8
	v_rcp_f32_e32 v10, v9
	v_rcp_f32_e32 v9, v6
	v_cvt_f32_ubyte3_e32 v6, v7
	v_cvt_f32_ubyte1_e32 v5, v7
	v_add_f32_e32 v6, 0.5, v6
	v_add_f32_e32 v5, 0.5, v5
	v_rcp_f32_e32 v11, v6
	v_cvt_f32_ubyte1_e32 v7, v0
	v_cvt_f32_ubyte0_e32 v6, v0
	v_cvt_f32_ubyte3_e32 v13, v0
	v_cvt_f32_ubyte2_e32 v12, v0
	v_rcp_f32_e32 v5, v5
	v_pk_add_f32 v[12:13], v[12:13], 0.5 op_sel_hi:[1,0]
	v_pk_add_f32 v[6:7], v[6:7], 0.5 op_sel_hi:[1,0]
	s_nop 0
	v_pk_mul_f32 v[2:3], v[6:7], v[2:3]
	v_pk_mul_f32 v[6:7], v[12:13], v[8:9]
	v_pk_mul_f32 v[136:137], v[136:137], v[2:3]
	v_pk_mul_f32 v[138:139], v[138:139], v[6:7]
	v_cvt_f32_ubyte1_e32 v3, v1
	v_cvt_f32_ubyte0_e32 v2, v1
	v_cvt_f32_ubyte3_e32 v7, v1
	v_cvt_f32_ubyte2_e32 v6, v1
	v_pk_add_f32 v[0:1], v[6:7], 0.5 op_sel_hi:[1,0]
	v_pk_add_f32 v[2:3], v[2:3], 0.5 op_sel_hi:[1,0]
	v_pk_mul_f32 v[0:1], v[0:1], v[10:11]
	v_pk_mul_f32 v[2:3], v[2:3], v[4:5]
	v_pk_mul_f32 v[142:143], v[142:143], v[0:1]
	v_pk_mul_f32 v[140:141], v[140:141], v[2:3]
	ds_read_b128 v[8:11], v231
	ds_read_b128 v[12:15], v231 offset:1024
	ds_read_b128 v[0:3], v231 offset:2048
	ds_read_b128 v[4:7], v231 offset:3072
	s_add_u32 s2, s48, 0x40480
	s_addc_u32 s3, s49, 0
	s_mov_b32 m0, s94
	v_lshl_add_u64 v[144:145], s[2:3], 0, v[148:149]
	ds_read_b128 v[174:177], v228
	ds_read_b128 v[178:181], v228 offset:1024
	ds_read_b128 v[182:185], v228 offset:2048
	ds_read_b128 v[186:189], v228 offset:3072
	ds_read_b128 v[190:193], v228 offset:4096
	ds_read_b128 v[194:197], v228 offset:5120
	ds_read_b128 v[198:201], v228 offset:6144
	ds_read_b128 v[202:205], v228 offset:7168
	global_load_lds_dwordx4 v[144:145], off
	v_lshl_add_u64 v[144:145], s[2:3], 0, v[152:153]
	s_mov_b32 m0, s93
	s_nop 0
	global_load_lds_dwordx4 v[144:145], off
	s_waitcnt lgkmcnt(8)
	s_barrier
	s_waitcnt lgkmcnt(0)
	s_setprio 1
	s_waitcnt lgkmcnt(0)
	v_mfma_f32_16x16x128_f8f6f4 v[16:19], v[8:15], v[174:181], v[16:19]
	v_mfma_f32_16x16x128_f8f6f4 v[20:23], v[0:7], v[174:181], v[20:23]
	v_mfma_f32_16x16x128_f8f6f4 v[24:27], v[8:15], v[182:189], v[24:27]
	v_mfma_f32_16x16x128_f8f6f4 v[28:31], v[0:7], v[182:189], v[28:31]
	v_mfma_f32_16x16x128_f8f6f4 v[32:35], v[8:15], v[190:197], v[32:35]
	v_mfma_f32_16x16x128_f8f6f4 v[36:39], v[0:7], v[190:197], v[36:39]
	v_mfma_f32_16x16x128_f8f6f4 v[40:43], v[8:15], v[198:205], v[40:43]
	v_mfma_f32_16x16x128_f8f6f4 v[44:47], v[0:7], v[198:205], v[44:47]
	s_setprio 0
	s_barrier
	v_lshl_add_u64 v[170:171], s[50:51], 0, v[150:151]
	s_mov_b32 m0, s96
	v_lshl_add_u64 v[144:145], v[170:171], 0, s[22:23]
	v_lshl_add_u64 v[172:173], s[50:51], 0, v[154:155]
	ds_read_b128 v[206:209], v232
	ds_read_b128 v[210:213], v232 offset:1024
	ds_read_b128 v[214:217], v232 offset:2048
	ds_read_b128 v[218:221], v232 offset:3072
	global_load_lds_dwordx4 v[144:145], off
	v_lshl_add_u64 v[144:145], v[172:173], 0, s[22:23]
	s_mov_b32 m0, s95
	s_nop 0
	global_load_lds_dwordx4 v[144:145], off
	s_barrier
	s_waitcnt lgkmcnt(0)
	s_setprio 1
	s_waitcnt lgkmcnt(0)
	v_mfma_f32_16x16x128_f8f6f4 v[48:51], v[206:213], v[174:181], v[48:51]
	v_mfma_f32_16x16x128_f8f6f4 v[52:55], v[214:221], v[174:181], v[52:55]
	v_mfma_f32_16x16x128_f8f6f4 v[56:59], v[206:213], v[182:189], v[56:59]
	v_mfma_f32_16x16x128_f8f6f4 v[60:63], v[214:221], v[182:189], v[60:63]
	v_mfma_f32_16x16x128_f8f6f4 v[64:67], v[206:213], v[190:197], v[64:67]
	v_mfma_f32_16x16x128_f8f6f4 v[68:71], v[214:221], v[190:197], v[68:71]
	v_mfma_f32_16x16x128_f8f6f4 v[72:75], v[206:213], v[198:205], v[72:75]
	v_mfma_f32_16x16x128_f8f6f4 v[76:79], v[214:221], v[198:205], v[76:79]
	s_setprio 0
	v_lshl_add_u64 v[174:175], s[48:49], 0, v[148:149]
	s_mov_b32 m0, s73
	v_lshl_add_u64 v[144:145], v[174:175], 0, s[22:23]
	s_barrier
	ds_read_b128 v[176:179], v228 offset:16384
	ds_read_b128 v[180:183], v228 offset:17408
	ds_read_b128 v[184:187], v228 offset:18432
	ds_read_b128 v[188:191], v228 offset:19456
	ds_read_b128 v[192:195], v228 offset:20480
	ds_read_b128 v[196:199], v228 offset:21504
	ds_read_b128 v[236:239], v228 offset:22528
	ds_read_b128 v[240:243], v228 offset:23552
	global_load_lds_dwordx4 v[144:145], off
	v_lshl_add_u64 v[144:145], v[168:169], 0, s[22:23]
	s_mov_b32 m0, s74
	s_nop 0
	global_load_lds_dwordx4 v[144:145], off
	s_barrier
	s_waitcnt lgkmcnt(0)
	s_setprio 1
	s_waitcnt lgkmcnt(0)
	v_mfma_f32_16x16x128_f8f6f4 v[80:83], v[8:15], v[176:183], v[80:83]
	v_mfma_f32_16x16x128_f8f6f4 v[84:87], v[0:7], v[176:183], v[84:87]
	v_mfma_f32_16x16x128_f8f6f4 v[88:91], v[8:15], v[184:191], v[88:91]
	v_mfma_f32_16x16x128_f8f6f4 v[92:95], v[0:7], v[184:191], v[92:95]
	v_mfma_f32_16x16x128_f8f6f4 v[96:99], v[8:15], v[192:199], v[96:99]
	v_mfma_f32_16x16x128_f8f6f4 v[100:103], v[0:7], v[192:199], v[100:103]
	v_mfma_f32_16x16x128_f8f6f4 v[104:107], v[8:15], v[236:243], v[104:107]
	v_mfma_f32_16x16x128_f8f6f4 v[108:111], v[0:7], v[236:243], v[108:111]
	s_setprio 0
	s_barrier
	s_add_u32 s2, s50, 0x40500
	s_addc_u32 s3, s51, 0
	s_mov_b32 m0, s97
	v_lshl_add_u64 v[0:1], s[2:3], 0, v[150:151]
	global_load_lds_dwordx4 v[0:1], off
	v_lshl_add_u64 v[0:1], s[2:3], 0, v[154:155]
	s_mov_b32 m0, s52
	s_nop 0
	global_load_lds_dwordx4 v[0:1], off
	s_waitcnt vmcnt(6)
	s_barrier
	s_setprio 1
	v_mfma_f32_16x16x128_f8f6f4 v[112:115], v[206:213], v[176:183], v[112:115]
	v_mfma_f32_16x16x128_f8f6f4 v[116:119], v[214:221], v[176:183], v[116:119]
	v_mfma_f32_16x16x128_f8f6f4 v[120:123], v[206:213], v[184:191], v[120:123]
	v_mfma_f32_16x16x128_f8f6f4 v[124:127], v[214:221], v[184:191], v[124:127]
	v_mfma_f32_16x16x128_f8f6f4 v[128:131], v[206:213], v[192:199], v[128:131]
	v_mfma_f32_16x16x128_f8f6f4 v[132:135], v[214:221], v[192:199], v[132:135]
	v_mfma_f32_16x16x128_f8f6f4 v[136:139], v[206:213], v[236:243], v[136:139]
	v_mfma_f32_16x16x128_f8f6f4 v[140:143], v[214:221], v[236:243], v[140:143]
	s_setprio 0
	s_barrier
	ds_read_b128 v[0:3], v235
	ds_read_b128 v[4:7], v235 offset:1024
	ds_read_b128 v[8:11], v235 offset:2048
	ds_read_b128 v[12:15], v235 offset:3072
	s_add_u32 s2, s48, 0x40500
	s_addc_u32 s3, s49, 0
	s_mov_b32 m0, s75
	v_lshl_add_u64 v[144:145], s[2:3], 0, v[148:149]
	ds_read_b128 v[176:179], v228 offset:32768
	ds_read_b128 v[180:183], v228 offset:33792
	ds_read_b128 v[184:187], v228 offset:34816
	ds_read_b128 v[188:191], v228 offset:35840
	ds_read_b128 v[192:195], v228 offset:36864
	ds_read_b128 v[196:199], v228 offset:37888
	ds_read_b128 v[200:203], v228 offset:38912
	ds_read_b128 v[204:207], v228 offset:39936
	global_load_lds_dwordx4 v[144:145], off
	v_lshl_add_u64 v[144:145], s[2:3], 0, v[152:153]
	s_mov_b32 m0, s76
	s_nop 0
	global_load_lds_dwordx4 v[144:145], off
	s_waitcnt lgkmcnt(8)
	s_barrier
	s_waitcnt lgkmcnt(0)
	s_setprio 1
	s_waitcnt lgkmcnt(0)
	v_mfma_f32_16x16x128_f8f6f4 v[16:19], v[0:7], v[176:183], v[16:19]
	v_mfma_f32_16x16x128_f8f6f4 v[20:23], v[8:15], v[176:183], v[20:23]
	v_mfma_f32_16x16x128_f8f6f4 v[24:27], v[0:7], v[184:191], v[24:27]
	v_mfma_f32_16x16x128_f8f6f4 v[28:31], v[8:15], v[184:191], v[28:31]
	v_mfma_f32_16x16x128_f8f6f4 v[32:35], v[0:7], v[192:199], v[32:35]
	v_mfma_f32_16x16x128_f8f6f4 v[36:39], v[8:15], v[192:199], v[36:39]
	v_mfma_f32_16x16x128_f8f6f4 v[40:43], v[0:7], v[200:207], v[40:43]
	v_mfma_f32_16x16x128_f8f6f4 v[44:47], v[8:15], v[200:207], v[44:47]
	s_setprio 0
	s_barrier
	s_mov_b32 m0, s62
	v_lshl_add_u64 v[144:145], v[170:171], 0, s[24:25]
	ds_read_b128 v[208:211], v234
	ds_read_b128 v[212:215], v234 offset:1024
	ds_read_b128 v[236:239], v234 offset:2048
	ds_read_b128 v[240:243], v234 offset:3072
	global_load_lds_dwordx4 v[144:145], off
	v_lshl_add_u64 v[144:145], v[172:173], 0, s[24:25]
	s_mov_b32 m0, s63
	s_nop 0
	global_load_lds_dwordx4 v[144:145], off
	s_barrier
	s_waitcnt lgkmcnt(0)
	s_setprio 1
	s_waitcnt lgkmcnt(0)
	v_mfma_f32_16x16x128_f8f6f4 v[48:51], v[208:215], v[176:183], v[48:51]
	v_mfma_f32_16x16x128_f8f6f4 v[52:55], v[236:243], v[176:183], v[52:55]
	v_mfma_f32_16x16x128_f8f6f4 v[56:59], v[208:215], v[184:191], v[56:59]
	v_mfma_f32_16x16x128_f8f6f4 v[60:63], v[236:243], v[184:191], v[60:63]
	v_mfma_f32_16x16x128_f8f6f4 v[64:67], v[208:215], v[192:199], v[64:67]
	v_mfma_f32_16x16x128_f8f6f4 v[68:71], v[236:243], v[192:199], v[68:71]
	v_mfma_f32_16x16x128_f8f6f4 v[72:75], v[208:215], v[200:207], v[72:75]
	v_mfma_f32_16x16x128_f8f6f4 v[76:79], v[236:243], v[200:207], v[76:79]
	s_setprio 0
	s_mov_b32 m0, s80
	v_lshl_add_u64 v[144:145], v[174:175], 0, s[24:25]
	s_barrier
	ds_read_b128 v[176:179], v228 offset:49152
	ds_read_b128 v[180:183], v228 offset:50176
	ds_read_b128 v[184:187], v228 offset:51200
	ds_read_b128 v[188:191], v228 offset:52224
	ds_read_b128 v[192:195], v228 offset:53248
	ds_read_b128 v[196:199], v228 offset:54272
	ds_read_b128 v[200:203], v228 offset:55296
	ds_read_b128 v[204:207], v228 offset:56320
	global_load_lds_dwordx4 v[144:145], off
	v_lshl_add_u64 v[144:145], v[168:169], 0, s[24:25]
	s_mov_b32 m0, s81
	s_nop 0
	global_load_lds_dwordx4 v[144:145], off
	s_barrier
	s_waitcnt lgkmcnt(0)
	s_setprio 1
	s_waitcnt lgkmcnt(0)
	v_mfma_f32_16x16x128_f8f6f4 v[80:83], v[0:7], v[176:183], v[80:83]
	v_mfma_f32_16x16x128_f8f6f4 v[84:87], v[8:15], v[176:183], v[84:87]
	v_mfma_f32_16x16x128_f8f6f4 v[88:91], v[0:7], v[184:191], v[88:91]
	v_mfma_f32_16x16x128_f8f6f4 v[92:95], v[8:15], v[184:191], v[92:95]
	v_mfma_f32_16x16x128_f8f6f4 v[96:99], v[0:7], v[192:199], v[96:99]
	v_mfma_f32_16x16x128_f8f6f4 v[100:103], v[8:15], v[192:199], v[100:103]
	v_mfma_f32_16x16x128_f8f6f4 v[104:107], v[0:7], v[200:207], v[104:107]
	v_mfma_f32_16x16x128_f8f6f4 v[108:111], v[8:15], v[200:207], v[108:111]
	s_setprio 0
	s_barrier
	s_add_u32 s2, s50, 0x40580
	s_addc_u32 s3, s51, 0
	s_mov_b32 m0, s53
	v_lshl_add_u64 v[0:1], s[2:3], 0, v[150:151]
	global_load_lds_dwordx4 v[0:1], off
	v_lshl_add_u64 v[0:1], s[2:3], 0, v[154:155]
	s_mov_b32 m0, s64
	s_nop 0
	global_load_lds_dwordx4 v[0:1], off
	s_waitcnt vmcnt(6)
	s_barrier
	s_setprio 1
	v_mfma_f32_16x16x128_f8f6f4 v[112:115], v[208:215], v[176:183], v[112:115]
	v_mfma_f32_16x16x128_f8f6f4 v[116:119], v[236:243], v[176:183], v[116:119]
	v_mfma_f32_16x16x128_f8f6f4 v[120:123], v[208:215], v[184:191], v[120:123]
	v_mfma_f32_16x16x128_f8f6f4 v[124:127], v[236:243], v[184:191], v[124:127]
	v_mfma_f32_16x16x128_f8f6f4 v[128:131], v[208:215], v[192:199], v[128:131]
	v_mfma_f32_16x16x128_f8f6f4 v[132:135], v[236:243], v[192:199], v[132:135]
	v_mfma_f32_16x16x128_f8f6f4 v[136:139], v[208:215], v[200:207], v[136:139]
	v_mfma_f32_16x16x128_f8f6f4 v[140:143], v[236:243], v[200:207], v[140:143]
	s_setprio 0
	s_barrier
	ds_read_b128 v[0:3], v231
	ds_read_b128 v[4:7], v231 offset:1024
	ds_read_b128 v[8:11], v231 offset:2048
	ds_read_b128 v[12:15], v231 offset:3072
	s_add_u32 s2, s48, 0x40580
	s_addc_u32 s3, s49, 0
	s_mov_b32 m0, s94
	v_lshl_add_u64 v[144:145], s[2:3], 0, v[148:149]
	ds_read_b128 v[176:179], v228
	ds_read_b128 v[180:183], v228 offset:1024
	ds_read_b128 v[184:187], v228 offset:2048
	ds_read_b128 v[188:191], v228 offset:3072
	ds_read_b128 v[192:195], v228 offset:4096
	ds_read_b128 v[196:199], v228 offset:5120
	ds_read_b128 v[200:203], v228 offset:6144
	ds_read_b128 v[204:207], v228 offset:7168
	global_load_lds_dwordx4 v[144:145], off
	v_lshl_add_u64 v[144:145], s[2:3], 0, v[152:153]
	s_mov_b32 m0, s93
	s_nop 0
	global_load_lds_dwordx4 v[144:145], off
	s_waitcnt lgkmcnt(8)
	s_barrier
	s_waitcnt lgkmcnt(0)
	s_setprio 1
	s_waitcnt lgkmcnt(0)
	v_mfma_f32_16x16x128_f8f6f4 v[16:19], v[0:7], v[176:183], v[16:19]
	v_mfma_f32_16x16x128_f8f6f4 v[20:23], v[8:15], v[176:183], v[20:23]
	v_mfma_f32_16x16x128_f8f6f4 v[24:27], v[0:7], v[184:191], v[24:27]
	v_mfma_f32_16x16x128_f8f6f4 v[28:31], v[8:15], v[184:191], v[28:31]
	v_mfma_f32_16x16x128_f8f6f4 v[32:35], v[0:7], v[192:199], v[32:35]
	v_mfma_f32_16x16x128_f8f6f4 v[36:39], v[8:15], v[192:199], v[36:39]
	v_mfma_f32_16x16x128_f8f6f4 v[40:43], v[0:7], v[200:207], v[40:43]
	v_mfma_f32_16x16x128_f8f6f4 v[44:47], v[8:15], v[200:207], v[44:47]
	s_setprio 0
	s_barrier
	s_mov_b32 m0, s96
	v_lshl_add_u64 v[144:145], v[170:171], 0, s[26:27]
	ds_read_b128 v[208:211], v232
	ds_read_b128 v[212:215], v232 offset:1024
	ds_read_b128 v[236:239], v232 offset:2048
	ds_read_b128 v[240:243], v232 offset:3072
	global_load_lds_dwordx4 v[144:145], off
	v_lshl_add_u64 v[144:145], v[172:173], 0, s[26:27]
	s_mov_b32 m0, s95
	s_nop 0
	global_load_lds_dwordx4 v[144:145], off
	s_barrier
	s_waitcnt lgkmcnt(0)
	s_setprio 1
	s_waitcnt lgkmcnt(0)
	v_mfma_f32_16x16x128_f8f6f4 v[48:51], v[208:215], v[176:183], v[48:51]
	v_mfma_f32_16x16x128_f8f6f4 v[52:55], v[236:243], v[176:183], v[52:55]
	v_mfma_f32_16x16x128_f8f6f4 v[56:59], v[208:215], v[184:191], v[56:59]
	v_mfma_f32_16x16x128_f8f6f4 v[60:63], v[236:243], v[184:191], v[60:63]
	v_mfma_f32_16x16x128_f8f6f4 v[64:67], v[208:215], v[192:199], v[64:67]
	v_mfma_f32_16x16x128_f8f6f4 v[68:71], v[236:243], v[192:199], v[68:71]
	v_mfma_f32_16x16x128_f8f6f4 v[72:75], v[208:215], v[200:207], v[72:75]
	v_mfma_f32_16x16x128_f8f6f4 v[76:79], v[236:243], v[200:207], v[76:79]
	s_setprio 0
	s_mov_b32 m0, s73
	v_lshl_add_u64 v[144:145], v[174:175], 0, s[26:27]
	s_barrier
	ds_read_b128 v[176:179], v228 offset:16384
	ds_read_b128 v[180:183], v228 offset:17408
	ds_read_b128 v[184:187], v228 offset:18432
	ds_read_b128 v[188:191], v228 offset:19456
	ds_read_b128 v[192:195], v228 offset:20480
	ds_read_b128 v[196:199], v228 offset:21504
	ds_read_b128 v[200:203], v228 offset:22528
	ds_read_b128 v[204:207], v228 offset:23552
	global_load_lds_dwordx4 v[144:145], off
	v_lshl_add_u64 v[144:145], v[168:169], 0, s[26:27]
	s_mov_b32 m0, s74
	s_nop 0
	global_load_lds_dwordx4 v[144:145], off
	s_barrier
	s_waitcnt lgkmcnt(0)
	s_setprio 1
	s_waitcnt lgkmcnt(0)
	v_mfma_f32_16x16x128_f8f6f4 v[80:83], v[0:7], v[176:183], v[80:83]
	v_mfma_f32_16x16x128_f8f6f4 v[84:87], v[8:15], v[176:183], v[84:87]
	v_mfma_f32_16x16x128_f8f6f4 v[88:91], v[0:7], v[184:191], v[88:91]
	v_mfma_f32_16x16x128_f8f6f4 v[92:95], v[8:15], v[184:191], v[92:95]
	v_mfma_f32_16x16x128_f8f6f4 v[96:99], v[0:7], v[192:199], v[96:99]
	v_mfma_f32_16x16x128_f8f6f4 v[100:103], v[8:15], v[192:199], v[100:103]
	v_mfma_f32_16x16x128_f8f6f4 v[104:107], v[0:7], v[200:207], v[104:107]
	v_mfma_f32_16x16x128_f8f6f4 v[108:111], v[8:15], v[200:207], v[108:111]
	s_setprio 0
	s_barrier
	s_add_u32 s2, s50, 0x40600
	s_addc_u32 s3, s51, 0
	s_mov_b32 m0, s97
	v_lshl_add_u64 v[0:1], s[2:3], 0, v[150:151]
	global_load_lds_dwordx4 v[0:1], off
	v_lshl_add_u64 v[0:1], s[2:3], 0, v[154:155]
	s_mov_b32 m0, s52
	s_nop 0
	global_load_lds_dwordx4 v[0:1], off
	s_waitcnt vmcnt(6)
	s_barrier
	s_setprio 1
	v_mfma_f32_16x16x128_f8f6f4 v[112:115], v[208:215], v[176:183], v[112:115]
	v_mfma_f32_16x16x128_f8f6f4 v[116:119], v[236:243], v[176:183], v[116:119]
	v_mfma_f32_16x16x128_f8f6f4 v[120:123], v[208:215], v[184:191], v[120:123]
	v_mfma_f32_16x16x128_f8f6f4 v[124:127], v[236:243], v[184:191], v[124:127]
	v_mfma_f32_16x16x128_f8f6f4 v[128:131], v[208:215], v[192:199], v[128:131]
	v_mfma_f32_16x16x128_f8f6f4 v[132:135], v[236:243], v[192:199], v[132:135]
	v_mfma_f32_16x16x128_f8f6f4 v[136:139], v[208:215], v[200:207], v[136:139]
	v_mfma_f32_16x16x128_f8f6f4 v[140:143], v[236:243], v[200:207], v[140:143]
	s_setprio 0
	s_barrier
	ds_read_b128 v[0:3], v235
	ds_read_b128 v[4:7], v235 offset:1024
	ds_read_b128 v[8:11], v235 offset:2048
	ds_read_b128 v[12:15], v235 offset:3072
	s_add_u32 s2, s48, 0x40600
	s_addc_u32 s3, s49, 0
	s_mov_b32 m0, s75
	v_lshl_add_u64 v[144:145], s[2:3], 0, v[148:149]
	ds_read_b128 v[176:179], v228 offset:32768
	ds_read_b128 v[180:183], v228 offset:33792
	ds_read_b128 v[184:187], v228 offset:34816
	ds_read_b128 v[188:191], v228 offset:35840
	ds_read_b128 v[192:195], v228 offset:36864
	ds_read_b128 v[196:199], v228 offset:37888
	ds_read_b128 v[200:203], v228 offset:38912
	ds_read_b128 v[204:207], v228 offset:39936
	global_load_lds_dwordx4 v[144:145], off
	v_lshl_add_u64 v[144:145], s[2:3], 0, v[152:153]
	s_mov_b32 m0, s76
	s_nop 0
	global_load_lds_dwordx4 v[144:145], off
	s_waitcnt lgkmcnt(8)
	s_barrier
	s_waitcnt lgkmcnt(0)
	s_setprio 1
	s_waitcnt lgkmcnt(0)
	v_mfma_f32_16x16x128_f8f6f4 v[16:19], v[0:7], v[176:183], v[16:19]
	v_mfma_f32_16x16x128_f8f6f4 v[20:23], v[8:15], v[176:183], v[20:23]
	v_mfma_f32_16x16x128_f8f6f4 v[24:27], v[0:7], v[184:191], v[24:27]
	v_mfma_f32_16x16x128_f8f6f4 v[28:31], v[8:15], v[184:191], v[28:31]
	v_mfma_f32_16x16x128_f8f6f4 v[32:35], v[0:7], v[192:199], v[32:35]
	v_mfma_f32_16x16x128_f8f6f4 v[36:39], v[8:15], v[192:199], v[36:39]
	v_mfma_f32_16x16x128_f8f6f4 v[40:43], v[0:7], v[200:207], v[40:43]
	v_mfma_f32_16x16x128_f8f6f4 v[44:47], v[8:15], v[200:207], v[44:47]
	s_setprio 0
	s_barrier
	s_mov_b32 m0, s62
	v_lshl_add_u64 v[144:145], v[170:171], 0, s[28:29]
	ds_read_b128 v[208:211], v234
	ds_read_b128 v[212:215], v234 offset:1024
	ds_read_b128 v[236:239], v234 offset:2048
	ds_read_b128 v[240:243], v234 offset:3072
	global_load_lds_dwordx4 v[144:145], off
	v_lshl_add_u64 v[144:145], v[172:173], 0, s[28:29]
	s_mov_b32 m0, s63
	s_nop 0
	global_load_lds_dwordx4 v[144:145], off
	s_barrier
	s_waitcnt lgkmcnt(0)
	s_setprio 1
	s_waitcnt lgkmcnt(0)
	v_mfma_f32_16x16x128_f8f6f4 v[48:51], v[208:215], v[176:183], v[48:51]
	v_mfma_f32_16x16x128_f8f6f4 v[52:55], v[236:243], v[176:183], v[52:55]
	v_mfma_f32_16x16x128_f8f6f4 v[56:59], v[208:215], v[184:191], v[56:59]
	v_mfma_f32_16x16x128_f8f6f4 v[60:63], v[236:243], v[184:191], v[60:63]
	v_mfma_f32_16x16x128_f8f6f4 v[64:67], v[208:215], v[192:199], v[64:67]
	v_mfma_f32_16x16x128_f8f6f4 v[68:71], v[236:243], v[192:199], v[68:71]
	v_mfma_f32_16x16x128_f8f6f4 v[72:75], v[208:215], v[200:207], v[72:75]
	v_mfma_f32_16x16x128_f8f6f4 v[76:79], v[236:243], v[200:207], v[76:79]
	s_setprio 0
	s_mov_b32 m0, s80
	v_lshl_add_u64 v[144:145], v[174:175], 0, s[28:29]
	s_barrier
	ds_read_b128 v[176:179], v228 offset:49152
	ds_read_b128 v[180:183], v228 offset:50176
	ds_read_b128 v[184:187], v228 offset:51200
	ds_read_b128 v[188:191], v228 offset:52224
	ds_read_b128 v[192:195], v228 offset:53248
	ds_read_b128 v[196:199], v228 offset:54272
	ds_read_b128 v[200:203], v228 offset:55296
	ds_read_b128 v[204:207], v228 offset:56320
	global_load_lds_dwordx4 v[144:145], off
	v_lshl_add_u64 v[144:145], v[168:169], 0, s[28:29]
	s_mov_b32 m0, s81
	s_nop 0
	global_load_lds_dwordx4 v[144:145], off
	s_barrier
	s_waitcnt lgkmcnt(0)
	s_setprio 1
	s_waitcnt lgkmcnt(0)
	v_mfma_f32_16x16x128_f8f6f4 v[80:83], v[0:7], v[176:183], v[80:83]
	v_mfma_f32_16x16x128_f8f6f4 v[84:87], v[8:15], v[176:183], v[84:87]
	v_mfma_f32_16x16x128_f8f6f4 v[88:91], v[0:7], v[184:191], v[88:91]
	v_mfma_f32_16x16x128_f8f6f4 v[92:95], v[8:15], v[184:191], v[92:95]
	v_mfma_f32_16x16x128_f8f6f4 v[96:99], v[0:7], v[192:199], v[96:99]
	v_mfma_f32_16x16x128_f8f6f4 v[100:103], v[8:15], v[192:199], v[100:103]
	v_mfma_f32_16x16x128_f8f6f4 v[104:107], v[0:7], v[200:207], v[104:107]
	v_mfma_f32_16x16x128_f8f6f4 v[108:111], v[8:15], v[200:207], v[108:111]
	s_setprio 0
	s_barrier
	s_add_u32 s2, s50, 0x40680
	s_addc_u32 s3, s51, 0
	s_mov_b32 m0, s53
	v_lshl_add_u64 v[0:1], s[2:3], 0, v[150:151]
	global_load_lds_dwordx4 v[0:1], off
	v_lshl_add_u64 v[0:1], s[2:3], 0, v[154:155]
	s_mov_b32 m0, s64
	s_nop 0
	global_load_lds_dwordx4 v[0:1], off
	s_waitcnt vmcnt(6)
	s_barrier
	s_setprio 1
	v_mfma_f32_16x16x128_f8f6f4 v[112:115], v[208:215], v[176:183], v[112:115]
	v_mfma_f32_16x16x128_f8f6f4 v[116:119], v[236:243], v[176:183], v[116:119]
	v_mfma_f32_16x16x128_f8f6f4 v[120:123], v[208:215], v[184:191], v[120:123]
	v_mfma_f32_16x16x128_f8f6f4 v[124:127], v[236:243], v[184:191], v[124:127]
	v_mfma_f32_16x16x128_f8f6f4 v[128:131], v[208:215], v[192:199], v[128:131]
	v_mfma_f32_16x16x128_f8f6f4 v[132:135], v[236:243], v[192:199], v[132:135]
	v_mfma_f32_16x16x128_f8f6f4 v[136:139], v[208:215], v[200:207], v[136:139]
	v_mfma_f32_16x16x128_f8f6f4 v[140:143], v[236:243], v[200:207], v[140:143]
	s_setprio 0
	s_and_b64 s[2:3], vcc, exec
	s_cselect_b32 s61, s47, s51
	s_cselect_b32 s60, s46, s50
	s_add_i32 s2, s58, 16
	s_ashr_i32 s3, s2, 31
	v_mov_b32_e32 v156, v230
	s_lshl_b64 s[2:3], s[2:3], 16
	s_barrier
	s_nop 7
	s_nop 7
	s_nop 7
	s_add_u32 s2, s78, s2
	s_addc_u32 s3, s79, s3
	global_load_dwordx2 v[216:217], v156, s[56:57]
	global_load_dwordx2 v[236:237], v156, s[2:3]
	global_load_dwordx2 v[212:213], v156, s[56:57] offset:512
	global_load_dwordx2 v[214:215], v156, s[2:3] offset:512
	global_load_dwordx2 v[208:209], v156, s[56:57] offset:1024
	global_load_dwordx2 v[210:211], v156, s[2:3] offset:1024
	global_load_dwordx2 v[204:205], v156, s[56:57] offset:1536
	global_load_dwordx2 v[206:207], v156, s[2:3] offset:1536
	global_load_dwordx2 v[200:201], v156, s[56:57] offset:2048
	global_load_dwordx2 v[202:203], v156, s[2:3] offset:2048
	global_load_dwordx2 v[196:197], v156, s[56:57] offset:2560
	global_load_dwordx2 v[198:199], v156, s[2:3] offset:2560
	global_load_dwordx2 v[192:193], v156, s[56:57] offset:3072
	global_load_dwordx2 v[194:195], v156, s[2:3] offset:3072
	global_load_dwordx2 v[188:189], v156, s[56:57] offset:3584
	global_load_dwordx2 v[190:191], v156, s[2:3] offset:3584
	v_lshl_add_u64 v[0:1], s[56:57], 0, v[156:157]
	v_lshl_add_u64 v[2:3], s[2:3], 0, v[156:157]
	v_add_co_u32_e32 v0, vcc, s85, v0
	s_waitcnt vmcnt(0)
	v_cvt_f32_ubyte3_e32 v243, v216
	v_cvt_f32_ubyte0_e32 v156, v236
	v_add_f32_e32 v156, 0.5, v156
	v_rcp_f32_e32 v238, v156
	v_cvt_f32_ubyte0_e32 v156, v237
	v_add_f32_e32 v156, 0.5, v156
	v_rcp_f32_e32 v218, v156
	v_cvt_f32_ubyte1_e32 v156, v236
	v_add_f32_e32 v156, 0.5, v156
	v_rcp_f32_e32 v239, v156
	v_cvt_f32_ubyte1_e32 v156, v237
	v_add_f32_e32 v156, 0.5, v156
	v_rcp_f32_e32 v219, v156
	v_cvt_f32_ubyte2_e32 v156, v236
	v_add_f32_e32 v156, 0.5, v156
	v_rcp_f32_e32 v240, v156
	v_cvt_f32_ubyte2_e32 v156, v237
	v_add_f32_e32 v156, 0.5, v156
	v_rcp_f32_e32 v220, v156
	v_cvt_f32_ubyte3_e32 v156, v236
	v_add_f32_e32 v156, 0.5, v156
	v_rcp_f32_e32 v241, v156
	v_cvt_f32_ubyte3_e32 v156, v237
	v_add_f32_e32 v156, 0.5, v156
	v_cvt_f32_ubyte1_e32 v237, v216
	v_cvt_f32_ubyte0_e32 v236, v216
	v_cvt_f32_ubyte2_e32 v242, v216
	v_rcp_f32_e32 v221, v156
	v_pk_add_f32 v[242:243], v[242:243], 0.5 op_sel_hi:[1,0]
	v_pk_add_f32 v[236:237], v[236:237], 0.5 op_sel_hi:[1,0]
	v_cvt_f32_ubyte0_e32 v156, v214
	v_pk_mul_f32 v[236:237], v[236:237], v[238:239]
	v_pk_mul_f32 v[238:239], v[242:243], v[240:241]
	v_pk_mul_f32 v[16:17], v[16:17], v[236:237]
	v_pk_mul_f32 v[18:19], v[18:19], v[238:239]
	v_cvt_f32_ubyte3_e32 v239, v217
	v_cvt_f32_ubyte2_e32 v238, v217
	v_cvt_f32_ubyte1_e32 v237, v217
	v_cvt_f32_ubyte0_e32 v236, v217
	v_pk_add_f32 v[216:217], v[238:239], 0.5 op_sel_hi:[1,0]
	v_add_f32_e32 v156, 0.5, v156
	v_pk_mul_f32 v[216:217], v[216:217], v[220:221]
	v_pk_add_f32 v[236:237], v[236:237], 0.5 op_sel_hi:[1,0]
	v_pk_mul_f32 v[22:23], v[22:23], v[216:217]
	v_rcp_f32_e32 v216, v156
	v_cvt_f32_ubyte0_e32 v156, v215
	v_pk_mul_f32 v[218:219], v[236:237], v[218:219]
	v_add_f32_e32 v156, 0.5, v156
	v_pk_mul_f32 v[20:21], v[20:21], v[218:219]
	v_rcp_f32_e32 v218, v156
	v_cvt_f32_ubyte1_e32 v156, v214
	v_add_f32_e32 v156, 0.5, v156
	v_rcp_f32_e32 v217, v156
	v_cvt_f32_ubyte1_e32 v156, v215
	v_add_f32_e32 v156, 0.5, v156
	v_rcp_f32_e32 v219, v156
	v_cvt_f32_ubyte2_e32 v156, v214
	v_add_f32_e32 v156, 0.5, v156
	v_rcp_f32_e32 v220, v156
	v_cvt_f32_ubyte2_e32 v156, v215
	v_add_f32_e32 v156, 0.5, v156
	v_rcp_f32_e32 v236, v156
	v_cvt_f32_ubyte3_e32 v156, v214
	v_add_f32_e32 v156, 0.5, v156
	v_rcp_f32_e32 v221, v156
	v_cvt_f32_ubyte3_e32 v156, v215
	v_add_f32_e32 v156, 0.5, v156
	v_cvt_f32_ubyte1_e32 v215, v212
	v_cvt_f32_ubyte0_e32 v214, v212
	v_cvt_f32_ubyte3_e32 v239, v212
	v_cvt_f32_ubyte2_e32 v238, v212
	v_rcp_f32_e32 v237, v156
	v_pk_add_f32 v[238:239], v[238:239], 0.5 op_sel_hi:[1,0]
	v_pk_add_f32 v[214:215], v[214:215], 0.5 op_sel_hi:[1,0]
	v_cvt_f32_ubyte0_e32 v156, v210
	v_pk_mul_f32 v[214:215], v[214:215], v[216:217]
	v_pk_mul_f32 v[216:217], v[238:239], v[220:221]
	v_pk_mul_f32 v[48:49], v[48:49], v[214:215]
	v_pk_mul_f32 v[50:51], v[50:51], v[216:217]
	v_cvt_f32_ubyte3_e32 v217, v213
	v_cvt_f32_ubyte2_e32 v216, v213
	v_cvt_f32_ubyte1_e32 v215, v213
	v_cvt_f32_ubyte0_e32 v214, v213
	v_pk_add_f32 v[212:213], v[216:217], 0.5 op_sel_hi:[1,0]
	v_add_f32_e32 v156, 0.5, v156
	v_pk_mul_f32 v[212:213], v[212:213], v[236:237]
	v_pk_add_f32 v[214:215], v[214:215], 0.5 op_sel_hi:[1,0]
	v_pk_mul_f32 v[54:55], v[54:55], v[212:213]
	v_rcp_f32_e32 v212, v156
	v_cvt_f32_ubyte0_e32 v156, v211
	v_pk_mul_f32 v[214:215], v[214:215], v[218:219]
	v_add_f32_e32 v156, 0.5, v156
	v_pk_mul_f32 v[52:53], v[52:53], v[214:215]
	v_rcp_f32_e32 v214, v156
	v_cvt_f32_ubyte1_e32 v156, v210
	v_add_f32_e32 v156, 0.5, v156
	v_rcp_f32_e32 v213, v156
	v_cvt_f32_ubyte1_e32 v156, v211
	v_add_f32_e32 v156, 0.5, v156
	v_rcp_f32_e32 v215, v156
	v_cvt_f32_ubyte2_e32 v156, v210
	v_add_f32_e32 v156, 0.5, v156
	v_rcp_f32_e32 v216, v156
	v_cvt_f32_ubyte2_e32 v156, v211
	v_add_f32_e32 v156, 0.5, v156
	v_rcp_f32_e32 v218, v156
	v_cvt_f32_ubyte3_e32 v156, v210
	v_add_f32_e32 v156, 0.5, v156
	v_rcp_f32_e32 v217, v156
	v_cvt_f32_ubyte3_e32 v156, v211
	v_add_f32_e32 v156, 0.5, v156
	v_cvt_f32_ubyte1_e32 v211, v208
	v_cvt_f32_ubyte0_e32 v210, v208
	v_cvt_f32_ubyte3_e32 v221, v208
	v_cvt_f32_ubyte2_e32 v220, v208
	v_rcp_f32_e32 v219, v156
	v_pk_add_f32 v[220:221], v[220:221], 0.5 op_sel_hi:[1,0]
	v_pk_add_f32 v[210:211], v[210:211], 0.5 op_sel_hi:[1,0]
	v_cvt_f32_ubyte0_e32 v156, v206
	v_pk_mul_f32 v[210:211], v[210:211], v[212:213]
	v_pk_mul_f32 v[212:213], v[220:221], v[216:217]
	v_pk_mul_f32 v[24:25], v[24:25], v[210:211]
	v_pk_mul_f32 v[26:27], v[26:27], v[212:213]
	v_cvt_f32_ubyte3_e32 v213, v209
	v_cvt_f32_ubyte2_e32 v212, v209
	v_cvt_f32_ubyte1_e32 v211, v209
	v_cvt_f32_ubyte0_e32 v210, v209
	v_pk_add_f32 v[208:209], v[212:213], 0.5 op_sel_hi:[1,0]
	v_add_f32_e32 v156, 0.5, v156
	v_pk_mul_f32 v[208:209], v[208:209], v[218:219]
	v_pk_add_f32 v[210:211], v[210:211], 0.5 op_sel_hi:[1,0]
	v_pk_mul_f32 v[30:31], v[30:31], v[208:209]
	v_rcp_f32_e32 v208, v156
	v_cvt_f32_ubyte0_e32 v156, v207
	v_pk_mul_f32 v[210:211], v[210:211], v[214:215]
	v_add_f32_e32 v156, 0.5, v156
	v_pk_mul_f32 v[28:29], v[28:29], v[210:211]
	v_rcp_f32_e32 v210, v156
	v_cvt_f32_ubyte1_e32 v156, v206
	v_add_f32_e32 v156, 0.5, v156
	v_rcp_f32_e32 v209, v156
	v_cvt_f32_ubyte1_e32 v156, v207
	v_add_f32_e32 v156, 0.5, v156
	v_rcp_f32_e32 v211, v156
	v_cvt_f32_ubyte2_e32 v156, v206
	v_add_f32_e32 v156, 0.5, v156
	v_rcp_f32_e32 v212, v156
	v_cvt_f32_ubyte2_e32 v156, v207
	v_add_f32_e32 v156, 0.5, v156
	v_rcp_f32_e32 v214, v156
	v_cvt_f32_ubyte3_e32 v156, v206
	v_add_f32_e32 v156, 0.5, v156
	v_rcp_f32_e32 v213, v156
	v_cvt_f32_ubyte3_e32 v156, v207
	v_add_f32_e32 v156, 0.5, v156
	v_cvt_f32_ubyte1_e32 v207, v204
	v_cvt_f32_ubyte0_e32 v206, v204
	v_cvt_f32_ubyte3_e32 v217, v204
	v_cvt_f32_ubyte2_e32 v216, v204
	v_rcp_f32_e32 v215, v156
	v_pk_add_f32 v[216:217], v[216:217], 0.5 op_sel_hi:[1,0]
	v_pk_add_f32 v[206:207], v[206:207], 0.5 op_sel_hi:[1,0]
	v_cvt_f32_ubyte0_e32 v156, v202
	v_pk_mul_f32 v[206:207], v[206:207], v[208:209]
	v_pk_mul_f32 v[208:209], v[216:217], v[212:213]
	v_pk_mul_f32 v[56:57], v[56:57], v[206:207]
	v_pk_mul_f32 v[58:59], v[58:59], v[208:209]
	v_cvt_f32_ubyte3_e32 v209, v205
	v_cvt_f32_ubyte2_e32 v208, v205
	v_cvt_f32_ubyte1_e32 v207, v205
	v_cvt_f32_ubyte0_e32 v206, v205
	v_pk_add_f32 v[204:205], v[208:209], 0.5 op_sel_hi:[1,0]
	v_add_f32_e32 v156, 0.5, v156
	v_pk_mul_f32 v[204:205], v[204:205], v[214:215]
	v_pk_add_f32 v[206:207], v[206:207], 0.5 op_sel_hi:[1,0]
	v_pk_mul_f32 v[62:63], v[62:63], v[204:205]
	v_rcp_f32_e32 v204, v156
	v_cvt_f32_ubyte0_e32 v156, v203
	v_pk_mul_f32 v[206:207], v[206:207], v[210:211]
	v_add_f32_e32 v156, 0.5, v156
	v_pk_mul_f32 v[60:61], v[60:61], v[206:207]
	v_rcp_f32_e32 v206, v156
	v_cvt_f32_ubyte1_e32 v156, v202
	v_add_f32_e32 v156, 0.5, v156
	v_rcp_f32_e32 v205, v156
	v_cvt_f32_ubyte1_e32 v156, v203
	v_add_f32_e32 v156, 0.5, v156
	v_rcp_f32_e32 v207, v156
	v_cvt_f32_ubyte2_e32 v156, v202
	v_add_f32_e32 v156, 0.5, v156
	v_rcp_f32_e32 v208, v156
	v_cvt_f32_ubyte2_e32 v156, v203
	v_addc_co_u32_e32 v1, vcc, 0, v1, vcc
	v_add_f32_e32 v156, 0.5, v156
	v_add_co_u32_e32 v6, vcc, s85, v2
	v_rcp_f32_e32 v210, v156
	v_cvt_f32_ubyte3_e32 v156, v202
	v_addc_co_u32_e32 v7, vcc, 0, v3, vcc
	v_add_f32_e32 v156, 0.5, v156
	global_load_dwordx2 v[184:185], v[0:1], off
	global_load_dwordx2 v[186:187], v[6:7], off
	global_load_dwordx2 v[180:181], v[0:1], off offset:512
	global_load_dwordx2 v[182:183], v[6:7], off offset:512
	global_load_dwordx2 v[176:177], v[0:1], off offset:1024
	global_load_dwordx2 v[178:179], v[6:7], off offset:1024
	global_load_dwordx2 v[144:145], v[0:1], off offset:1536
	global_load_dwordx2 v[146:147], v[6:7], off offset:1536
	global_load_dwordx2 v[12:13], v[0:1], off offset:2048
	global_load_dwordx2 v[14:15], v[6:7], off offset:2048
	global_load_dwordx2 v[8:9], v[0:1], off offset:2560
	global_load_dwordx2 v[10:11], v[6:7], off offset:2560
	global_load_dwordx2 v[2:3], v[0:1], off offset:3072
	global_load_dwordx2 v[4:5], v[6:7], off offset:3072
	s_nop 0
	global_load_dwordx2 v[0:1], v[0:1], off offset:3584
	s_nop 0
	global_load_dwordx2 v[6:7], v[6:7], off offset:3584
	v_rcp_f32_e32 v209, v156
	v_cvt_f32_ubyte3_e32 v156, v203
	v_add_f32_e32 v156, 0.5, v156
	v_cvt_f32_ubyte1_e32 v203, v200
	v_cvt_f32_ubyte0_e32 v202, v200
	v_cvt_f32_ubyte3_e32 v213, v200
	v_cvt_f32_ubyte2_e32 v212, v200
	v_rcp_f32_e32 v211, v156
	v_pk_add_f32 v[212:213], v[212:213], 0.5 op_sel_hi:[1,0]
	v_pk_add_f32 v[202:203], v[202:203], 0.5 op_sel_hi:[1,0]
	v_cvt_f32_ubyte0_e32 v156, v198
	v_pk_mul_f32 v[202:203], v[202:203], v[204:205]
	v_pk_mul_f32 v[204:205], v[212:213], v[208:209]
	v_pk_mul_f32 v[32:33], v[32:33], v[202:203]
	v_pk_mul_f32 v[34:35], v[34:35], v[204:205]
	v_cvt_f32_ubyte3_e32 v205, v201
	v_cvt_f32_ubyte2_e32 v204, v201
	v_cvt_f32_ubyte1_e32 v203, v201
	v_cvt_f32_ubyte0_e32 v202, v201
	v_pk_add_f32 v[200:201], v[204:205], 0.5 op_sel_hi:[1,0]
	v_add_f32_e32 v156, 0.5, v156
	v_pk_mul_f32 v[200:201], v[200:201], v[210:211]
	v_pk_add_f32 v[202:203], v[202:203], 0.5 op_sel_hi:[1,0]
	v_pk_mul_f32 v[38:39], v[38:39], v[200:201]
	v_rcp_f32_e32 v200, v156
	v_cvt_f32_ubyte0_e32 v156, v199
	v_pk_mul_f32 v[202:203], v[202:203], v[206:207]
	v_add_f32_e32 v156, 0.5, v156
	v_pk_mul_f32 v[36:37], v[36:37], v[202:203]
	v_rcp_f32_e32 v202, v156
	v_cvt_f32_ubyte1_e32 v156, v198
	v_add_f32_e32 v156, 0.5, v156
	v_rcp_f32_e32 v201, v156
	v_cvt_f32_ubyte1_e32 v156, v199
	v_add_f32_e32 v156, 0.5, v156
	v_rcp_f32_e32 v203, v156
	v_cvt_f32_ubyte2_e32 v156, v198
	v_add_f32_e32 v156, 0.5, v156
	v_rcp_f32_e32 v204, v156
	v_cvt_f32_ubyte2_e32 v156, v199
	v_add_f32_e32 v156, 0.5, v156
	v_rcp_f32_e32 v206, v156
	v_cvt_f32_ubyte3_e32 v156, v198
	v_add_f32_e32 v156, 0.5, v156
	v_rcp_f32_e32 v205, v156
	v_cvt_f32_ubyte3_e32 v156, v199
	v_add_f32_e32 v156, 0.5, v156
	v_cvt_f32_ubyte1_e32 v199, v196
	v_cvt_f32_ubyte0_e32 v198, v196
	v_cvt_f32_ubyte3_e32 v209, v196
	v_cvt_f32_ubyte2_e32 v208, v196
	v_rcp_f32_e32 v207, v156
	v_pk_add_f32 v[208:209], v[208:209], 0.5 op_sel_hi:[1,0]
	v_pk_add_f32 v[198:199], v[198:199], 0.5 op_sel_hi:[1,0]
	v_cvt_f32_ubyte0_e32 v156, v194
	v_pk_mul_f32 v[198:199], v[198:199], v[200:201]
	v_pk_mul_f32 v[200:201], v[208:209], v[204:205]
	v_pk_mul_f32 v[64:65], v[64:65], v[198:199]
	v_pk_mul_f32 v[66:67], v[66:67], v[200:201]
	v_cvt_f32_ubyte3_e32 v201, v197
	v_cvt_f32_ubyte2_e32 v200, v197
	v_cvt_f32_ubyte1_e32 v199, v197
	v_cvt_f32_ubyte0_e32 v198, v197
	v_pk_add_f32 v[196:197], v[200:201], 0.5 op_sel_hi:[1,0]
	v_add_f32_e32 v156, 0.5, v156
	v_pk_mul_f32 v[196:197], v[196:197], v[206:207]
	v_pk_add_f32 v[198:199], v[198:199], 0.5 op_sel_hi:[1,0]
	v_pk_mul_f32 v[70:71], v[70:71], v[196:197]
	v_rcp_f32_e32 v196, v156
	v_cvt_f32_ubyte0_e32 v156, v195
	v_pk_mul_f32 v[198:199], v[198:199], v[202:203]
	v_add_f32_e32 v156, 0.5, v156
	v_pk_mul_f32 v[68:69], v[68:69], v[198:199]
	v_rcp_f32_e32 v198, v156
	v_cvt_f32_ubyte1_e32 v156, v194
	v_add_f32_e32 v156, 0.5, v156
	v_rcp_f32_e32 v197, v156
	v_cvt_f32_ubyte1_e32 v156, v195
	v_add_f32_e32 v156, 0.5, v156
	v_rcp_f32_e32 v199, v156
	v_cvt_f32_ubyte2_e32 v156, v194
	v_add_f32_e32 v156, 0.5, v156
	v_rcp_f32_e32 v200, v156
	v_cvt_f32_ubyte2_e32 v156, v195
	v_add_f32_e32 v156, 0.5, v156
	v_rcp_f32_e32 v202, v156
	v_cvt_f32_ubyte3_e32 v156, v194
	v_add_f32_e32 v156, 0.5, v156
	v_rcp_f32_e32 v201, v156
	v_cvt_f32_ubyte3_e32 v156, v195
	v_add_f32_e32 v156, 0.5, v156
	v_cvt_f32_ubyte1_e32 v195, v192
	v_cvt_f32_ubyte0_e32 v194, v192
	v_cvt_f32_ubyte3_e32 v205, v192
	v_cvt_f32_ubyte2_e32 v204, v192
	v_rcp_f32_e32 v203, v156
	v_pk_add_f32 v[204:205], v[204:205], 0.5 op_sel_hi:[1,0]
	v_pk_add_f32 v[194:195], v[194:195], 0.5 op_sel_hi:[1,0]
	v_cvt_f32_ubyte0_e32 v156, v190
	v_pk_mul_f32 v[194:195], v[194:195], v[196:197]
	v_pk_mul_f32 v[196:197], v[204:205], v[200:201]
	v_pk_mul_f32 v[40:41], v[40:41], v[194:195]
	v_pk_mul_f32 v[42:43], v[42:43], v[196:197]
	v_cvt_f32_ubyte3_e32 v197, v193
	v_cvt_f32_ubyte2_e32 v196, v193
	v_cvt_f32_ubyte1_e32 v195, v193
	v_cvt_f32_ubyte0_e32 v194, v193
	v_pk_add_f32 v[192:193], v[196:197], 0.5 op_sel_hi:[1,0]
	v_add_f32_e32 v156, 0.5, v156
	v_pk_mul_f32 v[192:193], v[192:193], v[202:203]
	v_pk_add_f32 v[194:195], v[194:195], 0.5 op_sel_hi:[1,0]
	v_pk_mul_f32 v[46:47], v[46:47], v[192:193]
	v_rcp_f32_e32 v192, v156
	v_cvt_f32_ubyte0_e32 v156, v191
	v_pk_mul_f32 v[194:195], v[194:195], v[198:199]
	v_add_f32_e32 v156, 0.5, v156
	v_pk_mul_f32 v[44:45], v[44:45], v[194:195]
	v_rcp_f32_e32 v194, v156
	v_cvt_f32_ubyte1_e32 v156, v190
	v_add_f32_e32 v156, 0.5, v156
	v_rcp_f32_e32 v193, v156
	v_cvt_f32_ubyte1_e32 v156, v191
	v_add_f32_e32 v156, 0.5, v156
	v_rcp_f32_e32 v195, v156
	v_cvt_f32_ubyte2_e32 v156, v190
	v_add_f32_e32 v156, 0.5, v156
	v_rcp_f32_e32 v196, v156
	v_cvt_f32_ubyte2_e32 v156, v191
	v_add_f32_e32 v156, 0.5, v156
	v_rcp_f32_e32 v198, v156
	v_cvt_f32_ubyte3_e32 v156, v190
	v_add_f32_e32 v156, 0.5, v156
	v_rcp_f32_e32 v197, v156
	v_cvt_f32_ubyte3_e32 v156, v191
	v_add_f32_e32 v156, 0.5, v156
	v_cvt_f32_ubyte1_e32 v191, v188
	v_cvt_f32_ubyte0_e32 v190, v188
	v_cvt_f32_ubyte3_e32 v201, v188
	v_cvt_f32_ubyte2_e32 v200, v188
	v_rcp_f32_e32 v199, v156
	v_pk_add_f32 v[200:201], v[200:201], 0.5 op_sel_hi:[1,0]
	v_pk_add_f32 v[190:191], v[190:191], 0.5 op_sel_hi:[1,0]
	s_waitcnt vmcnt(0)
	v_cvt_f32_ubyte0_e32 v156, v186
	v_pk_mul_f32 v[190:191], v[190:191], v[192:193]
	v_pk_mul_f32 v[192:193], v[200:201], v[196:197]
	v_pk_mul_f32 v[72:73], v[72:73], v[190:191]
	v_pk_mul_f32 v[74:75], v[74:75], v[192:193]
	v_cvt_f32_ubyte3_e32 v193, v189
	v_cvt_f32_ubyte2_e32 v192, v189
	v_cvt_f32_ubyte1_e32 v191, v189
	v_cvt_f32_ubyte0_e32 v190, v189
	v_pk_add_f32 v[188:189], v[192:193], 0.5 op_sel_hi:[1,0]
	v_add_f32_e32 v156, 0.5, v156
	v_pk_mul_f32 v[188:189], v[188:189], v[198:199]
	v_pk_add_f32 v[190:191], v[190:191], 0.5 op_sel_hi:[1,0]
	v_pk_mul_f32 v[78:79], v[78:79], v[188:189]
	v_rcp_f32_e32 v188, v156
	v_cvt_f32_ubyte0_e32 v156, v187
	v_pk_mul_f32 v[190:191], v[190:191], v[194:195]
	v_add_f32_e32 v156, 0.5, v156
	v_pk_mul_f32 v[76:77], v[76:77], v[190:191]
	v_rcp_f32_e32 v190, v156
	v_cvt_f32_ubyte1_e32 v156, v186
	v_add_f32_e32 v156, 0.5, v156
	v_rcp_f32_e32 v189, v156
	v_cvt_f32_ubyte1_e32 v156, v187
	v_add_f32_e32 v156, 0.5, v156
	v_rcp_f32_e32 v191, v156
	v_cvt_f32_ubyte2_e32 v156, v186
	v_add_f32_e32 v156, 0.5, v156
	v_rcp_f32_e32 v192, v156
	v_cvt_f32_ubyte2_e32 v156, v187
	v_add_f32_e32 v156, 0.5, v156
	v_rcp_f32_e32 v194, v156
	v_cvt_f32_ubyte3_e32 v156, v186
	v_add_f32_e32 v156, 0.5, v156
	v_rcp_f32_e32 v193, v156
	v_cvt_f32_ubyte3_e32 v156, v187
	v_add_f32_e32 v156, 0.5, v156
	v_cvt_f32_ubyte1_e32 v187, v184
	v_cvt_f32_ubyte0_e32 v186, v184
	v_cvt_f32_ubyte3_e32 v197, v184
	v_cvt_f32_ubyte2_e32 v196, v184
	v_rcp_f32_e32 v195, v156
	v_pk_add_f32 v[196:197], v[196:197], 0.5 op_sel_hi:[1,0]
	v_pk_add_f32 v[186:187], v[186:187], 0.5 op_sel_hi:[1,0]
	v_cvt_f32_ubyte0_e32 v156, v182
	v_pk_mul_f32 v[186:187], v[186:187], v[188:189]
	v_pk_mul_f32 v[188:189], v[196:197], v[192:193]
	v_pk_mul_f32 v[80:81], v[80:81], v[186:187]
	v_pk_mul_f32 v[82:83], v[82:83], v[188:189]
	v_cvt_f32_ubyte3_e32 v189, v185
	v_cvt_f32_ubyte2_e32 v188, v185
	v_cvt_f32_ubyte1_e32 v187, v185
	v_cvt_f32_ubyte0_e32 v186, v185
	v_pk_add_f32 v[184:185], v[188:189], 0.5 op_sel_hi:[1,0]
	v_add_f32_e32 v156, 0.5, v156
	v_pk_mul_f32 v[184:185], v[184:185], v[194:195]
	v_pk_add_f32 v[186:187], v[186:187], 0.5 op_sel_hi:[1,0]
	v_pk_mul_f32 v[86:87], v[86:87], v[184:185]
	v_rcp_f32_e32 v184, v156
	v_cvt_f32_ubyte0_e32 v156, v183
	v_pk_mul_f32 v[186:187], v[186:187], v[190:191]
	v_add_f32_e32 v156, 0.5, v156
	v_pk_mul_f32 v[84:85], v[84:85], v[186:187]
	v_rcp_f32_e32 v186, v156
	v_cvt_f32_ubyte1_e32 v156, v182
	v_add_f32_e32 v156, 0.5, v156
	v_rcp_f32_e32 v185, v156
	v_cvt_f32_ubyte1_e32 v156, v183
	v_add_f32_e32 v156, 0.5, v156
	v_rcp_f32_e32 v187, v156
	v_cvt_f32_ubyte2_e32 v156, v182
	v_add_f32_e32 v156, 0.5, v156
	v_rcp_f32_e32 v188, v156
	v_cvt_f32_ubyte2_e32 v156, v183
	v_add_f32_e32 v156, 0.5, v156
	v_rcp_f32_e32 v190, v156
	v_cvt_f32_ubyte3_e32 v156, v182
	v_add_f32_e32 v156, 0.5, v156
	v_rcp_f32_e32 v189, v156
	v_cvt_f32_ubyte3_e32 v156, v183
	v_add_f32_e32 v156, 0.5, v156
	v_cvt_f32_ubyte1_e32 v183, v180
	v_cvt_f32_ubyte0_e32 v182, v180
	v_cvt_f32_ubyte3_e32 v193, v180
	v_cvt_f32_ubyte2_e32 v192, v180
	v_rcp_f32_e32 v191, v156
	v_pk_add_f32 v[192:193], v[192:193], 0.5 op_sel_hi:[1,0]
	v_pk_add_f32 v[182:183], v[182:183], 0.5 op_sel_hi:[1,0]
	v_cvt_f32_ubyte0_e32 v156, v178
	v_pk_mul_f32 v[182:183], v[182:183], v[184:185]
	v_pk_mul_f32 v[184:185], v[192:193], v[188:189]
	v_pk_mul_f32 v[112:113], v[112:113], v[182:183]
	v_pk_mul_f32 v[114:115], v[114:115], v[184:185]
	v_cvt_f32_ubyte3_e32 v185, v181
	v_cvt_f32_ubyte2_e32 v184, v181
	v_cvt_f32_ubyte1_e32 v183, v181
	v_cvt_f32_ubyte0_e32 v182, v181
	v_pk_add_f32 v[180:181], v[184:185], 0.5 op_sel_hi:[1,0]
	v_add_f32_e32 v156, 0.5, v156
	v_pk_mul_f32 v[180:181], v[180:181], v[190:191]
	v_pk_add_f32 v[182:183], v[182:183], 0.5 op_sel_hi:[1,0]
	v_pk_mul_f32 v[118:119], v[118:119], v[180:181]
	v_rcp_f32_e32 v180, v156
	v_cvt_f32_ubyte0_e32 v156, v179
	v_pk_mul_f32 v[182:183], v[182:183], v[186:187]
	v_add_f32_e32 v156, 0.5, v156
	v_pk_mul_f32 v[116:117], v[116:117], v[182:183]
	v_rcp_f32_e32 v182, v156
	v_cvt_f32_ubyte1_e32 v156, v178
	v_add_f32_e32 v156, 0.5, v156
	v_rcp_f32_e32 v181, v156
	v_cvt_f32_ubyte1_e32 v156, v179
	v_add_f32_e32 v156, 0.5, v156
	v_rcp_f32_e32 v183, v156
	v_cvt_f32_ubyte2_e32 v156, v178
	v_add_f32_e32 v156, 0.5, v156
	v_rcp_f32_e32 v184, v156
	v_cvt_f32_ubyte2_e32 v156, v179
	v_add_f32_e32 v156, 0.5, v156
	v_rcp_f32_e32 v186, v156
	v_cvt_f32_ubyte3_e32 v156, v178
	v_add_f32_e32 v156, 0.5, v156
	v_rcp_f32_e32 v185, v156
	v_cvt_f32_ubyte3_e32 v156, v179
	v_add_f32_e32 v156, 0.5, v156
	v_cvt_f32_ubyte1_e32 v179, v176
	v_cvt_f32_ubyte0_e32 v178, v176
	v_cvt_f32_ubyte3_e32 v189, v176
	v_cvt_f32_ubyte2_e32 v188, v176
	v_rcp_f32_e32 v187, v156
	v_pk_add_f32 v[188:189], v[188:189], 0.5 op_sel_hi:[1,0]
	v_pk_add_f32 v[178:179], v[178:179], 0.5 op_sel_hi:[1,0]
	v_cvt_f32_ubyte0_e32 v156, v146
	v_pk_mul_f32 v[178:179], v[178:179], v[180:181]
	v_pk_mul_f32 v[180:181], v[188:189], v[184:185]
	v_pk_mul_f32 v[88:89], v[88:89], v[178:179]
	v_pk_mul_f32 v[90:91], v[90:91], v[180:181]
	v_cvt_f32_ubyte3_e32 v181, v177
	v_cvt_f32_ubyte2_e32 v180, v177
	v_cvt_f32_ubyte1_e32 v179, v177
	v_cvt_f32_ubyte0_e32 v178, v177
	v_pk_add_f32 v[176:177], v[180:181], 0.5 op_sel_hi:[1,0]
	v_add_f32_e32 v156, 0.5, v156
	v_pk_mul_f32 v[176:177], v[176:177], v[186:187]
	v_pk_add_f32 v[178:179], v[178:179], 0.5 op_sel_hi:[1,0]
	v_pk_mul_f32 v[94:95], v[94:95], v[176:177]
	v_rcp_f32_e32 v176, v156
	v_cvt_f32_ubyte0_e32 v156, v147
	v_pk_mul_f32 v[178:179], v[178:179], v[182:183]
	v_add_f32_e32 v156, 0.5, v156
	v_pk_mul_f32 v[92:93], v[92:93], v[178:179]
	v_rcp_f32_e32 v178, v156
	v_cvt_f32_ubyte1_e32 v156, v146
	v_add_f32_e32 v156, 0.5, v156
	v_rcp_f32_e32 v177, v156
	v_cvt_f32_ubyte1_e32 v156, v147
	v_add_f32_e32 v156, 0.5, v156
	v_rcp_f32_e32 v179, v156
	v_cvt_f32_ubyte2_e32 v156, v146
	v_cvt_f32_ubyte3_e32 v146, v146
	v_add_f32_e32 v156, 0.5, v156
	v_add_f32_e32 v146, 0.5, v146
	v_rcp_f32_e32 v180, v156
	v_rcp_f32_e32 v181, v146
	v_cvt_f32_ubyte3_e32 v146, v147
	v_cvt_f32_ubyte2_e32 v156, v147
	v_add_f32_e32 v146, 0.5, v146
	v_add_f32_e32 v156, 0.5, v156
	v_rcp_f32_e32 v183, v146
	v_cvt_f32_ubyte1_e32 v147, v144
	v_cvt_f32_ubyte0_e32 v146, v144
	v_cvt_f32_ubyte3_e32 v185, v144
	v_cvt_f32_ubyte2_e32 v184, v144
	v_rcp_f32_e32 v182, v156
	v_pk_add_f32 v[184:185], v[184:185], 0.5 op_sel_hi:[1,0]
	v_pk_add_f32 v[146:147], v[146:147], 0.5 op_sel_hi:[1,0]
	v_cvt_f32_ubyte2_e32 v156, v14
	v_pk_mul_f32 v[146:147], v[146:147], v[176:177]
	v_pk_mul_f32 v[176:177], v[184:185], v[180:181]
	v_pk_mul_f32 v[120:121], v[120:121], v[146:147]
	v_pk_mul_f32 v[122:123], v[122:123], v[176:177]
	v_cvt_f32_ubyte3_e32 v177, v145
	v_cvt_f32_ubyte2_e32 v176, v145
	v_cvt_f32_ubyte1_e32 v147, v145
	v_cvt_f32_ubyte0_e32 v146, v145
	v_pk_add_f32 v[144:145], v[176:177], 0.5 op_sel_hi:[1,0]
	v_pk_add_f32 v[146:147], v[146:147], 0.5 op_sel_hi:[1,0]
	v_pk_mul_f32 v[144:145], v[144:145], v[182:183]
	v_pk_mul_f32 v[146:147], v[146:147], v[178:179]
	v_pk_mul_f32 v[126:127], v[126:127], v[144:145]
	v_cvt_f32_ubyte0_e32 v145, v15
	v_add_f32_e32 v145, 0.5, v145
	v_pk_mul_f32 v[124:125], v[124:125], v[146:147]
	v_cvt_f32_ubyte0_e32 v144, v14
	v_rcp_f32_e32 v146, v145
	v_cvt_f32_ubyte1_e32 v145, v14
	v_cvt_f32_ubyte3_e32 v14, v14
	v_add_f32_e32 v144, 0.5, v144
	v_add_f32_e32 v145, 0.5, v145
	v_add_f32_e32 v156, 0.5, v156
	v_add_f32_e32 v14, 0.5, v14
	v_rcp_f32_e32 v144, v144
	v_rcp_f32_e32 v145, v145
	v_rcp_f32_e32 v176, v156
	v_rcp_f32_e32 v177, v14
	v_cvt_f32_ubyte3_e32 v14, v15
	v_cvt_f32_ubyte2_e32 v156, v15
	v_add_f32_e32 v14, 0.5, v14
	v_cvt_f32_ubyte1_e32 v147, v15
	v_add_f32_e32 v156, 0.5, v156
	v_rcp_f32_e32 v179, v14
	v_cvt_f32_ubyte1_e32 v15, v12
	v_cvt_f32_ubyte0_e32 v14, v12
	v_cvt_f32_ubyte3_e32 v181, v12
	v_cvt_f32_ubyte2_e32 v180, v12
	v_rcp_f32_e32 v178, v156
	v_pk_add_f32 v[180:181], v[180:181], 0.5 op_sel_hi:[1,0]
	v_pk_add_f32 v[14:15], v[14:15], 0.5 op_sel_hi:[1,0]
	v_add_f32_e32 v147, 0.5, v147
	v_pk_mul_f32 v[14:15], v[14:15], v[144:145]
	v_pk_mul_f32 v[144:145], v[180:181], v[176:177]
	v_rcp_f32_e32 v147, v147
	v_pk_mul_f32 v[98:99], v[98:99], v[144:145]
	v_cvt_f32_ubyte3_e32 v145, v13
	v_cvt_f32_ubyte2_e32 v144, v13
	v_pk_mul_f32 v[96:97], v[96:97], v[14:15]
	v_cvt_f32_ubyte1_e32 v15, v13
	v_cvt_f32_ubyte0_e32 v14, v13
	v_pk_add_f32 v[12:13], v[144:145], 0.5 op_sel_hi:[1,0]
	v_pk_add_f32 v[14:15], v[14:15], 0.5 op_sel_hi:[1,0]
	v_pk_mul_f32 v[12:13], v[12:13], v[178:179]
	v_pk_mul_f32 v[14:15], v[14:15], v[146:147]
	v_pk_mul_f32 v[102:103], v[102:103], v[12:13]
	v_cvt_f32_ubyte0_e32 v13, v11
	v_add_f32_e32 v13, 0.5, v13
	v_pk_mul_f32 v[100:101], v[100:101], v[14:15]
	v_cvt_f32_ubyte0_e32 v12, v10
	v_rcp_f32_e32 v14, v13
	v_cvt_f32_ubyte1_e32 v13, v10
	v_cvt_f32_ubyte2_e32 v144, v10
	v_cvt_f32_ubyte2_e32 v145, v11
	v_cvt_f32_ubyte3_e32 v10, v10
	v_add_f32_e32 v12, 0.5, v12
	v_add_f32_e32 v13, 0.5, v13
	v_add_f32_e32 v144, 0.5, v144
	v_add_f32_e32 v145, 0.5, v145
	v_add_f32_e32 v10, 0.5, v10
	v_rcp_f32_e32 v12, v12
	v_rcp_f32_e32 v13, v13
	v_rcp_f32_e32 v144, v144
	v_rcp_f32_e32 v146, v145
	v_rcp_f32_e32 v145, v10
	v_cvt_f32_ubyte3_e32 v10, v11
	v_add_f32_e32 v10, 0.5, v10
	v_cvt_f32_ubyte1_e32 v15, v11
	v_rcp_f32_e32 v147, v10
	v_cvt_f32_ubyte1_e32 v11, v8
	v_cvt_f32_ubyte0_e32 v10, v8
	v_cvt_f32_ubyte3_e32 v177, v8
	v_cvt_f32_ubyte2_e32 v176, v8
	v_pk_add_f32 v[176:177], v[176:177], 0.5 op_sel_hi:[1,0]
	v_pk_add_f32 v[10:11], v[10:11], 0.5 op_sel_hi:[1,0]
	v_add_f32_e32 v15, 0.5, v15
	v_pk_mul_f32 v[10:11], v[10:11], v[12:13]
	v_pk_mul_f32 v[12:13], v[176:177], v[144:145]
	v_rcp_f32_e32 v15, v15
	v_pk_mul_f32 v[130:131], v[130:131], v[12:13]
	v_cvt_f32_ubyte3_e32 v13, v9
	v_cvt_f32_ubyte2_e32 v12, v9
	v_pk_mul_f32 v[128:129], v[128:129], v[10:11]
	v_cvt_f32_ubyte1_e32 v11, v9
	v_cvt_f32_ubyte0_e32 v10, v9
	v_pk_add_f32 v[8:9], v[12:13], 0.5 op_sel_hi:[1,0]
	v_pk_add_f32 v[10:11], v[10:11], 0.5 op_sel_hi:[1,0]
	v_pk_mul_f32 v[8:9], v[8:9], v[146:147]
	v_pk_mul_f32 v[10:11], v[10:11], v[14:15]
	v_pk_mul_f32 v[134:135], v[134:135], v[8:9]
	v_cvt_f32_ubyte0_e32 v9, v5
	v_add_f32_e32 v9, 0.5, v9
	v_pk_mul_f32 v[132:133], v[132:133], v[10:11]
	v_cvt_f32_ubyte0_e32 v8, v4
	v_rcp_f32_e32 v10, v9
	v_cvt_f32_ubyte1_e32 v9, v4
	v_cvt_f32_ubyte2_e32 v12, v4
	v_cvt_f32_ubyte2_e32 v13, v5
	v_cvt_f32_ubyte3_e32 v4, v4
	v_add_f32_e32 v8, 0.5, v8
	v_add_f32_e32 v9, 0.5, v9
	v_add_f32_e32 v12, 0.5, v12
	v_add_f32_e32 v13, 0.5, v13
	v_add_f32_e32 v4, 0.5, v4
	v_rcp_f32_e32 v8, v8
	v_rcp_f32_e32 v9, v9
	v_rcp_f32_e32 v12, v12
	v_rcp_f32_e32 v14, v13
	v_rcp_f32_e32 v13, v4
	v_cvt_f32_ubyte3_e32 v4, v5
	v_add_f32_e32 v4, 0.5, v4
	v_cvt_f32_ubyte1_e32 v11, v5
	v_rcp_f32_e32 v15, v4
	v_cvt_f32_ubyte1_e32 v5, v2
	v_cvt_f32_ubyte0_e32 v4, v2
	v_cvt_f32_ubyte3_e32 v145, v2
	v_cvt_f32_ubyte2_e32 v144, v2
	v_pk_add_f32 v[144:145], v[144:145], 0.5 op_sel_hi:[1,0]
	v_pk_add_f32 v[4:5], v[4:5], 0.5 op_sel_hi:[1,0]
	v_add_f32_e32 v11, 0.5, v11
	v_pk_mul_f32 v[4:5], v[4:5], v[8:9]
	v_pk_mul_f32 v[8:9], v[144:145], v[12:13]
	v_rcp_f32_e32 v11, v11
	v_pk_mul_f32 v[106:107], v[106:107], v[8:9]
	v_cvt_f32_ubyte3_e32 v9, v3
	v_cvt_f32_ubyte2_e32 v8, v3
	v_pk_mul_f32 v[104:105], v[104:105], v[4:5]
	v_cvt_f32_ubyte1_e32 v5, v3
	v_cvt_f32_ubyte0_e32 v4, v3
	v_pk_add_f32 v[2:3], v[8:9], 0.5 op_sel_hi:[1,0]
	v_pk_add_f32 v[4:5], v[4:5], 0.5 op_sel_hi:[1,0]
	v_pk_mul_f32 v[2:3], v[2:3], v[14:15]
	v_pk_mul_f32 v[4:5], v[4:5], v[10:11]
	v_pk_mul_f32 v[110:111], v[110:111], v[2:3]
	v_cvt_f32_ubyte0_e32 v3, v7
	v_add_f32_e32 v3, 0.5, v3
	v_pk_mul_f32 v[108:109], v[108:109], v[4:5]
	v_cvt_f32_ubyte0_e32 v2, v6
	v_rcp_f32_e32 v4, v3
	v_cvt_f32_ubyte1_e32 v3, v6
	v_cvt_f32_ubyte2_e32 v8, v6
	v_cvt_f32_ubyte2_e32 v9, v7
	v_cvt_f32_ubyte3_e32 v6, v6
	v_add_f32_e32 v2, 0.5, v2
	v_add_f32_e32 v3, 0.5, v3
	v_add_f32_e32 v8, 0.5, v8
	v_add_f32_e32 v9, 0.5, v9
	v_add_f32_e32 v6, 0.5, v6
	v_rcp_f32_e32 v2, v2
	v_rcp_f32_e32 v3, v3
	v_rcp_f32_e32 v8, v8
	v_rcp_f32_e32 v10, v9
	v_rcp_f32_e32 v9, v6
	v_cvt_f32_ubyte3_e32 v6, v7
	v_cvt_f32_ubyte1_e32 v5, v7
	v_add_f32_e32 v6, 0.5, v6
	v_add_f32_e32 v5, 0.5, v5
	v_rcp_f32_e32 v11, v6
	v_cvt_f32_ubyte1_e32 v7, v0
	v_cvt_f32_ubyte0_e32 v6, v0
	v_cvt_f32_ubyte3_e32 v13, v0
	v_cvt_f32_ubyte2_e32 v12, v0
	v_rcp_f32_e32 v5, v5
	v_pk_add_f32 v[12:13], v[12:13], 0.5 op_sel_hi:[1,0]
	v_pk_add_f32 v[6:7], v[6:7], 0.5 op_sel_hi:[1,0]
	s_nop 0
	v_pk_mul_f32 v[2:3], v[6:7], v[2:3]
	v_pk_mul_f32 v[6:7], v[12:13], v[8:9]
	v_pk_mul_f32 v[144:145], v[136:137], v[2:3]
	v_pk_mul_f32 v[146:147], v[138:139], v[6:7]
	v_cvt_f32_ubyte1_e32 v3, v1
	v_cvt_f32_ubyte0_e32 v2, v1
	v_cvt_f32_ubyte3_e32 v7, v1
	v_cvt_f32_ubyte2_e32 v6, v1
	v_pk_add_f32 v[0:1], v[6:7], 0.5 op_sel_hi:[1,0]
	v_pk_add_f32 v[2:3], v[2:3], 0.5 op_sel_hi:[1,0]
	v_pk_mul_f32 v[0:1], v[0:1], v[10:11]
	v_pk_mul_f32 v[2:3], v[2:3], v[4:5]
	v_pk_mul_f32 v[138:139], v[142:143], v[0:1]
	v_pk_mul_f32 v[136:137], v[140:141], v[2:3]
	ds_read_b128 v[8:11], v231
	ds_read_b128 v[12:15], v231 offset:1024
	ds_read_b128 v[0:3], v231 offset:2048
	ds_read_b128 v[4:7], v231 offset:3072
	s_add_u32 s56, s48, 0x40680
	s_addc_u32 s57, s49, 0
	s_mov_b32 m0, s94
	v_lshl_add_u64 v[140:141], s[56:57], 0, v[148:149]
	ds_read_b128 v[176:179], v228
	ds_read_b128 v[180:183], v228 offset:1024
	ds_read_b128 v[184:187], v228 offset:2048
	ds_read_b128 v[188:191], v228 offset:3072
	ds_read_b128 v[192:195], v228 offset:4096
	ds_read_b128 v[196:199], v228 offset:5120
	ds_read_b128 v[200:203], v228 offset:6144
	ds_read_b128 v[204:207], v228 offset:7168
	global_load_lds_dwordx4 v[140:141], off
	v_lshl_add_u64 v[140:141], s[56:57], 0, v[152:153]
	s_mov_b32 m0, s93
	s_nop 0
	global_load_lds_dwordx4 v[140:141], off
	s_waitcnt lgkmcnt(8)
	s_barrier
	s_waitcnt lgkmcnt(0)
	s_setprio 1
	s_waitcnt lgkmcnt(0)
	v_mfma_f32_16x16x128_f8f6f4 v[16:19], v[8:15], v[176:183], v[16:19]
	v_mfma_f32_16x16x128_f8f6f4 v[20:23], v[0:7], v[176:183], v[20:23]
	v_mfma_f32_16x16x128_f8f6f4 v[24:27], v[8:15], v[184:191], v[24:27]
	v_mfma_f32_16x16x128_f8f6f4 v[28:31], v[0:7], v[184:191], v[28:31]
	v_mfma_f32_16x16x128_f8f6f4 v[32:35], v[8:15], v[192:199], v[32:35]
	v_mfma_f32_16x16x128_f8f6f4 v[36:39], v[0:7], v[192:199], v[36:39]
	v_mfma_f32_16x16x128_f8f6f4 v[40:43], v[8:15], v[200:207], v[40:43]
	v_mfma_f32_16x16x128_f8f6f4 v[44:47], v[0:7], v[200:207], v[44:47]
	s_setprio 0
	s_barrier
	s_mov_b32 m0, s96
	v_lshl_add_u64 v[140:141], v[170:171], 0, s[30:31]
	ds_read_b128 v[208:211], v232
	ds_read_b128 v[212:215], v232 offset:1024
	ds_read_b128 v[236:239], v232 offset:2048
	ds_read_b128 v[240:243], v232 offset:3072
	global_load_lds_dwordx4 v[140:141], off
	v_lshl_add_u64 v[140:141], v[172:173], 0, s[30:31]
	s_mov_b32 m0, s95
	s_nop 0
	global_load_lds_dwordx4 v[140:141], off
	s_barrier
	s_waitcnt lgkmcnt(0)
	s_setprio 1
	s_waitcnt lgkmcnt(0)
	v_mfma_f32_16x16x128_f8f6f4 v[48:51], v[208:215], v[176:183], v[48:51]
	v_mfma_f32_16x16x128_f8f6f4 v[52:55], v[236:243], v[176:183], v[52:55]
	v_mfma_f32_16x16x128_f8f6f4 v[56:59], v[208:215], v[184:191], v[56:59]
	v_mfma_f32_16x16x128_f8f6f4 v[60:63], v[236:243], v[184:191], v[60:63]
	v_mfma_f32_16x16x128_f8f6f4 v[64:67], v[208:215], v[192:199], v[64:67]
	v_mfma_f32_16x16x128_f8f6f4 v[68:71], v[236:243], v[192:199], v[68:71]
	v_mfma_f32_16x16x128_f8f6f4 v[72:75], v[208:215], v[200:207], v[72:75]
	v_mfma_f32_16x16x128_f8f6f4 v[76:79], v[236:243], v[200:207], v[76:79]
	s_setprio 0
	s_mov_b32 m0, s73
	v_lshl_add_u64 v[140:141], v[174:175], 0, s[30:31]
	s_barrier
	ds_read_b128 v[176:179], v228 offset:16384
	ds_read_b128 v[180:183], v228 offset:17408
	ds_read_b128 v[184:187], v228 offset:18432
	ds_read_b128 v[188:191], v228 offset:19456
	ds_read_b128 v[192:195], v228 offset:20480
	ds_read_b128 v[196:199], v228 offset:21504
	ds_read_b128 v[200:203], v228 offset:22528
	ds_read_b128 v[204:207], v228 offset:23552
	global_load_lds_dwordx4 v[140:141], off
	v_lshl_add_u64 v[140:141], v[168:169], 0, s[30:31]
	s_mov_b32 m0, s74
	s_nop 0
	global_load_lds_dwordx4 v[140:141], off
	s_barrier
	s_waitcnt lgkmcnt(0)
	s_setprio 1
	s_waitcnt lgkmcnt(0)
	v_mfma_f32_16x16x128_f8f6f4 v[80:83], v[8:15], v[176:183], v[80:83]
	v_mfma_f32_16x16x128_f8f6f4 v[84:87], v[0:7], v[176:183], v[84:87]
	v_mfma_f32_16x16x128_f8f6f4 v[88:91], v[8:15], v[184:191], v[88:91]
	v_mfma_f32_16x16x128_f8f6f4 v[92:95], v[0:7], v[184:191], v[92:95]
	v_mfma_f32_16x16x128_f8f6f4 v[96:99], v[8:15], v[192:199], v[96:99]
	v_mfma_f32_16x16x128_f8f6f4 v[100:103], v[0:7], v[192:199], v[100:103]
	v_mfma_f32_16x16x128_f8f6f4 v[104:107], v[8:15], v[200:207], v[104:107]
	v_mfma_f32_16x16x128_f8f6f4 v[108:111], v[0:7], v[200:207], v[108:111]
	s_setprio 0
	s_barrier
	s_add_u32 s56, s50, 0x40700
	s_addc_u32 s57, s51, 0
	s_mov_b32 m0, s97
	v_lshl_add_u64 v[0:1], s[56:57], 0, v[150:151]
	global_load_lds_dwordx4 v[0:1], off
	v_lshl_add_u64 v[0:1], s[56:57], 0, v[154:155]
	s_mov_b32 m0, s52
	s_nop 0
	global_load_lds_dwordx4 v[0:1], off
	s_waitcnt vmcnt(6)
	s_barrier
	s_setprio 1
	v_mfma_f32_16x16x128_f8f6f4 v[112:115], v[208:215], v[176:183], v[112:115]
	v_mfma_f32_16x16x128_f8f6f4 v[116:119], v[236:243], v[176:183], v[116:119]
	v_mfma_f32_16x16x128_f8f6f4 v[120:123], v[208:215], v[184:191], v[120:123]
	v_mfma_f32_16x16x128_f8f6f4 v[124:127], v[236:243], v[184:191], v[124:127]
	v_mfma_f32_16x16x128_f8f6f4 v[128:131], v[208:215], v[192:199], v[128:131]
	v_mfma_f32_16x16x128_f8f6f4 v[132:135], v[236:243], v[192:199], v[132:135]
	v_mfma_f32_16x16x128_f8f6f4 v[144:147], v[208:215], v[200:207], v[144:147]
	v_mfma_f32_16x16x128_f8f6f4 v[136:139], v[236:243], v[200:207], v[136:139]
	s_setprio 0
	s_barrier
	ds_read_b128 v[0:3], v235
	ds_read_b128 v[4:7], v235 offset:1024
	ds_read_b128 v[8:11], v235 offset:2048
	ds_read_b128 v[12:15], v235 offset:3072
	s_add_u32 s56, s48, 0x40700
	s_addc_u32 s57, s49, 0
	s_mov_b32 m0, s75
	v_lshl_add_u64 v[140:141], s[56:57], 0, v[148:149]
	ds_read_b128 v[176:179], v228 offset:32768
	ds_read_b128 v[180:183], v228 offset:33792
	ds_read_b128 v[184:187], v228 offset:34816
	ds_read_b128 v[188:191], v228 offset:35840
	ds_read_b128 v[192:195], v228 offset:36864
	ds_read_b128 v[196:199], v228 offset:37888
	ds_read_b128 v[200:203], v228 offset:38912
	ds_read_b128 v[204:207], v228 offset:39936
	global_load_lds_dwordx4 v[140:141], off
	v_lshl_add_u64 v[140:141], s[56:57], 0, v[152:153]
	s_mov_b32 m0, s76
	s_nop 0
	global_load_lds_dwordx4 v[140:141], off
	s_waitcnt lgkmcnt(8)
	s_barrier
	s_waitcnt lgkmcnt(0)
	s_setprio 1
	s_waitcnt lgkmcnt(0)
	v_mfma_f32_16x16x128_f8f6f4 v[16:19], v[0:7], v[176:183], v[16:19]
	v_mfma_f32_16x16x128_f8f6f4 v[20:23], v[8:15], v[176:183], v[20:23]
	v_mfma_f32_16x16x128_f8f6f4 v[24:27], v[0:7], v[184:191], v[24:27]
	v_mfma_f32_16x16x128_f8f6f4 v[28:31], v[8:15], v[184:191], v[28:31]
	v_mfma_f32_16x16x128_f8f6f4 v[32:35], v[0:7], v[192:199], v[32:35]
	v_mfma_f32_16x16x128_f8f6f4 v[36:39], v[8:15], v[192:199], v[36:39]
	v_mfma_f32_16x16x128_f8f6f4 v[40:43], v[0:7], v[200:207], v[40:43]
	v_mfma_f32_16x16x128_f8f6f4 v[44:47], v[8:15], v[200:207], v[44:47]
	s_setprio 0
	s_barrier
	s_mov_b32 m0, s62
	v_lshl_add_u64 v[140:141], v[170:171], 0, s[38:39]
	ds_read_b128 v[208:211], v234
	ds_read_b128 v[212:215], v234 offset:1024
	ds_read_b128 v[236:239], v234 offset:2048
	ds_read_b128 v[240:243], v234 offset:3072
	global_load_lds_dwordx4 v[140:141], off
	v_lshl_add_u64 v[140:141], v[172:173], 0, s[38:39]
	s_mov_b32 m0, s63
	s_nop 0
	global_load_lds_dwordx4 v[140:141], off
	s_barrier
	s_waitcnt lgkmcnt(0)
	s_setprio 1
	s_waitcnt lgkmcnt(0)
	v_mfma_f32_16x16x128_f8f6f4 v[48:51], v[208:215], v[176:183], v[48:51]
	v_mfma_f32_16x16x128_f8f6f4 v[52:55], v[236:243], v[176:183], v[52:55]
	v_mfma_f32_16x16x128_f8f6f4 v[56:59], v[208:215], v[184:191], v[56:59]
	v_mfma_f32_16x16x128_f8f6f4 v[60:63], v[236:243], v[184:191], v[60:63]
	v_mfma_f32_16x16x128_f8f6f4 v[64:67], v[208:215], v[192:199], v[64:67]
	v_mfma_f32_16x16x128_f8f6f4 v[68:71], v[236:243], v[192:199], v[68:71]
	v_mfma_f32_16x16x128_f8f6f4 v[72:75], v[208:215], v[200:207], v[72:75]
	v_mfma_f32_16x16x128_f8f6f4 v[76:79], v[236:243], v[200:207], v[76:79]
	s_setprio 0
	s_mov_b32 m0, s80
	v_lshl_add_u64 v[140:141], v[174:175], 0, s[38:39]
	s_barrier
	ds_read_b128 v[176:179], v228 offset:49152
	ds_read_b128 v[180:183], v228 offset:50176
	ds_read_b128 v[184:187], v228 offset:51200
	ds_read_b128 v[188:191], v228 offset:52224
	ds_read_b128 v[192:195], v228 offset:53248
	ds_read_b128 v[196:199], v228 offset:54272
	ds_read_b128 v[200:203], v228 offset:55296
	ds_read_b128 v[204:207], v228 offset:56320
	global_load_lds_dwordx4 v[140:141], off
	v_lshl_add_u64 v[140:141], v[168:169], 0, s[38:39]
	s_mov_b32 m0, s81
	s_nop 0
	global_load_lds_dwordx4 v[140:141], off
	s_barrier
	s_waitcnt lgkmcnt(0)
	s_setprio 1
	s_waitcnt lgkmcnt(0)
	v_mfma_f32_16x16x128_f8f6f4 v[80:83], v[0:7], v[176:183], v[80:83]
	v_mfma_f32_16x16x128_f8f6f4 v[84:87], v[8:15], v[176:183], v[84:87]
	v_mfma_f32_16x16x128_f8f6f4 v[88:91], v[0:7], v[184:191], v[88:91]
	v_mfma_f32_16x16x128_f8f6f4 v[92:95], v[8:15], v[184:191], v[92:95]
	v_mfma_f32_16x16x128_f8f6f4 v[96:99], v[0:7], v[192:199], v[96:99]
	v_mfma_f32_16x16x128_f8f6f4 v[100:103], v[8:15], v[192:199], v[100:103]
	v_mfma_f32_16x16x128_f8f6f4 v[104:107], v[0:7], v[200:207], v[104:107]
	v_mfma_f32_16x16x128_f8f6f4 v[108:111], v[8:15], v[200:207], v[108:111]
	s_setprio 0
	s_barrier
	s_add_u32 s50, s50, 0x40780
	s_addc_u32 s51, s51, 0
	s_mov_b32 m0, s53
	v_lshl_add_u64 v[0:1], s[50:51], 0, v[150:151]
	global_load_lds_dwordx4 v[0:1], off
	v_lshl_add_u64 v[0:1], s[50:51], 0, v[154:155]
	s_mov_b32 m0, s64
	s_nop 0
	global_load_lds_dwordx4 v[0:1], off
	s_waitcnt vmcnt(6)
	s_barrier
	s_setprio 1
	v_mfma_f32_16x16x128_f8f6f4 v[112:115], v[208:215], v[176:183], v[112:115]
	v_mfma_f32_16x16x128_f8f6f4 v[116:119], v[236:243], v[176:183], v[116:119]
	v_mfma_f32_16x16x128_f8f6f4 v[120:123], v[208:215], v[184:191], v[120:123]
	v_mfma_f32_16x16x128_f8f6f4 v[124:127], v[236:243], v[184:191], v[124:127]
	v_mfma_f32_16x16x128_f8f6f4 v[128:131], v[208:215], v[192:199], v[128:131]
	v_mfma_f32_16x16x128_f8f6f4 v[132:135], v[236:243], v[192:199], v[132:135]
	v_mfma_f32_16x16x128_f8f6f4 v[144:147], v[208:215], v[200:207], v[144:147]
	v_mfma_f32_16x16x128_f8f6f4 v[136:139], v[236:243], v[200:207], v[136:139]
	s_setprio 0
	s_barrier
	ds_read_b128 v[8:11], v231
	ds_read_b128 v[12:15], v231 offset:1024
	ds_read_b128 v[168:171], v231 offset:2048
	ds_read_b128 v[172:175], v231 offset:3072
	s_add_u32 s48, s48, 0x40780
	s_addc_u32 s49, s49, 0
	s_mov_b32 m0, s94
	v_lshl_add_u64 v[0:1], s[48:49], 0, v[148:149]
	ds_read_b128 v[176:179], v228
	ds_read_b128 v[180:183], v228 offset:1024
	ds_read_b128 v[184:187], v228 offset:2048
	ds_read_b128 v[188:191], v228 offset:3072
	ds_read_b128 v[192:195], v228 offset:4096
	ds_read_b128 v[196:199], v228 offset:5120
	ds_read_b128 v[200:203], v228 offset:6144
	ds_read_b128 v[204:207], v228 offset:7168
	global_load_lds_dwordx4 v[0:1], off
	v_lshl_add_u64 v[0:1], s[48:49], 0, v[152:153]
	s_mov_b32 m0, s93
	s_nop 0
	global_load_lds_dwordx4 v[0:1], off
	s_waitcnt lgkmcnt(8)
	s_barrier
	s_waitcnt lgkmcnt(0)
	s_setprio 1
	s_waitcnt lgkmcnt(0)
	v_mfma_f32_16x16x128_f8f6f4 v[16:19], v[8:15], v[176:183], v[16:19]
	v_mfma_f32_16x16x128_f8f6f4 v[20:23], v[168:175], v[176:183], v[20:23]
	v_mfma_f32_16x16x128_f8f6f4 v[24:27], v[8:15], v[184:191], v[24:27]
	v_mfma_f32_16x16x128_f8f6f4 v[28:31], v[168:175], v[184:191], v[28:31]
	v_mfma_f32_16x16x128_f8f6f4 v[32:35], v[8:15], v[192:199], v[32:35]
	v_mfma_f32_16x16x128_f8f6f4 v[36:39], v[168:175], v[192:199], v[36:39]
	v_mfma_f32_16x16x128_f8f6f4 v[40:43], v[8:15], v[200:207], v[40:43]
	v_mfma_f32_16x16x128_f8f6f4 v[44:47], v[168:175], v[200:207], v[44:47]
	s_setprio 0
	s_barrier
	s_mov_b32 m0, s96
	v_lshl_add_u64 v[0:1], s[60:61], 0, v[150:151]
	ds_read_b128 v[208:211], v232
	ds_read_b128 v[212:215], v232 offset:1024
	ds_read_b128 v[236:239], v232 offset:2048
	ds_read_b128 v[240:243], v232 offset:3072
	global_load_lds_dwordx4 v[0:1], off
	v_lshl_add_u64 v[2:3], s[60:61], 0, v[154:155]
	s_mov_b32 m0, s95
	s_nop 0
	global_load_lds_dwordx4 v[2:3], off
	s_barrier
	s_waitcnt lgkmcnt(0)
	s_setprio 1
	s_waitcnt lgkmcnt(0)
	v_mfma_f32_16x16x128_f8f6f4 v[48:51], v[208:215], v[176:183], v[48:51]
	v_mfma_f32_16x16x128_f8f6f4 v[52:55], v[236:243], v[176:183], v[52:55]
	v_mfma_f32_16x16x128_f8f6f4 v[56:59], v[208:215], v[184:191], v[56:59]
	v_mfma_f32_16x16x128_f8f6f4 v[60:63], v[236:243], v[184:191], v[60:63]
	v_mfma_f32_16x16x128_f8f6f4 v[64:67], v[208:215], v[192:199], v[64:67]
	v_mfma_f32_16x16x128_f8f6f4 v[68:71], v[236:243], v[192:199], v[68:71]
	v_mfma_f32_16x16x128_f8f6f4 v[72:75], v[208:215], v[200:207], v[72:75]
	v_mfma_f32_16x16x128_f8f6f4 v[76:79], v[236:243], v[200:207], v[76:79]
	s_setprio 0
	s_mov_b32 m0, s73
	v_lshl_add_u64 v[4:5], s[54:55], 0, v[148:149]
	s_barrier
	ds_read_b128 v[176:179], v228 offset:16384
	ds_read_b128 v[180:183], v228 offset:17408
	ds_read_b128 v[184:187], v228 offset:18432
	ds_read_b128 v[188:191], v228 offset:19456
	ds_read_b128 v[192:195], v228 offset:20480
	ds_read_b128 v[196:199], v228 offset:21504
	ds_read_b128 v[200:203], v228 offset:22528
	ds_read_b128 v[204:207], v228 offset:23552
	global_load_lds_dwordx4 v[4:5], off
	v_lshl_add_u64 v[6:7], s[54:55], 0, v[152:153]
	s_mov_b32 m0, s74
	s_nop 0
	global_load_lds_dwordx4 v[6:7], off
	s_barrier
	s_waitcnt lgkmcnt(0)
	s_setprio 1
	s_waitcnt lgkmcnt(0)
	v_mfma_f32_16x16x128_f8f6f4 v[80:83], v[8:15], v[176:183], v[80:83]
	v_mfma_f32_16x16x128_f8f6f4 v[84:87], v[168:175], v[176:183], v[84:87]
	v_mfma_f32_16x16x128_f8f6f4 v[88:91], v[8:15], v[184:191], v[88:91]
	v_mfma_f32_16x16x128_f8f6f4 v[92:95], v[168:175], v[184:191], v[92:95]
	v_mfma_f32_16x16x128_f8f6f4 v[96:99], v[8:15], v[192:199], v[96:99]
	v_mfma_f32_16x16x128_f8f6f4 v[100:103], v[168:175], v[192:199], v[100:103]
	v_mfma_f32_16x16x128_f8f6f4 v[104:107], v[8:15], v[200:207], v[104:107]
	v_mfma_f32_16x16x128_f8f6f4 v[108:111], v[168:175], v[200:207], v[108:111]
	s_setprio 0
	s_barrier
	s_add_u32 s48, s60, 0x40000
	s_addc_u32 s49, s61, 0
	s_mov_b32 m0, s97
	v_lshl_add_u64 v[8:9], s[48:49], 0, v[150:151]
	global_load_lds_dwordx4 v[8:9], off
	v_lshl_add_u64 v[8:9], s[48:49], 0, v[154:155]
	s_mov_b32 m0, s52
	s_nop 0
	global_load_lds_dwordx4 v[8:9], off
	s_waitcnt vmcnt(6)
	s_barrier
	s_setprio 1
	v_mfma_f32_16x16x128_f8f6f4 v[112:115], v[208:215], v[176:183], v[112:115]
	v_mfma_f32_16x16x128_f8f6f4 v[116:119], v[236:243], v[176:183], v[116:119]
	v_mfma_f32_16x16x128_f8f6f4 v[120:123], v[208:215], v[184:191], v[120:123]
	v_mfma_f32_16x16x128_f8f6f4 v[124:127], v[236:243], v[184:191], v[124:127]
	v_mfma_f32_16x16x128_f8f6f4 v[128:131], v[208:215], v[192:199], v[128:131]
	v_mfma_f32_16x16x128_f8f6f4 v[132:135], v[236:243], v[192:199], v[132:135]
	v_mfma_f32_16x16x128_f8f6f4 v[144:147], v[208:215], v[200:207], v[144:147]
	v_mfma_f32_16x16x128_f8f6f4 v[136:139], v[236:243], v[200:207], v[136:139]
	s_setprio 0
	s_barrier
	ds_read_b128 v[8:11], v235
	ds_read_b128 v[12:15], v235 offset:1024
	ds_read_b128 v[168:171], v235 offset:2048
	ds_read_b128 v[172:175], v235 offset:3072
	s_add_u32 s48, s54, 0x40000
	s_addc_u32 s49, s55, 0
	s_mov_b32 m0, s75
	v_lshl_add_u64 v[140:141], s[48:49], 0, v[148:149]
	ds_read_b128 v[176:179], v228 offset:32768
	ds_read_b128 v[180:183], v228 offset:33792
	ds_read_b128 v[184:187], v228 offset:34816
	ds_read_b128 v[188:191], v228 offset:35840
	ds_read_b128 v[192:195], v228 offset:36864
	ds_read_b128 v[196:199], v228 offset:37888
	ds_read_b128 v[200:203], v228 offset:38912
	ds_read_b128 v[204:207], v228 offset:39936
	global_load_lds_dwordx4 v[140:141], off
	v_lshl_add_u64 v[140:141], s[48:49], 0, v[152:153]
	s_mov_b32 m0, s76
	s_nop 0
	global_load_lds_dwordx4 v[140:141], off
	s_waitcnt lgkmcnt(8)
	s_barrier
	s_waitcnt lgkmcnt(0)
	s_setprio 1
	s_waitcnt lgkmcnt(0)
	v_mfma_f32_16x16x128_f8f6f4 v[16:19], v[8:15], v[176:183], v[16:19]
	v_mfma_f32_16x16x128_f8f6f4 v[20:23], v[168:175], v[176:183], v[20:23]
	v_mfma_f32_16x16x128_f8f6f4 v[24:27], v[8:15], v[184:191], v[24:27]
	v_mfma_f32_16x16x128_f8f6f4 v[28:31], v[168:175], v[184:191], v[28:31]
	v_mfma_f32_16x16x128_f8f6f4 v[32:35], v[8:15], v[192:199], v[32:35]
	v_mfma_f32_16x16x128_f8f6f4 v[36:39], v[168:175], v[192:199], v[36:39]
	v_mfma_f32_16x16x128_f8f6f4 v[40:43], v[8:15], v[200:207], v[40:43]
	v_mfma_f32_16x16x128_f8f6f4 v[44:47], v[168:175], v[200:207], v[44:47]
	s_setprio 0
	s_barrier
	s_mov_b32 m0, s62
	v_lshl_add_u64 v[0:1], v[0:1], 0, s[8:9]
	ds_read_b128 v[208:211], v234
	ds_read_b128 v[212:215], v234 offset:1024
	ds_read_b128 v[236:239], v234 offset:2048
	ds_read_b128 v[240:243], v234 offset:3072
	global_load_lds_dwordx4 v[0:1], off
	v_lshl_add_u64 v[0:1], v[2:3], 0, s[8:9]
	s_mov_b32 m0, s63
	s_nop 0
	global_load_lds_dwordx4 v[0:1], off
	s_barrier
	s_waitcnt lgkmcnt(0)
	s_setprio 1
	s_waitcnt lgkmcnt(0)
	v_mfma_f32_16x16x128_f8f6f4 v[48:51], v[208:215], v[176:183], v[48:51]
	v_mfma_f32_16x16x128_f8f6f4 v[52:55], v[236:243], v[176:183], v[52:55]
	v_mfma_f32_16x16x128_f8f6f4 v[56:59], v[208:215], v[184:191], v[56:59]
	v_mfma_f32_16x16x128_f8f6f4 v[60:63], v[236:243], v[184:191], v[60:63]
	v_mfma_f32_16x16x128_f8f6f4 v[64:67], v[208:215], v[192:199], v[64:67]
	v_mfma_f32_16x16x128_f8f6f4 v[68:71], v[236:243], v[192:199], v[68:71]
	v_mfma_f32_16x16x128_f8f6f4 v[72:75], v[208:215], v[200:207], v[72:75]
	v_mfma_f32_16x16x128_f8f6f4 v[76:79], v[236:243], v[200:207], v[76:79]
	s_setprio 0
	s_mov_b32 m0, s80
	v_lshl_add_u64 v[0:1], v[4:5], 0, s[8:9]
	s_barrier
	ds_read_b128 v[176:179], v228 offset:49152
	ds_read_b128 v[180:183], v228 offset:50176
	ds_read_b128 v[184:187], v228 offset:51200
	ds_read_b128 v[188:191], v228 offset:52224
	ds_read_b128 v[192:195], v228 offset:53248
	ds_read_b128 v[196:199], v228 offset:54272
	ds_read_b128 v[200:203], v228 offset:55296
	ds_read_b128 v[204:207], v228 offset:56320
	global_load_lds_dwordx4 v[0:1], off
	v_lshl_add_u64 v[0:1], v[6:7], 0, s[8:9]
	s_mov_b32 m0, s81
	s_nop 0
	global_load_lds_dwordx4 v[0:1], off
	s_barrier
	s_waitcnt lgkmcnt(0)
	s_setprio 1
	s_waitcnt lgkmcnt(0)
	v_mfma_f32_16x16x128_f8f6f4 v[80:83], v[8:15], v[176:183], v[80:83]
	v_mfma_f32_16x16x128_f8f6f4 v[84:87], v[168:175], v[176:183], v[84:87]
	v_mfma_f32_16x16x128_f8f6f4 v[88:91], v[8:15], v[184:191], v[88:91]
	v_mfma_f32_16x16x128_f8f6f4 v[92:95], v[168:175], v[184:191], v[92:95]
	v_mfma_f32_16x16x128_f8f6f4 v[96:99], v[8:15], v[192:199], v[96:99]
	v_mfma_f32_16x16x128_f8f6f4 v[100:103], v[168:175], v[192:199], v[100:103]
	v_mfma_f32_16x16x128_f8f6f4 v[104:107], v[8:15], v[200:207], v[104:107]
	v_mfma_f32_16x16x128_f8f6f4 v[108:111], v[168:175], v[200:207], v[108:111]
	s_setprio 0
	s_barrier
	s_add_u32 s48, s60, 0x40080
	s_addc_u32 s49, s61, 0
	s_mov_b32 m0, s53
	v_lshl_add_u64 v[0:1], s[48:49], 0, v[150:151]
	global_load_lds_dwordx4 v[0:1], off
	v_lshl_add_u64 v[0:1], s[48:49], 0, v[154:155]
	s_mov_b32 m0, s64
	s_nop 0
	global_load_lds_dwordx4 v[0:1], off
	s_waitcnt vmcnt(6)
	s_barrier
	s_setprio 1
	v_mfma_f32_16x16x128_f8f6f4 v[112:115], v[208:215], v[176:183], v[112:115]
	v_mfma_f32_16x16x128_f8f6f4 v[116:119], v[236:243], v[176:183], v[116:119]
	v_mfma_f32_16x16x128_f8f6f4 v[120:123], v[208:215], v[184:191], v[120:123]
	v_mfma_f32_16x16x128_f8f6f4 v[124:127], v[236:243], v[184:191], v[124:127]
	v_mfma_f32_16x16x128_f8f6f4 v[128:131], v[208:215], v[192:199], v[128:131]
	v_mfma_f32_16x16x128_f8f6f4 v[132:135], v[236:243], v[192:199], v[132:135]
	v_mfma_f32_16x16x128_f8f6f4 v[144:147], v[208:215], v[200:207], v[144:147]
	v_mfma_f32_16x16x128_f8f6f4 v[136:139], v[236:243], v[200:207], v[136:139]
	s_setprio 0
	v_mov_b32_e32 v156, v230
	s_barrier
	s_nop 7
	s_nop 7
	s_nop 7
	global_load_dwordx2 v[4:5], v156, s[2:3]
	global_load_dwordx2 v[6:7], v156, s[2:3] offset:512
	global_load_dwordx2 v[8:9], v156, s[2:3] offset:1024
	global_load_dwordx2 v[10:11], v156, s[2:3] offset:1536
	global_load_dwordx2 v[168:169], v156, s[2:3] offset:2048
	global_load_dwordx2 v[202:203], v156, s[2:3] offset:2560
	global_load_dwordx2 v[200:201], v156, s[2:3] offset:3072
	global_load_dwordx2 v[198:199], v156, s[2:3] offset:3584
	v_lshl_add_u64 v[0:1], s[2:3], 0, v[156:157]
	v_add_co_u32_e32 v0, vcc, s85, v0
	s_mov_b64 s[2:3], 0x40000
	s_nop 0
	v_addc_co_u32_e32 v1, vcc, 0, v1, vcc
	global_load_dwordx2 v[196:197], v[0:1], off
	global_load_dwordx2 v[194:195], v[0:1], off offset:512
	global_load_dwordx2 v[192:193], v[0:1], off offset:1024
	global_load_dwordx2 v[190:191], v[0:1], off offset:1536
	global_load_dwordx2 v[180:181], v[0:1], off offset:2048
	global_load_dwordx2 v[170:171], v[0:1], off offset:2560
	global_load_dwordx2 v[2:3], v[0:1], off offset:3072
	s_nop 0
	global_load_dwordx2 v[0:1], v[0:1], off offset:3584
	s_mov_b64 s[50:51], s[46:47]
	s_mov_b64 s[48:49], s[44:45]
	s_waitcnt vmcnt(0)
	v_cvt_f32_ubyte1_e32 v13, v4
	v_cvt_f32_ubyte0_e32 v12, v4
	v_cvt_f32_ubyte3_e32 v15, v4
	v_cvt_f32_ubyte2_e32 v14, v4
	v_cvt_f32_ubyte1_e32 v141, v5
	v_cvt_f32_ubyte0_e32 v140, v5
	v_cvt_f32_ubyte3_e32 v143, v5
	v_cvt_f32_ubyte2_e32 v142, v5
	v_cvt_f32_ubyte1_e32 v5, v6
	v_cvt_f32_ubyte0_e32 v4, v6
	v_cvt_f32_ubyte1_e32 v175, v7
	v_cvt_f32_ubyte0_e32 v174, v7
	v_pk_add_f32 v[4:5], v[4:5], 0.5 op_sel_hi:[1,0]
	v_cvt_f32_ubyte3_e32 v173, v6
	v_cvt_f32_ubyte2_e32 v172, v6
	v_cvt_f32_ubyte3_e32 v177, v7
	v_cvt_f32_ubyte2_e32 v176, v7
	v_cvt_f32_ubyte1_e32 v7, v8
	v_cvt_f32_ubyte0_e32 v6, v8
	v_pk_add_f32 v[174:175], v[174:175], 0.5 op_sel_hi:[1,0]
	v_pk_mul_f32 v[4:5], v[4:5], s[40:41] op_sel_hi:[1,0]
	v_pk_add_f32 v[172:173], v[172:173], 0.5 op_sel_hi:[1,0]
	v_pk_add_f32 v[6:7], v[6:7], 0.5 op_sel_hi:[1,0]
	v_pk_mul_f32 v[204:205], v[174:175], s[40:41] op_sel_hi:[1,0]
	v_pk_mul_f32 v[174:175], v[48:49], v[4:5]
	v_cvt_f32_ubyte3_e32 v5, v10
	v_cvt_f32_ubyte2_e32 v4, v10
	v_cvt_f32_ubyte3_e32 v179, v8
	v_cvt_f32_ubyte2_e32 v178, v8
	v_cvt_f32_ubyte1_e32 v183, v9
	v_cvt_f32_ubyte0_e32 v182, v9
	v_cvt_f32_ubyte3_e32 v185, v9
	v_cvt_f32_ubyte2_e32 v184, v9
	v_cvt_f32_ubyte1_e32 v9, v10
	v_pk_add_f32 v[12:13], v[12:13], 0.5 op_sel_hi:[1,0]
	v_pk_mul_f32 v[172:173], v[172:173], s[40:41] op_sel_hi:[1,0]
	v_pk_mul_f32 v[6:7], v[6:7], s[40:41] op_sel_hi:[1,0]
	v_cvt_f32_ubyte0_e32 v8, v10
	v_pk_add_f32 v[4:5], v[4:5], 0.5 op_sel_hi:[1,0]
	v_pk_add_f32 v[14:15], v[14:15], 0.5 op_sel_hi:[1,0]
	v_pk_add_f32 v[184:185], v[184:185], 0.5 op_sel_hi:[1,0]
	v_pk_mul_f32 v[12:13], v[12:13], s[40:41] op_sel_hi:[1,0]
	v_pk_mul_f32 v[172:173], v[50:51], v[172:173]
	v_pk_mul_f32 v[50:51], v[24:25], v[6:7]
	v_pk_add_f32 v[6:7], v[8:9], 0.5 op_sel_hi:[1,0]
	v_pk_mul_f32 v[4:5], v[4:5], s[40:41] op_sel_hi:[1,0]
	v_pk_add_f32 v[182:183], v[182:183], 0.5 op_sel_hi:[1,0]
	v_pk_mul_f32 v[14:15], v[14:15], s[40:41] op_sel_hi:[1,0]
	v_pk_mul_f32 v[210:211], v[184:185], s[40:41] op_sel_hi:[1,0]
	v_pk_mul_f32 v[184:185], v[16:17], v[12:13]
	v_pk_mul_f32 v[6:7], v[6:7], s[40:41] op_sel_hi:[1,0]
	v_pk_mul_f32 v[12:13], v[58:59], v[4:5]
	v_cvt_f32_ubyte1_e32 v5, v11
	v_cvt_f32_ubyte0_e32 v4, v11
	v_pk_add_f32 v[142:143], v[142:143], 0.5 op_sel_hi:[1,0]
	v_pk_mul_f32 v[208:209], v[182:183], s[40:41] op_sel_hi:[1,0]
	v_pk_mul_f32 v[182:183], v[18:19], v[14:15]
	v_pk_mul_f32 v[14:15], v[56:57], v[6:7]
	v_cvt_f32_ubyte3_e32 v7, v11
	v_cvt_f32_ubyte2_e32 v6, v11
	v_pk_add_f32 v[4:5], v[4:5], 0.5 op_sel_hi:[1,0]
	v_pk_add_f32 v[140:141], v[140:141], 0.5 op_sel_hi:[1,0]
	v_pk_mul_f32 v[142:143], v[142:143], s[40:41] op_sel_hi:[1,0]
	v_pk_add_f32 v[6:7], v[6:7], 0.5 op_sel_hi:[1,0]
	v_pk_mul_f32 v[4:5], v[4:5], s[40:41] op_sel_hi:[1,0]
	v_pk_mul_f32 v[140:141], v[140:141], s[40:41] op_sel_hi:[1,0]
	v_pk_mul_f32 v[186:187], v[22:23], v[142:143]
	v_pk_mul_f32 v[6:7], v[6:7], s[40:41] op_sel_hi:[1,0]
	v_pk_mul_f32 v[142:143], v[60:61], v[4:5]
	v_cvt_f32_ubyte1_e32 v5, v168
	v_cvt_f32_ubyte0_e32 v4, v168
	v_pk_mul_f32 v[188:189], v[20:21], v[140:141]
	v_pk_mul_f32 v[140:141], v[62:63], v[6:7]
	v_cvt_f32_ubyte3_e32 v7, v168
	v_cvt_f32_ubyte2_e32 v6, v168
	v_pk_add_f32 v[4:5], v[4:5], 0.5 op_sel_hi:[1,0]
	v_pk_add_f32 v[6:7], v[6:7], 0.5 op_sel_hi:[1,0]
	v_pk_mul_f32 v[8:9], v[4:5], s[40:41] op_sel_hi:[1,0]
	v_pk_mul_f32 v[4:5], v[6:7], s[40:41] op_sel_hi:[1,0]
	v_pk_mul_f32 v[6:7], v[32:33], v[8:9]
	v_cvt_f32_ubyte1_e32 v9, v169
	v_cvt_f32_ubyte0_e32 v8, v169
	v_cvt_f32_ubyte3_e32 v11, v169
	v_cvt_f32_ubyte2_e32 v10, v169
	v_pk_add_f32 v[8:9], v[8:9], 0.5 op_sel_hi:[1,0]
	v_pk_add_f32 v[10:11], v[10:11], 0.5 op_sel_hi:[1,0]
	v_pk_mul_f32 v[8:9], v[8:9], s[40:41] op_sel_hi:[1,0]
	v_pk_mul_f32 v[10:11], v[10:11], s[40:41] op_sel_hi:[1,0]
	v_pk_mul_f32 v[58:59], v[36:37], v[8:9]
	v_cvt_f32_ubyte1_e32 v9, v202
	v_cvt_f32_ubyte0_e32 v8, v202
	v_pk_mul_f32 v[56:57], v[38:39], v[10:11]
	v_cvt_f32_ubyte3_e32 v11, v202
	v_cvt_f32_ubyte2_e32 v10, v202
	v_pk_add_f32 v[8:9], v[8:9], 0.5 op_sel_hi:[1,0]
	v_pk_add_f32 v[10:11], v[10:11], 0.5 op_sel_hi:[1,0]
	v_pk_mul_f32 v[8:9], v[8:9], s[40:41] op_sel_hi:[1,0]
	v_pk_mul_f32 v[10:11], v[10:11], s[40:41] op_sel_hi:[1,0]
	v_pk_mul_f32 v[18:19], v[64:65], v[8:9]
	v_cvt_f32_ubyte1_e32 v9, v203
	v_cvt_f32_ubyte0_e32 v8, v203
	v_pk_mul_f32 v[16:17], v[66:67], v[10:11]
	v_cvt_f32_ubyte3_e32 v11, v203
	v_cvt_f32_ubyte2_e32 v10, v203
	v_pk_add_f32 v[8:9], v[8:9], 0.5 op_sel_hi:[1,0]
	v_pk_add_f32 v[10:11], v[10:11], 0.5 op_sel_hi:[1,0]
	v_pk_mul_f32 v[8:9], v[8:9], s[40:41] op_sel_hi:[1,0]
	v_pk_mul_f32 v[10:11], v[10:11], s[40:41] op_sel_hi:[1,0]
	v_pk_mul_f32 v[168:169], v[68:69], v[8:9]
	v_cvt_f32_ubyte1_e32 v9, v200
	v_cvt_f32_ubyte0_e32 v8, v200
	v_pk_mul_f32 v[70:71], v[70:71], v[10:11]
	v_cvt_f32_ubyte3_e32 v11, v200
	v_cvt_f32_ubyte2_e32 v10, v200
	v_pk_add_f32 v[8:9], v[8:9], 0.5 op_sel_hi:[1,0]
	v_pk_add_f32 v[10:11], v[10:11], 0.5 op_sel_hi:[1,0]
	v_pk_mul_f32 v[20:21], v[8:9], s[40:41] op_sel_hi:[1,0]
	v_pk_mul_f32 v[8:9], v[10:11], s[40:41] op_sel_hi:[1,0]
	v_pk_mul_f32 v[10:11], v[40:41], v[20:21]
	v_cvt_f32_ubyte1_e32 v21, v201
	v_cvt_f32_ubyte0_e32 v20, v201
	v_cvt_f32_ubyte3_e32 v23, v201
	v_cvt_f32_ubyte2_e32 v22, v201
	v_pk_add_f32 v[20:21], v[20:21], 0.5 op_sel_hi:[1,0]
	v_pk_add_f32 v[22:23], v[22:23], 0.5 op_sel_hi:[1,0]
	v_pk_mul_f32 v[20:21], v[20:21], s[40:41] op_sel_hi:[1,0]
	v_pk_mul_f32 v[22:23], v[22:23], s[40:41] op_sel_hi:[1,0]
	v_pk_mul_f32 v[66:67], v[44:45], v[20:21]
	v_cvt_f32_ubyte1_e32 v21, v198
	v_cvt_f32_ubyte0_e32 v20, v198
	v_pk_mul_f32 v[64:65], v[46:47], v[22:23]
	v_cvt_f32_ubyte3_e32 v23, v198
	v_cvt_f32_ubyte2_e32 v22, v198
	v_pk_add_f32 v[20:21], v[20:21], 0.5 op_sel_hi:[1,0]
	v_pk_add_f32 v[178:179], v[178:179], 0.5 op_sel_hi:[1,0]
	v_pk_add_f32 v[22:23], v[22:23], 0.5 op_sel_hi:[1,0]
	v_pk_mul_f32 v[24:25], v[20:21], s[40:41] op_sel_hi:[1,0]
	v_pk_mul_f32 v[206:207], v[178:179], s[40:41] op_sel_hi:[1,0]
	v_pk_mul_f32 v[20:21], v[22:23], s[40:41] op_sel_hi:[1,0]
	v_pk_mul_f32 v[22:23], v[72:73], v[24:25]
	v_cvt_f32_ubyte1_e32 v25, v199
	v_cvt_f32_ubyte0_e32 v24, v199
	v_pk_mul_f32 v[48:49], v[26:27], v[206:207]
	v_cvt_f32_ubyte3_e32 v27, v199
	v_cvt_f32_ubyte2_e32 v26, v199
	v_pk_add_f32 v[24:25], v[24:25], 0.5 op_sel_hi:[1,0]
	v_pk_add_f32 v[26:27], v[26:27], 0.5 op_sel_hi:[1,0]
	v_pk_mul_f32 v[24:25], v[24:25], s[40:41] op_sel_hi:[1,0]
	v_pk_add_f32 v[176:177], v[176:177], 0.5 op_sel_hi:[1,0]
	v_pk_mul_f32 v[20:21], v[74:75], v[20:21]
	v_pk_mul_f32 v[26:27], v[26:27], s[40:41] op_sel_hi:[1,0]
	v_pk_mul_f32 v[74:75], v[76:77], v[24:25]
	v_cvt_f32_ubyte1_e32 v25, v196
	v_cvt_f32_ubyte0_e32 v24, v196
	v_pk_mul_f32 v[176:177], v[176:177], s[40:41] op_sel_hi:[1,0]
	v_pk_mul_f32 v[72:73], v[78:79], v[26:27]
	v_cvt_f32_ubyte3_e32 v27, v196
	v_cvt_f32_ubyte2_e32 v26, v196
	v_pk_add_f32 v[24:25], v[24:25], 0.5 op_sel_hi:[1,0]
	v_pk_mul_f32 v[176:177], v[54:55], v[176:177]
	v_pk_mul_f32 v[54:55], v[28:29], v[208:209]
	v_pk_add_f32 v[26:27], v[26:27], 0.5 op_sel_hi:[1,0]
	v_pk_mul_f32 v[28:29], v[24:25], s[40:41] op_sel_hi:[1,0]
	v_pk_mul_f32 v[24:25], v[26:27], s[40:41] op_sel_hi:[1,0]
	v_pk_mul_f32 v[26:27], v[80:81], v[28:29]
	v_cvt_f32_ubyte1_e32 v29, v197
	v_cvt_f32_ubyte0_e32 v28, v197
	v_pk_mul_f32 v[178:179], v[52:53], v[204:205]
	v_pk_mul_f32 v[52:53], v[30:31], v[210:211]
	v_cvt_f32_ubyte3_e32 v31, v197
	v_cvt_f32_ubyte2_e32 v30, v197
	v_pk_add_f32 v[28:29], v[28:29], 0.5 op_sel_hi:[1,0]
	v_pk_add_f32 v[30:31], v[30:31], 0.5 op_sel_hi:[1,0]
	v_pk_mul_f32 v[28:29], v[28:29], s[40:41] op_sel_hi:[1,0]
	v_pk_mul_f32 v[30:31], v[30:31], s[40:41] op_sel_hi:[1,0]
	v_pk_mul_f32 v[78:79], v[84:85], v[28:29]
	v_cvt_f32_ubyte1_e32 v29, v194
	v_cvt_f32_ubyte0_e32 v28, v194
	v_pk_mul_f32 v[76:77], v[86:87], v[30:31]
	v_cvt_f32_ubyte3_e32 v31, v194
	v_cvt_f32_ubyte2_e32 v30, v194
	v_pk_add_f32 v[28:29], v[28:29], 0.5 op_sel_hi:[1,0]
	v_pk_add_f32 v[30:31], v[30:31], 0.5 op_sel_hi:[1,0]
	v_pk_mul_f32 v[32:33], v[28:29], s[40:41] op_sel_hi:[1,0]
	v_pk_mul_f32 v[28:29], v[30:31], s[40:41] op_sel_hi:[1,0]
	v_pk_mul_f32 v[30:31], v[112:113], v[32:33]
	v_cvt_f32_ubyte1_e32 v33, v195
	v_cvt_f32_ubyte0_e32 v32, v195
	v_pk_mul_f32 v[4:5], v[34:35], v[4:5]
	v_cvt_f32_ubyte3_e32 v35, v195
	v_cvt_f32_ubyte2_e32 v34, v195
	v_pk_add_f32 v[32:33], v[32:33], 0.5 op_sel_hi:[1,0]
	v_pk_add_f32 v[34:35], v[34:35], 0.5 op_sel_hi:[1,0]
	v_pk_mul_f32 v[32:33], v[32:33], s[40:41] op_sel_hi:[1,0]
	v_pk_mul_f32 v[24:25], v[82:83], v[24:25]
	v_pk_mul_f32 v[34:35], v[34:35], s[40:41] op_sel_hi:[1,0]
	v_pk_mul_f32 v[82:83], v[116:117], v[32:33]
	v_cvt_f32_ubyte1_e32 v33, v192
	v_cvt_f32_ubyte0_e32 v32, v192
	v_pk_mul_f32 v[80:81], v[118:119], v[34:35]
	v_cvt_f32_ubyte3_e32 v35, v192
	v_cvt_f32_ubyte2_e32 v34, v192
	v_pk_add_f32 v[32:33], v[32:33], 0.5 op_sel_hi:[1,0]
	v_pk_add_f32 v[34:35], v[34:35], 0.5 op_sel_hi:[1,0]
	v_pk_mul_f32 v[36:37], v[32:33], s[40:41] op_sel_hi:[1,0]
	v_pk_mul_f32 v[32:33], v[34:35], s[40:41] op_sel_hi:[1,0]
	v_pk_mul_f32 v[34:35], v[88:89], v[36:37]
	v_cvt_f32_ubyte1_e32 v37, v193
	v_cvt_f32_ubyte0_e32 v36, v193
	v_cvt_f32_ubyte3_e32 v39, v193
	v_cvt_f32_ubyte2_e32 v38, v193
	v_pk_add_f32 v[36:37], v[36:37], 0.5 op_sel_hi:[1,0]
	v_pk_add_f32 v[38:39], v[38:39], 0.5 op_sel_hi:[1,0]
	v_pk_mul_f32 v[36:37], v[36:37], s[40:41] op_sel_hi:[1,0]
	v_pk_mul_f32 v[38:39], v[38:39], s[40:41] op_sel_hi:[1,0]
	v_pk_mul_f32 v[86:87], v[92:93], v[36:37]
	v_cvt_f32_ubyte1_e32 v37, v190
	v_cvt_f32_ubyte0_e32 v36, v190
	v_pk_mul_f32 v[84:85], v[94:95], v[38:39]
	v_cvt_f32_ubyte3_e32 v39, v190
	v_cvt_f32_ubyte2_e32 v38, v190
	v_pk_add_f32 v[36:37], v[36:37], 0.5 op_sel_hi:[1,0]
	v_pk_add_f32 v[38:39], v[38:39], 0.5 op_sel_hi:[1,0]
	v_pk_mul_f32 v[40:41], v[36:37], s[40:41] op_sel_hi:[1,0]
	v_pk_mul_f32 v[36:37], v[38:39], s[40:41] op_sel_hi:[1,0]
	v_pk_mul_f32 v[38:39], v[120:121], v[40:41]
	v_cvt_f32_ubyte1_e32 v41, v191
	v_cvt_f32_ubyte0_e32 v40, v191
	v_pk_mul_f32 v[8:9], v[42:43], v[8:9]
	v_cvt_f32_ubyte3_e32 v43, v191
	v_cvt_f32_ubyte2_e32 v42, v191
	v_pk_add_f32 v[40:41], v[40:41], 0.5 op_sel_hi:[1,0]
	v_pk_add_f32 v[42:43], v[42:43], 0.5 op_sel_hi:[1,0]
	v_pk_mul_f32 v[40:41], v[40:41], s[40:41] op_sel_hi:[1,0]
	v_pk_mul_f32 v[32:33], v[90:91], v[32:33]
	v_pk_mul_f32 v[42:43], v[42:43], s[40:41] op_sel_hi:[1,0]
	v_pk_mul_f32 v[90:91], v[124:125], v[40:41]
	v_cvt_f32_ubyte1_e32 v41, v180
	v_cvt_f32_ubyte0_e32 v40, v180
	v_pk_mul_f32 v[88:89], v[126:127], v[42:43]
	v_cvt_f32_ubyte3_e32 v43, v180
	v_cvt_f32_ubyte2_e32 v42, v180
	v_pk_add_f32 v[40:41], v[40:41], 0.5 op_sel_hi:[1,0]
	v_pk_add_f32 v[42:43], v[42:43], 0.5 op_sel_hi:[1,0]
	v_pk_mul_f32 v[44:45], v[40:41], s[40:41] op_sel_hi:[1,0]
	v_pk_mul_f32 v[40:41], v[42:43], s[40:41] op_sel_hi:[1,0]
	v_pk_mul_f32 v[42:43], v[96:97], v[44:45]
	v_cvt_f32_ubyte1_e32 v45, v181
	v_cvt_f32_ubyte0_e32 v44, v181
	v_cvt_f32_ubyte3_e32 v47, v181
	v_cvt_f32_ubyte2_e32 v46, v181
	v_pk_add_f32 v[44:45], v[44:45], 0.5 op_sel_hi:[1,0]
	v_pk_add_f32 v[46:47], v[46:47], 0.5 op_sel_hi:[1,0]
	v_pk_mul_f32 v[44:45], v[44:45], s[40:41] op_sel_hi:[1,0]
	v_pk_mul_f32 v[46:47], v[46:47], s[40:41] op_sel_hi:[1,0]
	v_pk_mul_f32 v[94:95], v[100:101], v[44:45]
	v_cvt_f32_ubyte1_e32 v45, v170
	v_cvt_f32_ubyte0_e32 v44, v170
	v_pk_mul_f32 v[92:93], v[102:103], v[46:47]
	v_cvt_f32_ubyte3_e32 v47, v170
	v_cvt_f32_ubyte2_e32 v46, v170
	v_pk_add_f32 v[44:45], v[44:45], 0.5 op_sel_hi:[1,0]
	v_pk_add_f32 v[46:47], v[46:47], 0.5 op_sel_hi:[1,0]
	v_pk_mul_f32 v[60:61], v[44:45], s[40:41] op_sel_hi:[1,0]
	v_pk_mul_f32 v[44:45], v[46:47], s[40:41] op_sel_hi:[1,0]
	v_pk_mul_f32 v[46:47], v[128:129], v[60:61]
	v_cvt_f32_ubyte1_e32 v61, v171
	v_cvt_f32_ubyte0_e32 v60, v171
	v_cvt_f32_ubyte3_e32 v63, v171
	v_cvt_f32_ubyte2_e32 v62, v171
	v_pk_add_f32 v[60:61], v[60:61], 0.5 op_sel_hi:[1,0]
	v_pk_add_f32 v[62:63], v[62:63], 0.5 op_sel_hi:[1,0]
	v_pk_mul_f32 v[60:61], v[60:61], s[40:41] op_sel_hi:[1,0]
	v_pk_mul_f32 v[40:41], v[98:99], v[40:41]
	v_pk_mul_f32 v[62:63], v[62:63], s[40:41] op_sel_hi:[1,0]
	v_pk_mul_f32 v[98:99], v[132:133], v[60:61]
	v_cvt_f32_ubyte1_e32 v61, v2
	v_cvt_f32_ubyte0_e32 v60, v2
	v_pk_mul_f32 v[96:97], v[134:135], v[62:63]
	v_cvt_f32_ubyte3_e32 v63, v2
	v_cvt_f32_ubyte2_e32 v62, v2
	v_pk_add_f32 v[60:61], v[60:61], 0.5 op_sel_hi:[1,0]
	v_pk_add_f32 v[62:63], v[62:63], 0.5 op_sel_hi:[1,0]
	v_pk_mul_f32 v[68:69], v[60:61], s[40:41] op_sel_hi:[1,0]
	v_cvt_f32_ubyte3_e32 v101, v3
	v_cvt_f32_ubyte2_e32 v100, v3
	v_pk_mul_f32 v[60:61], v[62:63], s[40:41] op_sel_hi:[1,0]
	v_pk_mul_f32 v[62:63], v[104:105], v[68:69]
	v_cvt_f32_ubyte1_e32 v69, v3
	v_cvt_f32_ubyte0_e32 v68, v3
	v_pk_add_f32 v[2:3], v[100:101], 0.5 op_sel_hi:[1,0]
	v_pk_add_f32 v[68:69], v[68:69], 0.5 op_sel_hi:[1,0]
	v_pk_mul_f32 v[2:3], v[2:3], s[40:41] op_sel_hi:[1,0]
	v_pk_mul_f32 v[68:69], v[68:69], s[40:41] op_sel_hi:[1,0]
	v_pk_mul_f32 v[100:101], v[110:111], v[2:3]
	v_cvt_f32_ubyte1_e32 v3, v0
	v_cvt_f32_ubyte0_e32 v2, v0
	v_pk_mul_f32 v[102:103], v[108:109], v[68:69]
	v_cvt_f32_ubyte3_e32 v69, v0
	v_cvt_f32_ubyte2_e32 v68, v0
	v_pk_add_f32 v[2:3], v[2:3], 0.5 op_sel_hi:[1,0]
	v_lshl_add_u32 v108, s92, 8, v226
	v_pk_mul_f32 v[28:29], v[114:115], v[28:29]
	v_pk_mul_f32 v[60:61], v[106:107], v[60:61]
	v_pk_add_f32 v[68:69], v[68:69], 0.5 op_sel_hi:[1,0]
	v_pk_mul_f32 v[104:105], v[2:3], s[40:41] op_sel_hi:[1,0]
	v_cvt_f32_ubyte3_e32 v107, v1
	v_cvt_f32_ubyte2_e32 v106, v1
	v_ashrrev_i32_e32 v109, 31, v108
	v_pk_mul_f32 v[112:113], v[182:183], s[42:43] op_sel_hi:[1,0]
	v_pk_mul_f32 v[114:115], v[184:185], s[42:43] op_sel_hi:[1,0]
	v_pk_mul_f32 v[2:3], v[68:69], s[40:41] op_sel_hi:[1,0]
	v_pk_mul_f32 v[68:69], v[144:145], v[104:105]
	v_cvt_f32_ubyte1_e32 v105, v1
	v_cvt_f32_ubyte0_e32 v104, v1
	v_pk_add_f32 v[0:1], v[106:107], 0.5 op_sel_hi:[1,0]
	v_lshlrev_b64 v[106:107], 11, v[108:109]
	v_pk_mul_f32 v[118:119], v[188:189], s[42:43] op_sel_hi:[1,0]
	v_med3_f32 v109, v114, s86, v233
	v_med3_f32 v114, v115, s86, v233
	v_med3_f32 v115, v112, s86, v233
	v_mov_b32_e32 v112, v157
	v_med3_f32 v120, v113, s86, v233
	v_cvt_pk_fp8_f32 v112, v109, v114
	v_med3_f32 v109, v118, s86, v233
	v_med3_f32 v114, v119, s86, v233
	v_mov_b32_e32 v113, v157
	v_cvt_pk_fp8_f32 v113, v109, v114
	v_pk_mul_f32 v[116:117], v[186:187], s[42:43] op_sel_hi:[1,0]
	v_cvt_pk_fp8_f32 v112, v115, v120 op_sel:[0,0,1]
	v_med3_f32 v109, v116, s86, v233
	v_med3_f32 v114, v117, s86, v233
	v_cvt_pk_fp8_f32 v113, v109, v114 op_sel:[0,0,1]
	v_pk_mul_f32 v[114:115], v[172:173], s[42:43] op_sel_hi:[1,0]
	v_pk_mul_f32 v[116:117], v[174:175], s[42:43] op_sel_hi:[1,0]
	v_pk_mul_f32 v[120:121], v[178:179], s[42:43] op_sel_hi:[1,0]
	v_med3_f32 v109, v116, s86, v233
	v_med3_f32 v116, v117, s86, v233
	v_med3_f32 v117, v114, s86, v233
	v_mov_b32_e32 v114, v157
	v_pk_mul_f32 v[36:37], v[122:123], v[36:37]
	v_med3_f32 v122, v115, s86, v233
	v_cvt_pk_fp8_f32 v114, v109, v116
	v_med3_f32 v109, v120, s86, v233
	v_med3_f32 v116, v121, s86, v233
	v_mov_b32_e32 v115, v157
	v_cvt_pk_fp8_f32 v115, v109, v116
	v_pk_mul_f32 v[118:119], v[176:177], s[42:43] op_sel_hi:[1,0]
	v_lshl_or_b32 v110, s91, 8, v229
	v_med3_f32 v109, v118, s86, v233
	v_med3_f32 v116, v119, s86, v233
	v_cvt_pk_fp8_f32 v114, v117, v122 op_sel:[0,0,1]
	v_cvt_pk_fp8_f32 v115, v109, v116 op_sel:[0,0,1]
	v_ashrrev_i32_e32 v111, 31, v110
	v_lshl_add_u64 v[106:107], s[6:7], 0, v[106:107]
	v_pk_mul_f32 v[48:49], v[48:49], s[42:43] op_sel_hi:[1,0]
	v_pk_mul_f32 v[50:51], v[50:51], s[42:43] op_sel_hi:[1,0]
	v_lshl_add_u64 v[106:107], v[106:107], 0, v[110:111]
	v_pk_mul_f32 v[54:55], v[54:55], s[42:43] op_sel_hi:[1,0]
	v_med3_f32 v50, v50, s86, v233
	v_med3_f32 v51, v51, s86, v233
	v_med3_f32 v109, v48, s86, v233
	v_mov_b32_e32 v48, v157
	global_store_dwordx2 v[106:107], v[112:113], off
	global_store_dwordx2 v[106:107], v[114:115], off offset:128
	v_pk_mul_f32 v[52:53], v[52:53], s[42:43] op_sel_hi:[1,0]
	v_med3_f32 v114, v49, s86, v233
	v_cvt_pk_fp8_f32 v48, v50, v51
	v_med3_f32 v50, v54, s86, v233
	v_med3_f32 v51, v55, s86, v233
	v_mov_b32_e32 v49, v157
	v_pk_mul_f32 v[12:13], v[12:13], s[42:43] op_sel_hi:[1,0]
	v_pk_mul_f32 v[14:15], v[14:15], s[42:43] op_sel_hi:[1,0]
	v_cvt_pk_fp8_f32 v49, v50, v51
	v_med3_f32 v50, v52, s86, v233
	v_med3_f32 v51, v53, s86, v233
	v_pk_mul_f32 v[52:53], v[142:143], s[42:43] op_sel_hi:[1,0]
	v_med3_f32 v14, v14, s86, v233
	v_med3_f32 v15, v15, s86, v233
	v_med3_f32 v54, v12, s86, v233
	v_mov_b32_e32 v12, v157
	v_med3_f32 v55, v13, s86, v233
	v_cvt_pk_fp8_f32 v12, v14, v15
	v_med3_f32 v14, v52, s86, v233
	v_med3_f32 v15, v53, s86, v233
	v_mov_b32_e32 v13, v157
	v_cvt_pk_fp8_f32 v13, v14, v15
	v_or_b32_e32 v112, 16, v108
	v_cvt_pk_fp8_f32 v49, v50, v51 op_sel:[0,0,1]
	v_pk_mul_f32 v[50:51], v[140:141], s[42:43] op_sel_hi:[1,0]
	v_ashrrev_i32_e32 v113, 31, v112
	v_cvt_pk_fp8_f32 v48, v109, v114 op_sel:[0,0,1]
	v_med3_f32 v14, v50, s86, v233
	v_med3_f32 v15, v51, s86, v233
	v_lshlrev_b64 v[112:113], 11, v[112:113]
	v_cvt_pk_fp8_f32 v12, v54, v55 op_sel:[0,0,1]
	v_cvt_pk_fp8_f32 v13, v14, v15 op_sel:[0,0,1]
	v_lshl_add_u64 v[14:15], s[6:7], 0, v[112:113]
	v_lshl_add_u64 v[14:15], v[14:15], 0, v[110:111]
	v_pk_mul_f32 v[4:5], v[4:5], s[42:43] op_sel_hi:[1,0]
	v_pk_mul_f32 v[6:7], v[6:7], s[42:43] op_sel_hi:[1,0]
	global_store_dwordx2 v[14:15], v[48:49], off
	global_store_dwordx2 v[14:15], v[12:13], off offset:128
	v_pk_mul_f32 v[48:49], v[58:59], s[42:43] op_sel_hi:[1,0]
	v_med3_f32 v6, v6, s86, v233
	v_med3_f32 v7, v7, s86, v233
	v_med3_f32 v50, v4, s86, v233
	v_mov_b32_e32 v4, v157
	v_med3_f32 v51, v5, s86, v233
	v_cvt_pk_fp8_f32 v4, v6, v7
	v_med3_f32 v6, v48, s86, v233
	v_med3_f32 v7, v49, s86, v233
	v_mov_b32_e32 v5, v157
	v_cvt_pk_fp8_f32 v5, v6, v7
	v_pk_mul_f32 v[14:15], v[56:57], s[42:43] op_sel_hi:[1,0]
	v_or_b32_e32 v12, 32, v108
	v_med3_f32 v6, v14, s86, v233
	v_med3_f32 v7, v15, s86, v233
	v_cvt_pk_fp8_f32 v5, v6, v7 op_sel:[0,0,1]
	v_pk_mul_f32 v[6:7], v[16:17], s[42:43] op_sel_hi:[1,0]
	v_pk_mul_f32 v[14:15], v[18:19], s[42:43] op_sel_hi:[1,0]
	v_pk_mul_f32 v[18:19], v[168:169], s[42:43] op_sel_hi:[1,0]
	v_med3_f32 v14, v14, s86, v233
	v_med3_f32 v15, v15, s86, v233
	v_med3_f32 v48, v6, s86, v233
	v_mov_b32_e32 v6, v157
	v_med3_f32 v49, v7, s86, v233
	v_cvt_pk_fp8_f32 v6, v14, v15
	v_med3_f32 v14, v18, s86, v233
	v_med3_f32 v15, v19, s86, v233
	v_mov_b32_e32 v7, v157
	v_cvt_pk_fp8_f32 v7, v14, v15
	v_pk_mul_f32 v[16:17], v[70:71], s[42:43] op_sel_hi:[1,0]
	v_ashrrev_i32_e32 v13, 31, v12
	v_cvt_pk_fp8_f32 v4, v50, v51 op_sel:[0,0,1]
	v_med3_f32 v14, v16, s86, v233
	v_med3_f32 v15, v17, s86, v233
	v_lshlrev_b64 v[12:13], 11, v[12:13]
	v_cvt_pk_fp8_f32 v6, v48, v49 op_sel:[0,0,1]
	v_cvt_pk_fp8_f32 v7, v14, v15 op_sel:[0,0,1]
	v_lshl_add_u64 v[12:13], s[6:7], 0, v[12:13]
	v_lshl_add_u64 v[12:13], v[12:13], 0, v[110:111]
	global_store_dwordx2 v[12:13], v[4:5], off
	global_store_dwordx2 v[12:13], v[6:7], off offset:128
	v_pk_mul_f32 v[6:7], v[8:9], s[42:43] op_sel_hi:[1,0]
	v_pk_mul_f32 v[8:9], v[10:11], s[42:43] op_sel_hi:[1,0]
	v_pk_mul_f32 v[12:13], v[66:67], s[42:43] op_sel_hi:[1,0]
	v_med3_f32 v8, v8, s86, v233
	v_med3_f32 v9, v9, s86, v233
	v_med3_f32 v14, v6, s86, v233
	v_mov_b32_e32 v6, v157
	v_med3_f32 v15, v7, s86, v233
	v_cvt_pk_fp8_f32 v6, v8, v9
	v_med3_f32 v8, v12, s86, v233
	v_med3_f32 v9, v13, s86, v233
	v_mov_b32_e32 v7, v157
	v_cvt_pk_fp8_f32 v7, v8, v9
	v_pk_mul_f32 v[10:11], v[64:65], s[42:43] op_sel_hi:[1,0]
	v_cvt_pk_fp8_f32 v6, v14, v15 op_sel:[0,0,1]
	v_med3_f32 v8, v10, s86, v233
	v_med3_f32 v9, v11, s86, v233
	v_cvt_pk_fp8_f32 v7, v8, v9 op_sel:[0,0,1]
	v_pk_mul_f32 v[8:9], v[20:21], s[42:43] op_sel_hi:[1,0]
	v_pk_mul_f32 v[10:11], v[22:23], s[42:43] op_sel_hi:[1,0]
	v_pk_mul_f32 v[14:15], v[74:75], s[42:43] op_sel_hi:[1,0]
	v_med3_f32 v10, v10, s86, v233
	v_med3_f32 v11, v11, s86, v233
	v_med3_f32 v16, v8, s86, v233
	v_mov_b32_e32 v8, v157
	v_med3_f32 v17, v9, s86, v233
	v_cvt_pk_fp8_f32 v8, v10, v11
	v_med3_f32 v10, v14, s86, v233
	v_med3_f32 v11, v15, s86, v233
	v_mov_b32_e32 v9, v157
	v_cvt_pk_fp8_f32 v9, v10, v11
	v_or_b32_e32 v4, 48, v108
	v_pk_mul_f32 v[12:13], v[72:73], s[42:43] op_sel_hi:[1,0]
	v_ashrrev_i32_e32 v5, 31, v4
	v_med3_f32 v10, v12, s86, v233
	v_med3_f32 v11, v13, s86, v233
	v_lshlrev_b64 v[4:5], 11, v[4:5]
	v_cvt_pk_fp8_f32 v8, v16, v17 op_sel:[0,0,1]
	v_cvt_pk_fp8_f32 v9, v10, v11 op_sel:[0,0,1]
	v_lshl_add_u64 v[4:5], s[6:7], 0, v[4:5]
	v_lshl_add_u64 v[4:5], v[4:5], 0, v[110:111]
	global_store_dwordx2 v[4:5], v[6:7], off
	global_store_dwordx2 v[4:5], v[8:9], off offset:128
	v_pk_mul_f32 v[6:7], v[24:25], s[42:43] op_sel_hi:[1,0]
	v_pk_mul_f32 v[8:9], v[26:27], s[42:43] op_sel_hi:[1,0]
	v_pk_mul_f32 v[12:13], v[78:79], s[42:43] op_sel_hi:[1,0]
	v_med3_f32 v8, v8, s86, v233
	v_med3_f32 v9, v9, s86, v233
	v_med3_f32 v14, v6, s86, v233
	v_mov_b32_e32 v6, v157
	v_med3_f32 v15, v7, s86, v233
	v_cvt_pk_fp8_f32 v6, v8, v9
	v_med3_f32 v8, v12, s86, v233
	v_med3_f32 v9, v13, s86, v233
	v_mov_b32_e32 v7, v157
	v_cvt_pk_fp8_f32 v7, v8, v9
	v_pk_mul_f32 v[10:11], v[76:77], s[42:43] op_sel_hi:[1,0]
	v_cvt_pk_fp8_f32 v6, v14, v15 op_sel:[0,0,1]
	v_med3_f32 v8, v10, s86, v233
	v_med3_f32 v9, v11, s86, v233
	v_cvt_pk_fp8_f32 v7, v8, v9 op_sel:[0,0,1]
	v_pk_mul_f32 v[8:9], v[28:29], s[42:43] op_sel_hi:[1,0]
	v_pk_mul_f32 v[10:11], v[30:31], s[42:43] op_sel_hi:[1,0]
	v_pk_mul_f32 v[14:15], v[82:83], s[42:43] op_sel_hi:[1,0]
	v_med3_f32 v10, v10, s86, v233
	v_med3_f32 v11, v11, s86, v233
	v_med3_f32 v16, v8, s86, v233
	v_mov_b32_e32 v8, v157
	v_med3_f32 v17, v9, s86, v233
	v_cvt_pk_fp8_f32 v8, v10, v11
	v_med3_f32 v10, v14, s86, v233
	v_med3_f32 v11, v15, s86, v233
	v_mov_b32_e32 v9, v157
	v_cvt_pk_fp8_f32 v9, v10, v11
	v_pk_mul_f32 v[12:13], v[80:81], s[42:43] op_sel_hi:[1,0]
	v_lshl_add_u64 v[4:5], v[106:107], 0, s[2:3]
	v_med3_f32 v10, v12, s86, v233
	v_med3_f32 v11, v13, s86, v233
	v_cvt_pk_fp8_f32 v8, v16, v17 op_sel:[0,0,1]
	v_cvt_pk_fp8_f32 v9, v10, v11 op_sel:[0,0,1]
	s_mov_b32 s2, 0x40000
	v_add_co_u32_e32 v10, vcc, s2, v106
	v_pk_mul_f32 v[12:13], v[86:87], s[42:43] op_sel_hi:[1,0]
	s_nop 0
	v_addc_co_u32_e32 v11, vcc, 0, v107, vcc
	global_store_dwordx2 v[10:11], v[6:7], off
	global_store_dwordx2 v[4:5], v[8:9], off offset:128
	v_pk_mul_f32 v[6:7], v[32:33], s[42:43] op_sel_hi:[1,0]
	v_pk_mul_f32 v[8:9], v[34:35], s[42:43] op_sel_hi:[1,0]
	v_med3_f32 v14, v6, s86, v233
	v_med3_f32 v8, v8, s86, v233
	v_med3_f32 v9, v9, s86, v233
	v_mov_b32_e32 v6, v157
	v_med3_f32 v15, v7, s86, v233
	v_cvt_pk_fp8_f32 v6, v8, v9
	v_med3_f32 v8, v12, s86, v233
	v_med3_f32 v9, v13, s86, v233
	v_mov_b32_e32 v7, v157
	v_cvt_pk_fp8_f32 v7, v8, v9
	v_pk_mul_f32 v[10:11], v[84:85], s[42:43] op_sel_hi:[1,0]
	v_cvt_pk_fp8_f32 v6, v14, v15 op_sel:[0,0,1]
	v_med3_f32 v8, v10, s86, v233
	v_med3_f32 v9, v11, s86, v233
	v_cvt_pk_fp8_f32 v7, v8, v9 op_sel:[0,0,1]
	v_pk_mul_f32 v[8:9], v[36:37], s[42:43] op_sel_hi:[1,0]
	v_pk_mul_f32 v[10:11], v[38:39], s[42:43] op_sel_hi:[1,0]
	v_pk_mul_f32 v[14:15], v[90:91], s[42:43] op_sel_hi:[1,0]
	v_med3_f32 v10, v10, s86, v233
	v_med3_f32 v11, v11, s86, v233
	v_med3_f32 v16, v8, s86, v233
	v_mov_b32_e32 v8, v157
	v_med3_f32 v17, v9, s86, v233
	v_cvt_pk_fp8_f32 v8, v10, v11
	v_med3_f32 v10, v14, s86, v233
	v_med3_f32 v11, v15, s86, v233
	v_mov_b32_e32 v9, v157
	v_cvt_pk_fp8_f32 v9, v10, v11
	v_pk_mul_f32 v[12:13], v[88:89], s[42:43] op_sel_hi:[1,0]
	s_mov_b64 s[2:3], 0x48000
	v_med3_f32 v10, v12, s86, v233
	v_med3_f32 v11, v13, s86, v233
	v_lshl_add_u64 v[4:5], v[106:107], 0, s[2:3]
	v_cvt_pk_fp8_f32 v8, v16, v17 op_sel:[0,0,1]
	v_cvt_pk_fp8_f32 v9, v10, v11 op_sel:[0,0,1]
	s_mov_b32 s2, 0x48000
	v_add_co_u32_e32 v10, vcc, s2, v106
	v_pk_mul_f32 v[12:13], v[94:95], s[42:43] op_sel_hi:[1,0]
	s_nop 0
	v_addc_co_u32_e32 v11, vcc, 0, v107, vcc
	global_store_dwordx2 v[10:11], v[6:7], off
	global_store_dwordx2 v[4:5], v[8:9], off offset:128
	v_pk_mul_f32 v[6:7], v[40:41], s[42:43] op_sel_hi:[1,0]
	v_pk_mul_f32 v[8:9], v[42:43], s[42:43] op_sel_hi:[1,0]
	v_med3_f32 v14, v6, s86, v233
	v_med3_f32 v8, v8, s86, v233
	v_med3_f32 v9, v9, s86, v233
	v_mov_b32_e32 v6, v157
	v_med3_f32 v15, v7, s86, v233
	v_cvt_pk_fp8_f32 v6, v8, v9
	v_med3_f32 v8, v12, s86, v233
	v_med3_f32 v9, v13, s86, v233
	v_mov_b32_e32 v7, v157
	v_cvt_pk_fp8_f32 v7, v8, v9
	v_pk_mul_f32 v[10:11], v[92:93], s[42:43] op_sel_hi:[1,0]
	v_pk_mul_f32 v[44:45], v[130:131], v[44:45]
	v_med3_f32 v8, v10, s86, v233
	v_med3_f32 v9, v11, s86, v233
	v_cvt_pk_fp8_f32 v7, v8, v9 op_sel:[0,0,1]
	v_pk_mul_f32 v[8:9], v[44:45], s[42:43] op_sel_hi:[1,0]
	v_pk_mul_f32 v[10:11], v[46:47], s[42:43] op_sel_hi:[1,0]
	v_cvt_pk_fp8_f32 v6, v14, v15 op_sel:[0,0,1]
	v_pk_mul_f32 v[14:15], v[98:99], s[42:43] op_sel_hi:[1,0]
	v_med3_f32 v10, v10, s86, v233
	v_med3_f32 v11, v11, s86, v233
	v_med3_f32 v16, v8, s86, v233
	v_mov_b32_e32 v8, v157
	v_med3_f32 v17, v9, s86, v233
	v_cvt_pk_fp8_f32 v8, v10, v11
	v_med3_f32 v10, v14, s86, v233
	v_med3_f32 v11, v15, s86, v233
	v_mov_b32_e32 v9, v157
	v_cvt_pk_fp8_f32 v9, v10, v11
	v_pk_mul_f32 v[12:13], v[96:97], s[42:43] op_sel_hi:[1,0]
	s_mov_b64 s[2:3], 0x50000
	v_med3_f32 v10, v12, s86, v233
	v_med3_f32 v11, v13, s86, v233
	v_lshl_add_u64 v[4:5], v[106:107], 0, s[2:3]
	v_cvt_pk_fp8_f32 v8, v16, v17 op_sel:[0,0,1]
	v_cvt_pk_fp8_f32 v9, v10, v11 op_sel:[0,0,1]
	s_mov_b32 s2, 0x50000
	v_add_co_u32_e32 v10, vcc, s2, v106
	v_pk_mul_f32 v[12:13], v[102:103], s[42:43] op_sel_hi:[1,0]
	s_nop 0
	v_addc_co_u32_e32 v11, vcc, 0, v107, vcc
	global_store_dwordx2 v[10:11], v[6:7], off
	global_store_dwordx2 v[4:5], v[8:9], off offset:128
	v_pk_mul_f32 v[6:7], v[60:61], s[42:43] op_sel_hi:[1,0]
	v_pk_mul_f32 v[8:9], v[62:63], s[42:43] op_sel_hi:[1,0]
	v_med3_f32 v14, v6, s86, v233
	v_med3_f32 v8, v8, s86, v233
	v_med3_f32 v9, v9, s86, v233
	v_mov_b32_e32 v6, v157
	v_med3_f32 v15, v7, s86, v233
	v_cvt_pk_fp8_f32 v6, v8, v9
	v_med3_f32 v8, v12, s86, v233
	v_med3_f32 v9, v13, s86, v233
	v_mov_b32_e32 v7, v157
	v_cvt_pk_fp8_f32 v7, v8, v9
	v_pk_add_f32 v[104:105], v[104:105], 0.5 op_sel_hi:[1,0]
	v_pk_mul_f32 v[10:11], v[100:101], s[42:43] op_sel_hi:[1,0]
	v_pk_mul_f32 v[2:3], v[146:147], v[2:3]
	v_pk_mul_f32 v[104:105], v[104:105], s[40:41] op_sel_hi:[1,0]
	v_med3_f32 v8, v10, s86, v233
	v_med3_f32 v9, v11, s86, v233
	v_pk_mul_f32 v[104:105], v[136:137], v[104:105]
	v_cvt_pk_fp8_f32 v7, v8, v9 op_sel:[0,0,1]
	v_pk_mul_f32 v[2:3], v[2:3], s[42:43] op_sel_hi:[1,0]
	v_pk_mul_f32 v[8:9], v[68:69], s[42:43] op_sel_hi:[1,0]
	v_pk_mul_f32 v[10:11], v[104:105], s[42:43] op_sel_hi:[1,0]
	v_med3_f32 v8, v8, s86, v233
	v_med3_f32 v9, v9, s86, v233
	v_med3_f32 v12, v2, s86, v233
	v_mov_b32_e32 v2, v157
	v_med3_f32 v13, v3, s86, v233
	v_cvt_pk_fp8_f32 v2, v8, v9
	v_med3_f32 v8, v10, s86, v233
	v_med3_f32 v9, v11, s86, v233
	v_mov_b32_e32 v3, v157
	v_pk_mul_f32 v[0:1], v[0:1], s[40:41] op_sel_hi:[1,0]
	v_cvt_pk_fp8_f32 v3, v8, v9
	v_pk_mul_f32 v[0:1], v[138:139], v[0:1]
	s_mov_b64 s[2:3], 0x58000
	v_pk_mul_f32 v[0:1], v[0:1], s[42:43] op_sel_hi:[1,0]
	v_lshl_add_u64 v[4:5], v[106:107], 0, s[2:3]
	v_cvt_pk_fp8_f32 v6, v14, v15 op_sel:[0,0,1]
	v_med3_f32 v0, v0, s86, v233
	v_med3_f32 v1, v1, s86, v233
	s_mov_b32 s2, 0x58000
	v_cvt_pk_fp8_f32 v2, v12, v13 op_sel:[0,0,1]
	v_cvt_pk_fp8_f32 v3, v0, v1 op_sel:[0,0,1]
	v_add_co_u32_e32 v0, vcc, s2, v106
	s_mov_b32 s91, s87
	s_nop 0
	v_addc_co_u32_e32 v1, vcc, 0, v107, vcc
	s_and_b64 vcc, exec, s[0:1]
	s_mov_b32 s92, s88
	global_store_dwordx2 v[0:1], v[6:7], off
	global_store_dwordx2 v[4:5], v[2:3], off offset:128
	s_cbranch_vccz .LBB0_904
	s_waitcnt vmcnt(0)
	s_cmpk_gt_u32 s68, 0xff
	s_cbranch_scc1 .LBB0_915
	s_barrier

.LBB0_985:
	ds_read_b128 v[8:11], v176
	ds_read_b128 v[12:15], v176 offset:1024
	ds_read_b128 v[0:3], v176 offset:2048
	ds_read_b128 v[4:7], v176 offset:3072
	s_add_u32 s20, s18, 0xfffc0080
	s_addc_u32 s21, s19, -1
	s_cmp_eq_u32 s67, 12
	s_cselect_b32 s23, s61, s21
	s_cselect_b32 s22, s62, s20
	s_cselect_b32 s21, s63, s66
	s_cselect_b32 s20, s64, s65
	v_lshl_add_u64 v[158:159], s[18:19], 0, v[156:157]
	s_add_i32 m0, s44, 0xc000
	ds_read_b128 v[180:183], v177
	ds_read_b128 v[184:187], v177 offset:1024
	ds_read_b128 v[188:191], v177 offset:2048
	ds_read_b128 v[192:195], v177 offset:3072
	ds_read_b128 v[196:199], v177 offset:4096
	ds_read_b128 v[200:203], v177 offset:5120
	ds_read_b128 v[204:207], v177 offset:6144
	ds_read_b128 v[208:211], v177 offset:7168
	global_load_lds_dwordx4 v[158:159], off
	v_lshl_add_u64 v[158:159], s[18:19], 0, v[154:155]
	s_add_i32 m0, s44, 0xe000
	s_nop 0
	global_load_lds_dwordx4 v[158:159], off
	s_waitcnt lgkmcnt(8)
	s_barrier
	s_waitcnt lgkmcnt(0)
	s_setprio 1
	s_waitcnt lgkmcnt(0)
	v_mfma_f32_16x16x128_f8f6f4 v[140:143], v[8:15], v[180:187], v[140:143]
	v_mfma_f32_16x16x128_f8f6f4 v[136:139], v[0:7], v[180:187], v[136:139]
	v_mfma_f32_16x16x128_f8f6f4 v[128:131], v[8:15], v[188:195], v[128:131]
	v_mfma_f32_16x16x128_f8f6f4 v[120:123], v[0:7], v[188:195], v[120:123]
	v_mfma_f32_16x16x128_f8f6f4 v[112:115], v[8:15], v[196:203], v[112:115]
	v_mfma_f32_16x16x128_f8f6f4 v[104:107], v[0:7], v[196:203], v[104:107]
	v_mfma_f32_16x16x128_f8f6f4 v[96:99], v[8:15], v[204:211], v[96:99]
	v_mfma_f32_16x16x128_f8f6f4 v[88:91], v[0:7], v[204:211], v[88:91]
	s_setprio 0
	s_barrier
	s_add_i32 s68, s53, s43
	v_lshl_add_u64 v[162:163], s[20:21], 0, v[146:147]
	s_mov_b32 m0, s68
	ds_read_b128 v[212:215], v178
	ds_read_b128 v[216:219], v178 offset:1024
	ds_read_b128 v[224:227], v178 offset:2048
	ds_read_b128 v[228:231], v178 offset:3072
	global_load_lds_dwordx4 v[162:163], off
	v_lshl_add_u64 v[164:165], s[20:21], 0, v[150:151]
	s_add_i32 m0, s68, 0x2000
	s_nop 0
	global_load_lds_dwordx4 v[164:165], off
	s_barrier
	s_waitcnt lgkmcnt(0)
	s_setprio 1
	s_waitcnt lgkmcnt(0)
	v_mfma_f32_16x16x128_f8f6f4 v[132:135], v[212:219], v[180:187], v[132:135]
	v_mfma_f32_16x16x128_f8f6f4 v[124:127], v[224:231], v[180:187], v[124:127]
	v_mfma_f32_16x16x128_f8f6f4 v[116:119], v[212:219], v[188:195], v[116:119]
	v_mfma_f32_16x16x128_f8f6f4 v[108:111], v[224:231], v[188:195], v[108:111]
	v_mfma_f32_16x16x128_f8f6f4 v[100:103], v[212:219], v[196:203], v[100:103]
	v_mfma_f32_16x16x128_f8f6f4 v[92:95], v[224:231], v[196:203], v[92:95]
	v_mfma_f32_16x16x128_f8f6f4 v[84:87], v[212:219], v[204:211], v[84:87]
	v_mfma_f32_16x16x128_f8f6f4 v[80:83], v[224:231], v[204:211], v[80:83]
	s_setprio 0
	s_mov_b32 m0, s44
	v_lshl_add_u64 v[166:167], s[22:23], 0, v[144:145]
	s_barrier
	ds_read_b128 v[180:183], v177 offset:16384
	ds_read_b128 v[184:187], v177 offset:17408
	ds_read_b128 v[188:191], v177 offset:18432
	ds_read_b128 v[192:195], v177 offset:19456
	ds_read_b128 v[196:199], v177 offset:20480
	ds_read_b128 v[200:203], v177 offset:21504
	ds_read_b128 v[204:207], v177 offset:22528
	ds_read_b128 v[208:211], v177 offset:23552
	global_load_lds_dwordx4 v[166:167], off
	v_lshl_add_u64 v[168:169], s[22:23], 0, v[148:149]
	s_mov_b32 m0, s45
	s_nop 0
	global_load_lds_dwordx4 v[168:169], off
	s_barrier
	s_waitcnt lgkmcnt(0)
	s_setprio 1
	s_waitcnt lgkmcnt(0)
	v_mfma_f32_16x16x128_f8f6f4 v[76:79], v[8:15], v[180:187], v[76:79]
	v_mfma_f32_16x16x128_f8f6f4 v[72:75], v[0:7], v[180:187], v[72:75]
	v_mfma_f32_16x16x128_f8f6f4 v[64:67], v[8:15], v[188:195], v[64:67]
	v_mfma_f32_16x16x128_f8f6f4 v[56:59], v[0:7], v[188:195], v[56:59]
	v_mfma_f32_16x16x128_f8f6f4 v[48:51], v[8:15], v[196:203], v[48:51]
	v_mfma_f32_16x16x128_f8f6f4 v[40:43], v[0:7], v[196:203], v[40:43]
	v_mfma_f32_16x16x128_f8f6f4 v[32:35], v[8:15], v[204:211], v[32:35]
	v_mfma_f32_16x16x128_f8f6f4 v[24:27], v[0:7], v[204:211], v[24:27]
	s_setprio 0
	s_barrier
	s_add_u32 s68, s20, 0x40000
	s_addc_u32 s69, s21, 0
	s_add_i32 s70, s54, s43
	v_lshl_add_u64 v[0:1], s[68:69], 0, v[146:147]
	s_mov_b32 m0, s70
	s_nop 0
	global_load_lds_dwordx4 v[0:1], off
	v_lshl_add_u64 v[0:1], s[68:69], 0, v[150:151]
	s_add_i32 m0, s70, 0x2000
	s_nop 0
	global_load_lds_dwordx4 v[0:1], off
	s_waitcnt vmcnt(6)
	s_barrier
	s_setprio 1
	v_mfma_f32_16x16x128_f8f6f4 v[68:71], v[212:219], v[180:187], v[68:71]
	v_mfma_f32_16x16x128_f8f6f4 v[60:63], v[224:231], v[180:187], v[60:63]
	v_mfma_f32_16x16x128_f8f6f4 v[52:55], v[212:219], v[188:195], v[52:55]
	v_mfma_f32_16x16x128_f8f6f4 v[44:47], v[224:231], v[188:195], v[44:47]
	v_mfma_f32_16x16x128_f8f6f4 v[36:39], v[212:219], v[196:203], v[36:39]
	v_mfma_f32_16x16x128_f8f6f4 v[28:31], v[224:231], v[196:203], v[28:31]
	v_mfma_f32_16x16x128_f8f6f4 v[20:23], v[212:219], v[204:211], v[20:23]
	v_mfma_f32_16x16x128_f8f6f4 v[16:19], v[224:231], v[204:211], v[16:19]
	s_setprio 0
	s_add_i32 s68, 0, 0x18000
	v_add_u32_e32 v12, s68, v173
	s_barrier
	ds_read_b128 v[0:3], v12
	ds_read_b128 v[4:7], v12 offset:1024
	ds_read_b128 v[8:11], v12 offset:2048
	ds_read_b128 v[12:15], v12 offset:3072
	s_add_u32 s22, s22, 0x40000
	s_addc_u32 s23, s23, 0
	s_mov_b32 m0, s46
	v_lshl_add_u64 v[158:159], s[22:23], 0, v[144:145]
	ds_read_b128 v[180:183], v177 offset:32768
	ds_read_b128 v[184:187], v177 offset:33792
	ds_read_b128 v[188:191], v177 offset:34816
	ds_read_b128 v[192:195], v177 offset:35840
	ds_read_b128 v[196:199], v177 offset:36864
	ds_read_b128 v[200:203], v177 offset:37888
	ds_read_b128 v[204:207], v177 offset:38912
	ds_read_b128 v[208:211], v177 offset:39936
	global_load_lds_dwordx4 v[158:159], off
	v_lshl_add_u64 v[158:159], s[22:23], 0, v[148:149]
	s_mov_b32 m0, s47
	s_nop 0
	global_load_lds_dwordx4 v[158:159], off
	s_waitcnt lgkmcnt(8)
	s_barrier
	s_waitcnt lgkmcnt(0)
	s_setprio 1
	s_waitcnt lgkmcnt(0)
	v_mfma_f32_16x16x128_f8f6f4 v[140:143], v[0:7], v[180:187], v[140:143]
	v_mfma_f32_16x16x128_f8f6f4 v[136:139], v[8:15], v[180:187], v[136:139]
	v_mfma_f32_16x16x128_f8f6f4 v[128:131], v[0:7], v[188:195], v[128:131]
	v_mfma_f32_16x16x128_f8f6f4 v[120:123], v[8:15], v[188:195], v[120:123]
	v_mfma_f32_16x16x128_f8f6f4 v[112:115], v[0:7], v[196:203], v[112:115]
	v_mfma_f32_16x16x128_f8f6f4 v[104:107], v[8:15], v[196:203], v[104:107]
	v_mfma_f32_16x16x128_f8f6f4 v[96:99], v[0:7], v[204:211], v[96:99]
	v_mfma_f32_16x16x128_f8f6f4 v[88:91], v[8:15], v[204:211], v[88:91]
	s_setprio 0
	s_barrier
	s_add_i32 s22, 0, 0x1c000
	s_add_i32 s23, s68, s43
	v_add_u32_e32 v152, s22, v173
	v_lshl_add_u64 v[158:159], v[162:163], 0, s[6:7]
	s_mov_b32 m0, s23
	ds_read_b128 v[212:215], v152
	ds_read_b128 v[216:219], v152 offset:1024
	ds_read_b128 v[224:227], v152 offset:2048
	ds_read_b128 v[228:231], v152 offset:3072
	global_load_lds_dwordx4 v[158:159], off
	v_lshl_add_u64 v[158:159], v[164:165], 0, s[6:7]
	s_add_i32 m0, s23, 0x2000
	s_nop 0
	global_load_lds_dwordx4 v[158:159], off
	s_barrier
	s_waitcnt lgkmcnt(0)
	s_setprio 1
	s_waitcnt lgkmcnt(0)
	v_mfma_f32_16x16x128_f8f6f4 v[132:135], v[212:219], v[180:187], v[132:135]
	v_mfma_f32_16x16x128_f8f6f4 v[124:127], v[224:231], v[180:187], v[124:127]
	v_mfma_f32_16x16x128_f8f6f4 v[116:119], v[212:219], v[188:195], v[116:119]
	v_mfma_f32_16x16x128_f8f6f4 v[108:111], v[224:231], v[188:195], v[108:111]
	v_mfma_f32_16x16x128_f8f6f4 v[100:103], v[212:219], v[196:203], v[100:103]
	v_mfma_f32_16x16x128_f8f6f4 v[92:95], v[224:231], v[196:203], v[92:95]
	v_mfma_f32_16x16x128_f8f6f4 v[84:87], v[212:219], v[204:211], v[84:87]
	v_mfma_f32_16x16x128_f8f6f4 v[80:83], v[224:231], v[204:211], v[80:83]
	s_setprio 0
	s_mov_b32 m0, s50
	v_lshl_add_u64 v[158:159], v[166:167], 0, s[6:7]
	s_barrier
	ds_read_b128 v[180:183], v177 offset:49152
	ds_read_b128 v[184:187], v177 offset:50176
	ds_read_b128 v[188:191], v177 offset:51200
	ds_read_b128 v[192:195], v177 offset:52224
	ds_read_b128 v[196:199], v177 offset:53248
	ds_read_b128 v[200:203], v177 offset:54272
	ds_read_b128 v[204:207], v177 offset:55296
	ds_read_b128 v[208:211], v177 offset:56320
	global_load_lds_dwordx4 v[158:159], off
	v_lshl_add_u64 v[158:159], v[168:169], 0, s[6:7]
	s_mov_b32 m0, s51
	s_nop 0
	global_load_lds_dwordx4 v[158:159], off
	s_barrier
	s_waitcnt lgkmcnt(0)
	s_setprio 1
	s_waitcnt lgkmcnt(0)
	v_mfma_f32_16x16x128_f8f6f4 v[76:79], v[0:7], v[180:187], v[76:79]
	v_mfma_f32_16x16x128_f8f6f4 v[72:75], v[8:15], v[180:187], v[72:75]
	v_mfma_f32_16x16x128_f8f6f4 v[64:67], v[0:7], v[188:195], v[64:67]
	v_mfma_f32_16x16x128_f8f6f4 v[56:59], v[8:15], v[188:195], v[56:59]
	v_mfma_f32_16x16x128_f8f6f4 v[48:51], v[0:7], v[196:203], v[48:51]
	v_mfma_f32_16x16x128_f8f6f4 v[40:43], v[8:15], v[196:203], v[40:43]
	v_mfma_f32_16x16x128_f8f6f4 v[32:35], v[0:7], v[204:211], v[32:35]
	v_mfma_f32_16x16x128_f8f6f4 v[24:27], v[8:15], v[204:211], v[24:27]
	s_setprio 0
	s_barrier
	s_add_u32 s20, s20, 0x40080
	s_addc_u32 s21, s21, 0
	s_add_i32 s22, s22, s43
	v_lshl_add_u64 v[0:1], s[20:21], 0, v[146:147]
	s_mov_b32 m0, s22
	s_nop 0
	global_load_lds_dwordx4 v[0:1], off
	v_lshl_add_u64 v[0:1], s[20:21], 0, v[150:151]
	s_add_i32 m0, s22, 0x2000
	s_nop 0
	global_load_lds_dwordx4 v[0:1], off
	s_waitcnt vmcnt(6)
	s_barrier
	s_setprio 1
	v_mfma_f32_16x16x128_f8f6f4 v[68:71], v[212:219], v[180:187], v[68:71]
	v_mfma_f32_16x16x128_f8f6f4 v[60:63], v[224:231], v[180:187], v[60:63]
	v_mfma_f32_16x16x128_f8f6f4 v[52:55], v[212:219], v[188:195], v[52:55]
	v_mfma_f32_16x16x128_f8f6f4 v[44:47], v[224:231], v[188:195], v[44:47]
	v_mfma_f32_16x16x128_f8f6f4 v[36:39], v[212:219], v[196:203], v[36:39]
	v_mfma_f32_16x16x128_f8f6f4 v[28:31], v[224:231], v[196:203], v[28:31]
	v_mfma_f32_16x16x128_f8f6f4 v[20:23], v[212:219], v[204:211], v[20:23]
	v_mfma_f32_16x16x128_f8f6f4 v[16:19], v[224:231], v[204:211], v[16:19]
	s_setprio 0
	s_add_i32 s67, s67, 2
	s_add_u32 s65, s65, 0x100
	s_addc_u32 s66, s66, 0
	s_add_u32 s18, s18, 0x100
	s_addc_u32 s19, s19, 0
	s_cmp_gt_u32 s67, 13
	s_barrier
	s_cbranch_scc0 .LBB0_985
	s_lshl_b32 s18, s60, 8
	s_min_i32 s19, s60, 32
	s_ashr_i32 s22, s19, 4
	s_add_i32 s19, s18, 0xffffe000
	s_cmp_lt_i32 s60, 32
	s_cselect_b32 s20, s18, s19
	s_mul_i32 s22, s22, 6
	s_cselect_b32 s60, s28, s30
	s_cselect_b32 s61, s27, s29
	s_ashr_i32 s21, s20, 31
	s_ashr_i32 s19, s18, 31
	s_ashr_i32 s23, s22, 31
	s_lshl_b64 s[20:21], s[20:21], 13
	s_lshl_b64 s[18:19], s[18:19], 12
	s_lshl_b64 s[22:23], s[22:23], 13
	v_lshl_or_b32 v8, s59, 8, v175
	s_add_u32 s22, s4, s22
	s_addc_u32 s23, s5, s23
	v_ashrrev_i32_e32 v9, 31, v8
	v_lshl_add_u64 v[0:1], v[8:9], 2, s[22:23]
	v_lshl_add_u64 v[10:11], v[0:1], 0, s[8:9]
	v_add_co_u32_e32 v0, vcc, s49, v0
	s_add_u32 s20, s61, s20
	s_nop 7
	s_nop 7
	s_nop 7
	s_nop 0
	v_addc_co_u32_e32 v1, vcc, 0, v1, vcc
	s_addc_u32 s21, s60, s21
	v_add_u32_e32 v152, v174, v8
	global_load_dwordx4 v[0:3], v[0:1], off
	s_nop 0
	global_load_dwordx4 v[164:167], v[10:11], off offset:528
	global_load_dwordx4 v[4:7], v[10:11], off offset:16
	global_load_dwordx4 v[180:183], v[10:11], off offset:512
	v_mov_b32_e32 v169, v153
	v_lshl_add_u64 v[8:9], v[152:153], 2, s[20:21]
	v_add_u32_e32 v168, 0x80, v152
	global_load_dwordx4 v[184:187], v[8:9], off
	global_load_dwordx4 v[188:191], v[8:9], off offset:16
	v_lshl_add_u64 v[8:9], v[168:169], 2, s[20:21]
	global_load_dwordx4 v[192:195], v[8:9], off
	global_load_dwordx4 v[196:199], v[8:9], off offset:16
	v_add_u32_e32 v220, 0x8000, v152
	v_mov_b32_e32 v221, v153
	v_lshl_add_u64 v[8:9], v[220:221], 2, s[20:21]
	v_add_u32_e32 v252, 0x8080, v152
	v_mov_b32_e32 v253, v153
	global_load_dwordx4 v[200:203], v[8:9], off
	global_load_dwordx4 v[204:207], v[8:9], off offset:16
	v_lshl_add_u64 v[8:9], v[252:253], 2, s[20:21]
	global_load_dwordx4 v[208:211], v[8:9], off
	global_load_dwordx4 v[212:215], v[8:9], off offset:16
	v_mov_b32_e32 v223, v153
	v_add_u32_e32 v222, 0x10000, v152
	v_lshl_add_u64 v[8:9], v[222:223], 2, s[20:21]
	v_mov_b32_e32 v171, v153
	v_add_u32_e32 v170, 0x10080, v152
	global_load_dwordx4 v[216:219], v[8:9], off
	global_load_dwordx4 v[224:227], v[8:9], off offset:16
	v_lshl_add_u64 v[8:9], v[170:171], 2, s[20:21]
	v_mov_b32_e32 v159, v153
	v_add_u32_e32 v158, 0x18000, v152
	global_load_dwordx4 v[228:231], v[8:9], off
	global_load_dwordx4 v[232:235], v[8:9], off offset:16
	v_lshl_add_u64 v[8:9], v[158:159], 2, s[20:21]
	v_mov_b32_e32 v163, v153
	v_add_u32_e32 v162, 0x18080, v152
	global_load_dwordx4 v[236:239], v[8:9], off
	global_load_dwordx4 v[240:243], v[8:9], off offset:16
	v_lshl_add_u64 v[8:9], v[162:163], 2, s[20:21]
	global_load_dwordx4 v[244:247], v[8:9], off offset:16
	global_load_dwordx4 v[248:251], v[8:9], off
	s_add_u32 s18, s2, s18
	s_addc_u32 s19, s3, s19
	v_lshl_add_u64 v[160:161], v[152:153], 1, s[18:19]
	s_and_b64 vcc, exec, s[0:1]
	s_mov_b32 s59, s55
	s_mov_b32 s60, s56
	s_waitcnt vmcnt(0)
	v_pk_mul_f32 v[14:15], v[0:1], s[10:11] op_sel_hi:[1,0]
	v_pk_mul_f32 v[12:13], v[2:3], s[10:11] op_sel_hi:[1,0]
	v_pk_mul_f32 v[8:9], v[6:7], s[10:11] op_sel_hi:[1,0]
	v_pk_mul_f32 v[10:11], v[4:5], s[10:11] op_sel_hi:[1,0]
	v_pk_mul_f32 v[6:7], v[180:181], s[10:11] op_sel_hi:[1,0]
	v_pk_mul_f32 v[4:5], v[182:183], s[10:11] op_sel_hi:[1,0]
	v_pk_mul_f32 v[0:1], v[166:167], s[10:11] op_sel_hi:[1,0]
	v_pk_mul_f32 v[2:3], v[164:165], s[10:11] op_sel_hi:[1,0]
	v_pk_fma_f32 v[140:141], v[140:141], v[14:15], v[184:185]
	v_pk_fma_f32 v[164:165], v[138:139], v[8:9], v[190:191]
	v_pk_fma_f32 v[138:139], v[136:137], v[10:11], v[188:189]
	v_pk_fma_f32 v[132:133], v[132:133], v[6:7], v[192:193]
	v_pk_fma_f32 v[142:143], v[142:143], v[12:13], v[186:187]
	v_cvt_pk_bf16_f32 v136, v140, v141
	v_pk_fma_f32 v[134:135], v[134:135], v[4:5], v[194:195]
	v_cvt_pk_bf16_f32 v137, v142, v143
	v_cvt_pk_bf16_f32 v138, v138, v139
	v_cvt_pk_bf16_f32 v139, v164, v165
	v_pk_fma_f32 v[140:141], v[126:127], v[0:1], v[198:199]
	global_store_dwordx4 v[160:161], v[136:139], off
	v_pk_fma_f32 v[126:127], v[124:125], v[2:3], v[196:197]
	v_cvt_pk_bf16_f32 v124, v132, v133
	v_cvt_pk_bf16_f32 v125, v134, v135
	v_lshl_add_u64 v[132:133], v[168:169], 1, s[18:19]
	v_cvt_pk_bf16_f32 v126, v126, v127
	v_cvt_pk_bf16_f32 v127, v140, v141
	global_store_dwordx4 v[132:133], v[124:127], off
	v_pk_fma_f32 v[116:117], v[116:117], v[6:7], v[208:209]
	v_pk_fma_f32 v[118:119], v[118:119], v[4:5], v[210:211]
	v_pk_fma_f32 v[124:125], v[130:131], v[12:13], v[202:203]
	v_pk_fma_f32 v[126:127], v[128:129], v[14:15], v[200:201]
	v_pk_fma_f32 v[128:129], v[122:123], v[8:9], v[206:207]
	v_pk_fma_f32 v[122:123], v[120:121], v[10:11], v[204:205]
	v_cvt_pk_bf16_f32 v120, v126, v127
	v_cvt_pk_bf16_f32 v121, v124, v125
	v_lshl_add_u64 v[124:125], v[220:221], 1, s[18:19]
	v_cvt_pk_bf16_f32 v122, v122, v123
	v_cvt_pk_bf16_f32 v123, v128, v129
	global_store_dwordx4 v[124:125], v[120:123], off
	v_pk_fma_f32 v[100:101], v[100:101], v[6:7], v[228:229]
	v_pk_fma_f32 v[102:103], v[102:103], v[4:5], v[230:231]
	v_pk_fma_f32 v[120:121], v[110:111], v[0:1], v[214:215]
	v_pk_fma_f32 v[110:111], v[108:109], v[2:3], v[212:213]
	v_cvt_pk_bf16_f32 v108, v116, v117
	v_cvt_pk_bf16_f32 v109, v118, v119
	v_lshl_add_u64 v[116:117], v[252:253], 1, s[18:19]
	v_cvt_pk_bf16_f32 v110, v110, v111
	v_cvt_pk_bf16_f32 v111, v120, v121
	global_store_dwordx4 v[116:117], v[108:111], off
	v_pk_fma_f32 v[84:85], v[84:85], v[6:7], v[248:249]
	v_pk_fma_f32 v[86:87], v[86:87], v[4:5], v[250:251]
	v_pk_fma_f32 v[108:109], v[114:115], v[12:13], v[218:219]
	v_pk_fma_f32 v[110:111], v[112:113], v[14:15], v[216:217]
	v_pk_fma_f32 v[112:113], v[106:107], v[8:9], v[226:227]
	v_pk_fma_f32 v[106:107], v[104:105], v[10:11], v[224:225]
	v_cvt_pk_bf16_f32 v104, v110, v111
	v_cvt_pk_bf16_f32 v105, v108, v109
	v_lshl_add_u64 v[108:109], v[222:223], 1, s[18:19]
	v_cvt_pk_bf16_f32 v106, v106, v107
	v_cvt_pk_bf16_f32 v107, v112, v113
	global_store_dwordx4 v[108:109], v[104:107], off
	v_add_u32_e32 v160, 0x40080, v152
	v_mov_b32_e32 v161, v153
	v_pk_fma_f32 v[104:105], v[94:95], v[0:1], v[234:235]
	v_pk_fma_f32 v[94:95], v[92:93], v[2:3], v[232:233]
	v_cvt_pk_bf16_f32 v92, v100, v101
	v_cvt_pk_bf16_f32 v93, v102, v103
	v_lshl_add_u64 v[100:101], v[170:171], 1, s[18:19]
	v_cvt_pk_bf16_f32 v94, v94, v95
	v_cvt_pk_bf16_f32 v95, v104, v105
	global_store_dwordx4 v[100:101], v[92:95], off
	v_add_u32_e32 v164, 0x48080, v152
	v_mov_b32_e32 v165, v153
	v_pk_fma_f32 v[92:93], v[98:99], v[12:13], v[238:239]
	v_pk_fma_f32 v[94:95], v[96:97], v[14:15], v[236:237]
	v_pk_fma_f32 v[96:97], v[90:91], v[8:9], v[242:243]
	v_pk_fma_f32 v[90:91], v[88:89], v[10:11], v[240:241]
	v_cvt_pk_bf16_f32 v88, v94, v95
	v_cvt_pk_bf16_f32 v89, v92, v93
	v_lshl_add_u64 v[92:93], v[158:159], 1, s[18:19]
	v_cvt_pk_bf16_f32 v90, v90, v91
	v_cvt_pk_bf16_f32 v91, v96, v97
	global_store_dwordx4 v[92:93], v[88:91], off
	v_add_u32_e32 v158, 0x40000, v152
	v_lshl_add_u64 v[92:93], v[160:161], 2, s[20:21]
	v_pk_fma_f32 v[88:89], v[82:83], v[0:1], v[246:247]
	v_pk_fma_f32 v[82:83], v[80:81], v[2:3], v[244:245]
	v_cvt_pk_bf16_f32 v80, v84, v85
	v_lshl_add_u64 v[84:85], v[162:163], 1, s[18:19]
	v_cvt_pk_bf16_f32 v81, v86, v87
	v_cvt_pk_bf16_f32 v82, v82, v83
	v_cvt_pk_bf16_f32 v83, v88, v89
	global_store_dwordx4 v[84:85], v[80:83], off
	v_lshl_add_u64 v[84:85], v[158:159], 2, s[20:21]
	global_load_dwordx4 v[80:83], v[84:85], off
	s_nop 0
	global_load_dwordx4 v[84:87], v[84:85], off offset:16
	s_nop 0
	global_load_dwordx4 v[88:91], v[92:93], off
	s_nop 0
	global_load_dwordx4 v[92:95], v[92:93], off offset:16
	v_add_u32_e32 v162, 0x48000, v152
	v_lshl_add_u64 v[100:101], v[162:163], 2, s[20:21]
	global_load_dwordx4 v[96:99], v[100:101], off
	s_nop 0
	global_load_dwordx4 v[100:103], v[100:101], off offset:16
	v_lshl_add_u64 v[108:109], v[164:165], 2, s[20:21]
	global_load_dwordx4 v[104:107], v[108:109], off
	s_nop 0
	global_load_dwordx4 v[108:111], v[108:109], off offset:16
	v_add_u32_e32 v166, 0x50000, v152
	v_mov_b32_e32 v167, v153
	v_lshl_add_u64 v[116:117], v[166:167], 2, s[20:21]
	v_add_u32_e32 v168, 0x50080, v152
	global_load_dwordx4 v[112:115], v[116:117], off
	s_nop 0
	global_load_dwordx4 v[116:119], v[116:117], off offset:16
	v_lshl_add_u64 v[124:125], v[168:169], 2, s[20:21]
	v_add_u32_e32 v170, 0x58000, v152
	global_load_dwordx4 v[120:123], v[124:125], off
	s_nop 0
	global_load_dwordx4 v[124:127], v[124:125], off offset:16
	v_lshl_add_u64 v[132:133], v[170:171], 2, s[20:21]
	v_add_u32_e32 v152, 0x58080, v152
	global_load_dwordx4 v[128:131], v[132:133], off
	s_nop 0
	global_load_dwordx4 v[132:135], v[132:133], off offset:16
	v_lshl_add_u64 v[140:141], v[152:153], 2, s[20:21]
	global_load_dwordx4 v[136:139], v[140:141], off
	s_nop 0
	global_load_dwordx4 v[140:143], v[140:141], off offset:16
	s_mov_b64 s[20:21], s[12:13]
	s_waitcnt vmcnt(0)
	v_pk_fma_f32 v[76:77], v[76:77], v[14:15], v[80:81]
	v_pk_fma_f32 v[78:79], v[78:79], v[12:13], v[82:83]
	v_pk_fma_f32 v[80:81], v[74:75], v[8:9], v[86:87]
	v_pk_fma_f32 v[74:75], v[72:73], v[10:11], v[84:85]
	v_cvt_pk_bf16_f32 v72, v76, v77
	v_cvt_pk_bf16_f32 v73, v78, v79
	v_lshl_add_u64 v[76:77], v[158:159], 1, s[18:19]
	v_pk_fma_f32 v[68:69], v[68:69], v[6:7], v[88:89]
	v_cvt_pk_bf16_f32 v74, v74, v75
	v_cvt_pk_bf16_f32 v75, v80, v81
	global_store_dwordx4 v[76:77], v[72:75], off
	v_pk_fma_f32 v[70:71], v[70:71], v[4:5], v[90:91]
	v_pk_fma_f32 v[52:53], v[52:53], v[6:7], v[104:105]
	v_pk_fma_f32 v[72:73], v[62:63], v[0:1], v[94:95]
	v_pk_fma_f32 v[62:63], v[60:61], v[2:3], v[92:93]
	v_cvt_pk_bf16_f32 v60, v68, v69
	v_cvt_pk_bf16_f32 v61, v70, v71
	v_lshl_add_u64 v[68:69], v[160:161], 1, s[18:19]
	v_cvt_pk_bf16_f32 v62, v62, v63
	v_cvt_pk_bf16_f32 v63, v72, v73
	global_store_dwordx4 v[68:69], v[60:63], off
	v_pk_fma_f32 v[54:55], v[54:55], v[4:5], v[106:107]
	v_pk_fma_f32 v[36:37], v[36:37], v[6:7], v[120:121]
	v_pk_fma_f32 v[60:61], v[66:67], v[12:13], v[98:99]
	v_pk_fma_f32 v[62:63], v[64:65], v[14:15], v[96:97]
	v_pk_fma_f32 v[64:65], v[58:59], v[8:9], v[102:103]
	v_pk_fma_f32 v[58:59], v[56:57], v[10:11], v[100:101]
	v_cvt_pk_bf16_f32 v56, v62, v63
	v_cvt_pk_bf16_f32 v57, v60, v61
	v_lshl_add_u64 v[60:61], v[162:163], 1, s[18:19]
	v_cvt_pk_bf16_f32 v58, v58, v59
	v_cvt_pk_bf16_f32 v59, v64, v65
	global_store_dwordx4 v[60:61], v[56:59], off
	v_pk_fma_f32 v[38:39], v[38:39], v[4:5], v[122:123]
	v_pk_fma_f32 v[26:27], v[26:27], v[8:9], v[134:135]
	v_pk_fma_f32 v[56:57], v[46:47], v[0:1], v[110:111]
	v_pk_fma_f32 v[46:47], v[44:45], v[2:3], v[108:109]
	v_cvt_pk_bf16_f32 v44, v52, v53
	v_cvt_pk_bf16_f32 v45, v54, v55
	v_lshl_add_u64 v[52:53], v[164:165], 1, s[18:19]
	v_cvt_pk_bf16_f32 v46, v46, v47
	v_cvt_pk_bf16_f32 v47, v56, v57
	global_store_dwordx4 v[52:53], v[44:47], off
	v_pk_fma_f32 v[4:5], v[22:23], v[4:5], v[138:139]
	v_pk_fma_f32 v[6:7], v[20:21], v[6:7], v[136:137]
	v_pk_fma_f32 v[44:45], v[50:51], v[12:13], v[114:115]
	v_pk_fma_f32 v[46:47], v[48:49], v[14:15], v[112:113]
	v_pk_fma_f32 v[48:49], v[42:43], v[8:9], v[118:119]
	v_pk_fma_f32 v[42:43], v[40:41], v[10:11], v[116:117]
	v_cvt_pk_bf16_f32 v40, v46, v47
	v_cvt_pk_bf16_f32 v41, v44, v45
	v_lshl_add_u64 v[44:45], v[166:167], 1, s[18:19]
	v_cvt_pk_bf16_f32 v42, v42, v43
	v_cvt_pk_bf16_f32 v43, v48, v49
	global_store_dwordx4 v[44:45], v[40:43], off
	v_pk_fma_f32 v[12:13], v[34:35], v[12:13], v[130:131]
	v_pk_fma_f32 v[14:15], v[32:33], v[14:15], v[128:129]
	v_pk_fma_f32 v[40:41], v[30:31], v[0:1], v[126:127]
	v_pk_fma_f32 v[30:31], v[28:29], v[2:3], v[124:125]
	v_cvt_pk_bf16_f32 v28, v36, v37
	v_lshl_add_u64 v[36:37], v[168:169], 1, s[18:19]
	v_cvt_pk_bf16_f32 v29, v38, v39
	v_cvt_pk_bf16_f32 v30, v30, v31
	v_cvt_pk_bf16_f32 v31, v40, v41
	global_store_dwordx4 v[36:37], v[28:31], off
	v_pk_fma_f32 v[10:11], v[24:25], v[10:11], v[132:133]
	v_cvt_pk_bf16_f32 v8, v14, v15
	v_cvt_pk_bf16_f32 v9, v12, v13
	v_lshl_add_u64 v[12:13], v[170:171], 1, s[18:19]
	v_cvt_pk_bf16_f32 v10, v10, v11
	v_cvt_pk_bf16_f32 v11, v26, v27
	global_store_dwordx4 v[12:13], v[8:11], off
	v_pk_fma_f32 v[2:3], v[16:17], v[2:3], v[140:141]
	s_nop 0
	v_pk_fma_f32 v[8:9], v[18:19], v[0:1], v[142:143]
	v_cvt_pk_bf16_f32 v0, v6, v7
	v_cvt_pk_bf16_f32 v1, v4, v5
	v_lshl_add_u64 v[4:5], v[152:153], 1, s[18:19]
	v_cvt_pk_bf16_f32 v2, v2, v3
	v_cvt_pk_bf16_f32 v3, v8, v9
	global_store_dwordx4 v[4:5], v[0:3], off
	s_mov_b64 s[18:19], s[16:17]
	s_cbranch_vccz .LBB0_978
	s_waitcnt vmcnt(0)
	s_cmpk_gt_u32 s31, 0xff
	s_cbranch_scc1 .LBB0_989
	s_barrier

.LBB0_1209:
	s_add_u32 s30, s4, s2
	s_addc_u32 s31, s5, s3
	v_add_u32_e32 v4, s60, v193
	s_add_u32 s38, s30, 0x3280c100
	ds_read_b128 v[8:11], v4
	ds_read_b128 v[12:15], v4 offset:1024
	ds_read_b128 v[0:3], v4 offset:2048
	ds_read_b128 v[4:7], v4 offset:3072
	s_addc_u32 s39, s31, 0
	s_add_u32 s71, s11, s2
	s_addc_u32 s72, s69, s3
	s_cmpk_eq_i32 s2, 0x700
	s_cselect_b64 vcc, -1, 0
	s_and_b64 s[30:31], vcc, exec
	s_cselect_b32 s39, s9, s39
	s_cselect_b32 s38, s8, s38
	s_cselect_b32 s31, s67, s72
	s_cselect_b32 s30, s68, s71
	v_lshl_add_u64 v[16:17], v[176:177], 0, s[2:3]
	s_add_i32 m0, s29, 0xc000
	ds_read_b128 v[202:205], v195
	ds_read_b128 v[206:209], v195 offset:1024
	ds_read_b128 v[210:213], v195 offset:2048
	ds_read_b128 v[214:217], v195 offset:3072
	ds_read_b128 v[224:227], v195 offset:4096
	ds_read_b128 v[228:231], v195 offset:5120
	ds_read_b128 v[232:235], v195 offset:6144
	ds_read_b128 v[236:239], v195 offset:7168
	global_load_lds_dwordx4 v[16:17], off
	v_lshl_add_u64 v[16:17], v[174:175], 0, s[2:3]
	s_add_i32 m0, s29, 0xe000
	s_nop 0
	global_load_lds_dwordx4 v[16:17], off
	s_waitcnt lgkmcnt(8)
	s_barrier
	s_waitcnt lgkmcnt(0)
	s_setprio 1
	s_waitcnt lgkmcnt(0)
	v_mfma_f32_16x16x128_f8f6f4 v[156:159], v[8:15], v[202:209], v[156:159]
	v_mfma_f32_16x16x128_f8f6f4 v[152:155], v[0:7], v[202:209], v[152:155]
	v_mfma_f32_16x16x128_f8f6f4 v[140:143], v[8:15], v[210:217], v[140:143]
	v_mfma_f32_16x16x128_f8f6f4 v[136:139], v[0:7], v[210:217], v[136:139]
	v_mfma_f32_16x16x128_f8f6f4 v[124:127], v[8:15], v[224:231], v[124:127]
	v_mfma_f32_16x16x128_f8f6f4 v[120:123], v[0:7], v[224:231], v[120:123]
	v_mfma_f32_16x16x128_f8f6f4 v[108:111], v[8:15], v[232:239], v[108:111]
	v_mfma_f32_16x16x128_f8f6f4 v[104:107], v[0:7], v[232:239], v[104:107]
	s_setprio 0
	s_barrier
	s_add_i32 s71, s60, s50
	v_add_u32_e32 v20, s61, v193
	v_lshl_add_u64 v[178:179], s[30:31], 0, v[162:163]
	s_mov_b32 m0, s71
	ds_read_b128 v[24:27], v20
	ds_read_b128 v[28:31], v20 offset:1024
	ds_read_b128 v[16:19], v20 offset:2048
	ds_read_b128 v[20:23], v20 offset:3072
	global_load_lds_dwordx4 v[178:179], off
	v_lshl_add_u64 v[180:181], s[30:31], 0, v[164:165]
	s_add_i32 m0, s71, 0x2000
	s_nop 0
	global_load_lds_dwordx4 v[180:181], off
	s_barrier
	s_waitcnt lgkmcnt(0)
	s_setprio 1
	s_waitcnt lgkmcnt(0)
	v_mfma_f32_16x16x128_f8f6f4 v[148:151], v[24:31], v[202:209], v[148:151]
	v_mfma_f32_16x16x128_f8f6f4 v[144:147], v[16:23], v[202:209], v[144:147]
	v_mfma_f32_16x16x128_f8f6f4 v[132:135], v[24:31], v[210:217], v[132:135]
	v_mfma_f32_16x16x128_f8f6f4 v[128:131], v[16:23], v[210:217], v[128:131]
	v_mfma_f32_16x16x128_f8f6f4 v[116:119], v[24:31], v[224:231], v[116:119]
	v_mfma_f32_16x16x128_f8f6f4 v[112:115], v[16:23], v[224:231], v[112:115]
	v_mfma_f32_16x16x128_f8f6f4 v[100:103], v[24:31], v[232:239], v[100:103]
	v_mfma_f32_16x16x128_f8f6f4 v[96:99], v[16:23], v[232:239], v[96:99]
	s_setprio 0
	s_mov_b32 m0, s29
	v_cndmask_b32_e32 v160, v201, v197, vcc
	s_barrier
	ds_read_b128 v[202:205], v195 offset:16384
	ds_read_b128 v[206:209], v195 offset:17408
	ds_read_b128 v[210:213], v195 offset:18432
	ds_read_b128 v[214:217], v195 offset:19456
	ds_read_b128 v[224:227], v195 offset:20480
	ds_read_b128 v[228:231], v195 offset:21504
	ds_read_b128 v[232:235], v195 offset:22528
	ds_read_b128 v[236:239], v195 offset:23552
	v_cndmask_b32_e32 v182, v172, v198, vcc
	global_load_lds_dwordx4 v160, s[38:39]
	s_mov_b32 m0, s51
	v_mov_b32_e32 v183, v161
	global_load_lds_dwordx4 v182, s[38:39]
	s_barrier
	s_waitcnt lgkmcnt(0)
	v_lshl_add_u64 v[184:185], s[38:39], 0, v[160:161]
	v_lshl_add_u64 v[182:183], s[38:39], 0, v[182:183]
	s_setprio 1
	s_waitcnt lgkmcnt(0)
	v_mfma_f32_16x16x128_f8f6f4 v[92:95], v[8:15], v[202:209], v[92:95]
	v_mfma_f32_16x16x128_f8f6f4 v[88:91], v[0:7], v[202:209], v[88:91]
	v_mfma_f32_16x16x128_f8f6f4 v[76:79], v[8:15], v[210:217], v[76:79]
	v_mfma_f32_16x16x128_f8f6f4 v[72:75], v[0:7], v[210:217], v[72:75]
	v_mfma_f32_16x16x128_f8f6f4 v[60:63], v[8:15], v[224:231], v[60:63]
	v_mfma_f32_16x16x128_f8f6f4 v[56:59], v[0:7], v[224:231], v[56:59]
	v_mfma_f32_16x16x128_f8f6f4 v[36:39], v[8:15], v[232:239], v[36:39]
	v_mfma_f32_16x16x128_f8f6f4 v[32:35], v[0:7], v[232:239], v[32:35]
	s_setprio 0
	s_barrier
	s_add_u32 s72, s30, 0x40000
	s_addc_u32 s73, s31, 0
	s_add_i32 s71, s61, s50
	v_lshl_add_u64 v[0:1], s[72:73], 0, v[162:163]
	s_mov_b32 m0, s71
	s_nop 0
	global_load_lds_dwordx4 v[0:1], off
	v_lshl_add_u64 v[0:1], s[72:73], 0, v[164:165]
	s_add_i32 m0, s71, 0x2000
	s_nop 0
	global_load_lds_dwordx4 v[0:1], off
	s_waitcnt vmcnt(6)
	s_barrier
	s_setprio 1
	v_mfma_f32_16x16x128_f8f6f4 v[84:87], v[24:31], v[202:209], v[84:87]
	v_mfma_f32_16x16x128_f8f6f4 v[80:83], v[16:23], v[202:209], v[80:83]
	v_mfma_f32_16x16x128_f8f6f4 v[68:71], v[24:31], v[210:217], v[68:71]
	v_mfma_f32_16x16x128_f8f6f4 v[64:67], v[16:23], v[210:217], v[64:67]
	v_mfma_f32_16x16x128_f8f6f4 v[52:55], v[24:31], v[224:231], v[52:55]
	v_mfma_f32_16x16x128_f8f6f4 v[40:43], v[16:23], v[224:231], v[40:43]
	v_mfma_f32_16x16x128_f8f6f4 v[48:51], v[24:31], v[232:239], v[48:51]
	v_mfma_f32_16x16x128_f8f6f4 v[44:47], v[16:23], v[232:239], v[44:47]
	s_setprio 0
	s_add_i32 s71, 0, 0x18000
	v_add_u32_e32 v12, s71, v193
	s_barrier
	ds_read_b128 v[0:3], v12
	ds_read_b128 v[4:7], v12 offset:1024
	ds_read_b128 v[8:11], v12 offset:2048
	ds_read_b128 v[12:15], v12 offset:3072
	s_mov_b32 m0, s52
	v_cndmask_b32_e32 v160, v170, v199, vcc
	ds_read_b128 v[16:19], v195 offset:32768
	ds_read_b128 v[20:23], v195 offset:33792
	ds_read_b128 v[24:27], v195 offset:34816
	ds_read_b128 v[28:31], v195 offset:35840
	ds_read_b128 v[202:205], v195 offset:36864
	ds_read_b128 v[206:209], v195 offset:37888
	ds_read_b128 v[210:213], v195 offset:38912
	ds_read_b128 v[214:217], v195 offset:39936
	v_cndmask_b32_e32 v169, v168, v200, vcc
	global_load_lds_dwordx4 v160, s[38:39]
	s_mov_b32 m0, s53
	s_nop 0
	global_load_lds_dwordx4 v169, s[38:39]
	s_waitcnt lgkmcnt(8)
	s_barrier
	s_waitcnt lgkmcnt(0)
	s_setprio 1
	s_waitcnt lgkmcnt(0)
	v_mfma_f32_16x16x128_f8f6f4 v[156:159], v[0:7], v[16:23], v[156:159]
	v_mfma_f32_16x16x128_f8f6f4 v[152:155], v[8:15], v[16:23], v[152:155]
	v_mfma_f32_16x16x128_f8f6f4 v[140:143], v[0:7], v[24:31], v[140:143]
	v_mfma_f32_16x16x128_f8f6f4 v[136:139], v[8:15], v[24:31], v[136:139]
	v_mfma_f32_16x16x128_f8f6f4 v[124:127], v[0:7], v[202:209], v[124:127]
	v_mfma_f32_16x16x128_f8f6f4 v[120:123], v[8:15], v[202:209], v[120:123]
	v_mfma_f32_16x16x128_f8f6f4 v[108:111], v[0:7], v[210:217], v[108:111]
	v_mfma_f32_16x16x128_f8f6f4 v[104:107], v[8:15], v[210:217], v[104:107]
	s_setprio 0
	s_barrier
	s_add_i32 s38, 0, 0x1c000
	s_add_i32 s39, s71, s50
	v_add_u32_e32 v160, s38, v193
	v_lshl_add_u64 v[178:179], v[178:179], 0, s[16:17]
	s_mov_b32 m0, s39
	ds_read_b128 v[224:227], v160
	ds_read_b128 v[228:231], v160 offset:1024
	ds_read_b128 v[232:235], v160 offset:2048
	ds_read_b128 v[236:239], v160 offset:3072
	global_load_lds_dwordx4 v[178:179], off
	v_lshl_add_u64 v[178:179], v[180:181], 0, s[16:17]
	s_add_i32 m0, s39, 0x2000
	s_nop 0
	global_load_lds_dwordx4 v[178:179], off
	s_barrier
	s_waitcnt lgkmcnt(0)
	s_setprio 1
	s_waitcnt lgkmcnt(0)
	v_mfma_f32_16x16x128_f8f6f4 v[148:151], v[224:231], v[16:23], v[148:151]
	v_mfma_f32_16x16x128_f8f6f4 v[144:147], v[232:239], v[16:23], v[144:147]
	v_mfma_f32_16x16x128_f8f6f4 v[132:135], v[224:231], v[24:31], v[132:135]
	v_mfma_f32_16x16x128_f8f6f4 v[128:131], v[232:239], v[24:31], v[128:131]
	v_mfma_f32_16x16x128_f8f6f4 v[116:119], v[224:231], v[202:209], v[116:119]
	v_mfma_f32_16x16x128_f8f6f4 v[112:115], v[232:239], v[202:209], v[112:115]
	v_mfma_f32_16x16x128_f8f6f4 v[100:103], v[224:231], v[210:217], v[100:103]
	v_mfma_f32_16x16x128_f8f6f4 v[96:99], v[232:239], v[210:217], v[96:99]
	s_setprio 0
	s_mov_b32 m0, s57
	v_lshl_add_u64 v[178:179], v[184:185], 0, s[16:17]
	s_barrier
	ds_read_b128 v[16:19], v195 offset:49152
	ds_read_b128 v[20:23], v195 offset:50176
	ds_read_b128 v[24:27], v195 offset:51200
	ds_read_b128 v[28:31], v195 offset:52224
	ds_read_b128 v[202:205], v195 offset:53248
	ds_read_b128 v[206:209], v195 offset:54272
	ds_read_b128 v[210:213], v195 offset:55296
	ds_read_b128 v[214:217], v195 offset:56320
	global_load_lds_dwordx4 v[178:179], off
	v_lshl_add_u64 v[178:179], v[182:183], 0, s[16:17]
	s_mov_b32 m0, s58
	s_nop 0
	global_load_lds_dwordx4 v[178:179], off
	s_barrier
	s_waitcnt lgkmcnt(0)
	s_setprio 1
	s_waitcnt lgkmcnt(0)
	v_mfma_f32_16x16x128_f8f6f4 v[92:95], v[0:7], v[16:23], v[92:95]
	v_mfma_f32_16x16x128_f8f6f4 v[88:91], v[8:15], v[16:23], v[88:91]
	v_mfma_f32_16x16x128_f8f6f4 v[76:79], v[0:7], v[24:31], v[76:79]
	v_mfma_f32_16x16x128_f8f6f4 v[72:75], v[8:15], v[24:31], v[72:75]
	v_mfma_f32_16x16x128_f8f6f4 v[60:63], v[0:7], v[202:209], v[60:63]
	v_mfma_f32_16x16x128_f8f6f4 v[56:59], v[8:15], v[202:209], v[56:59]
	v_mfma_f32_16x16x128_f8f6f4 v[36:39], v[0:7], v[210:217], v[36:39]
	v_mfma_f32_16x16x128_f8f6f4 v[32:35], v[8:15], v[210:217], v[32:35]
	s_setprio 0
	s_barrier
	s_add_u32 s30, s30, 0x40080
	s_addc_u32 s31, s31, 0
	s_add_i32 s38, s38, s50
	v_lshl_add_u64 v[0:1], s[30:31], 0, v[162:163]
	s_mov_b32 m0, s38
	s_nop 0
	global_load_lds_dwordx4 v[0:1], off
	v_lshl_add_u64 v[0:1], s[30:31], 0, v[164:165]
	s_add_i32 m0, s38, 0x2000
	s_nop 0
	global_load_lds_dwordx4 v[0:1], off
	s_waitcnt vmcnt(6)
	s_barrier
	s_setprio 1
	v_mfma_f32_16x16x128_f8f6f4 v[84:87], v[224:231], v[16:23], v[84:87]
	v_mfma_f32_16x16x128_f8f6f4 v[80:83], v[232:239], v[16:23], v[80:83]
	v_mfma_f32_16x16x128_f8f6f4 v[68:71], v[224:231], v[24:31], v[68:71]
	v_mfma_f32_16x16x128_f8f6f4 v[64:67], v[232:239], v[24:31], v[64:67]
	v_mfma_f32_16x16x128_f8f6f4 v[52:55], v[224:231], v[202:209], v[52:55]
	v_mfma_f32_16x16x128_f8f6f4 v[40:43], v[232:239], v[202:209], v[40:43]
	v_mfma_f32_16x16x128_f8f6f4 v[48:51], v[224:231], v[210:217], v[48:51]
	v_mfma_f32_16x16x128_f8f6f4 v[44:47], v[232:239], v[210:217], v[44:47]
	s_setprio 0
	s_add_i32 s70, s70, 2
	s_add_u32 s2, s2, 0x100
	s_addc_u32 s3, s3, 0
	s_cmp_gt_u32 s70, 13
	s_barrier
	s_cbranch_scc1 .LBB0_1203

.LBB0_1347:
	ds_read_b128 v[12:15], v156
	ds_read_b128 v[16:19], v156 offset:1024
	ds_read_b128 v[28:31], v156 offset:2048
	ds_read_b128 v[32:35], v156 offset:3072
	s_add_u32 s22, s43, s21
	s_addc_u32 s23, s44, 0
	s_and_b64 s[24:25], s[2:3], exec
	s_cselect_b32 s29, s23, s31
	s_cselect_b32 s28, s22, s30
	s_add_u32 s24, s45, s67
	s_addc_u32 s25, s46, 0
	s_and_b64 s[2:3], s[2:3], exec
	s_cselect_b32 s3, s25, s39
	s_cselect_b32 s2, s24, s38
	s_add_u32 s70, s30, 0x10080
	s_addc_u32 s71, s31, 0
	s_mov_b32 m0, s57
	v_lshl_add_u64 v[44:45], s[70:71], 0, v[134:135]
	ds_read_b128 v[4:7], v157
	ds_read_b128 v[8:11], v157 offset:1024
	ds_read_b128 v[20:23], v157 offset:2048
	ds_read_b128 v[24:27], v157 offset:3072
	ds_read_b128 v[36:39], v157 offset:4096
	ds_read_b128 v[40:43], v157 offset:5120
	ds_read_b128 v[52:55], v157 offset:6144
	ds_read_b128 v[56:59], v157 offset:7168
	global_load_lds_dwordx4 v[44:45], off
	v_lshl_add_u64 v[44:45], s[70:71], 0, v[138:139]
	s_mov_b32 m0, s58
	s_nop 0
	global_load_lds_dwordx4 v[44:45], off
	s_waitcnt lgkmcnt(8)
	s_barrier
	s_waitcnt lgkmcnt(0)
	s_setprio 1
	v_mov_b64_e32 v[110:111], v[2:3]
	v_mov_b64_e32 v[114:115], v[2:3]
	v_mov_b64_e32 v[106:107], v[2:3]
	v_mov_b64_e32 v[102:103], v[2:3]
	v_mov_b64_e32 v[82:83], v[2:3]
	v_mov_b64_e32 v[78:79], v[2:3]
	v_mov_b64_e32 v[50:51], v[2:3]
	v_mov_b64_e32 v[46:47], v[2:3]
	v_mov_b64_e32 v[108:109], v[0:1]
	v_mov_b64_e32 v[112:113], v[0:1]
	v_mov_b64_e32 v[104:105], v[0:1]
	v_mov_b64_e32 v[100:101], v[0:1]
	v_mov_b64_e32 v[80:81], v[0:1]
	v_mov_b64_e32 v[76:77], v[0:1]
	v_mov_b64_e32 v[48:49], v[0:1]
	v_mov_b64_e32 v[44:45], v[0:1]
	s_waitcnt lgkmcnt(0)
	v_mfma_f32_16x16x128_f8f6f4 v[108:111], v[12:19], v[4:11], v[108:111]
	v_mfma_f32_16x16x128_f8f6f4 v[112:115], v[28:35], v[4:11], v[112:115]
	v_mfma_f32_16x16x128_f8f6f4 v[104:107], v[12:19], v[20:27], v[104:107]
	v_mfma_f32_16x16x128_f8f6f4 v[100:103], v[28:35], v[20:27], v[100:103]
	v_mfma_f32_16x16x128_f8f6f4 v[80:83], v[12:19], v[36:43], v[80:83]
	v_mfma_f32_16x16x128_f8f6f4 v[76:79], v[28:35], v[36:43], v[76:79]
	v_mfma_f32_16x16x128_f8f6f4 v[48:51], v[12:19], v[52:59], v[48:51]
	v_mfma_f32_16x16x128_f8f6f4 v[44:47], v[28:35], v[52:59], v[44:47]
	s_setprio 0
	s_barrier
	v_lshl_add_u64 v[144:145], s[38:39], 0, v[132:133]
	s_add_i32 s71, s56, s47
	v_lshl_add_u64 v[60:61], v[144:145], 0, s[6:7]
	s_mov_b32 m0, s71
	v_lshl_add_u64 v[146:147], s[38:39], 0, v[136:137]
	s_add_i32 s69, s71, 0x2000
	ds_read_b128 v[160:163], v158
	ds_read_b128 v[164:167], v158 offset:1024
	ds_read_b128 v[168:171], v158 offset:2048
	ds_read_b128 v[172:175], v158 offset:3072
	global_load_lds_dwordx4 v[60:61], off
	v_lshl_add_u64 v[60:61], v[146:147], 0, s[6:7]
	s_mov_b32 m0, s69
	s_nop 0
	global_load_lds_dwordx4 v[60:61], off
	s_barrier
	s_waitcnt lgkmcnt(0)
	s_setprio 1
	v_mov_b64_e32 v[126:127], v[2:3]
	v_mov_b64_e32 v[130:131], v[2:3]
	v_mov_b64_e32 v[122:123], v[2:3]
	v_mov_b64_e32 v[118:119], v[2:3]
	v_mov_b64_e32 v[98:99], v[2:3]
	v_mov_b64_e32 v[94:95], v[2:3]
	v_mov_b64_e32 v[66:67], v[2:3]
	v_mov_b64_e32 v[62:63], v[2:3]
	v_mov_b64_e32 v[124:125], v[0:1]
	v_mov_b64_e32 v[128:129], v[0:1]
	v_mov_b64_e32 v[120:121], v[0:1]
	v_mov_b64_e32 v[116:117], v[0:1]
	v_mov_b64_e32 v[96:97], v[0:1]
	v_mov_b64_e32 v[92:93], v[0:1]
	v_mov_b64_e32 v[64:65], v[0:1]
	v_mov_b64_e32 v[60:61], v[0:1]
	s_waitcnt lgkmcnt(0)
	v_mfma_f32_16x16x128_f8f6f4 v[124:127], v[160:167], v[4:11], v[124:127]
	v_mfma_f32_16x16x128_f8f6f4 v[128:131], v[168:175], v[4:11], v[128:131]
	v_mfma_f32_16x16x128_f8f6f4 v[120:123], v[160:167], v[20:27], v[120:123]
	v_mfma_f32_16x16x128_f8f6f4 v[116:119], v[168:175], v[20:27], v[116:119]
	v_mfma_f32_16x16x128_f8f6f4 v[96:99], v[160:167], v[36:43], v[96:99]
	v_mfma_f32_16x16x128_f8f6f4 v[92:95], v[168:175], v[36:43], v[92:95]
	v_mfma_f32_16x16x128_f8f6f4 v[64:67], v[160:167], v[52:59], v[64:67]
	v_mfma_f32_16x16x128_f8f6f4 v[60:63], v[168:175], v[52:59], v[60:63]
	s_setprio 0
	v_lshl_add_u64 v[148:149], s[30:31], 0, v[134:135]
	s_mov_b32 m0, s27
	v_lshl_add_u64 v[4:5], v[148:149], 0, s[6:7]
	v_lshl_add_u64 v[150:151], s[30:31], 0, v[138:139]
	s_barrier
	ds_read_b128 v[52:55], v157 offset:16384
	ds_read_b128 v[56:59], v157 offset:17408
	ds_read_b128 v[176:179], v157 offset:18432
	ds_read_b128 v[180:183], v157 offset:19456
	ds_read_b128 v[184:187], v157 offset:20480
	ds_read_b128 v[188:191], v157 offset:21504
	ds_read_b128 v[192:195], v157 offset:22528
	ds_read_b128 v[196:199], v157 offset:23552
	global_load_lds_dwordx4 v[4:5], off
	v_lshl_add_u64 v[4:5], v[150:151], 0, s[6:7]
	s_mov_b32 m0, s48
	s_nop 0
	global_load_lds_dwordx4 v[4:5], off
	s_barrier
	s_waitcnt lgkmcnt(0)
	s_setprio 1
	v_mov_b64_e32 v[74:75], v[2:3]
	v_mov_b64_e32 v[70:71], v[2:3]
	v_mov_b64_e32 v[42:43], v[2:3]
	v_mov_b64_e32 v[38:39], v[2:3]
	v_mov_b64_e32 v[26:27], v[2:3]
	v_mov_b64_e32 v[22:23], v[2:3]
	v_mov_b64_e32 v[10:11], v[2:3]
	v_mov_b64_e32 v[6:7], v[2:3]
	v_mov_b64_e32 v[72:73], v[0:1]
	v_mov_b64_e32 v[68:69], v[0:1]
	v_mov_b64_e32 v[40:41], v[0:1]
	v_mov_b64_e32 v[36:37], v[0:1]
	v_mov_b64_e32 v[24:25], v[0:1]
	v_mov_b64_e32 v[20:21], v[0:1]
	v_mov_b64_e32 v[8:9], v[0:1]
	v_mov_b64_e32 v[4:5], v[0:1]
	s_waitcnt lgkmcnt(0)
	v_mfma_f32_16x16x128_f8f6f4 v[72:75], v[12:19], v[52:59], v[72:75]
	v_mfma_f32_16x16x128_f8f6f4 v[68:71], v[28:35], v[52:59], v[68:71]
	v_mfma_f32_16x16x128_f8f6f4 v[40:43], v[12:19], v[176:183], v[40:43]
	v_mfma_f32_16x16x128_f8f6f4 v[36:39], v[28:35], v[176:183], v[36:39]
	v_mfma_f32_16x16x128_f8f6f4 v[24:27], v[12:19], v[184:191], v[24:27]
	v_mfma_f32_16x16x128_f8f6f4 v[20:23], v[28:35], v[184:191], v[20:23]
	v_mfma_f32_16x16x128_f8f6f4 v[8:11], v[12:19], v[192:199], v[8:11]
	v_mfma_f32_16x16x128_f8f6f4 v[4:7], v[28:35], v[192:199], v[4:7]
	s_setprio 0
	s_barrier
	s_add_u32 s74, s38, 0x10100
	s_addc_u32 s75, s39, 0
	s_add_i32 s72, s59, s47
	v_lshl_add_u64 v[12:13], s[74:75], 0, v[132:133]
	s_mov_b32 m0, s72
	s_add_i32 s70, s72, 0x2000
	global_load_lds_dwordx4 v[12:13], off
	v_lshl_add_u64 v[12:13], s[74:75], 0, v[136:137]
	s_mov_b32 m0, s70
	s_nop 0
	global_load_lds_dwordx4 v[12:13], off
	s_waitcnt vmcnt(6)
	s_barrier
	s_setprio 1
	v_mov_b64_e32 v[90:91], v[2:3]
	v_mov_b64_e32 v[86:87], v[2:3]
	v_mov_b64_e32 v[88:89], v[0:1]
	v_mov_b64_e32 v[84:85], v[0:1]
	v_mfma_f32_16x16x128_f8f6f4 v[88:91], v[160:167], v[52:59], v[88:91]
	v_mfma_f32_16x16x128_f8f6f4 v[84:87], v[168:175], v[52:59], v[84:87]
	v_mov_b64_e32 v[58:59], v[2:3]
	v_mov_b64_e32 v[54:55], v[2:3]
	v_mov_b64_e32 v[34:35], v[2:3]
	v_mov_b64_e32 v[30:31], v[2:3]
	v_mov_b64_e32 v[18:19], v[2:3]
	v_mov_b64_e32 v[14:15], v[2:3]
	v_mov_b64_e32 v[56:57], v[0:1]
	v_mov_b64_e32 v[52:53], v[0:1]
	v_mov_b64_e32 v[32:33], v[0:1]
	v_mov_b64_e32 v[28:29], v[0:1]
	v_mov_b64_e32 v[16:17], v[0:1]
	v_mov_b64_e32 v[12:13], v[0:1]
	v_mfma_f32_16x16x128_f8f6f4 v[56:59], v[160:167], v[176:183], v[56:59]
	v_mfma_f32_16x16x128_f8f6f4 v[52:55], v[168:175], v[176:183], v[52:55]
	v_mfma_f32_16x16x128_f8f6f4 v[32:35], v[160:167], v[184:191], v[32:35]
	v_mfma_f32_16x16x128_f8f6f4 v[28:31], v[168:175], v[184:191], v[28:31]
	v_mfma_f32_16x16x128_f8f6f4 v[16:19], v[160:167], v[192:199], v[16:19]
	v_mfma_f32_16x16x128_f8f6f4 v[12:15], v[168:175], v[192:199], v[12:15]
	s_setprio 0
	s_add_i32 s73, 0, 0x18000
	v_add_u32_e32 v159, s73, v155
	s_barrier
	ds_read_b128 v[162:165], v159
	ds_read_b128 v[166:169], v159 offset:1024
	ds_read_b128 v[170:173], v159 offset:2048
	ds_read_b128 v[174:177], v159 offset:3072
	s_add_u32 s74, s30, 0x10100
	s_addc_u32 s75, s31, 0
	s_mov_b32 m0, s49
	v_lshl_add_u64 v[160:161], s[74:75], 0, v[134:135]
	ds_read_b128 v[178:181], v157 offset:32768
	ds_read_b128 v[182:185], v157 offset:33792
	ds_read_b128 v[186:189], v157 offset:34816
	ds_read_b128 v[190:193], v157 offset:35840
	ds_read_b128 v[194:197], v157 offset:36864
	ds_read_b128 v[198:201], v157 offset:37888
	ds_read_b128 v[202:205], v157 offset:38912
	ds_read_b128 v[206:209], v157 offset:39936
	global_load_lds_dwordx4 v[160:161], off
	v_lshl_add_u64 v[160:161], s[74:75], 0, v[138:139]
	s_mov_b32 m0, s50
	s_nop 0
	global_load_lds_dwordx4 v[160:161], off
	s_waitcnt lgkmcnt(8)
	s_barrier
	s_waitcnt lgkmcnt(0)
	s_setprio 1
	s_waitcnt lgkmcnt(0)
	v_mfma_f32_16x16x128_f8f6f4 v[108:111], v[162:169], v[178:185], v[108:111]
	v_mfma_f32_16x16x128_f8f6f4 v[112:115], v[170:177], v[178:185], v[112:115]
	v_mfma_f32_16x16x128_f8f6f4 v[104:107], v[162:169], v[186:193], v[104:107]
	v_mfma_f32_16x16x128_f8f6f4 v[100:103], v[170:177], v[186:193], v[100:103]
	v_mfma_f32_16x16x128_f8f6f4 v[80:83], v[162:169], v[194:201], v[80:83]
	v_mfma_f32_16x16x128_f8f6f4 v[76:79], v[170:177], v[194:201], v[76:79]
	v_mfma_f32_16x16x128_f8f6f4 v[48:51], v[162:169], v[202:209], v[48:51]
	v_mfma_f32_16x16x128_f8f6f4 v[44:47], v[170:177], v[202:209], v[44:47]
	s_setprio 0
	s_barrier
	s_add_i32 s75, 0, 0x1c000
	s_add_i32 s74, s73, s47
	v_add_u32_e32 v160, s75, v155
	v_lshl_add_u64 v[144:145], v[144:145], 0, s[16:17]
	s_mov_b32 m0, s74
	s_add_i32 s73, s74, 0x2000
	ds_read_b128 v[210:213], v160
	ds_read_b128 v[214:217], v160 offset:1024
	ds_read_b128 v[224:227], v160 offset:2048
	ds_read_b128 v[228:231], v160 offset:3072
	global_load_lds_dwordx4 v[144:145], off
	v_lshl_add_u64 v[144:145], v[146:147], 0, s[16:17]
	s_mov_b32 m0, s73
	s_nop 0
	global_load_lds_dwordx4 v[144:145], off
	s_barrier
	s_waitcnt lgkmcnt(0)
	s_setprio 1
	s_waitcnt lgkmcnt(0)
	v_mfma_f32_16x16x128_f8f6f4 v[124:127], v[210:217], v[178:185], v[124:127]
	v_mfma_f32_16x16x128_f8f6f4 v[128:131], v[224:231], v[178:185], v[128:131]
	v_mfma_f32_16x16x128_f8f6f4 v[120:123], v[210:217], v[186:193], v[120:123]
	v_mfma_f32_16x16x128_f8f6f4 v[116:119], v[224:231], v[186:193], v[116:119]
	v_mfma_f32_16x16x128_f8f6f4 v[96:99], v[210:217], v[194:201], v[96:99]
	v_mfma_f32_16x16x128_f8f6f4 v[92:95], v[224:231], v[194:201], v[92:95]
	v_mfma_f32_16x16x128_f8f6f4 v[64:67], v[210:217], v[202:209], v[64:67]
	v_mfma_f32_16x16x128_f8f6f4 v[60:63], v[224:231], v[202:209], v[60:63]
	s_setprio 0
	s_mov_b32 m0, s52
	v_lshl_add_u64 v[144:145], v[148:149], 0, s[16:17]
	s_barrier
	ds_read_b128 v[178:181], v157 offset:49152
	ds_read_b128 v[182:185], v157 offset:50176
	ds_read_b128 v[186:189], v157 offset:51200
	ds_read_b128 v[190:193], v157 offset:52224
	ds_read_b128 v[194:197], v157 offset:53248
	ds_read_b128 v[198:201], v157 offset:54272
	ds_read_b128 v[202:205], v157 offset:55296
	ds_read_b128 v[206:209], v157 offset:56320
	global_load_lds_dwordx4 v[144:145], off
	v_lshl_add_u64 v[144:145], v[150:151], 0, s[16:17]
	s_mov_b32 m0, s53
	s_nop 0
	global_load_lds_dwordx4 v[144:145], off
	s_barrier
	s_waitcnt lgkmcnt(0)
	s_setprio 1
	s_waitcnt lgkmcnt(0)
	v_mfma_f32_16x16x128_f8f6f4 v[72:75], v[162:169], v[178:185], v[72:75]
	v_mfma_f32_16x16x128_f8f6f4 v[68:71], v[170:177], v[178:185], v[68:71]
	v_mfma_f32_16x16x128_f8f6f4 v[40:43], v[162:169], v[186:193], v[40:43]
	v_mfma_f32_16x16x128_f8f6f4 v[36:39], v[170:177], v[186:193], v[36:39]
	v_mfma_f32_16x16x128_f8f6f4 v[24:27], v[162:169], v[194:201], v[24:27]
	v_mfma_f32_16x16x128_f8f6f4 v[20:23], v[170:177], v[194:201], v[20:23]
	v_mfma_f32_16x16x128_f8f6f4 v[8:11], v[162:169], v[202:209], v[8:11]
	v_mfma_f32_16x16x128_f8f6f4 v[4:7], v[170:177], v[202:209], v[4:7]
	s_setprio 0
	s_barrier
	s_add_u32 s76, s38, 0x10180
	s_addc_u32 s77, s39, 0
	s_add_i32 s39, s75, s47
	v_lshl_add_u64 v[144:145], s[76:77], 0, v[132:133]
	s_mov_b32 m0, s39
	s_add_i32 s38, s39, 0x2000
	global_load_lds_dwordx4 v[144:145], off
	v_lshl_add_u64 v[144:145], s[76:77], 0, v[136:137]
	s_mov_b32 m0, s38
	s_nop 0
	global_load_lds_dwordx4 v[144:145], off
	s_waitcnt vmcnt(6)
	s_barrier
	s_setprio 1
	v_mfma_f32_16x16x128_f8f6f4 v[88:91], v[210:217], v[178:185], v[88:91]
	v_mfma_f32_16x16x128_f8f6f4 v[84:87], v[224:231], v[178:185], v[84:87]
	v_mfma_f32_16x16x128_f8f6f4 v[56:59], v[210:217], v[186:193], v[56:59]
	v_mfma_f32_16x16x128_f8f6f4 v[52:55], v[224:231], v[186:193], v[52:55]
	v_mfma_f32_16x16x128_f8f6f4 v[32:35], v[210:217], v[194:201], v[32:35]
	v_mfma_f32_16x16x128_f8f6f4 v[28:31], v[224:231], v[194:201], v[28:31]
	v_mfma_f32_16x16x128_f8f6f4 v[16:19], v[210:217], v[202:209], v[16:19]
	v_mfma_f32_16x16x128_f8f6f4 v[12:15], v[224:231], v[202:209], v[12:15]
	s_setprio 0
	s_barrier
	ds_read_b128 v[162:165], v156
	ds_read_b128 v[166:169], v156 offset:1024
	ds_read_b128 v[170:173], v156 offset:2048
	ds_read_b128 v[174:177], v156 offset:3072
	s_add_u32 s30, s30, 0x10180
	s_addc_u32 s31, s31, 0
	s_mov_b32 m0, s57
	v_lshl_add_u64 v[144:145], s[30:31], 0, v[134:135]
	ds_read_b128 v[178:181], v157
	ds_read_b128 v[182:185], v157 offset:1024
	ds_read_b128 v[186:189], v157 offset:2048
	ds_read_b128 v[190:193], v157 offset:3072
	ds_read_b128 v[194:197], v157 offset:4096
	ds_read_b128 v[198:201], v157 offset:5120
	ds_read_b128 v[202:205], v157 offset:6144
	ds_read_b128 v[206:209], v157 offset:7168
	global_load_lds_dwordx4 v[144:145], off
	v_lshl_add_u64 v[144:145], s[30:31], 0, v[138:139]
	s_mov_b32 m0, s58
	s_nop 0
	global_load_lds_dwordx4 v[144:145], off
	s_waitcnt lgkmcnt(8)
	s_barrier
	s_waitcnt lgkmcnt(0)
	s_setprio 1
	s_waitcnt lgkmcnt(0)
	v_mfma_f32_16x16x128_f8f6f4 v[108:111], v[162:169], v[178:185], v[108:111]
	v_mfma_f32_16x16x128_f8f6f4 v[112:115], v[170:177], v[178:185], v[112:115]
	v_mfma_f32_16x16x128_f8f6f4 v[104:107], v[162:169], v[186:193], v[104:107]
	v_mfma_f32_16x16x128_f8f6f4 v[100:103], v[170:177], v[186:193], v[100:103]
	v_mfma_f32_16x16x128_f8f6f4 v[80:83], v[162:169], v[194:201], v[80:83]
	v_mfma_f32_16x16x128_f8f6f4 v[76:79], v[170:177], v[194:201], v[76:79]
	v_mfma_f32_16x16x128_f8f6f4 v[48:51], v[162:169], v[202:209], v[48:51]
	v_mfma_f32_16x16x128_f8f6f4 v[44:47], v[170:177], v[202:209], v[44:47]
	s_setprio 0
	s_barrier
	s_mov_b32 m0, s71
	v_lshl_add_u64 v[144:145], s[2:3], 0, v[132:133]
	ds_read_b128 v[210:213], v158
	ds_read_b128 v[214:217], v158 offset:1024
	ds_read_b128 v[224:227], v158 offset:2048
	ds_read_b128 v[228:231], v158 offset:3072
	global_load_lds_dwordx4 v[144:145], off
	v_lshl_add_u64 v[146:147], s[2:3], 0, v[136:137]
	s_mov_b32 m0, s69
	s_nop 0
	global_load_lds_dwordx4 v[146:147], off
	s_barrier
	s_waitcnt lgkmcnt(0)
	s_setprio 1
	s_waitcnt lgkmcnt(0)
	v_mfma_f32_16x16x128_f8f6f4 v[124:127], v[210:217], v[178:185], v[124:127]
	v_mfma_f32_16x16x128_f8f6f4 v[128:131], v[224:231], v[178:185], v[128:131]
	v_mfma_f32_16x16x128_f8f6f4 v[120:123], v[210:217], v[186:193], v[120:123]
	v_mfma_f32_16x16x128_f8f6f4 v[116:119], v[224:231], v[186:193], v[116:119]
	v_mfma_f32_16x16x128_f8f6f4 v[96:99], v[210:217], v[194:201], v[96:99]
	v_mfma_f32_16x16x128_f8f6f4 v[92:95], v[224:231], v[194:201], v[92:95]
	v_mfma_f32_16x16x128_f8f6f4 v[64:67], v[210:217], v[202:209], v[64:67]
	v_mfma_f32_16x16x128_f8f6f4 v[60:63], v[224:231], v[202:209], v[60:63]
	s_setprio 0
	s_mov_b32 m0, s27
	v_lshl_add_u64 v[148:149], s[28:29], 0, v[134:135]
	s_barrier
	ds_read_b128 v[178:181], v157 offset:16384
	ds_read_b128 v[182:185], v157 offset:17408
	ds_read_b128 v[186:189], v157 offset:18432
	ds_read_b128 v[190:193], v157 offset:19456
	ds_read_b128 v[194:197], v157 offset:20480
	ds_read_b128 v[198:201], v157 offset:21504
	ds_read_b128 v[202:205], v157 offset:22528
	ds_read_b128 v[206:209], v157 offset:23552
	global_load_lds_dwordx4 v[148:149], off
	v_lshl_add_u64 v[150:151], s[28:29], 0, v[138:139]
	s_mov_b32 m0, s48
	s_nop 0
	global_load_lds_dwordx4 v[150:151], off
	s_barrier
	s_waitcnt lgkmcnt(0)
	s_setprio 1
	s_waitcnt lgkmcnt(0)
	v_mfma_f32_16x16x128_f8f6f4 v[72:75], v[162:169], v[178:185], v[72:75]
	v_mfma_f32_16x16x128_f8f6f4 v[68:71], v[170:177], v[178:185], v[68:71]
	v_mfma_f32_16x16x128_f8f6f4 v[40:43], v[162:169], v[186:193], v[40:43]
	v_mfma_f32_16x16x128_f8f6f4 v[36:39], v[170:177], v[186:193], v[36:39]
	v_mfma_f32_16x16x128_f8f6f4 v[24:27], v[162:169], v[194:201], v[24:27]
	v_mfma_f32_16x16x128_f8f6f4 v[20:23], v[170:177], v[194:201], v[20:23]
	v_mfma_f32_16x16x128_f8f6f4 v[8:11], v[162:169], v[202:209], v[8:11]
	v_mfma_f32_16x16x128_f8f6f4 v[4:7], v[170:177], v[202:209], v[4:7]
	s_setprio 0
	s_barrier
	s_add_u32 s30, s2, 0x10000
	s_addc_u32 s31, s3, 0
	s_mov_b32 m0, s72
	v_lshl_add_u64 v[162:163], s[30:31], 0, v[132:133]
	global_load_lds_dwordx4 v[162:163], off
	v_lshl_add_u64 v[162:163], s[30:31], 0, v[136:137]
	s_mov_b32 m0, s70
	s_nop 0
	global_load_lds_dwordx4 v[162:163], off
	s_waitcnt vmcnt(6)
	s_barrier
	s_setprio 1
	v_mfma_f32_16x16x128_f8f6f4 v[88:91], v[210:217], v[178:185], v[88:91]
	v_mfma_f32_16x16x128_f8f6f4 v[84:87], v[224:231], v[178:185], v[84:87]
	v_mfma_f32_16x16x128_f8f6f4 v[56:59], v[210:217], v[186:193], v[56:59]
	v_mfma_f32_16x16x128_f8f6f4 v[52:55], v[224:231], v[186:193], v[52:55]
	v_mfma_f32_16x16x128_f8f6f4 v[32:35], v[210:217], v[194:201], v[32:35]
	v_mfma_f32_16x16x128_f8f6f4 v[28:31], v[224:231], v[194:201], v[28:31]
	v_mfma_f32_16x16x128_f8f6f4 v[16:19], v[210:217], v[202:209], v[16:19]
	v_mfma_f32_16x16x128_f8f6f4 v[12:15], v[224:231], v[202:209], v[12:15]
	s_setprio 0
	s_barrier
	ds_read_b128 v[162:165], v159
	ds_read_b128 v[166:169], v159 offset:1024
	ds_read_b128 v[170:173], v159 offset:2048
	ds_read_b128 v[174:177], v159 offset:3072
	s_add_u32 s28, s28, 0x10000
	s_addc_u32 s29, s29, 0
	s_mov_b32 m0, s49
	v_lshl_add_u64 v[210:211], s[28:29], 0, v[134:135]
	ds_read_b128 v[178:181], v157 offset:32768
	ds_read_b128 v[182:185], v157 offset:33792
	ds_read_b128 v[186:189], v157 offset:34816
	ds_read_b128 v[190:193], v157 offset:35840
	ds_read_b128 v[194:197], v157 offset:36864
	ds_read_b128 v[198:201], v157 offset:37888
	ds_read_b128 v[202:205], v157 offset:38912
	ds_read_b128 v[206:209], v157 offset:39936
	global_load_lds_dwordx4 v[210:211], off
	v_lshl_add_u64 v[210:211], s[28:29], 0, v[138:139]
	s_mov_b32 m0, s50
	s_nop 0
	global_load_lds_dwordx4 v[210:211], off
	s_waitcnt lgkmcnt(8)
	s_barrier
	s_waitcnt lgkmcnt(0)
	s_setprio 1
	s_waitcnt lgkmcnt(0)
	v_mfma_f32_16x16x128_f8f6f4 v[108:111], v[162:169], v[178:185], v[108:111]
	v_mfma_f32_16x16x128_f8f6f4 v[112:115], v[170:177], v[178:185], v[112:115]
	v_mfma_f32_16x16x128_f8f6f4 v[104:107], v[162:169], v[186:193], v[104:107]
	v_mfma_f32_16x16x128_f8f6f4 v[100:103], v[170:177], v[186:193], v[100:103]
	v_mfma_f32_16x16x128_f8f6f4 v[80:83], v[162:169], v[194:201], v[80:83]
	v_mfma_f32_16x16x128_f8f6f4 v[76:79], v[170:177], v[194:201], v[76:79]
	v_mfma_f32_16x16x128_f8f6f4 v[48:51], v[162:169], v[202:209], v[48:51]
	v_mfma_f32_16x16x128_f8f6f4 v[44:47], v[170:177], v[202:209], v[44:47]
	s_setprio 0
	s_barrier
	s_mov_b32 m0, s74
	v_lshl_add_u64 v[144:145], v[144:145], 0, s[12:13]
	ds_read_b128 v[210:213], v160
	ds_read_b128 v[214:217], v160 offset:1024
	ds_read_b128 v[224:227], v160 offset:2048
	ds_read_b128 v[228:231], v160 offset:3072
	global_load_lds_dwordx4 v[144:145], off
	v_lshl_add_u64 v[144:145], v[146:147], 0, s[12:13]
	s_mov_b32 m0, s73
	s_nop 0
	global_load_lds_dwordx4 v[144:145], off
	s_barrier
	s_waitcnt lgkmcnt(0)
	s_setprio 1
	s_waitcnt lgkmcnt(0)
	v_mfma_f32_16x16x128_f8f6f4 v[124:127], v[210:217], v[178:185], v[124:127]
	v_mfma_f32_16x16x128_f8f6f4 v[128:131], v[224:231], v[178:185], v[128:131]
	v_mfma_f32_16x16x128_f8f6f4 v[120:123], v[210:217], v[186:193], v[120:123]
	v_mfma_f32_16x16x128_f8f6f4 v[116:119], v[224:231], v[186:193], v[116:119]
	v_mfma_f32_16x16x128_f8f6f4 v[96:99], v[210:217], v[194:201], v[96:99]
	v_mfma_f32_16x16x128_f8f6f4 v[92:95], v[224:231], v[194:201], v[92:95]
	v_mfma_f32_16x16x128_f8f6f4 v[64:67], v[210:217], v[202:209], v[64:67]
	v_mfma_f32_16x16x128_f8f6f4 v[60:63], v[224:231], v[202:209], v[60:63]
	s_setprio 0
	s_mov_b32 m0, s52
	v_lshl_add_u64 v[144:145], v[148:149], 0, s[12:13]
	s_barrier
	ds_read_b128 v[178:181], v157 offset:49152
	ds_read_b128 v[182:185], v157 offset:50176
	ds_read_b128 v[186:189], v157 offset:51200
	ds_read_b128 v[190:193], v157 offset:52224
	ds_read_b128 v[194:197], v157 offset:53248
	ds_read_b128 v[198:201], v157 offset:54272
	ds_read_b128 v[202:205], v157 offset:55296
	ds_read_b128 v[206:209], v157 offset:56320
	global_load_lds_dwordx4 v[144:145], off
	v_lshl_add_u64 v[144:145], v[150:151], 0, s[12:13]
	s_mov_b32 m0, s53
	s_nop 0
	global_load_lds_dwordx4 v[144:145], off
	s_barrier
	s_waitcnt lgkmcnt(0)
	s_setprio 1
	s_waitcnt lgkmcnt(0)
	v_mfma_f32_16x16x128_f8f6f4 v[72:75], v[162:169], v[178:185], v[72:75]
	v_mfma_f32_16x16x128_f8f6f4 v[68:71], v[170:177], v[178:185], v[68:71]
	v_mfma_f32_16x16x128_f8f6f4 v[40:43], v[162:169], v[186:193], v[40:43]
	v_mfma_f32_16x16x128_f8f6f4 v[36:39], v[170:177], v[186:193], v[36:39]
	v_mfma_f32_16x16x128_f8f6f4 v[24:27], v[162:169], v[194:201], v[24:27]
	v_mfma_f32_16x16x128_f8f6f4 v[20:23], v[170:177], v[194:201], v[20:23]
	v_mfma_f32_16x16x128_f8f6f4 v[8:11], v[162:169], v[202:209], v[8:11]
	v_mfma_f32_16x16x128_f8f6f4 v[4:7], v[170:177], v[202:209], v[4:7]
	s_setprio 0
	s_barrier
	s_add_u32 s2, s2, 0x10080
	s_addc_u32 s3, s3, 0
	s_mov_b32 m0, s39
	v_lshl_add_u64 v[144:145], s[2:3], 0, v[132:133]
	global_load_lds_dwordx4 v[144:145], off
	v_lshl_add_u64 v[144:145], s[2:3], 0, v[136:137]
	s_mov_b32 m0, s38
	s_nop 0
	global_load_lds_dwordx4 v[144:145], off
	s_waitcnt vmcnt(6)
	s_barrier
	s_setprio 1
	v_mfma_f32_16x16x128_f8f6f4 v[88:91], v[210:217], v[178:185], v[88:91]
	v_mfma_f32_16x16x128_f8f6f4 v[84:87], v[224:231], v[178:185], v[84:87]
	v_mfma_f32_16x16x128_f8f6f4 v[56:59], v[210:217], v[186:193], v[56:59]
	v_mfma_f32_16x16x128_f8f6f4 v[52:55], v[224:231], v[186:193], v[52:55]
	v_mfma_f32_16x16x128_f8f6f4 v[32:35], v[210:217], v[194:201], v[32:35]
	v_mfma_f32_16x16x128_f8f6f4 v[28:31], v[224:231], v[194:201], v[28:31]
	v_mfma_f32_16x16x128_f8f6f4 v[16:19], v[210:217], v[202:209], v[16:19]
	v_mfma_f32_16x16x128_f8f6f4 v[12:15], v[224:231], v[202:209], v[12:15]
	s_setprio 0
	v_lshl_add_u32 v144, s26, 8, v154
	v_ashrrev_i32_e32 v145, 31, v144
	v_lshlrev_b64 v[144:145], 12, v[144:145]
	s_lshl_b32 s2, s68, 8
	v_lshl_add_u64 v[144:145], s[10:11], 0, v[144:145]
	s_ashr_i32 s3, s2, 31
	v_lshl_add_u64 v[144:145], s[2:3], 1, v[144:145]
	v_lshl_add_u64 v[144:145], v[144:145], 0, s[4:5]
	v_pk_mul_f32 v[108:109], v[108:109], s[18:19] op_sel_hi:[1,0]
	s_barrier
	s_nop 7
	s_nop 7
	s_nop 7
	v_lshl_add_u64 v[144:145], v[144:145], 0, v[142:143]
	v_pk_mul_f32 v[110:111], v[110:111], s[18:19] op_sel_hi:[1,0]
	v_cvt_pk_bf16_f32 v108, v108, v109
	v_pk_mul_f32 v[114:115], v[114:115], s[18:19] op_sel_hi:[1,0]
	v_cvt_pk_bf16_f32 v109, v110, v111
	v_pk_mul_f32 v[112:113], v[112:113], s[18:19] op_sel_hi:[1,0]
	v_pk_mul_f32 v[104:105], v[104:105], s[18:19] op_sel_hi:[1,0]
	v_cvt_pk_bf16_f32 v110, v112, v113
	v_cvt_pk_bf16_f32 v111, v114, v115
	global_store_dwordx4 v[144:145], v[108:111], off
	v_pk_mul_f32 v[112:113], v[130:131], s[18:19] op_sel_hi:[1,0]
	v_pk_mul_f32 v[114:115], v[128:129], s[18:19] op_sel_hi:[1,0]
	v_pk_mul_f32 v[108:109], v[124:125], s[18:19] op_sel_hi:[1,0]
	v_pk_mul_f32 v[110:111], v[126:127], s[18:19] op_sel_hi:[1,0]
	v_cvt_pk_bf16_f32 v108, v108, v109
	v_pk_mul_f32 v[106:107], v[106:107], s[18:19] op_sel_hi:[1,0]
	v_cvt_pk_bf16_f32 v109, v110, v111
	v_cvt_pk_bf16_f32 v110, v114, v115
	v_cvt_pk_bf16_f32 v111, v112, v113
	global_store_dwordx4 v[144:145], v[108:111], off offset:256
	v_pk_mul_f32 v[80:81], v[80:81], s[18:19] op_sel_hi:[1,0]
	v_pk_mul_f32 v[82:83], v[82:83], s[18:19] op_sel_hi:[1,0]
	v_pk_mul_f32 v[108:109], v[102:103], s[18:19] op_sel_hi:[1,0]
	v_pk_mul_f32 v[102:103], v[100:101], s[18:19] op_sel_hi:[1,0]
	v_cvt_pk_bf16_f32 v100, v104, v105
	v_add_co_u32_e32 v104, vcc, s51, v144
	v_cvt_pk_bf16_f32 v101, v106, v107
	v_cvt_pk_bf16_f32 v102, v102, v103
	v_cvt_pk_bf16_f32 v103, v108, v109
	v_pk_mul_f32 v[106:107], v[118:119], s[18:19] op_sel_hi:[1,0]
	s_nop 0
	v_addc_co_u32_e32 v105, vcc, 0, v145, vcc
	global_store_dwordx4 v[104:105], v[100:103], off
	v_pk_mul_f32 v[108:109], v[116:117], s[18:19] op_sel_hi:[1,0]
	v_pk_mul_f32 v[48:49], v[48:49], s[18:19] op_sel_hi:[1,0]
	v_pk_mul_f32 v[100:101], v[120:121], s[18:19] op_sel_hi:[1,0]
	v_pk_mul_f32 v[102:103], v[122:123], s[18:19] op_sel_hi:[1,0]
	v_cvt_pk_bf16_f32 v100, v100, v101
	v_pk_mul_f32 v[92:93], v[92:93], s[18:19] op_sel_hi:[1,0]
	v_cvt_pk_bf16_f32 v101, v102, v103
	v_cvt_pk_bf16_f32 v102, v108, v109
	v_cvt_pk_bf16_f32 v103, v106, v107
	global_store_dwordx4 v[104:105], v[100:103], off offset:256
	v_pk_mul_f32 v[50:51], v[50:51], s[18:19] op_sel_hi:[1,0]
	v_pk_mul_f32 v[60:61], v[60:61], s[18:19] op_sel_hi:[1,0]
	v_pk_mul_f32 v[100:101], v[78:79], s[18:19] op_sel_hi:[1,0]
	v_pk_mul_f32 v[78:79], v[76:77], s[18:19] op_sel_hi:[1,0]
	v_cvt_pk_bf16_f32 v76, v80, v81
	v_add_co_u32_e32 v80, vcc, s60, v144
	v_cvt_pk_bf16_f32 v77, v82, v83
	v_cvt_pk_bf16_f32 v78, v78, v79
	v_cvt_pk_bf16_f32 v79, v100, v101
	v_pk_mul_f32 v[82:83], v[94:95], s[18:19] op_sel_hi:[1,0]
	s_nop 0
	v_addc_co_u32_e32 v81, vcc, 0, v145, vcc
	global_store_dwordx4 v[80:81], v[76:79], off
	v_pk_mul_f32 v[40:41], v[40:41], s[18:19] op_sel_hi:[1,0]
	v_pk_mul_f32 v[42:43], v[42:43], s[18:19] op_sel_hi:[1,0]
	v_pk_mul_f32 v[76:77], v[96:97], s[18:19] op_sel_hi:[1,0]
	v_pk_mul_f32 v[78:79], v[98:99], s[18:19] op_sel_hi:[1,0]
	v_cvt_pk_bf16_f32 v76, v76, v77
	v_pk_mul_f32 v[24:25], v[24:25], s[18:19] op_sel_hi:[1,0]
	v_cvt_pk_bf16_f32 v77, v78, v79
	v_cvt_pk_bf16_f32 v78, v92, v93
	v_cvt_pk_bf16_f32 v79, v82, v83
	global_store_dwordx4 v[80:81], v[76:79], off offset:256
	v_pk_mul_f32 v[26:27], v[26:27], s[18:19] op_sel_hi:[1,0]
	v_pk_mul_f32 v[8:9], v[8:9], s[18:19] op_sel_hi:[1,0]
	v_pk_mul_f32 v[76:77], v[46:47], s[18:19] op_sel_hi:[1,0]
	v_pk_mul_f32 v[46:47], v[44:45], s[18:19] op_sel_hi:[1,0]
	v_cvt_pk_bf16_f32 v44, v48, v49
	v_add_co_u32_e32 v48, vcc, s61, v144
	v_cvt_pk_bf16_f32 v45, v50, v51
	v_cvt_pk_bf16_f32 v46, v46, v47
	v_cvt_pk_bf16_f32 v47, v76, v77
	v_pk_mul_f32 v[50:51], v[62:63], s[18:19] op_sel_hi:[1,0]
	s_nop 0
	v_addc_co_u32_e32 v49, vcc, 0, v145, vcc
	global_store_dwordx4 v[48:49], v[44:47], off
	v_pk_mul_f32 v[28:29], v[28:29], s[18:19] op_sel_hi:[1,0]
	v_pk_mul_f32 v[10:11], v[10:11], s[18:19] op_sel_hi:[1,0]
	v_pk_mul_f32 v[46:47], v[66:67], s[18:19] op_sel_hi:[1,0]
	v_pk_mul_f32 v[44:45], v[64:65], s[18:19] op_sel_hi:[1,0]
	s_add_i32 s55, s55, s19
	v_cvt_pk_bf16_f32 v44, v44, v45
	v_cvt_pk_bf16_f32 v45, v46, v47
	v_cvt_pk_bf16_f32 v46, v60, v61
	v_cvt_pk_bf16_f32 v47, v50, v51
	global_store_dwordx4 v[48:49], v[44:47], off offset:256
	v_pk_mul_f32 v[48:49], v[70:71], s[18:19] op_sel_hi:[1,0]
	v_pk_mul_f32 v[50:51], v[68:69], s[18:19] op_sel_hi:[1,0]
	v_pk_mul_f32 v[46:47], v[74:75], s[18:19] op_sel_hi:[1,0]
	v_pk_mul_f32 v[44:45], v[72:73], s[18:19] op_sel_hi:[1,0]
	v_pk_mul_f32 v[60:61], v[84:85], s[18:19] op_sel_hi:[1,0]
	v_cvt_pk_bf16_f32 v44, v44, v45
	v_cvt_pk_bf16_f32 v45, v46, v47
	v_cvt_pk_bf16_f32 v46, v50, v51
	v_cvt_pk_bf16_f32 v47, v48, v49
	v_add_co_u32_e32 v48, vcc, s62, v144
	v_pk_mul_f32 v[50:51], v[86:87], s[18:19] op_sel_hi:[1,0]
	s_nop 0
	v_addc_co_u32_e32 v49, vcc, 0, v145, vcc
	global_store_dwordx4 v[48:49], v[44:47], off
	s_mov_b32 s68, s66
	s_mov_b32 s26, s20
	v_pk_mul_f32 v[44:45], v[88:89], s[18:19] op_sel_hi:[1,0]
	v_pk_mul_f32 v[46:47], v[90:91], s[18:19] op_sel_hi:[1,0]
	v_cvt_pk_bf16_f32 v44, v44, v45
	s_mov_b64 s[38:39], s[24:25]
	v_cvt_pk_bf16_f32 v45, v46, v47
	v_cvt_pk_bf16_f32 v46, v60, v61
	v_cvt_pk_bf16_f32 v47, v50, v51
	global_store_dwordx4 v[48:49], v[44:47], off offset:256
	s_mov_b64 s[30:31], s[22:23]
	v_pk_mul_f32 v[12:13], v[12:13], s[18:19] op_sel_hi:[1,0]
	v_pk_mul_f32 v[44:45], v[38:39], s[18:19] op_sel_hi:[1,0]
	v_pk_mul_f32 v[38:39], v[36:37], s[18:19] op_sel_hi:[1,0]
	v_cvt_pk_bf16_f32 v36, v40, v41
	v_add_co_u32_e32 v40, vcc, s63, v144
	v_cvt_pk_bf16_f32 v37, v42, v43
	v_cvt_pk_bf16_f32 v38, v38, v39
	v_cvt_pk_bf16_f32 v39, v44, v45
	v_pk_mul_f32 v[42:43], v[54:55], s[18:19] op_sel_hi:[1,0]
	s_nop 0
	v_addc_co_u32_e32 v41, vcc, 0, v145, vcc
	global_store_dwordx4 v[40:41], v[36:39], off
	v_pk_mul_f32 v[44:45], v[52:53], s[18:19] op_sel_hi:[1,0]
	s_nop 0
	v_pk_mul_f32 v[36:37], v[56:57], s[18:19] op_sel_hi:[1,0]
	v_pk_mul_f32 v[38:39], v[58:59], s[18:19] op_sel_hi:[1,0]
	v_cvt_pk_bf16_f32 v36, v36, v37
	s_nop 0
	v_cvt_pk_bf16_f32 v37, v38, v39
	v_cvt_pk_bf16_f32 v38, v44, v45
	v_cvt_pk_bf16_f32 v39, v42, v43
	global_store_dwordx4 v[40:41], v[36:39], off offset:256
	s_nop 1
	v_pk_mul_f32 v[36:37], v[22:23], s[18:19] op_sel_hi:[1,0]
	v_pk_mul_f32 v[22:23], v[20:21], s[18:19] op_sel_hi:[1,0]
	v_cvt_pk_bf16_f32 v20, v24, v25
	v_add_co_u32_e32 v24, vcc, s64, v144
	v_cvt_pk_bf16_f32 v21, v26, v27
	v_cvt_pk_bf16_f32 v22, v22, v23
	v_cvt_pk_bf16_f32 v23, v36, v37
	v_pk_mul_f32 v[26:27], v[30:31], s[18:19] op_sel_hi:[1,0]
	s_nop 0
	v_addc_co_u32_e32 v25, vcc, 0, v145, vcc
	global_store_dwordx4 v[24:25], v[20:23], off
	s_nop 1
	v_pk_mul_f32 v[20:21], v[32:33], s[18:19] op_sel_hi:[1,0]
	v_pk_mul_f32 v[22:23], v[34:35], s[18:19] op_sel_hi:[1,0]
	v_cvt_pk_bf16_f32 v20, v20, v21
	s_nop 0
	v_cvt_pk_bf16_f32 v21, v22, v23
	v_cvt_pk_bf16_f32 v22, v28, v29
	v_cvt_pk_bf16_f32 v23, v26, v27
	global_store_dwordx4 v[24:25], v[20:23], off offset:256
	s_nop 1
	v_pk_mul_f32 v[20:21], v[6:7], s[18:19] op_sel_hi:[1,0]
	v_pk_mul_f32 v[6:7], v[4:5], s[18:19] op_sel_hi:[1,0]
	v_cvt_pk_bf16_f32 v4, v8, v9
	v_add_co_u32_e32 v8, vcc, s65, v144
	v_cvt_pk_bf16_f32 v5, v10, v11
	v_cvt_pk_bf16_f32 v6, v6, v7
	v_cvt_pk_bf16_f32 v7, v20, v21
	v_pk_mul_f32 v[10:11], v[14:15], s[18:19] op_sel_hi:[1,0]
	s_nop 0
	v_addc_co_u32_e32 v9, vcc, 0, v145, vcc
	global_store_dwordx4 v[8:9], v[4:7], off
	s_andn2_b64 vcc, exec, s[0:1]
	s_nop 0
	v_pk_mul_f32 v[6:7], v[18:19], s[18:19] op_sel_hi:[1,0]
	v_pk_mul_f32 v[4:5], v[16:17], s[18:19] op_sel_hi:[1,0]
	s_nop 0
	v_cvt_pk_bf16_f32 v4, v4, v5
	v_cvt_pk_bf16_f32 v5, v6, v7
	v_cvt_pk_bf16_f32 v6, v12, v13
	v_cvt_pk_bf16_f32 v7, v10, v11
	global_store_dwordx4 v[8:9], v[4:7], off offset:256
	s_cbranch_vccz .LBB0_1350

.LBB0_1680:
	ds_read_b128 v[12:15], v176
	ds_read_b128 v[16:19], v176 offset:1024
	ds_read_b128 v[28:31], v176 offset:2048
	ds_read_b128 v[32:35], v176 offset:3072
	s_add_u32 s18, s29, s57
	v_cmp_lt_i64_e32 vcc, s[6:7], v[144:145]
	s_addc_u32 s19, s30, 0
	s_and_b64 s[2:3], vcc, exec
	s_cselect_b32 s25, s19, s23
	s_cselect_b32 s24, s18, s22
	s_add_u32 s20, s31, s58
	s_addc_u32 s21, s38, 0
	s_and_b64 s[2:3], vcc, exec
	s_cselect_b32 s3, s21, s27
	s_cselect_b32 s2, s20, s26
	s_add_u32 s62, s22, 0x20080
	s_addc_u32 s63, s23, 0
	s_add_i32 s67, s40, 0xc000
	v_lshl_add_u64 v[44:45], s[62:63], 0, v[136:137]
	s_mov_b32 m0, s67
	s_add_i32 s61, s40, 0xe000
	ds_read_b128 v[4:7], v177
	ds_read_b128 v[8:11], v177 offset:1024
	ds_read_b128 v[20:23], v177 offset:2048
	ds_read_b128 v[24:27], v177 offset:3072
	ds_read_b128 v[36:39], v177 offset:4096
	ds_read_b128 v[40:43], v177 offset:5120
	ds_read_b128 v[52:55], v177 offset:6144
	ds_read_b128 v[56:59], v177 offset:7168
	global_load_lds_dwordx4 v[44:45], off
	v_lshl_add_u64 v[44:45], s[62:63], 0, v[140:141]
	s_mov_b32 m0, s61
	s_nop 0
	global_load_lds_dwordx4 v[44:45], off
	s_waitcnt lgkmcnt(8)
	s_barrier
	s_waitcnt lgkmcnt(0)
	s_setprio 1
	v_mov_b64_e32 v[110:111], v[2:3]
	v_mov_b64_e32 v[114:115], v[2:3]
	v_mov_b64_e32 v[106:107], v[2:3]
	v_mov_b64_e32 v[102:103], v[2:3]
	v_mov_b64_e32 v[82:83], v[2:3]
	v_mov_b64_e32 v[78:79], v[2:3]
	v_mov_b64_e32 v[50:51], v[2:3]
	v_mov_b64_e32 v[46:47], v[2:3]
	v_mov_b64_e32 v[108:109], v[0:1]
	v_mov_b64_e32 v[112:113], v[0:1]
	v_mov_b64_e32 v[104:105], v[0:1]
	v_mov_b64_e32 v[100:101], v[0:1]
	v_mov_b64_e32 v[80:81], v[0:1]
	v_mov_b64_e32 v[76:77], v[0:1]
	v_mov_b64_e32 v[48:49], v[0:1]
	v_mov_b64_e32 v[44:45], v[0:1]
	s_waitcnt lgkmcnt(0)
	v_mfma_f32_16x16x128_f8f6f4 v[108:111], v[12:19], v[4:11], v[108:111]
	v_mfma_f32_16x16x128_f8f6f4 v[112:115], v[28:35], v[4:11], v[112:115]
	v_mfma_f32_16x16x128_f8f6f4 v[104:107], v[12:19], v[20:27], v[104:107]
	v_mfma_f32_16x16x128_f8f6f4 v[100:103], v[28:35], v[20:27], v[100:103]
	v_mfma_f32_16x16x128_f8f6f4 v[80:83], v[12:19], v[36:43], v[80:83]
	v_mfma_f32_16x16x128_f8f6f4 v[76:79], v[28:35], v[36:43], v[76:79]
	v_mfma_f32_16x16x128_f8f6f4 v[48:51], v[12:19], v[52:59], v[48:51]
	v_mfma_f32_16x16x128_f8f6f4 v[44:47], v[28:35], v[52:59], v[44:47]
	s_setprio 0
	s_barrier
	v_lshl_add_u64 v[132:133], s[26:27], 0, v[138:139]
	s_add_i32 s64, s50, s39
	v_lshl_add_u64 v[60:61], v[132:133], 0, s[10:11]
	s_mov_b32 m0, s64
	v_lshl_add_u64 v[134:135], s[26:27], 0, v[142:143]
	s_add_i32 s62, s64, 0x2000
	ds_read_b128 v[154:157], v178
	ds_read_b128 v[158:161], v178 offset:1024
	ds_read_b128 v[180:183], v178 offset:2048
	ds_read_b128 v[184:187], v178 offset:3072
	global_load_lds_dwordx4 v[60:61], off
	v_lshl_add_u64 v[60:61], v[134:135], 0, s[10:11]
	s_mov_b32 m0, s62
	s_nop 0
	global_load_lds_dwordx4 v[60:61], off
	s_barrier
	s_waitcnt lgkmcnt(0)
	s_setprio 1
	v_mov_b64_e32 v[126:127], v[2:3]
	v_mov_b64_e32 v[130:131], v[2:3]
	v_mov_b64_e32 v[122:123], v[2:3]
	v_mov_b64_e32 v[118:119], v[2:3]
	v_mov_b64_e32 v[98:99], v[2:3]
	v_mov_b64_e32 v[94:95], v[2:3]
	v_mov_b64_e32 v[66:67], v[2:3]
	v_mov_b64_e32 v[62:63], v[2:3]
	v_mov_b64_e32 v[124:125], v[0:1]
	v_mov_b64_e32 v[128:129], v[0:1]
	v_mov_b64_e32 v[120:121], v[0:1]
	v_mov_b64_e32 v[116:117], v[0:1]
	v_mov_b64_e32 v[96:97], v[0:1]
	v_mov_b64_e32 v[92:93], v[0:1]
	v_mov_b64_e32 v[64:65], v[0:1]
	v_mov_b64_e32 v[60:61], v[0:1]
	s_waitcnt lgkmcnt(0)
	v_mfma_f32_16x16x128_f8f6f4 v[124:127], v[154:161], v[4:11], v[124:127]
	v_mfma_f32_16x16x128_f8f6f4 v[128:131], v[180:187], v[4:11], v[128:131]
	v_mfma_f32_16x16x128_f8f6f4 v[120:123], v[154:161], v[20:27], v[120:123]
	v_mfma_f32_16x16x128_f8f6f4 v[116:119], v[180:187], v[20:27], v[116:119]
	v_mfma_f32_16x16x128_f8f6f4 v[96:99], v[154:161], v[36:43], v[96:99]
	v_mfma_f32_16x16x128_f8f6f4 v[92:95], v[180:187], v[36:43], v[92:95]
	v_mfma_f32_16x16x128_f8f6f4 v[64:67], v[154:161], v[52:59], v[64:67]
	v_mfma_f32_16x16x128_f8f6f4 v[60:63], v[180:187], v[52:59], v[60:63]
	s_setprio 0
	v_lshl_add_u64 v[150:151], s[22:23], 0, v[136:137]
	s_mov_b32 m0, s40
	v_lshl_add_u64 v[4:5], v[150:151], 0, s[10:11]
	v_lshl_add_u64 v[152:153], s[22:23], 0, v[140:141]
	s_barrier
	ds_read_b128 v[52:55], v177 offset:16384
	ds_read_b128 v[56:59], v177 offset:17408
	ds_read_b128 v[188:191], v177 offset:18432
	ds_read_b128 v[192:195], v177 offset:19456
	ds_read_b128 v[196:199], v177 offset:20480
	ds_read_b128 v[200:203], v177 offset:21504
	ds_read_b128 v[204:207], v177 offset:22528
	ds_read_b128 v[208:211], v177 offset:23552
	global_load_lds_dwordx4 v[4:5], off
	v_lshl_add_u64 v[4:5], v[152:153], 0, s[10:11]
	s_mov_b32 m0, s41
	s_nop 0
	global_load_lds_dwordx4 v[4:5], off
	s_barrier
	s_waitcnt lgkmcnt(0)
	s_setprio 1
	v_mov_b64_e32 v[74:75], v[2:3]
	v_mov_b64_e32 v[70:71], v[2:3]
	v_mov_b64_e32 v[42:43], v[2:3]
	v_mov_b64_e32 v[38:39], v[2:3]
	v_mov_b64_e32 v[26:27], v[2:3]
	v_mov_b64_e32 v[22:23], v[2:3]
	v_mov_b64_e32 v[10:11], v[2:3]
	v_mov_b64_e32 v[6:7], v[2:3]
	v_mov_b64_e32 v[72:73], v[0:1]
	v_mov_b64_e32 v[68:69], v[0:1]
	v_mov_b64_e32 v[40:41], v[0:1]
	v_mov_b64_e32 v[36:37], v[0:1]
	v_mov_b64_e32 v[24:25], v[0:1]
	v_mov_b64_e32 v[20:21], v[0:1]
	v_mov_b64_e32 v[8:9], v[0:1]
	v_mov_b64_e32 v[4:5], v[0:1]
	s_waitcnt lgkmcnt(0)
	v_mfma_f32_16x16x128_f8f6f4 v[72:75], v[12:19], v[52:59], v[72:75]
	v_mfma_f32_16x16x128_f8f6f4 v[68:71], v[28:35], v[52:59], v[68:71]
	v_mfma_f32_16x16x128_f8f6f4 v[40:43], v[12:19], v[188:195], v[40:43]
	v_mfma_f32_16x16x128_f8f6f4 v[36:39], v[28:35], v[188:195], v[36:39]
	v_mfma_f32_16x16x128_f8f6f4 v[24:27], v[12:19], v[196:203], v[24:27]
	v_mfma_f32_16x16x128_f8f6f4 v[20:23], v[28:35], v[196:203], v[20:23]
	v_mfma_f32_16x16x128_f8f6f4 v[8:11], v[12:19], v[204:211], v[8:11]
	v_mfma_f32_16x16x128_f8f6f4 v[4:7], v[28:35], v[204:211], v[4:7]
	s_setprio 0
	s_barrier
	s_add_u32 s68, s26, 0x10100
	s_addc_u32 s69, s27, 0
	s_add_i32 s65, s51, s39
	v_lshl_add_u64 v[12:13], s[68:69], 0, v[138:139]
	s_mov_b32 m0, s65
	s_add_i32 s63, s65, 0x2000
	global_load_lds_dwordx4 v[12:13], off
	v_lshl_add_u64 v[12:13], s[68:69], 0, v[142:143]
	s_mov_b32 m0, s63
	s_nop 0
	global_load_lds_dwordx4 v[12:13], off
	s_waitcnt vmcnt(6)
	s_barrier
	s_setprio 1
	v_mov_b64_e32 v[90:91], v[2:3]
	v_mov_b64_e32 v[86:87], v[2:3]
	v_mov_b64_e32 v[88:89], v[0:1]
	v_mov_b64_e32 v[84:85], v[0:1]
	v_mfma_f32_16x16x128_f8f6f4 v[88:91], v[154:161], v[52:59], v[88:91]
	v_mfma_f32_16x16x128_f8f6f4 v[84:87], v[180:187], v[52:59], v[84:87]
	v_mov_b64_e32 v[58:59], v[2:3]
	v_mov_b64_e32 v[54:55], v[2:3]
	v_mov_b64_e32 v[34:35], v[2:3]
	v_mov_b64_e32 v[30:31], v[2:3]
	v_mov_b64_e32 v[18:19], v[2:3]
	v_mov_b64_e32 v[14:15], v[2:3]
	v_mov_b64_e32 v[56:57], v[0:1]
	v_mov_b64_e32 v[52:53], v[0:1]
	v_mov_b64_e32 v[32:33], v[0:1]
	v_mov_b64_e32 v[28:29], v[0:1]
	v_mov_b64_e32 v[16:17], v[0:1]
	v_mov_b64_e32 v[12:13], v[0:1]
	v_mfma_f32_16x16x128_f8f6f4 v[56:59], v[154:161], v[188:195], v[56:59]
	v_mfma_f32_16x16x128_f8f6f4 v[52:55], v[180:187], v[188:195], v[52:55]
	v_mfma_f32_16x16x128_f8f6f4 v[32:35], v[154:161], v[196:203], v[32:35]
	v_mfma_f32_16x16x128_f8f6f4 v[28:31], v[180:187], v[196:203], v[28:31]
	v_mfma_f32_16x16x128_f8f6f4 v[16:19], v[154:161], v[204:211], v[16:19]
	v_mfma_f32_16x16x128_f8f6f4 v[12:15], v[180:187], v[204:211], v[12:15]
	s_setprio 0
	s_add_i32 s66, 0, 0x18000
	v_add_u32_e32 v154, s66, v174
	s_barrier
	ds_read_b128 v[156:159], v154
	ds_read_b128 v[160:163], v154 offset:1024
	ds_read_b128 v[180:183], v154 offset:2048
	ds_read_b128 v[184:187], v154 offset:3072
	s_add_u32 s68, s22, 0x20100
	s_addc_u32 s69, s23, 0
	s_mov_b32 m0, s42
	v_lshl_add_u64 v[164:165], s[68:69], 0, v[136:137]
	ds_read_b128 v[188:191], v177 offset:32768
	ds_read_b128 v[192:195], v177 offset:33792
	ds_read_b128 v[196:199], v177 offset:34816
	ds_read_b128 v[200:203], v177 offset:35840
	ds_read_b128 v[204:207], v177 offset:36864
	ds_read_b128 v[208:211], v177 offset:37888
	ds_read_b128 v[212:215], v177 offset:38912
	ds_read_b128 v[216:219], v177 offset:39936
	global_load_lds_dwordx4 v[164:165], off
	v_lshl_add_u64 v[164:165], s[68:69], 0, v[140:141]
	s_mov_b32 m0, s43
	s_nop 0
	global_load_lds_dwordx4 v[164:165], off
	s_waitcnt lgkmcnt(8)
	s_barrier
	s_waitcnt lgkmcnt(0)
	s_setprio 1
	s_waitcnt lgkmcnt(0)
	v_mfma_f32_16x16x128_f8f6f4 v[108:111], v[156:163], v[188:195], v[108:111]
	v_mfma_f32_16x16x128_f8f6f4 v[112:115], v[180:187], v[188:195], v[112:115]
	v_mfma_f32_16x16x128_f8f6f4 v[104:107], v[156:163], v[196:203], v[104:107]
	v_mfma_f32_16x16x128_f8f6f4 v[100:103], v[180:187], v[196:203], v[100:103]
	v_mfma_f32_16x16x128_f8f6f4 v[80:83], v[156:163], v[204:211], v[80:83]
	v_mfma_f32_16x16x128_f8f6f4 v[76:79], v[180:187], v[204:211], v[76:79]
	v_mfma_f32_16x16x128_f8f6f4 v[48:51], v[156:163], v[212:219], v[48:51]
	v_mfma_f32_16x16x128_f8f6f4 v[44:47], v[180:187], v[212:219], v[44:47]
	s_setprio 0
	s_barrier
	s_add_i32 s69, 0, 0x1c000
	s_add_i32 s68, s66, s39
	v_add_u32_e32 v155, s69, v174
	v_lshl_add_u64 v[132:133], v[132:133], 0, s[12:13]
	s_mov_b32 m0, s68
	s_add_i32 s66, s68, 0x2000
	ds_read_b128 v[224:227], v155
	ds_read_b128 v[228:231], v155 offset:1024
	ds_read_b128 v[232:235], v155 offset:2048
	ds_read_b128 v[236:239], v155 offset:3072
	global_load_lds_dwordx4 v[132:133], off
	v_lshl_add_u64 v[132:133], v[134:135], 0, s[12:13]
	s_mov_b32 m0, s66
	s_nop 0
	global_load_lds_dwordx4 v[132:133], off
	s_barrier
	s_waitcnt lgkmcnt(0)
	s_setprio 1
	s_waitcnt lgkmcnt(0)
	v_mfma_f32_16x16x128_f8f6f4 v[124:127], v[224:231], v[188:195], v[124:127]
	v_mfma_f32_16x16x128_f8f6f4 v[128:131], v[232:239], v[188:195], v[128:131]
	v_mfma_f32_16x16x128_f8f6f4 v[120:123], v[224:231], v[196:203], v[120:123]
	v_mfma_f32_16x16x128_f8f6f4 v[116:119], v[232:239], v[196:203], v[116:119]
	v_mfma_f32_16x16x128_f8f6f4 v[96:99], v[224:231], v[204:211], v[96:99]
	v_mfma_f32_16x16x128_f8f6f4 v[92:95], v[232:239], v[204:211], v[92:95]
	v_mfma_f32_16x16x128_f8f6f4 v[64:67], v[224:231], v[212:219], v[64:67]
	v_mfma_f32_16x16x128_f8f6f4 v[60:63], v[232:239], v[212:219], v[60:63]
	s_setprio 0
	s_mov_b32 m0, s46
	v_lshl_add_u64 v[132:133], v[150:151], 0, s[12:13]
	s_barrier
	ds_read_b128 v[188:191], v177 offset:49152
	ds_read_b128 v[192:195], v177 offset:50176
	ds_read_b128 v[196:199], v177 offset:51200
	ds_read_b128 v[200:203], v177 offset:52224
	ds_read_b128 v[204:207], v177 offset:53248
	ds_read_b128 v[208:211], v177 offset:54272
	ds_read_b128 v[212:215], v177 offset:55296
	ds_read_b128 v[216:219], v177 offset:56320
	global_load_lds_dwordx4 v[132:133], off
	v_lshl_add_u64 v[132:133], v[152:153], 0, s[12:13]
	s_mov_b32 m0, s47
	s_nop 0
	global_load_lds_dwordx4 v[132:133], off
	s_barrier
	s_waitcnt lgkmcnt(0)
	s_setprio 1
	s_waitcnt lgkmcnt(0)
	v_mfma_f32_16x16x128_f8f6f4 v[72:75], v[156:163], v[188:195], v[72:75]
	v_mfma_f32_16x16x128_f8f6f4 v[68:71], v[180:187], v[188:195], v[68:71]
	v_mfma_f32_16x16x128_f8f6f4 v[40:43], v[156:163], v[196:203], v[40:43]
	v_mfma_f32_16x16x128_f8f6f4 v[36:39], v[180:187], v[196:203], v[36:39]
	v_mfma_f32_16x16x128_f8f6f4 v[24:27], v[156:163], v[204:211], v[24:27]
	v_mfma_f32_16x16x128_f8f6f4 v[20:23], v[180:187], v[204:211], v[20:23]
	v_mfma_f32_16x16x128_f8f6f4 v[8:11], v[156:163], v[212:219], v[8:11]
	v_mfma_f32_16x16x128_f8f6f4 v[4:7], v[180:187], v[212:219], v[4:7]
	s_setprio 0
	s_barrier
	s_add_u32 s70, s26, 0x10180
	s_addc_u32 s71, s27, 0
	s_add_i32 s27, s69, s39
	v_lshl_add_u64 v[132:133], s[70:71], 0, v[138:139]
	s_mov_b32 m0, s27
	s_add_i32 s26, s27, 0x2000
	global_load_lds_dwordx4 v[132:133], off
	v_lshl_add_u64 v[132:133], s[70:71], 0, v[142:143]
	s_mov_b32 m0, s26
	s_nop 0
	global_load_lds_dwordx4 v[132:133], off
	s_waitcnt vmcnt(6)
	s_barrier
	s_setprio 1
	v_mfma_f32_16x16x128_f8f6f4 v[88:91], v[224:231], v[188:195], v[88:91]
	v_mfma_f32_16x16x128_f8f6f4 v[84:87], v[232:239], v[188:195], v[84:87]
	v_mfma_f32_16x16x128_f8f6f4 v[56:59], v[224:231], v[196:203], v[56:59]
	v_mfma_f32_16x16x128_f8f6f4 v[52:55], v[232:239], v[196:203], v[52:55]
	v_mfma_f32_16x16x128_f8f6f4 v[32:35], v[224:231], v[204:211], v[32:35]
	v_mfma_f32_16x16x128_f8f6f4 v[28:31], v[232:239], v[204:211], v[28:31]
	v_mfma_f32_16x16x128_f8f6f4 v[16:19], v[224:231], v[212:219], v[16:19]
	v_mfma_f32_16x16x128_f8f6f4 v[12:15], v[232:239], v[212:219], v[12:15]
	s_setprio 0
	s_barrier
	ds_read_b128 v[156:159], v176
	ds_read_b128 v[160:163], v176 offset:1024
	ds_read_b128 v[180:183], v176 offset:2048
	ds_read_b128 v[184:187], v176 offset:3072
	s_add_u32 s22, s22, 0x20180
	s_addc_u32 s23, s23, 0
	s_mov_b32 m0, s67
	v_lshl_add_u64 v[132:133], s[22:23], 0, v[136:137]
	ds_read_b128 v[188:191], v177
	ds_read_b128 v[192:195], v177 offset:1024
	ds_read_b128 v[196:199], v177 offset:2048
	ds_read_b128 v[200:203], v177 offset:3072
	ds_read_b128 v[204:207], v177 offset:4096
	ds_read_b128 v[208:211], v177 offset:5120
	ds_read_b128 v[212:215], v177 offset:6144
	ds_read_b128 v[216:219], v177 offset:7168
	global_load_lds_dwordx4 v[132:133], off
	v_lshl_add_u64 v[132:133], s[22:23], 0, v[140:141]
	s_mov_b32 m0, s61
	s_nop 0
	global_load_lds_dwordx4 v[132:133], off
	s_waitcnt lgkmcnt(8)
	s_barrier
	s_waitcnt lgkmcnt(0)
	s_setprio 1
	s_waitcnt lgkmcnt(0)
	v_mfma_f32_16x16x128_f8f6f4 v[108:111], v[156:163], v[188:195], v[108:111]
	v_mfma_f32_16x16x128_f8f6f4 v[112:115], v[180:187], v[188:195], v[112:115]
	v_mfma_f32_16x16x128_f8f6f4 v[104:107], v[156:163], v[196:203], v[104:107]
	v_mfma_f32_16x16x128_f8f6f4 v[100:103], v[180:187], v[196:203], v[100:103]
	v_mfma_f32_16x16x128_f8f6f4 v[80:83], v[156:163], v[204:211], v[80:83]
	v_mfma_f32_16x16x128_f8f6f4 v[76:79], v[180:187], v[204:211], v[76:79]
	v_mfma_f32_16x16x128_f8f6f4 v[48:51], v[156:163], v[212:219], v[48:51]
	v_mfma_f32_16x16x128_f8f6f4 v[44:47], v[180:187], v[212:219], v[44:47]
	s_setprio 0
	s_barrier
	s_mov_b32 m0, s64
	v_lshl_add_u64 v[132:133], s[2:3], 0, v[138:139]
	ds_read_b128 v[224:227], v178
	ds_read_b128 v[228:231], v178 offset:1024
	ds_read_b128 v[232:235], v178 offset:2048
	ds_read_b128 v[236:239], v178 offset:3072
	global_load_lds_dwordx4 v[132:133], off
	v_lshl_add_u64 v[134:135], s[2:3], 0, v[142:143]
	s_mov_b32 m0, s62
	s_nop 0
	global_load_lds_dwordx4 v[134:135], off
	s_barrier
	s_waitcnt lgkmcnt(0)
	s_setprio 1
	s_waitcnt lgkmcnt(0)
	v_mfma_f32_16x16x128_f8f6f4 v[124:127], v[224:231], v[188:195], v[124:127]
	v_mfma_f32_16x16x128_f8f6f4 v[128:131], v[232:239], v[188:195], v[128:131]
	v_mfma_f32_16x16x128_f8f6f4 v[120:123], v[224:231], v[196:203], v[120:123]
	v_mfma_f32_16x16x128_f8f6f4 v[116:119], v[232:239], v[196:203], v[116:119]
	v_mfma_f32_16x16x128_f8f6f4 v[96:99], v[224:231], v[204:211], v[96:99]
	v_mfma_f32_16x16x128_f8f6f4 v[92:95], v[232:239], v[204:211], v[92:95]
	v_mfma_f32_16x16x128_f8f6f4 v[64:67], v[224:231], v[212:219], v[64:67]
	v_mfma_f32_16x16x128_f8f6f4 v[60:63], v[232:239], v[212:219], v[60:63]
	s_setprio 0
	s_mov_b32 m0, s40
	v_lshl_add_u64 v[150:151], s[24:25], 0, v[136:137]
	s_barrier
	ds_read_b128 v[188:191], v177 offset:16384
	ds_read_b128 v[192:195], v177 offset:17408
	ds_read_b128 v[196:199], v177 offset:18432
	ds_read_b128 v[200:203], v177 offset:19456
	ds_read_b128 v[204:207], v177 offset:20480
	ds_read_b128 v[208:211], v177 offset:21504
	ds_read_b128 v[212:215], v177 offset:22528
	ds_read_b128 v[216:219], v177 offset:23552
	global_load_lds_dwordx4 v[150:151], off
	v_lshl_add_u64 v[152:153], s[24:25], 0, v[140:141]
	s_mov_b32 m0, s41
	s_nop 0
	global_load_lds_dwordx4 v[152:153], off
	s_barrier
	s_waitcnt lgkmcnt(0)
	s_setprio 1
	s_waitcnt lgkmcnt(0)
	v_mfma_f32_16x16x128_f8f6f4 v[72:75], v[156:163], v[188:195], v[72:75]
	v_mfma_f32_16x16x128_f8f6f4 v[68:71], v[180:187], v[188:195], v[68:71]
	v_mfma_f32_16x16x128_f8f6f4 v[40:43], v[156:163], v[196:203], v[40:43]
	v_mfma_f32_16x16x128_f8f6f4 v[36:39], v[180:187], v[196:203], v[36:39]
	v_mfma_f32_16x16x128_f8f6f4 v[24:27], v[156:163], v[204:211], v[24:27]
	v_mfma_f32_16x16x128_f8f6f4 v[20:23], v[180:187], v[204:211], v[20:23]
	v_mfma_f32_16x16x128_f8f6f4 v[8:11], v[156:163], v[212:219], v[8:11]
	v_mfma_f32_16x16x128_f8f6f4 v[4:7], v[180:187], v[212:219], v[4:7]
	s_setprio 0
	s_barrier
	s_add_u32 s22, s2, 0x10000
	s_addc_u32 s23, s3, 0
	s_mov_b32 m0, s65
	v_lshl_add_u64 v[156:157], s[22:23], 0, v[138:139]
	global_load_lds_dwordx4 v[156:157], off
	v_lshl_add_u64 v[156:157], s[22:23], 0, v[142:143]
	s_mov_b32 m0, s63
	s_nop 0
	global_load_lds_dwordx4 v[156:157], off
	s_waitcnt vmcnt(6)
	s_barrier
	s_setprio 1
	v_mfma_f32_16x16x128_f8f6f4 v[88:91], v[224:231], v[188:195], v[88:91]
	v_mfma_f32_16x16x128_f8f6f4 v[84:87], v[232:239], v[188:195], v[84:87]
	v_mfma_f32_16x16x128_f8f6f4 v[56:59], v[224:231], v[196:203], v[56:59]
	v_mfma_f32_16x16x128_f8f6f4 v[52:55], v[232:239], v[196:203], v[52:55]
	v_mfma_f32_16x16x128_f8f6f4 v[32:35], v[224:231], v[204:211], v[32:35]
	v_mfma_f32_16x16x128_f8f6f4 v[28:31], v[232:239], v[204:211], v[28:31]
	v_mfma_f32_16x16x128_f8f6f4 v[16:19], v[224:231], v[212:219], v[16:19]
	v_mfma_f32_16x16x128_f8f6f4 v[12:15], v[232:239], v[212:219], v[12:15]
	s_setprio 0
	s_barrier
	ds_read_b128 v[156:159], v154
	ds_read_b128 v[160:163], v154 offset:1024
	ds_read_b128 v[180:183], v154 offset:2048
	ds_read_b128 v[184:187], v154 offset:3072
	s_add_u32 s22, s24, 0x20000
	s_addc_u32 s23, s25, 0
	s_mov_b32 m0, s42
	v_lshl_add_u64 v[164:165], s[22:23], 0, v[136:137]
	ds_read_b128 v[188:191], v177 offset:32768
	ds_read_b128 v[192:195], v177 offset:33792
	ds_read_b128 v[196:199], v177 offset:34816
	ds_read_b128 v[200:203], v177 offset:35840
	ds_read_b128 v[204:207], v177 offset:36864
	ds_read_b128 v[208:211], v177 offset:37888
	ds_read_b128 v[212:215], v177 offset:38912
	ds_read_b128 v[216:219], v177 offset:39936
	global_load_lds_dwordx4 v[164:165], off
	v_lshl_add_u64 v[164:165], s[22:23], 0, v[140:141]
	s_mov_b32 m0, s43
	s_nop 0
	global_load_lds_dwordx4 v[164:165], off
	s_waitcnt lgkmcnt(8)
	s_barrier
	s_waitcnt lgkmcnt(0)
	s_setprio 1
	s_waitcnt lgkmcnt(0)
	v_mfma_f32_16x16x128_f8f6f4 v[108:111], v[156:163], v[188:195], v[108:111]
	v_mfma_f32_16x16x128_f8f6f4 v[112:115], v[180:187], v[188:195], v[112:115]
	v_mfma_f32_16x16x128_f8f6f4 v[104:107], v[156:163], v[196:203], v[104:107]
	v_mfma_f32_16x16x128_f8f6f4 v[100:103], v[180:187], v[196:203], v[100:103]
	v_mfma_f32_16x16x128_f8f6f4 v[80:83], v[156:163], v[204:211], v[80:83]
	v_mfma_f32_16x16x128_f8f6f4 v[76:79], v[180:187], v[204:211], v[76:79]
	v_mfma_f32_16x16x128_f8f6f4 v[48:51], v[156:163], v[212:219], v[48:51]
	v_mfma_f32_16x16x128_f8f6f4 v[44:47], v[180:187], v[212:219], v[44:47]
	s_setprio 0
	s_barrier
	s_mov_b32 m0, s68
	v_lshl_add_u64 v[132:133], v[132:133], 0, s[8:9]
	ds_read_b128 v[224:227], v155
	ds_read_b128 v[228:231], v155 offset:1024
	ds_read_b128 v[232:235], v155 offset:2048
	ds_read_b128 v[236:239], v155 offset:3072
	global_load_lds_dwordx4 v[132:133], off
	v_lshl_add_u64 v[132:133], v[134:135], 0, s[8:9]
	s_mov_b32 m0, s66
	s_nop 0
	global_load_lds_dwordx4 v[132:133], off
	s_barrier
	s_waitcnt lgkmcnt(0)
	s_setprio 1
	s_waitcnt lgkmcnt(0)
	v_mfma_f32_16x16x128_f8f6f4 v[124:127], v[224:231], v[188:195], v[124:127]
	v_mfma_f32_16x16x128_f8f6f4 v[128:131], v[232:239], v[188:195], v[128:131]
	v_mfma_f32_16x16x128_f8f6f4 v[120:123], v[224:231], v[196:203], v[120:123]
	v_mfma_f32_16x16x128_f8f6f4 v[116:119], v[232:239], v[196:203], v[116:119]
	v_mfma_f32_16x16x128_f8f6f4 v[96:99], v[224:231], v[204:211], v[96:99]
	v_mfma_f32_16x16x128_f8f6f4 v[92:95], v[232:239], v[204:211], v[92:95]
	v_mfma_f32_16x16x128_f8f6f4 v[64:67], v[224:231], v[212:219], v[64:67]
	v_mfma_f32_16x16x128_f8f6f4 v[60:63], v[232:239], v[212:219], v[60:63]
	s_setprio 0
	s_mov_b32 m0, s46
	v_lshl_add_u64 v[132:133], v[150:151], 0, s[8:9]
	s_barrier
	ds_read_b128 v[188:191], v177 offset:49152
	ds_read_b128 v[192:195], v177 offset:50176
	ds_read_b128 v[196:199], v177 offset:51200
	ds_read_b128 v[200:203], v177 offset:52224
	ds_read_b128 v[204:207], v177 offset:53248
	ds_read_b128 v[208:211], v177 offset:54272
	ds_read_b128 v[212:215], v177 offset:55296
	ds_read_b128 v[216:219], v177 offset:56320
	global_load_lds_dwordx4 v[132:133], off
	v_lshl_add_u64 v[132:133], v[152:153], 0, s[8:9]
	s_mov_b32 m0, s47
	s_nop 0
	global_load_lds_dwordx4 v[132:133], off
	s_barrier
	s_waitcnt lgkmcnt(0)
	s_setprio 1
	s_waitcnt lgkmcnt(0)
	v_mfma_f32_16x16x128_f8f6f4 v[72:75], v[156:163], v[188:195], v[72:75]
	v_mfma_f32_16x16x128_f8f6f4 v[68:71], v[180:187], v[188:195], v[68:71]
	v_mfma_f32_16x16x128_f8f6f4 v[40:43], v[156:163], v[196:203], v[40:43]
	v_mfma_f32_16x16x128_f8f6f4 v[36:39], v[180:187], v[196:203], v[36:39]
	v_mfma_f32_16x16x128_f8f6f4 v[24:27], v[156:163], v[204:211], v[24:27]
	v_mfma_f32_16x16x128_f8f6f4 v[20:23], v[180:187], v[204:211], v[20:23]
	v_mfma_f32_16x16x128_f8f6f4 v[8:11], v[156:163], v[212:219], v[8:11]
	v_mfma_f32_16x16x128_f8f6f4 v[4:7], v[180:187], v[212:219], v[4:7]
	s_setprio 0
	s_barrier
	s_add_u32 s2, s2, 0x10080
	s_addc_u32 s3, s3, 0
	s_mov_b32 m0, s27
	v_lshl_add_u64 v[132:133], s[2:3], 0, v[138:139]
	global_load_lds_dwordx4 v[132:133], off
	v_lshl_add_u64 v[132:133], s[2:3], 0, v[142:143]
	s_mov_b32 m0, s26
	s_nop 0
	global_load_lds_dwordx4 v[132:133], off
	s_waitcnt vmcnt(6)
	s_barrier
	s_setprio 1
	v_mfma_f32_16x16x128_f8f6f4 v[88:91], v[224:231], v[188:195], v[88:91]
	v_mfma_f32_16x16x128_f8f6f4 v[84:87], v[232:239], v[188:195], v[84:87]
	v_mfma_f32_16x16x128_f8f6f4 v[56:59], v[224:231], v[196:203], v[56:59]
	v_mfma_f32_16x16x128_f8f6f4 v[52:55], v[232:239], v[196:203], v[52:55]
	v_mfma_f32_16x16x128_f8f6f4 v[32:35], v[224:231], v[204:211], v[32:35]
	v_mfma_f32_16x16x128_f8f6f4 v[28:31], v[232:239], v[204:211], v[28:31]
	v_mfma_f32_16x16x128_f8f6f4 v[16:19], v[224:231], v[212:219], v[16:19]
	v_mfma_f32_16x16x128_f8f6f4 v[12:15], v[232:239], v[212:219], v[12:15]
	s_setprio 0
	v_lshl_add_u32 v164, s60, 8, v173
	s_cmp_lt_i32 s59, 6
	s_cselect_b32 s2, 0, 32
	v_or_b32_e32 v162, 16, v164
	s_cselect_b32 s24, s52, 0x47b1c000
	s_cselect_b32 s22, s53, 0x800
	s_cselect_b32 s23, 0, -6
	s_add_u32 s2, s44, s2
	v_ashrrev_i32_e32 v165, 31, v164
	v_ashrrev_i32_e32 v163, 31, v162
	s_addc_u32 s3, s45, 0
	v_lshlrev_b64 v[132:133], 6, v[164:165]
	v_lshlrev_b64 v[150:151], 6, v[162:163]
	s_barrier
	s_nop 7
	s_nop 7
	s_nop 7
	v_lshl_add_u64 v[132:133], s[2:3], 0, v[132:133]
	v_lshl_add_u64 v[150:151], s[2:3], 0, v[150:151]
	global_load_dwordx4 v[180:183], v[132:133], off
	s_nop 0
	global_load_dwordx4 v[132:135], v[132:133], off offset:16
	s_nop 0
	global_load_dwordx4 v[184:187], v[150:151], off
	global_load_dwordx4 v[188:191], v[150:151], off offset:16
	v_or_b32_e32 v160, 32, v164
	v_ashrrev_i32_e32 v161, 31, v160
	v_lshlrev_b64 v[150:151], 6, v[160:161]
	v_or_b32_e32 v158, 48, v164
	v_lshl_add_u64 v[150:151], s[2:3], 0, v[150:151]
	v_ashrrev_i32_e32 v159, 31, v158
	global_load_dwordx4 v[192:195], v[150:151], off
	global_load_dwordx4 v[196:199], v[150:151], off offset:16
	v_lshlrev_b64 v[150:151], 6, v[158:159]
	v_lshl_add_u64 v[150:151], s[2:3], 0, v[150:151]
	global_load_dwordx4 v[200:203], v[150:151], off
	global_load_dwordx4 v[204:207], v[150:151], off offset:16
	v_add_u32_e32 v156, 0x80, v164
	v_add_u32_e32 v150, 0xb0, v164
	v_add_u32_e32 v154, 0x90, v164
	v_add_u32_e32 v152, 0xa0, v164
	v_ashrrev_i32_e32 v157, 31, v156
	v_ashrrev_i32_e32 v151, 31, v150
	v_ashrrev_i32_e32 v155, 31, v154
	v_ashrrev_i32_e32 v153, 31, v152
	v_lshlrev_b64 v[208:209], 6, v[156:157]
	v_lshlrev_b64 v[214:215], 6, v[150:151]
	v_lshlrev_b64 v[210:211], 6, v[154:155]
	v_lshlrev_b64 v[212:213], 6, v[152:153]
	v_lshl_add_u64 v[216:217], s[2:3], 0, v[208:209]
	v_lshl_add_u64 v[240:241], s[2:3], 0, v[214:215]
	v_lshl_add_u64 v[220:221], s[2:3], 0, v[210:211]
	v_lshl_add_u64 v[222:223], s[2:3], 0, v[212:213]
	global_load_dwordx4 v[208:211], v[216:217], off
	global_load_dwordx4 v[212:215], v[216:217], off offset:16
	s_nop 0
	global_load_dwordx4 v[216:219], v[220:221], off
	global_load_dwordx4 v[224:227], v[220:221], off offset:16
	global_load_dwordx4 v[228:231], v[222:223], off
	global_load_dwordx4 v[232:235], v[222:223], off offset:16
	global_load_dwordx4 v[236:239], v[240:241], off
	s_nop 0
	global_load_dwordx4 v[240:243], v[240:241], off offset:16
	s_mov_b32 s60, s56
	s_mov_b64 s[26:27], s[20:21]
	s_waitcnt vmcnt(0)
	v_mov_b32_e32 v220, v180
	v_mov_b32_e32 v221, v132
	v_mov_b32_e32 v132, v181
	v_mov_b32_e32 v180, v182
	v_mov_b32_e32 v181, v134
	v_mov_b32_e32 v134, v183
	v_mov_b32_e32 v182, v184
	v_mov_b32_e32 v183, v188
	v_mov_b32_e32 v188, v185
	v_mov_b32_e32 v184, v186
	v_mov_b32_e32 v185, v190
	v_mov_b32_e32 v190, v187
	v_pk_add_f32 v[132:133], v[220:221], v[132:133]
	v_pk_add_f32 v[134:135], v[180:181], v[134:135]
	v_pk_add_f32 v[180:181], v[182:183], v[188:189]
	v_pk_add_f32 v[182:183], v[184:185], v[190:191]
	v_pk_add_f32 v[132:133], v[132:133], v[134:135]
	v_pk_add_f32 v[134:135], v[180:181], v[182:183]
	v_mov_b32_e32 v181, v132
	v_mov_b32_e32 v180, v134
	v_mov_b32_e32 v132, v135
	v_pk_add_f32 v[132:133], v[180:181], v[132:133]
	v_mov_b32_e32 v186, v192
	v_pk_fma_f32 v[132:133], v[132:133], s[16:17], v[148:149] op_sel_hi:[1,0,0]
	v_mov_b32_e32 v187, v196
	v_mul_f32_e32 v134, 0x4b800000, v133
	v_mul_f32_e32 v135, 0x4b800000, v132
	v_cmp_gt_f32_e32 vcc, s54, v133
	v_cmp_gt_f32_e64 s[2:3], s54, v132
	v_mov_b32_e32 v196, v193
	v_cndmask_b32_e32 v133, v133, v134, vcc
	v_cndmask_b32_e64 v132, v132, v135, s[2:3]
	v_rsq_f32_e32 v134, v133
	v_rsq_f32_e32 v135, v132
	v_mov_b32_e32 v192, v194
	v_mov_b32_e32 v193, v198
	v_mul_f32_e32 v151, 0x45800000, v134
	v_mul_f32_e32 v153, 0x45800000, v135
	v_cndmask_b32_e32 v134, v134, v151, vcc
	v_cndmask_b32_e64 v135, v135, v153, s[2:3]
	v_mov_b32_e32 v198, v195
	v_pk_add_f32 v[132:133], v[186:187], v[196:197]
	v_mul_f32_e32 v180, 0x3c800000, v134
	v_mul_f32_e32 v182, 0x3c800000, v135
	v_pk_add_f32 v[134:135], v[192:193], v[198:199]
	v_mov_b32_e32 v184, v202
	v_pk_add_f32 v[132:133], v[132:133], v[134:135]
	v_mov_b32_e32 v134, v200
	v_mov_b32_e32 v135, v204
	v_mov_b32_e32 v204, v201
	v_mov_b32_e32 v185, v206
	v_mov_b32_e32 v206, v203
	v_pk_add_f32 v[134:135], v[134:135], v[204:205]
	v_pk_add_f32 v[184:185], v[184:185], v[206:207]
	v_mov_b32_e32 v186, v218
	v_pk_add_f32 v[134:135], v[134:135], v[184:185]
	v_mov_b32_e32 v185, v132
	v_mov_b32_e32 v184, v134
	v_mov_b32_e32 v132, v135
	v_pk_add_f32 v[132:133], v[184:185], v[132:133]
	v_mov_b32_e32 v135, v214
	v_pk_fma_f32 v[132:133], v[132:133], s[16:17], v[148:149] op_sel_hi:[1,0,0]
	v_mov_b32_e32 v214, v211
	v_mul_f32_e32 v134, 0x4b800000, v133
	v_cmp_gt_f32_e32 vcc, s54, v133
	v_cmp_gt_f32_e64 s[2:3], s54, v132
	v_mov_b32_e32 v187, v226
	v_cndmask_b32_e32 v133, v133, v134, vcc
	v_rsq_f32_e32 v133, v133
	v_mul_f32_e32 v134, 0x4b800000, v132
	v_cndmask_b32_e64 v132, v132, v134, s[2:3]
	v_rsq_f32_e32 v132, v132
	v_mul_f32_e32 v134, 0x45800000, v133
	v_cndmask_b32_e32 v133, v133, v134, vcc
	v_mul_f32_e32 v184, 0x3c800000, v133
	v_mul_f32_e32 v133, 0x45800000, v132
	v_cndmask_b32_e64 v132, v132, v133, s[2:3]
	v_mul_f32_e32 v172, 0x3c800000, v132
	v_mov_b32_e32 v132, v208
	v_mov_b32_e32 v133, v212
	v_mov_b32_e32 v212, v209
	v_mov_b32_e32 v134, v210
	v_pk_add_f32 v[132:133], v[132:133], v[212:213]
	v_pk_add_f32 v[134:135], v[134:135], v[214:215]
	v_mov_b32_e32 v226, v219
	v_pk_add_f32 v[132:133], v[132:133], v[134:135]
	v_mov_b32_e32 v134, v216
	v_mov_b32_e32 v135, v224
	v_mov_b32_e32 v224, v217
	v_pk_add_f32 v[134:135], v[134:135], v[224:225]
	v_pk_add_f32 v[186:187], v[186:187], v[226:227]
	v_pk_mul_f32 v[108:109], v[108:109], v[180:181] op_sel_hi:[1,0]
	v_pk_add_f32 v[134:135], v[134:135], v[186:187]
	v_mov_b32_e32 v187, v132
	v_mov_b32_e32 v186, v134
	v_mov_b32_e32 v132, v135
	v_pk_add_f32 v[132:133], v[186:187], v[132:133]
	v_mov_b32_e32 v135, v234
	v_pk_fma_f32 v[132:133], v[132:133], s[16:17], v[148:149] op_sel_hi:[1,0,0]
	v_mov_b32_e32 v234, v231
	v_mul_f32_e32 v134, 0x4b800000, v133
	v_cmp_gt_f32_e32 vcc, s54, v133
	v_cmp_gt_f32_e64 s[2:3], s54, v132
	v_mov_b32_e32 v186, v238
	v_cndmask_b32_e32 v133, v133, v134, vcc
	v_rsq_f32_e32 v133, v133
	v_mul_f32_e32 v134, 0x4b800000, v132
	v_cndmask_b32_e64 v132, v132, v134, s[2:3]
	v_rsq_f32_e32 v132, v132
	v_mul_f32_e32 v134, 0x45800000, v133
	v_cndmask_b32_e32 v133, v133, v134, vcc
	v_mul_f32_e32 v170, 0x3c800000, v133
	v_mul_f32_e32 v133, 0x45800000, v132
	v_cndmask_b32_e64 v132, v132, v133, s[2:3]
	v_mul_f32_e32 v168, 0x3c800000, v132
	v_mov_b32_e32 v132, v228
	v_mov_b32_e32 v133, v232
	v_mov_b32_e32 v232, v229
	v_mov_b32_e32 v134, v230
	v_pk_add_f32 v[132:133], v[132:133], v[232:233]
	v_pk_add_f32 v[134:135], v[134:135], v[234:235]
	v_mov_b32_e32 v187, v242
	v_pk_add_f32 v[132:133], v[132:133], v[134:135]
	v_mov_b32_e32 v134, v236
	v_mov_b32_e32 v135, v240
	v_mov_b32_e32 v240, v237
	v_mov_b32_e32 v242, v239
	v_pk_add_f32 v[134:135], v[134:135], v[240:241]
	v_pk_add_f32 v[186:187], v[186:187], v[242:243]
	v_pk_mul_f32 v[110:111], v[110:111], v[180:181] op_sel_hi:[1,0]
	v_pk_add_f32 v[134:135], v[134:135], v[186:187]
	v_mov_b32_e32 v187, v132
	v_mov_b32_e32 v186, v134
	v_mov_b32_e32 v132, v135
	v_pk_add_f32 v[132:133], v[186:187], v[132:133]
	v_cvt_pk_bf16_f32 v108, v108, v109
	v_cvt_pk_bf16_f32 v109, v110, v111
	v_pk_mul_f32 v[114:115], v[114:115], v[180:181] op_sel_hi:[1,0]
	v_pk_fma_f32 v[132:133], v[132:133], s[16:17], v[148:149] op_sel_hi:[1,0,0]
	v_pk_mul_f32 v[112:113], v[112:113], v[180:181] op_sel_hi:[1,0]
	v_mul_f32_e32 v134, 0x4b800000, v133
	v_cmp_gt_f32_e32 vcc, s54, v133
	v_cmp_gt_f32_e64 s[2:3], s54, v132
	v_cvt_pk_bf16_f32 v110, v112, v113
	v_cvt_pk_bf16_f32 v111, v114, v115
	v_pk_mul_f32 v[112:113], v[130:131], v[180:181] op_sel_hi:[1,0]
	v_cndmask_b32_e32 v133, v133, v134, vcc
	v_rsq_f32_e32 v133, v133
	v_mul_f32_e32 v134, 0x4b800000, v132
	v_cndmask_b32_e64 v132, v132, v134, s[2:3]
	v_rsq_f32_e32 v132, v132
	v_mul_f32_e32 v134, 0x45800000, v133
	v_cndmask_b32_e32 v133, v133, v134, vcc
	v_mul_f32_e32 v166, 0x3c800000, v133
	v_mul_f32_e32 v133, 0x45800000, v132
	v_cndmask_b32_e64 v132, v132, v133, s[2:3]
	s_add_u32 s2, s4, s24
	s_addc_u32 s3, s5, 0
	s_add_i32 s23, s23, s59
	v_lshl_or_b32 v134, s23, 8, v175
	v_ashrrev_i32_e32 v135, 31, v134
	v_lshl_add_u64 v[134:135], v[134:135], 1, s[2:3]
	v_mad_i64_i32 v[164:165], s[2:3], s22, v164, 0
	v_lshl_add_u64 v[164:165], v[164:165], 1, v[134:135]
	global_store_dwordx4 v[164:165], v[108:111], off
	v_pk_mul_f32 v[114:115], v[128:129], v[180:181] op_sel_hi:[1,0]
	v_pk_mul_f32 v[106:107], v[106:107], v[182:183] op_sel_hi:[1,0]
	v_pk_mul_f32 v[108:109], v[124:125], v[180:181] op_sel_hi:[1,0]
	v_pk_mul_f32 v[110:111], v[126:127], v[180:181] op_sel_hi:[1,0]
	v_cvt_pk_bf16_f32 v108, v108, v109
	v_pk_mul_f32 v[104:105], v[104:105], v[182:183] op_sel_hi:[1,0]
	v_cvt_pk_bf16_f32 v109, v110, v111
	v_cvt_pk_bf16_f32 v110, v114, v115
	v_cvt_pk_bf16_f32 v111, v112, v113
	global_store_dwordx4 v[164:165], v[108:111], off offset:256
	v_pk_mul_f32 v[82:83], v[82:83], v[184:185] op_sel_hi:[1,0]
	v_pk_mul_f32 v[80:81], v[80:81], v[184:185] op_sel_hi:[1,0]
	v_mad_i64_i32 v[108:109], s[2:3], s22, v162, 0
	v_lshl_add_u64 v[108:109], v[108:109], 1, v[134:135]
	v_pk_mul_f32 v[110:111], v[102:103], v[182:183] op_sel_hi:[1,0]
	v_pk_mul_f32 v[102:103], v[100:101], v[182:183] op_sel_hi:[1,0]
	v_cvt_pk_bf16_f32 v100, v104, v105
	v_cvt_pk_bf16_f32 v101, v106, v107
	v_pk_mul_f32 v[104:105], v[118:119], v[182:183] op_sel_hi:[1,0]
	v_cvt_pk_bf16_f32 v102, v102, v103
	v_cvt_pk_bf16_f32 v103, v110, v111
	global_store_dwordx4 v[108:109], v[100:103], off
	v_pk_mul_f32 v[106:107], v[116:117], v[182:183] op_sel_hi:[1,0]
	v_pk_mul_f32 v[50:51], v[50:51], v[172:173] op_sel_hi:[1,0]
	v_pk_mul_f32 v[100:101], v[120:121], v[182:183] op_sel_hi:[1,0]
	v_pk_mul_f32 v[102:103], v[122:123], v[182:183] op_sel_hi:[1,0]
	v_cvt_pk_bf16_f32 v100, v100, v101
	v_pk_mul_f32 v[48:49], v[48:49], v[172:173] op_sel_hi:[1,0]
	v_cvt_pk_bf16_f32 v101, v102, v103
	v_cvt_pk_bf16_f32 v102, v106, v107
	v_cvt_pk_bf16_f32 v103, v104, v105
	global_store_dwordx4 v[108:109], v[100:103], off offset:256
	v_pk_mul_f32 v[42:43], v[42:43], v[168:169] op_sel_hi:[1,0]
	v_pk_mul_f32 v[40:41], v[40:41], v[168:169] op_sel_hi:[1,0]
	v_mad_i64_i32 v[100:101], s[2:3], s22, v160, 0
	v_lshl_add_u64 v[100:101], v[100:101], 1, v[134:135]
	v_pk_mul_f32 v[102:103], v[78:79], v[184:185] op_sel_hi:[1,0]
	v_pk_mul_f32 v[78:79], v[76:77], v[184:185] op_sel_hi:[1,0]
	v_cvt_pk_bf16_f32 v76, v80, v81
	v_cvt_pk_bf16_f32 v77, v82, v83
	v_pk_mul_f32 v[80:81], v[94:95], v[184:185] op_sel_hi:[1,0]
	v_cvt_pk_bf16_f32 v78, v78, v79
	v_cvt_pk_bf16_f32 v79, v102, v103
	global_store_dwordx4 v[100:101], v[76:79], off
	v_pk_mul_f32 v[82:83], v[92:93], v[184:185] op_sel_hi:[1,0]
	v_pk_mul_f32 v[26:27], v[26:27], v[166:167] op_sel_hi:[1,0]
	v_pk_mul_f32 v[76:77], v[96:97], v[184:185] op_sel_hi:[1,0]
	v_pk_mul_f32 v[78:79], v[98:99], v[184:185] op_sel_hi:[1,0]
	v_cvt_pk_bf16_f32 v76, v76, v77
	v_pk_mul_f32 v[24:25], v[24:25], v[166:167] op_sel_hi:[1,0]
	v_cvt_pk_bf16_f32 v77, v78, v79
	v_cvt_pk_bf16_f32 v78, v82, v83
	v_cvt_pk_bf16_f32 v79, v80, v81
	global_store_dwordx4 v[100:101], v[76:79], off offset:256
	v_mul_f32_e32 v132, 0x3c800000, v132
	v_pk_mul_f32 v[10:11], v[10:11], v[132:133] op_sel_hi:[1,0]
	v_mad_i64_i32 v[76:77], s[2:3], s22, v158, 0
	v_lshl_add_u64 v[76:77], v[76:77], 1, v[134:135]
	v_pk_mul_f32 v[78:79], v[46:47], v[172:173] op_sel_hi:[1,0]
	v_pk_mul_f32 v[46:47], v[44:45], v[172:173] op_sel_hi:[1,0]
	v_cvt_pk_bf16_f32 v44, v48, v49
	v_cvt_pk_bf16_f32 v45, v50, v51
	v_pk_mul_f32 v[48:49], v[62:63], v[172:173] op_sel_hi:[1,0]
	v_cvt_pk_bf16_f32 v46, v46, v47
	v_cvt_pk_bf16_f32 v47, v78, v79
	global_store_dwordx4 v[76:77], v[44:47], off
	v_pk_mul_f32 v[50:51], v[60:61], v[172:173] op_sel_hi:[1,0]
	v_pk_mul_f32 v[60:61], v[68:69], v[170:171] op_sel_hi:[1,0]
	v_pk_mul_f32 v[44:45], v[64:65], v[172:173] op_sel_hi:[1,0]
	v_pk_mul_f32 v[46:47], v[66:67], v[172:173] op_sel_hi:[1,0]
	v_cvt_pk_bf16_f32 v44, v44, v45
	v_pk_mul_f32 v[8:9], v[8:9], v[132:133] op_sel_hi:[1,0]
	v_cvt_pk_bf16_f32 v45, v46, v47
	v_cvt_pk_bf16_f32 v46, v50, v51
	v_cvt_pk_bf16_f32 v47, v48, v49
	global_store_dwordx4 v[76:77], v[44:47], off offset:256
	v_pk_mul_f32 v[50:51], v[70:71], v[170:171] op_sel_hi:[1,0]
	s_add_i32 s49, s49, s17
	v_mad_i64_i32 v[44:45], s[2:3], s22, v156, 0
	v_lshl_add_u64 v[48:49], v[44:45], 1, v[134:135]
	v_pk_mul_f32 v[46:47], v[74:75], v[170:171] op_sel_hi:[1,0]
	v_pk_mul_f32 v[44:45], v[72:73], v[170:171] op_sel_hi:[1,0]
	s_andn2_b64 vcc, exec, s[0:1]
	v_cvt_pk_bf16_f32 v44, v44, v45
	v_cvt_pk_bf16_f32 v45, v46, v47
	v_cvt_pk_bf16_f32 v46, v60, v61
	v_cvt_pk_bf16_f32 v47, v50, v51
	global_store_dwordx4 v[48:49], v[44:47], off
	v_pk_mul_f32 v[50:51], v[86:87], v[170:171] op_sel_hi:[1,0]
	v_pk_mul_f32 v[60:61], v[84:85], v[170:171] op_sel_hi:[1,0]
	v_pk_mul_f32 v[46:47], v[90:91], v[170:171] op_sel_hi:[1,0]
	v_pk_mul_f32 v[44:45], v[88:89], v[170:171] op_sel_hi:[1,0]
	s_mov_b32 s59, s55
	v_cvt_pk_bf16_f32 v44, v44, v45
	v_cvt_pk_bf16_f32 v45, v46, v47
	v_cvt_pk_bf16_f32 v46, v60, v61
	v_cvt_pk_bf16_f32 v47, v50, v51
	global_store_dwordx4 v[48:49], v[44:47], off offset:256
	s_nop 1
	v_mad_i64_i32 v[44:45], s[2:3], s22, v154, 0
	v_pk_mul_f32 v[46:47], v[38:39], v[168:169] op_sel_hi:[1,0]
	v_pk_mul_f32 v[38:39], v[36:37], v[168:169] op_sel_hi:[1,0]
	v_lshl_add_u64 v[44:45], v[44:45], 1, v[134:135]
	v_cvt_pk_bf16_f32 v36, v40, v41
	v_cvt_pk_bf16_f32 v37, v42, v43
	v_cvt_pk_bf16_f32 v38, v38, v39
	v_cvt_pk_bf16_f32 v39, v46, v47
	global_store_dwordx4 v[44:45], v[36:39], off
	v_pk_mul_f32 v[40:41], v[54:55], v[168:169] op_sel_hi:[1,0]
	v_pk_mul_f32 v[42:43], v[52:53], v[168:169] op_sel_hi:[1,0]
	v_pk_mul_f32 v[38:39], v[58:59], v[168:169] op_sel_hi:[1,0]
	v_pk_mul_f32 v[36:37], v[56:57], v[168:169] op_sel_hi:[1,0]
	s_nop 0
	v_cvt_pk_bf16_f32 v36, v36, v37
	v_cvt_pk_bf16_f32 v37, v38, v39
	v_cvt_pk_bf16_f32 v38, v42, v43
	v_cvt_pk_bf16_f32 v39, v40, v41
	global_store_dwordx4 v[44:45], v[36:39], off offset:256
	s_nop 1
	v_mad_i64_i32 v[36:37], s[2:3], s22, v152, 0
	v_pk_mul_f32 v[38:39], v[22:23], v[166:167] op_sel_hi:[1,0]
	v_pk_mul_f32 v[22:23], v[20:21], v[166:167] op_sel_hi:[1,0]
	v_lshl_add_u64 v[36:37], v[36:37], 1, v[134:135]
	v_cvt_pk_bf16_f32 v20, v24, v25
	v_cvt_pk_bf16_f32 v21, v26, v27
	v_cvt_pk_bf16_f32 v22, v22, v23
	v_cvt_pk_bf16_f32 v23, v38, v39
	global_store_dwordx4 v[36:37], v[20:23], off
	v_pk_mul_f32 v[24:25], v[30:31], v[166:167] op_sel_hi:[1,0]
	v_pk_mul_f32 v[26:27], v[28:29], v[166:167] op_sel_hi:[1,0]
	v_pk_mul_f32 v[22:23], v[34:35], v[166:167] op_sel_hi:[1,0]
	v_pk_mul_f32 v[20:21], v[32:33], v[166:167] op_sel_hi:[1,0]
	s_nop 0
	v_cvt_pk_bf16_f32 v20, v20, v21
	v_cvt_pk_bf16_f32 v21, v22, v23
	v_cvt_pk_bf16_f32 v22, v26, v27
	v_cvt_pk_bf16_f32 v23, v24, v25
	global_store_dwordx4 v[36:37], v[20:23], off offset:256
	s_nop 1
	v_mad_i64_i32 v[20:21], s[2:3], s22, v150, 0
	v_pk_mul_f32 v[22:23], v[6:7], v[132:133] op_sel_hi:[1,0]
	v_pk_mul_f32 v[6:7], v[4:5], v[132:133] op_sel_hi:[1,0]
	v_lshl_add_u64 v[20:21], v[20:21], 1, v[134:135]
	v_cvt_pk_bf16_f32 v4, v8, v9
	v_cvt_pk_bf16_f32 v5, v10, v11
	v_cvt_pk_bf16_f32 v6, v6, v7
	v_cvt_pk_bf16_f32 v7, v22, v23
	global_store_dwordx4 v[20:21], v[4:7], off
	s_mov_b64 s[22:23], s[18:19]
	v_pk_mul_f32 v[8:9], v[14:15], v[132:133] op_sel_hi:[1,0]
	v_pk_mul_f32 v[6:7], v[18:19], v[132:133] op_sel_hi:[1,0]
	v_pk_mul_f32 v[4:5], v[16:17], v[132:133] op_sel_hi:[1,0]
	v_pk_mul_f32 v[10:11], v[12:13], v[132:133] op_sel_hi:[1,0]
	v_cvt_pk_bf16_f32 v4, v4, v5
	v_cvt_pk_bf16_f32 v5, v6, v7
	s_nop 0
	v_cvt_pk_bf16_f32 v6, v10, v11
	v_cvt_pk_bf16_f32 v7, v8, v9
	global_store_dwordx4 v[20:21], v[4:7], off offset:256
	s_cbranch_vccz .LBB0_1686

.LBB0_1862:
	s_or_b64 exec, exec, s[0:1]
	v_exp_f32_e32 v140, v100
	v_exp_f32_e32 v101, v101
	v_exp_f32_e32 v141, v102
	v_exp_f32_e32 v142, v103
	v_exp_f32_e32 v102, v128
	v_exp_f32_e32 v103, v129
	v_exp_f32_e32 v128, v130
	v_exp_f32_e32 v129, v131
	v_exp_f32_e32 v130, v132
	v_exp_f32_e32 v131, v133
	v_exp_f32_e32 v132, v134
	v_exp_f32_e32 v133, v135
	v_exp_f32_e32 v134, v136
	v_exp_f32_e32 v135, v137
	v_mov_b32_e32 v100, v187
	v_cvt_pk_fp8_f32 v100, v140, v101
	v_mov_b32_e32 v101, v187
	v_cvt_pk_fp8_f32 v101, v102, v103
	v_mov_b32_e32 v102, v187
	v_mov_b32_e32 v103, v187
	v_exp_f32_e32 v136, v138
	v_exp_f32_e32 v137, v139
	v_cvt_pk_fp8_f32 v102, v130, v131
	v_cvt_pk_fp8_f32 v103, v134, v135
	v_cvt_pk_fp8_f32 v100, v141, v142 op_sel:[0,0,1]
	v_cvt_pk_fp8_f32 v101, v128, v129 op_sel:[0,0,1]
	v_cvt_pk_fp8_f32 v102, v132, v133 op_sel:[0,0,1]
	v_cvt_pk_fp8_f32 v103, v136, v137 op_sel:[0,0,1]
	s_lshl_b32 s0, s72, 7
	s_add_u32 s0, s54, s0
	v_mfma_f32_32x32x64_f8f6f4 v[64:79], v[96:103], v[112:119], v[64:79]
	v_mov_b32_e32 v189, v187
	s_addc_u32 s1, s55, 0
	s_waitcnt lgkmcnt(0)
	s_add_i32 s69, s69, s42
	s_cmpk_gt_i32 s69, 0xff
	s_nop 15
	v_rcp_f32_e32 v64, v64
	v_mfma_f32_32x32x64_f8f6f4 v[48:63], v[96:103], v[120:127], v[48:63]
	v_mul_f32_e32 v64, 0x41800000, v64
	v_mfma_f32_32x32x64_f8f6f4 v[32:47], v[96:103], v[104:111], v[32:47]
	s_nop 15
	s_nop 1
	v_mul_f32_e32 v48, v48, v64
	v_med3_f32 v48, v48, s67, v205
	v_mfma_f32_32x32x64_f8f6f4 v[16:31], v[96:103], v[88:95], v[16:31]
	v_mul_f32_e32 v32, v32, v64
	v_med3_f32 v32, v32, s67, v205
	v_mov_b32_e32 v92, v187
	v_cvt_pk_fp8_f32 v92, v48, v32
	v_or_b32_e32 v90, s73, v186
	v_ashrrev_i32_e32 v91, 31, v90
	v_lshl_add_u64 v[88:89], s[0:1], 0, v[188:189]
	s_nop 12
	v_mul_f32_e32 v16, v16, v64
	v_mfma_f32_32x32x64_f8f6f4 v[0:15], v[96:103], v[80:87], v[0:15]
	v_med3_f32 v16, v16, s67, v205
	v_lshlrev_b64 v[80:81], 11, v[90:91]
	v_lshl_add_u64 v[80:81], v[88:89], 0, v[80:81]
	s_nop 15
	s_nop 0
	v_mul_f32_e32 v0, v0, v64
	v_med3_f32 v0, v0, s67, v205
	v_cvt_pk_fp8_f32 v92, v16, v0 op_sel:[0,0,1]
	global_store_byte v[80:81], v92, off
	v_lshrrev_b32_e32 v0, 8, v92
	global_store_byte v[80:81], v0, off offset:32
	v_rcp_f32_e32 v0, v65
	v_lshrrev_b32_e32 v16, 24, v92
	global_store_byte v[80:81], v16, off offset:96
	global_store_byte_d16_hi v[80:81], v92, off offset:64
	v_mul_f32_e32 v16, 0x41800000, v0
	v_mul_f32_e32 v48, v49, v16
	v_mul_f32_e32 v33, v33, v16
	v_med3_f32 v48, v48, s67, v205
	v_med3_f32 v33, v33, s67, v205
	v_mov_b32_e32 v49, v187
	v_cvt_pk_fp8_f32 v49, v48, v33
	v_mul_f32_e32 v17, v17, v16
	v_mul_f32_e32 v1, v1, v16
	v_or_b32_e32 v0, s70, v186
	v_med3_f32 v16, v17, s67, v205
	v_med3_f32 v1, v1, s67, v205
	v_add_u32_e32 v32, s71, v0
	v_cvt_pk_fp8_f32 v49, v16, v1 op_sel:[0,0,1]
	v_add_u32_e32 v0, 1, v32
	v_ashrrev_i32_e32 v1, 31, v0
	v_lshlrev_b64 v[0:1], 11, v[0:1]
	v_lshl_add_u64 v[0:1], v[88:89], 0, v[0:1]
	v_lshrrev_b32_e32 v16, 8, v49
	global_store_byte v[0:1], v16, off offset:32
	v_rcp_f32_e32 v16, v66
	v_lshrrev_b32_e32 v17, 24, v49
	global_store_byte v[0:1], v49, off
	global_store_byte_d16_hi v[0:1], v49, off offset:64
	global_store_byte v[0:1], v17, off offset:96
	v_mul_f32_e32 v1, 0x41800000, v16
	v_mul_f32_e32 v16, v50, v1
	v_mul_f32_e32 v17, v34, v1
	v_med3_f32 v16, v16, s67, v205
	v_med3_f32 v17, v17, s67, v205
	v_mov_b32_e32 v33, v187
	v_cvt_pk_fp8_f32 v33, v16, v17
	v_mul_f32_e32 v18, v18, v1
	v_mul_f32_e32 v1, v2, v1
	v_med3_f32 v2, v18, s67, v205
	v_med3_f32 v1, v1, s67, v205
	v_cvt_pk_fp8_f32 v33, v2, v1 op_sel:[0,0,1]
	v_add_u32_e32 v0, 2, v32
	v_ashrrev_i32_e32 v1, 31, v0
	v_lshlrev_b64 v[0:1], 11, v[0:1]
	v_lshl_add_u64 v[0:1], v[88:89], 0, v[0:1]
	v_lshrrev_b32_e32 v2, 8, v33
	global_store_byte v[0:1], v2, off offset:32
	v_rcp_f32_e32 v2, v67
	v_lshrrev_b32_e32 v16, 24, v33
	global_store_byte v[0:1], v33, off
	global_store_byte_d16_hi v[0:1], v33, off offset:64
	global_store_byte v[0:1], v16, off offset:96
	v_mul_f32_e32 v1, 0x41800000, v2
	v_mul_f32_e32 v2, v51, v1
	v_mul_f32_e32 v16, v35, v1
	v_med3_f32 v2, v2, s67, v205
	v_med3_f32 v16, v16, s67, v205
	v_mov_b32_e32 v18, v187
	v_cvt_pk_fp8_f32 v18, v2, v16
	v_mul_f32_e32 v17, v19, v1
	v_mul_f32_e32 v1, v3, v1
	v_med3_f32 v2, v17, s67, v205
	v_med3_f32 v1, v1, s67, v205
	v_cvt_pk_fp8_f32 v18, v2, v1 op_sel:[0,0,1]
	v_add_u32_e32 v0, 3, v32
	v_ashrrev_i32_e32 v1, 31, v0
	v_lshlrev_b64 v[0:1], 11, v[0:1]
	v_lshl_add_u64 v[0:1], v[88:89], 0, v[0:1]
	v_lshrrev_b32_e32 v2, 8, v18
	global_store_byte v[0:1], v2, off offset:32
	v_rcp_f32_e32 v2, v68
	v_lshrrev_b32_e32 v3, 24, v18
	global_store_byte v[0:1], v18, off
	global_store_byte_d16_hi v[0:1], v18, off offset:64
	global_store_byte v[0:1], v3, off offset:96
	v_mul_f32_e32 v1, 0x41800000, v2
	v_mul_f32_e32 v2, v52, v1
	v_mul_f32_e32 v3, v36, v1
	v_med3_f32 v2, v2, s67, v205
	v_med3_f32 v3, v3, s67, v205
	v_mov_b32_e32 v17, v187
	v_cvt_pk_fp8_f32 v17, v2, v3
	v_mul_f32_e32 v16, v20, v1
	v_mul_f32_e32 v1, v4, v1
	v_med3_f32 v2, v16, s67, v205
	v_med3_f32 v1, v1, s67, v205
	v_cvt_pk_fp8_f32 v17, v2, v1 op_sel:[0,0,1]
	v_add_u32_e32 v0, 8, v32
	v_ashrrev_i32_e32 v1, 31, v0
	v_lshlrev_b64 v[0:1], 11, v[0:1]
	v_lshl_add_u64 v[0:1], v[88:89], 0, v[0:1]
	v_lshrrev_b32_e32 v2, 8, v17
	global_store_byte v[0:1], v2, off offset:32
	v_rcp_f32_e32 v2, v69
	v_lshrrev_b32_e32 v3, 24, v17
	global_store_byte v[0:1], v17, off
	global_store_byte_d16_hi v[0:1], v17, off offset:64
	global_store_byte v[0:1], v3, off offset:96
	v_mul_f32_e32 v1, 0x41800000, v2
	v_mul_f32_e32 v2, v53, v1
	v_mul_f32_e32 v3, v37, v1
	v_med3_f32 v2, v2, s67, v205
	v_med3_f32 v3, v3, s67, v205
	v_mov_b32_e32 v16, v187
	v_cvt_pk_fp8_f32 v16, v2, v3
	v_mul_f32_e32 v4, v21, v1
	v_mul_f32_e32 v1, v5, v1
	v_med3_f32 v2, v4, s67, v205
	v_med3_f32 v1, v1, s67, v205
	v_cvt_pk_fp8_f32 v16, v2, v1 op_sel:[0,0,1]
	v_add_u32_e32 v0, 9, v32
	v_ashrrev_i32_e32 v1, 31, v0
	v_lshlrev_b64 v[0:1], 11, v[0:1]
	v_lshl_add_u64 v[0:1], v[88:89], 0, v[0:1]
	v_lshrrev_b32_e32 v2, 8, v16
	global_store_byte v[0:1], v2, off offset:32
	v_rcp_f32_e32 v2, v70
	v_lshrrev_b32_e32 v3, 24, v16
	global_store_byte v[0:1], v16, off
	global_store_byte_d16_hi v[0:1], v16, off offset:64
	global_store_byte v[0:1], v3, off offset:96
	v_mul_f32_e32 v1, 0x41800000, v2
	v_mul_f32_e32 v2, v54, v1
	v_mul_f32_e32 v3, v38, v1
	v_med3_f32 v2, v2, s67, v205
	v_med3_f32 v3, v3, s67, v205
	v_mov_b32_e32 v5, v187
	v_cvt_pk_fp8_f32 v5, v2, v3
	v_mul_f32_e32 v4, v22, v1
	v_mul_f32_e32 v1, v6, v1
	v_med3_f32 v2, v4, s67, v205
	v_med3_f32 v1, v1, s67, v205
	v_cvt_pk_fp8_f32 v5, v2, v1 op_sel:[0,0,1]
	v_add_u32_e32 v0, 10, v32
	v_ashrrev_i32_e32 v1, 31, v0
	v_lshlrev_b64 v[0:1], 11, v[0:1]
	v_lshl_add_u64 v[0:1], v[88:89], 0, v[0:1]
	v_lshrrev_b32_e32 v2, 8, v5
	global_store_byte v[0:1], v2, off offset:32
	v_rcp_f32_e32 v2, v71
	v_lshrrev_b32_e32 v3, 24, v5
	global_store_byte v[0:1], v5, off
	global_store_byte_d16_hi v[0:1], v5, off offset:64
	global_store_byte v[0:1], v3, off offset:96
	v_mul_f32_e32 v1, 0x41800000, v2
	v_mul_f32_e32 v2, v55, v1
	v_mul_f32_e32 v3, v39, v1
	v_med3_f32 v2, v2, s67, v205
	v_med3_f32 v3, v3, s67, v205
	v_mov_b32_e32 v5, v187
	v_cvt_pk_fp8_f32 v5, v2, v3
	v_mul_f32_e32 v4, v23, v1
	v_mul_f32_e32 v1, v7, v1
	v_med3_f32 v2, v4, s67, v205
	v_med3_f32 v1, v1, s67, v205
	v_cvt_pk_fp8_f32 v5, v2, v1 op_sel:[0,0,1]
	v_add_u32_e32 v0, 11, v32
	v_ashrrev_i32_e32 v1, 31, v0
	v_lshlrev_b64 v[0:1], 11, v[0:1]
	v_lshl_add_u64 v[0:1], v[88:89], 0, v[0:1]
	v_lshrrev_b32_e32 v2, 8, v5
	global_store_byte v[0:1], v2, off offset:32
	v_rcp_f32_e32 v2, v72
	v_lshrrev_b32_e32 v3, 24, v5
	global_store_byte v[0:1], v5, off
	global_store_byte_d16_hi v[0:1], v5, off offset:64
	global_store_byte v[0:1], v3, off offset:96
	v_mul_f32_e32 v1, 0x41800000, v2
	v_mul_f32_e32 v2, v56, v1
	v_mul_f32_e32 v3, v40, v1
	v_med3_f32 v2, v2, s67, v205
	v_med3_f32 v3, v3, s67, v205
	v_mov_b32_e32 v5, v187
	v_cvt_pk_fp8_f32 v5, v2, v3
	v_mul_f32_e32 v4, v24, v1
	v_mul_f32_e32 v1, v8, v1
	v_med3_f32 v2, v4, s67, v205
	v_med3_f32 v1, v1, s67, v205
	v_cvt_pk_fp8_f32 v5, v2, v1 op_sel:[0,0,1]
	v_add_u32_e32 v0, 16, v32
	v_ashrrev_i32_e32 v1, 31, v0
	v_lshlrev_b64 v[0:1], 11, v[0:1]
	v_lshl_add_u64 v[0:1], v[88:89], 0, v[0:1]
	v_lshrrev_b32_e32 v2, 8, v5
	global_store_byte v[0:1], v2, off offset:32
	v_rcp_f32_e32 v2, v73
	v_lshrrev_b32_e32 v3, 24, v5
	global_store_byte v[0:1], v5, off
	global_store_byte_d16_hi v[0:1], v5, off offset:64
	global_store_byte v[0:1], v3, off offset:96
	v_mul_f32_e32 v1, 0x41800000, v2
	v_mul_f32_e32 v2, v57, v1
	v_mul_f32_e32 v3, v41, v1
	v_med3_f32 v2, v2, s67, v205
	v_med3_f32 v3, v3, s67, v205
	v_mov_b32_e32 v5, v187
	v_cvt_pk_fp8_f32 v5, v2, v3
	v_mul_f32_e32 v4, v25, v1
	v_mul_f32_e32 v1, v9, v1
	v_med3_f32 v2, v4, s67, v205
	v_med3_f32 v1, v1, s67, v205
	v_cvt_pk_fp8_f32 v5, v2, v1 op_sel:[0,0,1]
	v_add_u32_e32 v0, 17, v32
	v_ashrrev_i32_e32 v1, 31, v0
	v_lshlrev_b64 v[0:1], 11, v[0:1]
	v_lshl_add_u64 v[0:1], v[88:89], 0, v[0:1]
	v_lshrrev_b32_e32 v2, 8, v5
	global_store_byte v[0:1], v2, off offset:32
	v_rcp_f32_e32 v2, v74
	v_lshrrev_b32_e32 v3, 24, v5
	global_store_byte v[0:1], v5, off
	global_store_byte_d16_hi v[0:1], v5, off offset:64
	global_store_byte v[0:1], v3, off offset:96
	v_mul_f32_e32 v1, 0x41800000, v2
	v_mul_f32_e32 v2, v58, v1
	v_mul_f32_e32 v3, v42, v1
	v_med3_f32 v2, v2, s67, v205
	v_med3_f32 v3, v3, s67, v205
	v_mov_b32_e32 v5, v187
	v_cvt_pk_fp8_f32 v5, v2, v3
	v_mul_f32_e32 v4, v26, v1
	v_mul_f32_e32 v1, v10, v1
	v_med3_f32 v2, v4, s67, v205
	v_med3_f32 v1, v1, s67, v205
	v_cvt_pk_fp8_f32 v5, v2, v1 op_sel:[0,0,1]
	v_add_u32_e32 v0, 18, v32
	v_ashrrev_i32_e32 v1, 31, v0
	v_lshlrev_b64 v[0:1], 11, v[0:1]
	v_lshl_add_u64 v[0:1], v[88:89], 0, v[0:1]
	v_lshrrev_b32_e32 v2, 8, v5
	global_store_byte v[0:1], v2, off offset:32
	v_rcp_f32_e32 v2, v75
	v_lshrrev_b32_e32 v3, 24, v5
	global_store_byte v[0:1], v5, off
	global_store_byte_d16_hi v[0:1], v5, off offset:64
	global_store_byte v[0:1], v3, off offset:96
	v_mul_f32_e32 v1, 0x41800000, v2
	v_mul_f32_e32 v2, v59, v1
	v_mul_f32_e32 v3, v43, v1
	v_med3_f32 v2, v2, s67, v205
	v_med3_f32 v3, v3, s67, v205
	v_mov_b32_e32 v5, v187
	v_cvt_pk_fp8_f32 v5, v2, v3
	v_mul_f32_e32 v4, v27, v1
	v_mul_f32_e32 v1, v11, v1
	v_med3_f32 v2, v4, s67, v205
	v_med3_f32 v1, v1, s67, v205
	v_cvt_pk_fp8_f32 v5, v2, v1 op_sel:[0,0,1]
	v_add_u32_e32 v0, 19, v32
	v_ashrrev_i32_e32 v1, 31, v0
	v_lshlrev_b64 v[0:1], 11, v[0:1]
	v_lshl_add_u64 v[0:1], v[88:89], 0, v[0:1]
	v_lshrrev_b32_e32 v2, 8, v5
	global_store_byte v[0:1], v2, off offset:32
	v_rcp_f32_e32 v2, v76
	v_lshrrev_b32_e32 v3, 24, v5
	global_store_byte v[0:1], v5, off
	global_store_byte_d16_hi v[0:1], v5, off offset:64
	global_store_byte v[0:1], v3, off offset:96
	v_mul_f32_e32 v1, 0x41800000, v2
	v_mul_f32_e32 v2, v60, v1
	v_mul_f32_e32 v3, v44, v1
	v_med3_f32 v2, v2, s67, v205
	v_med3_f32 v3, v3, s67, v205
	v_mov_b32_e32 v5, v187
	v_cvt_pk_fp8_f32 v5, v2, v3
	v_mul_f32_e32 v4, v28, v1
	v_mul_f32_e32 v1, v12, v1
	v_med3_f32 v2, v4, s67, v205
	v_med3_f32 v1, v1, s67, v205
	v_cvt_pk_fp8_f32 v5, v2, v1 op_sel:[0,0,1]
	v_add_u32_e32 v0, 24, v32
	v_ashrrev_i32_e32 v1, 31, v0
	v_lshlrev_b64 v[0:1], 11, v[0:1]
	v_lshl_add_u64 v[0:1], v[88:89], 0, v[0:1]
	v_lshrrev_b32_e32 v2, 8, v5
	global_store_byte v[0:1], v2, off offset:32
	v_rcp_f32_e32 v2, v77
	v_lshrrev_b32_e32 v3, 24, v5
	global_store_byte v[0:1], v5, off
	global_store_byte_d16_hi v[0:1], v5, off offset:64
	global_store_byte v[0:1], v3, off offset:96
	v_mul_f32_e32 v1, 0x41800000, v2
	v_mul_f32_e32 v2, v61, v1
	v_mul_f32_e32 v3, v45, v1
	v_med3_f32 v2, v2, s67, v205
	v_med3_f32 v3, v3, s67, v205
	v_mov_b32_e32 v5, v187
	v_cvt_pk_fp8_f32 v5, v2, v3
	v_mul_f32_e32 v4, v29, v1
	v_mul_f32_e32 v1, v13, v1
	v_med3_f32 v2, v4, s67, v205
	v_med3_f32 v1, v1, s67, v205
	v_cvt_pk_fp8_f32 v5, v2, v1 op_sel:[0,0,1]
	v_add_u32_e32 v0, 25, v32
	v_ashrrev_i32_e32 v1, 31, v0
	v_lshlrev_b64 v[0:1], 11, v[0:1]
	v_lshl_add_u64 v[0:1], v[88:89], 0, v[0:1]
	v_lshrrev_b32_e32 v2, 8, v5
	global_store_byte v[0:1], v2, off offset:32
	v_rcp_f32_e32 v2, v78
	v_lshrrev_b32_e32 v3, 24, v5
	global_store_byte v[0:1], v5, off
	global_store_byte_d16_hi v[0:1], v5, off offset:64
	global_store_byte v[0:1], v3, off offset:96
	v_mul_f32_e32 v1, 0x41800000, v2
	v_mul_f32_e32 v2, v62, v1
	v_mul_f32_e32 v3, v46, v1
	v_med3_f32 v2, v2, s67, v205
	v_med3_f32 v3, v3, s67, v205
	v_mov_b32_e32 v5, v187
	v_cvt_pk_fp8_f32 v5, v2, v3
	v_mul_f32_e32 v4, v30, v1
	v_mul_f32_e32 v1, v14, v1
	v_med3_f32 v2, v4, s67, v205
	v_med3_f32 v1, v1, s67, v205
	v_cvt_pk_fp8_f32 v5, v2, v1 op_sel:[0,0,1]
	v_add_u32_e32 v0, 26, v32
	v_ashrrev_i32_e32 v1, 31, v0
	v_lshlrev_b64 v[0:1], 11, v[0:1]
	v_lshl_add_u64 v[0:1], v[88:89], 0, v[0:1]
	v_lshrrev_b32_e32 v2, 8, v5
	global_store_byte v[0:1], v2, off offset:32
	v_rcp_f32_e32 v2, v79
	v_lshrrev_b32_e32 v3, 24, v5
	global_store_byte v[0:1], v5, off
	global_store_byte_d16_hi v[0:1], v5, off offset:64
	global_store_byte v[0:1], v3, off offset:96
	v_mul_f32_e32 v1, 0x41800000, v2
	v_mul_f32_e32 v2, v63, v1
	v_mul_f32_e32 v3, v47, v1
	v_med3_f32 v2, v2, s67, v205
	v_med3_f32 v3, v3, s67, v205
	v_mov_b32_e32 v5, v187
	v_cvt_pk_fp8_f32 v5, v2, v3
	v_mul_f32_e32 v4, v31, v1
	v_mul_f32_e32 v1, v15, v1
	v_med3_f32 v2, v4, s67, v205
	v_med3_f32 v1, v1, s67, v205
	v_cvt_pk_fp8_f32 v5, v2, v1 op_sel:[0,0,1]
	v_add_u32_e32 v0, 27, v32
	v_ashrrev_i32_e32 v1, 31, v0
	v_lshlrev_b64 v[0:1], 11, v[0:1]
	v_lshl_add_u64 v[0:1], v[88:89], 0, v[0:1]
	v_lshrrev_b32_e32 v2, 8, v5
	global_store_byte v[0:1], v5, off
	global_store_byte v[0:1], v2, off offset:32
	global_store_byte_d16_hi v[0:1], v5, off offset:64
	v_lshrrev_b32_e32 v2, 24, v5
	global_store_byte v[0:1], v2, off offset:96
	s_waitcnt lgkmcnt(0)
	s_barrier
	s_cbranch_scc1 .LBB0_1899

.LBB0_1873:
	s_or_b64 exec, exec, s[2:3]
	v_mul_f32_e32 v0, v106, v0
	v_mul_f32_e32 v1, v106, v1
	v_mul_f32_e32 v26, v106, v26
	v_mul_f32_e32 v0, v0, v113
	v_mul_f32_e32 v1, v1, v112
	v_mul_f32_e32 v26, v26, v135
	v_med3_f32 v0, v0, s67, v205
	v_med3_f32 v1, v1, s67, v205
	v_mov_b32_e32 v135, v187
	v_cvt_pk_fp8_f32 v135, v0, v1
	v_mul_f32_e32 v2, v106, v2
	v_mul_f32_e32 v3, v106, v3
	v_mul_f32_e32 v2, v2, v111
	v_mul_f32_e32 v3, v3, v110
	v_med3_f32 v0, v2, s67, v205
	v_med3_f32 v1, v3, s67, v205
	v_mul_f32_e32 v25, v106, v25
	v_cvt_pk_fp8_f32 v135, v0, v1 op_sel:[0,0,1]
	v_max_f32_e32 v0, v104, v104
	v_max_f32_e32 v1, v105, v105
	v_mul_f32_e32 v25, v25, v136
	v_med3_f32 v0, v0, s67, v205
	v_med3_f32 v1, v1, s67, v205
	v_mov_b32_e32 v136, v187
	v_cvt_pk_fp8_f32 v136, v0, v1
	v_max_f32_e32 v2, v100, v100
	v_max_f32_e32 v1, v101, v101
	v_med3_f32 v0, v2, s67, v205
	v_med3_f32 v1, v1, s67, v205
	v_mul_f32_e32 v24, v106, v24
	v_cvt_pk_fp8_f32 v136, v0, v1 op_sel:[0,0,1]
	v_max_f32_e32 v0, v98, v98
	v_max_f32_e32 v1, v99, v99
	v_mul_f32_e32 v24, v24, v137
	v_med3_f32 v0, v0, s67, v205
	v_med3_f32 v1, v1, s67, v205
	v_mov_b32_e32 v137, v187
	v_cvt_pk_fp8_f32 v137, v0, v1
	v_max_f32_e32 v2, v96, v96
	v_max_f32_e32 v1, v97, v97
	v_med3_f32 v0, v2, s67, v205
	v_med3_f32 v1, v1, s67, v205
	v_mul_f32_e32 v31, v106, v31
	v_cvt_pk_fp8_f32 v137, v0, v1 op_sel:[0,0,1]
	v_max_f32_e32 v0, v94, v94
	v_max_f32_e32 v1, v95, v95
	v_mul_f32_e32 v31, v31, v138
	v_med3_f32 v0, v0, s67, v205
	v_med3_f32 v1, v1, s67, v205
	v_mov_b32_e32 v138, v187
	v_cvt_pk_fp8_f32 v138, v0, v1
	v_max_f32_e32 v2, v92, v92
	v_max_f32_e32 v1, v93, v93
	v_med3_f32 v0, v2, s67, v205
	v_med3_f32 v1, v1, s67, v205
	v_mul_f32_e32 v30, v106, v30
	v_cvt_pk_fp8_f32 v138, v0, v1 op_sel:[0,0,1]
	v_max_f32_e32 v0, v90, v90
	v_max_f32_e32 v1, v91, v91
	v_mul_f32_e32 v30, v30, v139
	v_med3_f32 v0, v0, s67, v205
	v_med3_f32 v1, v1, s67, v205
	v_mov_b32_e32 v139, v187
	v_cvt_pk_fp8_f32 v139, v0, v1
	v_max_f32_e32 v2, v88, v88
	v_max_f32_e32 v1, v89, v89
	v_med3_f32 v0, v2, s67, v205
	v_med3_f32 v1, v1, s67, v205
	v_mul_f32_e32 v29, v106, v29
	v_cvt_pk_fp8_f32 v139, v0, v1 op_sel:[0,0,1]
	v_max_f32_e32 v0, v86, v86
	v_max_f32_e32 v1, v87, v87
	v_mul_f32_e32 v29, v29, v140
	v_med3_f32 v0, v0, s67, v205
	v_med3_f32 v1, v1, s67, v205
	v_mov_b32_e32 v140, v187
	v_cvt_pk_fp8_f32 v140, v0, v1
	v_max_f32_e32 v2, v84, v84
	v_max_f32_e32 v1, v85, v85
	v_med3_f32 v0, v2, s67, v205
	v_med3_f32 v1, v1, s67, v205
	v_mul_f32_e32 v28, v106, v28
	v_cvt_pk_fp8_f32 v140, v0, v1 op_sel:[0,0,1]
	v_max_f32_e32 v0, v82, v82
	v_max_f32_e32 v1, v83, v83
	v_mul_f32_e32 v28, v28, v141
	v_med3_f32 v0, v0, s67, v205
	v_med3_f32 v1, v1, s67, v205
	v_mov_b32_e32 v141, v187
	v_cvt_pk_fp8_f32 v141, v0, v1
	v_max_f32_e32 v2, v80, v80
	v_max_f32_e32 v1, v81, v81
	v_med3_f32 v0, v2, s67, v205
	v_med3_f32 v1, v1, s67, v205
	v_mul_f32_e32 v35, v106, v35
	v_cvt_pk_fp8_f32 v141, v0, v1 op_sel:[0,0,1]
	v_max_f32_e32 v0, v78, v78
	v_max_f32_e32 v1, v79, v79
	v_mul_f32_e32 v35, v35, v142
	v_med3_f32 v0, v0, s67, v205
	v_med3_f32 v1, v1, s67, v205
	v_mov_b32_e32 v142, v187
	v_cvt_pk_fp8_f32 v142, v0, v1
	v_mul_f32_e32 v8, v106, v8
	v_mul_f32_e32 v9, v106, v9
	v_mul_f32_e32 v4, v106, v4
	v_mul_f32_e32 v5, v106, v5
	v_mul_f32_e32 v60, v60, v106
	v_mul_f32_e32 v61, v61, v106
	v_mul_f32_e32 v56, v56, v106
	v_mul_f32_e32 v57, v57, v106
	v_mul_f32_e32 v52, v52, v106
	v_mul_f32_e32 v53, v106, v53
	v_mul_f32_e32 v48, v106, v48
	v_mul_f32_e32 v49, v106, v49
	v_mul_f32_e32 v44, v106, v44
	v_mul_f32_e32 v45, v106, v45
	v_mul_f32_e32 v40, v106, v40
	v_mul_f32_e32 v41, v106, v41
	v_mul_f32_e32 v36, v106, v36
	v_mul_f32_e32 v37, v106, v37
	v_mul_f32_e32 v32, v106, v32
	v_mul_f32_e32 v33, v106, v33
	v_mul_f32_e32 v27, v106, v27
	v_mul_f32_e32 v20, v106, v20
	v_mul_f32_e32 v8, v8, v121
	v_mul_f32_e32 v9, v9, v120
	v_mul_f32_e32 v4, v4, v117
	v_mul_f32_e32 v5, v5, v116
	v_max_f32_e32 v2, v76, v76
	v_max_f32_e32 v1, v77, v77
	v_mul_f32_e32 v60, v60, v181
	v_mul_f32_e32 v61, v61, v180
	v_mul_f32_e32 v56, v56, v177
	v_mul_f32_e32 v57, v57, v176
	v_mul_f32_e32 v52, v52, v173
	v_mul_f32_e32 v53, v53, v172
	v_mul_f32_e32 v48, v48, v161
	v_mul_f32_e32 v49, v49, v160
	v_mul_f32_e32 v44, v44, v157
	v_mul_f32_e32 v45, v45, v156
	v_mul_f32_e32 v40, v40, v153
	v_mul_f32_e32 v41, v41, v152
	v_mul_f32_e32 v36, v36, v149
	v_mul_f32_e32 v37, v37, v148
	v_mul_f32_e32 v32, v32, v145
	v_mul_f32_e32 v33, v33, v144
	v_mul_f32_e32 v27, v27, v134
	v_mul_f32_e32 v20, v20, v133
	v_mul_f32_e32 v18, v106, v18
	v_mul_f32_e32 v19, v106, v19
	v_mul_f32_e32 v12, v106, v12
	v_mul_f32_e32 v13, v106, v13
	v_mul_f32_e32 v14, v106, v14
	v_mul_f32_e32 v15, v106, v15
	v_med3_f32 v8, v8, s67, v205
	v_med3_f32 v9, v9, s67, v205
	v_mov_b32_e32 v133, v187
	v_med3_f32 v4, v4, s67, v205
	v_med3_f32 v5, v5, s67, v205
	v_mov_b32_e32 v134, v187
	v_med3_f32 v0, v2, s67, v205
	v_med3_f32 v1, v1, s67, v205
	v_mul_f32_e32 v34, v106, v34
	v_mul_f32_e32 v18, v18, v127
	v_mul_f32_e32 v19, v19, v126
	v_mul_f32_e32 v12, v12, v125
	v_mul_f32_e32 v13, v13, v124
	v_mul_f32_e32 v14, v14, v123
	v_mul_f32_e32 v15, v15, v122
	v_med3_f32 v60, v60, s67, v205
	v_med3_f32 v61, v61, s67, v205
	v_mov_b32_e32 v120, v187
	v_med3_f32 v56, v56, s67, v205
	v_med3_f32 v57, v57, s67, v205
	v_mov_b32_e32 v121, v187
	v_med3_f32 v52, v52, s67, v205
	v_med3_f32 v53, v53, s67, v205
	v_mov_b32_e32 v122, v187
	v_med3_f32 v48, v48, s67, v205
	v_med3_f32 v49, v49, s67, v205
	v_mov_b32_e32 v123, v187
	v_med3_f32 v44, v44, s67, v205
	v_med3_f32 v45, v45, s67, v205
	v_mov_b32_e32 v124, v187
	v_med3_f32 v40, v40, s67, v205
	v_med3_f32 v41, v41, s67, v205
	v_mov_b32_e32 v125, v187
	v_med3_f32 v36, v36, s67, v205
	v_med3_f32 v37, v37, s67, v205
	v_mov_b32_e32 v126, v187
	v_med3_f32 v32, v32, s67, v205
	v_med3_f32 v33, v33, s67, v205
	v_mov_b32_e32 v127, v187
	v_cvt_pk_fp8_f32 v133, v8, v9
	v_cvt_pk_fp8_f32 v134, v4, v5
	v_cvt_pk_fp8_f32 v142, v0, v1 op_sel:[0,0,1]
	v_max_f32_e32 v0, v74, v74
	v_max_f32_e32 v1, v75, v75
	s_and_b32 s2, s18, 0x3fffffc0
	v_mul_f32_e32 v34, v34, v143
	v_mul_f32_e32 v10, v106, v10
	v_mul_f32_e32 v11, v106, v11
	v_mul_f32_e32 v6, v106, v6
	v_mul_f32_e32 v7, v106, v7
	v_cvt_pk_fp8_f32 v120, v60, v61
	v_cvt_pk_fp8_f32 v121, v56, v57
	v_cvt_pk_fp8_f32 v122, v52, v53
	v_cvt_pk_fp8_f32 v123, v48, v49
	v_cvt_pk_fp8_f32 v124, v44, v45
	v_cvt_pk_fp8_f32 v125, v40, v41
	v_cvt_pk_fp8_f32 v126, v36, v37
	v_cvt_pk_fp8_f32 v127, v32, v33
	v_med3_f32 v0, v0, s67, v205
	v_med3_f32 v1, v1, s67, v205
	v_mov_b32_e32 v143, v187
	s_lshl_b32 s2, s2, 2
	v_mul_f32_e32 v62, v62, v106
	v_mul_f32_e32 v63, v63, v106
	v_mul_f32_e32 v58, v58, v106
	v_mul_f32_e32 v59, v59, v106
	v_mul_f32_e32 v54, v106, v54
	v_mul_f32_e32 v55, v106, v55
	v_mul_f32_e32 v50, v106, v50
	v_mul_f32_e32 v51, v106, v51
	v_mul_f32_e32 v46, v106, v46
	v_mul_f32_e32 v47, v106, v47
	v_mul_f32_e32 v42, v106, v42
	v_mul_f32_e32 v43, v106, v43
	v_mul_f32_e32 v38, v106, v38
	v_mul_f32_e32 v39, v106, v39
	v_mul_f32_e32 v21, v106, v21
	v_mul_f32_e32 v16, v106, v16
	v_mul_f32_e32 v17, v106, v17
	v_mul_f32_e32 v10, v10, v119
	v_mul_f32_e32 v11, v11, v118
	v_mul_f32_e32 v6, v6, v115
	v_mul_f32_e32 v7, v7, v114
	v_cvt_pk_fp8_f32 v143, v0, v1
	v_mul_u32_u24_e32 v0, 0xd0, v188
	s_add_i32 s2, s2, 0
	v_mul_f32_e32 v62, v62, v179
	v_mul_f32_e32 v63, v63, v178
	v_mul_f32_e32 v58, v58, v175
	v_mul_f32_e32 v59, v59, v174
	v_mul_f32_e32 v54, v54, v163
	v_mul_f32_e32 v55, v55, v162
	v_mul_f32_e32 v50, v50, v159
	v_mul_f32_e32 v51, v51, v158
	v_mul_f32_e32 v46, v46, v155
	v_mul_f32_e32 v47, v47, v154
	v_mul_f32_e32 v42, v42, v151
	v_mul_f32_e32 v43, v43, v150
	v_mul_f32_e32 v38, v38, v147
	v_mul_f32_e32 v39, v39, v146
	v_mul_f32_e32 v21, v21, v132
	v_mul_f32_e32 v22, v106, v22
	v_mul_f32_e32 v23, v106, v23
	v_mul_f32_e32 v16, v16, v129
	v_mul_f32_e32 v17, v17, v128
	v_med3_f32 v8, v10, s67, v205
	v_med3_f32 v9, v11, s67, v205
	v_med3_f32 v6, v6, s67, v205
	v_med3_f32 v7, v7, s67, v205
	v_max_f32_e32 v2, v72, v72
	v_add3_u32 v214, 0, v0, v186
	s_add_i32 s77, s2, 0x18000
	s_ashr_i32 s2, s19, 6
	v_mul_f32_e32 v22, v22, v131
	v_mul_f32_e32 v23, v23, v130
	v_med3_f32 v62, v62, s67, v205
	v_med3_f32 v63, v63, s67, v205
	v_med3_f32 v56, v58, s67, v205
	v_med3_f32 v57, v59, s67, v205
	v_med3_f32 v54, v54, s67, v205
	v_med3_f32 v55, v55, s67, v205
	v_med3_f32 v48, v50, s67, v205
	v_med3_f32 v49, v51, s67, v205
	v_med3_f32 v46, v46, s67, v205
	v_med3_f32 v47, v47, s67, v205
	v_med3_f32 v40, v42, s67, v205
	v_med3_f32 v41, v43, s67, v205
	v_med3_f32 v38, v38, s67, v205
	v_med3_f32 v39, v39, s67, v205
	v_med3_f32 v32, v34, s67, v205
	v_med3_f32 v33, v35, s67, v205
	v_med3_f32 v28, v28, s67, v205
	v_med3_f32 v29, v29, s67, v205
	v_mov_b32_e32 v128, v187
	v_med3_f32 v24, v24, s67, v205
	v_med3_f32 v25, v25, s67, v205
	v_mov_b32_e32 v129, v187
	v_med3_f32 v20, v20, s67, v205
	v_med3_f32 v21, v21, s67, v205
	v_mov_b32_e32 v130, v187
	v_med3_f32 v16, v16, s67, v205
	v_med3_f32 v17, v17, s67, v205
	v_mov_b32_e32 v131, v187
	v_cvt_pk_fp8_f32 v133, v8, v9 op_sel:[0,0,1]
	v_cvt_pk_fp8_f32 v134, v6, v7 op_sel:[0,0,1]
	v_med3_f32 v8, v2, s67, v205
	ds_read_b128 v[0:3], v214
	ds_read_b128 v[4:7], v214 offset:16
	s_lshl_b32 s75, s17, 8
	s_ashr_i32 s3, s2, 31
	v_cvt_pk_fp8_f32 v120, v62, v63 op_sel:[0,0,1]
	v_cvt_pk_fp8_f32 v121, v56, v57 op_sel:[0,0,1]
	v_cvt_pk_fp8_f32 v122, v54, v55 op_sel:[0,0,1]
	v_cvt_pk_fp8_f32 v123, v48, v49 op_sel:[0,0,1]
	v_cvt_pk_fp8_f32 v124, v46, v47 op_sel:[0,0,1]
	v_cvt_pk_fp8_f32 v125, v40, v41 op_sel:[0,0,1]
	v_cvt_pk_fp8_f32 v126, v38, v39 op_sel:[0,0,1]
	v_cvt_pk_fp8_f32 v127, v32, v33 op_sel:[0,0,1]
	v_cvt_pk_fp8_f32 v128, v28, v29
	v_cvt_pk_fp8_f32 v129, v24, v25
	v_cvt_pk_fp8_f32 v130, v20, v21
	v_cvt_pk_fp8_f32 v131, v16, v17
	s_addk_i32 s75, 0x2000
	s_lshl_b64 s[2:3], s[2:3], 16
	v_max_f32_e32 v9, v73, v73
	s_add_u32 s2, s40, s2
	v_med3_f32 v9, v9, s67, v205
	s_addc_u32 s3, s41, s3
	v_med3_f32 v30, v30, s67, v205
	v_med3_f32 v31, v31, s67, v205
	v_med3_f32 v24, v26, s67, v205
	v_med3_f32 v25, v27, s67, v205
	v_med3_f32 v22, v22, s67, v205
	v_med3_f32 v23, v23, s67, v205
	v_med3_f32 v16, v18, s67, v205
	v_med3_f32 v17, v19, s67, v205
	v_cvt_pk_fp8_f32 v143, v8, v9 op_sel:[0,0,1]
	v_lshl_add_u64 v[8:9], s[2:3], 0, v[102:103]
	v_cvt_pk_fp8_f32 v128, v30, v31 op_sel:[0,0,1]
	v_cvt_pk_fp8_f32 v129, v24, v25 op_sel:[0,0,1]
	v_cvt_pk_fp8_f32 v130, v22, v23 op_sel:[0,0,1]
	v_cvt_pk_fp8_f32 v131, v16, v17 op_sel:[0,0,1]
	s_waitcnt lgkmcnt(0)
	v_mfma_f32_32x32x64_f8f6f4 v[16:31], v[0:7], v[120:127], 0
	ds_read_b128 v[0:3], v214 offset:64
	ds_read_b128 v[4:7], v214 offset:80
	global_load_dwordx4 v[172:175], v[8:9], off
	v_med3_f32 v12, v12, s67, v205
	v_med3_f32 v13, v13, s67, v205
	v_mov_b32_e32 v132, v187
	v_cvt_pk_fp8_f32 v132, v12, v13
	v_med3_f32 v14, v14, s67, v205
	v_med3_f32 v15, v15, s67, v205
	s_mov_b32 s17, s16
	v_cvt_pk_fp8_f32 v132, v14, v15 op_sel:[0,0,1]
	s_mov_b32 s18, s16
	s_mov_b32 s19, s16
	s_mov_b32 s20, s16
	s_mov_b32 s21, s16
	s_mov_b32 s22, s16
	s_waitcnt lgkmcnt(0)
	v_mfma_f32_32x32x64_f8f6f4 v[16:31], v[0:7], v[128:135], v[16:31]
	v_sub_u32_e32 v0, v214, v108
	ds_read_b128 v[32:35], v0 offset:128
	ds_read_b128 v[36:39], v0 offset:160
	s_mov_b32 s23, s16
	s_mov_b32 s24, s16
	s_mov_b32 s25, s16
	s_mov_b32 s26, s16
	s_mov_b32 s27, s16
	s_mov_b32 s28, s16
	s_mov_b32 s29, s16
	s_mov_b32 s30, s16
	s_mov_b32 s31, s16
	v_mov_b64_e32 v[0:1], s[16:17]
	v_and_b32_e32 v64, 63, v109
	v_mov_b64_e32 v[14:15], s[30:31]
	v_mov_b64_e32 v[2:3], s[18:19]
	s_waitcnt lgkmcnt(0)
	v_mfma_f32_32x32x64_f8f6f4 v[16:31], v[32:39], v[136:143], v[16:31]
	v_mov_b64_e32 v[4:5], s[20:21]
	v_mov_b64_e32 v[6:7], s[22:23]
	v_mov_b64_e32 v[8:9], s[24:25]
	v_mov_b64_e32 v[10:11], s[26:27]
	v_mov_b64_e32 v[12:13], s[28:29]
	v_mov_b32_e32 v112, 0x38383838
	v_cmp_gt_u32_e64 s[2:3], 32, v64
	v_mov_b64_e32 v[62:63], v[14:15]
	v_mov_b64_e32 v[78:79], v[14:15]
	s_mov_b32 s76, 2
	v_sub_u32_e32 v215, 0, v108
	v_lshl_add_u32 v208, v188, 2, s77
	v_mov_b32_e32 v113, v112
	v_mov_b32_e32 v114, v112
	s_nop 5
	v_max_f32_e32 v32, v16, v17
	v_max3_f32 v32, v32, v18, v19
	v_max3_f32 v32, v32, v20, v21
	v_max3_f32 v32, v32, v22, v23
	v_max3_f32 v32, v32, v24, v25
	v_max3_f32 v32, v32, v26, v27
	v_max3_f32 v32, v32, v28, v29
	v_max3_f32 v32, v32, v30, v31
	v_mov_b32_e32 v33, v32
	s_nop 1
	v_permlane32_swap_b32_e32 v32, v33
	v_max_f32_e32 v32, v32, v33
	v_fmamk_f32 v33, v32, 0x3dd53b94, v203
	v_fmamk_f32 v32, v32, 0x3dd53b94, v204
	v_max_f32_e32 v32, 0xf149f2ca, v32
	v_cmp_ge_f32_e32 vcc, s68, v33
	v_sub_f32_e32 v33, 0xf149f2ca, v32
	s_cmp_eq_u64 vcc, exec
	v_exp_f32_e32 v33, v33
	s_cselect_b64 vcc, -1, 0
	v_cndmask_b32_e32 v194, v32, v206, vcc
	v_pk_fma_f32 v[178:179], v[16:17], s[38:39], v[194:195] op_sel_hi:[1,0,0] neg_lo:[0,0,1] neg_hi:[0,0,1]
	v_mul_u32_u24_e32 v16, 0x50, v188
	v_pk_fma_f32 v[152:153], v[30:31], s[38:39], v[194:195] op_sel_hi:[1,0,0] neg_lo:[0,0,1] neg_hi:[0,0,1]
	v_pk_fma_f32 v[154:155], v[28:29], s[38:39], v[194:195] op_sel_hi:[1,0,0] neg_lo:[0,0,1] neg_hi:[0,0,1]
	v_pk_fma_f32 v[156:157], v[26:27], s[38:39], v[194:195] op_sel_hi:[1,0,0] neg_lo:[0,0,1] neg_hi:[0,0,1]
	v_pk_fma_f32 v[158:159], v[24:25], s[38:39], v[194:195] op_sel_hi:[1,0,0] neg_lo:[0,0,1] neg_hi:[0,0,1]
	v_pk_fma_f32 v[160:161], v[22:23], s[38:39], v[194:195] op_sel_hi:[1,0,0] neg_lo:[0,0,1] neg_hi:[0,0,1]
	v_pk_fma_f32 v[162:163], v[20:21], s[38:39], v[194:195] op_sel_hi:[1,0,0] neg_lo:[0,0,1] neg_hi:[0,0,1]
	v_pk_fma_f32 v[176:177], v[18:19], s[38:39], v[194:195] op_sel_hi:[1,0,0] neg_lo:[0,0,1] neg_hi:[0,0,1]
	v_cndmask_b32_e64 v88, v33, 1.0, vcc
	v_add3_u32 v209, s65, v16, v186
	v_mov_b64_e32 v[30:31], v[14:15]
	v_mov_b64_e32 v[46:47], v[14:15]
	v_mov_b32_e32 v115, v112
	v_mov_b32_e32 v116, v112
	v_mov_b32_e32 v117, v112
	v_mov_b32_e32 v118, v112
	v_mov_b32_e32 v119, v112
	v_lshlrev_b32_e32 v186, 2, v107
	v_mul_lo_u32 v216, v212, s63
	v_lshl_add_u32 v213, v107, 4, s77
	v_lshl_add_u64 v[196:197], s[4:5], 0, v[190:191]
	v_lshl_add_u64 v[198:199], s[4:5], 0, v[192:193]
	v_lshl_add_u64 v[200:201], s[40:41], 0, v[102:103]
	s_mov_b32 s17, 0
	v_mov_b64_e32 v[28:29], v[12:13]
	v_mov_b64_e32 v[26:27], v[10:11]
	v_mov_b64_e32 v[24:25], v[8:9]
	v_mov_b64_e32 v[22:23], v[6:7]
	v_mov_b64_e32 v[20:21], v[4:5]
	v_mov_b64_e32 v[18:19], v[2:3]
	v_mov_b64_e32 v[16:17], v[0:1]
	v_mov_b64_e32 v[44:45], v[12:13]
	v_mov_b64_e32 v[42:43], v[10:11]
	v_mov_b64_e32 v[40:41], v[8:9]
	v_mov_b64_e32 v[38:39], v[6:7]
	v_mov_b64_e32 v[36:37], v[4:5]
	v_mov_b64_e32 v[34:35], v[2:3]
	v_mov_b64_e32 v[32:33], v[0:1]
	v_mov_b64_e32 v[60:61], v[12:13]
	v_mov_b64_e32 v[58:59], v[10:11]
	v_mov_b64_e32 v[56:57], v[8:9]
	v_mov_b64_e32 v[54:55], v[6:7]
	v_mov_b64_e32 v[52:53], v[4:5]
	v_mov_b64_e32 v[50:51], v[2:3]
	v_mov_b64_e32 v[48:49], v[0:1]
	v_mov_b64_e32 v[76:77], v[12:13]
	v_mov_b64_e32 v[74:75], v[10:11]
	v_mov_b64_e32 v[72:73], v[8:9]
	v_mov_b64_e32 v[70:71], v[6:7]
	v_mov_b64_e32 v[68:69], v[4:5]
	v_mov_b64_e32 v[66:67], v[2:3]
	v_mov_b64_e32 v[64:65], v[0:1]
	s_branch .LBB0_1876

.LBB0_1875:
	s_waitcnt lgkmcnt(4)
	v_mfma_f32_32x32x64_f8f6f4 v[96:111], v[96:103], v[120:127], 0
	v_cndmask_b32_e64 v176, v191, v194, s[4:5]
	v_fma_f32 v80, v80, s38, -v176
	v_fma_f32 v81, v81, s38, -v176
	v_fma_f32 v84, v84, s38, -v176
	v_fma_f32 v85, v85, s38, -v176
	v_fma_f32 v88, v88, s38, -v176
	v_fma_f32 v89, v89, s38, -v176
	v_fma_f32 v92, v92, s38, -v176
	v_fma_f32 v93, v93, s38, -v176
	v_exp_f32_e32 v80, v80
	v_exp_f32_e32 v81, v81
	v_exp_f32_e32 v84, v84
	v_exp_f32_e32 v85, v85
	v_exp_f32_e32 v88, v88
	v_exp_f32_e32 v89, v89
	s_waitcnt lgkmcnt(2)
	v_mfma_f32_32x32x64_f8f6f4 v[96:111], v[156:163], v[128:135], v[96:111]
	v_exp_f32_e32 v92, v92
	v_exp_f32_e32 v93, v93
	v_fma_f32 v82, v82, s38, -v176
	v_fma_f32 v83, v83, s38, -v176
	v_fma_f32 v86, v86, s38, -v176
	v_fma_f32 v87, v87, s38, -v176
	v_fma_f32 v90, v90, s38, -v176
	v_fma_f32 v91, v91, s38, -v176
	v_fma_f32 v94, v94, s38, -v176
	v_fma_f32 v95, v95, s38, -v176
	v_exp_f32_e32 v82, v82
	v_exp_f32_e32 v83, v83
	v_exp_f32_e32 v86, v86
	v_exp_f32_e32 v87, v87
	v_exp_f32_e32 v90, v90
	s_waitcnt lgkmcnt(0)
	v_mfma_f32_32x32x64_f8f6f4 v[96:111], v[148:155], v[136:143], v[96:111]
	v_lshl_add_u32 v240, s24, 14, v209
	ds_read_b128 v[224:227], v240
	ds_read_b128 v[228:231], v240 offset:16
	ds_read_b128 v[232:235], v240 offset:2560
	ds_read_b128 v[236:239], v240 offset:2576
	v_exp_f32_e32 v91, v91
	v_exp_f32_e32 v94, v94
	v_exp_f32_e32 v95, v95
	v_cvt_pk_fp8_f32 v148, v80, v81
	v_cvt_pk_fp8_f32 v149, v84, v85
	v_cvt_pk_fp8_f32 v150, v88, v89
	v_cvt_pk_fp8_f32 v151, v92, v93
	v_cvt_pk_fp8_f32 v148, v82, v83 op_sel:[0,0,1]
	v_cvt_pk_fp8_f32 v149, v86, v87 op_sel:[0,0,1]
	v_cvt_pk_fp8_f32 v150, v90, v91 op_sel:[0,0,1]
	v_cvt_pk_fp8_f32 v151, v94, v95 op_sel:[0,0,1]
	s_nop 0
	s_waitcnt lgkmcnt(2)
	v_mfma_f32_32x32x64_f8f6f4 v[48:63], v[144:151], v[224:231], v[48:63]
	ds_read_b128 v[80:83], v240 offset:5120
	ds_read_b128 v[84:87], v240 offset:5136
	ds_read_b128 v[152:155], v240 offset:7680
	ds_read_b128 v[156:159], v240 offset:7696
	s_waitcnt lgkmcnt(4)
	v_mfma_f32_32x32x64_f8f6f4 v[32:47], v[144:151], v[232:239], v[32:47]
	v_max_f32_e32 v88, v96, v97
	v_max3_f32 v88, v88, v98, v99
	v_max3_f32 v88, v88, v100, v101
	v_max3_f32 v88, v88, v102, v103
	v_max3_f32 v88, v88, v104, v105
	v_max3_f32 v88, v88, v106, v107
	s_waitcnt lgkmcnt(2)
	v_mfma_f32_32x32x64_f8f6f4 v[16:31], v[144:151], v[80:87], v[16:31]
	v_max3_f32 v88, v88, v108, v109
	v_max3_f32 v88, v88, v110, v111
	v_mov_b32_e32 v89, v88
	s_nop 1
	v_permlane32_swap_b32_e32 v88, v89
	v_max_f32_e32 v80, v88, v89
	v_fma_f32 v81, v80, s38, -v176
	v_cmp_ge_f32_e32 vcc, s68, v81
	s_waitcnt lgkmcnt(0)
	v_mfma_f32_32x32x64_f8f6f4 v[0:15], v[144:151], v[152:159], v[0:15]
	s_cmp_eq_u64 vcc, exec
	s_cbranch_scc0 .Lmla_rare_a1
	v_mov_b32_e32 v194, v176
	v_mov_b32_e32 v88, 1.0
.Lmla_back_a1:
	v_fma_f32 v178, v96, s38, -v194
	v_fma_f32 v179, v97, s38, -v194
	v_fma_f32 v176, v98, s38, -v194
	v_fma_f32 v177, v99, s38, -v194
	v_fma_f32 v162, v100, s38, -v194
	v_fma_f32 v163, v101, s38, -v194
	v_fma_f32 v160, v102, s38, -v194
	v_fma_f32 v161, v103, s38, -v194
	v_fma_f32 v158, v104, s38, -v194
	v_fma_f32 v159, v105, s38, -v194
	v_fma_f32 v156, v106, s38, -v194
	v_fma_f32 v157, v107, s38, -v194
	v_fma_f32 v154, v108, s38, -v194
	v_fma_f32 v155, v109, s38, -v194
	v_fma_f32 v152, v110, s38, -v194
	v_fma_f32 v153, v111, s38, -v194
	s_add_i32 s17, s17, 2
	s_add_i32 s76, s76, 1
	s_and_b64 vcc, exec, s[18:19]
	v_mfma_f32_32x32x64_f8f6f4 v[64:79], v[144:151], v[112:119], v[64:79]
	s_barrier
	s_cbranch_vccnz .LBB0_1889

.LBB0_1880:
	s_waitcnt lgkmcnt(4)
	v_mfma_f32_32x32x64_f8f6f4 v[80:95], v[80:87], v[120:127], 0
	s_xor_b32 s22, s24, 1
	s_lshl_b32 s18, s22, 15
	s_add_i32 s23, s18, 0
	s_mov_b64 s[20:21], exec
	s_waitcnt lgkmcnt(2)
	v_mfma_f32_32x32x64_f8f6f4 v[80:95], v[104:111], v[128:135], v[80:95]
	s_waitcnt lgkmcnt(0)
	v_mfma_f32_32x32x64_f8f6f4 v[80:95], v[96:103], v[136:143], v[80:95]
	s_nop 15
	s_nop 3
	v_max_f32_e32 v96, v80, v81
	v_max3_f32 v96, v96, v82, v83
	v_max3_f32 v96, v96, v84, v85
	v_max3_f32 v96, v96, v86, v87
	v_max3_f32 v96, v96, v88, v89
	v_max3_f32 v96, v96, v90, v91
	v_max3_f32 v96, v96, v92, v93
	v_max3_f32 v96, v96, v94, v95
	v_mov_b32_e32 v97, v96
	s_nop 1
	v_permlane32_swap_b32_e32 v96, v97
	v_max_f32_e32 v96, v96, v97
	v_fma_f32 v97, v96, s38, -v194
	v_cmp_ge_f32_e64 s[4:5], s68, v97
	v_add3_u32 v97, s23, v210, v190
	s_waitcnt vmcnt(1)
	ds_write_b128 v97, v[168:171]
	s_and_saveexec_b64 s[18:19], s[0:1]
	v_add3_u32 v97, s23, v216, v192
	ds_write_b128 v97, v[164:167]
	s_or_b64 exec, exec, s[18:19]
	s_cmpk_gt_u32 s17, 0x83
	s_cselect_b64 s[18:19], -1, 0
	v_lshl_add_u32 v97, s22, 14, v211
	s_and_b64 vcc, exec, s[18:19]
	s_waitcnt vmcnt(0)
	ds_write_b128 v97, v[172:175]
	s_cbranch_vccnz .LBB0_1886
	s_cmpk_lt_u32 s17, 0x7c
	s_cselect_b32 s22, 0, 0xffffffc0
	s_cselect_b32 s23, s74, s75
	s_add_i32 s22, s22, s76
	s_lshl_b32 s26, s22, 6
	s_add_i32 s26, s26, s23
	v_add_u32_e32 v97, s26, v189
	v_mad_i64_i32 v[98:99], s[22:23], v97, s62, v[196:197]
	global_load_dwordx4 v[168:171], v[98:99], off
	s_and_saveexec_b64 s[22:23], s[0:1]
	s_cbranch_execz .LBB0_1885
	v_add_u32_e32 v97, s26, v212
	v_mad_i64_i32 v[98:99], s[28:29], v97, s62, v[198:199]
	global_load_dwordx4 v[164:167], v[98:99], off

.LBB0_1893:
	s_waitcnt lgkmcnt(4)
	v_mfma_f32_32x32x64_f8f6f4 v[80:95], v[80:87], v[120:127], 0
	v_exp_f32_e32 v120, v153
	s_waitcnt lgkmcnt(0)
	s_barrier
	v_mfma_f32_32x32x64_f8f6f4 v[80:95], v[104:111], v[128:135], v[80:95]
	v_exp_f32_e32 v105, v158
	v_exp_f32_e32 v106, v159
	v_exp_f32_e32 v109, v154
	v_exp_f32_e32 v110, v155
	v_exp_f32_e32 v104, v161
	v_exp_f32_e32 v107, v156
	v_exp_f32_e32 v108, v157
	v_exp_f32_e32 v111, v152
	v_mfma_f32_32x32x64_f8f6f4 v[80:95], v[96:103], v[136:143], v[80:95]
	v_exp_f32_e32 v97, v178
	v_exp_f32_e32 v98, v179
	v_mov_b32_e32 v96, v187
	v_exp_f32_e32 v100, v176
	v_exp_f32_e32 v101, v177
	v_cvt_pk_fp8_f32 v96, v97, v98
	v_exp_f32_e32 v99, v162
	v_exp_f32_e32 v102, v163
	v_mov_b32_e32 v97, v187
	v_cvt_pk_fp8_f32 v96, v100, v101 op_sel:[0,0,1]
	v_mov_b32_e32 v98, v187
	v_cvt_pk_fp8_f32 v97, v99, v102
	v_mov_b32_e32 v99, v187
	v_max_f32_e32 v102, v194, v194
	v_exp_f32_e32 v103, v160
	s_nop 4
	v_max_f32_e32 v100, v80, v81
	v_max3_f32 v100, v100, v82, v83
	v_max3_f32 v100, v100, v84, v85
	v_max3_f32 v100, v100, v86, v87
	v_max3_f32 v100, v100, v88, v89
	v_max3_f32 v100, v100, v90, v91
	v_max3_f32 v100, v100, v92, v93
	v_max3_f32 v100, v100, v94, v95
	v_mov_b32_e32 v101, v100
	s_nop 1
	v_permlane32_swap_b32_e32 v100, v101
	v_max_f32_e32 v100, v100, v101
	v_fma_f32 v101, v100, s38, -v194
	v_fmamk_f32 v100, v100, 0x3dd53b94, v204
	v_cvt_pk_fp8_f32 v98, v105, v106
	v_cvt_pk_fp8_f32 v99, v109, v110
	v_max_f32_e32 v124, v102, v100
	v_sub_f32_e32 v100, v194, v124
	v_exp_f32_e32 v100, v100
	v_cmp_ge_f32_e32 vcc, s68, v101
	v_cvt_pk_fp8_f32 v97, v103, v104 op_sel:[0,0,1]
	v_cvt_pk_fp8_f32 v98, v107, v108 op_sel:[0,0,1]
	v_cvt_pk_fp8_f32 v99, v111, v120 op_sel:[0,0,1]
	s_cmp_eq_u64 vcc, exec
	s_cselect_b64 s[0:1], -1, 0
	v_cndmask_b32_e64 v125, v100, 1.0, s[0:1]
	v_cmp_gt_f32_e32 vcc, 1.0, v125
	s_cbranch_vccz .LBB0_1897
	s_and_saveexec_b64 s[4:5], s[2:3]
	ds_write_b32 v208, v125 offset:128
	s_or_b64 exec, exec, s[4:5]
	v_cvt_f32_fp8_e32 v126, v96
	v_cvt_f32_fp8_sdwa v127, v96 src0_sel:BYTE_1
	v_cvt_f32_fp8_sdwa v128, v96 src0_sel:BYTE_2
	v_cvt_f32_fp8_sdwa v96, v96 src0_sel:BYTE_3
	v_mul_f32_e32 v126, v125, v126
	v_mul_f32_e32 v127, v125, v127
	v_med3_f32 v126, v126, s67, v205
	v_mul_f32_e32 v96, v125, v96
	v_med3_f32 v127, v127, s67, v205
	v_med3_f32 v129, v96, s67, v205
	v_mov_b32_e32 v96, v187
	v_cvt_pk_fp8_f32 v96, v126, v127
	v_cvt_f32_fp8_e32 v126, v97
	v_cvt_f32_fp8_sdwa v127, v97 src0_sel:BYTE_1
	v_mul_f32_e32 v128, v125, v128
	v_med3_f32 v128, v128, s67, v205
	v_cvt_f32_fp8_sdwa v130, v97 src0_sel:BYTE_2
	v_cvt_pk_fp8_f32 v96, v128, v129 op_sel:[0,0,1]
	v_mul_f32_e32 v126, v125, v126
	v_mul_f32_e32 v127, v125, v127
	v_cvt_f32_fp8_sdwa v129, v97 src0_sel:BYTE_3
	v_med3_f32 v126, v126, s67, v205
	v_med3_f32 v127, v127, s67, v205
	v_mov_b32_e32 v97, v187
	v_cvt_pk_fp8_f32 v97, v126, v127
	v_mul_f32_e32 v128, v125, v130
	v_mul_f32_e32 v126, v125, v129
	v_med3_f32 v127, v128, s67, v205
	v_med3_f32 v126, v126, s67, v205
	v_cvt_pk_fp8_f32 v97, v127, v126 op_sel:[0,0,1]
	v_cvt_f32_fp8_e32 v126, v98
	v_cvt_f32_fp8_sdwa v127, v98 src0_sel:BYTE_1
	v_cvt_f32_fp8_sdwa v128, v98 src0_sel:BYTE_2
	v_cvt_f32_fp8_sdwa v98, v98 src0_sel:BYTE_3
	v_mul_f32_e32 v126, v125, v126
	v_mul_f32_e32 v127, v125, v127
	v_med3_f32 v126, v126, s67, v205
	v_mul_f32_e32 v98, v125, v98
	v_med3_f32 v127, v127, s67, v205
	v_med3_f32 v129, v98, s67, v205
	v_mov_b32_e32 v98, v187
	v_cvt_pk_fp8_f32 v98, v126, v127
	v_cvt_f32_fp8_e32 v126, v99
	v_cvt_f32_fp8_sdwa v127, v99 src0_sel:BYTE_1
	v_mul_f32_e32 v128, v125, v128
	v_med3_f32 v128, v128, s67, v205
	v_cvt_f32_fp8_sdwa v130, v99 src0_sel:BYTE_2
	v_cvt_pk_fp8_f32 v98, v128, v129 op_sel:[0,0,1]
	v_mul_f32_e32 v126, v125, v126
	v_mul_f32_e32 v127, v125, v127
	v_cvt_f32_fp8_sdwa v129, v99 src0_sel:BYTE_3
	v_med3_f32 v126, v126, s67, v205
	v_med3_f32 v127, v127, s67, v205
	v_mov_b32_e32 v99, v187
	v_cvt_pk_fp8_f32 v99, v126, v127
	s_waitcnt lgkmcnt(0)
	ds_read_b128 v[120:123], v213 offset:224
	ds_read_b128 v[108:111], v213 offset:192
	ds_read_b128 v[104:107], v213 offset:160
	ds_read_b128 v[100:103], v213 offset:128
	v_mul_f32_e32 v128, v125, v130
	v_mul_f32_e32 v125, v125, v129
	v_med3_f32 v126, v128, s67, v205
	v_med3_f32 v125, v125, s67, v205
	v_cvt_pk_fp8_f32 v99, v126, v125 op_sel:[0,0,1]
	s_waitcnt lgkmcnt(3)
	v_pk_mul_f32 v[62:63], v[62:63], v[122:123]
	s_waitcnt lgkmcnt(2)
	v_pk_mul_f32 v[58:59], v[58:59], v[110:111]
	s_waitcnt lgkmcnt(1)
	v_pk_mul_f32 v[54:55], v[54:55], v[106:107]
	s_waitcnt lgkmcnt(0)
	v_pk_mul_f32 v[50:51], v[50:51], v[102:103]
	v_pk_mul_f32 v[60:61], v[60:61], v[120:121]
	v_pk_mul_f32 v[56:57], v[56:57], v[108:109]
	v_pk_mul_f32 v[52:53], v[52:53], v[104:105]
	v_pk_mul_f32 v[48:49], v[48:49], v[100:101]
	v_pk_mul_f32 v[46:47], v[46:47], v[122:123]
	v_pk_mul_f32 v[42:43], v[42:43], v[110:111]
	v_pk_mul_f32 v[38:39], v[38:39], v[106:107]
	v_pk_mul_f32 v[34:35], v[34:35], v[102:103]
	v_pk_mul_f32 v[44:45], v[44:45], v[120:121]
	v_pk_mul_f32 v[40:41], v[40:41], v[108:109]
	v_pk_mul_f32 v[36:37], v[36:37], v[104:105]
	v_pk_mul_f32 v[32:33], v[32:33], v[100:101]
	v_pk_mul_f32 v[30:31], v[30:31], v[122:123]
	v_pk_mul_f32 v[26:27], v[26:27], v[110:111]
	v_pk_mul_f32 v[22:23], v[22:23], v[106:107]
	v_pk_mul_f32 v[18:19], v[18:19], v[102:103]
	v_pk_mul_f32 v[28:29], v[28:29], v[120:121]
	v_pk_mul_f32 v[24:25], v[24:25], v[108:109]
	v_pk_mul_f32 v[20:21], v[20:21], v[104:105]
	v_pk_mul_f32 v[16:17], v[16:17], v[100:101]
	v_pk_mul_f32 v[14:15], v[14:15], v[122:123]
	v_pk_mul_f32 v[10:11], v[10:11], v[110:111]
	v_pk_mul_f32 v[6:7], v[6:7], v[106:107]
	v_pk_mul_f32 v[2:3], v[2:3], v[102:103]
	v_pk_mul_f32 v[12:13], v[12:13], v[120:121]
	v_pk_mul_f32 v[8:9], v[8:9], v[108:109]
	v_pk_mul_f32 v[4:5], v[4:5], v[104:105]
	v_pk_mul_f32 v[0:1], v[0:1], v[100:101]
	v_pk_mul_f32 v[78:79], v[78:79], v[122:123]
	v_pk_mul_f32 v[74:75], v[74:75], v[110:111]
	v_pk_mul_f32 v[70:71], v[70:71], v[106:107]
	v_pk_mul_f32 v[66:67], v[66:67], v[102:103]
	v_pk_mul_f32 v[76:77], v[76:77], v[120:121]
	v_pk_mul_f32 v[72:73], v[72:73], v[108:109]
	v_pk_mul_f32 v[68:69], v[68:69], v[104:105]
	v_pk_mul_f32 v[64:65], v[64:65], v[100:101]

.LBB0_2191:
	ds_read_b128 v[8:11], v230
	ds_read_b128 v[12:15], v230 offset:1024
	ds_read_b128 v[0:3], v230 offset:2048
	ds_read_b128 v[4:7], v230 offset:3072
	v_lshl_add_u64 v[172:173], v[170:171], 0, s[2:3]
	s_add_i32 s92, s70, 0xc000
	v_lshl_add_u64 v[174:175], v[172:173], 0, s[8:9]
	s_mov_b32 m0, s92
	ds_read_b128 v[180:183], v227
	ds_read_b128 v[184:187], v227 offset:1024
	ds_read_b128 v[188:191], v227 offset:2048
	ds_read_b128 v[192:195], v227 offset:3072
	ds_read_b128 v[196:199], v227 offset:4096
	ds_read_b128 v[200:203], v227 offset:5120
	ds_read_b128 v[204:207], v227 offset:6144
	ds_read_b128 v[208:211], v227 offset:7168
	global_load_lds_dwordx4 v[174:175], off
	v_lshl_add_u64 v[174:175], v[168:169], 0, s[2:3]
	s_add_i32 s91, s70, 0xe000
	v_lshl_add_u64 v[176:177], v[174:175], 0, s[8:9]
	s_mov_b32 m0, s91
	s_nop 0
	global_load_lds_dwordx4 v[176:177], off
	s_waitcnt lgkmcnt(8)
	s_barrier
	s_waitcnt lgkmcnt(0)
	s_setprio 1
	s_waitcnt lgkmcnt(0)
	v_mfma_f32_16x16x128_f8f6f4 v[16:19], v[8:15], v[180:187], v[16:19]
	v_mfma_f32_16x16x128_f8f6f4 v[20:23], v[0:7], v[180:187], v[20:23]
	v_mfma_f32_16x16x128_f8f6f4 v[24:27], v[8:15], v[188:195], v[24:27]
	v_mfma_f32_16x16x128_f8f6f4 v[28:31], v[0:7], v[188:195], v[28:31]
	v_mfma_f32_16x16x128_f8f6f4 v[32:35], v[8:15], v[196:203], v[32:35]
	v_mfma_f32_16x16x128_f8f6f4 v[36:39], v[0:7], v[196:203], v[36:39]
	v_mfma_f32_16x16x128_f8f6f4 v[40:43], v[8:15], v[204:211], v[40:43]
	v_mfma_f32_16x16x128_f8f6f4 v[44:47], v[0:7], v[204:211], v[44:47]
	s_setprio 0
	s_barrier
	v_lshl_add_u64 v[176:177], v[146:147], 0, s[2:3]
	s_add_i32 s94, s80, s69
	v_lshl_add_u64 v[178:179], v[176:177], 0, s[10:11]
	s_mov_b32 m0, s94
	ds_read_b128 v[212:215], v231
	ds_read_b128 v[216:219], v231 offset:1024
	ds_read_b128 v[234:237], v231 offset:2048
	ds_read_b128 v[238:241], v231 offset:3072
	global_load_lds_dwordx4 v[178:179], off
	v_lshl_add_u64 v[178:179], v[144:145], 0, s[2:3]
	s_add_i32 s93, s94, 0x2000
	v_lshl_add_u64 v[220:221], v[178:179], 0, s[10:11]
	s_mov_b32 m0, s93
	s_nop 0
	global_load_lds_dwordx4 v[220:221], off
	s_barrier
	s_waitcnt lgkmcnt(0)
	s_setprio 1
	s_waitcnt lgkmcnt(0)
	v_mfma_f32_16x16x128_f8f6f4 v[48:51], v[212:219], v[180:187], v[48:51]
	v_mfma_f32_16x16x128_f8f6f4 v[52:55], v[234:241], v[180:187], v[52:55]
	v_mfma_f32_16x16x128_f8f6f4 v[56:59], v[212:219], v[188:195], v[56:59]
	v_mfma_f32_16x16x128_f8f6f4 v[60:63], v[234:241], v[188:195], v[60:63]
	v_mfma_f32_16x16x128_f8f6f4 v[64:67], v[212:219], v[196:203], v[64:67]
	v_mfma_f32_16x16x128_f8f6f4 v[68:71], v[234:241], v[196:203], v[68:71]
	v_mfma_f32_16x16x128_f8f6f4 v[72:75], v[212:219], v[204:211], v[72:75]
	v_mfma_f32_16x16x128_f8f6f4 v[76:79], v[234:241], v[204:211], v[76:79]
	s_setprio 0
	s_mov_b32 m0, s70
	v_lshl_add_u64 v[220:221], v[172:173], 0, s[10:11]
	s_barrier
	ds_read_b128 v[180:183], v227 offset:16384
	ds_read_b128 v[184:187], v227 offset:17408
	ds_read_b128 v[188:191], v227 offset:18432
	ds_read_b128 v[192:195], v227 offset:19456
	ds_read_b128 v[196:199], v227 offset:20480
	ds_read_b128 v[200:203], v227 offset:21504
	ds_read_b128 v[204:207], v227 offset:22528
	ds_read_b128 v[208:211], v227 offset:23552
	global_load_lds_dwordx4 v[220:221], off
	v_lshl_add_u64 v[220:221], v[174:175], 0, s[10:11]
	s_mov_b32 m0, s71
	s_nop 0
	global_load_lds_dwordx4 v[220:221], off
	s_barrier
	s_waitcnt lgkmcnt(0)
	s_setprio 1
	s_waitcnt lgkmcnt(0)
	v_mfma_f32_16x16x128_f8f6f4 v[80:83], v[8:15], v[180:187], v[80:83]
	v_mfma_f32_16x16x128_f8f6f4 v[84:87], v[0:7], v[180:187], v[84:87]
	v_mfma_f32_16x16x128_f8f6f4 v[88:91], v[8:15], v[188:195], v[88:91]
	v_mfma_f32_16x16x128_f8f6f4 v[92:95], v[0:7], v[188:195], v[92:95]
	v_mfma_f32_16x16x128_f8f6f4 v[96:99], v[8:15], v[196:203], v[96:99]
	v_mfma_f32_16x16x128_f8f6f4 v[100:103], v[0:7], v[196:203], v[100:103]
	v_mfma_f32_16x16x128_f8f6f4 v[104:107], v[8:15], v[204:211], v[104:107]
	v_mfma_f32_16x16x128_f8f6f4 v[108:111], v[0:7], v[204:211], v[108:111]
	s_setprio 0
	s_barrier
	s_add_i32 s52, s81, s69
	v_lshl_add_u64 v[0:1], v[176:177], 0, s[12:13]
	s_mov_b32 m0, s52
	s_add_i32 s95, s52, 0x2000
	global_load_lds_dwordx4 v[0:1], off
	v_lshl_add_u64 v[0:1], v[178:179], 0, s[12:13]
	s_mov_b32 m0, s95
	s_nop 0
	global_load_lds_dwordx4 v[0:1], off
	s_waitcnt vmcnt(6)
	s_barrier
	s_setprio 1
	v_mfma_f32_16x16x128_f8f6f4 v[112:115], v[212:219], v[180:187], v[112:115]
	v_mfma_f32_16x16x128_f8f6f4 v[116:119], v[234:241], v[180:187], v[116:119]
	v_mfma_f32_16x16x128_f8f6f4 v[120:123], v[212:219], v[188:195], v[120:123]
	v_mfma_f32_16x16x128_f8f6f4 v[124:127], v[234:241], v[188:195], v[124:127]
	v_mfma_f32_16x16x128_f8f6f4 v[128:131], v[212:219], v[196:203], v[128:131]
	v_mfma_f32_16x16x128_f8f6f4 v[132:135], v[234:241], v[196:203], v[132:135]
	v_mfma_f32_16x16x128_f8f6f4 v[136:139], v[212:219], v[204:211], v[136:139]
	v_mfma_f32_16x16x128_f8f6f4 v[140:143], v[234:241], v[204:211], v[140:143]
	s_setprio 0
	s_add_i32 s63, 0, 0x18000
	v_add_u32_e32 v234, s63, v226
	s_barrier
	ds_read_b128 v[0:3], v234
	ds_read_b128 v[4:7], v234 offset:1024
	ds_read_b128 v[8:11], v234 offset:2048
	ds_read_b128 v[12:15], v234 offset:3072
	s_mov_b32 m0, s72
	v_lshl_add_u64 v[212:213], v[172:173], 0, s[12:13]
	ds_read_b128 v[180:183], v227 offset:32768
	ds_read_b128 v[184:187], v227 offset:33792
	ds_read_b128 v[188:191], v227 offset:34816
	ds_read_b128 v[192:195], v227 offset:35840
	ds_read_b128 v[196:199], v227 offset:36864
	ds_read_b128 v[200:203], v227 offset:37888
	ds_read_b128 v[204:207], v227 offset:38912
	ds_read_b128 v[208:211], v227 offset:39936
	global_load_lds_dwordx4 v[212:213], off
	v_lshl_add_u64 v[212:213], v[174:175], 0, s[12:13]
	s_mov_b32 m0, s73
	s_nop 0
	global_load_lds_dwordx4 v[212:213], off
	s_waitcnt lgkmcnt(8)
	s_barrier
	s_waitcnt lgkmcnt(0)
	s_setprio 1
	s_waitcnt lgkmcnt(0)
	v_mfma_f32_16x16x128_f8f6f4 v[16:19], v[0:7], v[180:187], v[16:19]
	v_mfma_f32_16x16x128_f8f6f4 v[20:23], v[8:15], v[180:187], v[20:23]
	v_mfma_f32_16x16x128_f8f6f4 v[24:27], v[0:7], v[188:195], v[24:27]
	v_mfma_f32_16x16x128_f8f6f4 v[28:31], v[8:15], v[188:195], v[28:31]
	v_mfma_f32_16x16x128_f8f6f4 v[32:35], v[0:7], v[196:203], v[32:35]
	v_mfma_f32_16x16x128_f8f6f4 v[36:39], v[8:15], v[196:203], v[36:39]
	v_mfma_f32_16x16x128_f8f6f4 v[40:43], v[0:7], v[204:211], v[40:43]
	v_mfma_f32_16x16x128_f8f6f4 v[44:47], v[8:15], v[204:211], v[44:47]
	s_setprio 0
	s_barrier
	s_add_i32 s64, 0, 0x1c000
	s_add_i32 s63, s63, s69
	v_add_u32_e32 v233, s64, v226
	v_lshl_add_u64 v[220:221], v[176:177], 0, s[16:17]
	s_mov_b32 m0, s63
	s_add_i32 s62, s63, 0x2000
	ds_read_b128 v[212:215], v233
	ds_read_b128 v[216:219], v233 offset:1024
	ds_read_b128 v[236:239], v233 offset:2048
	ds_read_b128 v[240:243], v233 offset:3072
	global_load_lds_dwordx4 v[220:221], off
	v_lshl_add_u64 v[220:221], v[178:179], 0, s[16:17]
	s_mov_b32 m0, s62
	s_nop 0
	global_load_lds_dwordx4 v[220:221], off
	s_barrier
	s_waitcnt lgkmcnt(0)
	s_setprio 1
	s_waitcnt lgkmcnt(0)
	v_mfma_f32_16x16x128_f8f6f4 v[48:51], v[212:219], v[180:187], v[48:51]
	v_mfma_f32_16x16x128_f8f6f4 v[52:55], v[236:243], v[180:187], v[52:55]
	v_mfma_f32_16x16x128_f8f6f4 v[56:59], v[212:219], v[188:195], v[56:59]
	v_mfma_f32_16x16x128_f8f6f4 v[60:63], v[236:243], v[188:195], v[60:63]
	v_mfma_f32_16x16x128_f8f6f4 v[64:67], v[212:219], v[196:203], v[64:67]
	v_mfma_f32_16x16x128_f8f6f4 v[68:71], v[236:243], v[196:203], v[68:71]
	v_mfma_f32_16x16x128_f8f6f4 v[72:75], v[212:219], v[204:211], v[72:75]
	v_mfma_f32_16x16x128_f8f6f4 v[76:79], v[236:243], v[204:211], v[76:79]
	s_setprio 0
	s_mov_b32 m0, s77
	v_lshl_add_u64 v[172:173], v[172:173], 0, s[16:17]
	s_barrier
	ds_read_b128 v[180:183], v227 offset:49152
	ds_read_b128 v[184:187], v227 offset:50176
	ds_read_b128 v[188:191], v227 offset:51200
	ds_read_b128 v[192:195], v227 offset:52224
	ds_read_b128 v[196:199], v227 offset:53248
	ds_read_b128 v[200:203], v227 offset:54272
	ds_read_b128 v[204:207], v227 offset:55296
	ds_read_b128 v[208:211], v227 offset:56320
	global_load_lds_dwordx4 v[172:173], off
	v_lshl_add_u64 v[172:173], v[174:175], 0, s[16:17]
	s_mov_b32 m0, s78
	s_nop 0
	global_load_lds_dwordx4 v[172:173], off
	s_barrier
	s_waitcnt lgkmcnt(0)
	s_setprio 1
	s_waitcnt lgkmcnt(0)
	v_mfma_f32_16x16x128_f8f6f4 v[80:83], v[0:7], v[180:187], v[80:83]
	v_mfma_f32_16x16x128_f8f6f4 v[84:87], v[8:15], v[180:187], v[84:87]
	v_mfma_f32_16x16x128_f8f6f4 v[88:91], v[0:7], v[188:195], v[88:91]
	v_mfma_f32_16x16x128_f8f6f4 v[92:95], v[8:15], v[188:195], v[92:95]
	v_mfma_f32_16x16x128_f8f6f4 v[96:99], v[0:7], v[196:203], v[96:99]
	v_mfma_f32_16x16x128_f8f6f4 v[100:103], v[8:15], v[196:203], v[100:103]
	v_mfma_f32_16x16x128_f8f6f4 v[104:107], v[0:7], v[204:211], v[104:107]
	v_mfma_f32_16x16x128_f8f6f4 v[108:111], v[8:15], v[204:211], v[108:111]
	s_setprio 0
	s_barrier
	s_add_i32 s64, s64, s69
	v_lshl_add_u64 v[0:1], v[176:177], 0, s[18:19]
	s_mov_b32 m0, s64
	s_add_i32 s53, s64, 0x2000
	global_load_lds_dwordx4 v[0:1], off
	v_lshl_add_u64 v[0:1], v[178:179], 0, s[18:19]
	s_mov_b32 m0, s53
	s_nop 0
	global_load_lds_dwordx4 v[0:1], off
	s_waitcnt vmcnt(6)
	s_barrier
	s_setprio 1
	v_mfma_f32_16x16x128_f8f6f4 v[112:115], v[212:219], v[180:187], v[112:115]
	v_mfma_f32_16x16x128_f8f6f4 v[116:119], v[236:243], v[180:187], v[116:119]
	v_mfma_f32_16x16x128_f8f6f4 v[120:123], v[212:219], v[188:195], v[120:123]
	v_mfma_f32_16x16x128_f8f6f4 v[124:127], v[236:243], v[188:195], v[124:127]
	v_mfma_f32_16x16x128_f8f6f4 v[128:131], v[212:219], v[196:203], v[128:131]
	v_mfma_f32_16x16x128_f8f6f4 v[132:135], v[236:243], v[196:203], v[132:135]
	v_mfma_f32_16x16x128_f8f6f4 v[136:139], v[212:219], v[204:211], v[136:139]
	v_mfma_f32_16x16x128_f8f6f4 v[140:143], v[236:243], v[204:211], v[140:143]
	s_setprio 0
	s_add_i32 s42, s42, 2
	s_add_u32 s2, s2, 0x100
	s_addc_u32 s3, s3, 0
	s_cmp_gt_u32 s42, 5
	s_barrier
	s_cbranch_scc0 .LBB0_2191
	s_add_u32 s42, s65, s87
	s_addc_u32 s43, s66, 0
	s_add_u32 s44, s67, s88
	s_addc_u32 s45, s68, 0
	s_and_b64 s[2:3], vcc, exec
	s_mul_i32 s2, s90, 24
	s_cselect_b32 s51, s43, s47
	s_cselect_b32 s50, s42, s46
	s_add_i32 s56, s2, s89
	s_ashr_i32 s57, s56, 31
	s_lshl_b64 s[2:3], s[56:57], 16
	s_add_u32 s2, s75, s2
	s_addc_u32 s3, s76, s3
	s_add_i32 s54, s56, 8
	s_ashr_i32 s55, s54, 31
	v_mov_b32_e32 v156, v229
	s_lshl_b64 s[54:55], s[54:55], 16
	s_nop 7
	s_nop 7
	s_nop 7
	s_add_u32 s54, s75, s54
	s_addc_u32 s55, s76, s55
	global_load_dwordx2 v[210:211], v156, s[2:3]
	global_load_dwordx2 v[216:217], v156, s[54:55]
	global_load_dwordx2 v[206:207], v156, s[2:3] offset:512
	global_load_dwordx2 v[208:209], v156, s[54:55] offset:512
	global_load_dwordx2 v[202:203], v156, s[2:3] offset:1024
	global_load_dwordx2 v[204:205], v156, s[54:55] offset:1024
	global_load_dwordx2 v[198:199], v156, s[2:3] offset:1536
	global_load_dwordx2 v[200:201], v156, s[54:55] offset:1536
	global_load_dwordx2 v[194:195], v156, s[2:3] offset:2048
	global_load_dwordx2 v[196:197], v156, s[54:55] offset:2048
	global_load_dwordx2 v[190:191], v156, s[2:3] offset:2560
	global_load_dwordx2 v[192:193], v156, s[54:55] offset:2560
	global_load_dwordx2 v[186:187], v156, s[2:3] offset:3072
	global_load_dwordx2 v[188:189], v156, s[54:55] offset:3072
	global_load_dwordx2 v[182:183], v156, s[2:3] offset:3584
	global_load_dwordx2 v[184:185], v156, s[54:55] offset:3584
	v_lshl_add_u64 v[0:1], s[2:3], 0, v[156:157]
	v_lshl_add_u64 v[2:3], s[54:55], 0, v[156:157]
	v_add_co_u32_e64 v0, s[2:3], s82, v0
	s_waitcnt vmcnt(0)
	v_cvt_f32_ubyte3_e32 v237, v210
	v_cvt_f32_ubyte0_e32 v156, v216
	v_add_f32_e32 v156, 0.5, v156
	v_rcp_f32_e32 v218, v156
	v_cvt_f32_ubyte0_e32 v156, v217
	v_add_f32_e32 v156, 0.5, v156
	v_rcp_f32_e32 v212, v156
	v_cvt_f32_ubyte1_e32 v156, v216
	v_add_f32_e32 v156, 0.5, v156
	v_rcp_f32_e32 v219, v156
	v_cvt_f32_ubyte1_e32 v156, v217
	v_add_f32_e32 v156, 0.5, v156
	v_rcp_f32_e32 v213, v156
	v_cvt_f32_ubyte2_e32 v156, v216
	v_add_f32_e32 v156, 0.5, v156
	v_rcp_f32_e32 v220, v156
	v_cvt_f32_ubyte2_e32 v156, v217
	v_add_f32_e32 v156, 0.5, v156
	v_rcp_f32_e32 v214, v156
	v_cvt_f32_ubyte3_e32 v156, v216
	v_add_f32_e32 v156, 0.5, v156
	v_rcp_f32_e32 v221, v156
	v_cvt_f32_ubyte3_e32 v156, v217
	v_add_f32_e32 v156, 0.5, v156
	v_cvt_f32_ubyte1_e32 v217, v210
	v_cvt_f32_ubyte0_e32 v216, v210
	v_cvt_f32_ubyte2_e32 v236, v210
	v_rcp_f32_e32 v215, v156
	v_pk_add_f32 v[236:237], v[236:237], 0.5 op_sel_hi:[1,0]
	v_pk_add_f32 v[216:217], v[216:217], 0.5 op_sel_hi:[1,0]
	v_cvt_f32_ubyte0_e32 v156, v208
	v_pk_mul_f32 v[216:217], v[216:217], v[218:219]
	v_pk_mul_f32 v[218:219], v[236:237], v[220:221]
	v_pk_mul_f32 v[16:17], v[16:17], v[216:217]
	v_pk_mul_f32 v[18:19], v[18:19], v[218:219]
	v_cvt_f32_ubyte3_e32 v219, v211
	v_cvt_f32_ubyte2_e32 v218, v211
	v_cvt_f32_ubyte1_e32 v217, v211
	v_cvt_f32_ubyte0_e32 v216, v211
	v_pk_add_f32 v[210:211], v[218:219], 0.5 op_sel_hi:[1,0]
	v_add_f32_e32 v156, 0.5, v156
	v_pk_mul_f32 v[210:211], v[210:211], v[214:215]
	v_pk_add_f32 v[216:217], v[216:217], 0.5 op_sel_hi:[1,0]
	v_pk_mul_f32 v[22:23], v[22:23], v[210:211]
	v_rcp_f32_e32 v210, v156
	v_cvt_f32_ubyte0_e32 v156, v209
	v_pk_mul_f32 v[212:213], v[216:217], v[212:213]
	v_add_f32_e32 v156, 0.5, v156
	v_pk_mul_f32 v[20:21], v[20:21], v[212:213]
	v_rcp_f32_e32 v212, v156
	v_cvt_f32_ubyte1_e32 v156, v208
	v_add_f32_e32 v156, 0.5, v156
	v_rcp_f32_e32 v211, v156
	v_cvt_f32_ubyte1_e32 v156, v209
	v_add_f32_e32 v156, 0.5, v156
	v_rcp_f32_e32 v213, v156
	v_cvt_f32_ubyte2_e32 v156, v208
	v_add_f32_e32 v156, 0.5, v156
	v_rcp_f32_e32 v214, v156
	v_cvt_f32_ubyte2_e32 v156, v209
	v_add_f32_e32 v156, 0.5, v156
	v_rcp_f32_e32 v216, v156
	v_cvt_f32_ubyte3_e32 v156, v208
	v_add_f32_e32 v156, 0.5, v156
	v_rcp_f32_e32 v215, v156
	v_cvt_f32_ubyte3_e32 v156, v209
	v_add_f32_e32 v156, 0.5, v156
	v_cvt_f32_ubyte1_e32 v209, v206
	v_cvt_f32_ubyte0_e32 v208, v206
	v_cvt_f32_ubyte3_e32 v219, v206
	v_cvt_f32_ubyte2_e32 v218, v206
	v_rcp_f32_e32 v217, v156
	v_pk_add_f32 v[218:219], v[218:219], 0.5 op_sel_hi:[1,0]
	v_pk_add_f32 v[208:209], v[208:209], 0.5 op_sel_hi:[1,0]
	v_cvt_f32_ubyte0_e32 v156, v204
	v_pk_mul_f32 v[208:209], v[208:209], v[210:211]
	v_pk_mul_f32 v[210:211], v[218:219], v[214:215]
	v_pk_mul_f32 v[48:49], v[48:49], v[208:209]
	v_pk_mul_f32 v[50:51], v[50:51], v[210:211]
	v_cvt_f32_ubyte3_e32 v211, v207
	v_cvt_f32_ubyte2_e32 v210, v207
	v_cvt_f32_ubyte1_e32 v209, v207
	v_cvt_f32_ubyte0_e32 v208, v207
	v_pk_add_f32 v[206:207], v[210:211], 0.5 op_sel_hi:[1,0]
	v_add_f32_e32 v156, 0.5, v156
	v_pk_mul_f32 v[206:207], v[206:207], v[216:217]
	v_pk_add_f32 v[208:209], v[208:209], 0.5 op_sel_hi:[1,0]
	v_pk_mul_f32 v[54:55], v[54:55], v[206:207]
	v_rcp_f32_e32 v206, v156
	v_cvt_f32_ubyte0_e32 v156, v205
	v_pk_mul_f32 v[208:209], v[208:209], v[212:213]
	v_add_f32_e32 v156, 0.5, v156
	v_pk_mul_f32 v[52:53], v[52:53], v[208:209]
	v_rcp_f32_e32 v208, v156
	v_cvt_f32_ubyte1_e32 v156, v204
	v_add_f32_e32 v156, 0.5, v156
	v_rcp_f32_e32 v207, v156
	v_cvt_f32_ubyte1_e32 v156, v205
	v_add_f32_e32 v156, 0.5, v156
	v_rcp_f32_e32 v209, v156
	v_cvt_f32_ubyte2_e32 v156, v204
	v_add_f32_e32 v156, 0.5, v156
	v_rcp_f32_e32 v210, v156
	v_cvt_f32_ubyte2_e32 v156, v205
	v_add_f32_e32 v156, 0.5, v156
	v_rcp_f32_e32 v212, v156
	v_cvt_f32_ubyte3_e32 v156, v204
	v_add_f32_e32 v156, 0.5, v156
	v_rcp_f32_e32 v211, v156
	v_cvt_f32_ubyte3_e32 v156, v205
	v_add_f32_e32 v156, 0.5, v156
	v_cvt_f32_ubyte1_e32 v205, v202
	v_cvt_f32_ubyte0_e32 v204, v202
	v_cvt_f32_ubyte3_e32 v215, v202
	v_cvt_f32_ubyte2_e32 v214, v202
	v_rcp_f32_e32 v213, v156
	v_pk_add_f32 v[214:215], v[214:215], 0.5 op_sel_hi:[1,0]
	v_pk_add_f32 v[204:205], v[204:205], 0.5 op_sel_hi:[1,0]
	v_cvt_f32_ubyte0_e32 v156, v200
	v_pk_mul_f32 v[204:205], v[204:205], v[206:207]
	v_pk_mul_f32 v[206:207], v[214:215], v[210:211]
	v_pk_mul_f32 v[24:25], v[24:25], v[204:205]
	v_pk_mul_f32 v[26:27], v[26:27], v[206:207]
	v_cvt_f32_ubyte3_e32 v207, v203
	v_cvt_f32_ubyte2_e32 v206, v203
	v_cvt_f32_ubyte1_e32 v205, v203
	v_cvt_f32_ubyte0_e32 v204, v203
	v_pk_add_f32 v[202:203], v[206:207], 0.5 op_sel_hi:[1,0]
	v_add_f32_e32 v156, 0.5, v156
	v_pk_mul_f32 v[202:203], v[202:203], v[212:213]
	v_pk_add_f32 v[204:205], v[204:205], 0.5 op_sel_hi:[1,0]
	v_pk_mul_f32 v[30:31], v[30:31], v[202:203]
	v_rcp_f32_e32 v202, v156
	v_cvt_f32_ubyte0_e32 v156, v201
	v_pk_mul_f32 v[204:205], v[204:205], v[208:209]
	v_add_f32_e32 v156, 0.5, v156
	v_pk_mul_f32 v[28:29], v[28:29], v[204:205]
	v_rcp_f32_e32 v204, v156
	v_cvt_f32_ubyte1_e32 v156, v200
	v_add_f32_e32 v156, 0.5, v156
	v_rcp_f32_e32 v203, v156
	v_cvt_f32_ubyte1_e32 v156, v201
	v_add_f32_e32 v156, 0.5, v156
	v_rcp_f32_e32 v205, v156
	v_cvt_f32_ubyte2_e32 v156, v200
	v_add_f32_e32 v156, 0.5, v156
	v_rcp_f32_e32 v206, v156
	v_cvt_f32_ubyte2_e32 v156, v201
	v_add_f32_e32 v156, 0.5, v156
	v_rcp_f32_e32 v208, v156
	v_cvt_f32_ubyte3_e32 v156, v200
	v_add_f32_e32 v156, 0.5, v156
	v_rcp_f32_e32 v207, v156
	v_cvt_f32_ubyte3_e32 v156, v201
	v_add_f32_e32 v156, 0.5, v156
	v_cvt_f32_ubyte1_e32 v201, v198
	v_cvt_f32_ubyte0_e32 v200, v198
	v_cvt_f32_ubyte3_e32 v211, v198
	v_cvt_f32_ubyte2_e32 v210, v198
	v_rcp_f32_e32 v209, v156
	v_pk_add_f32 v[210:211], v[210:211], 0.5 op_sel_hi:[1,0]
	v_pk_add_f32 v[200:201], v[200:201], 0.5 op_sel_hi:[1,0]
	v_cvt_f32_ubyte0_e32 v156, v196
	v_pk_mul_f32 v[200:201], v[200:201], v[202:203]
	v_pk_mul_f32 v[202:203], v[210:211], v[206:207]
	v_pk_mul_f32 v[56:57], v[56:57], v[200:201]
	v_pk_mul_f32 v[58:59], v[58:59], v[202:203]
	v_cvt_f32_ubyte3_e32 v203, v199
	v_cvt_f32_ubyte2_e32 v202, v199
	v_cvt_f32_ubyte1_e32 v201, v199
	v_cvt_f32_ubyte0_e32 v200, v199
	v_pk_add_f32 v[198:199], v[202:203], 0.5 op_sel_hi:[1,0]
	v_add_f32_e32 v156, 0.5, v156
	v_pk_mul_f32 v[198:199], v[198:199], v[208:209]
	v_pk_add_f32 v[200:201], v[200:201], 0.5 op_sel_hi:[1,0]
	v_pk_mul_f32 v[62:63], v[62:63], v[198:199]
	v_rcp_f32_e32 v198, v156
	v_cvt_f32_ubyte0_e32 v156, v197
	v_pk_mul_f32 v[200:201], v[200:201], v[204:205]
	v_add_f32_e32 v156, 0.5, v156
	v_pk_mul_f32 v[60:61], v[60:61], v[200:201]
	v_rcp_f32_e32 v200, v156
	v_cvt_f32_ubyte1_e32 v156, v196
	v_add_f32_e32 v156, 0.5, v156
	v_rcp_f32_e32 v199, v156
	v_cvt_f32_ubyte1_e32 v156, v197
	v_add_f32_e32 v156, 0.5, v156
	v_rcp_f32_e32 v201, v156
	v_cvt_f32_ubyte2_e32 v156, v196
	v_add_f32_e32 v156, 0.5, v156
	v_rcp_f32_e32 v202, v156
	v_cvt_f32_ubyte2_e32 v156, v197
	v_addc_co_u32_e64 v1, s[2:3], 0, v1, s[2:3]
	v_add_f32_e32 v156, 0.5, v156
	v_add_co_u32_e64 v6, s[2:3], s82, v2
	v_rcp_f32_e32 v204, v156
	v_cvt_f32_ubyte3_e32 v156, v196
	v_addc_co_u32_e64 v7, s[2:3], 0, v3, s[2:3]
	v_add_f32_e32 v156, 0.5, v156
	global_load_dwordx2 v[178:179], v[0:1], off
	global_load_dwordx2 v[180:181], v[6:7], off
	global_load_dwordx2 v[174:175], v[0:1], off offset:512
	global_load_dwordx2 v[176:177], v[6:7], off offset:512
	global_load_dwordx2 v[170:171], v[0:1], off offset:1024
	global_load_dwordx2 v[172:173], v[6:7], off offset:1024
	global_load_dwordx2 v[144:145], v[0:1], off offset:1536
	global_load_dwordx2 v[146:147], v[6:7], off offset:1536
	global_load_dwordx2 v[12:13], v[0:1], off offset:2048
	global_load_dwordx2 v[14:15], v[6:7], off offset:2048
	global_load_dwordx2 v[8:9], v[0:1], off offset:2560
	global_load_dwordx2 v[10:11], v[6:7], off offset:2560
	global_load_dwordx2 v[2:3], v[0:1], off offset:3072
	global_load_dwordx2 v[4:5], v[6:7], off offset:3072
	s_nop 0
	global_load_dwordx2 v[0:1], v[0:1], off offset:3584
	s_nop 0
	global_load_dwordx2 v[6:7], v[6:7], off offset:3584
	v_rcp_f32_e32 v203, v156
	v_cvt_f32_ubyte3_e32 v156, v197
	v_add_f32_e32 v156, 0.5, v156
	v_cvt_f32_ubyte1_e32 v197, v194
	v_cvt_f32_ubyte0_e32 v196, v194
	v_cvt_f32_ubyte3_e32 v207, v194
	v_cvt_f32_ubyte2_e32 v206, v194
	v_rcp_f32_e32 v205, v156
	v_pk_add_f32 v[206:207], v[206:207], 0.5 op_sel_hi:[1,0]
	v_pk_add_f32 v[196:197], v[196:197], 0.5 op_sel_hi:[1,0]
	v_cvt_f32_ubyte0_e32 v156, v192
	v_pk_mul_f32 v[196:197], v[196:197], v[198:199]
	v_pk_mul_f32 v[198:199], v[206:207], v[202:203]
	v_pk_mul_f32 v[32:33], v[32:33], v[196:197]
	v_pk_mul_f32 v[34:35], v[34:35], v[198:199]
	v_cvt_f32_ubyte3_e32 v199, v195
	v_cvt_f32_ubyte2_e32 v198, v195
	v_cvt_f32_ubyte1_e32 v197, v195
	v_cvt_f32_ubyte0_e32 v196, v195
	v_pk_add_f32 v[194:195], v[198:199], 0.5 op_sel_hi:[1,0]
	v_add_f32_e32 v156, 0.5, v156
	v_pk_mul_f32 v[194:195], v[194:195], v[204:205]
	v_pk_add_f32 v[196:197], v[196:197], 0.5 op_sel_hi:[1,0]
	v_pk_mul_f32 v[38:39], v[38:39], v[194:195]
	v_rcp_f32_e32 v194, v156
	v_cvt_f32_ubyte0_e32 v156, v193
	v_pk_mul_f32 v[196:197], v[196:197], v[200:201]
	v_add_f32_e32 v156, 0.5, v156
	v_pk_mul_f32 v[36:37], v[36:37], v[196:197]
	v_rcp_f32_e32 v196, v156
	v_cvt_f32_ubyte1_e32 v156, v192
	v_add_f32_e32 v156, 0.5, v156
	v_rcp_f32_e32 v195, v156
	v_cvt_f32_ubyte1_e32 v156, v193
	v_add_f32_e32 v156, 0.5, v156
	v_rcp_f32_e32 v197, v156
	v_cvt_f32_ubyte2_e32 v156, v192
	v_add_f32_e32 v156, 0.5, v156
	v_rcp_f32_e32 v198, v156
	v_cvt_f32_ubyte2_e32 v156, v193
	v_add_f32_e32 v156, 0.5, v156
	v_rcp_f32_e32 v200, v156
	v_cvt_f32_ubyte3_e32 v156, v192
	v_add_f32_e32 v156, 0.5, v156
	v_rcp_f32_e32 v199, v156
	v_cvt_f32_ubyte3_e32 v156, v193
	v_add_f32_e32 v156, 0.5, v156
	v_cvt_f32_ubyte1_e32 v193, v190
	v_cvt_f32_ubyte0_e32 v192, v190
	v_cvt_f32_ubyte3_e32 v203, v190
	v_cvt_f32_ubyte2_e32 v202, v190
	v_rcp_f32_e32 v201, v156
	v_pk_add_f32 v[202:203], v[202:203], 0.5 op_sel_hi:[1,0]
	v_pk_add_f32 v[192:193], v[192:193], 0.5 op_sel_hi:[1,0]
	v_cvt_f32_ubyte0_e32 v156, v188
	v_pk_mul_f32 v[192:193], v[192:193], v[194:195]
	v_pk_mul_f32 v[194:195], v[202:203], v[198:199]
	v_pk_mul_f32 v[64:65], v[64:65], v[192:193]
	v_pk_mul_f32 v[66:67], v[66:67], v[194:195]
	v_cvt_f32_ubyte3_e32 v195, v191
	v_cvt_f32_ubyte2_e32 v194, v191
	v_cvt_f32_ubyte1_e32 v193, v191
	v_cvt_f32_ubyte0_e32 v192, v191
	v_pk_add_f32 v[190:191], v[194:195], 0.5 op_sel_hi:[1,0]
	v_add_f32_e32 v156, 0.5, v156
	v_pk_mul_f32 v[190:191], v[190:191], v[200:201]
	v_pk_add_f32 v[192:193], v[192:193], 0.5 op_sel_hi:[1,0]
	v_pk_mul_f32 v[70:71], v[70:71], v[190:191]
	v_rcp_f32_e32 v190, v156
	v_cvt_f32_ubyte0_e32 v156, v189
	v_pk_mul_f32 v[192:193], v[192:193], v[196:197]
	v_add_f32_e32 v156, 0.5, v156
	v_pk_mul_f32 v[68:69], v[68:69], v[192:193]
	v_rcp_f32_e32 v192, v156
	v_cvt_f32_ubyte1_e32 v156, v188
	v_add_f32_e32 v156, 0.5, v156
	v_rcp_f32_e32 v191, v156
	v_cvt_f32_ubyte1_e32 v156, v189
	v_add_f32_e32 v156, 0.5, v156
	v_rcp_f32_e32 v193, v156
	v_cvt_f32_ubyte2_e32 v156, v188
	v_add_f32_e32 v156, 0.5, v156
	v_rcp_f32_e32 v194, v156
	v_cvt_f32_ubyte2_e32 v156, v189
	v_add_f32_e32 v156, 0.5, v156
	v_rcp_f32_e32 v196, v156
	v_cvt_f32_ubyte3_e32 v156, v188
	v_add_f32_e32 v156, 0.5, v156
	v_rcp_f32_e32 v195, v156
	v_cvt_f32_ubyte3_e32 v156, v189
	v_add_f32_e32 v156, 0.5, v156
	v_cvt_f32_ubyte1_e32 v189, v186
	v_cvt_f32_ubyte0_e32 v188, v186
	v_cvt_f32_ubyte3_e32 v199, v186
	v_cvt_f32_ubyte2_e32 v198, v186
	v_rcp_f32_e32 v197, v156
	v_pk_add_f32 v[198:199], v[198:199], 0.5 op_sel_hi:[1,0]
	v_pk_add_f32 v[188:189], v[188:189], 0.5 op_sel_hi:[1,0]
	v_cvt_f32_ubyte0_e32 v156, v184
	v_pk_mul_f32 v[188:189], v[188:189], v[190:191]
	v_pk_mul_f32 v[190:191], v[198:199], v[194:195]
	v_pk_mul_f32 v[40:41], v[40:41], v[188:189]
	v_pk_mul_f32 v[42:43], v[42:43], v[190:191]
	v_cvt_f32_ubyte3_e32 v191, v187
	v_cvt_f32_ubyte2_e32 v190, v187
	v_cvt_f32_ubyte1_e32 v189, v187
	v_cvt_f32_ubyte0_e32 v188, v187
	v_pk_add_f32 v[186:187], v[190:191], 0.5 op_sel_hi:[1,0]
	v_add_f32_e32 v156, 0.5, v156
	v_pk_mul_f32 v[186:187], v[186:187], v[196:197]
	v_pk_add_f32 v[188:189], v[188:189], 0.5 op_sel_hi:[1,0]
	v_pk_mul_f32 v[46:47], v[46:47], v[186:187]
	v_rcp_f32_e32 v186, v156
	v_cvt_f32_ubyte0_e32 v156, v185
	v_pk_mul_f32 v[188:189], v[188:189], v[192:193]
	v_add_f32_e32 v156, 0.5, v156
	v_pk_mul_f32 v[44:45], v[44:45], v[188:189]
	v_rcp_f32_e32 v188, v156
	v_cvt_f32_ubyte1_e32 v156, v184
	v_add_f32_e32 v156, 0.5, v156
	v_rcp_f32_e32 v187, v156
	v_cvt_f32_ubyte1_e32 v156, v185
	v_add_f32_e32 v156, 0.5, v156
	v_rcp_f32_e32 v189, v156
	v_cvt_f32_ubyte2_e32 v156, v184
	v_add_f32_e32 v156, 0.5, v156
	v_rcp_f32_e32 v190, v156
	v_cvt_f32_ubyte2_e32 v156, v185
	v_add_f32_e32 v156, 0.5, v156
	v_rcp_f32_e32 v192, v156
	v_cvt_f32_ubyte3_e32 v156, v184
	v_add_f32_e32 v156, 0.5, v156
	v_rcp_f32_e32 v191, v156
	v_cvt_f32_ubyte3_e32 v156, v185
	v_add_f32_e32 v156, 0.5, v156
	v_cvt_f32_ubyte1_e32 v185, v182
	v_cvt_f32_ubyte0_e32 v184, v182
	v_cvt_f32_ubyte3_e32 v195, v182
	v_cvt_f32_ubyte2_e32 v194, v182
	v_rcp_f32_e32 v193, v156
	v_pk_add_f32 v[194:195], v[194:195], 0.5 op_sel_hi:[1,0]
	v_pk_add_f32 v[184:185], v[184:185], 0.5 op_sel_hi:[1,0]
	s_waitcnt vmcnt(0)
	v_cvt_f32_ubyte0_e32 v156, v180
	v_pk_mul_f32 v[184:185], v[184:185], v[186:187]
	v_pk_mul_f32 v[186:187], v[194:195], v[190:191]
	v_pk_mul_f32 v[72:73], v[72:73], v[184:185]
	v_pk_mul_f32 v[74:75], v[74:75], v[186:187]
	v_cvt_f32_ubyte3_e32 v187, v183
	v_cvt_f32_ubyte2_e32 v186, v183
	v_cvt_f32_ubyte1_e32 v185, v183
	v_cvt_f32_ubyte0_e32 v184, v183
	v_pk_add_f32 v[182:183], v[186:187], 0.5 op_sel_hi:[1,0]
	v_add_f32_e32 v156, 0.5, v156
	v_pk_mul_f32 v[182:183], v[182:183], v[192:193]
	v_pk_add_f32 v[184:185], v[184:185], 0.5 op_sel_hi:[1,0]
	v_pk_mul_f32 v[78:79], v[78:79], v[182:183]
	v_rcp_f32_e32 v182, v156
	v_cvt_f32_ubyte0_e32 v156, v181
	v_pk_mul_f32 v[184:185], v[184:185], v[188:189]
	v_add_f32_e32 v156, 0.5, v156
	v_pk_mul_f32 v[76:77], v[76:77], v[184:185]
	v_rcp_f32_e32 v184, v156
	v_cvt_f32_ubyte1_e32 v156, v180
	v_add_f32_e32 v156, 0.5, v156
	v_rcp_f32_e32 v183, v156
	v_cvt_f32_ubyte1_e32 v156, v181
	v_add_f32_e32 v156, 0.5, v156
	v_rcp_f32_e32 v185, v156
	v_cvt_f32_ubyte2_e32 v156, v180
	v_add_f32_e32 v156, 0.5, v156
	v_rcp_f32_e32 v186, v156
	v_cvt_f32_ubyte2_e32 v156, v181
	v_add_f32_e32 v156, 0.5, v156
	v_rcp_f32_e32 v188, v156
	v_cvt_f32_ubyte3_e32 v156, v180
	v_add_f32_e32 v156, 0.5, v156
	v_rcp_f32_e32 v187, v156
	v_cvt_f32_ubyte3_e32 v156, v181
	v_add_f32_e32 v156, 0.5, v156
	v_cvt_f32_ubyte1_e32 v181, v178
	v_cvt_f32_ubyte0_e32 v180, v178
	v_cvt_f32_ubyte3_e32 v191, v178
	v_cvt_f32_ubyte2_e32 v190, v178
	v_rcp_f32_e32 v189, v156
	v_pk_add_f32 v[190:191], v[190:191], 0.5 op_sel_hi:[1,0]
	v_pk_add_f32 v[180:181], v[180:181], 0.5 op_sel_hi:[1,0]
	v_cvt_f32_ubyte0_e32 v156, v176
	v_pk_mul_f32 v[180:181], v[180:181], v[182:183]
	v_pk_mul_f32 v[182:183], v[190:191], v[186:187]
	v_pk_mul_f32 v[80:81], v[80:81], v[180:181]
	v_pk_mul_f32 v[82:83], v[82:83], v[182:183]
	v_cvt_f32_ubyte3_e32 v183, v179
	v_cvt_f32_ubyte2_e32 v182, v179
	v_cvt_f32_ubyte1_e32 v181, v179
	v_cvt_f32_ubyte0_e32 v180, v179
	v_pk_add_f32 v[178:179], v[182:183], 0.5 op_sel_hi:[1,0]
	v_add_f32_e32 v156, 0.5, v156
	v_pk_mul_f32 v[178:179], v[178:179], v[188:189]
	v_pk_add_f32 v[180:181], v[180:181], 0.5 op_sel_hi:[1,0]
	v_pk_mul_f32 v[86:87], v[86:87], v[178:179]
	v_rcp_f32_e32 v178, v156
	v_cvt_f32_ubyte0_e32 v156, v177
	v_pk_mul_f32 v[180:181], v[180:181], v[184:185]
	v_add_f32_e32 v156, 0.5, v156
	v_pk_mul_f32 v[84:85], v[84:85], v[180:181]
	v_rcp_f32_e32 v180, v156
	v_cvt_f32_ubyte1_e32 v156, v176
	v_add_f32_e32 v156, 0.5, v156
	v_rcp_f32_e32 v179, v156
	v_cvt_f32_ubyte1_e32 v156, v177
	v_add_f32_e32 v156, 0.5, v156
	v_rcp_f32_e32 v181, v156
	v_cvt_f32_ubyte2_e32 v156, v176
	v_add_f32_e32 v156, 0.5, v156
	v_rcp_f32_e32 v182, v156
	v_cvt_f32_ubyte2_e32 v156, v177
	v_add_f32_e32 v156, 0.5, v156
	v_rcp_f32_e32 v184, v156
	v_cvt_f32_ubyte3_e32 v156, v176
	v_add_f32_e32 v156, 0.5, v156
	v_rcp_f32_e32 v183, v156
	v_cvt_f32_ubyte3_e32 v156, v177
	v_add_f32_e32 v156, 0.5, v156
	v_cvt_f32_ubyte1_e32 v177, v174
	v_cvt_f32_ubyte0_e32 v176, v174
	v_cvt_f32_ubyte3_e32 v187, v174
	v_cvt_f32_ubyte2_e32 v186, v174
	v_rcp_f32_e32 v185, v156
	v_pk_add_f32 v[186:187], v[186:187], 0.5 op_sel_hi:[1,0]
	v_pk_add_f32 v[176:177], v[176:177], 0.5 op_sel_hi:[1,0]
	v_cvt_f32_ubyte0_e32 v156, v172
	v_pk_mul_f32 v[176:177], v[176:177], v[178:179]
	v_pk_mul_f32 v[178:179], v[186:187], v[182:183]
	v_pk_mul_f32 v[112:113], v[112:113], v[176:177]
	v_pk_mul_f32 v[114:115], v[114:115], v[178:179]
	v_cvt_f32_ubyte3_e32 v179, v175
	v_cvt_f32_ubyte2_e32 v178, v175
	v_cvt_f32_ubyte1_e32 v177, v175
	v_cvt_f32_ubyte0_e32 v176, v175
	v_pk_add_f32 v[174:175], v[178:179], 0.5 op_sel_hi:[1,0]
	v_add_f32_e32 v156, 0.5, v156
	v_pk_mul_f32 v[174:175], v[174:175], v[184:185]
	v_pk_add_f32 v[176:177], v[176:177], 0.5 op_sel_hi:[1,0]
	v_pk_mul_f32 v[118:119], v[118:119], v[174:175]
	v_rcp_f32_e32 v174, v156
	v_cvt_f32_ubyte0_e32 v156, v173
	v_pk_mul_f32 v[176:177], v[176:177], v[180:181]
	v_add_f32_e32 v156, 0.5, v156
	v_pk_mul_f32 v[116:117], v[116:117], v[176:177]
	v_rcp_f32_e32 v176, v156
	v_cvt_f32_ubyte1_e32 v156, v172
	v_add_f32_e32 v156, 0.5, v156
	v_rcp_f32_e32 v175, v156
	v_cvt_f32_ubyte1_e32 v156, v173
	v_add_f32_e32 v156, 0.5, v156
	v_rcp_f32_e32 v177, v156
	v_cvt_f32_ubyte2_e32 v156, v172
	v_add_f32_e32 v156, 0.5, v156
	v_rcp_f32_e32 v178, v156
	v_cvt_f32_ubyte2_e32 v156, v173
	v_add_f32_e32 v156, 0.5, v156
	v_rcp_f32_e32 v180, v156
	v_cvt_f32_ubyte3_e32 v156, v172
	v_add_f32_e32 v156, 0.5, v156
	v_rcp_f32_e32 v179, v156
	v_cvt_f32_ubyte3_e32 v156, v173
	v_add_f32_e32 v156, 0.5, v156
	v_cvt_f32_ubyte1_e32 v173, v170
	v_cvt_f32_ubyte0_e32 v172, v170
	v_cvt_f32_ubyte3_e32 v183, v170
	v_cvt_f32_ubyte2_e32 v182, v170
	v_rcp_f32_e32 v181, v156
	v_pk_add_f32 v[182:183], v[182:183], 0.5 op_sel_hi:[1,0]
	v_pk_add_f32 v[172:173], v[172:173], 0.5 op_sel_hi:[1,0]
	v_cvt_f32_ubyte0_e32 v156, v146
	v_pk_mul_f32 v[172:173], v[172:173], v[174:175]
	v_pk_mul_f32 v[174:175], v[182:183], v[178:179]
	v_pk_mul_f32 v[88:89], v[88:89], v[172:173]
	v_pk_mul_f32 v[90:91], v[90:91], v[174:175]
	v_cvt_f32_ubyte3_e32 v175, v171
	v_cvt_f32_ubyte2_e32 v174, v171
	v_cvt_f32_ubyte1_e32 v173, v171
	v_cvt_f32_ubyte0_e32 v172, v171
	v_pk_add_f32 v[170:171], v[174:175], 0.5 op_sel_hi:[1,0]
	v_add_f32_e32 v156, 0.5, v156
	v_pk_mul_f32 v[170:171], v[170:171], v[180:181]
	v_pk_add_f32 v[172:173], v[172:173], 0.5 op_sel_hi:[1,0]
	v_pk_mul_f32 v[94:95], v[94:95], v[170:171]
	v_rcp_f32_e32 v170, v156
	v_cvt_f32_ubyte0_e32 v156, v147
	v_pk_mul_f32 v[172:173], v[172:173], v[176:177]
	v_add_f32_e32 v156, 0.5, v156
	v_pk_mul_f32 v[92:93], v[92:93], v[172:173]
	v_rcp_f32_e32 v172, v156
	v_cvt_f32_ubyte1_e32 v156, v146
	v_add_f32_e32 v156, 0.5, v156
	v_rcp_f32_e32 v171, v156
	v_cvt_f32_ubyte1_e32 v156, v147
	v_add_f32_e32 v156, 0.5, v156
	v_rcp_f32_e32 v173, v156
	v_cvt_f32_ubyte2_e32 v156, v146
	v_cvt_f32_ubyte3_e32 v146, v146
	v_add_f32_e32 v156, 0.5, v156
	v_add_f32_e32 v146, 0.5, v146
	v_rcp_f32_e32 v174, v156
	v_rcp_f32_e32 v175, v146
	v_cvt_f32_ubyte3_e32 v146, v147
	v_cvt_f32_ubyte2_e32 v156, v147
	v_add_f32_e32 v146, 0.5, v146
	v_add_f32_e32 v156, 0.5, v156
	v_rcp_f32_e32 v177, v146
	v_cvt_f32_ubyte1_e32 v147, v144
	v_cvt_f32_ubyte0_e32 v146, v144
	v_cvt_f32_ubyte3_e32 v179, v144
	v_cvt_f32_ubyte2_e32 v178, v144
	v_rcp_f32_e32 v176, v156
	v_pk_add_f32 v[178:179], v[178:179], 0.5 op_sel_hi:[1,0]
	v_pk_add_f32 v[146:147], v[146:147], 0.5 op_sel_hi:[1,0]
	v_cvt_f32_ubyte2_e32 v156, v14
	v_pk_mul_f32 v[146:147], v[146:147], v[170:171]
	v_pk_mul_f32 v[170:171], v[178:179], v[174:175]
	v_pk_mul_f32 v[120:121], v[120:121], v[146:147]
	v_pk_mul_f32 v[122:123], v[122:123], v[170:171]
	v_cvt_f32_ubyte3_e32 v171, v145
	v_cvt_f32_ubyte2_e32 v170, v145
	v_cvt_f32_ubyte1_e32 v147, v145
	v_cvt_f32_ubyte0_e32 v146, v145
	v_pk_add_f32 v[144:145], v[170:171], 0.5 op_sel_hi:[1,0]
	v_pk_add_f32 v[146:147], v[146:147], 0.5 op_sel_hi:[1,0]
	v_pk_mul_f32 v[144:145], v[144:145], v[176:177]
	v_pk_mul_f32 v[146:147], v[146:147], v[172:173]
	v_pk_mul_f32 v[126:127], v[126:127], v[144:145]
	v_cvt_f32_ubyte0_e32 v145, v15
	v_add_f32_e32 v145, 0.5, v145
	v_pk_mul_f32 v[124:125], v[124:125], v[146:147]
	v_cvt_f32_ubyte0_e32 v144, v14
	v_rcp_f32_e32 v146, v145
	v_cvt_f32_ubyte1_e32 v145, v14
	v_cvt_f32_ubyte3_e32 v14, v14
	v_add_f32_e32 v144, 0.5, v144
	v_add_f32_e32 v145, 0.5, v145
	v_add_f32_e32 v156, 0.5, v156
	v_add_f32_e32 v14, 0.5, v14
	v_rcp_f32_e32 v144, v144
	v_rcp_f32_e32 v145, v145
	v_rcp_f32_e32 v170, v156
	v_rcp_f32_e32 v171, v14
	v_cvt_f32_ubyte3_e32 v14, v15
	v_cvt_f32_ubyte2_e32 v156, v15
	v_add_f32_e32 v14, 0.5, v14
	v_cvt_f32_ubyte1_e32 v147, v15
	v_add_f32_e32 v156, 0.5, v156
	v_rcp_f32_e32 v173, v14
	v_cvt_f32_ubyte1_e32 v15, v12
	v_cvt_f32_ubyte0_e32 v14, v12
	v_cvt_f32_ubyte3_e32 v175, v12
	v_cvt_f32_ubyte2_e32 v174, v12
	v_rcp_f32_e32 v172, v156
	v_pk_add_f32 v[174:175], v[174:175], 0.5 op_sel_hi:[1,0]
	v_pk_add_f32 v[14:15], v[14:15], 0.5 op_sel_hi:[1,0]
	v_add_f32_e32 v147, 0.5, v147
	v_pk_mul_f32 v[14:15], v[14:15], v[144:145]
	v_pk_mul_f32 v[144:145], v[174:175], v[170:171]
	v_rcp_f32_e32 v147, v147
	v_pk_mul_f32 v[98:99], v[98:99], v[144:145]
	v_cvt_f32_ubyte3_e32 v145, v13
	v_cvt_f32_ubyte2_e32 v144, v13
	v_pk_mul_f32 v[96:97], v[96:97], v[14:15]
	v_cvt_f32_ubyte1_e32 v15, v13
	v_cvt_f32_ubyte0_e32 v14, v13
	v_pk_add_f32 v[12:13], v[144:145], 0.5 op_sel_hi:[1,0]
	v_pk_add_f32 v[14:15], v[14:15], 0.5 op_sel_hi:[1,0]
	v_pk_mul_f32 v[12:13], v[12:13], v[172:173]
	v_pk_mul_f32 v[14:15], v[14:15], v[146:147]
	v_pk_mul_f32 v[102:103], v[102:103], v[12:13]
	v_cvt_f32_ubyte0_e32 v13, v11
	v_add_f32_e32 v13, 0.5, v13
	v_pk_mul_f32 v[100:101], v[100:101], v[14:15]
	v_cvt_f32_ubyte0_e32 v12, v10
	v_rcp_f32_e32 v14, v13
	v_cvt_f32_ubyte1_e32 v13, v10
	v_cvt_f32_ubyte2_e32 v144, v10
	v_cvt_f32_ubyte2_e32 v145, v11
	v_cvt_f32_ubyte3_e32 v10, v10
	v_add_f32_e32 v12, 0.5, v12
	v_add_f32_e32 v13, 0.5, v13
	v_add_f32_e32 v144, 0.5, v144
	v_add_f32_e32 v145, 0.5, v145
	v_add_f32_e32 v10, 0.5, v10
	v_rcp_f32_e32 v12, v12
	v_rcp_f32_e32 v13, v13
	v_rcp_f32_e32 v144, v144
	v_rcp_f32_e32 v146, v145
	v_rcp_f32_e32 v145, v10
	v_cvt_f32_ubyte3_e32 v10, v11
	v_add_f32_e32 v10, 0.5, v10
	v_cvt_f32_ubyte1_e32 v15, v11
	v_rcp_f32_e32 v147, v10
	v_cvt_f32_ubyte1_e32 v11, v8
	v_cvt_f32_ubyte0_e32 v10, v8
	v_cvt_f32_ubyte3_e32 v171, v8
	v_cvt_f32_ubyte2_e32 v170, v8
	v_pk_add_f32 v[170:171], v[170:171], 0.5 op_sel_hi:[1,0]
	v_pk_add_f32 v[10:11], v[10:11], 0.5 op_sel_hi:[1,0]
	v_add_f32_e32 v15, 0.5, v15
	v_pk_mul_f32 v[10:11], v[10:11], v[12:13]
	v_pk_mul_f32 v[12:13], v[170:171], v[144:145]
	v_rcp_f32_e32 v15, v15
	v_pk_mul_f32 v[130:131], v[130:131], v[12:13]
	v_cvt_f32_ubyte3_e32 v13, v9
	v_cvt_f32_ubyte2_e32 v12, v9
	v_pk_mul_f32 v[128:129], v[128:129], v[10:11]
	v_cvt_f32_ubyte1_e32 v11, v9
	v_cvt_f32_ubyte0_e32 v10, v9
	v_pk_add_f32 v[8:9], v[12:13], 0.5 op_sel_hi:[1,0]
	v_pk_add_f32 v[10:11], v[10:11], 0.5 op_sel_hi:[1,0]
	v_pk_mul_f32 v[8:9], v[8:9], v[146:147]
	v_pk_mul_f32 v[10:11], v[10:11], v[14:15]
	v_pk_mul_f32 v[134:135], v[134:135], v[8:9]
	v_cvt_f32_ubyte0_e32 v9, v5
	v_add_f32_e32 v9, 0.5, v9
	v_pk_mul_f32 v[132:133], v[132:133], v[10:11]
	v_cvt_f32_ubyte0_e32 v8, v4
	v_rcp_f32_e32 v10, v9
	v_cvt_f32_ubyte1_e32 v9, v4
	v_cvt_f32_ubyte2_e32 v12, v4
	v_cvt_f32_ubyte2_e32 v13, v5
	v_cvt_f32_ubyte3_e32 v4, v4
	v_add_f32_e32 v8, 0.5, v8
	v_add_f32_e32 v9, 0.5, v9
	v_add_f32_e32 v12, 0.5, v12
	v_add_f32_e32 v13, 0.5, v13
	v_add_f32_e32 v4, 0.5, v4
	v_rcp_f32_e32 v8, v8
	v_rcp_f32_e32 v9, v9
	v_rcp_f32_e32 v12, v12
	v_rcp_f32_e32 v14, v13
	v_rcp_f32_e32 v13, v4
	v_cvt_f32_ubyte3_e32 v4, v5
	v_add_f32_e32 v4, 0.5, v4
	v_cvt_f32_ubyte1_e32 v11, v5
	v_rcp_f32_e32 v15, v4
	v_cvt_f32_ubyte1_e32 v5, v2
	v_cvt_f32_ubyte0_e32 v4, v2
	v_cvt_f32_ubyte3_e32 v145, v2
	v_cvt_f32_ubyte2_e32 v144, v2
	v_pk_add_f32 v[144:145], v[144:145], 0.5 op_sel_hi:[1,0]
	v_pk_add_f32 v[4:5], v[4:5], 0.5 op_sel_hi:[1,0]
	v_add_f32_e32 v11, 0.5, v11
	v_pk_mul_f32 v[4:5], v[4:5], v[8:9]
	v_pk_mul_f32 v[8:9], v[144:145], v[12:13]
	v_rcp_f32_e32 v11, v11
	v_pk_mul_f32 v[106:107], v[106:107], v[8:9]
	v_cvt_f32_ubyte3_e32 v9, v3
	v_cvt_f32_ubyte2_e32 v8, v3
	v_pk_mul_f32 v[104:105], v[104:105], v[4:5]
	v_cvt_f32_ubyte1_e32 v5, v3
	v_cvt_f32_ubyte0_e32 v4, v3
	v_pk_add_f32 v[2:3], v[8:9], 0.5 op_sel_hi:[1,0]
	v_pk_add_f32 v[4:5], v[4:5], 0.5 op_sel_hi:[1,0]
	v_pk_mul_f32 v[2:3], v[2:3], v[14:15]
	v_pk_mul_f32 v[4:5], v[4:5], v[10:11]
	v_pk_mul_f32 v[110:111], v[110:111], v[2:3]
	v_cvt_f32_ubyte0_e32 v3, v7
	v_add_f32_e32 v3, 0.5, v3
	v_pk_mul_f32 v[108:109], v[108:109], v[4:5]
	v_cvt_f32_ubyte0_e32 v2, v6
	v_rcp_f32_e32 v4, v3
	v_cvt_f32_ubyte1_e32 v3, v6
	v_cvt_f32_ubyte2_e32 v8, v6
	v_cvt_f32_ubyte2_e32 v9, v7
	v_cvt_f32_ubyte3_e32 v6, v6
	v_add_f32_e32 v2, 0.5, v2
	v_add_f32_e32 v3, 0.5, v3
	v_add_f32_e32 v8, 0.5, v8
	v_add_f32_e32 v9, 0.5, v9
	v_add_f32_e32 v6, 0.5, v6
	v_rcp_f32_e32 v2, v2
	v_rcp_f32_e32 v3, v3
	v_rcp_f32_e32 v8, v8
	v_rcp_f32_e32 v10, v9
	v_rcp_f32_e32 v9, v6
	v_cvt_f32_ubyte3_e32 v6, v7
	v_cvt_f32_ubyte1_e32 v5, v7
	v_add_f32_e32 v6, 0.5, v6
	v_add_f32_e32 v5, 0.5, v5
	v_rcp_f32_e32 v11, v6
	v_cvt_f32_ubyte1_e32 v7, v0
	v_cvt_f32_ubyte0_e32 v6, v0
	v_cvt_f32_ubyte3_e32 v13, v0
	v_cvt_f32_ubyte2_e32 v12, v0
	v_rcp_f32_e32 v5, v5
	v_pk_add_f32 v[12:13], v[12:13], 0.5 op_sel_hi:[1,0]
	v_pk_add_f32 v[6:7], v[6:7], 0.5 op_sel_hi:[1,0]
	s_nop 0
	v_pk_mul_f32 v[2:3], v[6:7], v[2:3]
	v_pk_mul_f32 v[6:7], v[12:13], v[8:9]
	v_pk_mul_f32 v[136:137], v[136:137], v[2:3]
	v_pk_mul_f32 v[138:139], v[138:139], v[6:7]
	v_cvt_f32_ubyte1_e32 v3, v1
	v_cvt_f32_ubyte0_e32 v2, v1
	v_cvt_f32_ubyte3_e32 v7, v1
	v_cvt_f32_ubyte2_e32 v6, v1
	v_pk_add_f32 v[0:1], v[6:7], 0.5 op_sel_hi:[1,0]
	v_pk_add_f32 v[2:3], v[2:3], 0.5 op_sel_hi:[1,0]
	v_pk_mul_f32 v[0:1], v[0:1], v[10:11]
	v_pk_mul_f32 v[2:3], v[2:3], v[4:5]
	v_pk_mul_f32 v[142:143], v[142:143], v[0:1]
	v_pk_mul_f32 v[140:141], v[140:141], v[2:3]
	ds_read_b128 v[8:11], v230
	ds_read_b128 v[12:15], v230 offset:1024
	ds_read_b128 v[0:3], v230 offset:2048
	ds_read_b128 v[4:7], v230 offset:3072
	s_add_u32 s2, s46, 0x40480
	s_addc_u32 s3, s47, 0
	s_mov_b32 m0, s92
	v_lshl_add_u64 v[144:145], s[2:3], 0, v[148:149]
	ds_read_b128 v[174:177], v227
	ds_read_b128 v[178:181], v227 offset:1024
	ds_read_b128 v[182:185], v227 offset:2048
	ds_read_b128 v[186:189], v227 offset:3072
	ds_read_b128 v[190:193], v227 offset:4096
	ds_read_b128 v[194:197], v227 offset:5120
	ds_read_b128 v[198:201], v227 offset:6144
	ds_read_b128 v[202:205], v227 offset:7168
	global_load_lds_dwordx4 v[144:145], off
	v_lshl_add_u64 v[144:145], s[2:3], 0, v[152:153]
	s_mov_b32 m0, s91
	s_nop 0
	global_load_lds_dwordx4 v[144:145], off
	s_waitcnt lgkmcnt(8)
	s_barrier
	s_waitcnt lgkmcnt(0)
	s_setprio 1
	s_waitcnt lgkmcnt(0)
	v_mfma_f32_16x16x128_f8f6f4 v[16:19], v[8:15], v[174:181], v[16:19]
	v_mfma_f32_16x16x128_f8f6f4 v[20:23], v[0:7], v[174:181], v[20:23]
	v_mfma_f32_16x16x128_f8f6f4 v[24:27], v[8:15], v[182:189], v[24:27]
	v_mfma_f32_16x16x128_f8f6f4 v[28:31], v[0:7], v[182:189], v[28:31]
	v_mfma_f32_16x16x128_f8f6f4 v[32:35], v[8:15], v[190:197], v[32:35]
	v_mfma_f32_16x16x128_f8f6f4 v[36:39], v[0:7], v[190:197], v[36:39]
	v_mfma_f32_16x16x128_f8f6f4 v[40:43], v[8:15], v[198:205], v[40:43]
	v_mfma_f32_16x16x128_f8f6f4 v[44:47], v[0:7], v[198:205], v[44:47]
	s_setprio 0
	s_barrier
	v_lshl_add_u64 v[170:171], s[48:49], 0, v[150:151]
	s_mov_b32 m0, s94
	v_lshl_add_u64 v[144:145], v[170:171], 0, s[20:21]
	v_lshl_add_u64 v[172:173], s[48:49], 0, v[154:155]
	ds_read_b128 v[206:209], v231
	ds_read_b128 v[210:213], v231 offset:1024
	ds_read_b128 v[214:217], v231 offset:2048
	ds_read_b128 v[218:221], v231 offset:3072
	global_load_lds_dwordx4 v[144:145], off
	v_lshl_add_u64 v[144:145], v[172:173], 0, s[20:21]
	s_mov_b32 m0, s93
	s_nop 0
	global_load_lds_dwordx4 v[144:145], off
	s_barrier
	s_waitcnt lgkmcnt(0)
	s_setprio 1
	s_waitcnt lgkmcnt(0)
	v_mfma_f32_16x16x128_f8f6f4 v[48:51], v[206:213], v[174:181], v[48:51]
	v_mfma_f32_16x16x128_f8f6f4 v[52:55], v[214:221], v[174:181], v[52:55]
	v_mfma_f32_16x16x128_f8f6f4 v[56:59], v[206:213], v[182:189], v[56:59]
	v_mfma_f32_16x16x128_f8f6f4 v[60:63], v[214:221], v[182:189], v[60:63]
	v_mfma_f32_16x16x128_f8f6f4 v[64:67], v[206:213], v[190:197], v[64:67]
	v_mfma_f32_16x16x128_f8f6f4 v[68:71], v[214:221], v[190:197], v[68:71]
	v_mfma_f32_16x16x128_f8f6f4 v[72:75], v[206:213], v[198:205], v[72:75]
	v_mfma_f32_16x16x128_f8f6f4 v[76:79], v[214:221], v[198:205], v[76:79]
	s_setprio 0
	v_lshl_add_u64 v[174:175], s[46:47], 0, v[148:149]
	s_mov_b32 m0, s70
	v_lshl_add_u64 v[144:145], v[174:175], 0, s[20:21]
	s_barrier
	ds_read_b128 v[176:179], v227 offset:16384
	ds_read_b128 v[180:183], v227 offset:17408
	ds_read_b128 v[184:187], v227 offset:18432
	ds_read_b128 v[188:191], v227 offset:19456
	ds_read_b128 v[192:195], v227 offset:20480
	ds_read_b128 v[196:199], v227 offset:21504
	ds_read_b128 v[236:239], v227 offset:22528
	ds_read_b128 v[240:243], v227 offset:23552
	global_load_lds_dwordx4 v[144:145], off
	v_lshl_add_u64 v[144:145], v[168:169], 0, s[20:21]
	s_mov_b32 m0, s71
	s_nop 0
	global_load_lds_dwordx4 v[144:145], off
	s_barrier
	s_waitcnt lgkmcnt(0)
	s_setprio 1
	s_waitcnt lgkmcnt(0)
	v_mfma_f32_16x16x128_f8f6f4 v[80:83], v[8:15], v[176:183], v[80:83]
	v_mfma_f32_16x16x128_f8f6f4 v[84:87], v[0:7], v[176:183], v[84:87]
	v_mfma_f32_16x16x128_f8f6f4 v[88:91], v[8:15], v[184:191], v[88:91]
	v_mfma_f32_16x16x128_f8f6f4 v[92:95], v[0:7], v[184:191], v[92:95]
	v_mfma_f32_16x16x128_f8f6f4 v[96:99], v[8:15], v[192:199], v[96:99]
	v_mfma_f32_16x16x128_f8f6f4 v[100:103], v[0:7], v[192:199], v[100:103]
	v_mfma_f32_16x16x128_f8f6f4 v[104:107], v[8:15], v[236:243], v[104:107]
	v_mfma_f32_16x16x128_f8f6f4 v[108:111], v[0:7], v[236:243], v[108:111]
	s_setprio 0
	s_barrier
	s_add_u32 s2, s48, 0x40500
	s_addc_u32 s3, s49, 0
	s_mov_b32 m0, s52
	v_lshl_add_u64 v[0:1], s[2:3], 0, v[150:151]
	global_load_lds_dwordx4 v[0:1], off
	v_lshl_add_u64 v[0:1], s[2:3], 0, v[154:155]
	s_mov_b32 m0, s95
	s_nop 0
	global_load_lds_dwordx4 v[0:1], off
	s_waitcnt vmcnt(6)
	s_barrier
	s_setprio 1
	v_mfma_f32_16x16x128_f8f6f4 v[112:115], v[206:213], v[176:183], v[112:115]
	v_mfma_f32_16x16x128_f8f6f4 v[116:119], v[214:221], v[176:183], v[116:119]
	v_mfma_f32_16x16x128_f8f6f4 v[120:123], v[206:213], v[184:191], v[120:123]
	v_mfma_f32_16x16x128_f8f6f4 v[124:127], v[214:221], v[184:191], v[124:127]
	v_mfma_f32_16x16x128_f8f6f4 v[128:131], v[206:213], v[192:199], v[128:131]
	v_mfma_f32_16x16x128_f8f6f4 v[132:135], v[214:221], v[192:199], v[132:135]
	v_mfma_f32_16x16x128_f8f6f4 v[136:139], v[206:213], v[236:243], v[136:139]
	v_mfma_f32_16x16x128_f8f6f4 v[140:143], v[214:221], v[236:243], v[140:143]
	s_setprio 0
	s_barrier
	ds_read_b128 v[0:3], v234
	ds_read_b128 v[4:7], v234 offset:1024
	ds_read_b128 v[8:11], v234 offset:2048
	ds_read_b128 v[12:15], v234 offset:3072
	s_add_u32 s2, s46, 0x40500
	s_addc_u32 s3, s47, 0
	s_mov_b32 m0, s72
	v_lshl_add_u64 v[144:145], s[2:3], 0, v[148:149]
	ds_read_b128 v[176:179], v227 offset:32768
	ds_read_b128 v[180:183], v227 offset:33792
	ds_read_b128 v[184:187], v227 offset:34816
	ds_read_b128 v[188:191], v227 offset:35840
	ds_read_b128 v[192:195], v227 offset:36864
	ds_read_b128 v[196:199], v227 offset:37888
	ds_read_b128 v[200:203], v227 offset:38912
	ds_read_b128 v[204:207], v227 offset:39936
	global_load_lds_dwordx4 v[144:145], off
	v_lshl_add_u64 v[144:145], s[2:3], 0, v[152:153]
	s_mov_b32 m0, s73
	s_nop 0
	global_load_lds_dwordx4 v[144:145], off
	s_waitcnt lgkmcnt(8)
	s_barrier
	s_waitcnt lgkmcnt(0)
	s_setprio 1
	s_waitcnt lgkmcnt(0)
	v_mfma_f32_16x16x128_f8f6f4 v[16:19], v[0:7], v[176:183], v[16:19]
	v_mfma_f32_16x16x128_f8f6f4 v[20:23], v[8:15], v[176:183], v[20:23]
	v_mfma_f32_16x16x128_f8f6f4 v[24:27], v[0:7], v[184:191], v[24:27]
	v_mfma_f32_16x16x128_f8f6f4 v[28:31], v[8:15], v[184:191], v[28:31]
	v_mfma_f32_16x16x128_f8f6f4 v[32:35], v[0:7], v[192:199], v[32:35]
	v_mfma_f32_16x16x128_f8f6f4 v[36:39], v[8:15], v[192:199], v[36:39]
	v_mfma_f32_16x16x128_f8f6f4 v[40:43], v[0:7], v[200:207], v[40:43]
	v_mfma_f32_16x16x128_f8f6f4 v[44:47], v[8:15], v[200:207], v[44:47]
	s_setprio 0
	s_barrier
	s_mov_b32 m0, s63
	v_lshl_add_u64 v[144:145], v[170:171], 0, s[22:23]
	ds_read_b128 v[208:211], v233
	ds_read_b128 v[212:215], v233 offset:1024
	ds_read_b128 v[236:239], v233 offset:2048
	ds_read_b128 v[240:243], v233 offset:3072
	global_load_lds_dwordx4 v[144:145], off
	v_lshl_add_u64 v[144:145], v[172:173], 0, s[22:23]
	s_mov_b32 m0, s62
	s_nop 0
	global_load_lds_dwordx4 v[144:145], off
	s_barrier
	s_waitcnt lgkmcnt(0)
	s_setprio 1
	s_waitcnt lgkmcnt(0)
	v_mfma_f32_16x16x128_f8f6f4 v[48:51], v[208:215], v[176:183], v[48:51]
	v_mfma_f32_16x16x128_f8f6f4 v[52:55], v[236:243], v[176:183], v[52:55]
	v_mfma_f32_16x16x128_f8f6f4 v[56:59], v[208:215], v[184:191], v[56:59]
	v_mfma_f32_16x16x128_f8f6f4 v[60:63], v[236:243], v[184:191], v[60:63]
	v_mfma_f32_16x16x128_f8f6f4 v[64:67], v[208:215], v[192:199], v[64:67]
	v_mfma_f32_16x16x128_f8f6f4 v[68:71], v[236:243], v[192:199], v[68:71]
	v_mfma_f32_16x16x128_f8f6f4 v[72:75], v[208:215], v[200:207], v[72:75]
	v_mfma_f32_16x16x128_f8f6f4 v[76:79], v[236:243], v[200:207], v[76:79]
	s_setprio 0
	s_mov_b32 m0, s77
	v_lshl_add_u64 v[144:145], v[174:175], 0, s[22:23]
	s_barrier
	ds_read_b128 v[176:179], v227 offset:49152
	ds_read_b128 v[180:183], v227 offset:50176
	ds_read_b128 v[184:187], v227 offset:51200
	ds_read_b128 v[188:191], v227 offset:52224
	ds_read_b128 v[192:195], v227 offset:53248
	ds_read_b128 v[196:199], v227 offset:54272
	ds_read_b128 v[200:203], v227 offset:55296
	ds_read_b128 v[204:207], v227 offset:56320
	global_load_lds_dwordx4 v[144:145], off
	v_lshl_add_u64 v[144:145], v[168:169], 0, s[22:23]
	s_mov_b32 m0, s78
	s_nop 0
	global_load_lds_dwordx4 v[144:145], off
	s_barrier
	s_waitcnt lgkmcnt(0)
	s_setprio 1
	s_waitcnt lgkmcnt(0)
	v_mfma_f32_16x16x128_f8f6f4 v[80:83], v[0:7], v[176:183], v[80:83]
	v_mfma_f32_16x16x128_f8f6f4 v[84:87], v[8:15], v[176:183], v[84:87]
	v_mfma_f32_16x16x128_f8f6f4 v[88:91], v[0:7], v[184:191], v[88:91]
	v_mfma_f32_16x16x128_f8f6f4 v[92:95], v[8:15], v[184:191], v[92:95]
	v_mfma_f32_16x16x128_f8f6f4 v[96:99], v[0:7], v[192:199], v[96:99]
	v_mfma_f32_16x16x128_f8f6f4 v[100:103], v[8:15], v[192:199], v[100:103]
	v_mfma_f32_16x16x128_f8f6f4 v[104:107], v[0:7], v[200:207], v[104:107]
	v_mfma_f32_16x16x128_f8f6f4 v[108:111], v[8:15], v[200:207], v[108:111]
	s_setprio 0
	s_barrier
	s_add_u32 s2, s48, 0x40580
	s_addc_u32 s3, s49, 0
	s_mov_b32 m0, s64
	v_lshl_add_u64 v[0:1], s[2:3], 0, v[150:151]
	global_load_lds_dwordx4 v[0:1], off
	v_lshl_add_u64 v[0:1], s[2:3], 0, v[154:155]
	s_mov_b32 m0, s53
	s_nop 0
	global_load_lds_dwordx4 v[0:1], off
	s_waitcnt vmcnt(6)
	s_barrier
	s_setprio 1
	v_mfma_f32_16x16x128_f8f6f4 v[112:115], v[208:215], v[176:183], v[112:115]
	v_mfma_f32_16x16x128_f8f6f4 v[116:119], v[236:243], v[176:183], v[116:119]
	v_mfma_f32_16x16x128_f8f6f4 v[120:123], v[208:215], v[184:191], v[120:123]
	v_mfma_f32_16x16x128_f8f6f4 v[124:127], v[236:243], v[184:191], v[124:127]
	v_mfma_f32_16x16x128_f8f6f4 v[128:131], v[208:215], v[192:199], v[128:131]
	v_mfma_f32_16x16x128_f8f6f4 v[132:135], v[236:243], v[192:199], v[132:135]
	v_mfma_f32_16x16x128_f8f6f4 v[136:139], v[208:215], v[200:207], v[136:139]
	v_mfma_f32_16x16x128_f8f6f4 v[140:143], v[236:243], v[200:207], v[140:143]
	s_setprio 0
	s_barrier
	ds_read_b128 v[0:3], v230
	ds_read_b128 v[4:7], v230 offset:1024
	ds_read_b128 v[8:11], v230 offset:2048
	ds_read_b128 v[12:15], v230 offset:3072
	s_add_u32 s2, s46, 0x40580
	s_addc_u32 s3, s47, 0
	s_mov_b32 m0, s92
	v_lshl_add_u64 v[144:145], s[2:3], 0, v[148:149]
	ds_read_b128 v[176:179], v227
	ds_read_b128 v[180:183], v227 offset:1024
	ds_read_b128 v[184:187], v227 offset:2048
	ds_read_b128 v[188:191], v227 offset:3072
	ds_read_b128 v[192:195], v227 offset:4096
	ds_read_b128 v[196:199], v227 offset:5120
	ds_read_b128 v[200:203], v227 offset:6144
	ds_read_b128 v[204:207], v227 offset:7168
	global_load_lds_dwordx4 v[144:145], off
	v_lshl_add_u64 v[144:145], s[2:3], 0, v[152:153]
	s_mov_b32 m0, s91
	s_nop 0
	global_load_lds_dwordx4 v[144:145], off
	s_waitcnt lgkmcnt(8)
	s_barrier
	s_waitcnt lgkmcnt(0)
	s_setprio 1
	s_waitcnt lgkmcnt(0)
	v_mfma_f32_16x16x128_f8f6f4 v[16:19], v[0:7], v[176:183], v[16:19]
	v_mfma_f32_16x16x128_f8f6f4 v[20:23], v[8:15], v[176:183], v[20:23]
	v_mfma_f32_16x16x128_f8f6f4 v[24:27], v[0:7], v[184:191], v[24:27]
	v_mfma_f32_16x16x128_f8f6f4 v[28:31], v[8:15], v[184:191], v[28:31]
	v_mfma_f32_16x16x128_f8f6f4 v[32:35], v[0:7], v[192:199], v[32:35]
	v_mfma_f32_16x16x128_f8f6f4 v[36:39], v[8:15], v[192:199], v[36:39]
	v_mfma_f32_16x16x128_f8f6f4 v[40:43], v[0:7], v[200:207], v[40:43]
	v_mfma_f32_16x16x128_f8f6f4 v[44:47], v[8:15], v[200:207], v[44:47]
	s_setprio 0
	s_barrier
	s_mov_b32 m0, s94
	v_lshl_add_u64 v[144:145], v[170:171], 0, s[24:25]
	ds_read_b128 v[208:211], v231
	ds_read_b128 v[212:215], v231 offset:1024
	ds_read_b128 v[236:239], v231 offset:2048
	ds_read_b128 v[240:243], v231 offset:3072
	global_load_lds_dwordx4 v[144:145], off
	v_lshl_add_u64 v[144:145], v[172:173], 0, s[24:25]
	s_mov_b32 m0, s93
	s_nop 0
	global_load_lds_dwordx4 v[144:145], off
	s_barrier
	s_waitcnt lgkmcnt(0)
	s_setprio 1
	s_waitcnt lgkmcnt(0)
	v_mfma_f32_16x16x128_f8f6f4 v[48:51], v[208:215], v[176:183], v[48:51]
	v_mfma_f32_16x16x128_f8f6f4 v[52:55], v[236:243], v[176:183], v[52:55]
	v_mfma_f32_16x16x128_f8f6f4 v[56:59], v[208:215], v[184:191], v[56:59]
	v_mfma_f32_16x16x128_f8f6f4 v[60:63], v[236:243], v[184:191], v[60:63]
	v_mfma_f32_16x16x128_f8f6f4 v[64:67], v[208:215], v[192:199], v[64:67]
	v_mfma_f32_16x16x128_f8f6f4 v[68:71], v[236:243], v[192:199], v[68:71]
	v_mfma_f32_16x16x128_f8f6f4 v[72:75], v[208:215], v[200:207], v[72:75]
	v_mfma_f32_16x16x128_f8f6f4 v[76:79], v[236:243], v[200:207], v[76:79]
	s_setprio 0
	s_mov_b32 m0, s70
	v_lshl_add_u64 v[144:145], v[174:175], 0, s[24:25]
	s_barrier
	ds_read_b128 v[176:179], v227 offset:16384
	ds_read_b128 v[180:183], v227 offset:17408
	ds_read_b128 v[184:187], v227 offset:18432
	ds_read_b128 v[188:191], v227 offset:19456
	ds_read_b128 v[192:195], v227 offset:20480
	ds_read_b128 v[196:199], v227 offset:21504
	ds_read_b128 v[200:203], v227 offset:22528
	ds_read_b128 v[204:207], v227 offset:23552
	global_load_lds_dwordx4 v[144:145], off
	v_lshl_add_u64 v[144:145], v[168:169], 0, s[24:25]
	s_mov_b32 m0, s71
	s_nop 0
	global_load_lds_dwordx4 v[144:145], off
	s_barrier
	s_waitcnt lgkmcnt(0)
	s_setprio 1
	s_waitcnt lgkmcnt(0)
	v_mfma_f32_16x16x128_f8f6f4 v[80:83], v[0:7], v[176:183], v[80:83]
	v_mfma_f32_16x16x128_f8f6f4 v[84:87], v[8:15], v[176:183], v[84:87]
	v_mfma_f32_16x16x128_f8f6f4 v[88:91], v[0:7], v[184:191], v[88:91]
	v_mfma_f32_16x16x128_f8f6f4 v[92:95], v[8:15], v[184:191], v[92:95]
	v_mfma_f32_16x16x128_f8f6f4 v[96:99], v[0:7], v[192:199], v[96:99]
	v_mfma_f32_16x16x128_f8f6f4 v[100:103], v[8:15], v[192:199], v[100:103]
	v_mfma_f32_16x16x128_f8f6f4 v[104:107], v[0:7], v[200:207], v[104:107]
	v_mfma_f32_16x16x128_f8f6f4 v[108:111], v[8:15], v[200:207], v[108:111]
	s_setprio 0
	s_barrier
	s_add_u32 s2, s48, 0x40600
	s_addc_u32 s3, s49, 0
	s_mov_b32 m0, s52
	v_lshl_add_u64 v[0:1], s[2:3], 0, v[150:151]
	global_load_lds_dwordx4 v[0:1], off
	v_lshl_add_u64 v[0:1], s[2:3], 0, v[154:155]
	s_mov_b32 m0, s95
	s_nop 0
	global_load_lds_dwordx4 v[0:1], off
	s_waitcnt vmcnt(6)
	s_barrier
	s_setprio 1
	v_mfma_f32_16x16x128_f8f6f4 v[112:115], v[208:215], v[176:183], v[112:115]
	v_mfma_f32_16x16x128_f8f6f4 v[116:119], v[236:243], v[176:183], v[116:119]
	v_mfma_f32_16x16x128_f8f6f4 v[120:123], v[208:215], v[184:191], v[120:123]
	v_mfma_f32_16x16x128_f8f6f4 v[124:127], v[236:243], v[184:191], v[124:127]
	v_mfma_f32_16x16x128_f8f6f4 v[128:131], v[208:215], v[192:199], v[128:131]
	v_mfma_f32_16x16x128_f8f6f4 v[132:135], v[236:243], v[192:199], v[132:135]
	v_mfma_f32_16x16x128_f8f6f4 v[136:139], v[208:215], v[200:207], v[136:139]
	v_mfma_f32_16x16x128_f8f6f4 v[140:143], v[236:243], v[200:207], v[140:143]
	s_setprio 0
	s_barrier
	ds_read_b128 v[0:3], v234
	ds_read_b128 v[4:7], v234 offset:1024
	ds_read_b128 v[8:11], v234 offset:2048
	ds_read_b128 v[12:15], v234 offset:3072
	s_add_u32 s2, s46, 0x40600
	s_addc_u32 s3, s47, 0
	s_mov_b32 m0, s72
	v_lshl_add_u64 v[144:145], s[2:3], 0, v[148:149]
	ds_read_b128 v[176:179], v227 offset:32768
	ds_read_b128 v[180:183], v227 offset:33792
	ds_read_b128 v[184:187], v227 offset:34816
	ds_read_b128 v[188:191], v227 offset:35840
	ds_read_b128 v[192:195], v227 offset:36864
	ds_read_b128 v[196:199], v227 offset:37888
	ds_read_b128 v[200:203], v227 offset:38912
	ds_read_b128 v[204:207], v227 offset:39936
	global_load_lds_dwordx4 v[144:145], off
	v_lshl_add_u64 v[144:145], s[2:3], 0, v[152:153]
	s_mov_b32 m0, s73
	s_nop 0
	global_load_lds_dwordx4 v[144:145], off
	s_waitcnt lgkmcnt(8)
	s_barrier
	s_waitcnt lgkmcnt(0)
	s_setprio 1
	s_waitcnt lgkmcnt(0)
	v_mfma_f32_16x16x128_f8f6f4 v[16:19], v[0:7], v[176:183], v[16:19]
	v_mfma_f32_16x16x128_f8f6f4 v[20:23], v[8:15], v[176:183], v[20:23]
	v_mfma_f32_16x16x128_f8f6f4 v[24:27], v[0:7], v[184:191], v[24:27]
	v_mfma_f32_16x16x128_f8f6f4 v[28:31], v[8:15], v[184:191], v[28:31]
	v_mfma_f32_16x16x128_f8f6f4 v[32:35], v[0:7], v[192:199], v[32:35]
	v_mfma_f32_16x16x128_f8f6f4 v[36:39], v[8:15], v[192:199], v[36:39]
	v_mfma_f32_16x16x128_f8f6f4 v[40:43], v[0:7], v[200:207], v[40:43]
	v_mfma_f32_16x16x128_f8f6f4 v[44:47], v[8:15], v[200:207], v[44:47]
	s_setprio 0
	s_barrier
	s_mov_b32 m0, s63
	v_lshl_add_u64 v[144:145], v[170:171], 0, s[26:27]
	ds_read_b128 v[208:211], v233
	ds_read_b128 v[212:215], v233 offset:1024
	ds_read_b128 v[236:239], v233 offset:2048
	ds_read_b128 v[240:243], v233 offset:3072
	global_load_lds_dwordx4 v[144:145], off
	v_lshl_add_u64 v[144:145], v[172:173], 0, s[26:27]
	s_mov_b32 m0, s62
	s_nop 0
	global_load_lds_dwordx4 v[144:145], off
	s_barrier
	s_waitcnt lgkmcnt(0)
	s_setprio 1
	s_waitcnt lgkmcnt(0)
	v_mfma_f32_16x16x128_f8f6f4 v[48:51], v[208:215], v[176:183], v[48:51]
	v_mfma_f32_16x16x128_f8f6f4 v[52:55], v[236:243], v[176:183], v[52:55]
	v_mfma_f32_16x16x128_f8f6f4 v[56:59], v[208:215], v[184:191], v[56:59]
	v_mfma_f32_16x16x128_f8f6f4 v[60:63], v[236:243], v[184:191], v[60:63]
	v_mfma_f32_16x16x128_f8f6f4 v[64:67], v[208:215], v[192:199], v[64:67]
	v_mfma_f32_16x16x128_f8f6f4 v[68:71], v[236:243], v[192:199], v[68:71]
	v_mfma_f32_16x16x128_f8f6f4 v[72:75], v[208:215], v[200:207], v[72:75]
	v_mfma_f32_16x16x128_f8f6f4 v[76:79], v[236:243], v[200:207], v[76:79]
	s_setprio 0
	s_mov_b32 m0, s77
	v_lshl_add_u64 v[144:145], v[174:175], 0, s[26:27]
	s_barrier
	ds_read_b128 v[176:179], v227 offset:49152
	ds_read_b128 v[180:183], v227 offset:50176
	ds_read_b128 v[184:187], v227 offset:51200
	ds_read_b128 v[188:191], v227 offset:52224
	ds_read_b128 v[192:195], v227 offset:53248
	ds_read_b128 v[196:199], v227 offset:54272
	ds_read_b128 v[200:203], v227 offset:55296
	ds_read_b128 v[204:207], v227 offset:56320
	global_load_lds_dwordx4 v[144:145], off
	v_lshl_add_u64 v[144:145], v[168:169], 0, s[26:27]
	s_mov_b32 m0, s78
	s_nop 0
	global_load_lds_dwordx4 v[144:145], off
	s_barrier
	s_waitcnt lgkmcnt(0)
	s_setprio 1
	s_waitcnt lgkmcnt(0)
	v_mfma_f32_16x16x128_f8f6f4 v[80:83], v[0:7], v[176:183], v[80:83]
	v_mfma_f32_16x16x128_f8f6f4 v[84:87], v[8:15], v[176:183], v[84:87]
	v_mfma_f32_16x16x128_f8f6f4 v[88:91], v[0:7], v[184:191], v[88:91]
	v_mfma_f32_16x16x128_f8f6f4 v[92:95], v[8:15], v[184:191], v[92:95]
	v_mfma_f32_16x16x128_f8f6f4 v[96:99], v[0:7], v[192:199], v[96:99]
	v_mfma_f32_16x16x128_f8f6f4 v[100:103], v[8:15], v[192:199], v[100:103]
	v_mfma_f32_16x16x128_f8f6f4 v[104:107], v[0:7], v[200:207], v[104:107]
	v_mfma_f32_16x16x128_f8f6f4 v[108:111], v[8:15], v[200:207], v[108:111]
	s_setprio 0
	s_barrier
	s_add_u32 s2, s48, 0x40680
	s_addc_u32 s3, s49, 0
	s_mov_b32 m0, s64
	v_lshl_add_u64 v[0:1], s[2:3], 0, v[150:151]
	global_load_lds_dwordx4 v[0:1], off
	v_lshl_add_u64 v[0:1], s[2:3], 0, v[154:155]
	s_mov_b32 m0, s53
	s_nop 0
	global_load_lds_dwordx4 v[0:1], off
	s_waitcnt vmcnt(6)
	s_barrier
	s_setprio 1
	v_mfma_f32_16x16x128_f8f6f4 v[112:115], v[208:215], v[176:183], v[112:115]
	v_mfma_f32_16x16x128_f8f6f4 v[116:119], v[236:243], v[176:183], v[116:119]
	v_mfma_f32_16x16x128_f8f6f4 v[120:123], v[208:215], v[184:191], v[120:123]
	v_mfma_f32_16x16x128_f8f6f4 v[124:127], v[236:243], v[184:191], v[124:127]
	v_mfma_f32_16x16x128_f8f6f4 v[128:131], v[208:215], v[192:199], v[128:131]
	v_mfma_f32_16x16x128_f8f6f4 v[132:135], v[236:243], v[192:199], v[132:135]
	v_mfma_f32_16x16x128_f8f6f4 v[136:139], v[208:215], v[200:207], v[136:139]
	v_mfma_f32_16x16x128_f8f6f4 v[140:143], v[236:243], v[200:207], v[140:143]
	s_setprio 0
	s_and_b64 s[2:3], vcc, exec
	s_cselect_b32 s59, s45, s49
	s_cselect_b32 s58, s44, s48
	s_add_i32 s2, s56, 16
	s_ashr_i32 s3, s2, 31
	v_mov_b32_e32 v156, v229
	s_lshl_b64 s[2:3], s[2:3], 16
	s_barrier
	s_nop 7
	s_nop 7
	s_nop 7
	s_add_u32 s2, s75, s2
	s_addc_u32 s3, s76, s3
	global_load_dwordx2 v[216:217], v156, s[54:55]
	global_load_dwordx2 v[236:237], v156, s[2:3]
	global_load_dwordx2 v[212:213], v156, s[54:55] offset:512
	global_load_dwordx2 v[214:215], v156, s[2:3] offset:512
	global_load_dwordx2 v[208:209], v156, s[54:55] offset:1024
	global_load_dwordx2 v[210:211], v156, s[2:3] offset:1024
	global_load_dwordx2 v[204:205], v156, s[54:55] offset:1536
	global_load_dwordx2 v[206:207], v156, s[2:3] offset:1536
	global_load_dwordx2 v[200:201], v156, s[54:55] offset:2048
	global_load_dwordx2 v[202:203], v156, s[2:3] offset:2048
	global_load_dwordx2 v[196:197], v156, s[54:55] offset:2560
	global_load_dwordx2 v[198:199], v156, s[2:3] offset:2560
	global_load_dwordx2 v[192:193], v156, s[54:55] offset:3072
	global_load_dwordx2 v[194:195], v156, s[2:3] offset:3072
	global_load_dwordx2 v[188:189], v156, s[54:55] offset:3584
	global_load_dwordx2 v[190:191], v156, s[2:3] offset:3584
	v_lshl_add_u64 v[0:1], s[54:55], 0, v[156:157]
	v_lshl_add_u64 v[2:3], s[2:3], 0, v[156:157]
	v_add_co_u32_e32 v0, vcc, s82, v0
	s_waitcnt vmcnt(0)
	v_cvt_f32_ubyte3_e32 v243, v216
	v_cvt_f32_ubyte0_e32 v156, v236
	v_add_f32_e32 v156, 0.5, v156
	v_rcp_f32_e32 v238, v156
	v_cvt_f32_ubyte0_e32 v156, v237
	v_add_f32_e32 v156, 0.5, v156
	v_rcp_f32_e32 v218, v156
	v_cvt_f32_ubyte1_e32 v156, v236
	v_add_f32_e32 v156, 0.5, v156
	v_rcp_f32_e32 v239, v156
	v_cvt_f32_ubyte1_e32 v156, v237
	v_add_f32_e32 v156, 0.5, v156
	v_rcp_f32_e32 v219, v156
	v_cvt_f32_ubyte2_e32 v156, v236
	v_add_f32_e32 v156, 0.5, v156
	v_rcp_f32_e32 v240, v156
	v_cvt_f32_ubyte2_e32 v156, v237
	v_add_f32_e32 v156, 0.5, v156
	v_rcp_f32_e32 v220, v156
	v_cvt_f32_ubyte3_e32 v156, v236
	v_add_f32_e32 v156, 0.5, v156
	v_rcp_f32_e32 v241, v156
	v_cvt_f32_ubyte3_e32 v156, v237
	v_add_f32_e32 v156, 0.5, v156
	v_cvt_f32_ubyte1_e32 v237, v216
	v_cvt_f32_ubyte0_e32 v236, v216
	v_cvt_f32_ubyte2_e32 v242, v216
	v_rcp_f32_e32 v221, v156
	v_pk_add_f32 v[242:243], v[242:243], 0.5 op_sel_hi:[1,0]
	v_pk_add_f32 v[236:237], v[236:237], 0.5 op_sel_hi:[1,0]
	v_cvt_f32_ubyte0_e32 v156, v214
	v_pk_mul_f32 v[236:237], v[236:237], v[238:239]
	v_pk_mul_f32 v[238:239], v[242:243], v[240:241]
	v_pk_mul_f32 v[16:17], v[16:17], v[236:237]
	v_pk_mul_f32 v[18:19], v[18:19], v[238:239]
	v_cvt_f32_ubyte3_e32 v239, v217
	v_cvt_f32_ubyte2_e32 v238, v217
	v_cvt_f32_ubyte1_e32 v237, v217
	v_cvt_f32_ubyte0_e32 v236, v217
	v_pk_add_f32 v[216:217], v[238:239], 0.5 op_sel_hi:[1,0]
	v_add_f32_e32 v156, 0.5, v156
	v_pk_mul_f32 v[216:217], v[216:217], v[220:221]
	v_pk_add_f32 v[236:237], v[236:237], 0.5 op_sel_hi:[1,0]
	v_pk_mul_f32 v[22:23], v[22:23], v[216:217]
	v_rcp_f32_e32 v216, v156
	v_cvt_f32_ubyte0_e32 v156, v215
	v_pk_mul_f32 v[218:219], v[236:237], v[218:219]
	v_add_f32_e32 v156, 0.5, v156
	v_pk_mul_f32 v[20:21], v[20:21], v[218:219]
	v_rcp_f32_e32 v218, v156
	v_cvt_f32_ubyte1_e32 v156, v214
	v_add_f32_e32 v156, 0.5, v156
	v_rcp_f32_e32 v217, v156
	v_cvt_f32_ubyte1_e32 v156, v215
	v_add_f32_e32 v156, 0.5, v156
	v_rcp_f32_e32 v219, v156
	v_cvt_f32_ubyte2_e32 v156, v214
	v_add_f32_e32 v156, 0.5, v156
	v_rcp_f32_e32 v220, v156
	v_cvt_f32_ubyte2_e32 v156, v215
	v_add_f32_e32 v156, 0.5, v156
	v_rcp_f32_e32 v236, v156
	v_cvt_f32_ubyte3_e32 v156, v214
	v_add_f32_e32 v156, 0.5, v156
	v_rcp_f32_e32 v221, v156
	v_cvt_f32_ubyte3_e32 v156, v215
	v_add_f32_e32 v156, 0.5, v156
	v_cvt_f32_ubyte1_e32 v215, v212
	v_cvt_f32_ubyte0_e32 v214, v212
	v_cvt_f32_ubyte3_e32 v239, v212
	v_cvt_f32_ubyte2_e32 v238, v212
	v_rcp_f32_e32 v237, v156
	v_pk_add_f32 v[238:239], v[238:239], 0.5 op_sel_hi:[1,0]
	v_pk_add_f32 v[214:215], v[214:215], 0.5 op_sel_hi:[1,0]
	v_cvt_f32_ubyte0_e32 v156, v210
	v_pk_mul_f32 v[214:215], v[214:215], v[216:217]
	v_pk_mul_f32 v[216:217], v[238:239], v[220:221]
	v_pk_mul_f32 v[48:49], v[48:49], v[214:215]
	v_pk_mul_f32 v[50:51], v[50:51], v[216:217]
	v_cvt_f32_ubyte3_e32 v217, v213
	v_cvt_f32_ubyte2_e32 v216, v213
	v_cvt_f32_ubyte1_e32 v215, v213
	v_cvt_f32_ubyte0_e32 v214, v213
	v_pk_add_f32 v[212:213], v[216:217], 0.5 op_sel_hi:[1,0]
	v_add_f32_e32 v156, 0.5, v156
	v_pk_mul_f32 v[212:213], v[212:213], v[236:237]
	v_pk_add_f32 v[214:215], v[214:215], 0.5 op_sel_hi:[1,0]
	v_pk_mul_f32 v[54:55], v[54:55], v[212:213]
	v_rcp_f32_e32 v212, v156
	v_cvt_f32_ubyte0_e32 v156, v211
	v_pk_mul_f32 v[214:215], v[214:215], v[218:219]
	v_add_f32_e32 v156, 0.5, v156
	v_pk_mul_f32 v[52:53], v[52:53], v[214:215]
	v_rcp_f32_e32 v214, v156
	v_cvt_f32_ubyte1_e32 v156, v210
	v_add_f32_e32 v156, 0.5, v156
	v_rcp_f32_e32 v213, v156
	v_cvt_f32_ubyte1_e32 v156, v211
	v_add_f32_e32 v156, 0.5, v156
	v_rcp_f32_e32 v215, v156
	v_cvt_f32_ubyte2_e32 v156, v210
	v_add_f32_e32 v156, 0.5, v156
	v_rcp_f32_e32 v216, v156
	v_cvt_f32_ubyte2_e32 v156, v211
	v_add_f32_e32 v156, 0.5, v156
	v_rcp_f32_e32 v218, v156
	v_cvt_f32_ubyte3_e32 v156, v210
	v_add_f32_e32 v156, 0.5, v156
	v_rcp_f32_e32 v217, v156
	v_cvt_f32_ubyte3_e32 v156, v211
	v_add_f32_e32 v156, 0.5, v156
	v_cvt_f32_ubyte1_e32 v211, v208
	v_cvt_f32_ubyte0_e32 v210, v208
	v_cvt_f32_ubyte3_e32 v221, v208
	v_cvt_f32_ubyte2_e32 v220, v208
	v_rcp_f32_e32 v219, v156
	v_pk_add_f32 v[220:221], v[220:221], 0.5 op_sel_hi:[1,0]
	v_pk_add_f32 v[210:211], v[210:211], 0.5 op_sel_hi:[1,0]
	v_cvt_f32_ubyte0_e32 v156, v206
	v_pk_mul_f32 v[210:211], v[210:211], v[212:213]
	v_pk_mul_f32 v[212:213], v[220:221], v[216:217]
	v_pk_mul_f32 v[24:25], v[24:25], v[210:211]
	v_pk_mul_f32 v[26:27], v[26:27], v[212:213]
	v_cvt_f32_ubyte3_e32 v213, v209
	v_cvt_f32_ubyte2_e32 v212, v209
	v_cvt_f32_ubyte1_e32 v211, v209
	v_cvt_f32_ubyte0_e32 v210, v209
	v_pk_add_f32 v[208:209], v[212:213], 0.5 op_sel_hi:[1,0]
	v_add_f32_e32 v156, 0.5, v156
	v_pk_mul_f32 v[208:209], v[208:209], v[218:219]
	v_pk_add_f32 v[210:211], v[210:211], 0.5 op_sel_hi:[1,0]
	v_pk_mul_f32 v[30:31], v[30:31], v[208:209]
	v_rcp_f32_e32 v208, v156
	v_cvt_f32_ubyte0_e32 v156, v207
	v_pk_mul_f32 v[210:211], v[210:211], v[214:215]
	v_add_f32_e32 v156, 0.5, v156
	v_pk_mul_f32 v[28:29], v[28:29], v[210:211]
	v_rcp_f32_e32 v210, v156
	v_cvt_f32_ubyte1_e32 v156, v206
	v_add_f32_e32 v156, 0.5, v156
	v_rcp_f32_e32 v209, v156
	v_cvt_f32_ubyte1_e32 v156, v207
	v_add_f32_e32 v156, 0.5, v156
	v_rcp_f32_e32 v211, v156
	v_cvt_f32_ubyte2_e32 v156, v206
	v_add_f32_e32 v156, 0.5, v156
	v_rcp_f32_e32 v212, v156
	v_cvt_f32_ubyte2_e32 v156, v207
	v_add_f32_e32 v156, 0.5, v156
	v_rcp_f32_e32 v214, v156
	v_cvt_f32_ubyte3_e32 v156, v206
	v_add_f32_e32 v156, 0.5, v156
	v_rcp_f32_e32 v213, v156
	v_cvt_f32_ubyte3_e32 v156, v207
	v_add_f32_e32 v156, 0.5, v156
	v_cvt_f32_ubyte1_e32 v207, v204
	v_cvt_f32_ubyte0_e32 v206, v204
	v_cvt_f32_ubyte3_e32 v217, v204
	v_cvt_f32_ubyte2_e32 v216, v204
	v_rcp_f32_e32 v215, v156
	v_pk_add_f32 v[216:217], v[216:217], 0.5 op_sel_hi:[1,0]
	v_pk_add_f32 v[206:207], v[206:207], 0.5 op_sel_hi:[1,0]
	v_cvt_f32_ubyte0_e32 v156, v202
	v_pk_mul_f32 v[206:207], v[206:207], v[208:209]
	v_pk_mul_f32 v[208:209], v[216:217], v[212:213]
	v_pk_mul_f32 v[56:57], v[56:57], v[206:207]
	v_pk_mul_f32 v[58:59], v[58:59], v[208:209]
	v_cvt_f32_ubyte3_e32 v209, v205
	v_cvt_f32_ubyte2_e32 v208, v205
	v_cvt_f32_ubyte1_e32 v207, v205
	v_cvt_f32_ubyte0_e32 v206, v205
	v_pk_add_f32 v[204:205], v[208:209], 0.5 op_sel_hi:[1,0]
	v_add_f32_e32 v156, 0.5, v156
	v_pk_mul_f32 v[204:205], v[204:205], v[214:215]
	v_pk_add_f32 v[206:207], v[206:207], 0.5 op_sel_hi:[1,0]
	v_pk_mul_f32 v[62:63], v[62:63], v[204:205]
	v_rcp_f32_e32 v204, v156
	v_cvt_f32_ubyte0_e32 v156, v203
	v_pk_mul_f32 v[206:207], v[206:207], v[210:211]
	v_add_f32_e32 v156, 0.5, v156
	v_pk_mul_f32 v[60:61], v[60:61], v[206:207]
	v_rcp_f32_e32 v206, v156
	v_cvt_f32_ubyte1_e32 v156, v202
	v_add_f32_e32 v156, 0.5, v156
	v_rcp_f32_e32 v205, v156
	v_cvt_f32_ubyte1_e32 v156, v203
	v_add_f32_e32 v156, 0.5, v156
	v_rcp_f32_e32 v207, v156
	v_cvt_f32_ubyte2_e32 v156, v202
	v_add_f32_e32 v156, 0.5, v156
	v_rcp_f32_e32 v208, v156
	v_cvt_f32_ubyte2_e32 v156, v203
	v_addc_co_u32_e32 v1, vcc, 0, v1, vcc
	v_add_f32_e32 v156, 0.5, v156
	v_add_co_u32_e32 v6, vcc, s82, v2
	v_rcp_f32_e32 v210, v156
	v_cvt_f32_ubyte3_e32 v156, v202
	v_addc_co_u32_e32 v7, vcc, 0, v3, vcc
	v_add_f32_e32 v156, 0.5, v156
	global_load_dwordx2 v[184:185], v[0:1], off
	global_load_dwordx2 v[186:187], v[6:7], off
	global_load_dwordx2 v[180:181], v[0:1], off offset:512
	global_load_dwordx2 v[182:183], v[6:7], off offset:512
	global_load_dwordx2 v[176:177], v[0:1], off offset:1024
	global_load_dwordx2 v[178:179], v[6:7], off offset:1024
	global_load_dwordx2 v[144:145], v[0:1], off offset:1536
	global_load_dwordx2 v[146:147], v[6:7], off offset:1536
	global_load_dwordx2 v[12:13], v[0:1], off offset:2048
	global_load_dwordx2 v[14:15], v[6:7], off offset:2048
	global_load_dwordx2 v[8:9], v[0:1], off offset:2560
	global_load_dwordx2 v[10:11], v[6:7], off offset:2560
	global_load_dwordx2 v[2:3], v[0:1], off offset:3072
	global_load_dwordx2 v[4:5], v[6:7], off offset:3072
	s_nop 0
	global_load_dwordx2 v[0:1], v[0:1], off offset:3584
	s_nop 0
	global_load_dwordx2 v[6:7], v[6:7], off offset:3584
	v_rcp_f32_e32 v209, v156
	v_cvt_f32_ubyte3_e32 v156, v203
	v_add_f32_e32 v156, 0.5, v156
	v_cvt_f32_ubyte1_e32 v203, v200
	v_cvt_f32_ubyte0_e32 v202, v200
	v_cvt_f32_ubyte3_e32 v213, v200
	v_cvt_f32_ubyte2_e32 v212, v200
	v_rcp_f32_e32 v211, v156
	v_pk_add_f32 v[212:213], v[212:213], 0.5 op_sel_hi:[1,0]
	v_pk_add_f32 v[202:203], v[202:203], 0.5 op_sel_hi:[1,0]
	v_cvt_f32_ubyte0_e32 v156, v198
	v_pk_mul_f32 v[202:203], v[202:203], v[204:205]
	v_pk_mul_f32 v[204:205], v[212:213], v[208:209]
	v_pk_mul_f32 v[32:33], v[32:33], v[202:203]
	v_pk_mul_f32 v[34:35], v[34:35], v[204:205]
	v_cvt_f32_ubyte3_e32 v205, v201
	v_cvt_f32_ubyte2_e32 v204, v201
	v_cvt_f32_ubyte1_e32 v203, v201
	v_cvt_f32_ubyte0_e32 v202, v201
	v_pk_add_f32 v[200:201], v[204:205], 0.5 op_sel_hi:[1,0]
	v_add_f32_e32 v156, 0.5, v156
	v_pk_mul_f32 v[200:201], v[200:201], v[210:211]
	v_pk_add_f32 v[202:203], v[202:203], 0.5 op_sel_hi:[1,0]
	v_pk_mul_f32 v[38:39], v[38:39], v[200:201]
	v_rcp_f32_e32 v200, v156
	v_cvt_f32_ubyte0_e32 v156, v199
	v_pk_mul_f32 v[202:203], v[202:203], v[206:207]
	v_add_f32_e32 v156, 0.5, v156
	v_pk_mul_f32 v[36:37], v[36:37], v[202:203]
	v_rcp_f32_e32 v202, v156
	v_cvt_f32_ubyte1_e32 v156, v198
	v_add_f32_e32 v156, 0.5, v156
	v_rcp_f32_e32 v201, v156
	v_cvt_f32_ubyte1_e32 v156, v199
	v_add_f32_e32 v156, 0.5, v156
	v_rcp_f32_e32 v203, v156
	v_cvt_f32_ubyte2_e32 v156, v198
	v_add_f32_e32 v156, 0.5, v156
	v_rcp_f32_e32 v204, v156
	v_cvt_f32_ubyte2_e32 v156, v199
	v_add_f32_e32 v156, 0.5, v156
	v_rcp_f32_e32 v206, v156
	v_cvt_f32_ubyte3_e32 v156, v198
	v_add_f32_e32 v156, 0.5, v156
	v_rcp_f32_e32 v205, v156
	v_cvt_f32_ubyte3_e32 v156, v199
	v_add_f32_e32 v156, 0.5, v156
	v_cvt_f32_ubyte1_e32 v199, v196
	v_cvt_f32_ubyte0_e32 v198, v196
	v_cvt_f32_ubyte3_e32 v209, v196
	v_cvt_f32_ubyte2_e32 v208, v196
	v_rcp_f32_e32 v207, v156
	v_pk_add_f32 v[208:209], v[208:209], 0.5 op_sel_hi:[1,0]
	v_pk_add_f32 v[198:199], v[198:199], 0.5 op_sel_hi:[1,0]
	v_cvt_f32_ubyte0_e32 v156, v194
	v_pk_mul_f32 v[198:199], v[198:199], v[200:201]
	v_pk_mul_f32 v[200:201], v[208:209], v[204:205]
	v_pk_mul_f32 v[64:65], v[64:65], v[198:199]
	v_pk_mul_f32 v[66:67], v[66:67], v[200:201]
	v_cvt_f32_ubyte3_e32 v201, v197
	v_cvt_f32_ubyte2_e32 v200, v197
	v_cvt_f32_ubyte1_e32 v199, v197
	v_cvt_f32_ubyte0_e32 v198, v197
	v_pk_add_f32 v[196:197], v[200:201], 0.5 op_sel_hi:[1,0]
	v_add_f32_e32 v156, 0.5, v156
	v_pk_mul_f32 v[196:197], v[196:197], v[206:207]
	v_pk_add_f32 v[198:199], v[198:199], 0.5 op_sel_hi:[1,0]
	v_pk_mul_f32 v[70:71], v[70:71], v[196:197]
	v_rcp_f32_e32 v196, v156
	v_cvt_f32_ubyte0_e32 v156, v195
	v_pk_mul_f32 v[198:199], v[198:199], v[202:203]
	v_add_f32_e32 v156, 0.5, v156
	v_pk_mul_f32 v[68:69], v[68:69], v[198:199]
	v_rcp_f32_e32 v198, v156
	v_cvt_f32_ubyte1_e32 v156, v194
	v_add_f32_e32 v156, 0.5, v156
	v_rcp_f32_e32 v197, v156
	v_cvt_f32_ubyte1_e32 v156, v195
	v_add_f32_e32 v156, 0.5, v156
	v_rcp_f32_e32 v199, v156
	v_cvt_f32_ubyte2_e32 v156, v194
	v_add_f32_e32 v156, 0.5, v156
	v_rcp_f32_e32 v200, v156
	v_cvt_f32_ubyte2_e32 v156, v195
	v_add_f32_e32 v156, 0.5, v156
	v_rcp_f32_e32 v202, v156
	v_cvt_f32_ubyte3_e32 v156, v194
	v_add_f32_e32 v156, 0.5, v156
	v_rcp_f32_e32 v201, v156
	v_cvt_f32_ubyte3_e32 v156, v195
	v_add_f32_e32 v156, 0.5, v156
	v_cvt_f32_ubyte1_e32 v195, v192
	v_cvt_f32_ubyte0_e32 v194, v192
	v_cvt_f32_ubyte3_e32 v205, v192
	v_cvt_f32_ubyte2_e32 v204, v192
	v_rcp_f32_e32 v203, v156
	v_pk_add_f32 v[204:205], v[204:205], 0.5 op_sel_hi:[1,0]
	v_pk_add_f32 v[194:195], v[194:195], 0.5 op_sel_hi:[1,0]
	v_cvt_f32_ubyte0_e32 v156, v190
	v_pk_mul_f32 v[194:195], v[194:195], v[196:197]
	v_pk_mul_f32 v[196:197], v[204:205], v[200:201]
	v_pk_mul_f32 v[40:41], v[40:41], v[194:195]
	v_pk_mul_f32 v[42:43], v[42:43], v[196:197]
	v_cvt_f32_ubyte3_e32 v197, v193
	v_cvt_f32_ubyte2_e32 v196, v193
	v_cvt_f32_ubyte1_e32 v195, v193
	v_cvt_f32_ubyte0_e32 v194, v193
	v_pk_add_f32 v[192:193], v[196:197], 0.5 op_sel_hi:[1,0]
	v_add_f32_e32 v156, 0.5, v156
	v_pk_mul_f32 v[192:193], v[192:193], v[202:203]
	v_pk_add_f32 v[194:195], v[194:195], 0.5 op_sel_hi:[1,0]
	v_pk_mul_f32 v[46:47], v[46:47], v[192:193]
	v_rcp_f32_e32 v192, v156
	v_cvt_f32_ubyte0_e32 v156, v191
	v_pk_mul_f32 v[194:195], v[194:195], v[198:199]
	v_add_f32_e32 v156, 0.5, v156
	v_pk_mul_f32 v[44:45], v[44:45], v[194:195]
	v_rcp_f32_e32 v194, v156
	v_cvt_f32_ubyte1_e32 v156, v190
	v_add_f32_e32 v156, 0.5, v156
	v_rcp_f32_e32 v193, v156
	v_cvt_f32_ubyte1_e32 v156, v191
	v_add_f32_e32 v156, 0.5, v156
	v_rcp_f32_e32 v195, v156
	v_cvt_f32_ubyte2_e32 v156, v190
	v_add_f32_e32 v156, 0.5, v156
	v_rcp_f32_e32 v196, v156
	v_cvt_f32_ubyte2_e32 v156, v191
	v_add_f32_e32 v156, 0.5, v156
	v_rcp_f32_e32 v198, v156
	v_cvt_f32_ubyte3_e32 v156, v190
	v_add_f32_e32 v156, 0.5, v156
	v_rcp_f32_e32 v197, v156
	v_cvt_f32_ubyte3_e32 v156, v191
	v_add_f32_e32 v156, 0.5, v156
	v_cvt_f32_ubyte1_e32 v191, v188
	v_cvt_f32_ubyte0_e32 v190, v188
	v_cvt_f32_ubyte3_e32 v201, v188
	v_cvt_f32_ubyte2_e32 v200, v188
	v_rcp_f32_e32 v199, v156
	v_pk_add_f32 v[200:201], v[200:201], 0.5 op_sel_hi:[1,0]
	v_pk_add_f32 v[190:191], v[190:191], 0.5 op_sel_hi:[1,0]
	s_waitcnt vmcnt(0)
	v_cvt_f32_ubyte0_e32 v156, v186
	v_pk_mul_f32 v[190:191], v[190:191], v[192:193]
	v_pk_mul_f32 v[192:193], v[200:201], v[196:197]
	v_pk_mul_f32 v[72:73], v[72:73], v[190:191]
	v_pk_mul_f32 v[74:75], v[74:75], v[192:193]
	v_cvt_f32_ubyte3_e32 v193, v189
	v_cvt_f32_ubyte2_e32 v192, v189
	v_cvt_f32_ubyte1_e32 v191, v189
	v_cvt_f32_ubyte0_e32 v190, v189
	v_pk_add_f32 v[188:189], v[192:193], 0.5 op_sel_hi:[1,0]
	v_add_f32_e32 v156, 0.5, v156
	v_pk_mul_f32 v[188:189], v[188:189], v[198:199]
	v_pk_add_f32 v[190:191], v[190:191], 0.5 op_sel_hi:[1,0]
	v_pk_mul_f32 v[78:79], v[78:79], v[188:189]
	v_rcp_f32_e32 v188, v156
	v_cvt_f32_ubyte0_e32 v156, v187
	v_pk_mul_f32 v[190:191], v[190:191], v[194:195]
	v_add_f32_e32 v156, 0.5, v156
	v_pk_mul_f32 v[76:77], v[76:77], v[190:191]
	v_rcp_f32_e32 v190, v156
	v_cvt_f32_ubyte1_e32 v156, v186
	v_add_f32_e32 v156, 0.5, v156
	v_rcp_f32_e32 v189, v156
	v_cvt_f32_ubyte1_e32 v156, v187
	v_add_f32_e32 v156, 0.5, v156
	v_rcp_f32_e32 v191, v156
	v_cvt_f32_ubyte2_e32 v156, v186
	v_add_f32_e32 v156, 0.5, v156
	v_rcp_f32_e32 v192, v156
	v_cvt_f32_ubyte2_e32 v156, v187
	v_add_f32_e32 v156, 0.5, v156
	v_rcp_f32_e32 v194, v156
	v_cvt_f32_ubyte3_e32 v156, v186
	v_add_f32_e32 v156, 0.5, v156
	v_rcp_f32_e32 v193, v156
	v_cvt_f32_ubyte3_e32 v156, v187
	v_add_f32_e32 v156, 0.5, v156
	v_cvt_f32_ubyte1_e32 v187, v184
	v_cvt_f32_ubyte0_e32 v186, v184
	v_cvt_f32_ubyte3_e32 v197, v184
	v_cvt_f32_ubyte2_e32 v196, v184
	v_rcp_f32_e32 v195, v156
	v_pk_add_f32 v[196:197], v[196:197], 0.5 op_sel_hi:[1,0]
	v_pk_add_f32 v[186:187], v[186:187], 0.5 op_sel_hi:[1,0]
	v_cvt_f32_ubyte0_e32 v156, v182
	v_pk_mul_f32 v[186:187], v[186:187], v[188:189]
	v_pk_mul_f32 v[188:189], v[196:197], v[192:193]
	v_pk_mul_f32 v[80:81], v[80:81], v[186:187]
	v_pk_mul_f32 v[82:83], v[82:83], v[188:189]
	v_cvt_f32_ubyte3_e32 v189, v185
	v_cvt_f32_ubyte2_e32 v188, v185
	v_cvt_f32_ubyte1_e32 v187, v185
	v_cvt_f32_ubyte0_e32 v186, v185
	v_pk_add_f32 v[184:185], v[188:189], 0.5 op_sel_hi:[1,0]
	v_add_f32_e32 v156, 0.5, v156
	v_pk_mul_f32 v[184:185], v[184:185], v[194:195]
	v_pk_add_f32 v[186:187], v[186:187], 0.5 op_sel_hi:[1,0]
	v_pk_mul_f32 v[86:87], v[86:87], v[184:185]
	v_rcp_f32_e32 v184, v156
	v_cvt_f32_ubyte0_e32 v156, v183
	v_pk_mul_f32 v[186:187], v[186:187], v[190:191]
	v_add_f32_e32 v156, 0.5, v156
	v_pk_mul_f32 v[84:85], v[84:85], v[186:187]
	v_rcp_f32_e32 v186, v156
	v_cvt_f32_ubyte1_e32 v156, v182
	v_add_f32_e32 v156, 0.5, v156
	v_rcp_f32_e32 v185, v156
	v_cvt_f32_ubyte1_e32 v156, v183
	v_add_f32_e32 v156, 0.5, v156
	v_rcp_f32_e32 v187, v156
	v_cvt_f32_ubyte2_e32 v156, v182
	v_add_f32_e32 v156, 0.5, v156
	v_rcp_f32_e32 v188, v156
	v_cvt_f32_ubyte2_e32 v156, v183
	v_add_f32_e32 v156, 0.5, v156
	v_rcp_f32_e32 v190, v156
	v_cvt_f32_ubyte3_e32 v156, v182
	v_add_f32_e32 v156, 0.5, v156
	v_rcp_f32_e32 v189, v156
	v_cvt_f32_ubyte3_e32 v156, v183
	v_add_f32_e32 v156, 0.5, v156
	v_cvt_f32_ubyte1_e32 v183, v180
	v_cvt_f32_ubyte0_e32 v182, v180
	v_cvt_f32_ubyte3_e32 v193, v180
	v_cvt_f32_ubyte2_e32 v192, v180
	v_rcp_f32_e32 v191, v156
	v_pk_add_f32 v[192:193], v[192:193], 0.5 op_sel_hi:[1,0]
	v_pk_add_f32 v[182:183], v[182:183], 0.5 op_sel_hi:[1,0]
	v_cvt_f32_ubyte0_e32 v156, v178
	v_pk_mul_f32 v[182:183], v[182:183], v[184:185]
	v_pk_mul_f32 v[184:185], v[192:193], v[188:189]
	v_pk_mul_f32 v[112:113], v[112:113], v[182:183]
	v_pk_mul_f32 v[114:115], v[114:115], v[184:185]
	v_cvt_f32_ubyte3_e32 v185, v181
	v_cvt_f32_ubyte2_e32 v184, v181
	v_cvt_f32_ubyte1_e32 v183, v181
	v_cvt_f32_ubyte0_e32 v182, v181
	v_pk_add_f32 v[180:181], v[184:185], 0.5 op_sel_hi:[1,0]
	v_add_f32_e32 v156, 0.5, v156
	v_pk_mul_f32 v[180:181], v[180:181], v[190:191]
	v_pk_add_f32 v[182:183], v[182:183], 0.5 op_sel_hi:[1,0]
	v_pk_mul_f32 v[118:119], v[118:119], v[180:181]
	v_rcp_f32_e32 v180, v156
	v_cvt_f32_ubyte0_e32 v156, v179
	v_pk_mul_f32 v[182:183], v[182:183], v[186:187]
	v_add_f32_e32 v156, 0.5, v156
	v_pk_mul_f32 v[116:117], v[116:117], v[182:183]
	v_rcp_f32_e32 v182, v156
	v_cvt_f32_ubyte1_e32 v156, v178
	v_add_f32_e32 v156, 0.5, v156
	v_rcp_f32_e32 v181, v156
	v_cvt_f32_ubyte1_e32 v156, v179
	v_add_f32_e32 v156, 0.5, v156
	v_rcp_f32_e32 v183, v156
	v_cvt_f32_ubyte2_e32 v156, v178
	v_add_f32_e32 v156, 0.5, v156
	v_rcp_f32_e32 v184, v156
	v_cvt_f32_ubyte2_e32 v156, v179
	v_add_f32_e32 v156, 0.5, v156
	v_rcp_f32_e32 v186, v156
	v_cvt_f32_ubyte3_e32 v156, v178
	v_add_f32_e32 v156, 0.5, v156
	v_rcp_f32_e32 v185, v156
	v_cvt_f32_ubyte3_e32 v156, v179
	v_add_f32_e32 v156, 0.5, v156
	v_cvt_f32_ubyte1_e32 v179, v176
	v_cvt_f32_ubyte0_e32 v178, v176
	v_cvt_f32_ubyte3_e32 v189, v176
	v_cvt_f32_ubyte2_e32 v188, v176
	v_rcp_f32_e32 v187, v156
	v_pk_add_f32 v[188:189], v[188:189], 0.5 op_sel_hi:[1,0]
	v_pk_add_f32 v[178:179], v[178:179], 0.5 op_sel_hi:[1,0]
	v_cvt_f32_ubyte0_e32 v156, v146
	v_pk_mul_f32 v[178:179], v[178:179], v[180:181]
	v_pk_mul_f32 v[180:181], v[188:189], v[184:185]
	v_pk_mul_f32 v[88:89], v[88:89], v[178:179]
	v_pk_mul_f32 v[90:91], v[90:91], v[180:181]
	v_cvt_f32_ubyte3_e32 v181, v177
	v_cvt_f32_ubyte2_e32 v180, v177
	v_cvt_f32_ubyte1_e32 v179, v177
	v_cvt_f32_ubyte0_e32 v178, v177
	v_pk_add_f32 v[176:177], v[180:181], 0.5 op_sel_hi:[1,0]
	v_add_f32_e32 v156, 0.5, v156
	v_pk_mul_f32 v[176:177], v[176:177], v[186:187]
	v_pk_add_f32 v[178:179], v[178:179], 0.5 op_sel_hi:[1,0]
	v_pk_mul_f32 v[94:95], v[94:95], v[176:177]
	v_rcp_f32_e32 v176, v156
	v_cvt_f32_ubyte0_e32 v156, v147
	v_pk_mul_f32 v[178:179], v[178:179], v[182:183]
	v_add_f32_e32 v156, 0.5, v156
	v_pk_mul_f32 v[92:93], v[92:93], v[178:179]
	v_rcp_f32_e32 v178, v156
	v_cvt_f32_ubyte1_e32 v156, v146
	v_add_f32_e32 v156, 0.5, v156
	v_rcp_f32_e32 v177, v156
	v_cvt_f32_ubyte1_e32 v156, v147
	v_add_f32_e32 v156, 0.5, v156
	v_rcp_f32_e32 v179, v156
	v_cvt_f32_ubyte2_e32 v156, v146
	v_cvt_f32_ubyte3_e32 v146, v146
	v_add_f32_e32 v156, 0.5, v156
	v_add_f32_e32 v146, 0.5, v146
	v_rcp_f32_e32 v180, v156
	v_rcp_f32_e32 v181, v146
	v_cvt_f32_ubyte3_e32 v146, v147
	v_cvt_f32_ubyte2_e32 v156, v147
	v_add_f32_e32 v146, 0.5, v146
	v_add_f32_e32 v156, 0.5, v156
	v_rcp_f32_e32 v183, v146
	v_cvt_f32_ubyte1_e32 v147, v144
	v_cvt_f32_ubyte0_e32 v146, v144
	v_cvt_f32_ubyte3_e32 v185, v144
	v_cvt_f32_ubyte2_e32 v184, v144
	v_rcp_f32_e32 v182, v156
	v_pk_add_f32 v[184:185], v[184:185], 0.5 op_sel_hi:[1,0]
	v_pk_add_f32 v[146:147], v[146:147], 0.5 op_sel_hi:[1,0]
	v_cvt_f32_ubyte2_e32 v156, v14
	v_pk_mul_f32 v[146:147], v[146:147], v[176:177]
	v_pk_mul_f32 v[176:177], v[184:185], v[180:181]
	v_pk_mul_f32 v[120:121], v[120:121], v[146:147]
	v_pk_mul_f32 v[122:123], v[122:123], v[176:177]
	v_cvt_f32_ubyte3_e32 v177, v145
	v_cvt_f32_ubyte2_e32 v176, v145
	v_cvt_f32_ubyte1_e32 v147, v145
	v_cvt_f32_ubyte0_e32 v146, v145
	v_pk_add_f32 v[144:145], v[176:177], 0.5 op_sel_hi:[1,0]
	v_pk_add_f32 v[146:147], v[146:147], 0.5 op_sel_hi:[1,0]
	v_pk_mul_f32 v[144:145], v[144:145], v[182:183]
	v_pk_mul_f32 v[146:147], v[146:147], v[178:179]
	v_pk_mul_f32 v[126:127], v[126:127], v[144:145]
	v_cvt_f32_ubyte0_e32 v145, v15
	v_add_f32_e32 v145, 0.5, v145
	v_pk_mul_f32 v[124:125], v[124:125], v[146:147]
	v_cvt_f32_ubyte0_e32 v144, v14
	v_rcp_f32_e32 v146, v145
	v_cvt_f32_ubyte1_e32 v145, v14
	v_cvt_f32_ubyte3_e32 v14, v14
	v_add_f32_e32 v144, 0.5, v144
	v_add_f32_e32 v145, 0.5, v145
	v_add_f32_e32 v156, 0.5, v156
	v_add_f32_e32 v14, 0.5, v14
	v_rcp_f32_e32 v144, v144
	v_rcp_f32_e32 v145, v145
	v_rcp_f32_e32 v176, v156
	v_rcp_f32_e32 v177, v14
	v_cvt_f32_ubyte3_e32 v14, v15
	v_cvt_f32_ubyte2_e32 v156, v15
	v_add_f32_e32 v14, 0.5, v14
	v_cvt_f32_ubyte1_e32 v147, v15
	v_add_f32_e32 v156, 0.5, v156
	v_rcp_f32_e32 v179, v14
	v_cvt_f32_ubyte1_e32 v15, v12
	v_cvt_f32_ubyte0_e32 v14, v12
	v_cvt_f32_ubyte3_e32 v181, v12
	v_cvt_f32_ubyte2_e32 v180, v12
	v_rcp_f32_e32 v178, v156
	v_pk_add_f32 v[180:181], v[180:181], 0.5 op_sel_hi:[1,0]
	v_pk_add_f32 v[14:15], v[14:15], 0.5 op_sel_hi:[1,0]
	v_add_f32_e32 v147, 0.5, v147
	v_pk_mul_f32 v[14:15], v[14:15], v[144:145]
	v_pk_mul_f32 v[144:145], v[180:181], v[176:177]
	v_rcp_f32_e32 v147, v147
	v_pk_mul_f32 v[98:99], v[98:99], v[144:145]
	v_cvt_f32_ubyte3_e32 v145, v13
	v_cvt_f32_ubyte2_e32 v144, v13
	v_pk_mul_f32 v[96:97], v[96:97], v[14:15]
	v_cvt_f32_ubyte1_e32 v15, v13
	v_cvt_f32_ubyte0_e32 v14, v13
	v_pk_add_f32 v[12:13], v[144:145], 0.5 op_sel_hi:[1,0]
	v_pk_add_f32 v[14:15], v[14:15], 0.5 op_sel_hi:[1,0]
	v_pk_mul_f32 v[12:13], v[12:13], v[178:179]
	v_pk_mul_f32 v[14:15], v[14:15], v[146:147]
	v_pk_mul_f32 v[102:103], v[102:103], v[12:13]
	v_cvt_f32_ubyte0_e32 v13, v11
	v_add_f32_e32 v13, 0.5, v13
	v_pk_mul_f32 v[100:101], v[100:101], v[14:15]
	v_cvt_f32_ubyte0_e32 v12, v10
	v_rcp_f32_e32 v14, v13
	v_cvt_f32_ubyte1_e32 v13, v10
	v_cvt_f32_ubyte2_e32 v144, v10
	v_cvt_f32_ubyte2_e32 v145, v11
	v_cvt_f32_ubyte3_e32 v10, v10
	v_add_f32_e32 v12, 0.5, v12
	v_add_f32_e32 v13, 0.5, v13
	v_add_f32_e32 v144, 0.5, v144
	v_add_f32_e32 v145, 0.5, v145
	v_add_f32_e32 v10, 0.5, v10
	v_rcp_f32_e32 v12, v12
	v_rcp_f32_e32 v13, v13
	v_rcp_f32_e32 v144, v144
	v_rcp_f32_e32 v146, v145
	v_rcp_f32_e32 v145, v10
	v_cvt_f32_ubyte3_e32 v10, v11
	v_add_f32_e32 v10, 0.5, v10
	v_cvt_f32_ubyte1_e32 v15, v11
	v_rcp_f32_e32 v147, v10
	v_cvt_f32_ubyte1_e32 v11, v8
	v_cvt_f32_ubyte0_e32 v10, v8
	v_cvt_f32_ubyte3_e32 v177, v8
	v_cvt_f32_ubyte2_e32 v176, v8
	v_pk_add_f32 v[176:177], v[176:177], 0.5 op_sel_hi:[1,0]
	v_pk_add_f32 v[10:11], v[10:11], 0.5 op_sel_hi:[1,0]
	v_add_f32_e32 v15, 0.5, v15
	v_pk_mul_f32 v[10:11], v[10:11], v[12:13]
	v_pk_mul_f32 v[12:13], v[176:177], v[144:145]
	v_rcp_f32_e32 v15, v15
	v_pk_mul_f32 v[130:131], v[130:131], v[12:13]
	v_cvt_f32_ubyte3_e32 v13, v9
	v_cvt_f32_ubyte2_e32 v12, v9
	v_pk_mul_f32 v[128:129], v[128:129], v[10:11]
	v_cvt_f32_ubyte1_e32 v11, v9
	v_cvt_f32_ubyte0_e32 v10, v9
	v_pk_add_f32 v[8:9], v[12:13], 0.5 op_sel_hi:[1,0]
	v_pk_add_f32 v[10:11], v[10:11], 0.5 op_sel_hi:[1,0]
	v_pk_mul_f32 v[8:9], v[8:9], v[146:147]
	v_pk_mul_f32 v[10:11], v[10:11], v[14:15]
	v_pk_mul_f32 v[134:135], v[134:135], v[8:9]
	v_cvt_f32_ubyte0_e32 v9, v5
	v_add_f32_e32 v9, 0.5, v9
	v_pk_mul_f32 v[132:133], v[132:133], v[10:11]
	v_cvt_f32_ubyte0_e32 v8, v4
	v_rcp_f32_e32 v10, v9
	v_cvt_f32_ubyte1_e32 v9, v4
	v_cvt_f32_ubyte2_e32 v12, v4
	v_cvt_f32_ubyte2_e32 v13, v5
	v_cvt_f32_ubyte3_e32 v4, v4
	v_add_f32_e32 v8, 0.5, v8
	v_add_f32_e32 v9, 0.5, v9
	v_add_f32_e32 v12, 0.5, v12
	v_add_f32_e32 v13, 0.5, v13
	v_add_f32_e32 v4, 0.5, v4
	v_rcp_f32_e32 v8, v8
	v_rcp_f32_e32 v9, v9
	v_rcp_f32_e32 v12, v12
	v_rcp_f32_e32 v14, v13
	v_rcp_f32_e32 v13, v4
	v_cvt_f32_ubyte3_e32 v4, v5
	v_add_f32_e32 v4, 0.5, v4
	v_cvt_f32_ubyte1_e32 v11, v5
	v_rcp_f32_e32 v15, v4
	v_cvt_f32_ubyte1_e32 v5, v2
	v_cvt_f32_ubyte0_e32 v4, v2
	v_cvt_f32_ubyte3_e32 v145, v2
	v_cvt_f32_ubyte2_e32 v144, v2
	v_pk_add_f32 v[144:145], v[144:145], 0.5 op_sel_hi:[1,0]
	v_pk_add_f32 v[4:5], v[4:5], 0.5 op_sel_hi:[1,0]
	v_add_f32_e32 v11, 0.5, v11
	v_pk_mul_f32 v[4:5], v[4:5], v[8:9]
	v_pk_mul_f32 v[8:9], v[144:145], v[12:13]
	v_rcp_f32_e32 v11, v11
	v_pk_mul_f32 v[106:107], v[106:107], v[8:9]
	v_cvt_f32_ubyte3_e32 v9, v3
	v_cvt_f32_ubyte2_e32 v8, v3
	v_pk_mul_f32 v[104:105], v[104:105], v[4:5]
	v_cvt_f32_ubyte1_e32 v5, v3
	v_cvt_f32_ubyte0_e32 v4, v3
	v_pk_add_f32 v[2:3], v[8:9], 0.5 op_sel_hi:[1,0]
	v_pk_add_f32 v[4:5], v[4:5], 0.5 op_sel_hi:[1,0]
	v_pk_mul_f32 v[2:3], v[2:3], v[14:15]
	v_pk_mul_f32 v[4:5], v[4:5], v[10:11]
	v_pk_mul_f32 v[110:111], v[110:111], v[2:3]
	v_cvt_f32_ubyte0_e32 v3, v7
	v_add_f32_e32 v3, 0.5, v3
	v_pk_mul_f32 v[108:109], v[108:109], v[4:5]
	v_cvt_f32_ubyte0_e32 v2, v6
	v_rcp_f32_e32 v4, v3
	v_cvt_f32_ubyte1_e32 v3, v6
	v_cvt_f32_ubyte2_e32 v8, v6
	v_cvt_f32_ubyte2_e32 v9, v7
	v_cvt_f32_ubyte3_e32 v6, v6
	v_add_f32_e32 v2, 0.5, v2
	v_add_f32_e32 v3, 0.5, v3
	v_add_f32_e32 v8, 0.5, v8
	v_add_f32_e32 v9, 0.5, v9
	v_add_f32_e32 v6, 0.5, v6
	v_rcp_f32_e32 v2, v2
	v_rcp_f32_e32 v3, v3
	v_rcp_f32_e32 v8, v8
	v_rcp_f32_e32 v10, v9
	v_rcp_f32_e32 v9, v6
	v_cvt_f32_ubyte3_e32 v6, v7
	v_cvt_f32_ubyte1_e32 v5, v7
	v_add_f32_e32 v6, 0.5, v6
	v_add_f32_e32 v5, 0.5, v5
	v_rcp_f32_e32 v11, v6
	v_cvt_f32_ubyte1_e32 v7, v0
	v_cvt_f32_ubyte0_e32 v6, v0
	v_cvt_f32_ubyte3_e32 v13, v0
	v_cvt_f32_ubyte2_e32 v12, v0
	v_rcp_f32_e32 v5, v5
	v_pk_add_f32 v[12:13], v[12:13], 0.5 op_sel_hi:[1,0]
	v_pk_add_f32 v[6:7], v[6:7], 0.5 op_sel_hi:[1,0]
	s_nop 0
	v_pk_mul_f32 v[2:3], v[6:7], v[2:3]
	v_pk_mul_f32 v[6:7], v[12:13], v[8:9]
	v_pk_mul_f32 v[144:145], v[136:137], v[2:3]
	v_pk_mul_f32 v[146:147], v[138:139], v[6:7]
	v_cvt_f32_ubyte1_e32 v3, v1
	v_cvt_f32_ubyte0_e32 v2, v1
	v_cvt_f32_ubyte3_e32 v7, v1
	v_cvt_f32_ubyte2_e32 v6, v1
	v_pk_add_f32 v[0:1], v[6:7], 0.5 op_sel_hi:[1,0]
	v_pk_add_f32 v[2:3], v[2:3], 0.5 op_sel_hi:[1,0]
	v_pk_mul_f32 v[0:1], v[0:1], v[10:11]
	v_pk_mul_f32 v[2:3], v[2:3], v[4:5]
	v_pk_mul_f32 v[138:139], v[142:143], v[0:1]
	v_pk_mul_f32 v[136:137], v[140:141], v[2:3]
	ds_read_b128 v[8:11], v230
	ds_read_b128 v[12:15], v230 offset:1024
	ds_read_b128 v[0:3], v230 offset:2048
	ds_read_b128 v[4:7], v230 offset:3072
	s_add_u32 s54, s46, 0x40680
	s_addc_u32 s55, s47, 0
	s_mov_b32 m0, s92
	v_lshl_add_u64 v[140:141], s[54:55], 0, v[148:149]
	ds_read_b128 v[176:179], v227
	ds_read_b128 v[180:183], v227 offset:1024
	ds_read_b128 v[184:187], v227 offset:2048
	ds_read_b128 v[188:191], v227 offset:3072
	ds_read_b128 v[192:195], v227 offset:4096
	ds_read_b128 v[196:199], v227 offset:5120
	ds_read_b128 v[200:203], v227 offset:6144
	ds_read_b128 v[204:207], v227 offset:7168
	global_load_lds_dwordx4 v[140:141], off
	v_lshl_add_u64 v[140:141], s[54:55], 0, v[152:153]
	s_mov_b32 m0, s91
	s_nop 0
	global_load_lds_dwordx4 v[140:141], off
	s_waitcnt lgkmcnt(8)
	s_barrier
	s_waitcnt lgkmcnt(0)
	s_setprio 1
	s_waitcnt lgkmcnt(0)
	v_mfma_f32_16x16x128_f8f6f4 v[16:19], v[8:15], v[176:183], v[16:19]
	v_mfma_f32_16x16x128_f8f6f4 v[20:23], v[0:7], v[176:183], v[20:23]
	v_mfma_f32_16x16x128_f8f6f4 v[24:27], v[8:15], v[184:191], v[24:27]
	v_mfma_f32_16x16x128_f8f6f4 v[28:31], v[0:7], v[184:191], v[28:31]
	v_mfma_f32_16x16x128_f8f6f4 v[32:35], v[8:15], v[192:199], v[32:35]
	v_mfma_f32_16x16x128_f8f6f4 v[36:39], v[0:7], v[192:199], v[36:39]
	v_mfma_f32_16x16x128_f8f6f4 v[40:43], v[8:15], v[200:207], v[40:43]
	v_mfma_f32_16x16x128_f8f6f4 v[44:47], v[0:7], v[200:207], v[44:47]
	s_setprio 0
	s_barrier
	s_mov_b32 m0, s94
	v_lshl_add_u64 v[140:141], v[170:171], 0, s[28:29]
	ds_read_b128 v[208:211], v231
	ds_read_b128 v[212:215], v231 offset:1024
	ds_read_b128 v[236:239], v231 offset:2048
	ds_read_b128 v[240:243], v231 offset:3072
	global_load_lds_dwordx4 v[140:141], off
	v_lshl_add_u64 v[140:141], v[172:173], 0, s[28:29]
	s_mov_b32 m0, s93
	s_nop 0
	global_load_lds_dwordx4 v[140:141], off
	s_barrier
	s_waitcnt lgkmcnt(0)
	s_setprio 1
	s_waitcnt lgkmcnt(0)
	v_mfma_f32_16x16x128_f8f6f4 v[48:51], v[208:215], v[176:183], v[48:51]
	v_mfma_f32_16x16x128_f8f6f4 v[52:55], v[236:243], v[176:183], v[52:55]
	v_mfma_f32_16x16x128_f8f6f4 v[56:59], v[208:215], v[184:191], v[56:59]
	v_mfma_f32_16x16x128_f8f6f4 v[60:63], v[236:243], v[184:191], v[60:63]
	v_mfma_f32_16x16x128_f8f6f4 v[64:67], v[208:215], v[192:199], v[64:67]
	v_mfma_f32_16x16x128_f8f6f4 v[68:71], v[236:243], v[192:199], v[68:71]
	v_mfma_f32_16x16x128_f8f6f4 v[72:75], v[208:215], v[200:207], v[72:75]
	v_mfma_f32_16x16x128_f8f6f4 v[76:79], v[236:243], v[200:207], v[76:79]
	s_setprio 0
	s_mov_b32 m0, s70
	v_lshl_add_u64 v[140:141], v[174:175], 0, s[28:29]
	s_barrier
	ds_read_b128 v[176:179], v227 offset:16384
	ds_read_b128 v[180:183], v227 offset:17408
	ds_read_b128 v[184:187], v227 offset:18432
	ds_read_b128 v[188:191], v227 offset:19456
	ds_read_b128 v[192:195], v227 offset:20480
	ds_read_b128 v[196:199], v227 offset:21504
	ds_read_b128 v[200:203], v227 offset:22528
	ds_read_b128 v[204:207], v227 offset:23552
	global_load_lds_dwordx4 v[140:141], off
	v_lshl_add_u64 v[140:141], v[168:169], 0, s[28:29]
	s_mov_b32 m0, s71
	s_nop 0
	global_load_lds_dwordx4 v[140:141], off
	s_barrier
	s_waitcnt lgkmcnt(0)
	s_setprio 1
	s_waitcnt lgkmcnt(0)
	v_mfma_f32_16x16x128_f8f6f4 v[80:83], v[8:15], v[176:183], v[80:83]
	v_mfma_f32_16x16x128_f8f6f4 v[84:87], v[0:7], v[176:183], v[84:87]
	v_mfma_f32_16x16x128_f8f6f4 v[88:91], v[8:15], v[184:191], v[88:91]
	v_mfma_f32_16x16x128_f8f6f4 v[92:95], v[0:7], v[184:191], v[92:95]
	v_mfma_f32_16x16x128_f8f6f4 v[96:99], v[8:15], v[192:199], v[96:99]
	v_mfma_f32_16x16x128_f8f6f4 v[100:103], v[0:7], v[192:199], v[100:103]
	v_mfma_f32_16x16x128_f8f6f4 v[104:107], v[8:15], v[200:207], v[104:107]
	v_mfma_f32_16x16x128_f8f6f4 v[108:111], v[0:7], v[200:207], v[108:111]
	s_setprio 0
	s_barrier
	s_add_u32 s54, s48, 0x40700
	s_addc_u32 s55, s49, 0
	s_mov_b32 m0, s52
	v_lshl_add_u64 v[0:1], s[54:55], 0, v[150:151]
	global_load_lds_dwordx4 v[0:1], off
	v_lshl_add_u64 v[0:1], s[54:55], 0, v[154:155]
	s_mov_b32 m0, s95
	s_nop 0
	global_load_lds_dwordx4 v[0:1], off
	s_waitcnt vmcnt(6)
	s_barrier
	s_setprio 1
	v_mfma_f32_16x16x128_f8f6f4 v[112:115], v[208:215], v[176:183], v[112:115]
	v_mfma_f32_16x16x128_f8f6f4 v[116:119], v[236:243], v[176:183], v[116:119]
	v_mfma_f32_16x16x128_f8f6f4 v[120:123], v[208:215], v[184:191], v[120:123]
	v_mfma_f32_16x16x128_f8f6f4 v[124:127], v[236:243], v[184:191], v[124:127]
	v_mfma_f32_16x16x128_f8f6f4 v[128:131], v[208:215], v[192:199], v[128:131]
	v_mfma_f32_16x16x128_f8f6f4 v[132:135], v[236:243], v[192:199], v[132:135]
	v_mfma_f32_16x16x128_f8f6f4 v[144:147], v[208:215], v[200:207], v[144:147]
	v_mfma_f32_16x16x128_f8f6f4 v[136:139], v[236:243], v[200:207], v[136:139]
	s_setprio 0
	s_barrier
	ds_read_b128 v[0:3], v234
	ds_read_b128 v[4:7], v234 offset:1024
	ds_read_b128 v[8:11], v234 offset:2048
	ds_read_b128 v[12:15], v234 offset:3072
	s_add_u32 s54, s46, 0x40700
	s_addc_u32 s55, s47, 0
	s_mov_b32 m0, s72
	v_lshl_add_u64 v[140:141], s[54:55], 0, v[148:149]
	ds_read_b128 v[176:179], v227 offset:32768
	ds_read_b128 v[180:183], v227 offset:33792
	ds_read_b128 v[184:187], v227 offset:34816
	ds_read_b128 v[188:191], v227 offset:35840
	ds_read_b128 v[192:195], v227 offset:36864
	ds_read_b128 v[196:199], v227 offset:37888
	ds_read_b128 v[200:203], v227 offset:38912
	ds_read_b128 v[204:207], v227 offset:39936
	global_load_lds_dwordx4 v[140:141], off
	v_lshl_add_u64 v[140:141], s[54:55], 0, v[152:153]
	s_mov_b32 m0, s73
	s_nop 0
	global_load_lds_dwordx4 v[140:141], off
	s_waitcnt lgkmcnt(8)
	s_barrier
	s_waitcnt lgkmcnt(0)
	s_setprio 1
	s_waitcnt lgkmcnt(0)
	v_mfma_f32_16x16x128_f8f6f4 v[16:19], v[0:7], v[176:183], v[16:19]
	v_mfma_f32_16x16x128_f8f6f4 v[20:23], v[8:15], v[176:183], v[20:23]
	v_mfma_f32_16x16x128_f8f6f4 v[24:27], v[0:7], v[184:191], v[24:27]
	v_mfma_f32_16x16x128_f8f6f4 v[28:31], v[8:15], v[184:191], v[28:31]
	v_mfma_f32_16x16x128_f8f6f4 v[32:35], v[0:7], v[192:199], v[32:35]
	v_mfma_f32_16x16x128_f8f6f4 v[36:39], v[8:15], v[192:199], v[36:39]
	v_mfma_f32_16x16x128_f8f6f4 v[40:43], v[0:7], v[200:207], v[40:43]
	v_mfma_f32_16x16x128_f8f6f4 v[44:47], v[8:15], v[200:207], v[44:47]
	s_setprio 0
	s_barrier
	s_mov_b32 m0, s63
	v_lshl_add_u64 v[140:141], v[170:171], 0, s[30:31]
	ds_read_b128 v[208:211], v233
	ds_read_b128 v[212:215], v233 offset:1024
	ds_read_b128 v[236:239], v233 offset:2048
	ds_read_b128 v[240:243], v233 offset:3072
	global_load_lds_dwordx4 v[140:141], off
	v_lshl_add_u64 v[140:141], v[172:173], 0, s[30:31]
	s_mov_b32 m0, s62
	s_nop 0
	global_load_lds_dwordx4 v[140:141], off
	s_barrier
	s_waitcnt lgkmcnt(0)
	s_setprio 1
	s_waitcnt lgkmcnt(0)
	v_mfma_f32_16x16x128_f8f6f4 v[48:51], v[208:215], v[176:183], v[48:51]
	v_mfma_f32_16x16x128_f8f6f4 v[52:55], v[236:243], v[176:183], v[52:55]
	v_mfma_f32_16x16x128_f8f6f4 v[56:59], v[208:215], v[184:191], v[56:59]
	v_mfma_f32_16x16x128_f8f6f4 v[60:63], v[236:243], v[184:191], v[60:63]
	v_mfma_f32_16x16x128_f8f6f4 v[64:67], v[208:215], v[192:199], v[64:67]
	v_mfma_f32_16x16x128_f8f6f4 v[68:71], v[236:243], v[192:199], v[68:71]
	v_mfma_f32_16x16x128_f8f6f4 v[72:75], v[208:215], v[200:207], v[72:75]
	v_mfma_f32_16x16x128_f8f6f4 v[76:79], v[236:243], v[200:207], v[76:79]
	s_setprio 0
	s_mov_b32 m0, s77
	v_lshl_add_u64 v[140:141], v[174:175], 0, s[30:31]
	s_barrier
	ds_read_b128 v[176:179], v227 offset:49152
	ds_read_b128 v[180:183], v227 offset:50176
	ds_read_b128 v[184:187], v227 offset:51200
	ds_read_b128 v[188:191], v227 offset:52224
	ds_read_b128 v[192:195], v227 offset:53248
	ds_read_b128 v[196:199], v227 offset:54272
	ds_read_b128 v[200:203], v227 offset:55296
	ds_read_b128 v[204:207], v227 offset:56320
	global_load_lds_dwordx4 v[140:141], off
	v_lshl_add_u64 v[140:141], v[168:169], 0, s[30:31]
	s_mov_b32 m0, s78
	s_nop 0
	global_load_lds_dwordx4 v[140:141], off
	s_barrier
	s_waitcnt lgkmcnt(0)
	s_setprio 1
	s_waitcnt lgkmcnt(0)
	v_mfma_f32_16x16x128_f8f6f4 v[80:83], v[0:7], v[176:183], v[80:83]
	v_mfma_f32_16x16x128_f8f6f4 v[84:87], v[8:15], v[176:183], v[84:87]
	v_mfma_f32_16x16x128_f8f6f4 v[88:91], v[0:7], v[184:191], v[88:91]
	v_mfma_f32_16x16x128_f8f6f4 v[92:95], v[8:15], v[184:191], v[92:95]
	v_mfma_f32_16x16x128_f8f6f4 v[96:99], v[0:7], v[192:199], v[96:99]
	v_mfma_f32_16x16x128_f8f6f4 v[100:103], v[8:15], v[192:199], v[100:103]
	v_mfma_f32_16x16x128_f8f6f4 v[104:107], v[0:7], v[200:207], v[104:107]
	v_mfma_f32_16x16x128_f8f6f4 v[108:111], v[8:15], v[200:207], v[108:111]
	s_setprio 0
	s_barrier
	s_add_u32 s48, s48, 0x40780
	s_addc_u32 s49, s49, 0
	s_mov_b32 m0, s64
	v_lshl_add_u64 v[0:1], s[48:49], 0, v[150:151]
	global_load_lds_dwordx4 v[0:1], off
	v_lshl_add_u64 v[0:1], s[48:49], 0, v[154:155]
	s_mov_b32 m0, s53
	s_nop 0
	global_load_lds_dwordx4 v[0:1], off
	s_waitcnt vmcnt(6)
	s_barrier
	s_setprio 1
	v_mfma_f32_16x16x128_f8f6f4 v[112:115], v[208:215], v[176:183], v[112:115]
	v_mfma_f32_16x16x128_f8f6f4 v[116:119], v[236:243], v[176:183], v[116:119]
	v_mfma_f32_16x16x128_f8f6f4 v[120:123], v[208:215], v[184:191], v[120:123]
	v_mfma_f32_16x16x128_f8f6f4 v[124:127], v[236:243], v[184:191], v[124:127]
	v_mfma_f32_16x16x128_f8f6f4 v[128:131], v[208:215], v[192:199], v[128:131]
	v_mfma_f32_16x16x128_f8f6f4 v[132:135], v[236:243], v[192:199], v[132:135]
	v_mfma_f32_16x16x128_f8f6f4 v[144:147], v[208:215], v[200:207], v[144:147]
	v_mfma_f32_16x16x128_f8f6f4 v[136:139], v[236:243], v[200:207], v[136:139]
	s_setprio 0
	s_barrier
	ds_read_b128 v[8:11], v230
	ds_read_b128 v[12:15], v230 offset:1024
	ds_read_b128 v[168:171], v230 offset:2048
	ds_read_b128 v[172:175], v230 offset:3072
	s_add_u32 s46, s46, 0x40780
	s_addc_u32 s47, s47, 0
	s_mov_b32 m0, s92
	v_lshl_add_u64 v[0:1], s[46:47], 0, v[148:149]
	ds_read_b128 v[176:179], v227
	ds_read_b128 v[180:183], v227 offset:1024
	ds_read_b128 v[184:187], v227 offset:2048
	ds_read_b128 v[188:191], v227 offset:3072
	ds_read_b128 v[192:195], v227 offset:4096
	ds_read_b128 v[196:199], v227 offset:5120
	ds_read_b128 v[200:203], v227 offset:6144
	ds_read_b128 v[204:207], v227 offset:7168
	global_load_lds_dwordx4 v[0:1], off
	v_lshl_add_u64 v[0:1], s[46:47], 0, v[152:153]
	s_mov_b32 m0, s91
	s_nop 0
	global_load_lds_dwordx4 v[0:1], off
	s_waitcnt lgkmcnt(8)
	s_barrier
	s_waitcnt lgkmcnt(0)
	s_setprio 1
	s_waitcnt lgkmcnt(0)
	v_mfma_f32_16x16x128_f8f6f4 v[16:19], v[8:15], v[176:183], v[16:19]
	v_mfma_f32_16x16x128_f8f6f4 v[20:23], v[168:175], v[176:183], v[20:23]
	v_mfma_f32_16x16x128_f8f6f4 v[24:27], v[8:15], v[184:191], v[24:27]
	v_mfma_f32_16x16x128_f8f6f4 v[28:31], v[168:175], v[184:191], v[28:31]
	v_mfma_f32_16x16x128_f8f6f4 v[32:35], v[8:15], v[192:199], v[32:35]
	v_mfma_f32_16x16x128_f8f6f4 v[36:39], v[168:175], v[192:199], v[36:39]
	v_mfma_f32_16x16x128_f8f6f4 v[40:43], v[8:15], v[200:207], v[40:43]
	v_mfma_f32_16x16x128_f8f6f4 v[44:47], v[168:175], v[200:207], v[44:47]
	s_setprio 0
	s_barrier
	s_mov_b32 m0, s94
	v_lshl_add_u64 v[0:1], s[58:59], 0, v[150:151]
	ds_read_b128 v[208:211], v231
	ds_read_b128 v[212:215], v231 offset:1024
	ds_read_b128 v[236:239], v231 offset:2048
	ds_read_b128 v[240:243], v231 offset:3072
	global_load_lds_dwordx4 v[0:1], off
	v_lshl_add_u64 v[2:3], s[58:59], 0, v[154:155]
	s_mov_b32 m0, s93
	s_nop 0
	global_load_lds_dwordx4 v[2:3], off
	s_barrier
	s_waitcnt lgkmcnt(0)
	s_setprio 1
	s_waitcnt lgkmcnt(0)
	v_mfma_f32_16x16x128_f8f6f4 v[48:51], v[208:215], v[176:183], v[48:51]
	v_mfma_f32_16x16x128_f8f6f4 v[52:55], v[236:243], v[176:183], v[52:55]
	v_mfma_f32_16x16x128_f8f6f4 v[56:59], v[208:215], v[184:191], v[56:59]
	v_mfma_f32_16x16x128_f8f6f4 v[60:63], v[236:243], v[184:191], v[60:63]
	v_mfma_f32_16x16x128_f8f6f4 v[64:67], v[208:215], v[192:199], v[64:67]
	v_mfma_f32_16x16x128_f8f6f4 v[68:71], v[236:243], v[192:199], v[68:71]
	v_mfma_f32_16x16x128_f8f6f4 v[72:75], v[208:215], v[200:207], v[72:75]
	v_mfma_f32_16x16x128_f8f6f4 v[76:79], v[236:243], v[200:207], v[76:79]
	s_setprio 0
	s_mov_b32 m0, s70
	v_lshl_add_u64 v[4:5], s[50:51], 0, v[148:149]
	s_barrier
	ds_read_b128 v[176:179], v227 offset:16384
	ds_read_b128 v[180:183], v227 offset:17408
	ds_read_b128 v[184:187], v227 offset:18432
	ds_read_b128 v[188:191], v227 offset:19456
	ds_read_b128 v[192:195], v227 offset:20480
	ds_read_b128 v[196:199], v227 offset:21504
	ds_read_b128 v[200:203], v227 offset:22528
	ds_read_b128 v[204:207], v227 offset:23552
	global_load_lds_dwordx4 v[4:5], off
	v_lshl_add_u64 v[6:7], s[50:51], 0, v[152:153]
	s_mov_b32 m0, s71
	s_nop 0
	global_load_lds_dwordx4 v[6:7], off
	s_barrier
	s_waitcnt lgkmcnt(0)
	s_setprio 1
	s_waitcnt lgkmcnt(0)
	v_mfma_f32_16x16x128_f8f6f4 v[80:83], v[8:15], v[176:183], v[80:83]
	v_mfma_f32_16x16x128_f8f6f4 v[84:87], v[168:175], v[176:183], v[84:87]
	v_mfma_f32_16x16x128_f8f6f4 v[88:91], v[8:15], v[184:191], v[88:91]
	v_mfma_f32_16x16x128_f8f6f4 v[92:95], v[168:175], v[184:191], v[92:95]
	v_mfma_f32_16x16x128_f8f6f4 v[96:99], v[8:15], v[192:199], v[96:99]
	v_mfma_f32_16x16x128_f8f6f4 v[100:103], v[168:175], v[192:199], v[100:103]
	v_mfma_f32_16x16x128_f8f6f4 v[104:107], v[8:15], v[200:207], v[104:107]
	v_mfma_f32_16x16x128_f8f6f4 v[108:111], v[168:175], v[200:207], v[108:111]
	s_setprio 0
	s_barrier
	s_add_u32 s46, s58, 0x40000
	s_addc_u32 s47, s59, 0
	s_mov_b32 m0, s52
	v_lshl_add_u64 v[8:9], s[46:47], 0, v[150:151]
	global_load_lds_dwordx4 v[8:9], off
	v_lshl_add_u64 v[8:9], s[46:47], 0, v[154:155]
	s_mov_b32 m0, s95
	s_nop 0
	global_load_lds_dwordx4 v[8:9], off
	s_waitcnt vmcnt(6)
	s_barrier
	s_setprio 1
	v_mfma_f32_16x16x128_f8f6f4 v[112:115], v[208:215], v[176:183], v[112:115]
	v_mfma_f32_16x16x128_f8f6f4 v[116:119], v[236:243], v[176:183], v[116:119]
	v_mfma_f32_16x16x128_f8f6f4 v[120:123], v[208:215], v[184:191], v[120:123]
	v_mfma_f32_16x16x128_f8f6f4 v[124:127], v[236:243], v[184:191], v[124:127]
	v_mfma_f32_16x16x128_f8f6f4 v[128:131], v[208:215], v[192:199], v[128:131]
	v_mfma_f32_16x16x128_f8f6f4 v[132:135], v[236:243], v[192:199], v[132:135]
	v_mfma_f32_16x16x128_f8f6f4 v[144:147], v[208:215], v[200:207], v[144:147]
	v_mfma_f32_16x16x128_f8f6f4 v[136:139], v[236:243], v[200:207], v[136:139]
	s_setprio 0
	s_barrier
	ds_read_b128 v[8:11], v234
	ds_read_b128 v[12:15], v234 offset:1024
	ds_read_b128 v[168:171], v234 offset:2048
	ds_read_b128 v[172:175], v234 offset:3072
	s_add_u32 s46, s50, 0x40000
	s_addc_u32 s47, s51, 0
	s_mov_b32 m0, s72
	v_lshl_add_u64 v[140:141], s[46:47], 0, v[148:149]
	ds_read_b128 v[176:179], v227 offset:32768
	ds_read_b128 v[180:183], v227 offset:33792
	ds_read_b128 v[184:187], v227 offset:34816
	ds_read_b128 v[188:191], v227 offset:35840
	ds_read_b128 v[192:195], v227 offset:36864
	ds_read_b128 v[196:199], v227 offset:37888
	ds_read_b128 v[200:203], v227 offset:38912
	ds_read_b128 v[204:207], v227 offset:39936
	global_load_lds_dwordx4 v[140:141], off
	v_lshl_add_u64 v[140:141], s[46:47], 0, v[152:153]
	s_mov_b32 m0, s73
	s_nop 0
	global_load_lds_dwordx4 v[140:141], off
	s_waitcnt lgkmcnt(8)
	s_barrier
	s_waitcnt lgkmcnt(0)
	s_setprio 1
	s_waitcnt lgkmcnt(0)
	v_mfma_f32_16x16x128_f8f6f4 v[16:19], v[8:15], v[176:183], v[16:19]
	v_mfma_f32_16x16x128_f8f6f4 v[20:23], v[168:175], v[176:183], v[20:23]
	v_mfma_f32_16x16x128_f8f6f4 v[24:27], v[8:15], v[184:191], v[24:27]
	v_mfma_f32_16x16x128_f8f6f4 v[28:31], v[168:175], v[184:191], v[28:31]
	v_mfma_f32_16x16x128_f8f6f4 v[32:35], v[8:15], v[192:199], v[32:35]
	v_mfma_f32_16x16x128_f8f6f4 v[36:39], v[168:175], v[192:199], v[36:39]
	v_mfma_f32_16x16x128_f8f6f4 v[40:43], v[8:15], v[200:207], v[40:43]
	v_mfma_f32_16x16x128_f8f6f4 v[44:47], v[168:175], v[200:207], v[44:47]
	s_setprio 0
	s_barrier
	s_mov_b32 m0, s63
	v_lshl_add_u64 v[0:1], v[0:1], 0, s[6:7]
	ds_read_b128 v[208:211], v233
	ds_read_b128 v[212:215], v233 offset:1024
	ds_read_b128 v[234:237], v233 offset:2048
	ds_read_b128 v[238:241], v233 offset:3072
	global_load_lds_dwordx4 v[0:1], off
	v_lshl_add_u64 v[0:1], v[2:3], 0, s[6:7]
	s_mov_b32 m0, s62
	s_nop 0
	global_load_lds_dwordx4 v[0:1], off
	s_barrier
	s_waitcnt lgkmcnt(0)
	s_setprio 1
	s_waitcnt lgkmcnt(0)
	v_mfma_f32_16x16x128_f8f6f4 v[48:51], v[208:215], v[176:183], v[48:51]
	v_mfma_f32_16x16x128_f8f6f4 v[52:55], v[234:241], v[176:183], v[52:55]
	v_mfma_f32_16x16x128_f8f6f4 v[56:59], v[208:215], v[184:191], v[56:59]
	v_mfma_f32_16x16x128_f8f6f4 v[60:63], v[234:241], v[184:191], v[60:63]
	v_mfma_f32_16x16x128_f8f6f4 v[64:67], v[208:215], v[192:199], v[64:67]
	v_mfma_f32_16x16x128_f8f6f4 v[68:71], v[234:241], v[192:199], v[68:71]
	v_mfma_f32_16x16x128_f8f6f4 v[72:75], v[208:215], v[200:207], v[72:75]
	v_mfma_f32_16x16x128_f8f6f4 v[76:79], v[234:241], v[200:207], v[76:79]
	s_setprio 0
	s_mov_b32 m0, s77
	v_lshl_add_u64 v[0:1], v[4:5], 0, s[6:7]
	s_barrier
	ds_read_b128 v[176:179], v227 offset:49152
	ds_read_b128 v[180:183], v227 offset:50176
	ds_read_b128 v[184:187], v227 offset:51200
	ds_read_b128 v[188:191], v227 offset:52224
	ds_read_b128 v[192:195], v227 offset:53248
	ds_read_b128 v[196:199], v227 offset:54272
	ds_read_b128 v[200:203], v227 offset:55296
	ds_read_b128 v[204:207], v227 offset:56320
	global_load_lds_dwordx4 v[0:1], off
	v_lshl_add_u64 v[0:1], v[6:7], 0, s[6:7]
	s_mov_b32 m0, s78
	s_nop 0
	global_load_lds_dwordx4 v[0:1], off
	s_barrier
	s_waitcnt lgkmcnt(0)
	s_setprio 1
	s_waitcnt lgkmcnt(0)
	v_mfma_f32_16x16x128_f8f6f4 v[80:83], v[8:15], v[176:183], v[80:83]
	v_mfma_f32_16x16x128_f8f6f4 v[84:87], v[168:175], v[176:183], v[84:87]
	v_mfma_f32_16x16x128_f8f6f4 v[88:91], v[8:15], v[184:191], v[88:91]
	v_mfma_f32_16x16x128_f8f6f4 v[92:95], v[168:175], v[184:191], v[92:95]
	v_mfma_f32_16x16x128_f8f6f4 v[96:99], v[8:15], v[192:199], v[96:99]
	v_mfma_f32_16x16x128_f8f6f4 v[100:103], v[168:175], v[192:199], v[100:103]
	v_mfma_f32_16x16x128_f8f6f4 v[104:107], v[8:15], v[200:207], v[104:107]
	v_mfma_f32_16x16x128_f8f6f4 v[108:111], v[168:175], v[200:207], v[108:111]
	s_setprio 0
	s_barrier
	s_add_u32 s46, s58, 0x40080
	s_addc_u32 s47, s59, 0
	s_mov_b32 m0, s64
	v_lshl_add_u64 v[0:1], s[46:47], 0, v[150:151]
	global_load_lds_dwordx4 v[0:1], off
	v_lshl_add_u64 v[0:1], s[46:47], 0, v[154:155]
	s_mov_b32 m0, s53
	s_nop 0
	global_load_lds_dwordx4 v[0:1], off
	s_waitcnt vmcnt(6)
	s_barrier
	s_setprio 1
	v_mfma_f32_16x16x128_f8f6f4 v[112:115], v[208:215], v[176:183], v[112:115]
	v_mfma_f32_16x16x128_f8f6f4 v[116:119], v[234:241], v[176:183], v[116:119]
	v_mfma_f32_16x16x128_f8f6f4 v[120:123], v[208:215], v[184:191], v[120:123]
	v_mfma_f32_16x16x128_f8f6f4 v[124:127], v[234:241], v[184:191], v[124:127]
	v_mfma_f32_16x16x128_f8f6f4 v[128:131], v[208:215], v[192:199], v[128:131]
	v_mfma_f32_16x16x128_f8f6f4 v[132:135], v[234:241], v[192:199], v[132:135]
	v_mfma_f32_16x16x128_f8f6f4 v[144:147], v[208:215], v[200:207], v[144:147]
	v_mfma_f32_16x16x128_f8f6f4 v[136:139], v[234:241], v[200:207], v[136:139]
	s_setprio 0
	v_mov_b32_e32 v156, v229
	s_barrier
	s_nop 7
	s_nop 7
	s_nop 7
	global_load_dwordx2 v[4:5], v156, s[2:3]
	global_load_dwordx2 v[6:7], v156, s[2:3] offset:512
	global_load_dwordx2 v[8:9], v156, s[2:3] offset:1024
	global_load_dwordx2 v[10:11], v156, s[2:3] offset:1536
	global_load_dwordx2 v[168:169], v156, s[2:3] offset:2048
	global_load_dwordx2 v[202:203], v156, s[2:3] offset:2560
	global_load_dwordx2 v[200:201], v156, s[2:3] offset:3072
	global_load_dwordx2 v[198:199], v156, s[2:3] offset:3584
	v_lshl_add_u64 v[0:1], s[2:3], 0, v[156:157]
	v_add_co_u32_e32 v0, vcc, s82, v0
	s_mov_b64 s[2:3], 0x40000
	s_nop 0
	v_addc_co_u32_e32 v1, vcc, 0, v1, vcc
	global_load_dwordx2 v[196:197], v[0:1], off
	global_load_dwordx2 v[194:195], v[0:1], off offset:512
	global_load_dwordx2 v[192:193], v[0:1], off offset:1024
	global_load_dwordx2 v[190:191], v[0:1], off offset:1536
	global_load_dwordx2 v[180:181], v[0:1], off offset:2048
	global_load_dwordx2 v[170:171], v[0:1], off offset:2560
	global_load_dwordx2 v[2:3], v[0:1], off offset:3072
	s_nop 0
	global_load_dwordx2 v[0:1], v[0:1], off offset:3584
	s_mov_b64 s[48:49], s[44:45]
	s_mov_b64 s[46:47], s[42:43]
	s_waitcnt vmcnt(0)
	v_cvt_f32_ubyte1_e32 v13, v4
	v_cvt_f32_ubyte0_e32 v12, v4
	v_cvt_f32_ubyte3_e32 v15, v4
	v_cvt_f32_ubyte2_e32 v14, v4
	v_cvt_f32_ubyte1_e32 v141, v5
	v_cvt_f32_ubyte0_e32 v140, v5
	v_cvt_f32_ubyte3_e32 v143, v5
	v_cvt_f32_ubyte2_e32 v142, v5
	v_cvt_f32_ubyte1_e32 v5, v6
	v_cvt_f32_ubyte0_e32 v4, v6
	v_cvt_f32_ubyte1_e32 v175, v7
	v_cvt_f32_ubyte0_e32 v174, v7
	v_pk_add_f32 v[4:5], v[4:5], 0.5 op_sel_hi:[1,0]
	v_cvt_f32_ubyte3_e32 v173, v6
	v_cvt_f32_ubyte2_e32 v172, v6
	v_cvt_f32_ubyte3_e32 v177, v7
	v_cvt_f32_ubyte2_e32 v176, v7
	v_cvt_f32_ubyte1_e32 v7, v8
	v_cvt_f32_ubyte0_e32 v6, v8
	v_pk_add_f32 v[174:175], v[174:175], 0.5 op_sel_hi:[1,0]
	v_pk_mul_f32 v[4:5], v[4:5], s[38:39] op_sel_hi:[1,0]
	v_pk_add_f32 v[172:173], v[172:173], 0.5 op_sel_hi:[1,0]
	v_pk_add_f32 v[6:7], v[6:7], 0.5 op_sel_hi:[1,0]
	v_pk_mul_f32 v[204:205], v[174:175], s[38:39] op_sel_hi:[1,0]
	v_pk_mul_f32 v[174:175], v[48:49], v[4:5]
	v_cvt_f32_ubyte3_e32 v5, v10
	v_cvt_f32_ubyte2_e32 v4, v10
	v_cvt_f32_ubyte3_e32 v179, v8
	v_cvt_f32_ubyte2_e32 v178, v8
	v_cvt_f32_ubyte1_e32 v183, v9
	v_cvt_f32_ubyte0_e32 v182, v9
	v_cvt_f32_ubyte3_e32 v185, v9
	v_cvt_f32_ubyte2_e32 v184, v9
	v_cvt_f32_ubyte1_e32 v9, v10
	v_pk_add_f32 v[12:13], v[12:13], 0.5 op_sel_hi:[1,0]
	v_pk_mul_f32 v[172:173], v[172:173], s[38:39] op_sel_hi:[1,0]
	v_pk_mul_f32 v[6:7], v[6:7], s[38:39] op_sel_hi:[1,0]
	v_cvt_f32_ubyte0_e32 v8, v10
	v_pk_add_f32 v[4:5], v[4:5], 0.5 op_sel_hi:[1,0]
	v_pk_add_f32 v[14:15], v[14:15], 0.5 op_sel_hi:[1,0]
	v_pk_add_f32 v[184:185], v[184:185], 0.5 op_sel_hi:[1,0]
	v_pk_mul_f32 v[12:13], v[12:13], s[38:39] op_sel_hi:[1,0]
	v_pk_mul_f32 v[172:173], v[50:51], v[172:173]
	v_pk_mul_f32 v[50:51], v[24:25], v[6:7]
	v_pk_add_f32 v[6:7], v[8:9], 0.5 op_sel_hi:[1,0]
	v_pk_mul_f32 v[4:5], v[4:5], s[38:39] op_sel_hi:[1,0]
	v_pk_add_f32 v[182:183], v[182:183], 0.5 op_sel_hi:[1,0]
	v_pk_mul_f32 v[14:15], v[14:15], s[38:39] op_sel_hi:[1,0]
	v_pk_mul_f32 v[210:211], v[184:185], s[38:39] op_sel_hi:[1,0]
	v_pk_mul_f32 v[184:185], v[16:17], v[12:13]
	v_pk_mul_f32 v[6:7], v[6:7], s[38:39] op_sel_hi:[1,0]
	v_pk_mul_f32 v[12:13], v[58:59], v[4:5]
	v_cvt_f32_ubyte1_e32 v5, v11
	v_cvt_f32_ubyte0_e32 v4, v11
	v_pk_add_f32 v[142:143], v[142:143], 0.5 op_sel_hi:[1,0]
	v_pk_mul_f32 v[208:209], v[182:183], s[38:39] op_sel_hi:[1,0]
	v_pk_mul_f32 v[182:183], v[18:19], v[14:15]
	v_pk_mul_f32 v[14:15], v[56:57], v[6:7]
	v_cvt_f32_ubyte3_e32 v7, v11
	v_cvt_f32_ubyte2_e32 v6, v11
	v_pk_add_f32 v[4:5], v[4:5], 0.5 op_sel_hi:[1,0]
	v_pk_add_f32 v[140:141], v[140:141], 0.5 op_sel_hi:[1,0]
	v_pk_mul_f32 v[142:143], v[142:143], s[38:39] op_sel_hi:[1,0]
	v_pk_add_f32 v[6:7], v[6:7], 0.5 op_sel_hi:[1,0]
	v_pk_mul_f32 v[4:5], v[4:5], s[38:39] op_sel_hi:[1,0]
	v_pk_mul_f32 v[140:141], v[140:141], s[38:39] op_sel_hi:[1,0]
	v_pk_mul_f32 v[186:187], v[22:23], v[142:143]
	v_pk_mul_f32 v[6:7], v[6:7], s[38:39] op_sel_hi:[1,0]
	v_pk_mul_f32 v[142:143], v[60:61], v[4:5]
	v_cvt_f32_ubyte1_e32 v5, v168
	v_cvt_f32_ubyte0_e32 v4, v168
	v_pk_mul_f32 v[188:189], v[20:21], v[140:141]
	v_pk_mul_f32 v[140:141], v[62:63], v[6:7]
	v_cvt_f32_ubyte3_e32 v7, v168
	v_cvt_f32_ubyte2_e32 v6, v168
	v_pk_add_f32 v[4:5], v[4:5], 0.5 op_sel_hi:[1,0]
	v_pk_add_f32 v[6:7], v[6:7], 0.5 op_sel_hi:[1,0]
	v_pk_mul_f32 v[8:9], v[4:5], s[38:39] op_sel_hi:[1,0]
	v_pk_mul_f32 v[4:5], v[6:7], s[38:39] op_sel_hi:[1,0]
	v_pk_mul_f32 v[6:7], v[32:33], v[8:9]
	v_cvt_f32_ubyte1_e32 v9, v169
	v_cvt_f32_ubyte0_e32 v8, v169
	v_cvt_f32_ubyte3_e32 v11, v169
	v_cvt_f32_ubyte2_e32 v10, v169
	v_pk_add_f32 v[8:9], v[8:9], 0.5 op_sel_hi:[1,0]
	v_pk_add_f32 v[10:11], v[10:11], 0.5 op_sel_hi:[1,0]
	v_pk_mul_f32 v[8:9], v[8:9], s[38:39] op_sel_hi:[1,0]
	v_pk_mul_f32 v[10:11], v[10:11], s[38:39] op_sel_hi:[1,0]
	v_pk_mul_f32 v[58:59], v[36:37], v[8:9]
	v_cvt_f32_ubyte1_e32 v9, v202
	v_cvt_f32_ubyte0_e32 v8, v202
	v_pk_mul_f32 v[56:57], v[38:39], v[10:11]
	v_cvt_f32_ubyte3_e32 v11, v202
	v_cvt_f32_ubyte2_e32 v10, v202
	v_pk_add_f32 v[8:9], v[8:9], 0.5 op_sel_hi:[1,0]
	v_pk_add_f32 v[10:11], v[10:11], 0.5 op_sel_hi:[1,0]
	v_pk_mul_f32 v[8:9], v[8:9], s[38:39] op_sel_hi:[1,0]
	v_pk_mul_f32 v[10:11], v[10:11], s[38:39] op_sel_hi:[1,0]
	v_pk_mul_f32 v[18:19], v[64:65], v[8:9]
	v_cvt_f32_ubyte1_e32 v9, v203
	v_cvt_f32_ubyte0_e32 v8, v203
	v_pk_mul_f32 v[16:17], v[66:67], v[10:11]
	v_cvt_f32_ubyte3_e32 v11, v203
	v_cvt_f32_ubyte2_e32 v10, v203
	v_pk_add_f32 v[8:9], v[8:9], 0.5 op_sel_hi:[1,0]
	v_pk_add_f32 v[10:11], v[10:11], 0.5 op_sel_hi:[1,0]
	v_pk_mul_f32 v[8:9], v[8:9], s[38:39] op_sel_hi:[1,0]
	v_pk_mul_f32 v[10:11], v[10:11], s[38:39] op_sel_hi:[1,0]
	v_pk_mul_f32 v[168:169], v[68:69], v[8:9]
	v_cvt_f32_ubyte1_e32 v9, v200
	v_cvt_f32_ubyte0_e32 v8, v200
	v_pk_mul_f32 v[70:71], v[70:71], v[10:11]
	v_cvt_f32_ubyte3_e32 v11, v200
	v_cvt_f32_ubyte2_e32 v10, v200
	v_pk_add_f32 v[8:9], v[8:9], 0.5 op_sel_hi:[1,0]
	v_pk_add_f32 v[10:11], v[10:11], 0.5 op_sel_hi:[1,0]
	v_pk_mul_f32 v[20:21], v[8:9], s[38:39] op_sel_hi:[1,0]
	v_pk_mul_f32 v[8:9], v[10:11], s[38:39] op_sel_hi:[1,0]
	v_pk_mul_f32 v[10:11], v[40:41], v[20:21]
	v_cvt_f32_ubyte1_e32 v21, v201
	v_cvt_f32_ubyte0_e32 v20, v201
	v_cvt_f32_ubyte3_e32 v23, v201
	v_cvt_f32_ubyte2_e32 v22, v201
	v_pk_add_f32 v[20:21], v[20:21], 0.5 op_sel_hi:[1,0]
	v_pk_add_f32 v[22:23], v[22:23], 0.5 op_sel_hi:[1,0]
	v_pk_mul_f32 v[20:21], v[20:21], s[38:39] op_sel_hi:[1,0]
	v_pk_mul_f32 v[22:23], v[22:23], s[38:39] op_sel_hi:[1,0]
	v_pk_mul_f32 v[66:67], v[44:45], v[20:21]
	v_cvt_f32_ubyte1_e32 v21, v198
	v_cvt_f32_ubyte0_e32 v20, v198
	v_pk_mul_f32 v[64:65], v[46:47], v[22:23]
	v_cvt_f32_ubyte3_e32 v23, v198
	v_cvt_f32_ubyte2_e32 v22, v198
	v_pk_add_f32 v[20:21], v[20:21], 0.5 op_sel_hi:[1,0]
	v_pk_add_f32 v[178:179], v[178:179], 0.5 op_sel_hi:[1,0]
	v_pk_add_f32 v[22:23], v[22:23], 0.5 op_sel_hi:[1,0]
	v_pk_mul_f32 v[24:25], v[20:21], s[38:39] op_sel_hi:[1,0]
	v_pk_mul_f32 v[206:207], v[178:179], s[38:39] op_sel_hi:[1,0]
	v_pk_mul_f32 v[20:21], v[22:23], s[38:39] op_sel_hi:[1,0]
	v_pk_mul_f32 v[22:23], v[72:73], v[24:25]
	v_cvt_f32_ubyte1_e32 v25, v199
	v_cvt_f32_ubyte0_e32 v24, v199
	v_pk_mul_f32 v[48:49], v[26:27], v[206:207]
	v_cvt_f32_ubyte3_e32 v27, v199
	v_cvt_f32_ubyte2_e32 v26, v199
	v_pk_add_f32 v[24:25], v[24:25], 0.5 op_sel_hi:[1,0]
	v_pk_add_f32 v[26:27], v[26:27], 0.5 op_sel_hi:[1,0]
	v_pk_mul_f32 v[24:25], v[24:25], s[38:39] op_sel_hi:[1,0]
	v_pk_add_f32 v[176:177], v[176:177], 0.5 op_sel_hi:[1,0]
	v_pk_mul_f32 v[20:21], v[74:75], v[20:21]
	v_pk_mul_f32 v[26:27], v[26:27], s[38:39] op_sel_hi:[1,0]
	v_pk_mul_f32 v[74:75], v[76:77], v[24:25]
	v_cvt_f32_ubyte1_e32 v25, v196
	v_cvt_f32_ubyte0_e32 v24, v196
	v_pk_mul_f32 v[176:177], v[176:177], s[38:39] op_sel_hi:[1,0]
	v_pk_mul_f32 v[72:73], v[78:79], v[26:27]
	v_cvt_f32_ubyte3_e32 v27, v196
	v_cvt_f32_ubyte2_e32 v26, v196
	v_pk_add_f32 v[24:25], v[24:25], 0.5 op_sel_hi:[1,0]
	v_pk_mul_f32 v[176:177], v[54:55], v[176:177]
	v_pk_mul_f32 v[54:55], v[28:29], v[208:209]
	v_pk_add_f32 v[26:27], v[26:27], 0.5 op_sel_hi:[1,0]
	v_pk_mul_f32 v[28:29], v[24:25], s[38:39] op_sel_hi:[1,0]
	v_pk_mul_f32 v[24:25], v[26:27], s[38:39] op_sel_hi:[1,0]
	v_pk_mul_f32 v[26:27], v[80:81], v[28:29]
	v_cvt_f32_ubyte1_e32 v29, v197
	v_cvt_f32_ubyte0_e32 v28, v197
	v_pk_mul_f32 v[178:179], v[52:53], v[204:205]
	v_pk_mul_f32 v[52:53], v[30:31], v[210:211]
	v_cvt_f32_ubyte3_e32 v31, v197
	v_cvt_f32_ubyte2_e32 v30, v197
	v_pk_add_f32 v[28:29], v[28:29], 0.5 op_sel_hi:[1,0]
	v_pk_add_f32 v[30:31], v[30:31], 0.5 op_sel_hi:[1,0]
	v_pk_mul_f32 v[28:29], v[28:29], s[38:39] op_sel_hi:[1,0]
	v_pk_mul_f32 v[30:31], v[30:31], s[38:39] op_sel_hi:[1,0]
	v_pk_mul_f32 v[78:79], v[84:85], v[28:29]
	v_cvt_f32_ubyte1_e32 v29, v194
	v_cvt_f32_ubyte0_e32 v28, v194
	v_pk_mul_f32 v[76:77], v[86:87], v[30:31]
	v_cvt_f32_ubyte3_e32 v31, v194
	v_cvt_f32_ubyte2_e32 v30, v194
	v_pk_add_f32 v[28:29], v[28:29], 0.5 op_sel_hi:[1,0]
	v_pk_add_f32 v[30:31], v[30:31], 0.5 op_sel_hi:[1,0]
	v_pk_mul_f32 v[32:33], v[28:29], s[38:39] op_sel_hi:[1,0]
	v_pk_mul_f32 v[28:29], v[30:31], s[38:39] op_sel_hi:[1,0]
	v_pk_mul_f32 v[30:31], v[112:113], v[32:33]
	v_cvt_f32_ubyte1_e32 v33, v195
	v_cvt_f32_ubyte0_e32 v32, v195
	v_pk_mul_f32 v[4:5], v[34:35], v[4:5]
	v_cvt_f32_ubyte3_e32 v35, v195
	v_cvt_f32_ubyte2_e32 v34, v195
	v_pk_add_f32 v[32:33], v[32:33], 0.5 op_sel_hi:[1,0]
	v_pk_add_f32 v[34:35], v[34:35], 0.5 op_sel_hi:[1,0]
	v_pk_mul_f32 v[32:33], v[32:33], s[38:39] op_sel_hi:[1,0]
	v_pk_mul_f32 v[24:25], v[82:83], v[24:25]
	v_pk_mul_f32 v[34:35], v[34:35], s[38:39] op_sel_hi:[1,0]
	v_pk_mul_f32 v[82:83], v[116:117], v[32:33]
	v_cvt_f32_ubyte1_e32 v33, v192
	v_cvt_f32_ubyte0_e32 v32, v192
	v_pk_mul_f32 v[80:81], v[118:119], v[34:35]
	v_cvt_f32_ubyte3_e32 v35, v192
	v_cvt_f32_ubyte2_e32 v34, v192
	v_pk_add_f32 v[32:33], v[32:33], 0.5 op_sel_hi:[1,0]
	v_pk_add_f32 v[34:35], v[34:35], 0.5 op_sel_hi:[1,0]
	v_pk_mul_f32 v[36:37], v[32:33], s[38:39] op_sel_hi:[1,0]
	v_pk_mul_f32 v[32:33], v[34:35], s[38:39] op_sel_hi:[1,0]
	v_pk_mul_f32 v[34:35], v[88:89], v[36:37]
	v_cvt_f32_ubyte1_e32 v37, v193
	v_cvt_f32_ubyte0_e32 v36, v193
	v_cvt_f32_ubyte3_e32 v39, v193
	v_cvt_f32_ubyte2_e32 v38, v193
	v_pk_add_f32 v[36:37], v[36:37], 0.5 op_sel_hi:[1,0]
	v_pk_add_f32 v[38:39], v[38:39], 0.5 op_sel_hi:[1,0]
	v_pk_mul_f32 v[36:37], v[36:37], s[38:39] op_sel_hi:[1,0]
	v_pk_mul_f32 v[38:39], v[38:39], s[38:39] op_sel_hi:[1,0]
	v_pk_mul_f32 v[86:87], v[92:93], v[36:37]
	v_cvt_f32_ubyte1_e32 v37, v190
	v_cvt_f32_ubyte0_e32 v36, v190
	v_pk_mul_f32 v[84:85], v[94:95], v[38:39]
	v_cvt_f32_ubyte3_e32 v39, v190
	v_cvt_f32_ubyte2_e32 v38, v190
	v_pk_add_f32 v[36:37], v[36:37], 0.5 op_sel_hi:[1,0]
	v_pk_add_f32 v[38:39], v[38:39], 0.5 op_sel_hi:[1,0]
	v_pk_mul_f32 v[40:41], v[36:37], s[38:39] op_sel_hi:[1,0]
	v_pk_mul_f32 v[36:37], v[38:39], s[38:39] op_sel_hi:[1,0]
	v_pk_mul_f32 v[38:39], v[120:121], v[40:41]
	v_cvt_f32_ubyte1_e32 v41, v191
	v_cvt_f32_ubyte0_e32 v40, v191
	v_pk_mul_f32 v[8:9], v[42:43], v[8:9]
	v_cvt_f32_ubyte3_e32 v43, v191
	v_cvt_f32_ubyte2_e32 v42, v191
	v_pk_add_f32 v[40:41], v[40:41], 0.5 op_sel_hi:[1,0]
	v_pk_add_f32 v[42:43], v[42:43], 0.5 op_sel_hi:[1,0]
	v_pk_mul_f32 v[40:41], v[40:41], s[38:39] op_sel_hi:[1,0]
	v_pk_mul_f32 v[32:33], v[90:91], v[32:33]
	v_pk_mul_f32 v[42:43], v[42:43], s[38:39] op_sel_hi:[1,0]
	v_pk_mul_f32 v[90:91], v[124:125], v[40:41]
	v_cvt_f32_ubyte1_e32 v41, v180
	v_cvt_f32_ubyte0_e32 v40, v180
	v_pk_mul_f32 v[88:89], v[126:127], v[42:43]
	v_cvt_f32_ubyte3_e32 v43, v180
	v_cvt_f32_ubyte2_e32 v42, v180
	v_pk_add_f32 v[40:41], v[40:41], 0.5 op_sel_hi:[1,0]
	v_pk_add_f32 v[42:43], v[42:43], 0.5 op_sel_hi:[1,0]
	v_pk_mul_f32 v[44:45], v[40:41], s[38:39] op_sel_hi:[1,0]
	v_pk_mul_f32 v[40:41], v[42:43], s[38:39] op_sel_hi:[1,0]
	v_pk_mul_f32 v[42:43], v[96:97], v[44:45]
	v_cvt_f32_ubyte1_e32 v45, v181
	v_cvt_f32_ubyte0_e32 v44, v181
	v_cvt_f32_ubyte3_e32 v47, v181
	v_cvt_f32_ubyte2_e32 v46, v181
	v_pk_add_f32 v[44:45], v[44:45], 0.5 op_sel_hi:[1,0]
	v_pk_add_f32 v[46:47], v[46:47], 0.5 op_sel_hi:[1,0]
	v_pk_mul_f32 v[44:45], v[44:45], s[38:39] op_sel_hi:[1,0]
	v_pk_mul_f32 v[46:47], v[46:47], s[38:39] op_sel_hi:[1,0]
	v_pk_mul_f32 v[94:95], v[100:101], v[44:45]
	v_cvt_f32_ubyte1_e32 v45, v170
	v_cvt_f32_ubyte0_e32 v44, v170
	v_pk_mul_f32 v[92:93], v[102:103], v[46:47]
	v_cvt_f32_ubyte3_e32 v47, v170
	v_cvt_f32_ubyte2_e32 v46, v170
	v_pk_add_f32 v[44:45], v[44:45], 0.5 op_sel_hi:[1,0]
	v_pk_add_f32 v[46:47], v[46:47], 0.5 op_sel_hi:[1,0]
	v_pk_mul_f32 v[60:61], v[44:45], s[38:39] op_sel_hi:[1,0]
	v_pk_mul_f32 v[44:45], v[46:47], s[38:39] op_sel_hi:[1,0]
	v_pk_mul_f32 v[46:47], v[128:129], v[60:61]
	v_cvt_f32_ubyte1_e32 v61, v171
	v_cvt_f32_ubyte0_e32 v60, v171
	v_cvt_f32_ubyte3_e32 v63, v171
	v_cvt_f32_ubyte2_e32 v62, v171
	v_pk_add_f32 v[60:61], v[60:61], 0.5 op_sel_hi:[1,0]
	v_pk_add_f32 v[62:63], v[62:63], 0.5 op_sel_hi:[1,0]
	v_pk_mul_f32 v[60:61], v[60:61], s[38:39] op_sel_hi:[1,0]
	v_pk_mul_f32 v[40:41], v[98:99], v[40:41]
	v_pk_mul_f32 v[62:63], v[62:63], s[38:39] op_sel_hi:[1,0]
	v_pk_mul_f32 v[98:99], v[132:133], v[60:61]
	v_cvt_f32_ubyte1_e32 v61, v2
	v_cvt_f32_ubyte0_e32 v60, v2
	v_pk_mul_f32 v[96:97], v[134:135], v[62:63]
	v_cvt_f32_ubyte3_e32 v63, v2
	v_cvt_f32_ubyte2_e32 v62, v2
	v_pk_add_f32 v[60:61], v[60:61], 0.5 op_sel_hi:[1,0]
	v_pk_add_f32 v[62:63], v[62:63], 0.5 op_sel_hi:[1,0]
	v_pk_mul_f32 v[68:69], v[60:61], s[38:39] op_sel_hi:[1,0]
	v_cvt_f32_ubyte3_e32 v101, v3
	v_cvt_f32_ubyte2_e32 v100, v3
	v_pk_mul_f32 v[60:61], v[62:63], s[38:39] op_sel_hi:[1,0]
	v_pk_mul_f32 v[62:63], v[104:105], v[68:69]
	v_cvt_f32_ubyte1_e32 v69, v3
	v_cvt_f32_ubyte0_e32 v68, v3
	v_pk_add_f32 v[2:3], v[100:101], 0.5 op_sel_hi:[1,0]
	v_pk_add_f32 v[68:69], v[68:69], 0.5 op_sel_hi:[1,0]
	v_pk_mul_f32 v[2:3], v[2:3], s[38:39] op_sel_hi:[1,0]
	v_pk_mul_f32 v[68:69], v[68:69], s[38:39] op_sel_hi:[1,0]
	v_pk_mul_f32 v[100:101], v[110:111], v[2:3]
	v_cvt_f32_ubyte1_e32 v3, v0
	v_cvt_f32_ubyte0_e32 v2, v0
	v_pk_mul_f32 v[102:103], v[108:109], v[68:69]
	v_cvt_f32_ubyte3_e32 v69, v0
	v_cvt_f32_ubyte2_e32 v68, v0
	v_pk_add_f32 v[2:3], v[2:3], 0.5 op_sel_hi:[1,0]
	v_lshl_add_u32 v108, s90, 8, v225
	v_pk_mul_f32 v[28:29], v[114:115], v[28:29]
	v_pk_mul_f32 v[60:61], v[106:107], v[60:61]
	v_pk_add_f32 v[68:69], v[68:69], 0.5 op_sel_hi:[1,0]
	v_pk_mul_f32 v[104:105], v[2:3], s[38:39] op_sel_hi:[1,0]
	v_cvt_f32_ubyte3_e32 v107, v1
	v_cvt_f32_ubyte2_e32 v106, v1
	v_ashrrev_i32_e32 v109, 31, v108
	v_pk_mul_f32 v[112:113], v[182:183], s[40:41] op_sel_hi:[1,0]
	v_pk_mul_f32 v[114:115], v[184:185], s[40:41] op_sel_hi:[1,0]
	v_pk_mul_f32 v[2:3], v[68:69], s[38:39] op_sel_hi:[1,0]
	v_pk_mul_f32 v[68:69], v[144:145], v[104:105]
	v_cvt_f32_ubyte1_e32 v105, v1
	v_cvt_f32_ubyte0_e32 v104, v1
	v_pk_add_f32 v[0:1], v[106:107], 0.5 op_sel_hi:[1,0]
	v_lshlrev_b64 v[106:107], 11, v[108:109]
	v_pk_mul_f32 v[118:119], v[188:189], s[40:41] op_sel_hi:[1,0]
	v_med3_f32 v109, v114, s83, v232
	v_med3_f32 v114, v115, s83, v232
	v_med3_f32 v115, v112, s83, v232
	v_mov_b32_e32 v112, v157
	v_med3_f32 v120, v113, s83, v232
	v_cvt_pk_fp8_f32 v112, v109, v114
	v_med3_f32 v109, v118, s83, v232
	v_med3_f32 v114, v119, s83, v232
	v_mov_b32_e32 v113, v157
	v_cvt_pk_fp8_f32 v113, v109, v114
	v_pk_mul_f32 v[116:117], v[186:187], s[40:41] op_sel_hi:[1,0]
	v_cvt_pk_fp8_f32 v112, v115, v120 op_sel:[0,0,1]
	v_med3_f32 v109, v116, s83, v232
	v_med3_f32 v114, v117, s83, v232
	v_cvt_pk_fp8_f32 v113, v109, v114 op_sel:[0,0,1]
	v_pk_mul_f32 v[114:115], v[172:173], s[40:41] op_sel_hi:[1,0]
	v_pk_mul_f32 v[116:117], v[174:175], s[40:41] op_sel_hi:[1,0]
	v_pk_mul_f32 v[120:121], v[178:179], s[40:41] op_sel_hi:[1,0]
	v_med3_f32 v109, v116, s83, v232
	v_med3_f32 v116, v117, s83, v232
	v_med3_f32 v117, v114, s83, v232
	v_mov_b32_e32 v114, v157
	v_pk_mul_f32 v[36:37], v[122:123], v[36:37]
	v_med3_f32 v122, v115, s83, v232
	v_cvt_pk_fp8_f32 v114, v109, v116
	v_med3_f32 v109, v120, s83, v232
	v_med3_f32 v116, v121, s83, v232
	v_mov_b32_e32 v115, v157
	v_cvt_pk_fp8_f32 v115, v109, v116
	v_pk_mul_f32 v[118:119], v[176:177], s[40:41] op_sel_hi:[1,0]
	v_lshl_or_b32 v110, s89, 8, v228
	v_med3_f32 v109, v118, s83, v232
	v_med3_f32 v116, v119, s83, v232
	v_cvt_pk_fp8_f32 v114, v117, v122 op_sel:[0,0,1]
	v_cvt_pk_fp8_f32 v115, v109, v116 op_sel:[0,0,1]
	v_ashrrev_i32_e32 v111, 31, v110
	v_lshl_add_u64 v[106:107], s[4:5], 0, v[106:107]
	v_pk_mul_f32 v[48:49], v[48:49], s[40:41] op_sel_hi:[1,0]
	v_pk_mul_f32 v[50:51], v[50:51], s[40:41] op_sel_hi:[1,0]
	v_lshl_add_u64 v[106:107], v[106:107], 0, v[110:111]
	v_pk_mul_f32 v[54:55], v[54:55], s[40:41] op_sel_hi:[1,0]
	v_med3_f32 v50, v50, s83, v232
	v_med3_f32 v51, v51, s83, v232
	v_med3_f32 v109, v48, s83, v232
	v_mov_b32_e32 v48, v157
	global_store_dwordx2 v[106:107], v[112:113], off
	global_store_dwordx2 v[106:107], v[114:115], off offset:128
	v_pk_mul_f32 v[52:53], v[52:53], s[40:41] op_sel_hi:[1,0]
	v_med3_f32 v114, v49, s83, v232
	v_cvt_pk_fp8_f32 v48, v50, v51
	v_med3_f32 v50, v54, s83, v232
	v_med3_f32 v51, v55, s83, v232
	v_mov_b32_e32 v49, v157
	v_pk_mul_f32 v[12:13], v[12:13], s[40:41] op_sel_hi:[1,0]
	v_pk_mul_f32 v[14:15], v[14:15], s[40:41] op_sel_hi:[1,0]
	v_cvt_pk_fp8_f32 v49, v50, v51
	v_med3_f32 v50, v52, s83, v232
	v_med3_f32 v51, v53, s83, v232
	v_pk_mul_f32 v[52:53], v[142:143], s[40:41] op_sel_hi:[1,0]
	v_med3_f32 v14, v14, s83, v232
	v_med3_f32 v15, v15, s83, v232
	v_med3_f32 v54, v12, s83, v232
	v_mov_b32_e32 v12, v157
	v_med3_f32 v55, v13, s83, v232
	v_cvt_pk_fp8_f32 v12, v14, v15
	v_med3_f32 v14, v52, s83, v232
	v_med3_f32 v15, v53, s83, v232
	v_mov_b32_e32 v13, v157
	v_cvt_pk_fp8_f32 v13, v14, v15
	v_or_b32_e32 v112, 16, v108
	v_cvt_pk_fp8_f32 v49, v50, v51 op_sel:[0,0,1]
	v_pk_mul_f32 v[50:51], v[140:141], s[40:41] op_sel_hi:[1,0]
	v_ashrrev_i32_e32 v113, 31, v112
	v_cvt_pk_fp8_f32 v48, v109, v114 op_sel:[0,0,1]
	v_med3_f32 v14, v50, s83, v232
	v_med3_f32 v15, v51, s83, v232
	v_lshlrev_b64 v[112:113], 11, v[112:113]
	v_cvt_pk_fp8_f32 v12, v54, v55 op_sel:[0,0,1]
	v_cvt_pk_fp8_f32 v13, v14, v15 op_sel:[0,0,1]
	v_lshl_add_u64 v[14:15], s[4:5], 0, v[112:113]
	v_lshl_add_u64 v[14:15], v[14:15], 0, v[110:111]
	v_pk_mul_f32 v[4:5], v[4:5], s[40:41] op_sel_hi:[1,0]
	v_pk_mul_f32 v[6:7], v[6:7], s[40:41] op_sel_hi:[1,0]
	global_store_dwordx2 v[14:15], v[48:49], off
	global_store_dwordx2 v[14:15], v[12:13], off offset:128
	v_pk_mul_f32 v[48:49], v[58:59], s[40:41] op_sel_hi:[1,0]
	v_med3_f32 v6, v6, s83, v232
	v_med3_f32 v7, v7, s83, v232
	v_med3_f32 v50, v4, s83, v232
	v_mov_b32_e32 v4, v157
	v_med3_f32 v51, v5, s83, v232
	v_cvt_pk_fp8_f32 v4, v6, v7
	v_med3_f32 v6, v48, s83, v232
	v_med3_f32 v7, v49, s83, v232
	v_mov_b32_e32 v5, v157
	v_cvt_pk_fp8_f32 v5, v6, v7
	v_pk_mul_f32 v[14:15], v[56:57], s[40:41] op_sel_hi:[1,0]
	v_or_b32_e32 v12, 32, v108
	v_med3_f32 v6, v14, s83, v232
	v_med3_f32 v7, v15, s83, v232
	v_cvt_pk_fp8_f32 v5, v6, v7 op_sel:[0,0,1]
	v_pk_mul_f32 v[6:7], v[16:17], s[40:41] op_sel_hi:[1,0]
	v_pk_mul_f32 v[14:15], v[18:19], s[40:41] op_sel_hi:[1,0]
	v_pk_mul_f32 v[18:19], v[168:169], s[40:41] op_sel_hi:[1,0]
	v_med3_f32 v14, v14, s83, v232
	v_med3_f32 v15, v15, s83, v232
	v_med3_f32 v48, v6, s83, v232
	v_mov_b32_e32 v6, v157
	v_med3_f32 v49, v7, s83, v232
	v_cvt_pk_fp8_f32 v6, v14, v15
	v_med3_f32 v14, v18, s83, v232
	v_med3_f32 v15, v19, s83, v232
	v_mov_b32_e32 v7, v157
	v_cvt_pk_fp8_f32 v7, v14, v15
	v_pk_mul_f32 v[16:17], v[70:71], s[40:41] op_sel_hi:[1,0]
	v_ashrrev_i32_e32 v13, 31, v12
	v_cvt_pk_fp8_f32 v4, v50, v51 op_sel:[0,0,1]
	v_med3_f32 v14, v16, s83, v232
	v_med3_f32 v15, v17, s83, v232
	v_lshlrev_b64 v[12:13], 11, v[12:13]
	v_cvt_pk_fp8_f32 v6, v48, v49 op_sel:[0,0,1]
	v_cvt_pk_fp8_f32 v7, v14, v15 op_sel:[0,0,1]
	v_lshl_add_u64 v[12:13], s[4:5], 0, v[12:13]
	v_lshl_add_u64 v[12:13], v[12:13], 0, v[110:111]
	global_store_dwordx2 v[12:13], v[4:5], off
	global_store_dwordx2 v[12:13], v[6:7], off offset:128
	v_pk_mul_f32 v[6:7], v[8:9], s[40:41] op_sel_hi:[1,0]
	v_pk_mul_f32 v[8:9], v[10:11], s[40:41] op_sel_hi:[1,0]
	v_pk_mul_f32 v[12:13], v[66:67], s[40:41] op_sel_hi:[1,0]
	v_med3_f32 v8, v8, s83, v232
	v_med3_f32 v9, v9, s83, v232
	v_med3_f32 v14, v6, s83, v232
	v_mov_b32_e32 v6, v157
	v_med3_f32 v15, v7, s83, v232
	v_cvt_pk_fp8_f32 v6, v8, v9
	v_med3_f32 v8, v12, s83, v232
	v_med3_f32 v9, v13, s83, v232
	v_mov_b32_e32 v7, v157
	v_cvt_pk_fp8_f32 v7, v8, v9
	v_pk_mul_f32 v[10:11], v[64:65], s[40:41] op_sel_hi:[1,0]
	v_cvt_pk_fp8_f32 v6, v14, v15 op_sel:[0,0,1]
	v_med3_f32 v8, v10, s83, v232
	v_med3_f32 v9, v11, s83, v232
	v_cvt_pk_fp8_f32 v7, v8, v9 op_sel:[0,0,1]
	v_pk_mul_f32 v[8:9], v[20:21], s[40:41] op_sel_hi:[1,0]
	v_pk_mul_f32 v[10:11], v[22:23], s[40:41] op_sel_hi:[1,0]
	v_pk_mul_f32 v[14:15], v[74:75], s[40:41] op_sel_hi:[1,0]
	v_med3_f32 v10, v10, s83, v232
	v_med3_f32 v11, v11, s83, v232
	v_med3_f32 v16, v8, s83, v232
	v_mov_b32_e32 v8, v157
	v_med3_f32 v17, v9, s83, v232
	v_cvt_pk_fp8_f32 v8, v10, v11
	v_med3_f32 v10, v14, s83, v232
	v_med3_f32 v11, v15, s83, v232
	v_mov_b32_e32 v9, v157
	v_cvt_pk_fp8_f32 v9, v10, v11
	v_or_b32_e32 v4, 48, v108
	v_pk_mul_f32 v[12:13], v[72:73], s[40:41] op_sel_hi:[1,0]
	v_ashrrev_i32_e32 v5, 31, v4
	v_med3_f32 v10, v12, s83, v232
	v_med3_f32 v11, v13, s83, v232
	v_lshlrev_b64 v[4:5], 11, v[4:5]
	v_cvt_pk_fp8_f32 v8, v16, v17 op_sel:[0,0,1]
	v_cvt_pk_fp8_f32 v9, v10, v11 op_sel:[0,0,1]
	v_lshl_add_u64 v[4:5], s[4:5], 0, v[4:5]
	v_lshl_add_u64 v[4:5], v[4:5], 0, v[110:111]
	global_store_dwordx2 v[4:5], v[6:7], off
	global_store_dwordx2 v[4:5], v[8:9], off offset:128
	v_pk_mul_f32 v[6:7], v[24:25], s[40:41] op_sel_hi:[1,0]
	v_pk_mul_f32 v[8:9], v[26:27], s[40:41] op_sel_hi:[1,0]
	v_pk_mul_f32 v[12:13], v[78:79], s[40:41] op_sel_hi:[1,0]
	v_med3_f32 v8, v8, s83, v232
	v_med3_f32 v9, v9, s83, v232
	v_med3_f32 v14, v6, s83, v232
	v_mov_b32_e32 v6, v157
	v_med3_f32 v15, v7, s83, v232
	v_cvt_pk_fp8_f32 v6, v8, v9
	v_med3_f32 v8, v12, s83, v232
	v_med3_f32 v9, v13, s83, v232
	v_mov_b32_e32 v7, v157
	v_cvt_pk_fp8_f32 v7, v8, v9
	v_pk_mul_f32 v[10:11], v[76:77], s[40:41] op_sel_hi:[1,0]
	v_cvt_pk_fp8_f32 v6, v14, v15 op_sel:[0,0,1]
	v_med3_f32 v8, v10, s83, v232
	v_med3_f32 v9, v11, s83, v232
	v_cvt_pk_fp8_f32 v7, v8, v9 op_sel:[0,0,1]
	v_pk_mul_f32 v[8:9], v[28:29], s[40:41] op_sel_hi:[1,0]
	v_pk_mul_f32 v[10:11], v[30:31], s[40:41] op_sel_hi:[1,0]
	v_pk_mul_f32 v[14:15], v[82:83], s[40:41] op_sel_hi:[1,0]
	v_med3_f32 v10, v10, s83, v232
	v_med3_f32 v11, v11, s83, v232
	v_med3_f32 v16, v8, s83, v232
	v_mov_b32_e32 v8, v157
	v_med3_f32 v17, v9, s83, v232
	v_cvt_pk_fp8_f32 v8, v10, v11
	v_med3_f32 v10, v14, s83, v232
	v_med3_f32 v11, v15, s83, v232
	v_mov_b32_e32 v9, v157
	v_cvt_pk_fp8_f32 v9, v10, v11
	v_pk_mul_f32 v[12:13], v[80:81], s[40:41] op_sel_hi:[1,0]
	v_lshl_add_u64 v[4:5], v[106:107], 0, s[2:3]
	v_med3_f32 v10, v12, s83, v232
	v_med3_f32 v11, v13, s83, v232
	v_cvt_pk_fp8_f32 v8, v16, v17 op_sel:[0,0,1]
	v_cvt_pk_fp8_f32 v9, v10, v11 op_sel:[0,0,1]
	s_mov_b32 s2, 0x40000
	v_add_co_u32_e32 v10, vcc, s2, v106
	v_pk_mul_f32 v[12:13], v[86:87], s[40:41] op_sel_hi:[1,0]
	s_nop 0
	v_addc_co_u32_e32 v11, vcc, 0, v107, vcc
	global_store_dwordx2 v[10:11], v[6:7], off
	global_store_dwordx2 v[4:5], v[8:9], off offset:128
	v_pk_mul_f32 v[6:7], v[32:33], s[40:41] op_sel_hi:[1,0]
	v_pk_mul_f32 v[8:9], v[34:35], s[40:41] op_sel_hi:[1,0]
	v_med3_f32 v14, v6, s83, v232
	v_med3_f32 v8, v8, s83, v232
	v_med3_f32 v9, v9, s83, v232
	v_mov_b32_e32 v6, v157
	v_med3_f32 v15, v7, s83, v232
	v_cvt_pk_fp8_f32 v6, v8, v9
	v_med3_f32 v8, v12, s83, v232
	v_med3_f32 v9, v13, s83, v232
	v_mov_b32_e32 v7, v157
	v_cvt_pk_fp8_f32 v7, v8, v9
	v_pk_mul_f32 v[10:11], v[84:85], s[40:41] op_sel_hi:[1,0]
	v_cvt_pk_fp8_f32 v6, v14, v15 op_sel:[0,0,1]
	v_med3_f32 v8, v10, s83, v232
	v_med3_f32 v9, v11, s83, v232
	v_cvt_pk_fp8_f32 v7, v8, v9 op_sel:[0,0,1]
	v_pk_mul_f32 v[8:9], v[36:37], s[40:41] op_sel_hi:[1,0]
	v_pk_mul_f32 v[10:11], v[38:39], s[40:41] op_sel_hi:[1,0]
	v_pk_mul_f32 v[14:15], v[90:91], s[40:41] op_sel_hi:[1,0]
	v_med3_f32 v10, v10, s83, v232
	v_med3_f32 v11, v11, s83, v232
	v_med3_f32 v16, v8, s83, v232
	v_mov_b32_e32 v8, v157
	v_med3_f32 v17, v9, s83, v232
	v_cvt_pk_fp8_f32 v8, v10, v11
	v_med3_f32 v10, v14, s83, v232
	v_med3_f32 v11, v15, s83, v232
	v_mov_b32_e32 v9, v157
	v_cvt_pk_fp8_f32 v9, v10, v11
	v_pk_mul_f32 v[12:13], v[88:89], s[40:41] op_sel_hi:[1,0]
	s_mov_b64 s[2:3], 0x48000
	v_med3_f32 v10, v12, s83, v232
	v_med3_f32 v11, v13, s83, v232
	v_lshl_add_u64 v[4:5], v[106:107], 0, s[2:3]
	v_cvt_pk_fp8_f32 v8, v16, v17 op_sel:[0,0,1]
	v_cvt_pk_fp8_f32 v9, v10, v11 op_sel:[0,0,1]
	s_mov_b32 s2, 0x48000
	v_add_co_u32_e32 v10, vcc, s2, v106
	v_pk_mul_f32 v[12:13], v[94:95], s[40:41] op_sel_hi:[1,0]
	s_nop 0
	v_addc_co_u32_e32 v11, vcc, 0, v107, vcc
	global_store_dwordx2 v[10:11], v[6:7], off
	global_store_dwordx2 v[4:5], v[8:9], off offset:128
	v_pk_mul_f32 v[6:7], v[40:41], s[40:41] op_sel_hi:[1,0]
	v_pk_mul_f32 v[8:9], v[42:43], s[40:41] op_sel_hi:[1,0]
	v_med3_f32 v14, v6, s83, v232
	v_med3_f32 v8, v8, s83, v232
	v_med3_f32 v9, v9, s83, v232
	v_mov_b32_e32 v6, v157
	v_med3_f32 v15, v7, s83, v232
	v_cvt_pk_fp8_f32 v6, v8, v9
	v_med3_f32 v8, v12, s83, v232
	v_med3_f32 v9, v13, s83, v232
	v_mov_b32_e32 v7, v157
	v_cvt_pk_fp8_f32 v7, v8, v9
	v_pk_mul_f32 v[10:11], v[92:93], s[40:41] op_sel_hi:[1,0]
	v_pk_mul_f32 v[44:45], v[130:131], v[44:45]
	v_med3_f32 v8, v10, s83, v232
	v_med3_f32 v9, v11, s83, v232
	v_cvt_pk_fp8_f32 v7, v8, v9 op_sel:[0,0,1]
	v_pk_mul_f32 v[8:9], v[44:45], s[40:41] op_sel_hi:[1,0]
	v_pk_mul_f32 v[10:11], v[46:47], s[40:41] op_sel_hi:[1,0]
	v_cvt_pk_fp8_f32 v6, v14, v15 op_sel:[0,0,1]
	v_pk_mul_f32 v[14:15], v[98:99], s[40:41] op_sel_hi:[1,0]
	v_med3_f32 v10, v10, s83, v232
	v_med3_f32 v11, v11, s83, v232
	v_med3_f32 v16, v8, s83, v232
	v_mov_b32_e32 v8, v157
	v_med3_f32 v17, v9, s83, v232
	v_cvt_pk_fp8_f32 v8, v10, v11
	v_med3_f32 v10, v14, s83, v232
	v_med3_f32 v11, v15, s83, v232
	v_mov_b32_e32 v9, v157
	v_cvt_pk_fp8_f32 v9, v10, v11
	v_pk_mul_f32 v[12:13], v[96:97], s[40:41] op_sel_hi:[1,0]
	s_mov_b64 s[2:3], 0x50000
	v_med3_f32 v10, v12, s83, v232
	v_med3_f32 v11, v13, s83, v232
	v_lshl_add_u64 v[4:5], v[106:107], 0, s[2:3]
	v_cvt_pk_fp8_f32 v8, v16, v17 op_sel:[0,0,1]
	v_cvt_pk_fp8_f32 v9, v10, v11 op_sel:[0,0,1]
	s_mov_b32 s2, 0x50000
	v_add_co_u32_e32 v10, vcc, s2, v106
	v_pk_mul_f32 v[12:13], v[102:103], s[40:41] op_sel_hi:[1,0]
	s_nop 0
	v_addc_co_u32_e32 v11, vcc, 0, v107, vcc
	global_store_dwordx2 v[10:11], v[6:7], off
	global_store_dwordx2 v[4:5], v[8:9], off offset:128
	v_pk_mul_f32 v[6:7], v[60:61], s[40:41] op_sel_hi:[1,0]
	v_pk_mul_f32 v[8:9], v[62:63], s[40:41] op_sel_hi:[1,0]
	v_med3_f32 v14, v6, s83, v232
	v_med3_f32 v8, v8, s83, v232
	v_med3_f32 v9, v9, s83, v232
	v_mov_b32_e32 v6, v157
	v_med3_f32 v15, v7, s83, v232
	v_cvt_pk_fp8_f32 v6, v8, v9
	v_med3_f32 v8, v12, s83, v232
	v_med3_f32 v9, v13, s83, v232
	v_mov_b32_e32 v7, v157
	v_cvt_pk_fp8_f32 v7, v8, v9
	v_pk_add_f32 v[104:105], v[104:105], 0.5 op_sel_hi:[1,0]
	v_pk_mul_f32 v[10:11], v[100:101], s[40:41] op_sel_hi:[1,0]
	v_pk_mul_f32 v[2:3], v[146:147], v[2:3]
	v_pk_mul_f32 v[104:105], v[104:105], s[38:39] op_sel_hi:[1,0]
	v_med3_f32 v8, v10, s83, v232
	v_med3_f32 v9, v11, s83, v232
	v_pk_mul_f32 v[104:105], v[136:137], v[104:105]
	v_cvt_pk_fp8_f32 v7, v8, v9 op_sel:[0,0,1]
	v_pk_mul_f32 v[2:3], v[2:3], s[40:41] op_sel_hi:[1,0]
	v_pk_mul_f32 v[8:9], v[68:69], s[40:41] op_sel_hi:[1,0]
	v_pk_mul_f32 v[10:11], v[104:105], s[40:41] op_sel_hi:[1,0]
	v_med3_f32 v8, v8, s83, v232
	v_med3_f32 v9, v9, s83, v232
	v_med3_f32 v12, v2, s83, v232
	v_mov_b32_e32 v2, v157
	v_med3_f32 v13, v3, s83, v232
	v_cvt_pk_fp8_f32 v2, v8, v9
	v_med3_f32 v8, v10, s83, v232
	v_med3_f32 v9, v11, s83, v232
	v_mov_b32_e32 v3, v157
	v_pk_mul_f32 v[0:1], v[0:1], s[38:39] op_sel_hi:[1,0]
	v_cvt_pk_fp8_f32 v3, v8, v9
	v_pk_mul_f32 v[0:1], v[138:139], v[0:1]
	v_cvt_pk_fp8_f32 v6, v14, v15 op_sel:[0,0,1]
	v_pk_mul_f32 v[0:1], v[0:1], s[40:41] op_sel_hi:[1,0]
	v_cvt_pk_fp8_f32 v2, v12, v13 op_sel:[0,0,1]
	v_med3_f32 v0, v0, s83, v232
	v_med3_f32 v1, v1, s83, v232
	v_cvt_pk_fp8_f32 v3, v0, v1 op_sel:[0,0,1]
	v_add_co_u32_e32 v0, vcc, s84, v106
	s_mov_b64 s[2:3], 0x58000
	s_nop 0
	v_addc_co_u32_e32 v1, vcc, 0, v107, vcc
	s_and_b64 vcc, exec, s[0:1]
	s_mov_b32 s89, s85
	s_mov_b32 s90, s86
	v_lshl_add_u64 v[4:5], v[106:107], 0, s[2:3]
	global_store_dwordx2 v[0:1], v[6:7], off
	global_store_dwordx2 v[4:5], v[2:3], off offset:128
	s_cbranch_vccz .LBB0_2184
	s_waitcnt vmcnt(0)
	s_cmpk_gt_u32 s60, 0xff
	s_cbranch_scc1 .LBB0_2195
	s_barrier

.LBB0_2262:
	ds_read_b128 v[8:11], v179
	ds_read_b128 v[12:15], v179 offset:1024
	ds_read_b128 v[0:3], v179 offset:2048
	ds_read_b128 v[4:7], v179 offset:3072
	s_add_u32 s18, s16, 0xfffc0080
	s_addc_u32 s19, s17, -1
	s_cmp_eq_u32 s62, 12
	s_cselect_b32 s21, s56, s19
	s_cselect_b32 s20, s57, s18
	s_cselect_b32 s19, s58, s61
	s_cselect_b32 s18, s59, s60
	v_lshl_add_u64 v[162:163], s[16:17], 0, v[156:157]
	s_add_i32 m0, s30, 0xc000
	ds_read_b128 v[166:169], v180
	ds_read_b128 v[170:173], v180 offset:1024
	ds_read_b128 v[182:185], v180 offset:2048
	ds_read_b128 v[186:189], v180 offset:3072
	ds_read_b128 v[190:193], v180 offset:4096
	ds_read_b128 v[194:197], v180 offset:5120
	ds_read_b128 v[198:201], v180 offset:6144
	ds_read_b128 v[202:205], v180 offset:7168
	global_load_lds_dwordx4 v[162:163], off
	v_lshl_add_u64 v[162:163], s[16:17], 0, v[154:155]
	s_add_i32 m0, s30, 0xe000
	s_nop 0
	global_load_lds_dwordx4 v[162:163], off
	s_waitcnt lgkmcnt(8)
	s_barrier
	s_waitcnt lgkmcnt(0)
	s_setprio 1
	s_waitcnt lgkmcnt(0)
	v_mfma_f32_16x16x128_f8f6f4 v[140:143], v[8:15], v[166:173], v[140:143]
	v_mfma_f32_16x16x128_f8f6f4 v[136:139], v[0:7], v[166:173], v[136:139]
	v_mfma_f32_16x16x128_f8f6f4 v[128:131], v[8:15], v[182:189], v[128:131]
	v_mfma_f32_16x16x128_f8f6f4 v[120:123], v[0:7], v[182:189], v[120:123]
	v_mfma_f32_16x16x128_f8f6f4 v[112:115], v[8:15], v[190:197], v[112:115]
	v_mfma_f32_16x16x128_f8f6f4 v[104:107], v[0:7], v[190:197], v[104:107]
	v_mfma_f32_16x16x128_f8f6f4 v[96:99], v[8:15], v[198:205], v[96:99]
	v_mfma_f32_16x16x128_f8f6f4 v[88:91], v[0:7], v[198:205], v[88:91]
	s_setprio 0
	s_barrier
	s_add_i32 s63, s46, s29
	v_lshl_add_u64 v[162:163], s[18:19], 0, v[146:147]
	s_mov_b32 m0, s63
	ds_read_b128 v[206:209], v181
	ds_read_b128 v[210:213], v181 offset:1024
	ds_read_b128 v[214:217], v181 offset:2048
	ds_read_b128 v[218:221], v181 offset:3072
	global_load_lds_dwordx4 v[162:163], off
	v_lshl_add_u64 v[164:165], s[18:19], 0, v[150:151]
	s_add_i32 m0, s63, 0x2000
	s_nop 0
	global_load_lds_dwordx4 v[164:165], off
	s_barrier
	s_waitcnt lgkmcnt(0)
	s_setprio 1
	s_waitcnt lgkmcnt(0)
	v_mfma_f32_16x16x128_f8f6f4 v[132:135], v[206:213], v[166:173], v[132:135]
	v_mfma_f32_16x16x128_f8f6f4 v[124:127], v[214:221], v[166:173], v[124:127]
	v_mfma_f32_16x16x128_f8f6f4 v[116:119], v[206:213], v[182:189], v[116:119]
	v_mfma_f32_16x16x128_f8f6f4 v[108:111], v[214:221], v[182:189], v[108:111]
	v_mfma_f32_16x16x128_f8f6f4 v[100:103], v[206:213], v[190:197], v[100:103]
	v_mfma_f32_16x16x128_f8f6f4 v[92:95], v[214:221], v[190:197], v[92:95]
	v_mfma_f32_16x16x128_f8f6f4 v[84:87], v[206:213], v[198:205], v[84:87]
	v_mfma_f32_16x16x128_f8f6f4 v[80:83], v[214:221], v[198:205], v[80:83]
	s_setprio 0
	s_mov_b32 m0, s30
	v_lshl_add_u64 v[166:167], s[20:21], 0, v[144:145]
	s_barrier
	ds_read_b128 v[182:185], v180 offset:16384
	ds_read_b128 v[186:189], v180 offset:17408
	ds_read_b128 v[190:193], v180 offset:18432
	ds_read_b128 v[194:197], v180 offset:19456
	ds_read_b128 v[198:201], v180 offset:20480
	ds_read_b128 v[202:205], v180 offset:21504
	ds_read_b128 v[224:227], v180 offset:22528
	ds_read_b128 v[228:231], v180 offset:23552
	global_load_lds_dwordx4 v[166:167], off
	v_lshl_add_u64 v[168:169], s[20:21], 0, v[148:149]
	s_mov_b32 m0, s31
	s_nop 0
	global_load_lds_dwordx4 v[168:169], off
	s_barrier
	s_waitcnt lgkmcnt(0)
	s_setprio 1
	s_waitcnt lgkmcnt(0)
	v_mfma_f32_16x16x128_f8f6f4 v[76:79], v[8:15], v[182:189], v[76:79]
	v_mfma_f32_16x16x128_f8f6f4 v[72:75], v[0:7], v[182:189], v[72:75]
	v_mfma_f32_16x16x128_f8f6f4 v[64:67], v[8:15], v[190:197], v[64:67]
	v_mfma_f32_16x16x128_f8f6f4 v[56:59], v[0:7], v[190:197], v[56:59]
	v_mfma_f32_16x16x128_f8f6f4 v[48:51], v[8:15], v[198:205], v[48:51]
	v_mfma_f32_16x16x128_f8f6f4 v[40:43], v[0:7], v[198:205], v[40:43]
	v_mfma_f32_16x16x128_f8f6f4 v[32:35], v[8:15], v[224:231], v[32:35]
	v_mfma_f32_16x16x128_f8f6f4 v[24:27], v[0:7], v[224:231], v[24:27]
	s_setprio 0
	s_barrier
	s_add_u32 s64, s18, 0x40000
	s_addc_u32 s65, s19, 0
	s_add_i32 s63, s47, s29
	v_lshl_add_u64 v[0:1], s[64:65], 0, v[146:147]
	s_mov_b32 m0, s63
	s_nop 0
	global_load_lds_dwordx4 v[0:1], off
	v_lshl_add_u64 v[0:1], s[64:65], 0, v[150:151]
	s_add_i32 m0, s63, 0x2000
	s_nop 0
	global_load_lds_dwordx4 v[0:1], off
	s_waitcnt vmcnt(6)
	s_barrier
	s_setprio 1
	v_mfma_f32_16x16x128_f8f6f4 v[68:71], v[206:213], v[182:189], v[68:71]
	v_mfma_f32_16x16x128_f8f6f4 v[60:63], v[214:221], v[182:189], v[60:63]
	v_mfma_f32_16x16x128_f8f6f4 v[52:55], v[206:213], v[190:197], v[52:55]
	v_mfma_f32_16x16x128_f8f6f4 v[44:47], v[214:221], v[190:197], v[44:47]
	v_mfma_f32_16x16x128_f8f6f4 v[36:39], v[206:213], v[198:205], v[36:39]
	v_mfma_f32_16x16x128_f8f6f4 v[28:31], v[214:221], v[198:205], v[28:31]
	v_mfma_f32_16x16x128_f8f6f4 v[20:23], v[206:213], v[224:231], v[20:23]
	v_mfma_f32_16x16x128_f8f6f4 v[16:19], v[214:221], v[224:231], v[16:19]
	s_setprio 0
	s_add_i32 s63, 0, 0x18000
	v_add_u32_e32 v12, s63, v176
	s_barrier
	ds_read_b128 v[0:3], v12
	ds_read_b128 v[4:7], v12 offset:1024
	ds_read_b128 v[8:11], v12 offset:2048
	ds_read_b128 v[12:15], v12 offset:3072
	s_add_u32 s20, s20, 0x40000
	s_addc_u32 s21, s21, 0
	s_mov_b32 m0, s38
	v_lshl_add_u64 v[170:171], s[20:21], 0, v[144:145]
	ds_read_b128 v[182:185], v180 offset:32768
	ds_read_b128 v[186:189], v180 offset:33792
	ds_read_b128 v[190:193], v180 offset:34816
	ds_read_b128 v[194:197], v180 offset:35840
	ds_read_b128 v[198:201], v180 offset:36864
	ds_read_b128 v[202:205], v180 offset:37888
	ds_read_b128 v[206:209], v180 offset:38912
	ds_read_b128 v[210:213], v180 offset:39936
	global_load_lds_dwordx4 v[170:171], off
	v_lshl_add_u64 v[170:171], s[20:21], 0, v[148:149]
	s_mov_b32 m0, s39
	s_nop 0
	global_load_lds_dwordx4 v[170:171], off
	s_waitcnt lgkmcnt(8)
	s_barrier
	s_waitcnt lgkmcnt(0)
	s_setprio 1
	s_waitcnt lgkmcnt(0)
	v_mfma_f32_16x16x128_f8f6f4 v[140:143], v[0:7], v[182:189], v[140:143]
	v_mfma_f32_16x16x128_f8f6f4 v[136:139], v[8:15], v[182:189], v[136:139]
	v_mfma_f32_16x16x128_f8f6f4 v[128:131], v[0:7], v[190:197], v[128:131]
	v_mfma_f32_16x16x128_f8f6f4 v[120:123], v[8:15], v[190:197], v[120:123]
	v_mfma_f32_16x16x128_f8f6f4 v[112:115], v[0:7], v[198:205], v[112:115]
	v_mfma_f32_16x16x128_f8f6f4 v[104:107], v[8:15], v[198:205], v[104:107]
	v_mfma_f32_16x16x128_f8f6f4 v[96:99], v[0:7], v[206:213], v[96:99]
	v_mfma_f32_16x16x128_f8f6f4 v[88:91], v[8:15], v[206:213], v[88:91]
	s_setprio 0
	s_barrier
	s_add_i32 s20, 0, 0x1c000
	s_add_i32 s21, s63, s29
	v_add_u32_e32 v152, s20, v176
	v_lshl_add_u64 v[162:163], v[162:163], 0, s[4:5]
	s_mov_b32 m0, s21
	ds_read_b128 v[214:217], v152
	ds_read_b128 v[218:221], v152 offset:1024
	ds_read_b128 v[224:227], v152 offset:2048
	ds_read_b128 v[228:231], v152 offset:3072
	global_load_lds_dwordx4 v[162:163], off
	v_lshl_add_u64 v[162:163], v[164:165], 0, s[4:5]
	s_add_i32 m0, s21, 0x2000
	s_nop 0
	global_load_lds_dwordx4 v[162:163], off
	s_barrier
	s_waitcnt lgkmcnt(0)
	s_setprio 1
	s_waitcnt lgkmcnt(0)
	v_mfma_f32_16x16x128_f8f6f4 v[132:135], v[214:221], v[182:189], v[132:135]
	v_mfma_f32_16x16x128_f8f6f4 v[124:127], v[224:231], v[182:189], v[124:127]
	v_mfma_f32_16x16x128_f8f6f4 v[116:119], v[214:221], v[190:197], v[116:119]
	v_mfma_f32_16x16x128_f8f6f4 v[108:111], v[224:231], v[190:197], v[108:111]
	v_mfma_f32_16x16x128_f8f6f4 v[100:103], v[214:221], v[198:205], v[100:103]
	v_mfma_f32_16x16x128_f8f6f4 v[92:95], v[224:231], v[198:205], v[92:95]
	v_mfma_f32_16x16x128_f8f6f4 v[84:87], v[214:221], v[206:213], v[84:87]
	v_mfma_f32_16x16x128_f8f6f4 v[80:83], v[224:231], v[206:213], v[80:83]
	s_setprio 0
	s_mov_b32 m0, s43
	v_lshl_add_u64 v[162:163], v[166:167], 0, s[4:5]
	s_barrier
	ds_read_b128 v[182:185], v180 offset:49152
	ds_read_b128 v[186:189], v180 offset:50176
	ds_read_b128 v[190:193], v180 offset:51200
	ds_read_b128 v[194:197], v180 offset:52224
	ds_read_b128 v[198:201], v180 offset:53248
	ds_read_b128 v[202:205], v180 offset:54272
	ds_read_b128 v[206:209], v180 offset:55296
	ds_read_b128 v[210:213], v180 offset:56320
	global_load_lds_dwordx4 v[162:163], off
	v_lshl_add_u64 v[162:163], v[168:169], 0, s[4:5]
	s_mov_b32 m0, s44
	s_nop 0
	global_load_lds_dwordx4 v[162:163], off
	s_barrier
	s_waitcnt lgkmcnt(0)
	s_setprio 1
	s_waitcnt lgkmcnt(0)
	v_mfma_f32_16x16x128_f8f6f4 v[76:79], v[0:7], v[182:189], v[76:79]
	v_mfma_f32_16x16x128_f8f6f4 v[72:75], v[8:15], v[182:189], v[72:75]
	v_mfma_f32_16x16x128_f8f6f4 v[64:67], v[0:7], v[190:197], v[64:67]
	v_mfma_f32_16x16x128_f8f6f4 v[56:59], v[8:15], v[190:197], v[56:59]
	v_mfma_f32_16x16x128_f8f6f4 v[48:51], v[0:7], v[198:205], v[48:51]
	v_mfma_f32_16x16x128_f8f6f4 v[40:43], v[8:15], v[198:205], v[40:43]
	v_mfma_f32_16x16x128_f8f6f4 v[32:35], v[0:7], v[206:213], v[32:35]
	v_mfma_f32_16x16x128_f8f6f4 v[24:27], v[8:15], v[206:213], v[24:27]
	s_setprio 0
	s_barrier
	s_add_u32 s18, s18, 0x40080
	s_addc_u32 s19, s19, 0
	s_add_i32 s20, s20, s29
	v_lshl_add_u64 v[0:1], s[18:19], 0, v[146:147]
	s_mov_b32 m0, s20
	s_nop 0
	global_load_lds_dwordx4 v[0:1], off
	v_lshl_add_u64 v[0:1], s[18:19], 0, v[150:151]
	s_add_i32 m0, s20, 0x2000
	s_nop 0
	global_load_lds_dwordx4 v[0:1], off
	s_waitcnt vmcnt(6)
	s_barrier
	s_setprio 1
	v_mfma_f32_16x16x128_f8f6f4 v[68:71], v[214:221], v[182:189], v[68:71]
	v_mfma_f32_16x16x128_f8f6f4 v[60:63], v[224:231], v[182:189], v[60:63]
	v_mfma_f32_16x16x128_f8f6f4 v[52:55], v[214:221], v[190:197], v[52:55]
	v_mfma_f32_16x16x128_f8f6f4 v[44:47], v[224:231], v[190:197], v[44:47]
	v_mfma_f32_16x16x128_f8f6f4 v[36:39], v[214:221], v[198:205], v[36:39]
	v_mfma_f32_16x16x128_f8f6f4 v[28:31], v[224:231], v[198:205], v[28:31]
	v_mfma_f32_16x16x128_f8f6f4 v[20:23], v[214:221], v[206:213], v[20:23]
	v_mfma_f32_16x16x128_f8f6f4 v[16:19], v[224:231], v[206:213], v[16:19]
	s_setprio 0
	s_add_i32 s62, s62, 2
	s_add_u32 s60, s60, 0x100
	s_addc_u32 s61, s61, 0
	s_add_u32 s16, s16, 0x100
	s_addc_u32 s17, s17, 0
	s_cmp_gt_u32 s62, 13
	s_barrier
	s_cbranch_scc0 .LBB0_2262
	s_lshl_b32 s16, s55, 8
	s_min_i32 s17, s55, 32
	s_ashr_i32 s20, s17, 4
	s_add_i32 s17, s16, 0xffffe000
	s_cmp_lt_i32 s55, 32
	s_cselect_b32 s19, s48, 0x302b8000
	s_cselect_b32 s18, s16, s17
	s_add_u32 s55, s2, s19
	s_mul_i32 s20, s20, 6
	s_addc_u32 s56, s3, 0
	s_ashr_i32 s19, s18, 31
	s_ashr_i32 s17, s16, 31
	s_ashr_i32 s21, s20, 31
	s_lshl_b64 s[18:19], s[18:19], 12
	s_lshl_b64 s[16:17], s[16:17], 12
	s_lshl_b64 s[20:21], s[20:21], 13
	v_lshl_or_b32 v8, s54, 8, v178
	s_add_u32 s20, s2, s20
	s_addc_u32 s21, s3, s21
	v_ashrrev_i32_e32 v9, 31, v8
	v_lshl_add_u64 v[0:1], v[8:9], 2, s[20:21]
	v_lshl_add_u64 v[10:11], v[0:1], 0, s[6:7]
	v_add_co_u32_e32 v0, vcc, s49, v0
	s_nop 7
	s_nop 7
	s_nop 7
	s_add_u32 s18, s55, s18
	s_nop 0
	v_addc_co_u32_e32 v1, vcc, 0, v1, vcc
	v_add_u32_e32 v152, v177, v8
	global_load_dwordx4 v[0:3], v[0:1], off
	s_nop 0
	global_load_dwordx4 v[182:185], v[10:11], off offset:528
	global_load_dwordx4 v[4:7], v[10:11], off offset:16
	global_load_dwordx4 v[186:189], v[10:11], off offset:512
	s_addc_u32 s19, s56, s19
	s_add_u32 s16, s41, s16
	v_lshlrev_b64 v[222:223], 1, v[152:153]
	v_lshl_add_u64 v[8:9], s[18:19], 0, v[222:223]
	global_load_dwordx4 v[190:193], v[8:9], off
	v_add_u32_e32 v8, 0x80, v152
	v_mov_b32_e32 v9, v153
	v_lshlrev_b64 v[224:225], 1, v[8:9]
	v_lshl_add_u64 v[8:9], s[18:19], 0, v[224:225]
	global_load_dwordx4 v[194:197], v[8:9], off
	v_add_u32_e32 v8, 0x8000, v152
	v_mov_b32_e32 v9, v153
	v_lshlrev_b64 v[226:227], 1, v[8:9]
	v_lshl_add_u64 v[8:9], s[18:19], 0, v[226:227]
	global_load_dwordx4 v[198:201], v[8:9], off
	v_add_u32_e32 v8, 0x8080, v152
	v_mov_b32_e32 v9, v153
	v_lshlrev_b64 v[170:171], 1, v[8:9]
	v_lshl_add_u64 v[8:9], s[18:19], 0, v[170:171]
	global_load_dwordx4 v[202:205], v[8:9], off
	v_add_u32_e32 v8, 0x10000, v152
	v_mov_b32_e32 v9, v153
	v_lshlrev_b64 v[168:169], 1, v[8:9]
	v_lshl_add_u64 v[8:9], s[18:19], 0, v[168:169]
	global_load_dwordx4 v[206:209], v[8:9], off
	v_add_u32_e32 v8, 0x10080, v152
	v_mov_b32_e32 v9, v153
	v_lshlrev_b64 v[166:167], 1, v[8:9]
	v_lshl_add_u64 v[8:9], s[18:19], 0, v[166:167]
	global_load_dwordx4 v[210:213], v[8:9], off
	v_mov_b32_e32 v9, v153
	v_add_u32_e32 v8, 0x18000, v152
	v_lshlrev_b64 v[164:165], 1, v[8:9]
	v_lshl_add_u64 v[8:9], s[18:19], 0, v[164:165]
	global_load_dwordx4 v[214:217], v[8:9], off
	v_mov_b32_e32 v9, v153
	v_add_u32_e32 v8, 0x18080, v152
	v_lshlrev_b64 v[162:163], 1, v[8:9]
	v_lshl_add_u64 v[8:9], s[18:19], 0, v[162:163]
	global_load_dwordx4 v[218:221], v[8:9], off
	s_addc_u32 s17, s42, s17
	s_and_b64 vcc, exec, s[0:1]
	s_mov_b32 s54, s50
	s_mov_b32 s55, s51
	s_waitcnt vmcnt(0)
	v_pk_mul_f32 v[12:13], v[0:1], s[8:9] op_sel_hi:[1,0]
	v_pk_mul_f32 v[0:1], v[182:183], s[8:9] op_sel_hi:[1,0]
	v_pk_mul_f32 v[14:15], v[2:3], s[8:9] op_sel_hi:[1,0]
	v_pk_mul_f32 v[10:11], v[6:7], s[8:9] op_sel_hi:[1,0]
	v_pk_mul_f32 v[8:9], v[4:5], s[8:9] op_sel_hi:[1,0]
	v_pk_mul_f32 v[6:7], v[188:189], s[8:9] op_sel_hi:[1,0]
	v_pk_mul_f32 v[4:5], v[186:187], s[8:9] op_sel_hi:[1,0]
	v_pk_mul_f32 v[2:3], v[184:185], s[8:9] op_sel_hi:[1,0]
	v_lshlrev_b32_e32 v182, 16, v190
	v_and_b32_e32 v183, 0xffff0000, v190
	v_lshlrev_b32_e32 v184, 16, v191
	v_and_b32_e32 v185, 0xffff0000, v191
	v_lshlrev_b32_e32 v186, 16, v192
	v_and_b32_e32 v187, 0xffff0000, v192
	v_lshlrev_b32_e32 v188, 16, v193
	v_and_b32_e32 v189, 0xffff0000, v193
	v_lshlrev_b32_e32 v190, 16, v194
	v_and_b32_e32 v191, 0xffff0000, v194
	v_pk_fma_f32 v[140:141], v[140:141], v[12:13], v[182:183]
	v_lshlrev_b32_e32 v192, 16, v195
	v_and_b32_e32 v193, 0xffff0000, v195
	v_lshlrev_b32_e32 v194, 16, v196
	v_and_b32_e32 v195, 0xffff0000, v196
	v_lshlrev_b32_e32 v196, 16, v197
	v_and_b32_e32 v197, 0xffff0000, v197
	v_pk_fma_f32 v[142:143], v[142:143], v[14:15], v[184:185]
	v_pk_fma_f32 v[182:183], v[138:139], v[10:11], v[188:189]
	v_pk_fma_f32 v[138:139], v[136:137], v[8:9], v[186:187]
	v_cvt_pk_bf16_f32 v136, v140, v141
	v_cvt_pk_bf16_f32 v137, v142, v143
	v_lshl_add_u64 v[140:141], s[16:17], 0, v[222:223]
	v_pk_fma_f32 v[132:133], v[132:133], v[4:5], v[190:191]
	v_lshlrev_b32_e32 v228, 16, v198
	v_and_b32_e32 v229, 0xffff0000, v198
	v_lshlrev_b32_e32 v198, 16, v199
	v_and_b32_e32 v199, 0xffff0000, v199
	v_cvt_pk_bf16_f32 v138, v138, v139
	v_cvt_pk_bf16_f32 v139, v182, v183
	global_store_dwordx4 v[140:141], v[136:139], off
	v_pk_fma_f32 v[134:135], v[134:135], v[6:7], v[192:193]
	v_lshlrev_b32_e32 v230, 16, v200
	v_pk_fma_f32 v[136:137], v[126:127], v[2:3], v[196:197]
	v_pk_fma_f32 v[126:127], v[124:125], v[0:1], v[194:195]
	v_cvt_pk_bf16_f32 v124, v132, v133
	v_cvt_pk_bf16_f32 v125, v134, v135
	v_lshl_add_u64 v[132:133], s[16:17], 0, v[224:225]
	v_and_b32_e32 v231, 0xffff0000, v200
	v_lshlrev_b32_e32 v200, 16, v201
	v_and_b32_e32 v201, 0xffff0000, v201
	v_lshlrev_b32_e32 v232, 16, v202
	v_and_b32_e32 v233, 0xffff0000, v202
	v_cvt_pk_bf16_f32 v126, v126, v127
	v_cvt_pk_bf16_f32 v127, v136, v137
	global_store_dwordx4 v[132:133], v[124:127], off
	v_lshlrev_b32_e32 v202, 16, v203
	v_and_b32_e32 v203, 0xffff0000, v203
	v_pk_fma_f32 v[124:125], v[130:131], v[14:15], v[198:199]
	v_lshlrev_b32_e32 v234, 16, v204
	v_and_b32_e32 v235, 0xffff0000, v204
	v_lshlrev_b32_e32 v204, 16, v205
	v_and_b32_e32 v205, 0xffff0000, v205
	v_pk_fma_f32 v[126:127], v[128:129], v[12:13], v[228:229]
	v_pk_fma_f32 v[128:129], v[122:123], v[10:11], v[200:201]
	v_pk_fma_f32 v[122:123], v[120:121], v[8:9], v[230:231]
	v_cvt_pk_bf16_f32 v120, v126, v127
	v_cvt_pk_bf16_f32 v121, v124, v125
	v_lshl_add_u64 v[124:125], s[16:17], 0, v[226:227]
	v_pk_fma_f32 v[116:117], v[116:117], v[4:5], v[232:233]
	v_lshlrev_b32_e32 v236, 16, v206
	v_and_b32_e32 v237, 0xffff0000, v206
	v_lshlrev_b32_e32 v206, 16, v207
	v_and_b32_e32 v207, 0xffff0000, v207
	v_cvt_pk_bf16_f32 v122, v122, v123
	v_cvt_pk_bf16_f32 v123, v128, v129
	global_store_dwordx4 v[124:125], v[120:123], off
	v_pk_fma_f32 v[118:119], v[118:119], v[6:7], v[202:203]
	v_lshlrev_b32_e32 v238, 16, v208
	v_pk_fma_f32 v[120:121], v[110:111], v[2:3], v[204:205]
	v_pk_fma_f32 v[110:111], v[108:109], v[0:1], v[234:235]
	v_cvt_pk_bf16_f32 v108, v116, v117
	v_cvt_pk_bf16_f32 v109, v118, v119
	v_lshl_add_u64 v[116:117], s[16:17], 0, v[170:171]
	v_and_b32_e32 v239, 0xffff0000, v208
	v_lshlrev_b32_e32 v208, 16, v209
	v_and_b32_e32 v209, 0xffff0000, v209
	v_lshlrev_b32_e32 v240, 16, v210
	v_and_b32_e32 v241, 0xffff0000, v210
	v_cvt_pk_bf16_f32 v110, v110, v111
	v_cvt_pk_bf16_f32 v111, v120, v121
	global_store_dwordx4 v[116:117], v[108:111], off
	v_lshlrev_b32_e32 v210, 16, v211
	v_and_b32_e32 v211, 0xffff0000, v211
	v_pk_fma_f32 v[108:109], v[114:115], v[14:15], v[206:207]
	v_lshlrev_b32_e32 v242, 16, v212
	v_and_b32_e32 v243, 0xffff0000, v212
	v_lshlrev_b32_e32 v212, 16, v213
	v_and_b32_e32 v213, 0xffff0000, v213
	v_pk_fma_f32 v[110:111], v[112:113], v[12:13], v[236:237]
	v_pk_fma_f32 v[112:113], v[106:107], v[10:11], v[208:209]
	v_pk_fma_f32 v[106:107], v[104:105], v[8:9], v[238:239]
	v_cvt_pk_bf16_f32 v104, v110, v111
	v_cvt_pk_bf16_f32 v105, v108, v109
	v_lshl_add_u64 v[108:109], s[16:17], 0, v[168:169]
	v_pk_fma_f32 v[100:101], v[100:101], v[4:5], v[240:241]
	v_lshlrev_b32_e32 v244, 16, v214
	v_and_b32_e32 v245, 0xffff0000, v214
	v_lshlrev_b32_e32 v214, 16, v215
	v_and_b32_e32 v215, 0xffff0000, v215
	v_cvt_pk_bf16_f32 v106, v106, v107
	v_cvt_pk_bf16_f32 v107, v112, v113
	global_store_dwordx4 v[108:109], v[104:107], off
	v_pk_fma_f32 v[102:103], v[102:103], v[6:7], v[210:211]
	v_lshlrev_b32_e32 v246, 16, v216
	v_pk_fma_f32 v[104:105], v[94:95], v[2:3], v[212:213]
	v_pk_fma_f32 v[94:95], v[92:93], v[0:1], v[242:243]
	v_cvt_pk_bf16_f32 v92, v100, v101
	v_cvt_pk_bf16_f32 v93, v102, v103
	v_lshl_add_u64 v[100:101], s[16:17], 0, v[166:167]
	v_and_b32_e32 v247, 0xffff0000, v216
	v_lshlrev_b32_e32 v216, 16, v217
	v_and_b32_e32 v217, 0xffff0000, v217
	v_lshlrev_b32_e32 v248, 16, v218
	v_and_b32_e32 v249, 0xffff0000, v218
	v_cvt_pk_bf16_f32 v94, v94, v95
	v_cvt_pk_bf16_f32 v95, v104, v105
	global_store_dwordx4 v[100:101], v[92:95], off
	v_lshlrev_b32_e32 v218, 16, v219
	v_and_b32_e32 v219, 0xffff0000, v219
	v_pk_fma_f32 v[92:93], v[98:99], v[14:15], v[214:215]
	v_lshlrev_b32_e32 v172, 16, v220
	v_and_b32_e32 v173, 0xffff0000, v220
	v_lshlrev_b32_e32 v220, 16, v221
	v_and_b32_e32 v221, 0xffff0000, v221
	v_pk_fma_f32 v[94:95], v[96:97], v[12:13], v[244:245]
	v_pk_fma_f32 v[96:97], v[90:91], v[10:11], v[216:217]
	v_pk_fma_f32 v[90:91], v[88:89], v[8:9], v[246:247]
	v_cvt_pk_bf16_f32 v88, v94, v95
	v_cvt_pk_bf16_f32 v89, v92, v93
	v_lshl_add_u64 v[92:93], s[16:17], 0, v[164:165]
	v_pk_fma_f32 v[84:85], v[84:85], v[4:5], v[248:249]
	v_cvt_pk_bf16_f32 v90, v90, v91
	v_cvt_pk_bf16_f32 v91, v96, v97
	global_store_dwordx4 v[92:93], v[88:91], off
	v_pk_fma_f32 v[86:87], v[86:87], v[6:7], v[218:219]
	s_nop 0
	v_pk_fma_f32 v[88:89], v[82:83], v[2:3], v[220:221]
	v_pk_fma_f32 v[82:83], v[80:81], v[0:1], v[172:173]
	v_cvt_pk_bf16_f32 v80, v84, v85
	v_cvt_pk_bf16_f32 v81, v86, v87
	v_lshl_add_u64 v[84:85], s[16:17], 0, v[162:163]
	v_cvt_pk_bf16_f32 v82, v82, v83
	v_cvt_pk_bf16_f32 v83, v88, v89
	global_store_dwordx4 v[84:85], v[80:83], off
	s_nop 1
	v_add_u32_e32 v80, 0x40000, v152
	v_mov_b32_e32 v81, v153
	v_lshlrev_b64 v[122:123], 1, v[80:81]
	v_lshl_add_u64 v[80:81], s[18:19], 0, v[122:123]
	global_load_dwordx4 v[90:93], v[80:81], off
	v_add_u32_e32 v80, 0x40080, v152
	v_mov_b32_e32 v81, v153
	v_lshlrev_b64 v[124:125], 1, v[80:81]
	v_lshl_add_u64 v[80:81], s[18:19], 0, v[124:125]
	global_load_dwordx4 v[94:97], v[80:81], off
	v_add_u32_e32 v80, 0x48000, v152
	v_mov_b32_e32 v81, v153
	v_lshlrev_b64 v[126:127], 1, v[80:81]
	v_lshl_add_u64 v[80:81], s[18:19], 0, v[126:127]
	global_load_dwordx4 v[98:101], v[80:81], off
	v_add_u32_e32 v80, 0x48080, v152
	v_mov_b32_e32 v81, v153
	v_lshlrev_b64 v[88:89], 1, v[80:81]
	v_lshl_add_u64 v[80:81], s[18:19], 0, v[88:89]
	global_load_dwordx4 v[102:105], v[80:81], off
	v_add_u32_e32 v80, 0x50000, v152
	v_mov_b32_e32 v81, v153
	v_lshlrev_b64 v[86:87], 1, v[80:81]
	v_lshl_add_u64 v[80:81], s[18:19], 0, v[86:87]
	global_load_dwordx4 v[106:109], v[80:81], off
	v_add_u32_e32 v80, 0x50080, v152
	v_mov_b32_e32 v81, v153
	v_lshlrev_b64 v[84:85], 1, v[80:81]
	v_lshl_add_u64 v[80:81], s[18:19], 0, v[84:85]
	global_load_dwordx4 v[110:113], v[80:81], off
	v_add_u32_e32 v80, 0x58000, v152
	v_mov_b32_e32 v81, v153
	v_lshlrev_b64 v[82:83], 1, v[80:81]
	v_lshl_add_u64 v[80:81], s[18:19], 0, v[82:83]
	v_add_u32_e32 v152, 0x58080, v152
	global_load_dwordx4 v[114:117], v[80:81], off
	v_lshlrev_b64 v[80:81], 1, v[152:153]
	v_lshl_add_u64 v[118:119], s[18:19], 0, v[80:81]
	global_load_dwordx4 v[118:121], v[118:119], off
	s_mov_b64 s[18:19], s[10:11]
	s_waitcnt vmcnt(0)
	v_lshlrev_b32_e32 v128, 16, v90
	v_and_b32_e32 v129, 0xffff0000, v90
	v_lshlrev_b32_e32 v130, 16, v91
	v_and_b32_e32 v131, 0xffff0000, v91
	v_lshlrev_b32_e32 v132, 16, v92
	v_and_b32_e32 v133, 0xffff0000, v92
	v_lshlrev_b32_e32 v92, 16, v93
	v_and_b32_e32 v93, 0xffff0000, v93
	v_lshlrev_b32_e32 v134, 16, v94
	v_and_b32_e32 v135, 0xffff0000, v94
	v_pk_fma_f32 v[76:77], v[76:77], v[12:13], v[128:129]
	v_lshlrev_b32_e32 v94, 16, v95
	v_and_b32_e32 v95, 0xffff0000, v95
	v_lshlrev_b32_e32 v136, 16, v96
	v_and_b32_e32 v137, 0xffff0000, v96
	v_lshlrev_b32_e32 v96, 16, v97
	v_and_b32_e32 v97, 0xffff0000, v97
	v_pk_fma_f32 v[78:79], v[78:79], v[14:15], v[130:131]
	v_pk_fma_f32 v[92:93], v[74:75], v[10:11], v[92:93]
	v_pk_fma_f32 v[74:75], v[72:73], v[8:9], v[132:133]
	v_cvt_pk_bf16_f32 v72, v76, v77
	v_cvt_pk_bf16_f32 v73, v78, v79
	v_lshl_add_u64 v[76:77], s[16:17], 0, v[122:123]
	v_pk_fma_f32 v[68:69], v[68:69], v[4:5], v[134:135]
	v_lshlrev_b32_e32 v138, 16, v98
	v_and_b32_e32 v139, 0xffff0000, v98
	v_lshlrev_b32_e32 v98, 16, v99
	v_and_b32_e32 v99, 0xffff0000, v99
	v_cvt_pk_bf16_f32 v74, v74, v75
	v_cvt_pk_bf16_f32 v75, v92, v93
	global_store_dwordx4 v[76:77], v[72:75], off
	v_pk_fma_f32 v[70:71], v[70:71], v[6:7], v[94:95]
	v_lshlrev_b32_e32 v140, 16, v100
	v_pk_fma_f32 v[72:73], v[62:63], v[2:3], v[96:97]
	v_pk_fma_f32 v[62:63], v[60:61], v[0:1], v[136:137]
	v_cvt_pk_bf16_f32 v60, v68, v69
	v_cvt_pk_bf16_f32 v61, v70, v71
	v_lshl_add_u64 v[68:69], s[16:17], 0, v[124:125]
	v_and_b32_e32 v141, 0xffff0000, v100
	v_lshlrev_b32_e32 v100, 16, v101
	v_and_b32_e32 v101, 0xffff0000, v101
	v_lshlrev_b32_e32 v142, 16, v102
	v_and_b32_e32 v143, 0xffff0000, v102
	v_cvt_pk_bf16_f32 v62, v62, v63
	v_cvt_pk_bf16_f32 v63, v72, v73
	global_store_dwordx4 v[68:69], v[60:63], off
	v_lshlrev_b32_e32 v102, 16, v103
	v_and_b32_e32 v103, 0xffff0000, v103
	v_pk_fma_f32 v[60:61], v[66:67], v[14:15], v[98:99]
	v_lshlrev_b32_e32 v162, 16, v104
	v_and_b32_e32 v163, 0xffff0000, v104
	v_lshlrev_b32_e32 v104, 16, v105
	v_and_b32_e32 v105, 0xffff0000, v105
	v_pk_fma_f32 v[62:63], v[64:65], v[12:13], v[138:139]
	v_pk_fma_f32 v[64:65], v[58:59], v[10:11], v[100:101]
	v_pk_fma_f32 v[58:59], v[56:57], v[8:9], v[140:141]
	v_cvt_pk_bf16_f32 v56, v62, v63
	v_cvt_pk_bf16_f32 v57, v60, v61
	v_lshl_add_u64 v[60:61], s[16:17], 0, v[126:127]
	v_pk_fma_f32 v[52:53], v[52:53], v[4:5], v[142:143]
	v_lshlrev_b32_e32 v164, 16, v106
	v_and_b32_e32 v165, 0xffff0000, v106
	v_lshlrev_b32_e32 v106, 16, v107
	v_and_b32_e32 v107, 0xffff0000, v107
	v_cvt_pk_bf16_f32 v58, v58, v59
	v_cvt_pk_bf16_f32 v59, v64, v65
	global_store_dwordx4 v[60:61], v[56:59], off
	v_pk_fma_f32 v[54:55], v[54:55], v[6:7], v[102:103]
	v_lshlrev_b32_e32 v166, 16, v108
	v_pk_fma_f32 v[56:57], v[46:47], v[2:3], v[104:105]
	v_pk_fma_f32 v[46:47], v[44:45], v[0:1], v[162:163]
	v_cvt_pk_bf16_f32 v44, v52, v53
	v_cvt_pk_bf16_f32 v45, v54, v55
	v_lshl_add_u64 v[52:53], s[16:17], 0, v[88:89]
	v_and_b32_e32 v167, 0xffff0000, v108
	v_lshlrev_b32_e32 v108, 16, v109
	v_and_b32_e32 v109, 0xffff0000, v109
	v_lshlrev_b32_e32 v168, 16, v110
	v_and_b32_e32 v169, 0xffff0000, v110
	v_cvt_pk_bf16_f32 v46, v46, v47
	v_cvt_pk_bf16_f32 v47, v56, v57
	global_store_dwordx4 v[52:53], v[44:47], off
	v_lshlrev_b32_e32 v170, 16, v112
	v_and_b32_e32 v171, 0xffff0000, v112
	v_pk_fma_f32 v[44:45], v[50:51], v[14:15], v[106:107]
	v_lshlrev_b32_e32 v112, 16, v113
	v_and_b32_e32 v113, 0xffff0000, v113
	v_lshlrev_b32_e32 v172, 16, v114
	v_and_b32_e32 v173, 0xffff0000, v114
	v_pk_fma_f32 v[46:47], v[48:49], v[12:13], v[164:165]
	v_pk_fma_f32 v[48:49], v[42:43], v[10:11], v[108:109]
	v_pk_fma_f32 v[42:43], v[40:41], v[8:9], v[166:167]
	v_cvt_pk_bf16_f32 v40, v46, v47
	v_cvt_pk_bf16_f32 v41, v44, v45
	v_lshl_add_u64 v[44:45], s[16:17], 0, v[86:87]
	v_pk_fma_f32 v[36:37], v[36:37], v[4:5], v[168:169]
	v_lshlrev_b32_e32 v110, 16, v111
	v_and_b32_e32 v111, 0xffff0000, v111
	v_lshlrev_b32_e32 v114, 16, v115
	v_and_b32_e32 v115, 0xffff0000, v115
	v_lshlrev_b32_e32 v182, 16, v116
	v_and_b32_e32 v183, 0xffff0000, v116
	v_lshlrev_b32_e32 v116, 16, v117
	v_and_b32_e32 v117, 0xffff0000, v117
	v_lshlrev_b32_e32 v184, 16, v118
	v_and_b32_e32 v185, 0xffff0000, v118
	v_cvt_pk_bf16_f32 v42, v42, v43
	v_cvt_pk_bf16_f32 v43, v48, v49
	global_store_dwordx4 v[44:45], v[40:43], off
	v_pk_fma_f32 v[12:13], v[32:33], v[12:13], v[172:173]
	v_lshlrev_b32_e32 v90, 16, v120
	v_pk_fma_f32 v[40:41], v[30:31], v[2:3], v[112:113]
	v_pk_fma_f32 v[30:31], v[28:29], v[0:1], v[170:171]
	v_cvt_pk_bf16_f32 v28, v36, v37
	v_lshl_add_u64 v[36:37], s[16:17], 0, v[84:85]
	v_and_b32_e32 v91, 0xffff0000, v120
	v_lshlrev_b32_e32 v120, 16, v121
	v_and_b32_e32 v121, 0xffff0000, v121
	v_pk_fma_f32 v[38:39], v[38:39], v[6:7], v[110:111]
	v_pk_fma_f32 v[14:15], v[34:35], v[14:15], v[114:115]
	v_cvt_pk_bf16_f32 v29, v38, v39
	v_cvt_pk_bf16_f32 v30, v30, v31
	v_cvt_pk_bf16_f32 v31, v40, v41
	global_store_dwordx4 v[36:37], v[28:31], off
	v_pk_fma_f32 v[26:27], v[26:27], v[10:11], v[116:117]
	v_pk_fma_f32 v[10:11], v[24:25], v[8:9], v[182:183]
	v_cvt_pk_bf16_f32 v8, v12, v13
	v_cvt_pk_bf16_f32 v9, v14, v15
	v_lshl_add_u64 v[12:13], s[16:17], 0, v[82:83]
	v_pk_fma_f32 v[4:5], v[20:21], v[4:5], v[184:185]
	v_lshlrev_b32_e32 v118, 16, v119
	v_and_b32_e32 v119, 0xffff0000, v119
	v_cvt_pk_bf16_f32 v10, v10, v11
	v_cvt_pk_bf16_f32 v11, v26, v27
	global_store_dwordx4 v[12:13], v[8:11], off
	v_pk_fma_f32 v[6:7], v[22:23], v[6:7], v[118:119]
	s_nop 0
	v_pk_fma_f32 v[8:9], v[18:19], v[2:3], v[120:121]
	v_pk_fma_f32 v[2:3], v[16:17], v[0:1], v[90:91]
	v_cvt_pk_bf16_f32 v0, v4, v5
	v_lshl_add_u64 v[4:5], s[16:17], 0, v[80:81]
	v_cvt_pk_bf16_f32 v1, v6, v7
	v_cvt_pk_bf16_f32 v2, v2, v3
	v_cvt_pk_bf16_f32 v3, v8, v9
	global_store_dwordx4 v[4:5], v[0:3], off
	s_mov_b64 s[16:17], s[12:13]
	s_cbranch_vccz .LBB0_2255
	s_waitcnt vmcnt(0)
	s_cmpk_gt_u32 s23, 0xff
	s_cbranch_scc1 .LBB0_2266
	s_barrier
